# agent-scope write-through (sc1) on all wide global stores after P0, to shrink the release fence's L2 write-back at each grid barrier
# baseline (speedup 1.0000x reference)
.LBB0_226:
	s_or_b64 exec, exec, s[8:9]
	s_waitcnt lgkmcnt(0)
	s_barrier
	ds_read_b128 v[4:7], v185 offset:32768
	ds_read_b128 v[8:11], v185 offset:32784
	s_mov_b32 s8, 0xf800000
	s_waitcnt lgkmcnt(0)
	s_barrier
	v_add_f32_e32 v4, 0, v4
	v_add_f32_e32 v4, v4, v5
	v_add_f32_e32 v4, v4, v6
	v_add_f32_e32 v4, v4, v7
	v_add_f32_e32 v4, v4, v8
	v_add_f32_e32 v4, v4, v9
	v_add_f32_e32 v4, v4, v10
	v_add_f32_e32 v4, v4, v11
	v_fmamk_f32 v4, v4, 0x3a000000, v212
	v_mul_f32_e32 v5, 0x4f800000, v4
	v_cmp_gt_f32_e32 vcc, s8, v4
	s_nop 1
	v_cndmask_b32_e32 v4, v4, v5, vcc
	v_sqrt_f32_e32 v5, v4
	s_nop 0
	v_add_u32_e32 v6, -1, v5
	v_add_u32_e32 v7, 1, v5
	v_fma_f32 v8, -v6, v5, v4
	v_fma_f32 v9, -v7, v5, v4
	v_cmp_ge_f32_e64 s[38:39], 0, v8
	s_nop 1
	v_cndmask_b32_e64 v5, v5, v6, s[38:39]
	v_cmp_lt_f32_e64 s[38:39], 0, v9
	s_nop 1
	v_cndmask_b32_e64 v5, v5, v7, s[38:39]
	v_mul_f32_e32 v6, 0x37800000, v5
	v_cndmask_b32_e32 v5, v5, v6, vcc
	v_cmp_class_f32_e32 vcc, v4, v213
	s_nop 1
	v_cndmask_b32_e32 v12, v5, v4, vcc
	v_div_scale_f32 v4, s[8:9], v12, v12, 1.0
	v_rcp_f32_e32 v13, v4
	s_add_i32 s8, s4, 0x4000
	s_ashr_i32 s9, s8, 31
	s_lshl_b64 s[8:9], s[8:9], 12
	v_fma_f32 v5, -v4, v13, 1.0
	v_fmac_f32_e32 v13, v5, v13
	v_div_scale_f32 v5, vcc, 1.0, v12, 1.0
	v_mul_f32_e32 v14, v5, v13
	v_fma_f32 v6, -v4, v14, v5
	v_fmac_f32_e32 v14, v6, v13
	v_fma_f32 v15, -v4, v14, v5
	ds_read_b128 v[4:7], v55 offset:8192
	ds_read_b128 v[8:11], v55 offset:24576
	v_div_fmas_f32 v13, v15, v13, v14
	v_div_fixup_f32 v12, v13, v12, 1.0
	v_pk_mul_f32 v[0:1], v[0:1], v[12:13] op_sel_hi:[1,0]
	v_pk_mul_f32 v[2:3], v[2:3], v[12:13] op_sel_hi:[1,0]
	s_waitcnt lgkmcnt(0)
	v_pk_fma_f32 v[0:1], v[4:5], v[0:1], v[8:9]
	v_pk_fma_f32 v[2:3], v[6:7], v[2:3], v[10:11]
	v_bfe_u32 v4, v0, 16, 1
	v_add3_u32 v0, v0, v4, s33
	v_bfe_u32 v4, v1, 16, 1
	v_lshrrev_b32_e32 v0, 16, v0
	v_add3_u32 v1, v1, v4, s33
	v_and_or_b32 v0, v1, s96, v0
	v_bfe_u32 v1, v2, 16, 1
	v_add3_u32 v1, v2, v1, s33
	v_bfe_u32 v2, v3, 16, 1
	v_lshrrev_b32_e32 v1, 16, v1
	v_add3_u32 v2, v3, v2, s33
	v_and_or_b32 v1, v2, s96, v1
	v_lshl_add_u64 v[2:3], v[48:49], 0, s[8:9]
	s_add_i32 s4, s4, s94
	v_readlane_b32 s8, v254, 42
	v_readlane_b32 s9, v254, 43
	s_add_u32 s6, s6, s8
	s_addc_u32 s7, s7, s9
	s_add_u32 s0, s0, s8
	s_addc_u32 s1, s1, s9
	s_cmpk_gt_i32 s4, 0xff
	global_store_dwordx2 v[2:3], v[0:1], off sc1
	s_cbranch_scc1 .LBB0_253

.LBB0_249:
	s_waitcnt vmcnt(0)
	v_pk_add_f32 v[10:11], v[2:3], v[10:11]
	v_pk_add_f32 v[8:9], v[0:1], v[8:9]
	v_pk_add_f32 v[6:7], v[10:11], v[6:7]
	v_pk_add_f32 v[4:5], v[8:9], v[4:5]
	v_pk_add_f32 v[6:7], v[6:7], v[18:19]
	v_pk_add_f32 v[4:5], v[4:5], v[16:17]
	v_pk_add_f32 v[6:7], v[6:7], v[14:15]
	v_pk_add_f32 v[4:5], v[4:5], v[12:13]
	v_pk_add_f32 v[6:7], v[6:7], v[26:27]
	v_pk_add_f32 v[4:5], v[4:5], v[24:25]
	v_pk_add_f32 v[6:7], v[6:7], v[22:23]
	v_pk_add_f32 v[4:5], v[4:5], v[20:21]
	v_pk_add_f32 v[6:7], v[6:7], v[34:35]
	v_pk_add_f32 v[4:5], v[4:5], v[32:33]
	v_pk_add_f32 v[6:7], v[6:7], v[30:31]
	v_pk_add_f32 v[4:5], v[4:5], v[28:29]
	v_pk_add_f32 v[6:7], v[6:7], v[42:43]
	v_pk_add_f32 v[4:5], v[4:5], v[40:41]
	v_pk_add_f32 v[6:7], v[6:7], v[38:39]
	v_pk_add_f32 v[4:5], v[4:5], v[36:37]
	v_pk_add_f32 v[6:7], v[6:7], v[46:47]
	v_pk_add_f32 v[4:5], v[4:5], v[44:45]
	v_cndmask_b32_e64 v3, v7, v3, s[80:81]
	v_cndmask_b32_e64 v1, v5, v1, s[80:81]
	v_cndmask_b32_e64 v0, v4, v0, s[80:81]
	s_and_b64 vcc, exec, s[38:39]
	v_cndmask_b32_e64 v2, v6, v2, s[80:81]
	s_cbranch_vccnz .LBB0_251
	v_add_co_u32_e32 v4, vcc, 0x3a100000, v52
	s_nop 1
	v_addc_co_u32_e32 v5, vcc, 0, v53, vcc
	global_store_dwordx4 v[4:5], v[0:3], off sc1

.LBB0_257:
	s_add_i32 s1, s0, s88
	s_cmpk_lt_i32 s1, 0x4000
	s_cselect_b64 s[18:19], -1, 0
	s_and_b64 s[6:7], s[18:19], exec
	s_cselect_b32 s38, s1, s0
	s_add_i32 s1, s1, s88
	s_cmpk_lt_i32 s1, 0x4000
	s_cselect_b64 s[12:13], -1, 0
	s_and_b64 s[6:7], s[12:13], exec
	s_cselect_b32 s16, s1, s0
	s_add_i32 s1, s1, s88
	s_cmpk_lt_i32 s1, 0x4000
	s_cselect_b64 s[6:7], -1, 0
	s_and_b64 s[8:9], s[6:7], exec
	s_cselect_b32 s10, s1, s0
	s_ashr_i32 s1, s0, 31
	s_lshl_b64 s[40:41], s[0:1], 12
	v_lshl_add_u64 v[64:65], v[96:97], 0, s[40:41]
	global_load_dwordx2 v[66:67], v[64:65], off
	global_load_dwordx2 v[68:69], v[64:65], off offset:512
	global_load_dwordx2 v[70:71], v[64:65], off offset:1024
	global_load_dwordx2 v[72:73], v[64:65], off offset:1536
	global_load_dwordx2 v[74:75], v[64:65], off offset:2048
	global_load_dwordx2 v[76:77], v[64:65], off offset:2560
	global_load_dwordx2 v[78:79], v[64:65], off offset:3072
	s_nop 0
	global_load_dwordx2 v[64:65], v[64:65], off offset:3584
	s_mov_b32 s1, 0xf800000
	s_ashr_i32 s39, s38, 31
	s_ashr_i32 s17, s16, 31
	s_ashr_i32 s11, s10, 31
	s_lshl_b64 s[30:31], s[38:39], 12
	s_lshl_b64 s[14:15], s[16:17], 12
	v_lshl_add_u64 v[130:131], v[96:97], 0, s[14:15]
	v_lshl_add_u64 v[146:147], v[104:105], 0, s[40:41]
	s_mov_b64 s[40:41], -1
	s_waitcnt vmcnt(7)
	v_and_b32_e32 v95, 0xffff0000, v66
	v_and_b32_e32 v107, 0xffff0000, v67
	s_waitcnt vmcnt(6)
	v_and_b32_e32 v115, 0xffff0000, v68
	v_and_b32_e32 v117, 0xffff0000, v69
	v_lshlrev_b32_e32 v94, 16, v66
	v_lshlrev_b32_e32 v106, 16, v67
	v_lshlrev_b32_e32 v114, 16, v68
	v_lshlrev_b32_e32 v116, 16, v69
	s_waitcnt vmcnt(5)
	v_lshlrev_b32_e32 v118, 16, v70
	v_and_b32_e32 v119, 0xffff0000, v70
	v_lshlrev_b32_e32 v92, 16, v71
	v_and_b32_e32 v93, 0xffff0000, v71
	s_waitcnt vmcnt(4)
	v_lshlrev_b32_e32 v90, 16, v72
	v_and_b32_e32 v91, 0xffff0000, v72
	v_lshlrev_b32_e32 v88, 16, v73
	v_and_b32_e32 v89, 0xffff0000, v73
	s_waitcnt vmcnt(3)
	v_lshlrev_b32_e32 v86, 16, v74
	v_and_b32_e32 v87, 0xffff0000, v74
	v_lshlrev_b32_e32 v84, 16, v75
	v_and_b32_e32 v85, 0xffff0000, v75
	s_waitcnt vmcnt(2)
	v_lshlrev_b32_e32 v74, 16, v76
	v_and_b32_e32 v75, 0xffff0000, v76
	v_lshlrev_b32_e32 v72, 16, v77
	v_and_b32_e32 v73, 0xffff0000, v77
	s_waitcnt vmcnt(1)
	v_lshlrev_b32_e32 v70, 16, v78
	v_and_b32_e32 v71, 0xffff0000, v78
	v_lshlrev_b32_e32 v68, 16, v79
	v_and_b32_e32 v69, 0xffff0000, v79
	v_mul_f32_e32 v76, v95, v95
	v_mul_f32_e32 v77, v107, v107
	v_mul_f32_e32 v78, v115, v115
	v_mul_f32_e32 v79, v117, v117
	v_mul_f32_e32 v80, v119, v119
	v_mul_f32_e32 v81, v93, v93
	v_fmac_f32_e32 v76, v94, v94
	v_fmac_f32_e32 v77, v106, v106
	v_fmac_f32_e32 v78, v114, v114
	v_fmac_f32_e32 v79, v116, v116
	v_mul_f32_e32 v82, v91, v91
	v_mul_f32_e32 v83, v89, v89
	v_fmac_f32_e32 v80, v118, v118
	v_fmac_f32_e32 v81, v92, v92
	v_add_f32_e32 v76, v76, v77
	v_add_f32_e32 v77, v78, v79
	v_mul_f32_e32 v108, v87, v87
	v_mul_f32_e32 v109, v85, v85
	v_fmac_f32_e32 v82, v90, v90
	v_fmac_f32_e32 v83, v88, v88
	v_add_f32_e32 v78, v80, v81
	v_add_f32_e32 v76, v76, v77
	v_mul_f32_e32 v110, v75, v75
	v_mul_f32_e32 v111, v73, v73
	v_fmac_f32_e32 v108, v86, v86
	v_fmac_f32_e32 v109, v84, v84
	v_add_f32_e32 v79, v82, v83
	v_add_f32_e32 v76, v78, v76
	s_waitcnt vmcnt(0)
	v_lshlrev_b32_e32 v66, 16, v64
	v_and_b32_e32 v67, 0xffff0000, v64
	v_lshlrev_b32_e32 v64, 16, v65
	v_and_b32_e32 v65, 0xffff0000, v65
	v_mul_f32_e32 v112, v71, v71
	v_mul_f32_e32 v113, v69, v69
	v_fmac_f32_e32 v110, v74, v74
	v_fmac_f32_e32 v111, v72, v72
	v_add_f32_e32 v80, v108, v109
	v_add_f32_e32 v76, v79, v76
	v_mul_f32_e32 v120, v67, v67
	v_mul_f32_e32 v121, v65, v65
	v_fmac_f32_e32 v112, v70, v70
	v_fmac_f32_e32 v113, v68, v68
	v_add_f32_e32 v81, v110, v111
	v_add_f32_e32 v76, v80, v76
	v_fmac_f32_e32 v120, v66, v66
	v_fmac_f32_e32 v121, v64, v64
	v_add_f32_e32 v82, v112, v113
	v_add_f32_e32 v76, v81, v76
	v_add_f32_e32 v83, v120, v121
	v_add_f32_e32 v76, v82, v76
	v_add_f32_e32 v76, v83, v76
	v_lshl_add_u64 v[120:121], v[96:97], 0, s[30:31]
	s_nop 0
	v_add_f32_dpp v76, v76, v76 quad_perm:[1,0,3,2] row_mask:0xf bank_mask:0xf bound_ctrl:1
	s_nop 1
	v_add_f32_dpp v76, v76, v76 quad_perm:[2,3,0,1] row_mask:0xf bank_mask:0xf bound_ctrl:1
	s_nop 1
	v_add_f32_dpp v76, v76, v76 row_half_mirror row_mask:0xf bank_mask:0xf bound_ctrl:1
	s_nop 1
	v_add_f32_dpp v76, v76, v76 row_mirror row_mask:0xf bank_mask:0xf bound_ctrl:1
	ds_swizzle_b32 v77, v76 offset:swizzle(SWAP,16)
	s_waitcnt lgkmcnt(0)
	v_add_f32_e32 v76, v76, v77
	v_mov_b32_e32 v77, v76
	s_nop 1
	v_permlane32_swap_b32_e32 v76, v77
	v_add_f32_e32 v76, v76, v77
	v_fmamk_f32 v76, v76, 0x3a000000, v212
	v_mul_f32_e32 v77, 0x4f800000, v76
	v_cmp_gt_f32_e32 vcc, s1, v76
	s_nop 1
	v_cndmask_b32_e32 v108, v76, v77, vcc
	v_sqrt_f32_e32 v109, v108
	global_load_dwordx2 v[82:83], v[120:121], off
	global_load_dwordx2 v[80:81], v[120:121], off offset:512
	global_load_dwordx2 v[78:79], v[120:121], off offset:1024
	global_load_dwordx2 v[76:77], v[120:121], off offset:1536
	global_load_dwordx2 v[128:129], v[130:131], off
	global_load_dwordx2 v[126:127], v[130:131], off offset:512
	global_load_dwordx2 v[124:125], v[130:131], off offset:1024
	global_load_dwordx2 v[122:123], v[130:131], off offset:1536
	v_add_u32_e32 v110, -1, v109
	v_fma_f32 v111, -v110, v109, v108
	v_cmp_ge_f32_e64 s[36:37], 0, v111
	v_add_u32_e32 v111, 1, v109
	s_nop 0
	v_cndmask_b32_e64 v110, v109, v110, s[36:37]
	v_fma_f32 v109, -v111, v109, v108
	v_cmp_lt_f32_e64 s[36:37], 0, v109
	s_nop 1
	v_cndmask_b32_e64 v109, v110, v111, s[36:37]
	v_mul_f32_e32 v110, 0x37800000, v109
	v_cndmask_b32_e32 v109, v109, v110, vcc
	v_cmp_class_f32_e32 vcc, v108, v213
	s_nop 1
	v_cndmask_b32_e32 v108, v109, v108, vcc
	v_div_scale_f32 v109, s[8:9], v108, v108, 1.0
	v_rcp_f32_e32 v110, v109
	s_lshl_b64 s[8:9], s[10:11], 12
	v_lshl_add_u64 v[144:145], v[96:97], 0, s[8:9]
	s_cmpk_gt_i32 s38, 0x3fff
	v_fma_f32 v111, -v109, v110, 1.0
	v_fmac_f32_e32 v110, v111, v110
	v_div_scale_f32 v111, vcc, 1.0, v108, 1.0
	v_mul_f32_e32 v112, v111, v110
	v_fma_f32 v113, -v109, v112, v111
	v_fmac_f32_e32 v112, v113, v110
	v_fma_f32 v109, -v109, v112, v111
	v_div_fmas_f32 v109, v109, v110, v112
	v_div_fixup_f32 v138, v109, v108, 1.0
	v_pk_mul_f32 v[94:95], v[94:95], v[138:139] op_sel_hi:[1,0]
	v_pk_mul_f32 v[106:107], v[106:107], v[138:139] op_sel_hi:[1,0]
	v_pk_fma_f32 v[94:95], v[0:1], v[94:95], v[8:9]
	v_pk_fma_f32 v[106:107], v[2:3], v[106:107], v[10:11]
	v_bfe_u32 v108, v95, 16, 1
	v_add3_u32 v95, v95, v108, s33
	v_bfe_u32 v108, v94, 16, 1
	v_add3_u32 v94, v94, v108, s33
	v_bfe_u32 v108, v107, 16, 1
	v_add3_u32 v107, v107, v108, s33
	v_bfe_u32 v108, v106, 16, 1
	v_add3_u32 v106, v106, v108, s33
	v_lshrrev_b32_e32 v94, 16, v94
	v_and_or_b32 v94, v95, s96, v94
	v_lshrrev_b32_e32 v95, 16, v106
	v_and_or_b32 v95, v107, s96, v95
	global_load_dwordx2 v[112:113], v[144:145], off
	global_load_dwordx2 v[110:111], v[144:145], off offset:512
	global_load_dwordx2 v[108:109], v[144:145], off offset:1024
	global_load_dwordx2 v[106:107], v[144:145], off offset:1536
	v_pk_mul_f32 v[92:93], v[92:93], v[138:139] op_sel_hi:[1,0]
	global_store_dwordx2 v[146:147], v[94:95], off sc1
	v_pk_mul_f32 v[94:95], v[114:115], v[138:139] op_sel_hi:[1,0]
	v_pk_fma_f32 v[92:93], v[18:19], v[92:93], v[26:27]
	v_pk_fma_f32 v[94:95], v[4:5], v[94:95], v[12:13]
	v_pk_mul_f32 v[90:91], v[90:91], v[138:139] op_sel_hi:[1,0]
	v_bfe_u32 v114, v95, 16, 1
	v_add3_u32 v114, v95, v114, s33
	v_bfe_u32 v95, v94, 16, 1
	v_add3_u32 v115, v94, v95, s33
	v_pk_mul_f32 v[94:95], v[116:117], v[138:139] op_sel_hi:[1,0]
	v_pk_fma_f32 v[90:91], v[90:91], v[20:21], v[28:29]
	v_pk_fma_f32 v[94:95], v[6:7], v[94:95], v[14:15]
	v_pk_mul_f32 v[88:89], v[88:89], v[138:139] op_sel_hi:[1,0]
	v_bfe_u32 v116, v95, 16, 1
	v_add3_u32 v95, v95, v116, s33
	v_bfe_u32 v116, v94, 16, 1
	v_add3_u32 v116, v94, v116, s33
	v_lshrrev_b32_e32 v94, 16, v115
	v_and_or_b32 v94, v114, s96, v94
	v_lshrrev_b32_e32 v114, 16, v116
	v_and_or_b32 v95, v95, s96, v114
	global_store_dwordx2 v[146:147], v[94:95], off offset:512 sc1
	v_pk_mul_f32 v[94:95], v[118:119], v[138:139] op_sel_hi:[1,0]
	v_pk_fma_f32 v[88:89], v[88:89], v[22:23], v[30:31]
	v_pk_fma_f32 v[94:95], v[16:17], v[94:95], v[24:25]
	v_pk_mul_f32 v[86:87], v[86:87], v[138:139] op_sel_hi:[1,0]
	v_bfe_u32 v114, v95, 16, 1
	v_add3_u32 v95, v95, v114, s33
	v_bfe_u32 v114, v94, 16, 1
	v_add3_u32 v94, v94, v114, s33
	v_bfe_u32 v114, v93, 16, 1
	v_add3_u32 v93, v93, v114, s33
	v_bfe_u32 v114, v92, 16, 1
	v_add3_u32 v114, v92, v114, s33
	v_lshrrev_b32_e32 v92, 16, v94
	v_lshrrev_b32_e32 v94, 16, v114
	v_and_or_b32 v92, v95, s96, v92
	v_and_or_b32 v93, v93, s96, v94
	global_store_dwordx2 v[146:147], v[92:93], off offset:1024 sc1
	v_bfe_u32 v92, v91, 16, 1
	v_add3_u32 v91, v91, v92, s33
	v_bfe_u32 v92, v90, 16, 1
	v_add3_u32 v90, v90, v92, s33
	v_bfe_u32 v92, v89, 16, 1
	v_add3_u32 v89, v89, v92, s33
	v_bfe_u32 v92, v88, 16, 1
	v_add3_u32 v92, v88, v92, s33
	v_lshrrev_b32_e32 v88, 16, v90
	v_lshrrev_b32_e32 v90, 16, v92
	v_and_or_b32 v88, v91, s96, v88
	v_and_or_b32 v89, v89, s96, v90
	global_store_dwordx2 v[146:147], v[88:89], off offset:1536 sc1
	global_load_dwordx2 v[148:149], v[120:121], off offset:2048
	global_load_dwordx2 v[150:151], v[120:121], off offset:2560
	global_load_dwordx2 v[152:153], v[120:121], off offset:3072
	global_load_dwordx2 v[154:155], v[120:121], off offset:3584
	global_load_dwordx2 v[136:137], v[130:131], off offset:2048
	global_load_dwordx2 v[134:135], v[130:131], off offset:2560
	global_load_dwordx2 v[132:133], v[130:131], off offset:3072
	s_nop 0
	global_load_dwordx2 v[130:131], v[130:131], off offset:3584
	s_nop 0
	global_load_dwordx2 v[120:121], v[144:145], off offset:2048
	global_load_dwordx2 v[118:119], v[144:145], off offset:2560
	global_load_dwordx2 v[116:117], v[144:145], off offset:3072
	global_load_dwordx2 v[114:115], v[144:145], off offset:3584
	v_pk_fma_f32 v[86:87], v[86:87], v[32:33], v[40:41]
	v_pk_mul_f32 v[84:85], v[84:85], v[138:139] op_sel_hi:[1,0]
	v_bfe_u32 v88, v87, 16, 1
	v_add3_u32 v87, v87, v88, s33
	v_bfe_u32 v88, v86, 16, 1
	v_add3_u32 v86, v86, v88, s33
	v_pk_fma_f32 v[84:85], v[84:85], v[34:35], v[42:43]
	v_lshrrev_b32_e32 v86, 16, v86
	v_and_or_b32 v86, v87, s96, v86
	v_bfe_u32 v87, v85, 16, 1
	v_add3_u32 v85, v85, v87, s33
	v_bfe_u32 v87, v84, 16, 1
	v_add3_u32 v84, v84, v87, s33
	v_pk_mul_f32 v[74:75], v[74:75], v[138:139] op_sel_hi:[1,0]
	v_lshrrev_b32_e32 v84, 16, v84
	v_pk_fma_f32 v[74:75], v[74:75], v[36:37], v[44:45]
	v_and_or_b32 v87, v85, s96, v84
	v_bfe_u32 v84, v75, 16, 1
	v_pk_mul_f32 v[72:73], v[72:73], v[138:139] op_sel_hi:[1,0]
	v_add3_u32 v75, v75, v84, s33
	v_bfe_u32 v84, v74, 16, 1
	v_pk_fma_f32 v[72:73], v[72:73], v[38:39], v[46:47]
	v_add3_u32 v74, v74, v84, s33
	v_bfe_u32 v84, v73, 16, 1
	v_add3_u32 v73, v73, v84, s33
	v_bfe_u32 v84, v72, 16, 1
	v_add3_u32 v84, v72, v84, s33
	v_lshrrev_b32_e32 v72, 16, v74
	v_lshrrev_b32_e32 v74, 16, v84
	v_pk_mul_f32 v[70:71], v[70:71], v[138:139] op_sel_hi:[1,0]
	v_and_or_b32 v72, v75, s96, v72
	v_and_or_b32 v73, v73, s96, v74
	v_pk_fma_f32 v[70:71], v[70:71], v[48:49], v[56:57]
	global_store_dwordx2 v[146:147], v[72:73], off offset:2560 sc1
	v_bfe_u32 v72, v71, 16, 1
	v_pk_mul_f32 v[68:69], v[68:69], v[138:139] op_sel_hi:[1,0]
	v_add3_u32 v71, v71, v72, s33
	v_bfe_u32 v72, v70, 16, 1
	v_pk_fma_f32 v[68:69], v[68:69], v[50:51], v[58:59]
	v_add3_u32 v70, v70, v72, s33
	v_bfe_u32 v72, v69, 16, 1
	v_add3_u32 v69, v69, v72, s33
	v_bfe_u32 v72, v68, 16, 1
	v_add3_u32 v72, v68, v72, s33
	v_lshrrev_b32_e32 v68, 16, v70
	v_lshrrev_b32_e32 v70, 16, v72
	v_pk_mul_f32 v[66:67], v[66:67], v[138:139] op_sel_hi:[1,0]
	v_and_or_b32 v68, v71, s96, v68
	v_and_or_b32 v69, v69, s96, v70
	v_pk_fma_f32 v[66:67], v[66:67], v[52:53], v[60:61]
	global_store_dwordx2 v[146:147], v[68:69], off offset:3072 sc1
	v_pk_mul_f32 v[64:65], v[64:65], v[138:139] op_sel_hi:[1,0]
	v_bfe_u32 v68, v67, 16, 1
	v_add3_u32 v67, v67, v68, s33
	v_bfe_u32 v68, v66, 16, 1
	v_pk_fma_f32 v[64:65], v[64:65], v[54:55], v[62:63]
	v_add3_u32 v66, v66, v68, s33
	v_bfe_u32 v68, v65, 16, 1
	v_add3_u32 v65, v65, v68, s33
	v_bfe_u32 v68, v64, 16, 1
	v_add3_u32 v68, v64, v68, s33
	v_lshrrev_b32_e32 v64, 16, v66
	v_lshrrev_b32_e32 v66, 16, v68
	v_and_or_b32 v64, v67, s96, v64
	v_and_or_b32 v65, v65, s96, v66
	s_cselect_b64 s[36:37], -1, 0
	global_store_dwordx2 v[146:147], v[86:87], off offset:2048 sc1
	global_store_dwordx2 v[146:147], v[64:65], off offset:3584 sc1
	s_waitcnt vmcnt(31)
	v_lshlrev_b32_e32 v92, 16, v82
	v_and_b32_e32 v93, 0xffff0000, v82
	v_lshlrev_b32_e32 v94, 16, v83
	v_and_b32_e32 v95, 0xffff0000, v83
	s_waitcnt vmcnt(30)
	v_lshlrev_b32_e32 v88, 16, v80
	v_and_b32_e32 v89, 0xffff0000, v80
	v_lshlrev_b32_e32 v90, 16, v81
	v_and_b32_e32 v91, 0xffff0000, v81
	s_waitcnt vmcnt(29)
	v_lshlrev_b32_e32 v84, 16, v78
	v_and_b32_e32 v85, 0xffff0000, v78
	v_lshlrev_b32_e32 v86, 16, v79
	v_and_b32_e32 v87, 0xffff0000, v79
	s_waitcnt vmcnt(28)
	v_lshlrev_b32_e32 v80, 16, v76
	v_and_b32_e32 v81, 0xffff0000, v76
	v_lshlrev_b32_e32 v82, 16, v77
	v_and_b32_e32 v83, 0xffff0000, v77
	s_waitcnt vmcnt(15)
	v_lshlrev_b32_e32 v76, 16, v148
	v_and_b32_e32 v77, 0xffff0000, v148
	v_lshlrev_b32_e32 v78, 16, v149
	v_and_b32_e32 v79, 0xffff0000, v149
	s_waitcnt vmcnt(14)
	v_lshlrev_b32_e32 v72, 16, v150
	v_and_b32_e32 v73, 0xffff0000, v150
	v_lshlrev_b32_e32 v74, 16, v151
	v_and_b32_e32 v75, 0xffff0000, v151
	s_waitcnt vmcnt(13)
	v_lshlrev_b32_e32 v68, 16, v152
	v_and_b32_e32 v69, 0xffff0000, v152
	v_lshlrev_b32_e32 v70, 16, v153
	v_and_b32_e32 v71, 0xffff0000, v153
	s_waitcnt vmcnt(12)
	v_lshlrev_b32_e32 v64, 16, v154
	v_and_b32_e32 v65, 0xffff0000, v154
	v_lshlrev_b32_e32 v66, 16, v155
	v_and_b32_e32 v67, 0xffff0000, v155
	s_and_b64 vcc, exec, s[36:37]
	s_cbranch_vccnz .LBB0_259
	s_mov_b64 s[40:41], 0

.LBB0_264:
	s_andn2_b64 vcc, exec, s[18:19]
	s_cbranch_vccnz .LBB0_266
	v_lshl_add_u64 v[138:139], s[38:39], 2, v[100:101]
	global_store_dwordx4 v[138:139], v[92:95], off sc1
	global_store_dwordx4 v[138:139], v[88:91], off offset:1024 sc1
	global_store_dwordx4 v[138:139], v[84:87], off offset:2048 sc1
	global_store_dwordx4 v[138:139], v[80:83], off offset:3072 sc1
	v_add_co_u32_e32 v138, vcc, 0x1000, v138
	s_nop 1
	v_addc_co_u32_e32 v139, vcc, 0, v139, vcc
	global_store_dwordx4 v[138:139], v[76:79], off sc1
	global_store_dwordx4 v[138:139], v[72:75], off offset:1024 sc1
	global_store_dwordx4 v[138:139], v[68:71], off offset:2048 sc1
	global_store_dwordx4 v[138:139], v[64:67], off offset:3072 sc1
.LBB0_266:
	v_mul_f32_e32 v138, v93, v93
	v_mul_f32_e32 v139, v95, v95
	v_fmac_f32_e32 v138, v92, v92
	v_fmac_f32_e32 v139, v94, v94
	v_add_f32_e32 v138, v138, v139
	v_mul_f32_e32 v139, v89, v89
	v_mul_f32_e32 v140, v91, v91
	v_fmac_f32_e32 v139, v88, v88
	v_fmac_f32_e32 v140, v90, v90
	v_add_f32_e32 v139, v139, v140
	v_add_f32_e32 v138, v138, v139
	v_mul_f32_e32 v139, v85, v85
	v_mul_f32_e32 v140, v87, v87
	v_fmac_f32_e32 v139, v84, v84
	v_fmac_f32_e32 v140, v86, v86
	v_add_f32_e32 v139, v139, v140
	v_add_f32_e32 v138, v139, v138
	v_mul_f32_e32 v139, v81, v81
	v_mul_f32_e32 v140, v83, v83
	v_fmac_f32_e32 v139, v80, v80
	v_fmac_f32_e32 v140, v82, v82
	v_add_f32_e32 v139, v139, v140
	v_add_f32_e32 v138, v139, v138
	v_mul_f32_e32 v139, v77, v77
	v_mul_f32_e32 v140, v79, v79
	v_fmac_f32_e32 v139, v76, v76
	v_fmac_f32_e32 v140, v78, v78
	v_add_f32_e32 v139, v139, v140
	v_add_f32_e32 v138, v139, v138
	v_mul_f32_e32 v139, v73, v73
	v_mul_f32_e32 v140, v75, v75
	v_fmac_f32_e32 v139, v72, v72
	v_fmac_f32_e32 v140, v74, v74
	v_add_f32_e32 v139, v139, v140
	v_add_f32_e32 v138, v139, v138
	v_mul_f32_e32 v139, v69, v69
	v_mul_f32_e32 v140, v71, v71
	v_fmac_f32_e32 v139, v68, v68
	v_fmac_f32_e32 v140, v70, v70
	v_add_f32_e32 v139, v139, v140
	v_add_f32_e32 v138, v139, v138
	v_mul_f32_e32 v139, v65, v65
	v_mul_f32_e32 v140, v67, v67
	v_fmac_f32_e32 v139, v64, v64
	v_fmac_f32_e32 v140, v66, v66
	v_add_f32_e32 v139, v139, v140
	v_add_f32_e32 v138, v139, v138
	s_andn2_b64 vcc, exec, s[18:19]
	s_nop 0
	v_add_f32_dpp v138, v138, v138 quad_perm:[1,0,3,2] row_mask:0xf bank_mask:0xf bound_ctrl:1
	s_nop 1
	v_add_f32_dpp v138, v138, v138 quad_perm:[2,3,0,1] row_mask:0xf bank_mask:0xf bound_ctrl:1
	s_nop 1
	v_add_f32_dpp v138, v138, v138 row_half_mirror row_mask:0xf bank_mask:0xf bound_ctrl:1
	s_nop 1
	v_add_f32_dpp v138, v138, v138 row_mirror row_mask:0xf bank_mask:0xf bound_ctrl:1
	ds_swizzle_b32 v139, v138 offset:swizzle(SWAP,16)
	s_waitcnt lgkmcnt(0)
	v_add_f32_e32 v138, v138, v139
	v_mov_b32_e32 v139, v138
	s_nop 1
	v_permlane32_swap_b32_e32 v138, v139
	s_cbranch_vccnz .LBB0_268
	v_add_f32_e32 v138, v138, v139
	v_fmamk_f32 v138, v138, 0x3a000000, v212
	s_mov_b32 s4, 0xf800000
	v_cmp_gt_f32_e32 vcc, s4, v138
	v_mul_f32_e32 v139, 0x4f800000, v138
	s_and_b64 s[18:19], exec, s[36:37]
	v_cndmask_b32_e32 v138, v138, v139, vcc
	v_sqrt_f32_e32 v139, v138
	s_cselect_b32 s1, 0x2000, 0
	v_add_u32_e32 v140, -1, v139
	v_fma_f32 v143, -v140, v139, v138
	v_cmp_ge_f32_e64 s[36:37], 0, v143
	v_add_u32_e32 v143, 1, v139
	s_nop 0
	v_cndmask_b32_e64 v140, v139, v140, s[36:37]
	v_fma_f32 v139, -v143, v139, v138
	v_cmp_lt_f32_e64 s[36:37], 0, v139
	s_nop 1
	v_cndmask_b32_e64 v139, v140, v143, s[36:37]
	v_mul_f32_e32 v140, 0x37800000, v139
	v_cndmask_b32_e32 v139, v139, v140, vcc
	v_cmp_class_f32_e32 vcc, v138, v213
	s_nop 1
	v_cndmask_b32_e32 v138, v139, v138, vcc
	v_div_scale_f32 v139, s[18:19], v138, v138, 1.0
	v_rcp_f32_e32 v140, v139
	s_nop 0
	v_fma_f32 v143, -v139, v140, 1.0
	v_fmac_f32_e32 v140, v143, v140
	v_div_scale_f32 v143, vcc, 1.0, v138, 1.0
	v_mul_f32_e32 v144, v143, v140
	v_fma_f32 v145, -v139, v144, v143
	v_fmac_f32_e32 v144, v145, v140
	v_fma_f32 v139, -v139, v144, v143
	v_div_fmas_f32 v139, v139, v140, v144
	v_div_fixup_f32 v140, v139, v138, 1.0
	v_pk_mul_f32 v[152:153], v[92:93], v[140:141] op_sel_hi:[1,0]
	v_add_u32_e32 v92, s1, v142
	ds_read_b128 v[144:147], v92
	ds_read_b128 v[148:151], v92 offset:16384
	v_pk_mul_f32 v[94:95], v[94:95], v[140:141] op_sel_hi:[1,0]
	v_lshl_add_u64 v[138:139], v[104:105], 0, s[30:31]
	s_waitcnt lgkmcnt(0)
	v_pk_fma_f32 v[144:145], v[152:153], v[144:145], v[148:149]
	s_nop 0
	v_bfe_u32 v143, v144, 16, 1
	v_bfe_u32 v93, v145, 16, 1
	v_add3_u32 v143, v144, v143, s33
	v_pk_fma_f32 v[94:95], v[94:95], v[146:147], v[150:151]
	v_add3_u32 v93, v145, v93, s33
	v_lshrrev_b32_e32 v143, 16, v143
	v_and_or_b32 v144, v93, s96, v143
	v_bfe_u32 v93, v95, 16, 1
	v_add3_u32 v93, v95, v93, s33
	v_bfe_u32 v95, v94, 16, 1
	v_add3_u32 v94, v94, v95, s33
	v_lshrrev_b32_e32 v94, 16, v94
	v_and_or_b32 v145, v93, s96, v94
	global_store_dwordx2 v[138:139], v[144:145], off sc1
	v_pk_mul_f32 v[94:95], v[88:89], v[140:141] op_sel_hi:[1,0]
	v_pk_mul_f32 v[148:149], v[90:91], v[140:141] op_sel_hi:[1,0]
	ds_read_b128 v[88:91], v92 offset:1024
	ds_read_b128 v[144:147], v92 offset:17408
	s_waitcnt lgkmcnt(0)
	v_pk_fma_f32 v[88:89], v[94:95], v[88:89], v[144:145]
	s_nop 0
	v_bfe_u32 v93, v89, 16, 1
	v_add3_u32 v89, v89, v93, s33
	v_bfe_u32 v93, v88, 16, 1
	v_add3_u32 v88, v88, v93, s33
	v_pk_fma_f32 v[90:91], v[148:149], v[90:91], v[146:147]
	v_lshrrev_b32_e32 v88, 16, v88
	v_and_or_b32 v88, v89, s96, v88
	v_bfe_u32 v89, v91, 16, 1
	v_add3_u32 v89, v91, v89, s33
	v_bfe_u32 v91, v90, 16, 1
	v_add3_u32 v90, v90, v91, s33
	v_lshrrev_b32_e32 v90, 16, v90
	v_and_or_b32 v89, v89, s96, v90
	global_store_dwordx2 v[138:139], v[88:89], off offset:512 sc1
	v_pk_mul_f32 v[94:95], v[84:85], v[140:141] op_sel_hi:[1,0]
	v_pk_mul_f32 v[144:145], v[86:87], v[140:141] op_sel_hi:[1,0]
	ds_read_b128 v[84:87], v92 offset:2048
	ds_read_b128 v[88:91], v92 offset:18432
	s_waitcnt lgkmcnt(0)
	v_pk_fma_f32 v[84:85], v[94:95], v[84:85], v[88:89]
	s_nop 0
	v_bfe_u32 v88, v85, 16, 1
	v_add3_u32 v85, v85, v88, s33
	v_bfe_u32 v88, v84, 16, 1
	v_add3_u32 v84, v84, v88, s33
	v_pk_fma_f32 v[86:87], v[144:145], v[86:87], v[90:91]
	v_lshrrev_b32_e32 v84, 16, v84
	v_and_or_b32 v84, v85, s96, v84
	v_bfe_u32 v85, v87, 16, 1
	v_add3_u32 v85, v87, v85, s33
	v_bfe_u32 v87, v86, 16, 1
	v_add3_u32 v86, v86, v87, s33
	v_lshrrev_b32_e32 v86, 16, v86
	v_and_or_b32 v85, v85, s96, v86
	global_store_dwordx2 v[138:139], v[84:85], off offset:1024 sc1
	v_pk_mul_f32 v[88:89], v[80:81], v[140:141] op_sel_hi:[1,0]
	v_pk_mul_f32 v[90:91], v[82:83], v[140:141] op_sel_hi:[1,0]
	ds_read_b128 v[80:83], v92 offset:3072
	ds_read_b128 v[84:87], v92 offset:19456
	s_waitcnt lgkmcnt(0)
	v_pk_fma_f32 v[80:81], v[88:89], v[80:81], v[84:85]
	s_nop 0
	v_bfe_u32 v84, v81, 16, 1
	v_add3_u32 v81, v81, v84, s33
	v_bfe_u32 v84, v80, 16, 1
	v_add3_u32 v80, v80, v84, s33
	v_pk_fma_f32 v[82:83], v[90:91], v[82:83], v[86:87]
	v_lshrrev_b32_e32 v80, 16, v80
	v_and_or_b32 v80, v81, s96, v80
	v_bfe_u32 v81, v83, 16, 1
	v_add3_u32 v81, v83, v81, s33
	v_bfe_u32 v83, v82, 16, 1
	v_add3_u32 v82, v82, v83, s33
	v_lshrrev_b32_e32 v82, 16, v82
	v_and_or_b32 v81, v81, s96, v82
	global_store_dwordx2 v[138:139], v[80:81], off offset:1536 sc1
	v_pk_mul_f32 v[84:85], v[76:77], v[140:141] op_sel_hi:[1,0]
	v_pk_mul_f32 v[86:87], v[78:79], v[140:141] op_sel_hi:[1,0]
	ds_read_b128 v[76:79], v92 offset:4096
	ds_read_b128 v[80:83], v92 offset:20480
	s_waitcnt lgkmcnt(0)
	v_pk_fma_f32 v[76:77], v[84:85], v[76:77], v[80:81]
	s_nop 0
	v_bfe_u32 v80, v77, 16, 1
	v_add3_u32 v77, v77, v80, s33
	v_bfe_u32 v80, v76, 16, 1
	v_add3_u32 v76, v76, v80, s33
	v_pk_fma_f32 v[78:79], v[86:87], v[78:79], v[82:83]
	v_lshrrev_b32_e32 v76, 16, v76
	v_and_or_b32 v76, v77, s96, v76
	v_bfe_u32 v77, v79, 16, 1
	v_add3_u32 v77, v79, v77, s33
	v_bfe_u32 v79, v78, 16, 1
	v_add3_u32 v78, v78, v79, s33
	v_lshrrev_b32_e32 v78, 16, v78
	v_and_or_b32 v77, v77, s96, v78
	global_store_dwordx2 v[138:139], v[76:77], off offset:2048 sc1
	v_pk_mul_f32 v[80:81], v[72:73], v[140:141] op_sel_hi:[1,0]
	v_pk_mul_f32 v[82:83], v[74:75], v[140:141] op_sel_hi:[1,0]
	ds_read_b128 v[72:75], v92 offset:5120
	ds_read_b128 v[76:79], v92 offset:21504
	s_waitcnt lgkmcnt(0)
	v_pk_fma_f32 v[72:73], v[80:81], v[72:73], v[76:77]
	s_nop 0
	v_bfe_u32 v76, v73, 16, 1
	v_add3_u32 v73, v73, v76, s33
	v_bfe_u32 v76, v72, 16, 1
	v_add3_u32 v72, v72, v76, s33
	v_pk_fma_f32 v[74:75], v[82:83], v[74:75], v[78:79]
	v_lshrrev_b32_e32 v72, 16, v72
	v_and_or_b32 v72, v73, s96, v72
	v_bfe_u32 v73, v75, 16, 1
	v_add3_u32 v73, v75, v73, s33
	v_bfe_u32 v75, v74, 16, 1
	v_add3_u32 v74, v74, v75, s33
	v_lshrrev_b32_e32 v74, 16, v74
	v_and_or_b32 v73, v73, s96, v74
	global_store_dwordx2 v[138:139], v[72:73], off offset:2560 sc1
	v_pk_mul_f32 v[76:77], v[68:69], v[140:141] op_sel_hi:[1,0]
	v_pk_mul_f32 v[78:79], v[70:71], v[140:141] op_sel_hi:[1,0]
	ds_read_b128 v[68:71], v92 offset:6144
	ds_read_b128 v[72:75], v92 offset:22528
	s_waitcnt lgkmcnt(0)
	v_pk_fma_f32 v[68:69], v[76:77], v[68:69], v[72:73]
	s_nop 0
	v_bfe_u32 v72, v69, 16, 1
	v_add3_u32 v69, v69, v72, s33
	v_bfe_u32 v72, v68, 16, 1
	v_add3_u32 v68, v68, v72, s33
	v_pk_fma_f32 v[70:71], v[78:79], v[70:71], v[74:75]
	v_lshrrev_b32_e32 v68, 16, v68
	v_and_or_b32 v68, v69, s96, v68
	v_bfe_u32 v69, v71, 16, 1
	v_add3_u32 v69, v71, v69, s33
	v_bfe_u32 v71, v70, 16, 1
	v_add3_u32 v70, v70, v71, s33
	v_lshrrev_b32_e32 v70, 16, v70
	v_and_or_b32 v69, v69, s96, v70
	global_store_dwordx2 v[138:139], v[68:69], off offset:3072 sc1
	v_pk_mul_f32 v[72:73], v[64:65], v[140:141] op_sel_hi:[1,0]
	v_pk_mul_f32 v[74:75], v[66:67], v[140:141] op_sel_hi:[1,0]
	ds_read_b128 v[64:67], v92 offset:7168
	ds_read_b128 v[68:71], v92 offset:23552
	s_waitcnt lgkmcnt(0)
	v_pk_fma_f32 v[64:65], v[72:73], v[64:65], v[68:69]
	s_nop 0
	v_bfe_u32 v68, v65, 16, 1
	v_add3_u32 v65, v65, v68, s33
	v_bfe_u32 v68, v64, 16, 1
	v_add3_u32 v64, v64, v68, s33
	v_pk_fma_f32 v[66:67], v[74:75], v[66:67], v[70:71]
	v_lshrrev_b32_e32 v64, 16, v64
	v_and_or_b32 v64, v65, s96, v64
	v_bfe_u32 v65, v67, 16, 1
	v_add3_u32 v65, v67, v65, s33
	v_bfe_u32 v67, v66, 16, 1
	v_add3_u32 v66, v66, v67, s33
	v_lshrrev_b32_e32 v66, 16, v66
	v_and_or_b32 v65, v65, s96, v66
	global_store_dwordx2 v[138:139], v[64:65], off offset:3584 sc1

.LBB0_273:
	s_andn2_b64 vcc, exec, s[12:13]
	s_cbranch_vccnz .LBB0_275
	v_lshl_add_u64 v[122:123], s[30:31], 2, v[100:101]
	global_store_dwordx4 v[122:123], v[92:95], off sc1
	global_store_dwordx4 v[122:123], v[88:91], off offset:1024 sc1
	global_store_dwordx4 v[122:123], v[84:87], off offset:2048 sc1
	global_store_dwordx4 v[122:123], v[80:83], off offset:3072 sc1
	v_add_co_u32_e32 v122, vcc, 0x1000, v122
	s_nop 1
	v_addc_co_u32_e32 v123, vcc, 0, v123, vcc
	global_store_dwordx4 v[122:123], v[76:79], off sc1
	global_store_dwordx4 v[122:123], v[72:75], off offset:1024 sc1
	global_store_dwordx4 v[122:123], v[68:71], off offset:2048 sc1
	global_store_dwordx4 v[122:123], v[64:67], off offset:3072 sc1
.LBB0_275:
	v_mul_f32_e32 v122, v93, v93
	v_mul_f32_e32 v123, v95, v95
	v_fmac_f32_e32 v122, v92, v92
	v_fmac_f32_e32 v123, v94, v94
	v_add_f32_e32 v122, v122, v123
	v_mul_f32_e32 v123, v89, v89
	v_mul_f32_e32 v124, v91, v91
	v_fmac_f32_e32 v123, v88, v88
	v_fmac_f32_e32 v124, v90, v90
	v_add_f32_e32 v123, v123, v124
	v_add_f32_e32 v122, v122, v123
	v_mul_f32_e32 v123, v85, v85
	v_mul_f32_e32 v124, v87, v87
	v_fmac_f32_e32 v123, v84, v84
	v_fmac_f32_e32 v124, v86, v86
	v_add_f32_e32 v123, v123, v124
	v_add_f32_e32 v122, v123, v122
	v_mul_f32_e32 v123, v81, v81
	v_mul_f32_e32 v124, v83, v83
	v_fmac_f32_e32 v123, v80, v80
	v_fmac_f32_e32 v124, v82, v82
	v_add_f32_e32 v123, v123, v124
	v_add_f32_e32 v122, v123, v122
	v_mul_f32_e32 v123, v77, v77
	v_mul_f32_e32 v124, v79, v79
	v_fmac_f32_e32 v123, v76, v76
	v_fmac_f32_e32 v124, v78, v78
	v_add_f32_e32 v123, v123, v124
	v_add_f32_e32 v122, v123, v122
	v_mul_f32_e32 v123, v73, v73
	v_mul_f32_e32 v124, v75, v75
	v_fmac_f32_e32 v123, v72, v72
	v_fmac_f32_e32 v124, v74, v74
	v_add_f32_e32 v123, v123, v124
	v_add_f32_e32 v122, v123, v122
	v_mul_f32_e32 v123, v69, v69
	v_mul_f32_e32 v124, v71, v71
	v_fmac_f32_e32 v123, v68, v68
	v_fmac_f32_e32 v124, v70, v70
	v_add_f32_e32 v123, v123, v124
	v_add_f32_e32 v122, v123, v122
	v_mul_f32_e32 v123, v65, v65
	v_mul_f32_e32 v124, v67, v67
	v_fmac_f32_e32 v123, v64, v64
	v_fmac_f32_e32 v124, v66, v66
	v_add_f32_e32 v123, v123, v124
	v_add_f32_e32 v122, v123, v122
	s_andn2_b64 vcc, exec, s[12:13]
	s_nop 0
	v_add_f32_dpp v122, v122, v122 quad_perm:[1,0,3,2] row_mask:0xf bank_mask:0xf bound_ctrl:1
	s_nop 1
	v_add_f32_dpp v122, v122, v122 quad_perm:[2,3,0,1] row_mask:0xf bank_mask:0xf bound_ctrl:1
	s_nop 1
	v_add_f32_dpp v122, v122, v122 row_half_mirror row_mask:0xf bank_mask:0xf bound_ctrl:1
	s_nop 1
	v_add_f32_dpp v122, v122, v122 row_mirror row_mask:0xf bank_mask:0xf bound_ctrl:1
	ds_swizzle_b32 v123, v122 offset:swizzle(SWAP,16)
	s_waitcnt lgkmcnt(0)
	v_add_f32_e32 v122, v122, v123
	v_mov_b32_e32 v123, v122
	s_nop 1
	v_permlane32_swap_b32_e32 v122, v123
	s_cbranch_vccnz .LBB0_277
	v_add_f32_e32 v122, v122, v123
	v_fmamk_f32 v122, v122, 0x3a000000, v212
	s_mov_b32 s4, 0xf800000
	v_cmp_gt_f32_e32 vcc, s4, v122
	v_mul_f32_e32 v123, 0x4f800000, v122
	s_and_b64 s[12:13], s[18:19], exec
	v_cndmask_b32_e32 v122, v122, v123, vcc
	v_sqrt_f32_e32 v123, v122
	s_cselect_b32 s1, 0x2000, 0
	v_add_u32_e32 v124, -1, v123
	v_fma_f32 v125, -v124, v123, v122
	v_cmp_ge_f32_e64 s[36:37], 0, v125
	v_add_u32_e32 v125, 1, v123
	s_nop 0
	v_cndmask_b32_e64 v124, v123, v124, s[36:37]
	v_fma_f32 v123, -v125, v123, v122
	v_cmp_lt_f32_e64 s[36:37], 0, v123
	s_nop 1
	v_cndmask_b32_e64 v123, v124, v125, s[36:37]
	v_mul_f32_e32 v124, 0x37800000, v123
	v_cndmask_b32_e32 v123, v123, v124, vcc
	v_cmp_class_f32_e32 vcc, v122, v213
	s_nop 1
	v_cndmask_b32_e32 v122, v123, v122, vcc
	v_div_scale_f32 v123, s[12:13], v122, v122, 1.0
	v_rcp_f32_e32 v124, v123
	s_nop 0
	v_fma_f32 v125, -v123, v124, 1.0
	v_fmac_f32_e32 v124, v125, v124
	v_div_scale_f32 v125, vcc, 1.0, v122, 1.0
	v_mul_f32_e32 v126, v125, v124
	v_fma_f32 v127, -v123, v126, v125
	v_fmac_f32_e32 v126, v127, v124
	v_fma_f32 v123, -v123, v126, v125
	v_div_fmas_f32 v123, v123, v124, v126
	v_div_fixup_f32 v124, v123, v122, 1.0
	v_pk_mul_f32 v[134:135], v[92:93], v[124:125] op_sel_hi:[1,0]
	v_add_u32_e32 v92, s1, v142
	ds_read_b128 v[126:129], v92
	ds_read_b128 v[130:133], v92 offset:16384
	v_pk_mul_f32 v[94:95], v[94:95], v[124:125] op_sel_hi:[1,0]
	v_lshl_add_u64 v[122:123], v[104:105], 0, s[14:15]
	s_waitcnt lgkmcnt(0)
	v_pk_fma_f32 v[126:127], v[134:135], v[126:127], v[130:131]
	s_nop 0
	v_bfe_u32 v125, v126, 16, 1
	v_bfe_u32 v93, v127, 16, 1
	v_add3_u32 v125, v126, v125, s33
	v_pk_fma_f32 v[94:95], v[94:95], v[128:129], v[132:133]
	v_add3_u32 v93, v127, v93, s33
	v_lshrrev_b32_e32 v125, 16, v125
	v_and_or_b32 v126, v93, s96, v125
	v_bfe_u32 v93, v95, 16, 1
	v_add3_u32 v93, v95, v93, s33
	v_bfe_u32 v95, v94, 16, 1
	v_add3_u32 v94, v94, v95, s33
	v_lshrrev_b32_e32 v94, 16, v94
	v_and_or_b32 v127, v93, s96, v94
	global_store_dwordx2 v[122:123], v[126:127], off sc1
	v_pk_mul_f32 v[94:95], v[88:89], v[124:125] op_sel_hi:[1,0]
	v_pk_mul_f32 v[130:131], v[90:91], v[124:125] op_sel_hi:[1,0]
	ds_read_b128 v[88:91], v92 offset:1024
	ds_read_b128 v[126:129], v92 offset:17408
	s_waitcnt lgkmcnt(0)
	v_pk_fma_f32 v[88:89], v[94:95], v[88:89], v[126:127]
	s_nop 0
	v_bfe_u32 v93, v89, 16, 1
	v_add3_u32 v89, v89, v93, s33
	v_bfe_u32 v93, v88, 16, 1
	v_add3_u32 v88, v88, v93, s33
	v_pk_fma_f32 v[90:91], v[130:131], v[90:91], v[128:129]
	v_lshrrev_b32_e32 v88, 16, v88
	v_and_or_b32 v88, v89, s96, v88
	v_bfe_u32 v89, v91, 16, 1
	v_add3_u32 v89, v91, v89, s33
	v_bfe_u32 v91, v90, 16, 1
	v_add3_u32 v90, v90, v91, s33
	v_lshrrev_b32_e32 v90, 16, v90
	v_and_or_b32 v89, v89, s96, v90
	global_store_dwordx2 v[122:123], v[88:89], off offset:512 sc1
	v_pk_mul_f32 v[94:95], v[84:85], v[124:125] op_sel_hi:[1,0]
	v_pk_mul_f32 v[126:127], v[86:87], v[124:125] op_sel_hi:[1,0]
	ds_read_b128 v[84:87], v92 offset:2048
	ds_read_b128 v[88:91], v92 offset:18432
	s_waitcnt lgkmcnt(0)
	v_pk_fma_f32 v[84:85], v[94:95], v[84:85], v[88:89]
	s_nop 0
	v_bfe_u32 v88, v85, 16, 1
	v_add3_u32 v85, v85, v88, s33
	v_bfe_u32 v88, v84, 16, 1
	v_add3_u32 v84, v84, v88, s33
	v_pk_fma_f32 v[86:87], v[126:127], v[86:87], v[90:91]
	v_lshrrev_b32_e32 v84, 16, v84
	v_and_or_b32 v84, v85, s96, v84
	v_bfe_u32 v85, v87, 16, 1
	v_add3_u32 v85, v87, v85, s33
	v_bfe_u32 v87, v86, 16, 1
	v_add3_u32 v86, v86, v87, s33
	v_lshrrev_b32_e32 v86, 16, v86
	v_and_or_b32 v85, v85, s96, v86
	global_store_dwordx2 v[122:123], v[84:85], off offset:1024 sc1
	v_pk_mul_f32 v[88:89], v[80:81], v[124:125] op_sel_hi:[1,0]
	v_pk_mul_f32 v[90:91], v[82:83], v[124:125] op_sel_hi:[1,0]
	ds_read_b128 v[80:83], v92 offset:3072
	ds_read_b128 v[84:87], v92 offset:19456
	s_waitcnt lgkmcnt(0)
	v_pk_fma_f32 v[80:81], v[88:89], v[80:81], v[84:85]
	s_nop 0
	v_bfe_u32 v84, v81, 16, 1
	v_add3_u32 v81, v81, v84, s33
	v_bfe_u32 v84, v80, 16, 1
	v_add3_u32 v80, v80, v84, s33
	v_pk_fma_f32 v[82:83], v[90:91], v[82:83], v[86:87]
	v_lshrrev_b32_e32 v80, 16, v80
	v_and_or_b32 v80, v81, s96, v80
	v_bfe_u32 v81, v83, 16, 1
	v_add3_u32 v81, v83, v81, s33
	v_bfe_u32 v83, v82, 16, 1
	v_add3_u32 v82, v82, v83, s33
	v_lshrrev_b32_e32 v82, 16, v82
	v_and_or_b32 v81, v81, s96, v82
	global_store_dwordx2 v[122:123], v[80:81], off offset:1536 sc1
	v_pk_mul_f32 v[84:85], v[76:77], v[124:125] op_sel_hi:[1,0]
	v_pk_mul_f32 v[86:87], v[78:79], v[124:125] op_sel_hi:[1,0]
	ds_read_b128 v[76:79], v92 offset:4096
	ds_read_b128 v[80:83], v92 offset:20480
	s_waitcnt lgkmcnt(0)
	v_pk_fma_f32 v[76:77], v[84:85], v[76:77], v[80:81]
	s_nop 0
	v_bfe_u32 v80, v77, 16, 1
	v_add3_u32 v77, v77, v80, s33
	v_bfe_u32 v80, v76, 16, 1
	v_add3_u32 v76, v76, v80, s33
	v_pk_fma_f32 v[78:79], v[86:87], v[78:79], v[82:83]
	v_lshrrev_b32_e32 v76, 16, v76
	v_and_or_b32 v76, v77, s96, v76
	v_bfe_u32 v77, v79, 16, 1
	v_add3_u32 v77, v79, v77, s33
	v_bfe_u32 v79, v78, 16, 1
	v_add3_u32 v78, v78, v79, s33
	v_lshrrev_b32_e32 v78, 16, v78
	v_and_or_b32 v77, v77, s96, v78
	global_store_dwordx2 v[122:123], v[76:77], off offset:2048 sc1
	v_pk_mul_f32 v[80:81], v[72:73], v[124:125] op_sel_hi:[1,0]
	v_pk_mul_f32 v[82:83], v[74:75], v[124:125] op_sel_hi:[1,0]
	ds_read_b128 v[72:75], v92 offset:5120
	ds_read_b128 v[76:79], v92 offset:21504
	s_waitcnt lgkmcnt(0)
	v_pk_fma_f32 v[72:73], v[80:81], v[72:73], v[76:77]
	s_nop 0
	v_bfe_u32 v76, v73, 16, 1
	v_add3_u32 v73, v73, v76, s33
	v_bfe_u32 v76, v72, 16, 1
	v_add3_u32 v72, v72, v76, s33
	v_pk_fma_f32 v[74:75], v[82:83], v[74:75], v[78:79]
	v_lshrrev_b32_e32 v72, 16, v72
	v_and_or_b32 v72, v73, s96, v72
	v_bfe_u32 v73, v75, 16, 1
	v_add3_u32 v73, v75, v73, s33
	v_bfe_u32 v75, v74, 16, 1
	v_add3_u32 v74, v74, v75, s33
	v_lshrrev_b32_e32 v74, 16, v74
	v_and_or_b32 v73, v73, s96, v74
	global_store_dwordx2 v[122:123], v[72:73], off offset:2560 sc1
	v_pk_mul_f32 v[76:77], v[68:69], v[124:125] op_sel_hi:[1,0]
	v_pk_mul_f32 v[78:79], v[70:71], v[124:125] op_sel_hi:[1,0]
	ds_read_b128 v[68:71], v92 offset:6144
	ds_read_b128 v[72:75], v92 offset:22528
	s_waitcnt lgkmcnt(0)
	v_pk_fma_f32 v[68:69], v[76:77], v[68:69], v[72:73]
	s_nop 0
	v_bfe_u32 v72, v69, 16, 1
	v_add3_u32 v69, v69, v72, s33
	v_bfe_u32 v72, v68, 16, 1
	v_add3_u32 v68, v68, v72, s33
	v_pk_fma_f32 v[70:71], v[78:79], v[70:71], v[74:75]
	v_lshrrev_b32_e32 v68, 16, v68
	v_and_or_b32 v68, v69, s96, v68
	v_bfe_u32 v69, v71, 16, 1
	v_add3_u32 v69, v71, v69, s33
	v_bfe_u32 v71, v70, 16, 1
	v_add3_u32 v70, v70, v71, s33
	v_lshrrev_b32_e32 v70, 16, v70
	v_and_or_b32 v69, v69, s96, v70
	global_store_dwordx2 v[122:123], v[68:69], off offset:3072 sc1
	v_pk_mul_f32 v[72:73], v[64:65], v[124:125] op_sel_hi:[1,0]
	v_pk_mul_f32 v[74:75], v[66:67], v[124:125] op_sel_hi:[1,0]
	ds_read_b128 v[64:67], v92 offset:7168
	ds_read_b128 v[68:71], v92 offset:23552
	s_waitcnt lgkmcnt(0)
	v_pk_fma_f32 v[64:65], v[72:73], v[64:65], v[68:69]
	s_nop 0
	v_bfe_u32 v68, v65, 16, 1
	v_add3_u32 v65, v65, v68, s33
	v_bfe_u32 v68, v64, 16, 1
	v_add3_u32 v64, v64, v68, s33
	v_pk_fma_f32 v[66:67], v[74:75], v[66:67], v[70:71]
	v_lshrrev_b32_e32 v64, 16, v64
	v_and_or_b32 v64, v65, s96, v64
	v_bfe_u32 v65, v67, 16, 1
	v_add3_u32 v65, v67, v65, s33
	v_bfe_u32 v67, v66, 16, 1
	v_add3_u32 v66, v66, v67, s33
	v_lshrrev_b32_e32 v66, 16, v66
	v_and_or_b32 v65, v65, s96, v66
	global_store_dwordx2 v[122:123], v[64:65], off offset:3584 sc1

.LBB0_284:
	s_andn2_b64 vcc, exec, s[6:7]
	s_cbranch_vccnz .LBB0_286
	v_lshl_add_u64 v[106:107], s[10:11], 2, v[100:101]
	global_store_dwordx4 v[106:107], v[92:95], off sc1
	global_store_dwordx4 v[106:107], v[88:91], off offset:1024 sc1
	global_store_dwordx4 v[106:107], v[84:87], off offset:2048 sc1
	global_store_dwordx4 v[106:107], v[80:83], off offset:3072 sc1
	v_add_co_u32_e32 v106, vcc, 0x1000, v106
	s_nop 1
	v_addc_co_u32_e32 v107, vcc, 0, v107, vcc
	global_store_dwordx4 v[106:107], v[76:79], off sc1
	global_store_dwordx4 v[106:107], v[72:75], off offset:1024 sc1
	global_store_dwordx4 v[106:107], v[68:71], off offset:2048 sc1
	global_store_dwordx4 v[106:107], v[64:67], off offset:3072 sc1
.LBB0_286:
	v_mul_f32_e32 v106, v93, v93
	v_mul_f32_e32 v107, v95, v95
	v_fmac_f32_e32 v106, v92, v92
	v_fmac_f32_e32 v107, v94, v94
	v_add_f32_e32 v106, v106, v107
	v_mul_f32_e32 v107, v89, v89
	v_mul_f32_e32 v108, v91, v91
	v_fmac_f32_e32 v107, v88, v88
	v_fmac_f32_e32 v108, v90, v90
	v_add_f32_e32 v107, v107, v108
	v_add_f32_e32 v106, v106, v107
	v_mul_f32_e32 v107, v85, v85
	v_mul_f32_e32 v108, v87, v87
	v_fmac_f32_e32 v107, v84, v84
	v_fmac_f32_e32 v108, v86, v86
	v_add_f32_e32 v107, v107, v108
	v_add_f32_e32 v106, v107, v106
	v_mul_f32_e32 v107, v81, v81
	v_mul_f32_e32 v108, v83, v83
	v_fmac_f32_e32 v107, v80, v80
	v_fmac_f32_e32 v108, v82, v82
	v_add_f32_e32 v107, v107, v108
	v_add_f32_e32 v106, v107, v106
	v_mul_f32_e32 v107, v77, v77
	v_mul_f32_e32 v108, v79, v79
	v_fmac_f32_e32 v107, v76, v76
	v_fmac_f32_e32 v108, v78, v78
	v_add_f32_e32 v107, v107, v108
	v_add_f32_e32 v106, v107, v106
	v_mul_f32_e32 v107, v73, v73
	v_mul_f32_e32 v108, v75, v75
	v_fmac_f32_e32 v107, v72, v72
	v_fmac_f32_e32 v108, v74, v74
	v_add_f32_e32 v107, v107, v108
	v_add_f32_e32 v106, v107, v106
	v_mul_f32_e32 v107, v69, v69
	v_mul_f32_e32 v108, v71, v71
	v_fmac_f32_e32 v107, v68, v68
	v_fmac_f32_e32 v108, v70, v70
	v_add_f32_e32 v107, v107, v108
	v_add_f32_e32 v106, v107, v106
	v_mul_f32_e32 v107, v65, v65
	v_mul_f32_e32 v108, v67, v67
	v_fmac_f32_e32 v107, v64, v64
	v_fmac_f32_e32 v108, v66, v66
	v_add_f32_e32 v107, v107, v108
	v_add_f32_e32 v106, v107, v106
	s_andn2_b64 vcc, exec, s[6:7]
	s_nop 0
	v_add_f32_dpp v106, v106, v106 quad_perm:[1,0,3,2] row_mask:0xf bank_mask:0xf bound_ctrl:1
	s_nop 1
	v_add_f32_dpp v106, v106, v106 quad_perm:[2,3,0,1] row_mask:0xf bank_mask:0xf bound_ctrl:1
	s_nop 1
	v_add_f32_dpp v106, v106, v106 row_half_mirror row_mask:0xf bank_mask:0xf bound_ctrl:1
	s_nop 1
	v_add_f32_dpp v106, v106, v106 row_mirror row_mask:0xf bank_mask:0xf bound_ctrl:1
	ds_swizzle_b32 v107, v106 offset:swizzle(SWAP,16)
	s_waitcnt lgkmcnt(0)
	v_add_f32_e32 v106, v106, v107
	v_mov_b32_e32 v107, v106
	s_nop 1
	v_permlane32_swap_b32_e32 v106, v107
	s_cbranch_vccnz .LBB0_256
	v_add_f32_e32 v106, v106, v107
	v_fmamk_f32 v106, v106, 0x3a000000, v212
	s_mov_b32 s4, 0xf800000
	v_cmp_gt_f32_e32 vcc, s4, v106
	v_mul_f32_e32 v107, 0x4f800000, v106
	s_and_b64 s[6:7], exec, s[12:13]
	v_cndmask_b32_e32 v106, v106, v107, vcc
	v_sqrt_f32_e32 v107, v106
	s_cselect_b32 s1, 0x2000, 0
	v_add_u32_e32 v108, -1, v107
	v_fma_f32 v109, -v108, v107, v106
	v_cmp_ge_f32_e64 s[36:37], 0, v109
	v_add_u32_e32 v109, 1, v107
	s_nop 0
	v_cndmask_b32_e64 v108, v107, v108, s[36:37]
	v_fma_f32 v107, -v109, v107, v106
	v_cmp_lt_f32_e64 s[36:37], 0, v107
	s_nop 1
	v_cndmask_b32_e64 v107, v108, v109, s[36:37]
	v_mul_f32_e32 v108, 0x37800000, v107
	v_cndmask_b32_e32 v107, v107, v108, vcc
	v_cmp_class_f32_e32 vcc, v106, v213
	s_nop 1
	v_cndmask_b32_e32 v106, v107, v106, vcc
	v_div_scale_f32 v107, s[6:7], v106, v106, 1.0
	v_rcp_f32_e32 v108, v107
	s_nop 0
	v_fma_f32 v109, -v107, v108, 1.0
	v_fmac_f32_e32 v108, v109, v108
	v_div_scale_f32 v109, vcc, 1.0, v106, 1.0
	v_mul_f32_e32 v110, v109, v108
	v_fma_f32 v111, -v107, v110, v109
	v_fmac_f32_e32 v110, v111, v108
	v_fma_f32 v107, -v107, v110, v109
	v_div_fmas_f32 v107, v107, v108, v110
	v_div_fixup_f32 v108, v107, v106, 1.0
	v_pk_mul_f32 v[118:119], v[92:93], v[108:109] op_sel_hi:[1,0]
	v_add_u32_e32 v92, s1, v142
	ds_read_b128 v[110:113], v92
	ds_read_b128 v[114:117], v92 offset:16384
	v_pk_mul_f32 v[94:95], v[94:95], v[108:109] op_sel_hi:[1,0]
	v_lshl_add_u64 v[106:107], v[104:105], 0, s[8:9]
	s_waitcnt lgkmcnt(0)
	v_pk_fma_f32 v[110:111], v[118:119], v[110:111], v[114:115]
	s_nop 0
	v_bfe_u32 v109, v110, 16, 1
	v_bfe_u32 v93, v111, 16, 1
	v_add3_u32 v109, v110, v109, s33
	v_pk_fma_f32 v[94:95], v[94:95], v[112:113], v[116:117]
	v_add3_u32 v93, v111, v93, s33
	v_lshrrev_b32_e32 v109, 16, v109
	v_and_or_b32 v110, v93, s96, v109
	v_bfe_u32 v93, v95, 16, 1
	v_add3_u32 v93, v95, v93, s33
	v_bfe_u32 v95, v94, 16, 1
	v_add3_u32 v94, v94, v95, s33
	v_lshrrev_b32_e32 v94, 16, v94
	v_and_or_b32 v111, v93, s96, v94
	global_store_dwordx2 v[106:107], v[110:111], off sc1
	v_pk_mul_f32 v[94:95], v[88:89], v[108:109] op_sel_hi:[1,0]
	v_pk_mul_f32 v[114:115], v[90:91], v[108:109] op_sel_hi:[1,0]
	ds_read_b128 v[88:91], v92 offset:1024
	ds_read_b128 v[110:113], v92 offset:17408
	s_waitcnt lgkmcnt(0)
	v_pk_fma_f32 v[88:89], v[94:95], v[88:89], v[110:111]
	s_nop 0
	v_bfe_u32 v93, v89, 16, 1
	v_add3_u32 v89, v89, v93, s33
	v_bfe_u32 v93, v88, 16, 1
	v_add3_u32 v88, v88, v93, s33
	v_pk_fma_f32 v[90:91], v[114:115], v[90:91], v[112:113]
	v_lshrrev_b32_e32 v88, 16, v88
	v_and_or_b32 v88, v89, s96, v88
	v_bfe_u32 v89, v91, 16, 1
	v_add3_u32 v89, v91, v89, s33
	v_bfe_u32 v91, v90, 16, 1
	v_add3_u32 v90, v90, v91, s33
	v_lshrrev_b32_e32 v90, 16, v90
	v_and_or_b32 v89, v89, s96, v90
	global_store_dwordx2 v[106:107], v[88:89], off offset:512 sc1
	v_pk_mul_f32 v[94:95], v[84:85], v[108:109] op_sel_hi:[1,0]
	v_pk_mul_f32 v[110:111], v[86:87], v[108:109] op_sel_hi:[1,0]
	ds_read_b128 v[84:87], v92 offset:2048
	ds_read_b128 v[88:91], v92 offset:18432
	s_waitcnt lgkmcnt(0)
	v_pk_fma_f32 v[84:85], v[94:95], v[84:85], v[88:89]
	s_nop 0
	v_bfe_u32 v88, v85, 16, 1
	v_add3_u32 v85, v85, v88, s33
	v_bfe_u32 v88, v84, 16, 1
	v_add3_u32 v84, v84, v88, s33
	v_pk_fma_f32 v[86:87], v[110:111], v[86:87], v[90:91]
	v_lshrrev_b32_e32 v84, 16, v84
	v_and_or_b32 v84, v85, s96, v84
	v_bfe_u32 v85, v87, 16, 1
	v_add3_u32 v85, v87, v85, s33
	v_bfe_u32 v87, v86, 16, 1
	v_add3_u32 v86, v86, v87, s33
	v_lshrrev_b32_e32 v86, 16, v86
	v_and_or_b32 v85, v85, s96, v86
	global_store_dwordx2 v[106:107], v[84:85], off offset:1024 sc1
	v_pk_mul_f32 v[88:89], v[80:81], v[108:109] op_sel_hi:[1,0]
	v_pk_mul_f32 v[90:91], v[82:83], v[108:109] op_sel_hi:[1,0]
	ds_read_b128 v[80:83], v92 offset:3072
	ds_read_b128 v[84:87], v92 offset:19456
	s_waitcnt lgkmcnt(0)
	v_pk_fma_f32 v[80:81], v[88:89], v[80:81], v[84:85]
	s_nop 0
	v_bfe_u32 v84, v81, 16, 1
	v_add3_u32 v81, v81, v84, s33
	v_bfe_u32 v84, v80, 16, 1
	v_add3_u32 v80, v80, v84, s33
	v_pk_fma_f32 v[82:83], v[90:91], v[82:83], v[86:87]
	v_lshrrev_b32_e32 v80, 16, v80
	v_and_or_b32 v80, v81, s96, v80
	v_bfe_u32 v81, v83, 16, 1
	v_add3_u32 v81, v83, v81, s33
	v_bfe_u32 v83, v82, 16, 1
	v_add3_u32 v82, v82, v83, s33
	v_lshrrev_b32_e32 v82, 16, v82
	v_and_or_b32 v81, v81, s96, v82
	global_store_dwordx2 v[106:107], v[80:81], off offset:1536 sc1
	v_pk_mul_f32 v[84:85], v[76:77], v[108:109] op_sel_hi:[1,0]
	v_pk_mul_f32 v[86:87], v[78:79], v[108:109] op_sel_hi:[1,0]
	ds_read_b128 v[76:79], v92 offset:4096
	ds_read_b128 v[80:83], v92 offset:20480
	s_waitcnt lgkmcnt(0)
	v_pk_fma_f32 v[76:77], v[84:85], v[76:77], v[80:81]
	s_nop 0
	v_bfe_u32 v80, v77, 16, 1
	v_add3_u32 v77, v77, v80, s33
	v_bfe_u32 v80, v76, 16, 1
	v_add3_u32 v76, v76, v80, s33
	v_pk_fma_f32 v[78:79], v[86:87], v[78:79], v[82:83]
	v_lshrrev_b32_e32 v76, 16, v76
	v_and_or_b32 v76, v77, s96, v76
	v_bfe_u32 v77, v79, 16, 1
	v_add3_u32 v77, v79, v77, s33
	v_bfe_u32 v79, v78, 16, 1
	v_add3_u32 v78, v78, v79, s33
	v_lshrrev_b32_e32 v78, 16, v78
	v_and_or_b32 v77, v77, s96, v78
	global_store_dwordx2 v[106:107], v[76:77], off offset:2048 sc1
	v_pk_mul_f32 v[80:81], v[72:73], v[108:109] op_sel_hi:[1,0]
	v_pk_mul_f32 v[82:83], v[74:75], v[108:109] op_sel_hi:[1,0]
	ds_read_b128 v[72:75], v92 offset:5120
	ds_read_b128 v[76:79], v92 offset:21504
	s_waitcnt lgkmcnt(0)
	v_pk_fma_f32 v[72:73], v[80:81], v[72:73], v[76:77]
	s_nop 0
	v_bfe_u32 v76, v73, 16, 1
	v_add3_u32 v73, v73, v76, s33
	v_bfe_u32 v76, v72, 16, 1
	v_add3_u32 v72, v72, v76, s33
	v_pk_fma_f32 v[74:75], v[82:83], v[74:75], v[78:79]
	v_lshrrev_b32_e32 v72, 16, v72
	v_and_or_b32 v72, v73, s96, v72
	v_bfe_u32 v73, v75, 16, 1
	v_add3_u32 v73, v75, v73, s33
	v_bfe_u32 v75, v74, 16, 1
	v_add3_u32 v74, v74, v75, s33
	v_lshrrev_b32_e32 v74, 16, v74
	v_and_or_b32 v73, v73, s96, v74
	global_store_dwordx2 v[106:107], v[72:73], off offset:2560 sc1
	v_pk_mul_f32 v[76:77], v[68:69], v[108:109] op_sel_hi:[1,0]
	v_pk_mul_f32 v[78:79], v[70:71], v[108:109] op_sel_hi:[1,0]
	ds_read_b128 v[68:71], v92 offset:6144
	ds_read_b128 v[72:75], v92 offset:22528
	s_waitcnt lgkmcnt(0)
	v_pk_fma_f32 v[68:69], v[76:77], v[68:69], v[72:73]
	s_nop 0
	v_bfe_u32 v72, v69, 16, 1
	v_add3_u32 v69, v69, v72, s33
	v_bfe_u32 v72, v68, 16, 1
	v_add3_u32 v68, v68, v72, s33
	v_pk_fma_f32 v[70:71], v[78:79], v[70:71], v[74:75]
	v_lshrrev_b32_e32 v68, 16, v68
	v_and_or_b32 v68, v69, s96, v68
	v_bfe_u32 v69, v71, 16, 1
	v_add3_u32 v69, v71, v69, s33
	v_bfe_u32 v71, v70, 16, 1
	v_add3_u32 v70, v70, v71, s33
	v_lshrrev_b32_e32 v70, 16, v70
	v_and_or_b32 v69, v69, s96, v70
	global_store_dwordx2 v[106:107], v[68:69], off offset:3072 sc1
	v_pk_mul_f32 v[72:73], v[64:65], v[108:109] op_sel_hi:[1,0]
	v_pk_mul_f32 v[74:75], v[66:67], v[108:109] op_sel_hi:[1,0]
	ds_read_b128 v[64:67], v92 offset:7168
	ds_read_b128 v[68:71], v92 offset:23552
	s_waitcnt lgkmcnt(0)
	v_pk_fma_f32 v[64:65], v[72:73], v[64:65], v[68:69]
	s_nop 0
	v_bfe_u32 v68, v65, 16, 1
	v_add3_u32 v65, v65, v68, s33
	v_bfe_u32 v68, v64, 16, 1
	v_add3_u32 v64, v64, v68, s33
	v_pk_fma_f32 v[66:67], v[74:75], v[66:67], v[70:71]
	v_lshrrev_b32_e32 v64, 16, v64
	v_and_or_b32 v64, v65, s96, v64
	v_bfe_u32 v65, v67, 16, 1
	v_add3_u32 v65, v67, v65, s33
	v_bfe_u32 v67, v66, 16, 1
	v_add3_u32 v66, v66, v67, s33
	v_lshrrev_b32_e32 v66, 16, v66
	v_and_or_b32 v65, v65, s96, v66
	global_store_dwordx2 v[106:107], v[64:65], off offset:3584 sc1
	s_branch .LBB0_256

.LBB0_293:
	s_add_i32 s12, s88, s4
	v_readlane_b32 s36, v249, 38
	s_cmpk_lt_i32 s12, 0x4000
	v_readlane_b32 s37, v249, 39
	s_cselect_b32 s13, s12, s4
	s_mov_b64 s[16:17], s[36:37]
	s_ashr_i32 s14, s13, 31
	s_add_i32 s15, s13, 0xffffc000
	v_lshl_add_u64 v[64:65], s[16:17], 0, v[130:131]
	s_cmpk_gt_i32 s13, 0x3fff
	global_load_dwordx4 v[124:127], v[64:65], off
	global_load_dwordx4 v[120:123], v[64:65], off offset:1024
	global_load_dwordx4 v[116:119], v[64:65], off offset:2048
	global_load_dwordx4 v[112:115], v[64:65], off offset:3072
	s_cselect_b64 s[8:9], -1, 0
	s_and_b64 s[10:11], s[8:9], exec
	s_cselect_b32 s11, 0, s14
	s_cselect_b32 s10, s15, s13
	v_readlane_b32 s14, v255, 49
	v_readlane_b32 s15, v255, 50
	s_cselect_b32 s13, s15, s17
	s_cselect_b32 s14, s14, s16
	s_lshl_b64 s[10:11], s[10:11], 13
	s_add_u32 s10, s14, s10
	s_addc_u32 s11, s13, s11
	s_cmpk_gt_i32 s12, 0x3fff
	s_movk_i32 s12, 0x1000
	v_add_co_u32_e32 v64, vcc, s12, v64
	v_readlane_b32 s38, v249, 40
	s_nop 0
	v_addc_co_u32_e32 v65, vcc, 0, v65, vcc
	global_load_dwordx4 v[108:111], v[64:65], off
	global_load_dwordx4 v[104:107], v[64:65], off offset:1024
	global_load_dwordx4 v[100:103], v[64:65], off offset:2048
	global_load_dwordx4 v[96:99], v[64:65], off offset:3072
	v_lshl_add_u64 v[64:65], s[10:11], 0, v[184:185]
	v_add_co_u32_e32 v64, vcc, s12, v64
	global_load_dwordx4 v[92:95], v184, s[10:11]
	global_load_dwordx4 v[88:91], v184, s[10:11] offset:1024
	global_load_dwordx4 v[84:87], v184, s[10:11] offset:2048
	global_load_dwordx4 v[80:83], v184, s[10:11] offset:3072
	v_addc_co_u32_e32 v65, vcc, 0, v65, vcc
	s_mov_b32 s10, 0xf800000
	global_load_dwordx4 v[76:79], v[64:65], off
	global_load_dwordx4 v[72:75], v[64:65], off offset:1024
	global_load_dwordx4 v[68:71], v[64:65], off offset:2048
	s_nop 0
	global_load_dwordx4 v[64:67], v[64:65], off offset:3072
	v_readlane_b32 s39, v249, 41
	v_readlane_b32 s40, v249, 42
	v_readlane_b32 s41, v249, 43
	v_readlane_b32 s42, v249, 44
	v_readlane_b32 s43, v249, 45
	v_readlane_b32 s44, v249, 46
	v_readlane_b32 s45, v249, 47
	v_readlane_b32 s46, v249, 48
	v_readlane_b32 s47, v249, 49
	v_readlane_b32 s48, v249, 50
	v_readlane_b32 s49, v249, 51
	v_readlane_b32 s50, v249, 52
	v_readlane_b32 s51, v249, 53
	s_waitcnt vmcnt(15)
	v_mul_f32_e32 v132, v125, v125
	v_mul_f32_e32 v134, v127, v127
	v_fmac_f32_e32 v132, v124, v124
	v_fmac_f32_e32 v134, v126, v126
	v_add_f32_e32 v132, v132, v134
	s_waitcnt vmcnt(14)
	v_mul_f32_e32 v134, v121, v121
	v_mul_f32_e32 v135, v123, v123
	v_fmac_f32_e32 v134, v120, v120
	v_fmac_f32_e32 v135, v122, v122
	v_add_f32_e32 v134, v134, v135
	v_add_f32_e32 v132, v132, v134
	s_waitcnt vmcnt(13)
	v_mul_f32_e32 v134, v117, v117
	v_mul_f32_e32 v135, v119, v119
	v_fmac_f32_e32 v134, v116, v116
	v_fmac_f32_e32 v135, v118, v118
	v_add_f32_e32 v134, v134, v135
	v_add_f32_e32 v132, v132, v134
	s_waitcnt vmcnt(12)
	v_mul_f32_e32 v134, v113, v113
	v_mul_f32_e32 v135, v115, v115
	v_fmac_f32_e32 v134, v112, v112
	v_fmac_f32_e32 v135, v114, v114
	v_add_f32_e32 v134, v134, v135
	v_add_f32_e32 v132, v132, v134
	s_waitcnt vmcnt(11)
	v_mul_f32_e32 v134, v109, v109
	v_mul_f32_e32 v135, v111, v111
	v_fmac_f32_e32 v134, v108, v108
	v_fmac_f32_e32 v135, v110, v110
	v_add_f32_e32 v134, v134, v135
	v_add_f32_e32 v132, v132, v134
	s_waitcnt vmcnt(10)
	v_mul_f32_e32 v134, v105, v105
	v_mul_f32_e32 v135, v107, v107
	v_fmac_f32_e32 v134, v104, v104
	v_fmac_f32_e32 v135, v106, v106
	v_add_f32_e32 v134, v134, v135
	v_add_f32_e32 v132, v132, v134
	s_waitcnt vmcnt(9)
	v_mul_f32_e32 v134, v101, v101
	v_mul_f32_e32 v135, v103, v103
	v_fmac_f32_e32 v134, v100, v100
	v_fmac_f32_e32 v135, v102, v102
	v_add_f32_e32 v134, v134, v135
	v_add_f32_e32 v132, v132, v134
	s_waitcnt vmcnt(8)
	v_mul_f32_e32 v134, v97, v97
	v_mul_f32_e32 v135, v99, v99
	v_fmac_f32_e32 v134, v96, v96
	v_fmac_f32_e32 v135, v98, v98
	v_add_f32_e32 v134, v134, v135
	v_add_f32_e32 v132, v132, v134
	s_nop 1
	v_add_f32_dpp v132, v132, v132 quad_perm:[1,0,3,2] row_mask:0xf bank_mask:0xf bound_ctrl:1
	s_nop 1
	v_add_f32_dpp v132, v132, v132 quad_perm:[2,3,0,1] row_mask:0xf bank_mask:0xf bound_ctrl:1
	s_nop 1
	v_add_f32_dpp v132, v132, v132 row_half_mirror row_mask:0xf bank_mask:0xf bound_ctrl:1
	s_nop 1
	v_add_f32_dpp v132, v132, v132 row_mirror row_mask:0xf bank_mask:0xf bound_ctrl:1
	ds_swizzle_b32 v134, v132 offset:swizzle(SWAP,16)
	s_waitcnt lgkmcnt(0)
	v_add_f32_e32 v132, v132, v134
	v_mov_b32_e32 v134, v132
	s_nop 1
	v_permlane32_swap_b32_e32 v132, v134
	v_add_f32_e32 v132, v132, v134
	v_fmamk_f32 v132, v132, 0x3a000000, v212
	v_cmp_gt_f32_e32 vcc, s10, v132
	v_mul_f32_e32 v134, 0x4f800000, v132
	s_nop 0
	v_cndmask_b32_e32 v132, v132, v134, vcc
	v_sqrt_f32_e32 v134, v132
	s_nop 0
	v_add_u32_e32 v135, -1, v134
	v_fma_f32 v136, -v135, v134, v132
	v_cmp_ge_f32_e64 s[36:37], 0, v136
	v_add_u32_e32 v136, 1, v134
	s_nop 0
	v_cndmask_b32_e64 v135, v134, v135, s[36:37]
	v_fma_f32 v134, -v136, v134, v132
	v_cmp_lt_f32_e64 s[36:37], 0, v134
	s_nop 1
	v_cndmask_b32_e64 v134, v135, v136, s[36:37]
	v_mul_f32_e32 v135, 0x37800000, v134
	v_cndmask_b32_e32 v134, v134, v135, vcc
	v_cmp_class_f32_e32 vcc, v132, v213
	s_nop 1
	v_cndmask_b32_e32 v132, v134, v132, vcc
	v_div_scale_f32 v134, s[10:11], v132, v132, 1.0
	v_rcp_f32_e32 v135, v134
	s_mov_b32 s10, 0x1b800000
	v_fma_f32 v136, -v134, v135, 1.0
	v_fmac_f32_e32 v135, v136, v135
	v_div_scale_f32 v136, vcc, 1.0, v132, 1.0
	v_mul_f32_e32 v137, v136, v135
	v_fma_f32 v138, -v134, v137, v136
	v_fmac_f32_e32 v137, v138, v135
	v_fma_f32 v134, -v134, v137, v136
	v_div_fmas_f32 v134, v134, v135, v137
	v_div_fixup_f32 v132, v134, v132, 1.0
	v_pk_mul_f32 v[124:125], v[124:125], v[132:133] op_sel_hi:[1,0]
	v_pk_mul_f32 v[126:127], v[126:127], v[132:133] op_sel_hi:[1,0]
	v_pk_fma_f32 v[124:125], v[0:1], v[124:125], v[8:9]
	v_pk_fma_f32 v[126:127], v[2:3], v[126:127], v[10:11]
	v_bfe_u32 v136, v125, 16, 1
	v_add3_u32 v125, v125, v136, s33
	v_bfe_u32 v136, v124, 16, 1
	v_add3_u32 v124, v124, v136, s33
	v_lshrrev_b32_e32 v124, 16, v124
	v_and_or_b32 v124, v125, s96, v124
	v_bfe_u32 v125, v127, 16, 1
	v_add3_u32 v125, v127, v125, s33
	v_bfe_u32 v127, v126, 16, 1
	v_add3_u32 v126, v126, v127, s33
	v_lshl_add_u64 v[134:135], s[6:7], 0, v[128:129]
	v_lshrrev_b32_e32 v126, 16, v126
	v_and_or_b32 v125, v125, s96, v126
	v_add_co_u32_e32 v126, vcc, s10, v134
	v_pk_mul_f32 v[120:121], v[120:121], v[132:133] op_sel_hi:[1,0]
	s_nop 0
	v_addc_co_u32_e32 v127, vcc, 0, v135, vcc
	v_pk_fma_f32 v[120:121], v[4:5], v[120:121], v[12:13]
	global_store_dwordx2 v[126:127], v[124:125], off sc1
	v_bfe_u32 v124, v121, 16, 1
	v_add3_u32 v121, v121, v124, s33
	v_bfe_u32 v124, v120, 16, 1
	v_pk_mul_f32 v[122:123], v[122:123], v[132:133] op_sel_hi:[1,0]
	v_add3_u32 v120, v120, v124, s33
	v_pk_fma_f32 v[122:123], v[6:7], v[122:123], v[14:15]
	v_lshrrev_b32_e32 v120, 16, v120
	v_and_or_b32 v120, v121, s96, v120
	v_bfe_u32 v121, v123, 16, 1
	v_add3_u32 v121, v123, v121, s33
	v_bfe_u32 v123, v122, 16, 1
	v_add3_u32 v122, v122, v123, s33
	v_lshrrev_b32_e32 v122, 16, v122
	v_pk_mul_f32 v[116:117], v[116:117], v[132:133] op_sel_hi:[1,0]
	v_and_or_b32 v121, v121, s96, v122
	v_pk_fma_f32 v[116:117], v[16:17], v[116:117], v[24:25]
	global_store_dwordx2 v[126:127], v[120:121], off offset:512 sc1
	v_bfe_u32 v120, v117, 16, 1
	v_add3_u32 v117, v117, v120, s33
	v_bfe_u32 v120, v116, 16, 1
	v_pk_mul_f32 v[118:119], v[118:119], v[132:133] op_sel_hi:[1,0]
	v_add3_u32 v116, v116, v120, s33
	v_pk_fma_f32 v[118:119], v[18:19], v[118:119], v[26:27]
	v_lshrrev_b32_e32 v116, 16, v116
	v_and_or_b32 v116, v117, s96, v116
	v_bfe_u32 v117, v119, 16, 1
	v_add3_u32 v117, v119, v117, s33
	v_bfe_u32 v119, v118, 16, 1
	v_add3_u32 v118, v118, v119, s33
	v_lshrrev_b32_e32 v118, 16, v118
	v_pk_mul_f32 v[112:113], v[112:113], v[132:133] op_sel_hi:[1,0]
	v_and_or_b32 v117, v117, s96, v118
	v_pk_fma_f32 v[112:113], v[112:113], v[20:21], v[28:29]
	global_store_dwordx2 v[126:127], v[116:117], off offset:1024 sc1
	v_bfe_u32 v116, v113, 16, 1
	v_add3_u32 v113, v113, v116, s33
	v_bfe_u32 v116, v112, 16, 1
	v_pk_mul_f32 v[114:115], v[114:115], v[132:133] op_sel_hi:[1,0]
	v_add3_u32 v112, v112, v116, s33
	v_pk_fma_f32 v[114:115], v[114:115], v[22:23], v[30:31]
	v_lshrrev_b32_e32 v112, 16, v112
	v_and_or_b32 v112, v113, s96, v112
	v_bfe_u32 v113, v115, 16, 1
	v_add3_u32 v113, v115, v113, s33
	v_bfe_u32 v115, v114, 16, 1
	v_add3_u32 v114, v114, v115, s33
	v_lshrrev_b32_e32 v114, 16, v114
	v_pk_mul_f32 v[108:109], v[108:109], v[132:133] op_sel_hi:[1,0]
	v_and_or_b32 v113, v113, s96, v114
	v_pk_fma_f32 v[108:109], v[108:109], v[32:33], v[40:41]
	global_store_dwordx2 v[126:127], v[112:113], off offset:1536 sc1
	v_bfe_u32 v112, v109, 16, 1
	v_add3_u32 v109, v109, v112, s33
	v_bfe_u32 v112, v108, 16, 1
	v_pk_mul_f32 v[110:111], v[110:111], v[132:133] op_sel_hi:[1,0]
	v_add3_u32 v108, v108, v112, s33
	v_pk_fma_f32 v[110:111], v[110:111], v[34:35], v[42:43]
	v_lshrrev_b32_e32 v108, 16, v108
	v_and_or_b32 v108, v109, s96, v108
	v_bfe_u32 v109, v111, 16, 1
	v_add3_u32 v109, v111, v109, s33
	v_bfe_u32 v111, v110, 16, 1
	v_add3_u32 v110, v110, v111, s33
	v_lshrrev_b32_e32 v110, 16, v110
	v_pk_mul_f32 v[104:105], v[104:105], v[132:133] op_sel_hi:[1,0]
	v_and_or_b32 v109, v109, s96, v110
	v_pk_fma_f32 v[104:105], v[104:105], v[36:37], v[44:45]
	global_store_dwordx2 v[126:127], v[108:109], off offset:2048 sc1
	v_bfe_u32 v108, v105, 16, 1
	v_add3_u32 v105, v105, v108, s33
	v_bfe_u32 v108, v104, 16, 1
	v_pk_mul_f32 v[106:107], v[106:107], v[132:133] op_sel_hi:[1,0]
	v_add3_u32 v104, v104, v108, s33
	v_pk_fma_f32 v[106:107], v[106:107], v[38:39], v[46:47]
	v_lshrrev_b32_e32 v104, 16, v104
	v_and_or_b32 v104, v105, s96, v104
	v_bfe_u32 v105, v107, 16, 1
	v_add3_u32 v105, v107, v105, s33
	v_bfe_u32 v107, v106, 16, 1
	v_add3_u32 v106, v106, v107, s33
	v_lshrrev_b32_e32 v106, 16, v106
	v_pk_mul_f32 v[100:101], v[100:101], v[132:133] op_sel_hi:[1,0]
	v_and_or_b32 v105, v105, s96, v106
	v_pk_fma_f32 v[100:101], v[100:101], v[48:49], v[56:57]
	global_store_dwordx2 v[126:127], v[104:105], off offset:2560 sc1
	v_bfe_u32 v104, v101, 16, 1
	v_add3_u32 v101, v101, v104, s33
	v_bfe_u32 v104, v100, 16, 1
	v_pk_mul_f32 v[102:103], v[102:103], v[132:133] op_sel_hi:[1,0]
	v_add3_u32 v100, v100, v104, s33
	v_pk_fma_f32 v[102:103], v[102:103], v[50:51], v[58:59]
	v_lshrrev_b32_e32 v100, 16, v100
	v_and_or_b32 v100, v101, s96, v100
	v_bfe_u32 v101, v103, 16, 1
	v_add3_u32 v101, v103, v101, s33
	v_bfe_u32 v103, v102, 16, 1
	v_add3_u32 v102, v102, v103, s33
	v_lshrrev_b32_e32 v102, 16, v102
	v_pk_mul_f32 v[96:97], v[96:97], v[132:133] op_sel_hi:[1,0]
	v_and_or_b32 v101, v101, s96, v102
	v_pk_fma_f32 v[96:97], v[96:97], v[52:53], v[60:61]
	global_store_dwordx2 v[126:127], v[100:101], off offset:3072 sc1
	v_bfe_u32 v100, v97, 16, 1
	v_add3_u32 v97, v97, v100, s33
	v_bfe_u32 v100, v96, 16, 1
	v_pk_mul_f32 v[98:99], v[98:99], v[132:133] op_sel_hi:[1,0]
	v_add3_u32 v96, v96, v100, s33
	v_pk_fma_f32 v[98:99], v[98:99], v[54:55], v[62:63]
	v_lshrrev_b32_e32 v96, 16, v96
	v_and_or_b32 v96, v97, s96, v96
	v_bfe_u32 v97, v99, 16, 1
	v_add3_u32 v97, v99, v97, s33
	v_bfe_u32 v99, v98, 16, 1
	v_add3_u32 v98, v98, v99, s33
	v_lshrrev_b32_e32 v98, 16, v98
	v_and_or_b32 v97, v97, s96, v98
	global_store_dwordx2 v[126:127], v[96:97], off offset:3584 sc1
	s_waitcnt vmcnt(15)
	v_mul_f32_e32 v96, v93, v93
	v_mul_f32_e32 v97, v95, v95
	v_fmac_f32_e32 v96, v92, v92
	v_fmac_f32_e32 v97, v94, v94
	v_add_f32_e32 v96, v96, v97
	s_waitcnt vmcnt(14)
	v_mul_f32_e32 v97, v89, v89
	v_mul_f32_e32 v98, v91, v91
	v_fmac_f32_e32 v97, v88, v88
	v_fmac_f32_e32 v98, v90, v90
	v_add_f32_e32 v97, v97, v98
	v_add_f32_e32 v96, v96, v97
	s_waitcnt vmcnt(13)
	v_mul_f32_e32 v97, v85, v85
	v_mul_f32_e32 v98, v87, v87
	v_fmac_f32_e32 v97, v84, v84
	v_fmac_f32_e32 v98, v86, v86
	v_add_f32_e32 v97, v97, v98
	v_add_f32_e32 v96, v97, v96
	s_waitcnt vmcnt(12)
	v_mul_f32_e32 v97, v81, v81
	v_mul_f32_e32 v98, v83, v83
	v_fmac_f32_e32 v97, v80, v80
	v_fmac_f32_e32 v98, v82, v82
	v_add_f32_e32 v97, v97, v98
	v_add_f32_e32 v96, v97, v96
	s_waitcnt vmcnt(11)
	v_mul_f32_e32 v97, v77, v77
	v_mul_f32_e32 v98, v79, v79
	v_fmac_f32_e32 v97, v76, v76
	v_fmac_f32_e32 v98, v78, v78
	v_add_f32_e32 v97, v97, v98
	v_add_f32_e32 v96, v97, v96
	s_waitcnt vmcnt(10)
	v_mul_f32_e32 v97, v73, v73
	v_mul_f32_e32 v98, v75, v75
	v_fmac_f32_e32 v97, v72, v72
	v_fmac_f32_e32 v98, v74, v74
	v_add_f32_e32 v97, v97, v98
	v_add_f32_e32 v96, v97, v96
	s_waitcnt vmcnt(9)
	v_mul_f32_e32 v97, v69, v69
	v_mul_f32_e32 v98, v71, v71
	v_fmac_f32_e32 v97, v68, v68
	v_fmac_f32_e32 v98, v70, v70
	v_add_f32_e32 v97, v97, v98
	v_add_f32_e32 v96, v97, v96
	s_waitcnt vmcnt(8)
	v_mul_f32_e32 v97, v65, v65
	v_mul_f32_e32 v98, v67, v67
	v_fmac_f32_e32 v97, v64, v64
	v_fmac_f32_e32 v98, v66, v66
	v_add_f32_e32 v97, v97, v98
	v_add_f32_e32 v96, v97, v96
	s_nop 1
	v_add_f32_dpp v96, v96, v96 quad_perm:[1,0,3,2] row_mask:0xf bank_mask:0xf bound_ctrl:1
	s_nop 1
	v_add_f32_dpp v96, v96, v96 quad_perm:[2,3,0,1] row_mask:0xf bank_mask:0xf bound_ctrl:1
	s_nop 1
	v_add_f32_dpp v96, v96, v96 row_half_mirror row_mask:0xf bank_mask:0xf bound_ctrl:1
	s_nop 1
	v_add_f32_dpp v96, v96, v96 row_mirror row_mask:0xf bank_mask:0xf bound_ctrl:1
	ds_swizzle_b32 v97, v96 offset:swizzle(SWAP,16)
	s_waitcnt lgkmcnt(0)
	v_add_f32_e32 v96, v96, v97
	v_mov_b32_e32 v97, v96
	s_nop 1
	v_permlane32_swap_b32_e32 v96, v97
	s_cbranch_scc1 .LBB0_292
	s_and_b64 s[8:9], s[8:9], exec
	v_add_f32_e32 v96, v96, v97
	v_fmamk_f32 v96, v96, 0x3a000000, v212
	s_mov_b32 s8, 0xf800000
	v_cmp_gt_f32_e32 vcc, s8, v96
	v_mul_f32_e32 v97, 0x4f800000, v96
	s_cselect_b32 s10, 0x2000, 0
	v_cndmask_b32_e32 v96, v96, v97, vcc
	v_sqrt_f32_e32 v97, v96
	v_lshl_add_u64 v[106:107], s[0:1], 0, v[128:129]
	v_add_u32_e32 v98, -1, v97
	v_fma_f32 v99, -v98, v97, v96
	v_cmp_ge_f32_e64 s[36:37], 0, v99
	v_add_u32_e32 v99, 1, v97
	s_nop 0
	v_cndmask_b32_e64 v98, v97, v98, s[36:37]
	v_fma_f32 v97, -v99, v97, v96
	v_cmp_lt_f32_e64 s[36:37], 0, v97
	s_nop 1
	v_cndmask_b32_e64 v97, v98, v99, s[36:37]
	v_mul_f32_e32 v98, 0x37800000, v97
	v_cndmask_b32_e32 v97, v97, v98, vcc
	v_cmp_class_f32_e32 vcc, v96, v213
	s_nop 1
	v_cndmask_b32_e32 v96, v97, v96, vcc
	v_div_scale_f32 v97, s[8:9], v96, v96, 1.0
	v_rcp_f32_e32 v98, v97
	s_mov_b32 s8, 0x1b800000
	v_fma_f32 v99, -v97, v98, 1.0
	v_fmac_f32_e32 v98, v99, v98
	v_div_scale_f32 v99, vcc, 1.0, v96, 1.0
	v_mul_f32_e32 v100, v99, v98
	v_fma_f32 v101, -v97, v100, v99
	v_fmac_f32_e32 v100, v101, v98
	v_fma_f32 v97, -v97, v100, v99
	v_div_fmas_f32 v97, v97, v98, v100
	v_div_fixup_f32 v96, v97, v96, 1.0
	v_pk_mul_f32 v[108:109], v[94:95], v[96:97] op_sel_hi:[1,0]
	v_add_u32_e32 v94, s10, v133
	ds_read_b128 v[98:101], v94
	ds_read_b128 v[102:105], v94 offset:16384
	v_pk_mul_f32 v[92:93], v[92:93], v[96:97] op_sel_hi:[1,0]
	s_waitcnt lgkmcnt(0)
	v_pk_fma_f32 v[100:101], v[108:109], v[100:101], v[104:105]
	v_pk_fma_f32 v[92:93], v[92:93], v[98:99], v[102:103]
	v_pk_mul_f32 v[102:103], v[88:89], v[96:97] op_sel_hi:[1,0]
	v_bfe_u32 v95, v93, 16, 1
	v_add3_u32 v93, v93, v95, s33
	v_bfe_u32 v95, v92, 16, 1
	v_add3_u32 v92, v92, v95, s33
	v_lshrrev_b32_e32 v92, 16, v92
	v_and_or_b32 v98, v93, s96, v92
	v_bfe_u32 v93, v100, 16, 1
	v_bfe_u32 v92, v101, 16, 1
	v_add3_u32 v93, v100, v93, s33
	v_add3_u32 v92, v101, v92, s33
	v_lshrrev_b32_e32 v93, 16, v93
	v_and_or_b32 v99, v92, s96, v93
	v_add_co_u32_e32 v92, vcc, s8, v106
	v_pk_mul_f32 v[104:105], v[90:91], v[96:97] op_sel_hi:[1,0]
	s_nop 0
	v_addc_co_u32_e32 v93, vcc, 0, v107, vcc
	global_store_dwordx2 v[92:93], v[98:99], off sc1
	ds_read_b128 v[88:91], v94 offset:1024
	ds_read_b128 v[98:101], v94 offset:17408
	s_waitcnt lgkmcnt(0)
	v_pk_fma_f32 v[88:89], v[102:103], v[88:89], v[98:99]
	s_nop 0
	v_bfe_u32 v95, v89, 16, 1
	v_add3_u32 v89, v89, v95, s33
	v_bfe_u32 v95, v88, 16, 1
	v_add3_u32 v88, v88, v95, s33
	v_pk_fma_f32 v[90:91], v[104:105], v[90:91], v[100:101]
	v_lshrrev_b32_e32 v88, 16, v88
	v_and_or_b32 v88, v89, s96, v88
	v_bfe_u32 v89, v91, 16, 1
	v_add3_u32 v89, v91, v89, s33
	v_bfe_u32 v91, v90, 16, 1
	v_add3_u32 v90, v90, v91, s33
	v_lshrrev_b32_e32 v90, 16, v90
	v_and_or_b32 v89, v89, s96, v90
	global_store_dwordx2 v[92:93], v[88:89], off offset:512 sc1
	v_pk_mul_f32 v[98:99], v[84:85], v[96:97] op_sel_hi:[1,0]
	v_pk_mul_f32 v[100:101], v[86:87], v[96:97] op_sel_hi:[1,0]
	ds_read_b128 v[84:87], v94 offset:2048
	ds_read_b128 v[88:91], v94 offset:18432
	s_waitcnt lgkmcnt(0)
	v_pk_fma_f32 v[84:85], v[98:99], v[84:85], v[88:89]
	s_nop 0
	v_bfe_u32 v88, v85, 16, 1
	v_add3_u32 v85, v85, v88, s33
	v_bfe_u32 v88, v84, 16, 1
	v_add3_u32 v84, v84, v88, s33
	v_pk_fma_f32 v[86:87], v[100:101], v[86:87], v[90:91]
	v_lshrrev_b32_e32 v84, 16, v84
	v_and_or_b32 v84, v85, s96, v84
	v_bfe_u32 v85, v87, 16, 1
	v_add3_u32 v85, v87, v85, s33
	v_bfe_u32 v87, v86, 16, 1
	v_add3_u32 v86, v86, v87, s33
	v_lshrrev_b32_e32 v86, 16, v86
	v_and_or_b32 v85, v85, s96, v86
	global_store_dwordx2 v[92:93], v[84:85], off offset:1024 sc1
	v_pk_mul_f32 v[88:89], v[80:81], v[96:97] op_sel_hi:[1,0]
	v_pk_mul_f32 v[90:91], v[82:83], v[96:97] op_sel_hi:[1,0]
	ds_read_b128 v[80:83], v94 offset:3072
	ds_read_b128 v[84:87], v94 offset:19456
	s_waitcnt lgkmcnt(0)
	v_pk_fma_f32 v[80:81], v[88:89], v[80:81], v[84:85]
	s_nop 0
	v_bfe_u32 v84, v81, 16, 1
	v_add3_u32 v81, v81, v84, s33
	v_bfe_u32 v84, v80, 16, 1
	v_add3_u32 v80, v80, v84, s33
	v_pk_fma_f32 v[82:83], v[90:91], v[82:83], v[86:87]
	v_lshrrev_b32_e32 v80, 16, v80
	v_and_or_b32 v80, v81, s96, v80
	v_bfe_u32 v81, v83, 16, 1
	v_add3_u32 v81, v83, v81, s33
	v_bfe_u32 v83, v82, 16, 1
	v_add3_u32 v82, v82, v83, s33
	v_lshrrev_b32_e32 v82, 16, v82
	v_and_or_b32 v81, v81, s96, v82
	global_store_dwordx2 v[92:93], v[80:81], off offset:1536 sc1
	v_pk_mul_f32 v[84:85], v[76:77], v[96:97] op_sel_hi:[1,0]
	v_pk_mul_f32 v[86:87], v[78:79], v[96:97] op_sel_hi:[1,0]
	ds_read_b128 v[76:79], v94 offset:4096
	ds_read_b128 v[80:83], v94 offset:20480
	s_waitcnt lgkmcnt(0)
	v_pk_fma_f32 v[76:77], v[84:85], v[76:77], v[80:81]
	s_nop 0
	v_bfe_u32 v80, v77, 16, 1
	v_add3_u32 v77, v77, v80, s33
	v_bfe_u32 v80, v76, 16, 1
	v_add3_u32 v76, v76, v80, s33
	v_pk_fma_f32 v[78:79], v[86:87], v[78:79], v[82:83]
	v_lshrrev_b32_e32 v76, 16, v76
	v_and_or_b32 v76, v77, s96, v76
	v_bfe_u32 v77, v79, 16, 1
	v_add3_u32 v77, v79, v77, s33
	v_bfe_u32 v79, v78, 16, 1
	v_add3_u32 v78, v78, v79, s33
	v_lshrrev_b32_e32 v78, 16, v78
	v_and_or_b32 v77, v77, s96, v78
	global_store_dwordx2 v[92:93], v[76:77], off offset:2048 sc1
	v_pk_mul_f32 v[80:81], v[72:73], v[96:97] op_sel_hi:[1,0]
	v_pk_mul_f32 v[82:83], v[74:75], v[96:97] op_sel_hi:[1,0]
	ds_read_b128 v[72:75], v94 offset:5120
	ds_read_b128 v[76:79], v94 offset:21504
	s_waitcnt lgkmcnt(0)
	v_pk_fma_f32 v[72:73], v[80:81], v[72:73], v[76:77]
	s_nop 0
	v_bfe_u32 v76, v73, 16, 1
	v_add3_u32 v73, v73, v76, s33
	v_bfe_u32 v76, v72, 16, 1
	v_add3_u32 v72, v72, v76, s33
	v_pk_fma_f32 v[74:75], v[82:83], v[74:75], v[78:79]
	v_lshrrev_b32_e32 v72, 16, v72
	v_and_or_b32 v72, v73, s96, v72
	v_bfe_u32 v73, v75, 16, 1
	v_add3_u32 v73, v75, v73, s33
	v_bfe_u32 v75, v74, 16, 1
	v_add3_u32 v74, v74, v75, s33
	v_lshrrev_b32_e32 v74, 16, v74
	v_and_or_b32 v73, v73, s96, v74
	global_store_dwordx2 v[92:93], v[72:73], off offset:2560 sc1
	v_pk_mul_f32 v[76:77], v[68:69], v[96:97] op_sel_hi:[1,0]
	v_pk_mul_f32 v[78:79], v[70:71], v[96:97] op_sel_hi:[1,0]
	ds_read_b128 v[68:71], v94 offset:6144
	ds_read_b128 v[72:75], v94 offset:22528
	s_waitcnt lgkmcnt(0)
	v_pk_fma_f32 v[68:69], v[76:77], v[68:69], v[72:73]
	s_nop 0
	v_bfe_u32 v72, v69, 16, 1
	v_add3_u32 v69, v69, v72, s33
	v_bfe_u32 v72, v68, 16, 1
	v_add3_u32 v68, v68, v72, s33
	v_pk_fma_f32 v[70:71], v[78:79], v[70:71], v[74:75]
	v_lshrrev_b32_e32 v68, 16, v68
	v_and_or_b32 v68, v69, s96, v68
	v_bfe_u32 v69, v71, 16, 1
	v_add3_u32 v69, v71, v69, s33
	v_bfe_u32 v71, v70, 16, 1
	v_add3_u32 v70, v70, v71, s33
	v_lshrrev_b32_e32 v70, 16, v70
	v_and_or_b32 v69, v69, s96, v70
	global_store_dwordx2 v[92:93], v[68:69], off offset:3072 sc1
	v_pk_mul_f32 v[72:73], v[64:65], v[96:97] op_sel_hi:[1,0]
	v_pk_mul_f32 v[74:75], v[66:67], v[96:97] op_sel_hi:[1,0]
	ds_read_b128 v[64:67], v94 offset:7168
	ds_read_b128 v[68:71], v94 offset:23552
	s_waitcnt lgkmcnt(0)
	v_pk_fma_f32 v[64:65], v[72:73], v[64:65], v[68:69]
	s_nop 0
	v_bfe_u32 v68, v65, 16, 1
	v_add3_u32 v65, v65, v68, s33
	v_bfe_u32 v68, v64, 16, 1
	v_add3_u32 v64, v64, v68, s33
	v_pk_fma_f32 v[66:67], v[74:75], v[66:67], v[70:71]
	v_lshrrev_b32_e32 v64, 16, v64
	v_and_or_b32 v64, v65, s96, v64
	v_bfe_u32 v65, v67, 16, 1
	v_add3_u32 v65, v67, v65, s33
	v_bfe_u32 v67, v66, 16, 1
	v_add3_u32 v66, v66, v67, s33
	v_lshrrev_b32_e32 v66, 16, v66
	v_and_or_b32 v65, v65, s96, v66
	global_store_dwordx2 v[92:93], v[64:65], off offset:3584 sc1
	s_branch .LBB0_292

.LBB0_408:
	v_lshl_add_u32 v173, s10, 8, v168
	v_ashrrev_i32_e32 v158, 31, v173
	v_mul_lo_u32 v174, s78, v158
	v_mul_lo_u32 v175, s79, v173
	v_mad_u64_u32 v[158:159], s[28:29], s78, v173, 0
	v_lshl_add_u64 v[156:157], v[156:157], 1, s[50:51]
	v_add3_u32 v159, v159, v174, v175
	v_lshl_add_u64 v[158:159], v[158:159], 1, v[156:157]
	v_cvt_pk_bf16_f32 v176, v162, v163
	v_cvt_pk_bf16_f32 v177, v160, v161
	v_cvt_pk_bf16_f32 v178, v166, v167
	v_cvt_pk_bf16_f32 v179, v164, v165
	v_pk_add_f32 v[160:161], v[114:115], v[134:135]
	v_pk_add_f32 v[162:163], v[112:113], v[132:133]
	v_pk_add_f32 v[164:165], v[106:107], v[130:131]
	s_and_b64 vcc, exec, s[36:37]
	v_pk_add_f32 v[166:167], v[104:105], v[128:129]
	global_store_dwordx4 v[158:159], v[176:179], off sc1
	s_cbranch_vccnz .LBB0_410
	v_mul_f32_e32 v162, 0xbfb8aa3b, v162
	v_mul_f32_e32 v166, 0xbfb8aa3b, v166
	v_mul_f32_e32 v163, 0xbfb8aa3b, v163
	v_mul_f32_e32 v167, 0xbfb8aa3b, v167
	v_mul_f32_e32 v160, 0xbfb8aa3b, v160
	v_mul_f32_e32 v164, 0xbfb8aa3b, v164
	v_mul_f32_e32 v161, 0xbfb8aa3b, v161
	v_mul_f32_e32 v165, 0xbfb8aa3b, v165
	v_exp_f32_e32 v162, v162
	v_exp_f32_e32 v166, v166
	v_exp_f32_e32 v163, v163
	v_exp_f32_e32 v167, v167
	v_exp_f32_e32 v160, v160
	v_exp_f32_e32 v164, v164
	v_exp_f32_e32 v161, v161
	v_exp_f32_e32 v165, v165
	v_add_f32_e32 v162, 1.0, v162
	v_add_f32_e32 v166, 1.0, v166
	v_add_f32_e32 v163, 1.0, v163
	v_add_f32_e32 v167, 1.0, v167
	v_add_f32_e32 v160, 1.0, v160
	v_add_f32_e32 v164, 1.0, v164
	v_add_f32_e32 v161, 1.0, v161
	v_add_f32_e32 v165, 1.0, v165
	v_rcp_f32_e32 v162, v162
	v_rcp_f32_e32 v166, v166
	v_rcp_f32_e32 v163, v163
	v_rcp_f32_e32 v167, v167
	v_rcp_f32_e32 v160, v160
	v_rcp_f32_e32 v164, v164
	v_rcp_f32_e32 v161, v161
	v_rcp_f32_e32 v165, v165
.LBB0_410:
	s_nop 0
	v_cvt_pk_bf16_f32 v176, v162, v163
	v_cvt_pk_bf16_f32 v177, v160, v161
	v_cvt_pk_bf16_f32 v178, v166, v167
	v_cvt_pk_bf16_f32 v179, v164, v165
	v_pk_add_f32 v[160:161], v[118:119], v[142:143]
	v_pk_add_f32 v[162:163], v[116:117], v[140:141]
	v_pk_add_f32 v[164:165], v[110:111], v[138:139]
	s_and_b64 vcc, exec, s[36:37]
	v_pk_add_f32 v[166:167], v[108:109], v[136:137]
	global_store_dwordx4 v[158:159], v[176:179], off offset:256 sc1
	s_cbranch_vccnz .LBB0_412
	v_mul_f32_e32 v158, 0xbfb8aa3b, v162
	v_exp_f32_e32 v158, v158
	v_mul_f32_e32 v159, 0xbfb8aa3b, v166
	v_exp_f32_e32 v159, v159
	v_add_f32_e32 v158, 1.0, v158
	v_rcp_f32_e32 v162, v158
	v_mul_f32_e32 v158, 0xbfb8aa3b, v163
	v_add_f32_e32 v159, 1.0, v159
	v_exp_f32_e32 v158, v158
	v_mul_f32_e32 v163, 0xbfb8aa3b, v167
	v_exp_f32_e32 v167, v163
	v_rcp_f32_e32 v166, v159
	v_mul_f32_e32 v159, 0xbfb8aa3b, v160
	v_exp_f32_e32 v159, v159
	v_add_f32_e32 v158, 1.0, v158
	v_rcp_f32_e32 v163, v158
	v_add_f32_e32 v158, 1.0, v167
	v_mul_f32_e32 v160, 0xbfb8aa3b, v164
	v_exp_f32_e32 v164, v160
	v_rcp_f32_e32 v167, v158
	v_add_f32_e32 v158, 1.0, v159
	v_mul_f32_e32 v159, 0xbfb8aa3b, v161
	v_exp_f32_e32 v159, v159
	v_mul_f32_e32 v161, 0xbfb8aa3b, v165
	v_exp_f32_e32 v165, v161
	v_rcp_f32_e32 v160, v158
	v_add_f32_e32 v158, 1.0, v164
	v_rcp_f32_e32 v164, v158
	v_add_f32_e32 v158, 1.0, v159
	v_rcp_f32_e32 v161, v158
	v_add_f32_e32 v158, 1.0, v165
	v_rcp_f32_e32 v165, v158
.LBB0_412:
	v_or_b32_e32 v158, 16, v173
	v_mul_lo_u32 v175, s79, v158
	v_mad_u64_u32 v[158:159], s[28:29], s78, v158, 0
	v_add3_u32 v159, v159, v174, v175
	v_lshl_add_u64 v[158:159], v[158:159], 1, v[156:157]
	v_cvt_pk_bf16_f32 v176, v162, v163
	v_cvt_pk_bf16_f32 v177, v160, v161
	v_cvt_pk_bf16_f32 v178, v166, v167
	v_cvt_pk_bf16_f32 v179, v164, v165
	v_pk_add_f32 v[160:161], v[98:99], v[134:135]
	v_pk_add_f32 v[162:163], v[96:97], v[132:133]
	v_pk_add_f32 v[164:165], v[90:91], v[130:131]
	s_and_b64 vcc, exec, s[36:37]
	v_pk_add_f32 v[166:167], v[88:89], v[128:129]
	global_store_dwordx4 v[158:159], v[176:179], off sc1
	s_cbranch_vccnz .LBB0_414
	v_mul_f32_e32 v162, 0xbfb8aa3b, v162
	v_mul_f32_e32 v166, 0xbfb8aa3b, v166
	v_mul_f32_e32 v163, 0xbfb8aa3b, v163
	v_mul_f32_e32 v167, 0xbfb8aa3b, v167
	v_mul_f32_e32 v160, 0xbfb8aa3b, v160
	v_mul_f32_e32 v164, 0xbfb8aa3b, v164
	v_mul_f32_e32 v161, 0xbfb8aa3b, v161
	v_mul_f32_e32 v165, 0xbfb8aa3b, v165
	v_exp_f32_e32 v162, v162
	v_exp_f32_e32 v166, v166
	v_exp_f32_e32 v163, v163
	v_exp_f32_e32 v167, v167
	v_exp_f32_e32 v160, v160
	v_exp_f32_e32 v164, v164
	v_exp_f32_e32 v161, v161
	v_exp_f32_e32 v165, v165
	v_add_f32_e32 v162, 1.0, v162
	v_add_f32_e32 v166, 1.0, v166
	v_add_f32_e32 v163, 1.0, v163
	v_add_f32_e32 v167, 1.0, v167
	v_add_f32_e32 v160, 1.0, v160
	v_add_f32_e32 v164, 1.0, v164
	v_add_f32_e32 v161, 1.0, v161
	v_add_f32_e32 v165, 1.0, v165
	v_rcp_f32_e32 v162, v162
	v_rcp_f32_e32 v166, v166
	v_rcp_f32_e32 v163, v163
	v_rcp_f32_e32 v167, v167
	v_rcp_f32_e32 v160, v160
	v_rcp_f32_e32 v164, v164
	v_rcp_f32_e32 v161, v161
	v_rcp_f32_e32 v165, v165
.LBB0_414:
	s_nop 0
	v_cvt_pk_bf16_f32 v176, v162, v163
	v_cvt_pk_bf16_f32 v177, v160, v161
	v_cvt_pk_bf16_f32 v178, v166, v167
	v_cvt_pk_bf16_f32 v179, v164, v165
	v_pk_add_f32 v[160:161], v[102:103], v[142:143]
	v_pk_add_f32 v[162:163], v[100:101], v[140:141]
	v_pk_add_f32 v[164:165], v[94:95], v[138:139]
	s_and_b64 vcc, exec, s[36:37]
	v_pk_add_f32 v[166:167], v[92:93], v[136:137]
	global_store_dwordx4 v[158:159], v[176:179], off offset:256 sc1
	s_cbranch_vccnz .LBB0_416
	v_mul_f32_e32 v158, 0xbfb8aa3b, v162
	v_exp_f32_e32 v158, v158
	v_mul_f32_e32 v159, 0xbfb8aa3b, v166
	v_exp_f32_e32 v159, v159
	v_add_f32_e32 v158, 1.0, v158
	v_rcp_f32_e32 v162, v158
	v_mul_f32_e32 v158, 0xbfb8aa3b, v163
	v_add_f32_e32 v159, 1.0, v159
	v_exp_f32_e32 v158, v158
	v_mul_f32_e32 v163, 0xbfb8aa3b, v167
	v_exp_f32_e32 v167, v163
	v_rcp_f32_e32 v166, v159
	v_mul_f32_e32 v159, 0xbfb8aa3b, v160
	v_exp_f32_e32 v159, v159
	v_add_f32_e32 v158, 1.0, v158
	v_rcp_f32_e32 v163, v158
	v_add_f32_e32 v158, 1.0, v167
	v_mul_f32_e32 v160, 0xbfb8aa3b, v164
	v_exp_f32_e32 v164, v160
	v_rcp_f32_e32 v167, v158
	v_add_f32_e32 v158, 1.0, v159
	v_mul_f32_e32 v159, 0xbfb8aa3b, v161
	v_exp_f32_e32 v159, v159
	v_mul_f32_e32 v161, 0xbfb8aa3b, v165
	v_exp_f32_e32 v165, v161
	v_rcp_f32_e32 v160, v158
	v_add_f32_e32 v158, 1.0, v164
	v_rcp_f32_e32 v164, v158
	v_add_f32_e32 v158, 1.0, v159
	v_rcp_f32_e32 v161, v158
	v_add_f32_e32 v158, 1.0, v165
	v_rcp_f32_e32 v165, v158
.LBB0_416:
	v_or_b32_e32 v158, 32, v173
	v_mul_lo_u32 v175, s79, v158
	v_mad_u64_u32 v[158:159], s[28:29], s78, v158, 0
	v_add3_u32 v159, v159, v174, v175
	v_lshl_add_u64 v[158:159], v[158:159], 1, v[156:157]
	v_cvt_pk_bf16_f32 v176, v162, v163
	v_cvt_pk_bf16_f32 v177, v160, v161
	v_cvt_pk_bf16_f32 v178, v166, v167
	v_cvt_pk_bf16_f32 v179, v164, v165
	v_pk_add_f32 v[160:161], v[82:83], v[134:135]
	v_pk_add_f32 v[162:163], v[80:81], v[132:133]
	v_pk_add_f32 v[164:165], v[74:75], v[130:131]
	s_and_b64 vcc, exec, s[36:37]
	v_pk_add_f32 v[166:167], v[72:73], v[128:129]
	global_store_dwordx4 v[158:159], v[176:179], off sc1
	s_cbranch_vccnz .LBB0_418
	v_mul_f32_e32 v162, 0xbfb8aa3b, v162
	v_mul_f32_e32 v166, 0xbfb8aa3b, v166
	v_mul_f32_e32 v163, 0xbfb8aa3b, v163
	v_mul_f32_e32 v167, 0xbfb8aa3b, v167
	v_mul_f32_e32 v160, 0xbfb8aa3b, v160
	v_mul_f32_e32 v164, 0xbfb8aa3b, v164
	v_mul_f32_e32 v161, 0xbfb8aa3b, v161
	v_mul_f32_e32 v165, 0xbfb8aa3b, v165
	v_exp_f32_e32 v162, v162
	v_exp_f32_e32 v166, v166
	v_exp_f32_e32 v163, v163
	v_exp_f32_e32 v167, v167
	v_exp_f32_e32 v160, v160
	v_exp_f32_e32 v164, v164
	v_exp_f32_e32 v161, v161
	v_exp_f32_e32 v165, v165
	v_add_f32_e32 v162, 1.0, v162
	v_add_f32_e32 v166, 1.0, v166
	v_add_f32_e32 v163, 1.0, v163
	v_add_f32_e32 v167, 1.0, v167
	v_add_f32_e32 v160, 1.0, v160
	v_add_f32_e32 v164, 1.0, v164
	v_add_f32_e32 v161, 1.0, v161
	v_add_f32_e32 v165, 1.0, v165
	v_rcp_f32_e32 v162, v162
	v_rcp_f32_e32 v166, v166
	v_rcp_f32_e32 v163, v163
	v_rcp_f32_e32 v167, v167
	v_rcp_f32_e32 v160, v160
	v_rcp_f32_e32 v164, v164
	v_rcp_f32_e32 v161, v161
	v_rcp_f32_e32 v165, v165
.LBB0_418:
	s_nop 0
	v_cvt_pk_bf16_f32 v176, v162, v163
	v_cvt_pk_bf16_f32 v177, v160, v161
	v_cvt_pk_bf16_f32 v178, v166, v167
	v_cvt_pk_bf16_f32 v179, v164, v165
	v_pk_add_f32 v[160:161], v[86:87], v[142:143]
	v_pk_add_f32 v[162:163], v[84:85], v[140:141]
	v_pk_add_f32 v[164:165], v[78:79], v[138:139]
	s_and_b64 vcc, exec, s[36:37]
	v_pk_add_f32 v[166:167], v[76:77], v[136:137]
	global_store_dwordx4 v[158:159], v[176:179], off offset:256 sc1
	s_cbranch_vccnz .LBB0_420
	v_mul_f32_e32 v158, 0xbfb8aa3b, v162
	v_exp_f32_e32 v158, v158
	v_mul_f32_e32 v159, 0xbfb8aa3b, v166
	v_exp_f32_e32 v159, v159
	v_add_f32_e32 v158, 1.0, v158
	v_rcp_f32_e32 v162, v158
	v_mul_f32_e32 v158, 0xbfb8aa3b, v163
	v_add_f32_e32 v159, 1.0, v159
	v_exp_f32_e32 v158, v158
	v_mul_f32_e32 v163, 0xbfb8aa3b, v167
	v_exp_f32_e32 v167, v163
	v_rcp_f32_e32 v166, v159
	v_mul_f32_e32 v159, 0xbfb8aa3b, v160
	v_exp_f32_e32 v159, v159
	v_add_f32_e32 v158, 1.0, v158
	v_rcp_f32_e32 v163, v158
	v_add_f32_e32 v158, 1.0, v167
	v_mul_f32_e32 v160, 0xbfb8aa3b, v164
	v_exp_f32_e32 v164, v160
	v_rcp_f32_e32 v167, v158
	v_add_f32_e32 v158, 1.0, v159
	v_mul_f32_e32 v159, 0xbfb8aa3b, v161
	v_exp_f32_e32 v159, v159
	v_mul_f32_e32 v161, 0xbfb8aa3b, v165
	v_exp_f32_e32 v165, v161
	v_rcp_f32_e32 v160, v158
	v_add_f32_e32 v158, 1.0, v164
	v_rcp_f32_e32 v164, v158
	v_add_f32_e32 v158, 1.0, v159
	v_rcp_f32_e32 v161, v158
	v_add_f32_e32 v158, 1.0, v165
	v_rcp_f32_e32 v165, v158
.LBB0_420:
	v_or_b32_e32 v158, 48, v173
	v_mul_lo_u32 v175, s79, v158
	v_mad_u64_u32 v[158:159], s[28:29], s78, v158, 0
	v_add3_u32 v159, v159, v174, v175
	v_lshl_add_u64 v[158:159], v[158:159], 1, v[156:157]
	v_cvt_pk_bf16_f32 v174, v162, v163
	v_cvt_pk_bf16_f32 v175, v160, v161
	v_cvt_pk_bf16_f32 v176, v166, v167
	v_cvt_pk_bf16_f32 v177, v164, v165
	v_pk_add_f32 v[160:161], v[70:71], v[134:135]
	v_pk_add_f32 v[162:163], v[68:69], v[132:133]
	v_pk_add_f32 v[164:165], v[66:67], v[130:131]
	s_and_b64 vcc, exec, s[36:37]
	v_pk_add_f32 v[166:167], v[64:65], v[128:129]
	global_store_dwordx4 v[158:159], v[174:177], off sc1
	s_cbranch_vccnz .LBB0_422
	v_mul_f32_e32 v162, 0xbfb8aa3b, v162
	v_mul_f32_e32 v166, 0xbfb8aa3b, v166
	v_mul_f32_e32 v163, 0xbfb8aa3b, v163
	v_mul_f32_e32 v167, 0xbfb8aa3b, v167
	v_mul_f32_e32 v160, 0xbfb8aa3b, v160
	v_mul_f32_e32 v164, 0xbfb8aa3b, v164
	v_mul_f32_e32 v161, 0xbfb8aa3b, v161
	v_mul_f32_e32 v165, 0xbfb8aa3b, v165
	v_exp_f32_e32 v162, v162
	v_exp_f32_e32 v166, v166
	v_exp_f32_e32 v163, v163
	v_exp_f32_e32 v167, v167
	v_exp_f32_e32 v160, v160
	v_exp_f32_e32 v164, v164
	v_exp_f32_e32 v161, v161
	v_exp_f32_e32 v165, v165
	v_add_f32_e32 v162, 1.0, v162
	v_add_f32_e32 v166, 1.0, v166
	v_add_f32_e32 v163, 1.0, v163
	v_add_f32_e32 v167, 1.0, v167
	v_add_f32_e32 v160, 1.0, v160
	v_add_f32_e32 v164, 1.0, v164
	v_add_f32_e32 v161, 1.0, v161
	v_add_f32_e32 v165, 1.0, v165
	v_rcp_f32_e32 v162, v162
	v_rcp_f32_e32 v166, v166
	v_rcp_f32_e32 v163, v163
	v_rcp_f32_e32 v167, v167
	v_rcp_f32_e32 v160, v160
	v_rcp_f32_e32 v164, v164
	v_rcp_f32_e32 v161, v161
	v_rcp_f32_e32 v165, v165
.LBB0_422:
	s_nop 0
	v_cvt_pk_bf16_f32 v174, v162, v163
	v_cvt_pk_bf16_f32 v175, v160, v161
	v_cvt_pk_bf16_f32 v176, v166, v167
	v_cvt_pk_bf16_f32 v177, v164, v165
	v_pk_add_f32 v[160:161], v[62:63], v[142:143]
	v_pk_add_f32 v[162:163], v[60:61], v[140:141]
	v_pk_add_f32 v[164:165], v[58:59], v[138:139]
	s_and_b64 vcc, exec, s[36:37]
	v_pk_add_f32 v[166:167], v[56:57], v[136:137]
	global_store_dwordx4 v[158:159], v[174:177], off offset:256 sc1
	s_cbranch_vccnz .LBB0_424
	v_mul_f32_e32 v158, 0xbfb8aa3b, v162
	v_exp_f32_e32 v158, v158
	v_mul_f32_e32 v159, 0xbfb8aa3b, v166
	v_exp_f32_e32 v159, v159
	v_add_f32_e32 v158, 1.0, v158
	v_rcp_f32_e32 v162, v158
	v_mul_f32_e32 v158, 0xbfb8aa3b, v163
	v_add_f32_e32 v159, 1.0, v159
	v_exp_f32_e32 v158, v158
	v_mul_f32_e32 v163, 0xbfb8aa3b, v167
	v_exp_f32_e32 v167, v163
	v_rcp_f32_e32 v166, v159
	v_mul_f32_e32 v159, 0xbfb8aa3b, v160
	v_exp_f32_e32 v159, v159
	v_add_f32_e32 v158, 1.0, v158
	v_rcp_f32_e32 v163, v158
	v_add_f32_e32 v158, 1.0, v167
	v_mul_f32_e32 v160, 0xbfb8aa3b, v164
	v_exp_f32_e32 v164, v160
	v_rcp_f32_e32 v167, v158
	v_add_f32_e32 v158, 1.0, v159
	v_mul_f32_e32 v159, 0xbfb8aa3b, v161
	v_exp_f32_e32 v159, v159
	v_mul_f32_e32 v161, 0xbfb8aa3b, v165
	v_exp_f32_e32 v165, v161
	v_rcp_f32_e32 v160, v158
	v_add_f32_e32 v158, 1.0, v164
	v_rcp_f32_e32 v164, v158
	v_add_f32_e32 v158, 1.0, v159
	v_rcp_f32_e32 v161, v158
	v_add_f32_e32 v158, 1.0, v165
	v_rcp_f32_e32 v165, v158
.LBB0_424:
	v_add_u32_e32 v158, 0x80, v173
	v_ashrrev_i32_e32 v159, 31, v158
	v_mul_lo_u32 v174, s78, v159
	v_mul_lo_u32 v175, s79, v158
	v_mad_u64_u32 v[158:159], s[28:29], s78, v158, 0
	v_add3_u32 v159, v159, v174, v175
	v_lshl_add_u64 v[158:159], v[158:159], 1, v[156:157]
	v_cvt_pk_bf16_f32 v174, v162, v163
	v_cvt_pk_bf16_f32 v175, v160, v161
	v_cvt_pk_bf16_f32 v176, v166, v167
	v_cvt_pk_bf16_f32 v177, v164, v165
	v_pk_add_f32 v[160:161], v[50:51], v[134:135]
	v_pk_add_f32 v[162:163], v[48:49], v[132:133]
	v_pk_add_f32 v[164:165], v[42:43], v[130:131]
	s_and_b64 vcc, exec, s[36:37]
	v_pk_add_f32 v[166:167], v[40:41], v[128:129]
	global_store_dwordx4 v[158:159], v[174:177], off sc1
	s_cbranch_vccnz .LBB0_426
	v_mul_f32_e32 v162, 0xbfb8aa3b, v162
	v_mul_f32_e32 v166, 0xbfb8aa3b, v166
	v_mul_f32_e32 v163, 0xbfb8aa3b, v163
	v_mul_f32_e32 v167, 0xbfb8aa3b, v167
	v_mul_f32_e32 v160, 0xbfb8aa3b, v160
	v_mul_f32_e32 v164, 0xbfb8aa3b, v164
	v_mul_f32_e32 v161, 0xbfb8aa3b, v161
	v_mul_f32_e32 v165, 0xbfb8aa3b, v165
	v_exp_f32_e32 v162, v162
	v_exp_f32_e32 v166, v166
	v_exp_f32_e32 v163, v163
	v_exp_f32_e32 v167, v167
	v_exp_f32_e32 v160, v160
	v_exp_f32_e32 v164, v164
	v_exp_f32_e32 v161, v161
	v_exp_f32_e32 v165, v165
	v_add_f32_e32 v162, 1.0, v162
	v_add_f32_e32 v166, 1.0, v166
	v_add_f32_e32 v163, 1.0, v163
	v_add_f32_e32 v167, 1.0, v167
	v_add_f32_e32 v160, 1.0, v160
	v_add_f32_e32 v164, 1.0, v164
	v_add_f32_e32 v161, 1.0, v161
	v_add_f32_e32 v165, 1.0, v165
	v_rcp_f32_e32 v162, v162
	v_rcp_f32_e32 v166, v166
	v_rcp_f32_e32 v163, v163
	v_rcp_f32_e32 v167, v167
	v_rcp_f32_e32 v160, v160
	v_rcp_f32_e32 v164, v164
	v_rcp_f32_e32 v161, v161
	v_rcp_f32_e32 v165, v165
.LBB0_426:
	s_nop 0
	v_cvt_pk_bf16_f32 v174, v162, v163
	v_cvt_pk_bf16_f32 v175, v160, v161
	v_cvt_pk_bf16_f32 v176, v166, v167
	v_cvt_pk_bf16_f32 v177, v164, v165
	v_pk_add_f32 v[160:161], v[54:55], v[142:143]
	v_pk_add_f32 v[162:163], v[52:53], v[140:141]
	v_pk_add_f32 v[164:165], v[46:47], v[138:139]
	s_and_b64 vcc, exec, s[36:37]
	v_pk_add_f32 v[166:167], v[44:45], v[136:137]
	global_store_dwordx4 v[158:159], v[174:177], off offset:256 sc1
	s_cbranch_vccnz .LBB0_428
	v_mul_f32_e32 v158, 0xbfb8aa3b, v162
	v_exp_f32_e32 v158, v158
	v_mul_f32_e32 v159, 0xbfb8aa3b, v166
	v_exp_f32_e32 v159, v159
	v_add_f32_e32 v158, 1.0, v158
	v_rcp_f32_e32 v162, v158
	v_mul_f32_e32 v158, 0xbfb8aa3b, v163
	v_add_f32_e32 v159, 1.0, v159
	v_exp_f32_e32 v158, v158
	v_mul_f32_e32 v163, 0xbfb8aa3b, v167
	v_exp_f32_e32 v167, v163
	v_rcp_f32_e32 v166, v159
	v_mul_f32_e32 v159, 0xbfb8aa3b, v160
	v_exp_f32_e32 v159, v159
	v_add_f32_e32 v158, 1.0, v158
	v_rcp_f32_e32 v163, v158
	v_add_f32_e32 v158, 1.0, v167
	v_mul_f32_e32 v160, 0xbfb8aa3b, v164
	v_exp_f32_e32 v164, v160
	v_rcp_f32_e32 v167, v158
	v_add_f32_e32 v158, 1.0, v159
	v_mul_f32_e32 v159, 0xbfb8aa3b, v161
	v_exp_f32_e32 v159, v159
	v_mul_f32_e32 v161, 0xbfb8aa3b, v165
	v_exp_f32_e32 v165, v161
	v_rcp_f32_e32 v160, v158
	v_add_f32_e32 v158, 1.0, v164
	v_rcp_f32_e32 v164, v158
	v_add_f32_e32 v158, 1.0, v159
	v_rcp_f32_e32 v161, v158
	v_add_f32_e32 v158, 1.0, v165
	v_rcp_f32_e32 v165, v158
.LBB0_428:
	v_add_u32_e32 v158, 0x90, v173
	v_ashrrev_i32_e32 v159, 31, v158
	v_mul_lo_u32 v174, s78, v159
	v_mul_lo_u32 v175, s79, v158
	v_mad_u64_u32 v[158:159], s[28:29], s78, v158, 0
	v_add3_u32 v159, v159, v174, v175
	v_lshl_add_u64 v[158:159], v[158:159], 1, v[156:157]
	v_cvt_pk_bf16_f32 v174, v162, v163
	v_cvt_pk_bf16_f32 v175, v160, v161
	v_cvt_pk_bf16_f32 v176, v166, v167
	v_cvt_pk_bf16_f32 v177, v164, v165
	v_pk_add_f32 v[160:161], v[34:35], v[134:135]
	v_pk_add_f32 v[162:163], v[32:33], v[132:133]
	v_pk_add_f32 v[164:165], v[26:27], v[130:131]
	s_and_b64 vcc, exec, s[36:37]
	v_pk_add_f32 v[166:167], v[24:25], v[128:129]
	global_store_dwordx4 v[158:159], v[174:177], off sc1
	s_cbranch_vccnz .LBB0_430
	v_mul_f32_e32 v162, 0xbfb8aa3b, v162
	v_mul_f32_e32 v166, 0xbfb8aa3b, v166
	v_mul_f32_e32 v163, 0xbfb8aa3b, v163
	v_mul_f32_e32 v167, 0xbfb8aa3b, v167
	v_mul_f32_e32 v160, 0xbfb8aa3b, v160
	v_mul_f32_e32 v164, 0xbfb8aa3b, v164
	v_mul_f32_e32 v161, 0xbfb8aa3b, v161
	v_mul_f32_e32 v165, 0xbfb8aa3b, v165
	v_exp_f32_e32 v162, v162
	v_exp_f32_e32 v166, v166
	v_exp_f32_e32 v163, v163
	v_exp_f32_e32 v167, v167
	v_exp_f32_e32 v160, v160
	v_exp_f32_e32 v164, v164
	v_exp_f32_e32 v161, v161
	v_exp_f32_e32 v165, v165
	v_add_f32_e32 v162, 1.0, v162
	v_add_f32_e32 v166, 1.0, v166
	v_add_f32_e32 v163, 1.0, v163
	v_add_f32_e32 v167, 1.0, v167
	v_add_f32_e32 v160, 1.0, v160
	v_add_f32_e32 v164, 1.0, v164
	v_add_f32_e32 v161, 1.0, v161
	v_add_f32_e32 v165, 1.0, v165
	v_rcp_f32_e32 v162, v162
	v_rcp_f32_e32 v166, v166
	v_rcp_f32_e32 v163, v163
	v_rcp_f32_e32 v167, v167
	v_rcp_f32_e32 v160, v160
	v_rcp_f32_e32 v164, v164
	v_rcp_f32_e32 v161, v161
	v_rcp_f32_e32 v165, v165
.LBB0_430:
	s_nop 0
	v_cvt_pk_bf16_f32 v174, v162, v163
	v_cvt_pk_bf16_f32 v175, v160, v161
	v_cvt_pk_bf16_f32 v176, v166, v167
	v_cvt_pk_bf16_f32 v177, v164, v165
	v_pk_add_f32 v[160:161], v[38:39], v[142:143]
	v_pk_add_f32 v[162:163], v[36:37], v[140:141]
	v_pk_add_f32 v[164:165], v[30:31], v[138:139]
	s_and_b64 vcc, exec, s[36:37]
	v_pk_add_f32 v[166:167], v[28:29], v[136:137]
	global_store_dwordx4 v[158:159], v[174:177], off offset:256 sc1
	s_cbranch_vccnz .LBB0_432
	v_mul_f32_e32 v158, 0xbfb8aa3b, v162
	v_exp_f32_e32 v158, v158
	v_mul_f32_e32 v159, 0xbfb8aa3b, v166
	v_exp_f32_e32 v159, v159
	v_add_f32_e32 v158, 1.0, v158
	v_rcp_f32_e32 v162, v158
	v_mul_f32_e32 v158, 0xbfb8aa3b, v163
	v_add_f32_e32 v159, 1.0, v159
	v_exp_f32_e32 v158, v158
	v_mul_f32_e32 v163, 0xbfb8aa3b, v167
	v_exp_f32_e32 v167, v163
	v_rcp_f32_e32 v166, v159
	v_mul_f32_e32 v159, 0xbfb8aa3b, v160
	v_exp_f32_e32 v159, v159
	v_add_f32_e32 v158, 1.0, v158
	v_rcp_f32_e32 v163, v158
	v_add_f32_e32 v158, 1.0, v167
	v_mul_f32_e32 v160, 0xbfb8aa3b, v164
	v_exp_f32_e32 v164, v160
	v_rcp_f32_e32 v167, v158
	v_add_f32_e32 v158, 1.0, v159
	v_mul_f32_e32 v159, 0xbfb8aa3b, v161
	v_exp_f32_e32 v159, v159
	v_mul_f32_e32 v161, 0xbfb8aa3b, v165
	v_exp_f32_e32 v165, v161
	v_rcp_f32_e32 v160, v158
	v_add_f32_e32 v158, 1.0, v164
	v_rcp_f32_e32 v164, v158
	v_add_f32_e32 v158, 1.0, v159
	v_rcp_f32_e32 v161, v158
	v_add_f32_e32 v158, 1.0, v165
	v_rcp_f32_e32 v165, v158
.LBB0_432:
	v_add_u32_e32 v158, 0xa0, v173
	v_ashrrev_i32_e32 v159, 31, v158
	v_mul_lo_u32 v174, s78, v159
	v_mul_lo_u32 v175, s79, v158
	v_mad_u64_u32 v[158:159], s[28:29], s78, v158, 0
	v_add3_u32 v159, v159, v174, v175
	v_lshl_add_u64 v[158:159], v[158:159], 1, v[156:157]
	v_cvt_pk_bf16_f32 v174, v162, v163
	v_cvt_pk_bf16_f32 v175, v160, v161
	v_cvt_pk_bf16_f32 v176, v166, v167
	v_cvt_pk_bf16_f32 v177, v164, v165
	v_pk_add_f32 v[160:161], v[18:19], v[134:135]
	v_pk_add_f32 v[162:163], v[16:17], v[132:133]
	v_pk_add_f32 v[164:165], v[10:11], v[130:131]
	s_and_b64 vcc, exec, s[36:37]
	v_pk_add_f32 v[166:167], v[8:9], v[128:129]
	global_store_dwordx4 v[158:159], v[174:177], off sc1
	s_cbranch_vccnz .LBB0_434
	v_mul_f32_e32 v162, 0xbfb8aa3b, v162
	v_mul_f32_e32 v166, 0xbfb8aa3b, v166
	v_mul_f32_e32 v163, 0xbfb8aa3b, v163
	v_mul_f32_e32 v167, 0xbfb8aa3b, v167
	v_mul_f32_e32 v160, 0xbfb8aa3b, v160
	v_mul_f32_e32 v164, 0xbfb8aa3b, v164
	v_mul_f32_e32 v161, 0xbfb8aa3b, v161
	v_mul_f32_e32 v165, 0xbfb8aa3b, v165
	v_exp_f32_e32 v162, v162
	v_exp_f32_e32 v166, v166
	v_exp_f32_e32 v163, v163
	v_exp_f32_e32 v167, v167
	v_exp_f32_e32 v160, v160
	v_exp_f32_e32 v164, v164
	v_exp_f32_e32 v161, v161
	v_exp_f32_e32 v165, v165
	v_add_f32_e32 v162, 1.0, v162
	v_add_f32_e32 v166, 1.0, v166
	v_add_f32_e32 v163, 1.0, v163
	v_add_f32_e32 v167, 1.0, v167
	v_add_f32_e32 v160, 1.0, v160
	v_add_f32_e32 v164, 1.0, v164
	v_add_f32_e32 v161, 1.0, v161
	v_add_f32_e32 v165, 1.0, v165
	v_rcp_f32_e32 v162, v162
	v_rcp_f32_e32 v166, v166
	v_rcp_f32_e32 v163, v163
	v_rcp_f32_e32 v167, v167
	v_rcp_f32_e32 v160, v160
	v_rcp_f32_e32 v164, v164
	v_rcp_f32_e32 v161, v161
	v_rcp_f32_e32 v165, v165
.LBB0_434:
	s_nop 0
	v_cvt_pk_bf16_f32 v174, v162, v163
	v_cvt_pk_bf16_f32 v175, v160, v161
	v_cvt_pk_bf16_f32 v176, v166, v167
	v_cvt_pk_bf16_f32 v177, v164, v165
	global_store_dwordx4 v[158:159], v[174:177], off offset:256 sc1
	v_pk_add_f32 v[142:143], v[22:23], v[142:143]
	v_pk_add_f32 v[140:141], v[20:21], v[140:141]
	v_pk_add_f32 v[138:139], v[14:15], v[138:139]
	s_and_b64 vcc, exec, s[36:37]
	v_pk_add_f32 v[158:159], v[12:13], v[136:137]
	s_cbranch_vccnz .LBB0_436
	v_mul_f32_e32 v136, 0xbfb8aa3b, v140
	v_exp_f32_e32 v136, v136
	v_mul_f32_e32 v137, 0xbfb8aa3b, v158
	v_exp_f32_e32 v137, v137
	v_mul_f32_e32 v138, 0xbfb8aa3b, v138
	v_add_f32_e32 v136, 1.0, v136
	v_rcp_f32_e32 v140, v136
	v_mul_f32_e32 v136, 0xbfb8aa3b, v141
	v_add_f32_e32 v137, 1.0, v137
	v_exp_f32_e32 v136, v136
	v_mul_f32_e32 v141, 0xbfb8aa3b, v159
	v_exp_f32_e32 v159, v141
	v_rcp_f32_e32 v158, v137
	v_mul_f32_e32 v137, 0xbfb8aa3b, v142
	v_exp_f32_e32 v137, v137
	v_exp_f32_e32 v138, v138
	v_add_f32_e32 v136, 1.0, v136
	v_rcp_f32_e32 v141, v136
	v_add_f32_e32 v136, 1.0, v159
	v_rcp_f32_e32 v159, v136
	v_add_f32_e32 v136, 1.0, v137
	v_mul_f32_e32 v137, 0xbfb8aa3b, v143
	v_rcp_f32_e32 v142, v136
	v_add_f32_e32 v136, 1.0, v138
	v_exp_f32_e32 v137, v137
	v_mul_f32_e32 v138, 0xbfb8aa3b, v139
	v_exp_f32_e32 v139, v138
	v_rcp_f32_e32 v138, v136
	v_add_f32_e32 v136, 1.0, v137
	v_rcp_f32_e32 v143, v136
	v_add_f32_e32 v136, 1.0, v139
	v_rcp_f32_e32 v139, v136
.LBB0_436:
	v_add_u32_e32 v136, 0xb0, v173
	v_ashrrev_i32_e32 v137, 31, v136
	v_mul_lo_u32 v160, s78, v137
	v_mul_lo_u32 v161, s79, v136
	v_mad_u64_u32 v[136:137], s[28:29], s78, v136, 0
	v_add3_u32 v137, v137, v160, v161
	v_lshl_add_u64 v[136:137], v[136:137], 1, v[156:157]
	v_cvt_pk_bf16_f32 v140, v140, v141
	v_cvt_pk_bf16_f32 v141, v142, v143
	v_cvt_pk_bf16_f32 v142, v158, v159
	v_cvt_pk_bf16_f32 v143, v138, v139
	v_pk_add_f32 v[134:135], v[6:7], v[134:135]
	v_pk_add_f32 v[138:139], v[4:5], v[132:133]
	v_pk_add_f32 v[132:133], v[2:3], v[130:131]
	s_and_b64 vcc, exec, s[36:37]
	v_pk_add_f32 v[130:131], v[0:1], v[128:129]
	global_store_dwordx4 v[136:137], v[140:143], off sc1
	s_cbranch_vccnz .LBB0_438
	v_mul_f32_e32 v128, 0xbfb8aa3b, v138
	v_exp_f32_e32 v128, v128
	v_mul_f32_e32 v129, 0xbfb8aa3b, v130
	v_exp_f32_e32 v129, v129
	v_mul_f32_e32 v130, 0xbfb8aa3b, v131
	v_add_f32_e32 v128, 1.0, v128
	v_rcp_f32_e32 v138, v128
	v_mul_f32_e32 v128, 0xbfb8aa3b, v139
	v_exp_f32_e32 v128, v128
	v_exp_f32_e32 v131, v130
	v_add_f32_e32 v129, 1.0, v129
	v_rcp_f32_e32 v130, v129
	v_add_f32_e32 v128, 1.0, v128
	v_mul_f32_e32 v129, 0xbfb8aa3b, v134
	v_rcp_f32_e32 v139, v128
	v_add_f32_e32 v128, 1.0, v131
	v_exp_f32_e32 v129, v129
	v_mul_f32_e32 v131, 0xbfb8aa3b, v132
	v_exp_f32_e32 v132, v131
	v_rcp_f32_e32 v131, v128
	v_add_f32_e32 v128, 1.0, v129
	v_mul_f32_e32 v129, 0xbfb8aa3b, v135
	v_rcp_f32_e32 v134, v128
	v_add_f32_e32 v128, 1.0, v132
	v_exp_f32_e32 v129, v129
	v_mul_f32_e32 v132, 0xbfb8aa3b, v133
	v_exp_f32_e32 v133, v132
	v_rcp_f32_e32 v132, v128
	v_add_f32_e32 v128, 1.0, v129
	v_rcp_f32_e32 v135, v128
	v_add_f32_e32 v128, 1.0, v133
	v_rcp_f32_e32 v133, v128

.LBB0_439:
	s_andn2_b64 vcc, exec, s[44:45]
	s_mov_b64 s[10:11], -1
	global_store_dwordx4 v[136:137], v[128:131], off offset:256 sc1
	s_cbranch_vccnz .LBB0_365
	s_branch .LBB0_442
.LBB0_440:
	s_and_b64 vcc, exec, s[36:37]
	s_cbranch_vccz .LBB0_439
	v_lshl_add_u32 v134, s10, 8, v168
	v_readlane_b32 s10, v251, 24
	v_readlane_b32 s11, v251, 25
	v_lshl_add_u32 v184, s12, 8, v171
	s_mov_b32 s12, 0x8200
	v_mov_b64_e32 v[128:129], s[10:11]
	v_mad_i64_i32 v[132:133], s[10:11], v134, s12, v[128:129]
	v_lshlrev_b64 v[130:131], 1, v[184:185]
	v_lshl_add_u64 v[132:133], v[132:133], 0, v[130:131]
	v_cvt_pk_bf16_f32 v124, v124, v125
	v_cvt_pk_bf16_f32 v125, v126, v127
	v_cvt_pk_bf16_f32 v126, v120, v121
	v_cvt_pk_bf16_f32 v127, v122, v123
	global_store_dwordx4 v[132:133], v[124:127], off sc1
	v_cvt_pk_bf16_f32 v112, v112, v113
	v_cvt_pk_bf16_f32 v113, v114, v115
	v_cvt_pk_bf16_f32 v114, v104, v105
	v_or_b32_e32 v104, 16, v134
	v_mad_i64_i32 v[104:105], s[10:11], v104, s12, v[128:129]
	v_cvt_pk_bf16_f32 v115, v106, v107
	global_store_dwordx4 v[132:133], v[112:115], off offset:256 sc1
	s_nop 1
	v_lshl_add_u64 v[112:113], v[104:105], 0, v[130:131]
	v_cvt_pk_bf16_f32 v104, v116, v117
	v_cvt_pk_bf16_f32 v105, v118, v119
	v_cvt_pk_bf16_f32 v106, v108, v109
	v_cvt_pk_bf16_f32 v107, v110, v111
	global_store_dwordx4 v[112:113], v[104:107], off sc1
	v_cvt_pk_bf16_f32 v96, v96, v97
	v_cvt_pk_bf16_f32 v97, v98, v99
	v_cvt_pk_bf16_f32 v98, v88, v89
	v_or_b32_e32 v88, 32, v134
	v_mad_i64_i32 v[88:89], s[10:11], v88, s12, v[128:129]
	v_cvt_pk_bf16_f32 v99, v90, v91
	global_store_dwordx4 v[112:113], v[96:99], off offset:256 sc1
	s_nop 1
	v_lshl_add_u64 v[96:97], v[88:89], 0, v[130:131]
	v_cvt_pk_bf16_f32 v88, v100, v101
	v_cvt_pk_bf16_f32 v89, v102, v103
	v_cvt_pk_bf16_f32 v90, v92, v93
	v_cvt_pk_bf16_f32 v91, v94, v95
	global_store_dwordx4 v[96:97], v[88:91], off sc1
	v_cvt_pk_bf16_f32 v80, v80, v81
	v_cvt_pk_bf16_f32 v81, v82, v83
	v_cvt_pk_bf16_f32 v82, v72, v73
	v_or_b32_e32 v72, 48, v134
	v_mad_i64_i32 v[72:73], s[10:11], v72, s12, v[128:129]
	v_cvt_pk_bf16_f32 v83, v74, v75
	global_store_dwordx4 v[96:97], v[80:83], off offset:256 sc1
	s_nop 1
	v_lshl_add_u64 v[80:81], v[72:73], 0, v[130:131]
	v_cvt_pk_bf16_f32 v72, v84, v85
	v_cvt_pk_bf16_f32 v73, v86, v87
	v_cvt_pk_bf16_f32 v74, v76, v77
	v_cvt_pk_bf16_f32 v75, v78, v79
	global_store_dwordx4 v[80:81], v[72:75], off sc1
	v_cvt_pk_bf16_f32 v68, v68, v69
	v_cvt_pk_bf16_f32 v69, v70, v71
	v_cvt_pk_bf16_f32 v70, v64, v65
	v_add_u32_e32 v64, 0x80, v134
	v_mad_i64_i32 v[64:65], s[10:11], v64, s12, v[128:129]
	v_lshl_add_u64 v[64:65], v[64:65], 0, v[130:131]
	v_cvt_pk_bf16_f32 v71, v66, v67
	global_store_dwordx4 v[80:81], v[68:71], off offset:256 sc1
	v_cvt_pk_bf16_f32 v60, v60, v61
	v_cvt_pk_bf16_f32 v61, v62, v63
	v_cvt_pk_bf16_f32 v62, v56, v57
	v_cvt_pk_bf16_f32 v63, v58, v59
	global_store_dwordx4 v[64:65], v[60:63], off sc1
	v_cvt_pk_bf16_f32 v48, v48, v49
	v_cvt_pk_bf16_f32 v49, v50, v51
	v_cvt_pk_bf16_f32 v50, v40, v41
	v_add_u32_e32 v40, 0x90, v134
	v_mad_i64_i32 v[40:41], s[10:11], v40, s12, v[128:129]
	v_cvt_pk_bf16_f32 v51, v42, v43
	global_store_dwordx4 v[64:65], v[48:51], off offset:256 sc1
	s_nop 1
	v_lshl_add_u64 v[48:49], v[40:41], 0, v[130:131]
	v_cvt_pk_bf16_f32 v40, v52, v53
	v_cvt_pk_bf16_f32 v41, v54, v55
	v_cvt_pk_bf16_f32 v42, v44, v45
	v_cvt_pk_bf16_f32 v43, v46, v47
	global_store_dwordx4 v[48:49], v[40:43], off sc1
	v_cvt_pk_bf16_f32 v32, v32, v33
	v_cvt_pk_bf16_f32 v33, v34, v35
	v_cvt_pk_bf16_f32 v34, v24, v25
	v_add_u32_e32 v24, 0xa0, v134
	v_mad_i64_i32 v[24:25], s[10:11], v24, s12, v[128:129]
	v_cvt_pk_bf16_f32 v35, v26, v27
	global_store_dwordx4 v[48:49], v[32:35], off offset:256 sc1
	s_nop 1
	v_lshl_add_u64 v[32:33], v[24:25], 0, v[130:131]
	v_cvt_pk_bf16_f32 v24, v36, v37
	v_cvt_pk_bf16_f32 v25, v38, v39
	v_cvt_pk_bf16_f32 v26, v28, v29
	v_cvt_pk_bf16_f32 v27, v30, v31
	global_store_dwordx4 v[32:33], v[24:27], off sc1
	v_cvt_pk_bf16_f32 v16, v16, v17
	v_cvt_pk_bf16_f32 v17, v18, v19
	v_cvt_pk_bf16_f32 v18, v8, v9
	v_add_u32_e32 v8, 0xb0, v134
	v_mad_i64_i32 v[8:9], s[10:11], v8, s12, v[128:129]
	v_lshl_add_u64 v[136:137], v[8:9], 0, v[130:131]
	v_cvt_pk_bf16_f32 v19, v10, v11
	global_store_dwordx4 v[32:33], v[16:19], off offset:256 sc1
	v_cvt_pk_bf16_f32 v8, v20, v21
	v_cvt_pk_bf16_f32 v9, v22, v23
	v_cvt_pk_bf16_f32 v10, v12, v13
	v_cvt_pk_bf16_f32 v11, v14, v15
	global_store_dwordx4 v[136:137], v[8:11], off sc1
	v_cvt_pk_bf16_f32 v128, v4, v5
	v_cvt_pk_bf16_f32 v129, v6, v7
	v_cvt_pk_bf16_f32 v130, v0, v1
	v_cvt_pk_bf16_f32 v131, v2, v3
	s_andn2_b64 vcc, exec, s[44:45]
	s_mov_b64 s[10:11], -1
	global_store_dwordx4 v[136:137], v[128:131], off offset:256 sc1
	s_cbranch_vccnz .LBB0_365

.LBB0_517:
	s_lshl_b32 s9, s61, 15
	s_lshl_b32 s28, s60, 1
	s_add_i32 s9, s28, s9
	v_cvt_pk_bf16_f32 v124, v124, v125
	v_cvt_pk_bf16_f32 v125, v126, v127
	v_cvt_pk_bf16_f32 v126, v120, v121
	v_add_u32_e32 v120, s9, v137
	s_lshl_b32 s18, s62, 7
	v_ashrrev_i32_e32 v121, 31, v120
	s_ashr_i32 s19, s18, 31
	v_cvt_pk_bf16_f32 v127, v122, v123
	v_lshlrev_b64 v[122:123], 9, v[120:121]
	v_lshl_add_u64 v[122:123], s[66:67], 0, v[122:123]
	s_lshl_b64 s[18:19], s[18:19], 1
	v_lshl_add_u64 v[122:123], v[122:123], 0, s[18:19]
	v_lshl_add_u64 v[122:123], v[122:123], 0, v[184:185]
	global_store_dwordx4 v[122:123], v[124:127], off sc1
	v_cvt_pk_bf16_f32 v116, v116, v117
	v_cvt_pk_bf16_f32 v117, v118, v119
	v_cvt_pk_bf16_f32 v118, v108, v109
	v_add_u32_e32 v108, 1, v120
	v_ashrrev_i32_e32 v109, 31, v108
	v_lshlrev_b64 v[108:109], 9, v[108:109]
	v_lshl_add_u64 v[108:109], s[66:67], 0, v[108:109]
	v_lshl_add_u64 v[108:109], v[108:109], 0, s[18:19]
	v_lshl_add_u64 v[108:109], v[108:109], 0, v[184:185]
	v_cvt_pk_bf16_f32 v119, v110, v111
	global_store_dwordx4 v[108:109], v[116:119], off sc1
	v_cvt_pk_bf16_f32 v108, v112, v113
	v_cvt_pk_bf16_f32 v109, v114, v115
	v_cvt_pk_bf16_f32 v110, v104, v105
	v_add_u32_e32 v104, s9, v138
	v_ashrrev_i32_e32 v105, 31, v104
	v_cvt_pk_bf16_f32 v111, v106, v107
	v_lshlrev_b64 v[106:107], 9, v[104:105]
	v_lshl_add_u64 v[106:107], s[66:67], 0, v[106:107]
	v_lshl_add_u64 v[106:107], v[106:107], 0, s[18:19]
	v_lshl_add_u64 v[106:107], v[106:107], 0, v[184:185]
	global_store_dwordx4 v[106:107], v[108:111], off sc1
	v_cvt_pk_bf16_f32 v100, v100, v101
	v_cvt_pk_bf16_f32 v101, v102, v103
	v_cvt_pk_bf16_f32 v102, v92, v93
	v_add_u32_e32 v92, 1, v104
	v_ashrrev_i32_e32 v93, 31, v92
	v_lshlrev_b64 v[92:93], 9, v[92:93]
	v_lshl_add_u64 v[92:93], s[66:67], 0, v[92:93]
	v_lshl_add_u64 v[92:93], v[92:93], 0, s[18:19]
	v_lshl_add_u64 v[92:93], v[92:93], 0, v[184:185]
	v_cvt_pk_bf16_f32 v103, v94, v95
	global_store_dwordx4 v[92:93], v[100:103], off sc1
	v_cvt_pk_bf16_f32 v92, v96, v97
	v_cvt_pk_bf16_f32 v93, v98, v99
	v_cvt_pk_bf16_f32 v94, v88, v89
	v_add_u32_e32 v88, s9, v139
	v_ashrrev_i32_e32 v89, 31, v88
	v_cvt_pk_bf16_f32 v95, v90, v91
	v_lshlrev_b64 v[90:91], 9, v[88:89]
	v_lshl_add_u64 v[90:91], s[66:67], 0, v[90:91]
	v_lshl_add_u64 v[90:91], v[90:91], 0, s[18:19]
	v_lshl_add_u64 v[90:91], v[90:91], 0, v[184:185]
	global_store_dwordx4 v[90:91], v[92:95], off sc1
	v_cvt_pk_bf16_f32 v84, v84, v85
	v_cvt_pk_bf16_f32 v85, v86, v87
	v_cvt_pk_bf16_f32 v86, v76, v77
	v_add_u32_e32 v76, 1, v88
	v_ashrrev_i32_e32 v77, 31, v76
	v_lshlrev_b64 v[76:77], 9, v[76:77]
	v_lshl_add_u64 v[76:77], s[66:67], 0, v[76:77]
	v_lshl_add_u64 v[76:77], v[76:77], 0, s[18:19]
	v_lshl_add_u64 v[76:77], v[76:77], 0, v[184:185]
	v_cvt_pk_bf16_f32 v87, v78, v79
	global_store_dwordx4 v[76:77], v[84:87], off sc1
	v_cvt_pk_bf16_f32 v76, v80, v81
	v_cvt_pk_bf16_f32 v77, v82, v83
	v_cvt_pk_bf16_f32 v78, v72, v73
	v_add_u32_e32 v72, s9, v140
	v_ashrrev_i32_e32 v73, 31, v72
	v_cvt_pk_bf16_f32 v79, v74, v75
	v_lshlrev_b64 v[74:75], 9, v[72:73]
	v_lshl_add_u64 v[74:75], s[66:67], 0, v[74:75]
	v_lshl_add_u64 v[74:75], v[74:75], 0, s[18:19]
	v_lshl_add_u64 v[74:75], v[74:75], 0, v[184:185]
	global_store_dwordx4 v[74:75], v[76:79], off sc1
	v_cvt_pk_bf16_f32 v68, v68, v69
	v_cvt_pk_bf16_f32 v69, v70, v71
	v_cvt_pk_bf16_f32 v70, v64, v65
	v_add_u32_e32 v64, 1, v72
	v_ashrrev_i32_e32 v65, 31, v64
	v_lshlrev_b64 v[64:65], 9, v[64:65]
	v_lshl_add_u64 v[64:65], s[66:67], 0, v[64:65]
	v_lshl_add_u64 v[64:65], v[64:65], 0, s[18:19]
	v_lshl_add_u64 v[64:65], v[64:65], 0, v[184:185]
	v_cvt_pk_bf16_f32 v71, v66, v67
	global_store_dwordx4 v[64:65], v[68:71], off sc1
	v_cvt_pk_bf16_f32 v60, v60, v61
	v_cvt_pk_bf16_f32 v61, v62, v63
	v_cvt_pk_bf16_f32 v62, v56, v57
	v_add_u32_e32 v56, s9, v141
	v_ashrrev_i32_e32 v57, 31, v56
	v_cvt_pk_bf16_f32 v63, v58, v59
	v_lshlrev_b64 v[58:59], 9, v[56:57]
	v_lshl_add_u64 v[58:59], s[66:67], 0, v[58:59]
	v_lshl_add_u64 v[58:59], v[58:59], 0, s[18:19]
	v_lshl_add_u64 v[58:59], v[58:59], 0, v[184:185]
	global_store_dwordx4 v[58:59], v[60:63], off sc1
	v_cvt_pk_bf16_f32 v52, v52, v53
	v_cvt_pk_bf16_f32 v53, v54, v55
	v_cvt_pk_bf16_f32 v54, v44, v45
	v_add_u32_e32 v44, 1, v56
	v_ashrrev_i32_e32 v45, 31, v44
	v_lshlrev_b64 v[44:45], 9, v[44:45]
	v_lshl_add_u64 v[44:45], s[66:67], 0, v[44:45]
	v_lshl_add_u64 v[44:45], v[44:45], 0, s[18:19]
	v_lshl_add_u64 v[44:45], v[44:45], 0, v[184:185]
	v_cvt_pk_bf16_f32 v55, v46, v47
	global_store_dwordx4 v[44:45], v[52:55], off sc1
	v_cvt_pk_bf16_f32 v44, v48, v49
	v_cvt_pk_bf16_f32 v45, v50, v51
	v_cvt_pk_bf16_f32 v46, v40, v41
	v_add_u32_e32 v40, s9, v142
	v_ashrrev_i32_e32 v41, 31, v40
	v_cvt_pk_bf16_f32 v47, v42, v43
	v_lshlrev_b64 v[42:43], 9, v[40:41]
	v_lshl_add_u64 v[42:43], s[66:67], 0, v[42:43]
	v_lshl_add_u64 v[42:43], v[42:43], 0, s[18:19]
	v_lshl_add_u64 v[42:43], v[42:43], 0, v[184:185]
	global_store_dwordx4 v[42:43], v[44:47], off sc1
	v_cvt_pk_bf16_f32 v36, v36, v37
	v_cvt_pk_bf16_f32 v37, v38, v39
	v_cvt_pk_bf16_f32 v38, v28, v29
	v_add_u32_e32 v28, 1, v40
	v_ashrrev_i32_e32 v29, 31, v28
	v_lshlrev_b64 v[28:29], 9, v[28:29]
	v_lshl_add_u64 v[28:29], s[66:67], 0, v[28:29]
	v_lshl_add_u64 v[28:29], v[28:29], 0, s[18:19]
	v_lshl_add_u64 v[28:29], v[28:29], 0, v[184:185]
	v_cvt_pk_bf16_f32 v39, v30, v31
	global_store_dwordx4 v[28:29], v[36:39], off sc1
	v_cvt_pk_bf16_f32 v28, v32, v33
	v_cvt_pk_bf16_f32 v29, v34, v35
	v_cvt_pk_bf16_f32 v30, v24, v25
	v_add_u32_e32 v24, s9, v143
	v_ashrrev_i32_e32 v25, 31, v24
	v_cvt_pk_bf16_f32 v31, v26, v27
	v_lshlrev_b64 v[26:27], 9, v[24:25]
	v_lshl_add_u64 v[26:27], s[66:67], 0, v[26:27]
	v_lshl_add_u64 v[26:27], v[26:27], 0, s[18:19]
	v_lshl_add_u64 v[26:27], v[26:27], 0, v[184:185]
	global_store_dwordx4 v[26:27], v[28:31], off sc1
	v_cvt_pk_bf16_f32 v20, v20, v21
	v_cvt_pk_bf16_f32 v21, v22, v23
	v_cvt_pk_bf16_f32 v22, v12, v13
	v_add_u32_e32 v12, 1, v24
	v_ashrrev_i32_e32 v13, 31, v12
	v_lshlrev_b64 v[12:13], 9, v[12:13]
	v_lshl_add_u64 v[12:13], s[66:67], 0, v[12:13]
	v_lshl_add_u64 v[12:13], v[12:13], 0, s[18:19]
	v_lshl_add_u64 v[12:13], v[12:13], 0, v[184:185]
	v_cvt_pk_bf16_f32 v23, v14, v15
	global_store_dwordx4 v[12:13], v[20:23], off sc1
	v_cvt_pk_bf16_f32 v12, v16, v17
	v_cvt_pk_bf16_f32 v13, v18, v19
	v_cvt_pk_bf16_f32 v14, v8, v9
	v_add_u32_e32 v8, s9, v144
	v_ashrrev_i32_e32 v9, 31, v8
	v_cvt_pk_bf16_f32 v15, v10, v11
	v_lshlrev_b64 v[10:11], 9, v[8:9]
	v_lshl_add_u64 v[10:11], s[66:67], 0, v[10:11]
	v_lshl_add_u64 v[10:11], v[10:11], 0, s[18:19]
	v_lshl_add_u64 v[10:11], v[10:11], 0, v[184:185]
	global_store_dwordx4 v[10:11], v[12:15], off sc1
	v_cvt_pk_bf16_f32 v4, v4, v5
	v_cvt_pk_bf16_f32 v5, v6, v7
	v_cvt_pk_bf16_f32 v6, v0, v1
	v_add_u32_e32 v0, 1, v8
	v_ashrrev_i32_e32 v1, 31, v0
	v_lshlrev_b64 v[0:1], 9, v[0:1]
	v_lshl_add_u64 v[0:1], s[66:67], 0, v[0:1]
	v_lshl_add_u64 v[0:1], v[0:1], 0, s[18:19]
	v_readlane_b32 s90, v255, 34
	v_lshl_add_u64 v[0:1], v[0:1], 0, v[184:185]
	s_andn2_b64 vcc, exec, s[12:13]
	s_mov_b64 s[12:13], -1
	v_readlane_b32 s91, v255, 35
	v_readlane_b32 s88, v255, 38
	v_readlane_b32 s48, v252, 42
	v_cvt_pk_bf16_f32 v7, v2, v3
	global_store_dwordx4 v[0:1], v[4:7], off sc1
	v_readlane_b32 s89, v255, 39
	s_cbranch_vccnz .LBB0_510
	s_andn2_b64 vcc, exec, s[0:1]
	s_cbranch_vccnz .LBB0_509
	s_barrier
	s_branch .LBB0_509

.LBB0_534:
	v_lshl_add_u32 v136, s62, 8, v138
	s_lshl_b32 s16, s63, 8
	v_ashrrev_i32_e32 v137, 31, v136
	v_readlane_b32 s18, v253, 59
	s_ashr_i32 s17, s16, 31
	v_lshlrev_b64 v[142:143], 10, v[136:137]
	v_readlane_b32 s19, v253, 60
	v_cvt_pk_bf16_f32 v124, v124, v125
	v_cvt_pk_bf16_f32 v125, v126, v127
	v_cvt_pk_bf16_f32 v126, v120, v121
	s_lshl_b64 s[16:17], s[16:17], 1
	v_cvt_pk_bf16_f32 v127, v122, v123
	s_nop 0
	v_lshl_add_u64 v[120:121], s[18:19], 0, v[142:143]
	v_lshl_add_u64 v[120:121], v[120:121], 0, s[16:17]
	v_lshl_add_u64 v[120:121], v[120:121], 0, v[184:185]
	global_store_dwordx4 v[120:121], v[124:127], off sc1
	v_cvt_pk_bf16_f32 v112, v112, v113
	v_cvt_pk_bf16_f32 v113, v114, v115
	v_cvt_pk_bf16_f32 v114, v104, v105
	v_or_b32_e32 v104, 16, v136
	v_ashrrev_i32_e32 v105, 31, v104
	v_cvt_pk_bf16_f32 v115, v106, v107
	global_store_dwordx4 v[120:121], v[112:115], off offset:256 sc1
	v_readlane_b32 s92, v255, 32
	v_readlane_b32 s94, v255, 36
	v_lshlrev_b64 v[112:113], 10, v[104:105]
	v_cvt_pk_bf16_f32 v104, v116, v117
	v_cvt_pk_bf16_f32 v105, v118, v119
	v_cvt_pk_bf16_f32 v106, v108, v109
	v_lshl_add_u64 v[108:109], s[18:19], 0, v[112:113]
	v_lshl_add_u64 v[108:109], v[108:109], 0, s[16:17]
	v_lshl_add_u64 v[108:109], v[108:109], 0, v[184:185]
	v_cvt_pk_bf16_f32 v107, v110, v111
	global_store_dwordx4 v[108:109], v[104:107], off sc1
	v_cvt_pk_bf16_f32 v96, v96, v97
	v_cvt_pk_bf16_f32 v97, v98, v99
	v_cvt_pk_bf16_f32 v98, v88, v89
	v_or_b32_e32 v88, 32, v136
	v_ashrrev_i32_e32 v89, 31, v88
	v_cvt_pk_bf16_f32 v99, v90, v91
	global_store_dwordx4 v[108:109], v[96:99], off offset:256 sc1
	s_andn2_b64 vcc, exec, s[10:11]
	s_mov_b64 s[10:11], -1
	v_lshlrev_b64 v[96:97], 10, v[88:89]
	v_cvt_pk_bf16_f32 v88, v100, v101
	v_cvt_pk_bf16_f32 v89, v102, v103
	v_cvt_pk_bf16_f32 v90, v92, v93
	v_lshl_add_u64 v[92:93], s[18:19], 0, v[96:97]
	v_lshl_add_u64 v[92:93], v[92:93], 0, s[16:17]
	v_lshl_add_u64 v[92:93], v[92:93], 0, v[184:185]
	v_cvt_pk_bf16_f32 v91, v94, v95
	global_store_dwordx4 v[92:93], v[88:91], off sc1
	v_cvt_pk_bf16_f32 v80, v80, v81
	v_cvt_pk_bf16_f32 v81, v82, v83
	v_cvt_pk_bf16_f32 v82, v72, v73
	v_or_b32_e32 v72, 48, v136
	v_ashrrev_i32_e32 v73, 31, v72
	v_cvt_pk_bf16_f32 v83, v74, v75
	global_store_dwordx4 v[92:93], v[80:83], off offset:256 sc1
	v_readlane_b32 s93, v255, 33
	v_readlane_b32 s95, v255, 37
	v_lshlrev_b64 v[80:81], 10, v[72:73]
	v_cvt_pk_bf16_f32 v72, v84, v85
	v_cvt_pk_bf16_f32 v73, v86, v87
	v_cvt_pk_bf16_f32 v74, v76, v77
	v_lshl_add_u64 v[76:77], s[18:19], 0, v[80:81]
	v_lshl_add_u64 v[76:77], v[76:77], 0, s[16:17]
	v_lshl_add_u64 v[76:77], v[76:77], 0, v[184:185]
	v_cvt_pk_bf16_f32 v75, v78, v79
	global_store_dwordx4 v[76:77], v[72:75], off sc1
	v_cvt_pk_bf16_f32 v68, v68, v69
	v_cvt_pk_bf16_f32 v69, v70, v71
	v_cvt_pk_bf16_f32 v70, v64, v65
	v_add_u32_e32 v64, 0x80, v136
	v_ashrrev_i32_e32 v65, 31, v64
	v_lshlrev_b64 v[64:65], 10, v[64:65]
	v_cvt_pk_bf16_f32 v71, v66, v67
	global_store_dwordx4 v[76:77], v[68:71], off offset:256 sc1
	v_cvt_pk_bf16_f32 v60, v60, v61
	v_cvt_pk_bf16_f32 v61, v62, v63
	v_cvt_pk_bf16_f32 v62, v56, v57
	v_lshl_add_u64 v[56:57], s[18:19], 0, v[64:65]
	v_lshl_add_u64 v[56:57], v[56:57], 0, s[16:17]
	v_lshl_add_u64 v[56:57], v[56:57], 0, v[184:185]
	v_cvt_pk_bf16_f32 v63, v58, v59
	global_store_dwordx4 v[56:57], v[60:63], off sc1
	v_cvt_pk_bf16_f32 v48, v48, v49
	v_cvt_pk_bf16_f32 v49, v50, v51
	v_cvt_pk_bf16_f32 v50, v40, v41
	v_add_u32_e32 v40, 0x90, v136
	v_ashrrev_i32_e32 v41, 31, v40
	v_cvt_pk_bf16_f32 v51, v42, v43
	global_store_dwordx4 v[56:57], v[48:51], off offset:256 sc1
	v_readlane_b32 s88, v255, 38
	v_readlane_b32 s48, v252, 42
	v_lshlrev_b64 v[48:49], 10, v[40:41]
	v_cvt_pk_bf16_f32 v40, v52, v53
	v_cvt_pk_bf16_f32 v41, v54, v55
	v_cvt_pk_bf16_f32 v42, v44, v45
	v_lshl_add_u64 v[44:45], s[18:19], 0, v[48:49]
	v_lshl_add_u64 v[44:45], v[44:45], 0, s[16:17]
	v_lshl_add_u64 v[44:45], v[44:45], 0, v[184:185]
	v_cvt_pk_bf16_f32 v43, v46, v47
	global_store_dwordx4 v[44:45], v[40:43], off sc1
	v_cvt_pk_bf16_f32 v32, v32, v33
	v_cvt_pk_bf16_f32 v33, v34, v35
	v_cvt_pk_bf16_f32 v34, v24, v25
	v_add_u32_e32 v24, 0xa0, v136
	v_ashrrev_i32_e32 v25, 31, v24
	v_cvt_pk_bf16_f32 v35, v26, v27
	global_store_dwordx4 v[44:45], v[32:35], off offset:256 sc1
	v_readlane_b32 s89, v255, 39
	s_nop 0
	v_lshlrev_b64 v[32:33], 10, v[24:25]
	v_cvt_pk_bf16_f32 v24, v36, v37
	v_cvt_pk_bf16_f32 v25, v38, v39
	v_cvt_pk_bf16_f32 v26, v28, v29
	v_lshl_add_u64 v[28:29], s[18:19], 0, v[32:33]
	v_lshl_add_u64 v[28:29], v[28:29], 0, s[16:17]
	v_lshl_add_u64 v[28:29], v[28:29], 0, v[184:185]
	v_cvt_pk_bf16_f32 v27, v30, v31
	global_store_dwordx4 v[28:29], v[24:27], off sc1
	v_cvt_pk_bf16_f32 v16, v16, v17
	v_cvt_pk_bf16_f32 v17, v18, v19
	v_cvt_pk_bf16_f32 v18, v8, v9
	v_add_u32_e32 v8, 0xb0, v136
	v_ashrrev_i32_e32 v9, 31, v8
	v_cvt_pk_bf16_f32 v19, v10, v11
	global_store_dwordx4 v[28:29], v[16:19], off offset:256 sc1
	s_nop 1
	v_lshlrev_b64 v[16:17], 10, v[8:9]
	v_cvt_pk_bf16_f32 v8, v20, v21
	v_cvt_pk_bf16_f32 v9, v22, v23
	v_cvt_pk_bf16_f32 v10, v12, v13
	v_lshl_add_u64 v[12:13], s[18:19], 0, v[16:17]
	v_lshl_add_u64 v[12:13], v[12:13], 0, s[16:17]
	v_lshl_add_u64 v[12:13], v[12:13], 0, v[184:185]
	v_cvt_pk_bf16_f32 v11, v14, v15
	global_store_dwordx4 v[12:13], v[8:11], off sc1
	v_cvt_pk_bf16_f32 v4, v4, v5
	v_cvt_pk_bf16_f32 v5, v6, v7
	v_cvt_pk_bf16_f32 v6, v0, v1
	v_cvt_pk_bf16_f32 v7, v2, v3
	global_store_dwordx4 v[12:13], v[4:7], off offset:256 sc1
	s_cbranch_vccnz .LBB0_527
	s_andn2_b64 vcc, exec, s[0:1]
	s_cbranch_vccnz .LBB0_526
	s_barrier
	s_branch .LBB0_526

.LBB0_602:
	v_mov_b32_e32 v137, v144
	v_mov_b32_e32 v142, v124
	v_mul_lo_u32 v152, v137, v146
	v_cvt_f32_i32_e32 v140, v152
	v_mov_b32_e32 v143, v120
	v_add_u32_e32 v156, v152, v137
	v_mul_lo_u32 v138, v137, v147
	v_mul_f32_e32 v141, 0x38800000, v140
	v_cos_f32_e32 v140, v141
	v_sin_f32_e32 v141, v141
	v_cvt_f32_i32_e32 v138, v138
	s_lshl_b32 s9, s53, 1
	s_and_b32 s16, s53, 0xffffff80
	v_pk_mul_f32 v[142:143], v[142:143], v[140:141]
	v_mul_f32_e32 v139, 0x38800000, v138
	v_add_f32_e32 v154, v142, v143
	v_mov_b32_e32 v142, v120
	v_cvt_f32_i32_e32 v120, v156
	v_mov_b32_e32 v143, v124
	v_pk_mul_f32 v[142:143], v[142:143], v[140:141]
	v_mov_b32_e32 v124, v121
	v_mul_f32_e32 v120, 0x38800000, v120
	v_sub_f32_e32 v155, v142, v143
	v_cos_f32_e32 v142, v120
	v_sin_f32_e32 v143, v120
	v_mov_b32_e32 v120, v125
	v_cos_f32_e32 v138, v139
	v_sin_f32_e32 v139, v139
	v_pk_mul_f32 v[152:153], v[120:121], v[142:143]
	v_pk_mul_f32 v[120:121], v[124:125], v[142:143]
	v_add_f32_e32 v157, v152, v153
	v_add_u32_e32 v152, v156, v137
	v_sub_f32_e32 v158, v120, v121
	v_cvt_f32_i32_e32 v120, v152
	v_mov_b32_e32 v124, v126
	v_mov_b32_e32 v125, v122
	v_add_u32_e32 v160, v152, v137
	v_mul_f32_e32 v121, 0x38800000, v120
	v_cos_f32_e32 v120, v121
	v_sin_f32_e32 v121, v121
	s_and_b32 s9, s9, 0xfe
	v_add_u32_e32 v136, s16, v137
	v_lshl_or_b32 v136, v136, 8, s9
	v_pk_mul_f32 v[124:125], v[124:125], v[120:121]
	v_readlane_b32 s62, v255, 40
	v_add_f32_e32 v156, v124, v125
	v_mov_b32_e32 v124, v122
	v_cvt_f32_i32_e32 v122, v160
	v_mov_b32_e32 v125, v126
	v_pk_mul_f32 v[124:125], v[124:125], v[120:121]
	v_mov_b32_e32 v126, v123
	v_mul_f32_e32 v122, 0x38800000, v122
	v_sub_f32_e32 v159, v124, v125
	v_cos_f32_e32 v124, v122
	v_sin_f32_e32 v125, v122
	v_mov_b32_e32 v122, v127
	v_lshl_add_u32 v160, v137, 1, v160
	s_andn2_b64 vcc, exec, s[14:15]
	v_pk_mul_f32 v[152:153], v[122:123], v[124:125]
	v_pk_mul_f32 v[122:123], v[126:127], v[124:125]
	v_add_f32_e32 v152, v152, v153
	v_sub_f32_e32 v153, v122, v123
	v_mov_b32_e32 v122, v116
	v_mov_b32_e32 v123, v112
	v_pk_mul_f32 v[122:123], v[122:123], v[138:139]
	v_readlane_b32 s63, v255, 41
	v_add_f32_e32 v161, v122, v123
	v_mov_b32_e32 v122, v112
	v_cvt_f32_i32_e32 v112, v160
	v_mov_b32_e32 v123, v116
	v_pk_mul_f32 v[122:123], v[122:123], v[138:139]
	v_mov_b32_e32 v116, v113
	v_mul_f32_e32 v112, 0x38800000, v112
	v_sub_f32_e32 v162, v122, v123
	v_cos_f32_e32 v122, v112
	v_sin_f32_e32 v123, v112
	v_mov_b32_e32 v112, v117
	v_readlane_b32 s48, v252, 42
	v_pk_mul_f32 v[126:127], v[112:113], v[122:123]
	s_nop 0
	v_add_f32_e32 v163, v126, v127
	v_pk_mul_f32 v[112:113], v[116:117], v[122:123]
	v_add_u32_e32 v126, v160, v137
	v_sub_f32_e32 v164, v112, v113
	v_cvt_f32_i32_e32 v112, v126
	v_mov_b32_e32 v113, v114
	v_mul_f32_e32 v112, 0x38800000, v112
	v_cos_f32_e32 v116, v112
	v_sin_f32_e32 v117, v112
	v_mov_b32_e32 v112, v118
	v_pk_mul_f32 v[112:113], v[112:113], v[116:117]
	s_nop 0
	v_add_f32_e32 v160, v112, v113
	v_mov_b32_e32 v112, v114
	v_mov_b32_e32 v113, v118
	v_pk_mul_f32 v[112:113], v[112:113], v[116:117]
	v_mov_b32_e32 v114, v119
	v_sub_f32_e32 v165, v112, v113
	v_add_u32_e32 v112, v126, v137
	v_cvt_f32_i32_e32 v112, v112
	v_mov_b32_e32 v118, v115
	v_ashrrev_i32_e32 v137, 31, v136
	v_mul_f32_e32 v112, 0x38800000, v112
	v_cos_f32_e32 v126, v112
	v_sin_f32_e32 v127, v112
	s_nop 0
	v_pk_mul_f32 v[112:113], v[114:115], v[126:127]
	s_nop 0
	v_add_f32_e32 v166, v112, v113
	v_pk_mul_f32 v[112:113], v[118:119], v[126:127]
	s_nop 0
	v_sub_f32_e32 v167, v112, v113
	v_lshlrev_b64 v[112:113], 9, v[136:137]
	v_lshl_add_u64 v[118:119], v[134:135], 0, v[112:113]
	v_cvt_pk_bf16_f32 v112, v154, v157
	v_cvt_pk_bf16_f32 v113, v156, v152
	v_cvt_pk_bf16_f32 v114, v161, v163
	v_cvt_pk_bf16_f32 v115, v160, v166
	global_store_dwordx4 v[118:119], v[112:115], off sc1
	s_nop 1
	v_cvt_pk_bf16_f32 v112, v155, v158
	v_cvt_pk_bf16_f32 v113, v159, v153
	v_cvt_pk_bf16_f32 v114, v162, v164
	v_cvt_pk_bf16_f32 v115, v165, v167
	global_store_dwordx4 v[118:119], v[112:115], off offset:256 sc1
	s_nop 1
	v_mov_b32_e32 v112, v108
	v_mov_b32_e32 v113, v100
	v_pk_mul_f32 v[112:113], v[112:113], v[140:141]
	s_nop 0
	v_add_f32_e32 v114, v112, v113
	v_mov_b32_e32 v112, v100
	v_mov_b32_e32 v113, v108
	v_pk_mul_f32 v[112:113], v[112:113], v[140:141]
	v_mov_b32_e32 v100, v109
	v_mov_b32_e32 v108, v101
	v_sub_f32_e32 v115, v112, v113
	v_pk_mul_f32 v[112:113], v[100:101], v[142:143]
	v_pk_mul_f32 v[100:101], v[108:109], v[142:143]
	v_add_f32_e32 v112, v112, v113
	v_sub_f32_e32 v108, v100, v101
	v_mov_b32_e32 v100, v110
	v_mov_b32_e32 v101, v102
	v_pk_mul_f32 v[100:101], v[100:101], v[120:121]
	s_nop 0
	v_add_f32_e32 v109, v100, v101
	v_mov_b32_e32 v100, v102
	v_mov_b32_e32 v101, v110
	v_pk_mul_f32 v[100:101], v[100:101], v[120:121]
	v_mov_b32_e32 v102, v111
	v_sub_f32_e32 v113, v100, v101
	v_pk_mul_f32 v[100:101], v[102:103], v[124:125]
	v_mov_b32_e32 v110, v103
	v_add_f32_e32 v102, v100, v101
	v_pk_mul_f32 v[100:101], v[110:111], v[124:125]
	s_nop 0
	v_sub_f32_e32 v103, v100, v101
	v_mov_b32_e32 v100, v104
	v_mov_b32_e32 v101, v96
	v_pk_mul_f32 v[100:101], v[100:101], v[138:139]
	s_nop 0
	v_add_f32_e32 v110, v100, v101
	v_mov_b32_e32 v100, v96
	v_mov_b32_e32 v101, v104
	v_pk_mul_f32 v[100:101], v[100:101], v[138:139]
	v_mov_b32_e32 v96, v105
	v_mov_b32_e32 v104, v97
	v_sub_f32_e32 v111, v100, v101
	v_pk_mul_f32 v[100:101], v[96:97], v[122:123]
	v_pk_mul_f32 v[96:97], v[104:105], v[122:123]
	v_add_f32_e32 v118, v100, v101
	v_sub_f32_e32 v104, v96, v97
	v_mov_b32_e32 v96, v106
	v_mov_b32_e32 v97, v98
	v_pk_mul_f32 v[96:97], v[96:97], v[116:117]
	s_nop 0
	v_add_f32_e32 v105, v96, v97
	v_mov_b32_e32 v96, v98
	v_mov_b32_e32 v97, v106
	v_pk_mul_f32 v[96:97], v[96:97], v[116:117]
	v_mov_b32_e32 v98, v107
	v_sub_f32_e32 v116, v96, v97
	v_pk_mul_f32 v[96:97], v[98:99], v[126:127]
	v_mov_b32_e32 v106, v99
	v_add_f32_e32 v117, v96, v97
	v_pk_mul_f32 v[96:97], v[106:107], v[126:127]
	s_nop 0
	v_sub_f32_e32 v106, v96, v97
	v_or_b32_e32 v96, 1, v136
	v_ashrrev_i32_e32 v97, 31, v96
	v_lshlrev_b64 v[96:97], 9, v[96:97]
	v_lshl_add_u64 v[100:101], v[134:135], 0, v[96:97]
	v_cvt_pk_bf16_f32 v96, v114, v112
	v_cvt_pk_bf16_f32 v97, v109, v102
	v_cvt_pk_bf16_f32 v98, v110, v118
	v_cvt_pk_bf16_f32 v99, v105, v117
	global_store_dwordx4 v[100:101], v[96:99], off sc1
	v_mov_b32_e32 v102, v92
	s_nop 0
	v_cvt_pk_bf16_f32 v96, v115, v108
	v_cvt_pk_bf16_f32 v97, v113, v103
	v_cvt_pk_bf16_f32 v98, v111, v104
	v_cvt_pk_bf16_f32 v99, v116, v106
	global_store_dwordx4 v[100:101], v[96:99], off offset:256 sc1
	v_mov_b32_e32 v103, v88
	s_nop 0
	v_mov_b32_e32 v97, v148
	s_nop 0
	v_mul_lo_u32 v104, v97, v146
	v_cvt_f32_i32_e32 v100, v104
	v_add_u32_e32 v108, v104, v97
	v_mul_lo_u32 v98, v97, v147
	v_cvt_f32_i32_e32 v98, v98
	v_mul_f32_e32 v101, 0x38800000, v100
	v_cos_f32_e32 v100, v101
	v_sin_f32_e32 v101, v101
	v_mul_f32_e32 v99, 0x38800000, v98
	v_cos_f32_e32 v98, v99
	v_sin_f32_e32 v99, v99
	v_pk_mul_f32 v[102:103], v[102:103], v[100:101]
	v_add_u32_e32 v96, s16, v97
	v_add_f32_e32 v106, v102, v103
	v_mov_b32_e32 v102, v88
	v_cvt_f32_i32_e32 v88, v108
	v_mov_b32_e32 v103, v92
	v_pk_mul_f32 v[102:103], v[102:103], v[100:101]
	v_mov_b32_e32 v92, v89
	v_mul_f32_e32 v88, 0x38800000, v88
	v_sub_f32_e32 v107, v102, v103
	v_cos_f32_e32 v102, v88
	v_sin_f32_e32 v103, v88
	v_mov_b32_e32 v88, v93
	v_lshl_or_b32 v96, v96, 8, s9
	v_pk_mul_f32 v[104:105], v[88:89], v[102:103]
	s_nop 0
	v_add_f32_e32 v109, v104, v105
	v_pk_mul_f32 v[88:89], v[92:93], v[102:103]
	v_add_u32_e32 v104, v108, v97
	v_sub_f32_e32 v110, v88, v89
	v_cvt_f32_i32_e32 v88, v104
	v_mov_b32_e32 v92, v94
	v_mov_b32_e32 v93, v90
	v_add_u32_e32 v112, v104, v97
	v_mul_f32_e32 v89, 0x38800000, v88
	v_cos_f32_e32 v88, v89
	v_sin_f32_e32 v89, v89
	s_nop 0
	v_pk_mul_f32 v[92:93], v[92:93], v[88:89]
	s_nop 0
	v_add_f32_e32 v108, v92, v93
	v_mov_b32_e32 v92, v90
	v_cvt_f32_i32_e32 v90, v112
	v_mov_b32_e32 v93, v94
	v_pk_mul_f32 v[92:93], v[92:93], v[88:89]
	v_mov_b32_e32 v94, v91
	v_mul_f32_e32 v90, 0x38800000, v90
	v_sub_f32_e32 v111, v92, v93
	v_cos_f32_e32 v92, v90
	v_sin_f32_e32 v93, v90
	v_mov_b32_e32 v90, v95
	v_lshl_add_u32 v112, v97, 1, v112
	v_pk_mul_f32 v[104:105], v[90:91], v[92:93]
	v_pk_mul_f32 v[90:91], v[94:95], v[92:93]
	v_add_f32_e32 v104, v104, v105
	v_sub_f32_e32 v105, v90, v91
	v_mov_b32_e32 v90, v84
	v_mov_b32_e32 v91, v80
	v_pk_mul_f32 v[90:91], v[90:91], v[98:99]
	s_nop 0
	v_add_f32_e32 v113, v90, v91
	v_mov_b32_e32 v90, v80
	v_cvt_f32_i32_e32 v80, v112
	v_mov_b32_e32 v91, v84
	v_pk_mul_f32 v[90:91], v[90:91], v[98:99]
	v_mov_b32_e32 v84, v81
	v_mul_f32_e32 v80, 0x38800000, v80
	v_sub_f32_e32 v114, v90, v91
	v_cos_f32_e32 v90, v80
	v_sin_f32_e32 v91, v80
	v_mov_b32_e32 v80, v85
	v_pk_mul_f32 v[94:95], v[80:81], v[90:91]
	s_nop 0
	v_add_f32_e32 v115, v94, v95
	v_pk_mul_f32 v[80:81], v[84:85], v[90:91]
	v_add_u32_e32 v94, v112, v97
	v_sub_f32_e32 v116, v80, v81
	v_cvt_f32_i32_e32 v80, v94
	v_mov_b32_e32 v81, v82
	v_mul_f32_e32 v80, 0x38800000, v80
	v_cos_f32_e32 v84, v80
	v_sin_f32_e32 v85, v80
	v_mov_b32_e32 v80, v86
	v_pk_mul_f32 v[80:81], v[80:81], v[84:85]
	s_nop 0
	v_add_f32_e32 v112, v80, v81
	v_mov_b32_e32 v80, v82
	v_mov_b32_e32 v81, v86
	v_pk_mul_f32 v[80:81], v[80:81], v[84:85]
	v_mov_b32_e32 v82, v87
	v_sub_f32_e32 v117, v80, v81
	v_add_u32_e32 v80, v94, v97
	v_cvt_f32_i32_e32 v80, v80
	v_mov_b32_e32 v86, v83
	v_ashrrev_i32_e32 v97, 31, v96
	v_mul_f32_e32 v80, 0x38800000, v80
	v_cos_f32_e32 v94, v80
	v_sin_f32_e32 v95, v80
	s_nop 0
	v_pk_mul_f32 v[80:81], v[82:83], v[94:95]
	s_nop 0
	v_add_f32_e32 v118, v80, v81
	v_pk_mul_f32 v[80:81], v[86:87], v[94:95]
	s_nop 0
	v_sub_f32_e32 v119, v80, v81
	v_lshlrev_b64 v[80:81], 9, v[96:97]
	v_lshl_add_u64 v[86:87], v[134:135], 0, v[80:81]
	v_cvt_pk_bf16_f32 v80, v106, v109
	v_cvt_pk_bf16_f32 v81, v108, v104
	v_cvt_pk_bf16_f32 v82, v113, v115
	v_cvt_pk_bf16_f32 v83, v112, v118
	global_store_dwordx4 v[86:87], v[80:83], off sc1
	s_nop 1
	v_cvt_pk_bf16_f32 v80, v107, v110
	v_cvt_pk_bf16_f32 v81, v111, v105
	v_cvt_pk_bf16_f32 v82, v114, v116
	v_cvt_pk_bf16_f32 v83, v117, v119
	global_store_dwordx4 v[86:87], v[80:83], off offset:256 sc1
	s_nop 1
	v_mov_b32_e32 v80, v76
	v_mov_b32_e32 v81, v68
	v_pk_mul_f32 v[80:81], v[80:81], v[100:101]
	s_nop 0
	v_add_f32_e32 v82, v80, v81
	v_mov_b32_e32 v80, v68
	v_mov_b32_e32 v81, v76
	v_pk_mul_f32 v[80:81], v[80:81], v[100:101]
	v_mov_b32_e32 v68, v77
	v_mov_b32_e32 v76, v69
	v_sub_f32_e32 v83, v80, v81
	v_pk_mul_f32 v[80:81], v[68:69], v[102:103]
	v_pk_mul_f32 v[68:69], v[76:77], v[102:103]
	v_add_f32_e32 v80, v80, v81
	v_sub_f32_e32 v76, v68, v69
	v_mov_b32_e32 v68, v78
	v_mov_b32_e32 v69, v70
	v_pk_mul_f32 v[68:69], v[68:69], v[88:89]
	s_nop 0
	v_add_f32_e32 v77, v68, v69
	v_mov_b32_e32 v68, v70
	v_mov_b32_e32 v69, v78
	v_pk_mul_f32 v[68:69], v[68:69], v[88:89]
	v_mov_b32_e32 v70, v79
	v_sub_f32_e32 v81, v68, v69
	v_pk_mul_f32 v[68:69], v[70:71], v[92:93]
	v_mov_b32_e32 v78, v71
	v_add_f32_e32 v70, v68, v69
	v_pk_mul_f32 v[68:69], v[78:79], v[92:93]
	s_nop 0
	v_sub_f32_e32 v71, v68, v69
	v_mov_b32_e32 v68, v72
	v_mov_b32_e32 v69, v64
	v_pk_mul_f32 v[68:69], v[68:69], v[98:99]
	s_nop 0
	v_add_f32_e32 v78, v68, v69
	v_mov_b32_e32 v68, v64
	v_mov_b32_e32 v69, v72
	v_pk_mul_f32 v[68:69], v[68:69], v[98:99]
	v_mov_b32_e32 v64, v73
	v_mov_b32_e32 v72, v65
	v_sub_f32_e32 v79, v68, v69
	v_pk_mul_f32 v[68:69], v[64:65], v[90:91]
	v_pk_mul_f32 v[64:65], v[72:73], v[90:91]
	v_add_f32_e32 v86, v68, v69
	v_sub_f32_e32 v72, v64, v65
	v_mov_b32_e32 v64, v74
	v_mov_b32_e32 v65, v66
	v_pk_mul_f32 v[64:65], v[64:65], v[84:85]
	s_nop 0
	v_add_f32_e32 v73, v64, v65
	v_mov_b32_e32 v64, v66
	v_mov_b32_e32 v65, v74
	v_pk_mul_f32 v[64:65], v[64:65], v[84:85]
	v_mov_b32_e32 v66, v75
	v_sub_f32_e32 v84, v64, v65
	v_pk_mul_f32 v[64:65], v[66:67], v[94:95]
	v_mov_b32_e32 v74, v67
	v_add_f32_e32 v85, v64, v65
	v_pk_mul_f32 v[64:65], v[74:75], v[94:95]
	s_nop 0
	v_sub_f32_e32 v74, v64, v65
	v_or_b32_e32 v64, 1, v96
	v_ashrrev_i32_e32 v65, 31, v64
	v_lshlrev_b64 v[64:65], 9, v[64:65]
	v_lshl_add_u64 v[68:69], v[134:135], 0, v[64:65]
	v_cvt_pk_bf16_f32 v64, v82, v80
	v_cvt_pk_bf16_f32 v65, v77, v70
	v_cvt_pk_bf16_f32 v66, v78, v86
	v_cvt_pk_bf16_f32 v67, v73, v85
	global_store_dwordx4 v[68:69], v[64:67], off sc1
	v_mov_b32_e32 v70, v60
	s_nop 0
	v_cvt_pk_bf16_f32 v64, v83, v76
	v_cvt_pk_bf16_f32 v65, v81, v71
	v_cvt_pk_bf16_f32 v66, v79, v72
	v_cvt_pk_bf16_f32 v67, v84, v74
	global_store_dwordx4 v[68:69], v[64:67], off offset:256 sc1
	v_mov_b32_e32 v71, v56
	s_nop 0
	v_mov_b32_e32 v65, v149
	s_nop 0
	v_mul_lo_u32 v72, v65, v146
	v_cvt_f32_i32_e32 v68, v72
	v_add_u32_e32 v76, v72, v65
	v_mul_lo_u32 v66, v65, v147
	v_cvt_f32_i32_e32 v66, v66
	v_mul_f32_e32 v69, 0x38800000, v68
	v_cos_f32_e32 v68, v69
	v_sin_f32_e32 v69, v69
	v_mul_f32_e32 v67, 0x38800000, v66
	v_cos_f32_e32 v66, v67
	v_sin_f32_e32 v67, v67
	v_pk_mul_f32 v[70:71], v[70:71], v[68:69]
	v_add_u32_e32 v64, s16, v65
	v_add_f32_e32 v74, v70, v71
	v_mov_b32_e32 v70, v56
	v_cvt_f32_i32_e32 v56, v76
	v_mov_b32_e32 v71, v60
	v_pk_mul_f32 v[70:71], v[70:71], v[68:69]
	v_mov_b32_e32 v60, v57
	v_mul_f32_e32 v56, 0x38800000, v56
	v_sub_f32_e32 v75, v70, v71
	v_cos_f32_e32 v70, v56
	v_sin_f32_e32 v71, v56
	v_mov_b32_e32 v56, v61
	v_lshl_or_b32 v64, v64, 8, s9
	v_pk_mul_f32 v[72:73], v[56:57], v[70:71]
	s_nop 0
	v_add_f32_e32 v77, v72, v73
	v_pk_mul_f32 v[56:57], v[60:61], v[70:71]
	v_add_u32_e32 v72, v76, v65
	v_sub_f32_e32 v78, v56, v57
	v_cvt_f32_i32_e32 v56, v72
	v_mov_b32_e32 v60, v62
	v_mov_b32_e32 v61, v58
	v_add_u32_e32 v80, v72, v65
	v_mul_f32_e32 v57, 0x38800000, v56
	v_cos_f32_e32 v56, v57
	v_sin_f32_e32 v57, v57
	s_nop 0
	v_pk_mul_f32 v[60:61], v[60:61], v[56:57]
	s_nop 0
	v_add_f32_e32 v76, v60, v61
	v_mov_b32_e32 v60, v58
	v_cvt_f32_i32_e32 v58, v80
	v_mov_b32_e32 v61, v62
	v_pk_mul_f32 v[60:61], v[60:61], v[56:57]
	v_mov_b32_e32 v62, v59
	v_mul_f32_e32 v58, 0x38800000, v58
	v_sub_f32_e32 v79, v60, v61
	v_cos_f32_e32 v60, v58
	v_sin_f32_e32 v61, v58
	v_mov_b32_e32 v58, v63
	v_lshl_add_u32 v80, v65, 1, v80
	v_pk_mul_f32 v[72:73], v[58:59], v[60:61]
	v_pk_mul_f32 v[58:59], v[62:63], v[60:61]
	v_add_f32_e32 v72, v72, v73
	v_sub_f32_e32 v73, v58, v59
	v_mov_b32_e32 v58, v52
	v_mov_b32_e32 v59, v48
	v_pk_mul_f32 v[58:59], v[58:59], v[66:67]
	s_nop 0
	v_add_f32_e32 v81, v58, v59
	v_mov_b32_e32 v58, v48
	v_cvt_f32_i32_e32 v48, v80
	v_mov_b32_e32 v59, v52
	v_pk_mul_f32 v[58:59], v[58:59], v[66:67]
	v_mov_b32_e32 v52, v49
	v_mul_f32_e32 v48, 0x38800000, v48
	v_sub_f32_e32 v82, v58, v59
	v_cos_f32_e32 v58, v48
	v_sin_f32_e32 v59, v48
	v_mov_b32_e32 v48, v53
	v_pk_mul_f32 v[62:63], v[48:49], v[58:59]
	s_nop 0
	v_add_f32_e32 v83, v62, v63
	v_pk_mul_f32 v[48:49], v[52:53], v[58:59]
	v_add_u32_e32 v62, v80, v65
	v_sub_f32_e32 v84, v48, v49
	v_cvt_f32_i32_e32 v48, v62
	v_mov_b32_e32 v49, v50
	v_mul_f32_e32 v48, 0x38800000, v48
	v_cos_f32_e32 v52, v48
	v_sin_f32_e32 v53, v48
	v_mov_b32_e32 v48, v54
	v_pk_mul_f32 v[48:49], v[48:49], v[52:53]
	s_nop 0
	v_add_f32_e32 v80, v48, v49
	v_mov_b32_e32 v48, v50
	v_mov_b32_e32 v49, v54
	v_pk_mul_f32 v[48:49], v[48:49], v[52:53]
	v_mov_b32_e32 v50, v55
	v_sub_f32_e32 v85, v48, v49
	v_add_u32_e32 v48, v62, v65
	v_cvt_f32_i32_e32 v48, v48
	v_mov_b32_e32 v54, v51
	v_ashrrev_i32_e32 v65, 31, v64
	v_mul_f32_e32 v48, 0x38800000, v48
	v_cos_f32_e32 v62, v48
	v_sin_f32_e32 v63, v48
	s_nop 0
	v_pk_mul_f32 v[48:49], v[50:51], v[62:63]
	s_nop 0
	v_add_f32_e32 v86, v48, v49
	v_pk_mul_f32 v[48:49], v[54:55], v[62:63]
	s_nop 0
	v_sub_f32_e32 v87, v48, v49
	v_lshlrev_b64 v[48:49], 9, v[64:65]
	v_lshl_add_u64 v[54:55], v[134:135], 0, v[48:49]
	v_cvt_pk_bf16_f32 v48, v74, v77
	v_cvt_pk_bf16_f32 v49, v76, v72
	v_cvt_pk_bf16_f32 v50, v81, v83
	v_cvt_pk_bf16_f32 v51, v80, v86
	global_store_dwordx4 v[54:55], v[48:51], off sc1
	s_nop 1
	v_cvt_pk_bf16_f32 v48, v75, v78
	v_cvt_pk_bf16_f32 v49, v79, v73
	v_cvt_pk_bf16_f32 v50, v82, v84
	v_cvt_pk_bf16_f32 v51, v85, v87
	global_store_dwordx4 v[54:55], v[48:51], off offset:256 sc1
	s_nop 1
	v_mov_b32_e32 v48, v44
	v_mov_b32_e32 v49, v36
	v_pk_mul_f32 v[48:49], v[48:49], v[68:69]
	s_nop 0
	v_add_f32_e32 v50, v48, v49
	v_mov_b32_e32 v48, v36
	v_mov_b32_e32 v49, v44
	v_pk_mul_f32 v[48:49], v[48:49], v[68:69]
	v_mov_b32_e32 v36, v45
	v_mov_b32_e32 v44, v37
	v_sub_f32_e32 v51, v48, v49
	v_pk_mul_f32 v[48:49], v[36:37], v[70:71]
	v_pk_mul_f32 v[36:37], v[44:45], v[70:71]
	v_add_f32_e32 v48, v48, v49
	v_sub_f32_e32 v44, v36, v37
	v_mov_b32_e32 v36, v46
	v_mov_b32_e32 v37, v38
	v_pk_mul_f32 v[36:37], v[36:37], v[56:57]
	s_nop 0
	v_add_f32_e32 v45, v36, v37
	v_mov_b32_e32 v36, v38
	v_mov_b32_e32 v37, v46
	v_pk_mul_f32 v[36:37], v[36:37], v[56:57]
	v_mov_b32_e32 v38, v47
	v_sub_f32_e32 v49, v36, v37
	v_pk_mul_f32 v[36:37], v[38:39], v[60:61]
	v_mov_b32_e32 v46, v39
	v_add_f32_e32 v38, v36, v37
	v_pk_mul_f32 v[36:37], v[46:47], v[60:61]
	s_nop 0
	v_sub_f32_e32 v39, v36, v37
	v_mov_b32_e32 v36, v40
	v_mov_b32_e32 v37, v32
	v_pk_mul_f32 v[36:37], v[36:37], v[66:67]
	s_nop 0
	v_add_f32_e32 v46, v36, v37
	v_mov_b32_e32 v36, v32
	v_mov_b32_e32 v37, v40
	v_pk_mul_f32 v[36:37], v[36:37], v[66:67]
	v_mov_b32_e32 v32, v41
	v_mov_b32_e32 v40, v33
	v_sub_f32_e32 v47, v36, v37
	v_pk_mul_f32 v[36:37], v[32:33], v[58:59]
	v_pk_mul_f32 v[32:33], v[40:41], v[58:59]
	v_add_f32_e32 v54, v36, v37
	v_sub_f32_e32 v40, v32, v33
	v_mov_b32_e32 v32, v42
	v_mov_b32_e32 v33, v34
	v_pk_mul_f32 v[32:33], v[32:33], v[52:53]
	s_nop 0
	v_add_f32_e32 v41, v32, v33
	v_mov_b32_e32 v32, v34
	v_mov_b32_e32 v33, v42
	v_pk_mul_f32 v[32:33], v[32:33], v[52:53]
	v_mov_b32_e32 v34, v43
	v_sub_f32_e32 v52, v32, v33
	v_pk_mul_f32 v[32:33], v[34:35], v[62:63]
	v_mov_b32_e32 v42, v35
	v_add_f32_e32 v53, v32, v33
	v_pk_mul_f32 v[32:33], v[42:43], v[62:63]
	s_nop 0
	v_sub_f32_e32 v42, v32, v33
	v_or_b32_e32 v32, 1, v64
	v_ashrrev_i32_e32 v33, 31, v32
	v_lshlrev_b64 v[32:33], 9, v[32:33]
	v_lshl_add_u64 v[36:37], v[134:135], 0, v[32:33]
	v_cvt_pk_bf16_f32 v32, v50, v48
	v_cvt_pk_bf16_f32 v33, v45, v38
	v_cvt_pk_bf16_f32 v34, v46, v54
	v_cvt_pk_bf16_f32 v35, v41, v53
	global_store_dwordx4 v[36:37], v[32:35], off sc1
	v_mov_b32_e32 v38, v28
	s_nop 0
	v_cvt_pk_bf16_f32 v32, v51, v44
	v_cvt_pk_bf16_f32 v33, v49, v39
	v_cvt_pk_bf16_f32 v34, v47, v40
	v_cvt_pk_bf16_f32 v35, v52, v42
	global_store_dwordx4 v[36:37], v[32:35], off offset:256 sc1
	v_mov_b32_e32 v39, v24
	s_nop 0
	v_mov_b32_e32 v33, v150
	s_nop 0
	v_mul_lo_u32 v40, v33, v146
	v_cvt_f32_i32_e32 v36, v40
	v_add_u32_e32 v44, v40, v33
	v_mul_lo_u32 v34, v33, v147
	v_cvt_f32_i32_e32 v34, v34
	v_mul_f32_e32 v37, 0x38800000, v36
	v_cos_f32_e32 v36, v37
	v_sin_f32_e32 v37, v37
	v_mul_f32_e32 v35, 0x38800000, v34
	v_cos_f32_e32 v34, v35
	v_sin_f32_e32 v35, v35
	v_pk_mul_f32 v[38:39], v[38:39], v[36:37]
	v_add_u32_e32 v32, s16, v33
	v_add_f32_e32 v42, v38, v39
	v_mov_b32_e32 v38, v24
	v_cvt_f32_i32_e32 v24, v44
	v_mov_b32_e32 v39, v28
	v_pk_mul_f32 v[38:39], v[38:39], v[36:37]
	v_mov_b32_e32 v28, v25
	v_mul_f32_e32 v24, 0x38800000, v24
	v_sub_f32_e32 v43, v38, v39
	v_cos_f32_e32 v38, v24
	v_sin_f32_e32 v39, v24
	v_mov_b32_e32 v24, v29
	v_lshl_or_b32 v32, v32, 8, s9
	s_mov_b64 s[16:17], -1
	v_pk_mul_f32 v[40:41], v[24:25], v[38:39]
	v_pk_mul_f32 v[24:25], v[28:29], v[38:39]
	v_add_f32_e32 v45, v40, v41
	v_add_u32_e32 v40, v44, v33
	v_sub_f32_e32 v46, v24, v25
	v_cvt_f32_i32_e32 v24, v40
	v_mov_b32_e32 v28, v30
	v_mov_b32_e32 v29, v26
	v_add_u32_e32 v48, v40, v33
	v_mul_f32_e32 v25, 0x38800000, v24
	v_cos_f32_e32 v24, v25
	v_sin_f32_e32 v25, v25
	s_nop 0
	v_pk_mul_f32 v[28:29], v[28:29], v[24:25]
	s_nop 0
	v_add_f32_e32 v44, v28, v29
	v_mov_b32_e32 v28, v26
	v_cvt_f32_i32_e32 v26, v48
	v_mov_b32_e32 v29, v30
	v_pk_mul_f32 v[28:29], v[28:29], v[24:25]
	v_mov_b32_e32 v30, v27
	v_mul_f32_e32 v26, 0x38800000, v26
	v_sub_f32_e32 v47, v28, v29
	v_cos_f32_e32 v28, v26
	v_sin_f32_e32 v29, v26
	v_mov_b32_e32 v26, v31
	v_lshl_add_u32 v48, v33, 1, v48
	v_pk_mul_f32 v[40:41], v[26:27], v[28:29]
	v_pk_mul_f32 v[26:27], v[30:31], v[28:29]
	v_add_f32_e32 v40, v40, v41
	v_sub_f32_e32 v41, v26, v27
	v_mov_b32_e32 v26, v20
	v_mov_b32_e32 v27, v16
	v_pk_mul_f32 v[26:27], v[26:27], v[34:35]
	s_nop 0
	v_add_f32_e32 v49, v26, v27
	v_mov_b32_e32 v26, v16
	v_cvt_f32_i32_e32 v16, v48
	v_mov_b32_e32 v27, v20
	v_pk_mul_f32 v[26:27], v[26:27], v[34:35]
	v_mov_b32_e32 v20, v17
	v_mul_f32_e32 v16, 0x38800000, v16
	v_sub_f32_e32 v50, v26, v27
	v_cos_f32_e32 v26, v16
	v_sin_f32_e32 v27, v16
	v_mov_b32_e32 v16, v21
	v_pk_mul_f32 v[30:31], v[16:17], v[26:27]
	s_nop 0
	v_add_f32_e32 v51, v30, v31
	v_pk_mul_f32 v[16:17], v[20:21], v[26:27]
	v_add_u32_e32 v30, v48, v33
	v_sub_f32_e32 v52, v16, v17
	v_cvt_f32_i32_e32 v16, v30
	v_mov_b32_e32 v17, v18
	v_mul_f32_e32 v16, 0x38800000, v16
	v_cos_f32_e32 v20, v16
	v_sin_f32_e32 v21, v16
	v_mov_b32_e32 v16, v22
	v_pk_mul_f32 v[16:17], v[16:17], v[20:21]
	s_nop 0
	v_add_f32_e32 v48, v16, v17
	v_mov_b32_e32 v16, v18
	v_mov_b32_e32 v17, v22
	v_pk_mul_f32 v[16:17], v[16:17], v[20:21]
	v_mov_b32_e32 v18, v23
	v_sub_f32_e32 v53, v16, v17
	v_add_u32_e32 v16, v30, v33
	v_cvt_f32_i32_e32 v16, v16
	v_mov_b32_e32 v22, v19
	v_ashrrev_i32_e32 v33, 31, v32
	v_mul_f32_e32 v16, 0x38800000, v16
	v_cos_f32_e32 v30, v16
	v_sin_f32_e32 v31, v16
	s_nop 0
	v_pk_mul_f32 v[16:17], v[18:19], v[30:31]
	s_nop 0
	v_add_f32_e32 v54, v16, v17
	v_pk_mul_f32 v[16:17], v[22:23], v[30:31]
	s_nop 0
	v_sub_f32_e32 v55, v16, v17
	v_lshlrev_b64 v[16:17], 9, v[32:33]
	v_lshl_add_u64 v[22:23], v[134:135], 0, v[16:17]
	v_cvt_pk_bf16_f32 v16, v42, v45
	v_cvt_pk_bf16_f32 v17, v44, v40
	v_cvt_pk_bf16_f32 v18, v49, v51
	v_cvt_pk_bf16_f32 v19, v48, v54
	global_store_dwordx4 v[22:23], v[16:19], off sc1
	s_nop 1
	v_cvt_pk_bf16_f32 v16, v43, v46
	v_cvt_pk_bf16_f32 v17, v47, v41
	v_cvt_pk_bf16_f32 v18, v50, v52
	v_cvt_pk_bf16_f32 v19, v53, v55
	global_store_dwordx4 v[22:23], v[16:19], off offset:256 sc1
	s_nop 1
	v_mov_b32_e32 v16, v12
	v_mov_b32_e32 v17, v4
	v_pk_mul_f32 v[16:17], v[16:17], v[36:37]
	s_nop 0
	v_add_f32_e32 v18, v16, v17
	v_mov_b32_e32 v16, v4
	v_mov_b32_e32 v17, v12
	v_pk_mul_f32 v[16:17], v[16:17], v[36:37]
	v_mov_b32_e32 v4, v13
	v_mov_b32_e32 v12, v5
	v_sub_f32_e32 v19, v16, v17
	v_pk_mul_f32 v[16:17], v[4:5], v[38:39]
	v_pk_mul_f32 v[4:5], v[12:13], v[38:39]
	v_add_f32_e32 v16, v16, v17
	v_sub_f32_e32 v12, v4, v5
	v_mov_b32_e32 v4, v14
	v_mov_b32_e32 v5, v6
	v_pk_mul_f32 v[4:5], v[4:5], v[24:25]
	s_nop 0
	v_add_f32_e32 v13, v4, v5
	v_mov_b32_e32 v4, v6
	v_mov_b32_e32 v5, v14
	v_pk_mul_f32 v[4:5], v[4:5], v[24:25]
	v_mov_b32_e32 v6, v15
	v_sub_f32_e32 v17, v4, v5
	v_pk_mul_f32 v[4:5], v[6:7], v[28:29]
	v_mov_b32_e32 v14, v7
	v_add_f32_e32 v6, v4, v5
	v_pk_mul_f32 v[4:5], v[14:15], v[28:29]
	s_nop 0
	v_sub_f32_e32 v7, v4, v5
	v_mov_b32_e32 v4, v8
	v_mov_b32_e32 v5, v0
	v_pk_mul_f32 v[4:5], v[4:5], v[34:35]
	s_nop 0
	v_add_f32_e32 v14, v4, v5
	v_mov_b32_e32 v4, v0
	v_mov_b32_e32 v5, v8
	v_pk_mul_f32 v[4:5], v[4:5], v[34:35]
	v_mov_b32_e32 v0, v9
	v_mov_b32_e32 v8, v1
	v_sub_f32_e32 v15, v4, v5
	v_pk_mul_f32 v[4:5], v[0:1], v[26:27]
	v_pk_mul_f32 v[0:1], v[8:9], v[26:27]
	v_add_f32_e32 v22, v4, v5
	v_sub_f32_e32 v8, v0, v1
	v_mov_b32_e32 v0, v10
	v_mov_b32_e32 v1, v2
	v_pk_mul_f32 v[0:1], v[0:1], v[20:21]
	s_nop 0
	v_add_f32_e32 v9, v0, v1
	v_mov_b32_e32 v0, v2
	v_mov_b32_e32 v1, v10
	v_pk_mul_f32 v[0:1], v[0:1], v[20:21]
	v_mov_b32_e32 v2, v11
	v_sub_f32_e32 v20, v0, v1
	v_pk_mul_f32 v[0:1], v[2:3], v[30:31]
	v_mov_b32_e32 v10, v3
	v_add_f32_e32 v21, v0, v1
	v_pk_mul_f32 v[0:1], v[10:11], v[30:31]
	s_nop 0
	v_sub_f32_e32 v10, v0, v1
	v_or_b32_e32 v0, 1, v32
	v_ashrrev_i32_e32 v1, 31, v0
	v_lshlrev_b64 v[0:1], 9, v[0:1]
	v_lshl_add_u64 v[4:5], v[134:135], 0, v[0:1]
	v_cvt_pk_bf16_f32 v0, v18, v16
	v_cvt_pk_bf16_f32 v1, v13, v6
	v_cvt_pk_bf16_f32 v2, v14, v22
	v_cvt_pk_bf16_f32 v3, v9, v21
	global_store_dwordx4 v[4:5], v[0:3], off sc1
	s_nop 1
	v_cvt_pk_bf16_f32 v0, v19, v12
	v_cvt_pk_bf16_f32 v1, v17, v7
	v_cvt_pk_bf16_f32 v2, v15, v8
	v_cvt_pk_bf16_f32 v3, v20, v10
	global_store_dwordx4 v[4:5], v[0:3], off offset:256 sc1
	s_cbranch_vccnz .LBB0_597
	s_andn2_b64 vcc, exec, s[0:1]
	s_cbranch_vccnz .LBB0_596
	s_barrier
	s_branch .LBB0_596

.LBB0_670:
	s_and_b32 s9, s53, 0x7f
	s_lshl_b32 s16, s53, 1
	v_or_b32_e32 v76, s9, v73
	s_and_b32 s16, s16, 0xffffff00
	v_ashrrev_i32_e32 v77, 31, v76
	v_readlane_b32 s18, v254, 12
	s_ashr_i32 s17, s16, 31
	v_lshlrev_b64 v[78:79], 11, v[76:77]
	v_readlane_b32 s19, v254, 13
	v_cvt_pk_bf16_f32 v60, v60, v61
	v_cvt_pk_bf16_f32 v61, v62, v63
	v_cvt_pk_bf16_f32 v62, v56, v57
	s_lshl_b64 s[16:17], s[16:17], 1
	v_cvt_pk_bf16_f32 v63, v58, v59
	s_nop 0
	v_lshl_add_u64 v[56:57], s[18:19], 0, v[78:79]
	v_lshl_add_u64 v[56:57], v[56:57], 0, s[16:17]
	v_lshl_add_u64 v[56:57], v[56:57], 0, v[184:185]
	global_store_dwordx4 v[56:57], v[60:63], off sc1
	v_cvt_pk_bf16_f32 v48, v48, v49
	v_cvt_pk_bf16_f32 v49, v50, v51
	v_cvt_pk_bf16_f32 v50, v40, v41
	v_or_b32_e32 v40, 0x800, v76
	v_ashrrev_i32_e32 v41, 31, v40
	v_cvt_pk_bf16_f32 v51, v42, v43
	global_store_dwordx4 v[56:57], v[48:51], off offset:256 sc1
	v_readlane_b32 s62, v255, 40
	s_andn2_b64 vcc, exec, s[14:15]
	v_lshlrev_b64 v[48:49], 11, v[40:41]
	v_cvt_pk_bf16_f32 v40, v52, v53
	v_cvt_pk_bf16_f32 v41, v54, v55
	v_cvt_pk_bf16_f32 v42, v44, v45
	v_lshl_add_u64 v[44:45], s[18:19], 0, v[48:49]
	v_lshl_add_u64 v[44:45], v[44:45], 0, s[16:17]
	v_lshl_add_u64 v[44:45], v[44:45], 0, v[184:185]
	v_cvt_pk_bf16_f32 v43, v46, v47
	global_store_dwordx4 v[44:45], v[40:43], off sc1
	v_cvt_pk_bf16_f32 v32, v32, v33
	v_cvt_pk_bf16_f32 v33, v34, v35
	v_cvt_pk_bf16_f32 v34, v24, v25
	v_or_b32_e32 v24, 0x1000, v76
	v_ashrrev_i32_e32 v25, 31, v24
	v_cvt_pk_bf16_f32 v35, v26, v27
	global_store_dwordx4 v[44:45], v[32:35], off offset:256 sc1
	s_mov_b64 s[14:15], -1
	v_readlane_b32 s63, v255, 41
	v_lshlrev_b64 v[32:33], 11, v[24:25]
	v_cvt_pk_bf16_f32 v24, v36, v37
	v_cvt_pk_bf16_f32 v25, v38, v39
	v_cvt_pk_bf16_f32 v26, v28, v29
	v_lshl_add_u64 v[28:29], s[18:19], 0, v[32:33]
	v_lshl_add_u64 v[28:29], v[28:29], 0, s[16:17]
	v_lshl_add_u64 v[28:29], v[28:29], 0, v[184:185]
	v_cvt_pk_bf16_f32 v27, v30, v31
	global_store_dwordx4 v[28:29], v[24:27], off sc1
	v_cvt_pk_bf16_f32 v16, v16, v17
	v_cvt_pk_bf16_f32 v17, v18, v19
	v_cvt_pk_bf16_f32 v18, v8, v9
	v_or_b32_e32 v8, 0x1800, v76
	v_ashrrev_i32_e32 v9, 31, v8
	v_cvt_pk_bf16_f32 v19, v10, v11
	global_store_dwordx4 v[28:29], v[16:19], off offset:256 sc1
	v_readlane_b32 s48, v252, 42
	s_nop 0
	v_lshlrev_b64 v[16:17], 11, v[8:9]
	v_cvt_pk_bf16_f32 v8, v20, v21
	v_cvt_pk_bf16_f32 v9, v22, v23
	v_cvt_pk_bf16_f32 v10, v12, v13
	v_lshl_add_u64 v[12:13], s[18:19], 0, v[16:17]
	v_lshl_add_u64 v[12:13], v[12:13], 0, s[16:17]
	v_lshl_add_u64 v[12:13], v[12:13], 0, v[184:185]
	v_cvt_pk_bf16_f32 v11, v14, v15
	global_store_dwordx4 v[12:13], v[8:11], off sc1
	v_cvt_pk_bf16_f32 v4, v4, v5
	v_cvt_pk_bf16_f32 v5, v6, v7
	v_cvt_pk_bf16_f32 v6, v0, v1
	v_cvt_pk_bf16_f32 v7, v2, v3
	global_store_dwordx4 v[12:13], v[4:7], off offset:256 sc1
	s_cbranch_vccnz .LBB0_665
	s_andn2_b64 vcc, exec, s[0:1]
	s_cbranch_vccnz .LBB0_664
	s_barrier
	s_branch .LBB0_664

.LBB0_685:
	s_lshl_b32 s16, s41, 8
	s_ashr_i32 s17, s16, 31
	s_lshl_b64 s[16:17], s[16:17], 1
	v_cvt_pk_bf16_f32 v124, v124, v125
	v_cvt_pk_bf16_f32 v125, v126, v127
	v_cvt_pk_bf16_f32 v126, v120, v121
	v_lshl_add_u64 v[120:121], v[134:135], 0, s[16:17]
	v_cvt_pk_bf16_f32 v127, v122, v123
	global_store_dwordx4 v[120:121], v[124:127], off sc1
	v_cvt_pk_bf16_f32 v112, v112, v113
	v_cvt_pk_bf16_f32 v113, v114, v115
	v_cvt_pk_bf16_f32 v114, v104, v105
	v_cvt_pk_bf16_f32 v115, v106, v107
	global_store_dwordx4 v[120:121], v[112:115], off offset:256 sc1
	v_cvt_pk_bf16_f32 v104, v116, v117
	v_cvt_pk_bf16_f32 v105, v118, v119
	v_cvt_pk_bf16_f32 v106, v108, v109
	v_lshl_add_u64 v[108:109], v[136:137], 0, s[16:17]
	v_cvt_pk_bf16_f32 v107, v110, v111
	global_store_dwordx4 v[108:109], v[104:107], off sc1
	v_cvt_pk_bf16_f32 v96, v96, v97
	v_cvt_pk_bf16_f32 v97, v98, v99
	v_cvt_pk_bf16_f32 v98, v88, v89
	v_cvt_pk_bf16_f32 v99, v90, v91
	global_store_dwordx4 v[108:109], v[96:99], off offset:256 sc1
	v_cvt_pk_bf16_f32 v88, v100, v101
	v_cvt_pk_bf16_f32 v89, v102, v103
	v_cvt_pk_bf16_f32 v90, v92, v93
	v_lshl_add_u64 v[92:93], v[138:139], 0, s[16:17]
	v_cvt_pk_bf16_f32 v91, v94, v95
	global_store_dwordx4 v[92:93], v[88:91], off sc1
	v_cvt_pk_bf16_f32 v80, v80, v81
	v_cvt_pk_bf16_f32 v81, v82, v83
	v_cvt_pk_bf16_f32 v82, v72, v73
	v_cvt_pk_bf16_f32 v83, v74, v75
	global_store_dwordx4 v[92:93], v[80:83], off offset:256 sc1
	v_cvt_pk_bf16_f32 v72, v84, v85
	v_cvt_pk_bf16_f32 v73, v86, v87
	v_cvt_pk_bf16_f32 v74, v76, v77
	v_lshl_add_u64 v[76:77], v[140:141], 0, s[16:17]
	v_cvt_pk_bf16_f32 v75, v78, v79
	global_store_dwordx4 v[76:77], v[72:75], off sc1
	v_cvt_pk_bf16_f32 v68, v68, v69
	v_cvt_pk_bf16_f32 v69, v70, v71
	v_cvt_pk_bf16_f32 v70, v64, v65
	v_cvt_pk_bf16_f32 v71, v66, v67
	global_store_dwordx4 v[76:77], v[68:71], off offset:256 sc1
	v_cvt_pk_bf16_f32 v60, v60, v61
	v_cvt_pk_bf16_f32 v61, v62, v63
	v_cvt_pk_bf16_f32 v62, v56, v57
	v_lshl_add_u64 v[56:57], v[142:143], 0, s[16:17]
	v_cvt_pk_bf16_f32 v63, v58, v59
	global_store_dwordx4 v[56:57], v[60:63], off sc1
	v_cvt_pk_bf16_f32 v48, v48, v49
	v_cvt_pk_bf16_f32 v49, v50, v51
	v_cvt_pk_bf16_f32 v50, v40, v41
	v_cvt_pk_bf16_f32 v51, v42, v43
	global_store_dwordx4 v[56:57], v[48:51], off offset:256 sc1
	v_cvt_pk_bf16_f32 v40, v52, v53
	v_cvt_pk_bf16_f32 v41, v54, v55
	v_cvt_pk_bf16_f32 v42, v44, v45
	v_lshl_add_u64 v[44:45], v[144:145], 0, s[16:17]
	v_cvt_pk_bf16_f32 v43, v46, v47
	global_store_dwordx4 v[44:45], v[40:43], off sc1
	v_cvt_pk_bf16_f32 v32, v32, v33
	v_cvt_pk_bf16_f32 v33, v34, v35
	v_cvt_pk_bf16_f32 v34, v24, v25
	v_cvt_pk_bf16_f32 v35, v26, v27
	global_store_dwordx4 v[44:45], v[32:35], off offset:256 sc1
	v_cvt_pk_bf16_f32 v24, v36, v37
	v_cvt_pk_bf16_f32 v25, v38, v39
	v_cvt_pk_bf16_f32 v26, v28, v29
	v_lshl_add_u64 v[28:29], v[146:147], 0, s[16:17]
	v_cvt_pk_bf16_f32 v27, v30, v31
	global_store_dwordx4 v[28:29], v[24:27], off sc1
	v_cvt_pk_bf16_f32 v16, v16, v17
	v_cvt_pk_bf16_f32 v17, v18, v19
	v_cvt_pk_bf16_f32 v18, v8, v9
	v_cvt_pk_bf16_f32 v19, v10, v11
	global_store_dwordx4 v[28:29], v[16:19], off offset:256 sc1
	v_cvt_pk_bf16_f32 v8, v20, v21
	v_cvt_pk_bf16_f32 v9, v22, v23
	v_cvt_pk_bf16_f32 v10, v12, v13
	v_lshl_add_u64 v[12:13], v[148:149], 0, s[16:17]
	s_andn2_b64 vcc, exec, s[14:15]
	s_mov_b64 s[14:15], -1
	v_cvt_pk_bf16_f32 v11, v14, v15
	global_store_dwordx4 v[12:13], v[8:11], off sc1
	v_cvt_pk_bf16_f32 v4, v4, v5
	v_cvt_pk_bf16_f32 v5, v6, v7
	v_cvt_pk_bf16_f32 v6, v0, v1
	v_cvt_pk_bf16_f32 v7, v2, v3
	global_store_dwordx4 v[12:13], v[4:7], off offset:256 sc1
	s_cbranch_vccnz .LBB0_680
	s_andn2_b64 vcc, exec, s[0:1]
	s_cbranch_vccnz .LBB0_679
	s_barrier
	s_branch .LBB0_679

.Lattn_pb3:
	s_waitcnt lgkmcnt(6)
	v_mfma_f32_16x16x32_bf16 v[64:67], v[160:163], v[96:99], 0
	v_exp_f32_e32 v88, v88
	v_mfma_f32_16x16x32_bf16 v[68:71], v[160:163], v[112:115], 0
	v_exp_f32_e32 v92, v92
	ds_read_b128 v[234:237], v209 offset:55296
	s_add_u32 s8, s16, 0x3bc00380
	s_addc_u32 s9, s17, 0
	s_add_u32 s6, s15, 0x23a80000
	s_addc_u32 s7, s14, 0
	s_waitcnt lgkmcnt(6)
	v_mfma_f32_16x16x32_bf16 v[0:3], v[164:167], v[216:219], v[0:3]
	v_cvt_pk_bf16_f32 v242, v80, v81
	v_mfma_f32_16x16x32_bf16 v[4:7], v[164:167], v[238:241], v[4:7]
	v_exp_f32_e32 v89, v89
	ds_read_b128 v[160:163], v201 offset:4096
	s_waitcnt vmcnt(4)
	ds_write_b128 v225, v[136:139] offset:32768
	s_waitcnt lgkmcnt(7)
	v_mfma_f32_16x16x32_bf16 v[68:71], v[168:171], v[116:119], v[68:71]
	v_exp_f32_e32 v93, v93
	v_mfma_f32_16x16x32_bf16 v[64:67], v[168:171], v[100:103], v[64:67]
	v_cvt_pk_bf16_f32 v243, v82, v83
	ds_read_b128 v[164:167], v209 offset:57344
	ds_write_b128 v226, v[140:143] offset:32768
	s_waitcnt lgkmcnt(8)
	v_mfma_f32_16x16x32_bf16 v[12:15], v[172:175], v[238:241], v[12:15]
	v_exp_f32_e32 v90, v90
	v_mfma_f32_16x16x32_bf16 v[8:11], v[172:175], v[216:219], v[8:11]
	v_exp_f32_e32 v94, v94
	ds_read_b128 v[168:171], v202 offset:4096
	ds_write_b64 v227, v[148:149] offset:16384
	s_waitcnt lgkmcnt(9)
	v_mfma_f32_16x16x32_bf16 v[64:67], v[176:179], v[104:107], v[64:67]
	v_cvt_pk_bf16_f32 v204, v84, v85
	v_mfma_f32_16x16x32_bf16 v[68:71], v[176:179], v[120:123], v[68:71]
	v_exp_f32_e32 v91, v91
	ds_read_b128 v[172:175], v209 offset:59392
	ds_write_b64 v228, v[150:151] offset:16384
	s_waitcnt lgkmcnt(10)
	v_mfma_f32_16x16x32_bf16 v[16:19], v[180:183], v[216:219], v[16:19]
	v_exp_f32_e32 v95, v95
	v_mfma_f32_16x16x32_bf16 v[20:23], v[180:183], v[238:241], v[20:23]
	v_cvt_pk_bf16_f32 v205, v86, v87
	v_add_f32_e32 v220, v220, v88
	ds_read_b128 v[176:179], v203 offset:4096
	ds_write_b64 v229, v[144:145] offset:16384
	s_waitcnt lgkmcnt(11)
	v_mfma_f32_16x16x32_bf16 v[68:71], v[230:233], v[124:127], v[68:71]
	v_add_f32_e32 v221, v221, v92
	v_add_f32_e32 v220, v220, v89
	v_mfma_f32_16x16x32_bf16 v[64:67], v[230:233], v[108:111], v[64:67]
	v_add_f32_e32 v221, v221, v93
	v_cvt_pk_bf16_f32 v244, v88, v89
	ds_read_b128 v[180:183], v209 offset:61440
	ds_write_b64 v184, v[146:147] offset:16384
	s_waitcnt lgkmcnt(12)
	v_mfma_f32_16x16x32_bf16 v[28:31], v[234:237], v[238:241], v[28:31]
	v_cvt_pk_bf16_f32 v245, v90, v91
	v_cvt_pk_bf16_f32 v206, v92, v93
	v_mfma_f32_16x16x32_bf16 v[24:27], v[234:237], v[216:219], v[24:27]
	v_cvt_pk_bf16_f32 v207, v94, v95
	ds_read_b128 v[230:233], v246 offset:4096
	global_load_dwordx4 v[148:151], v198, s[8:9]
	s_waitcnt lgkmcnt(12)
	v_mfma_f32_16x16x32_bf16 v[72:75], v[160:163], v[96:99], 0
	v_add_f32_e32 v220, v220, v90
	v_add_f32_e32 v221, v221, v94
	v_mfma_f32_16x16x32_bf16 v[76:79], v[160:163], v[112:115], 0
	v_add_f32_e32 v220, v220, v91
	v_add_f32_e32 v221, v221, v95
	ds_read_b128 v[234:237], v209 offset:63488
	global_load_dwordx4 v[144:147], v199, s[8:9]
	s_waitcnt lgkmcnt(11)
	v_mfma_f32_16x16x32_bf16 v[32:35], v[164:167], v[216:219], v[32:35]
	v_add_f32_e32 v194, v194, v220
	v_add_f32_e32 v195, v195, v221
	v_mfma_f32_16x16x32_bf16 v[36:39], v[164:167], v[238:241], v[36:39]
	v_exp_f32_e32 v64, v64
	ds_read_b128 v[160:163], v201 offset:8192
	global_load_dwordx4 v[136:139], v196, s[6:7]
	s_waitcnt lgkmcnt(10)
	v_mfma_f32_16x16x32_bf16 v[76:79], v[168:171], v[116:119], v[76:79]
	v_exp_f32_e32 v68, v68
	v_mfma_f32_16x16x32_bf16 v[72:75], v[168:171], v[100:103], v[72:75]
	v_exp_f32_e32 v65, v65
	ds_read_b128 v[164:167], v210 offset:49152
	global_load_dwordx4 v[140:143], v197, s[6:7]
	s_waitcnt lgkmcnt(9)
	v_mfma_f32_16x16x32_bf16 v[44:47], v[172:175], v[238:241], v[44:47]
	v_exp_f32_e32 v69, v69
	v_mfma_f32_16x16x32_bf16 v[40:43], v[172:175], v[216:219], v[40:43]
	v_exp_f32_e32 v66, v66
	ds_read_b128 v[168:171], v202 offset:8192
	s_waitcnt lgkmcnt(8)
	v_mfma_f32_16x16x32_bf16 v[72:75], v[176:179], v[104:107], v[72:75]
	v_exp_f32_e32 v70, v70
	v_mfma_f32_16x16x32_bf16 v[76:79], v[176:179], v[120:123], v[76:79]
	v_exp_f32_e32 v67, v67
	ds_read_b128 v[172:175], v210 offset:51200
	s_waitcnt lgkmcnt(7)
	v_mfma_f32_16x16x32_bf16 v[48:51], v[180:183], v[216:219], v[48:51]
	v_exp_f32_e32 v71, v71
	v_mfma_f32_16x16x32_bf16 v[52:55], v[180:183], v[238:241], v[52:55]
	v_add_f32_e32 v220, v64, v65
	ds_read_b128 v[176:179], v203 offset:8192
	s_waitcnt lgkmcnt(6)
	v_mfma_f32_16x16x32_bf16 v[76:79], v[230:233], v[124:127], v[76:79]
	v_add_f32_e32 v221, v68, v69
	v_mfma_f32_16x16x32_bf16 v[72:75], v[230:233], v[108:111], v[72:75]
	v_add_f32_e32 v220, v220, v66
	ds_read_b128 v[180:183], v210 offset:53248
	s_waitcnt lgkmcnt(6)
	v_mfma_f32_16x16x32_bf16 v[60:63], v[234:237], v[238:241], v[60:63]
	v_add_f32_e32 v221, v221, v70
	v_add_f32_e32 v220, v220, v67
	v_mfma_f32_16x16x32_bf16 v[56:59], v[234:237], v[216:219], v[56:59]
	v_add_f32_e32 v221, v221, v71
	ds_read_b128 v[230:233], v246 offset:8192
	s_waitcnt lgkmcnt(6)
	v_mfma_f32_16x16x32_bf16 v[80:83], v[160:163], v[96:99], 0
	v_exp_f32_e32 v72, v72
	v_mfma_f32_16x16x32_bf16 v[84:87], v[160:163], v[112:115], 0
	v_exp_f32_e32 v76, v76
	ds_read_b128 v[234:237], v210 offset:55296
	s_waitcnt lgkmcnt(6)
	v_mfma_f32_16x16x32_bf16 v[0:3], v[164:167], v[242:245], v[0:3]
	v_exp_f32_e32 v73, v73
	v_mfma_f32_16x16x32_bf16 v[4:7], v[164:167], v[204:207], v[4:7]
	v_exp_f32_e32 v77, v77
	ds_read_b128 v[160:163], v201 offset:12288
	s_waitcnt lgkmcnt(6)
	v_mfma_f32_16x16x32_bf16 v[84:87], v[168:171], v[116:119], v[84:87]
	v_exp_f32_e32 v74, v74
	v_mfma_f32_16x16x32_bf16 v[80:83], v[168:171], v[100:103], v[80:83]
	v_exp_f32_e32 v78, v78
	ds_read_b128 v[164:167], v210 offset:57344
	s_waitcnt lgkmcnt(6)
	v_mfma_f32_16x16x32_bf16 v[12:15], v[172:175], v[204:207], v[12:15]
	v_exp_f32_e32 v75, v75
	v_mfma_f32_16x16x32_bf16 v[8:11], v[172:175], v[242:245], v[8:11]
	v_exp_f32_e32 v79, v79
	ds_read_b128 v[168:171], v202 offset:12288
	s_waitcnt lgkmcnt(6)
	v_mfma_f32_16x16x32_bf16 v[80:83], v[176:179], v[104:107], v[80:83]
	v_add_f32_e32 v220, v220, v72
	v_add_f32_e32 v221, v221, v76
	v_mfma_f32_16x16x32_bf16 v[84:87], v[176:179], v[120:123], v[84:87]
	v_add_f32_e32 v220, v220, v73
	ds_read_b128 v[172:175], v210 offset:59392
	s_add_u32 s10, s10, 0x200
	s_addc_u32 s11, s11, 0
	s_add_u32 s12, s12, 0x40000
	s_addc_u32 s13, s13, 0
	s_add_i32 s4, s4, 4
	s_cmpk_lt_u32 s4, 0x104
	s_cselect_b64 s[6:7], -1, 0
	s_and_b64 s[6:7], s[0:1], s[6:7]
	s_and_b64 vcc, exec, s[6:7]
	s_waitcnt lgkmcnt(6)
	v_mfma_f32_16x16x32_bf16 v[16:19], v[180:183], v[242:245], v[16:19]
	v_add_f32_e32 v221, v221, v77
	v_add_f32_e32 v220, v220, v74
	v_mfma_f32_16x16x32_bf16 v[20:23], v[180:183], v[204:207], v[20:23]
	v_add_f32_e32 v221, v221, v78
	ds_read_b128 v[176:179], v203 offset:12288
	s_waitcnt lgkmcnt(6)
	v_mfma_f32_16x16x32_bf16 v[84:87], v[230:233], v[124:127], v[84:87]
	v_add_f32_e32 v220, v220, v75
	v_add_f32_e32 v221, v221, v79
	v_mfma_f32_16x16x32_bf16 v[80:83], v[230:233], v[108:111], v[80:83]
	v_cvt_pk_bf16_f32 v216, v64, v65
	ds_read_b128 v[180:183], v210 offset:61440
	s_waitcnt lgkmcnt(6)
	v_mfma_f32_16x16x32_bf16 v[28:31], v[234:237], v[204:207], v[28:31]
	v_cvt_pk_bf16_f32 v217, v66, v67
	v_cvt_pk_bf16_f32 v238, v68, v69
	v_mfma_f32_16x16x32_bf16 v[24:27], v[234:237], v[242:245], v[24:27]
	v_cvt_pk_bf16_f32 v239, v70, v71
	ds_read_b128 v[230:233], v246 offset:12288
	s_waitcnt lgkmcnt(6)
	v_mfma_f32_16x16x32_bf16 v[88:91], v[160:163], v[96:99], 0
	v_exp_f32_e32 v80, v80
	v_mfma_f32_16x16x32_bf16 v[92:95], v[160:163], v[112:115], 0
	v_exp_f32_e32 v84, v84
	ds_read_b128 v[234:237], v210 offset:63488
	s_waitcnt lgkmcnt(6)
	v_mfma_f32_16x16x32_bf16 v[32:35], v[164:167], v[242:245], v[32:35]
	v_exp_f32_e32 v81, v81
	v_mfma_f32_16x16x32_bf16 v[36:39], v[164:167], v[204:207], v[36:39]
	v_exp_f32_e32 v85, v85
	s_waitcnt lgkmcnt(5)
	v_mfma_f32_16x16x32_bf16 v[92:95], v[168:171], v[116:119], v[92:95]
	v_exp_f32_e32 v82, v82
	v_mfma_f32_16x16x32_bf16 v[88:91], v[168:171], v[100:103], v[88:91]
	v_exp_f32_e32 v86, v86
	s_waitcnt lgkmcnt(4)
	v_mfma_f32_16x16x32_bf16 v[44:47], v[172:175], v[204:207], v[44:47]
	v_exp_f32_e32 v83, v83
	v_mfma_f32_16x16x32_bf16 v[40:43], v[172:175], v[242:245], v[40:43]
	v_exp_f32_e32 v87, v87
	s_waitcnt lgkmcnt(3)
	v_mfma_f32_16x16x32_bf16 v[88:91], v[176:179], v[104:107], v[88:91]
	v_add_f32_e32 v220, v220, v80
	v_add_f32_e32 v221, v221, v84
	v_mfma_f32_16x16x32_bf16 v[92:95], v[176:179], v[120:123], v[92:95]
	v_add_f32_e32 v220, v220, v81
	s_waitcnt lgkmcnt(0)
	s_barrier
	ds_read_b128 v[160:163], v201 offset:16384
	ds_read_b128 v[164:167], v209 offset:0
	ds_read_b128 v[168:171], v202 offset:16384
	ds_read_b128 v[172:175], v209 offset:2048
	v_mfma_f32_16x16x32_bf16 v[48:51], v[180:183], v[242:245], v[48:51]
	v_add_f32_e32 v221, v221, v85
	v_add_f32_e32 v220, v220, v82
	v_mfma_f32_16x16x32_bf16 v[52:55], v[180:183], v[204:207], v[52:55]
	v_add_f32_e32 v221, v221, v86
	ds_read_b128 v[176:179], v203 offset:16384
	v_mfma_f32_16x16x32_bf16 v[92:95], v[230:233], v[124:127], v[92:95]
	v_add_f32_e32 v220, v220, v83
	v_add_f32_e32 v221, v221, v87
	v_mfma_f32_16x16x32_bf16 v[88:91], v[230:233], v[108:111], v[88:91]
	v_cvt_pk_bf16_f32 v218, v72, v73
	ds_read_b128 v[180:183], v209 offset:4096
	v_mfma_f32_16x16x32_bf16 v[60:63], v[234:237], v[204:207], v[60:63]
	v_cvt_pk_bf16_f32 v219, v74, v75
	v_cvt_pk_bf16_f32 v240, v76, v77
	v_mfma_f32_16x16x32_bf16 v[56:59], v[234:237], v[242:245], v[56:59]
	v_cvt_pk_bf16_f32 v241, v78, v79
	ds_read_b128 v[230:233], v246 offset:16384
	s_cbranch_vccnz .LBB0_734
	s_setprio 0
	s_waitcnt vmcnt(0)
	s_nop 7
	s_nop 7
	ds_swizzle_b32 v64, v194 offset:swizzle(SWAP,16)
	s_waitcnt lgkmcnt(0)
	v_add_f32_e32 v194, v194, v64
	v_mov_b32_e32 v65, v194
	s_nop 1
	v_permlane32_swap_b32_e32 v194, v65
	v_add_f32_e32 v194, v194, v65
	s_nop 0
	v_rcp_f32_e32 v66, v194
	ds_swizzle_b32 v64, v195 offset:swizzle(SWAP,16)
	s_waitcnt lgkmcnt(0)
	v_add_f32_e32 v195, v195, v64
	v_mov_b32_e32 v65, v195
	s_nop 1
	v_permlane32_swap_b32_e32 v195, v65
	v_add_f32_e32 v195, v195, v65
	s_nop 0
	v_rcp_f32_e32 v67, v195
	v_readlane_b32 s100, v250, 8
	v_mbcnt_lo_u32_b32 v68, -1, 0
	v_mbcnt_hi_u32_b32 v68, -1, v68
	v_and_b32_e32 v69, 15, v68
	v_lshrrev_b32_e32 v70, 4, v68
	s_lshr_b32 s101, s100, 1
	v_add_u32_e32 v69, s101, v69
	v_lshlrev_b32_e32 v69, 12, v69
	v_and_b32_e32 v71, 1, v70
	v_lshlrev_b32_e32 v71, 5, v71
	v_and_b32_e32 v70, 2, v70
	v_lshl_add_u32 v71, v70, 3, v71
	v_add_u32_e32 v70, v69, v71
	v_add_u32_e32 v71, 0x10000, v70
	v_mul_f32_e32 v0, v0, v66
	v_mul_f32_e32 v1, v1, v66
	v_mul_f32_e32 v2, v2, v66
	v_mul_f32_e32 v3, v3, v66
	v_mul_f32_e32 v8, v8, v66
	v_mul_f32_e32 v9, v9, v66
	v_mul_f32_e32 v10, v10, v66
	v_mul_f32_e32 v11, v11, v66
	v_cvt_pk_bf16_f32 v72, v0, v1
	v_cvt_pk_bf16_f32 v73, v2, v3
	v_cvt_pk_bf16_f32 v74, v8, v9
	v_cvt_pk_bf16_f32 v75, v10, v11
	s_nop 1
	v_permlane16_swap_b32_e32 v72, v74
	v_permlane16_swap_b32_e32 v73, v75
	s_nop 1
	global_store_dwordx4 v70, v[72:75], s[58:59] offset:0 sc1
	v_mul_f32_e32 v16, v16, v66
	v_mul_f32_e32 v17, v17, v66
	v_mul_f32_e32 v18, v18, v66
	v_mul_f32_e32 v19, v19, v66
	v_mul_f32_e32 v24, v24, v66
	v_mul_f32_e32 v25, v25, v66
	v_mul_f32_e32 v26, v26, v66
	v_mul_f32_e32 v27, v27, v66
	v_cvt_pk_bf16_f32 v76, v16, v17
	v_cvt_pk_bf16_f32 v77, v18, v19
	v_cvt_pk_bf16_f32 v78, v24, v25
	v_cvt_pk_bf16_f32 v79, v26, v27
	s_nop 1
	v_permlane16_swap_b32_e32 v76, v78
	v_permlane16_swap_b32_e32 v77, v79
	s_nop 1
	global_store_dwordx4 v70, v[76:79], s[58:59] offset:64 sc1
	v_mul_f32_e32 v32, v32, v66
	v_mul_f32_e32 v33, v33, v66
	v_mul_f32_e32 v34, v34, v66
	v_mul_f32_e32 v35, v35, v66
	v_mul_f32_e32 v40, v40, v66
	v_mul_f32_e32 v41, v41, v66
	v_mul_f32_e32 v42, v42, v66
	v_mul_f32_e32 v43, v43, v66
	v_cvt_pk_bf16_f32 v80, v32, v33
	v_cvt_pk_bf16_f32 v81, v34, v35
	v_cvt_pk_bf16_f32 v82, v40, v41
	v_cvt_pk_bf16_f32 v83, v42, v43
	s_nop 1
	v_permlane16_swap_b32_e32 v80, v82
	v_permlane16_swap_b32_e32 v81, v83
	s_nop 1
	global_store_dwordx4 v70, v[80:83], s[58:59] offset:128 sc1
	v_mul_f32_e32 v48, v48, v66
	v_mul_f32_e32 v49, v49, v66
	v_mul_f32_e32 v50, v50, v66
	v_mul_f32_e32 v51, v51, v66
	v_mul_f32_e32 v56, v56, v66
	v_mul_f32_e32 v57, v57, v66
	v_mul_f32_e32 v58, v58, v66
	v_mul_f32_e32 v59, v59, v66
	v_cvt_pk_bf16_f32 v84, v48, v49
	v_cvt_pk_bf16_f32 v85, v50, v51
	v_cvt_pk_bf16_f32 v86, v56, v57
	v_cvt_pk_bf16_f32 v87, v58, v59
	s_nop 1
	v_permlane16_swap_b32_e32 v84, v86
	v_permlane16_swap_b32_e32 v85, v87
	s_nop 1
	global_store_dwordx4 v70, v[84:87], s[58:59] offset:192 sc1
	v_mul_f32_e32 v4, v4, v67
	v_mul_f32_e32 v5, v5, v67
	v_mul_f32_e32 v6, v6, v67
	v_mul_f32_e32 v7, v7, v67
	v_mul_f32_e32 v12, v12, v67
	v_mul_f32_e32 v13, v13, v67
	v_mul_f32_e32 v14, v14, v67
	v_mul_f32_e32 v15, v15, v67
	v_cvt_pk_bf16_f32 v88, v4, v5
	v_cvt_pk_bf16_f32 v89, v6, v7
	v_cvt_pk_bf16_f32 v90, v12, v13
	v_cvt_pk_bf16_f32 v91, v14, v15
	s_nop 1
	v_permlane16_swap_b32_e32 v88, v90
	v_permlane16_swap_b32_e32 v89, v91
	s_nop 1
	global_store_dwordx4 v71, v[88:91], s[58:59] offset:0 sc1
	v_mul_f32_e32 v20, v20, v67
	v_mul_f32_e32 v21, v21, v67
	v_mul_f32_e32 v22, v22, v67
	v_mul_f32_e32 v23, v23, v67
	v_mul_f32_e32 v28, v28, v67
	v_mul_f32_e32 v29, v29, v67
	v_mul_f32_e32 v30, v30, v67
	v_mul_f32_e32 v31, v31, v67
	v_cvt_pk_bf16_f32 v92, v20, v21
	v_cvt_pk_bf16_f32 v93, v22, v23
	v_cvt_pk_bf16_f32 v94, v28, v29
	v_cvt_pk_bf16_f32 v95, v30, v31
	s_nop 1
	v_permlane16_swap_b32_e32 v92, v94
	v_permlane16_swap_b32_e32 v93, v95
	s_nop 1
	global_store_dwordx4 v71, v[92:95], s[58:59] offset:64 sc1
	v_mul_f32_e32 v36, v36, v67
	v_mul_f32_e32 v37, v37, v67
	v_mul_f32_e32 v38, v38, v67
	v_mul_f32_e32 v39, v39, v67
	v_mul_f32_e32 v44, v44, v67
	v_mul_f32_e32 v45, v45, v67
	v_mul_f32_e32 v46, v46, v67
	v_mul_f32_e32 v47, v47, v67
	v_cvt_pk_bf16_f32 v72, v36, v37
	v_cvt_pk_bf16_f32 v73, v38, v39
	v_cvt_pk_bf16_f32 v74, v44, v45
	v_cvt_pk_bf16_f32 v75, v46, v47
	s_nop 1
	v_permlane16_swap_b32_e32 v72, v74
	v_permlane16_swap_b32_e32 v73, v75
	s_nop 1
	global_store_dwordx4 v71, v[72:75], s[58:59] offset:128 sc1
	v_mul_f32_e32 v52, v52, v67
	v_mul_f32_e32 v53, v53, v67
	v_mul_f32_e32 v54, v54, v67
	v_mul_f32_e32 v55, v55, v67
	v_mul_f32_e32 v60, v60, v67
	v_mul_f32_e32 v61, v61, v67
	v_mul_f32_e32 v62, v62, v67
	v_mul_f32_e32 v63, v63, v67
	v_cvt_pk_bf16_f32 v76, v52, v53
	v_cvt_pk_bf16_f32 v77, v54, v55
	v_cvt_pk_bf16_f32 v78, v60, v61
	v_cvt_pk_bf16_f32 v79, v62, v63
	s_nop 1
	v_permlane16_swap_b32_e32 v76, v78
	v_permlane16_swap_b32_e32 v77, v79
	s_nop 1
	global_store_dwordx4 v71, v[76:79], s[58:59] offset:192 sc1
	s_barrier

.LBB0_808:
	v_lshl_add_u32 v140, s59, 8, v142
	v_lshl_or_b32 v138, s58, 8, v144
	v_ashrrev_i32_e32 v141, 31, v140
	v_lshlrev_b64 v[146:147], 13, v[140:141]
	v_ashrrev_i32_e32 v139, 31, v138
	v_lshl_add_u64 v[146:147], s[2:3], 0, v[146:147]
	v_lshlrev_b64 v[138:139], 1, v[138:139]
	v_lshl_add_u64 v[150:151], v[146:147], 0, v[138:139]
	global_load_dwordx4 v[146:149], v[150:151], off
	v_readlane_b32 s62, v255, 40
	v_readlane_b32 s63, v255, 41
	s_andn2_b64 vcc, exec, s[36:37]
	s_mov_b64 s[30:31], -1
	s_waitcnt vmcnt(0)
	v_lshlrev_b32_e32 v152, 16, v146
	v_and_b32_e32 v153, 0xffff0000, v146
	v_lshlrev_b32_e32 v146, 16, v147
	v_and_b32_e32 v147, 0xffff0000, v147
	v_lshlrev_b32_e32 v154, 16, v148
	v_and_b32_e32 v155, 0xffff0000, v148
	v_lshlrev_b32_e32 v148, 16, v149
	v_and_b32_e32 v149, 0xffff0000, v149
	v_pk_mul_f32 v[126:127], v[126:127], v[146:147]
	v_pk_mul_f32 v[124:125], v[124:125], v[152:153]
	v_pk_mul_f32 v[146:147], v[122:123], v[148:149]
	v_pk_mul_f32 v[122:123], v[120:121], v[154:155]
	v_cvt_pk_bf16_f32 v120, v124, v125
	v_cvt_pk_bf16_f32 v121, v126, v127
	v_lshlrev_b64 v[148:149], 12, v[140:141]
	v_cvt_pk_bf16_f32 v122, v122, v123
	v_cvt_pk_bf16_f32 v123, v146, v147
	global_load_dwordx4 v[124:127], v[150:151], off offset:256
	v_or_b32_e32 v146, 16, v140
	v_ashrrev_i32_e32 v147, 31, v146
	v_lshl_add_u64 v[148:149], s[62:63], 0, v[148:149]
	v_lshlrev_b64 v[150:151], 13, v[146:147]
	v_lshl_add_u64 v[148:149], v[148:149], 0, v[138:139]
	v_lshl_add_u64 v[150:151], s[2:3], 0, v[150:151]
	global_store_dwordx4 v[148:149], v[120:123], off sc1
	v_lshl_add_u64 v[150:151], v[150:151], 0, v[138:139]
	s_waitcnt vmcnt(1)
	v_lshlrev_b32_e32 v120, 16, v124
	v_and_b32_e32 v121, 0xffff0000, v124
	v_lshlrev_b32_e32 v122, 16, v125
	v_and_b32_e32 v123, 0xffff0000, v125
	v_lshlrev_b32_e32 v124, 16, v126
	v_and_b32_e32 v125, 0xffff0000, v126
	v_lshlrev_b32_e32 v126, 16, v127
	v_and_b32_e32 v127, 0xffff0000, v127
	v_pk_mul_f32 v[114:115], v[114:115], v[122:123]
	v_pk_mul_f32 v[112:113], v[112:113], v[120:121]
	v_pk_mul_f32 v[120:121], v[110:111], v[126:127]
	v_pk_mul_f32 v[110:111], v[108:109], v[124:125]
	v_cvt_pk_bf16_f32 v108, v112, v113
	v_cvt_pk_bf16_f32 v109, v114, v115
	s_nop 0
	v_cvt_pk_bf16_f32 v110, v110, v111
	v_cvt_pk_bf16_f32 v111, v120, v121
	global_load_dwordx4 v[112:115], v[150:151], off
	s_nop 0
	global_store_dwordx4 v[148:149], v[108:111], off offset:256 sc1
	s_waitcnt vmcnt(1)
	s_nop 0
	v_lshlrev_b32_e32 v108, 16, v112
	v_and_b32_e32 v109, 0xffff0000, v112
	v_lshlrev_b32_e32 v110, 16, v113
	v_and_b32_e32 v111, 0xffff0000, v113
	v_lshlrev_b32_e32 v112, 16, v114
	v_and_b32_e32 v113, 0xffff0000, v114
	v_lshlrev_b32_e32 v114, 16, v115
	v_and_b32_e32 v115, 0xffff0000, v115
	v_pk_mul_f32 v[110:111], v[118:119], v[110:111]
	v_pk_mul_f32 v[108:109], v[116:117], v[108:109]
	v_pk_mul_f32 v[114:115], v[106:107], v[114:115]
	v_pk_mul_f32 v[106:107], v[104:105], v[112:113]
	v_cvt_pk_bf16_f32 v104, v108, v109
	v_cvt_pk_bf16_f32 v105, v110, v111
	v_or_b32_e32 v112, 32, v140
	v_cvt_pk_bf16_f32 v106, v106, v107
	v_cvt_pk_bf16_f32 v107, v114, v115
	global_load_dwordx4 v[108:111], v[150:151], off offset:256
	v_lshlrev_b64 v[114:115], 12, v[146:147]
	v_ashrrev_i32_e32 v113, 31, v112
	v_lshl_add_u64 v[114:115], s[62:63], 0, v[114:115]
	v_lshlrev_b64 v[116:117], 13, v[112:113]
	v_lshl_add_u64 v[114:115], v[114:115], 0, v[138:139]
	v_lshl_add_u64 v[116:117], s[2:3], 0, v[116:117]
	global_store_dwordx4 v[114:115], v[104:107], off sc1
	v_lshl_add_u64 v[116:117], v[116:117], 0, v[138:139]
	s_waitcnt vmcnt(1)
	v_lshlrev_b32_e32 v104, 16, v108
	v_and_b32_e32 v105, 0xffff0000, v108
	v_lshlrev_b32_e32 v106, 16, v109
	v_and_b32_e32 v107, 0xffff0000, v109
	v_lshlrev_b32_e32 v108, 16, v110
	v_and_b32_e32 v109, 0xffff0000, v110
	v_lshlrev_b32_e32 v110, 16, v111
	v_and_b32_e32 v111, 0xffff0000, v111
	v_pk_mul_f32 v[98:99], v[98:99], v[106:107]
	v_pk_mul_f32 v[96:97], v[96:97], v[104:105]
	v_pk_mul_f32 v[104:105], v[94:95], v[110:111]
	v_pk_mul_f32 v[94:95], v[92:93], v[108:109]
	v_cvt_pk_bf16_f32 v92, v96, v97
	v_cvt_pk_bf16_f32 v93, v98, v99
	s_nop 0
	v_cvt_pk_bf16_f32 v94, v94, v95
	v_cvt_pk_bf16_f32 v95, v104, v105
	global_load_dwordx4 v[96:99], v[116:117], off
	s_nop 0
	global_store_dwordx4 v[114:115], v[92:95], off offset:256 sc1
	s_waitcnt vmcnt(1)
	s_nop 0
	v_lshlrev_b32_e32 v92, 16, v96
	v_and_b32_e32 v93, 0xffff0000, v96
	v_lshlrev_b32_e32 v94, 16, v97
	v_and_b32_e32 v95, 0xffff0000, v97
	v_lshlrev_b32_e32 v96, 16, v98
	v_and_b32_e32 v97, 0xffff0000, v98
	v_lshlrev_b32_e32 v98, 16, v99
	v_and_b32_e32 v99, 0xffff0000, v99
	v_pk_mul_f32 v[94:95], v[102:103], v[94:95]
	v_pk_mul_f32 v[92:93], v[100:101], v[92:93]
	v_pk_mul_f32 v[98:99], v[90:91], v[98:99]
	v_pk_mul_f32 v[90:91], v[88:89], v[96:97]
	v_cvt_pk_bf16_f32 v88, v92, v93
	v_cvt_pk_bf16_f32 v89, v94, v95
	v_or_b32_e32 v96, 48, v140
	v_cvt_pk_bf16_f32 v90, v90, v91
	v_cvt_pk_bf16_f32 v91, v98, v99
	global_load_dwordx4 v[92:95], v[116:117], off offset:256
	v_lshlrev_b64 v[98:99], 12, v[112:113]
	v_ashrrev_i32_e32 v97, 31, v96
	v_lshl_add_u64 v[98:99], s[62:63], 0, v[98:99]
	v_lshlrev_b64 v[100:101], 13, v[96:97]
	v_lshl_add_u64 v[98:99], v[98:99], 0, v[138:139]
	v_lshl_add_u64 v[100:101], s[2:3], 0, v[100:101]
	global_store_dwordx4 v[98:99], v[88:91], off sc1
	v_lshl_add_u64 v[100:101], v[100:101], 0, v[138:139]
	s_waitcnt vmcnt(1)
	v_lshlrev_b32_e32 v88, 16, v92
	v_and_b32_e32 v89, 0xffff0000, v92
	v_lshlrev_b32_e32 v90, 16, v93
	v_and_b32_e32 v91, 0xffff0000, v93
	v_lshlrev_b32_e32 v92, 16, v94
	v_and_b32_e32 v93, 0xffff0000, v94
	v_lshlrev_b32_e32 v94, 16, v95
	v_and_b32_e32 v95, 0xffff0000, v95
	v_pk_mul_f32 v[82:83], v[82:83], v[90:91]
	v_pk_mul_f32 v[80:81], v[80:81], v[88:89]
	v_pk_mul_f32 v[88:89], v[78:79], v[94:95]
	v_pk_mul_f32 v[78:79], v[76:77], v[92:93]
	v_cvt_pk_bf16_f32 v76, v80, v81
	v_cvt_pk_bf16_f32 v77, v82, v83
	s_nop 0
	v_cvt_pk_bf16_f32 v78, v78, v79
	v_cvt_pk_bf16_f32 v79, v88, v89
	global_load_dwordx4 v[80:83], v[100:101], off
	s_nop 0
	global_store_dwordx4 v[98:99], v[76:79], off offset:256 sc1
	s_waitcnt vmcnt(1)
	s_nop 0
	v_lshlrev_b32_e32 v76, 16, v80
	v_and_b32_e32 v77, 0xffff0000, v80
	v_lshlrev_b32_e32 v78, 16, v81
	v_and_b32_e32 v79, 0xffff0000, v81
	v_lshlrev_b32_e32 v80, 16, v82
	v_and_b32_e32 v81, 0xffff0000, v82
	v_lshlrev_b32_e32 v82, 16, v83
	v_and_b32_e32 v83, 0xffff0000, v83
	v_pk_mul_f32 v[78:79], v[86:87], v[78:79]
	v_pk_mul_f32 v[76:77], v[84:85], v[76:77]
	v_pk_mul_f32 v[82:83], v[74:75], v[82:83]
	v_pk_mul_f32 v[74:75], v[72:73], v[80:81]
	v_cvt_pk_bf16_f32 v72, v76, v77
	v_cvt_pk_bf16_f32 v73, v78, v79
	v_add_u32_e32 v80, 0x80, v140
	v_cvt_pk_bf16_f32 v74, v74, v75
	v_cvt_pk_bf16_f32 v75, v82, v83
	global_load_dwordx4 v[76:79], v[100:101], off offset:256
	v_lshlrev_b64 v[82:83], 12, v[96:97]
	v_ashrrev_i32_e32 v81, 31, v80
	v_lshl_add_u64 v[82:83], s[62:63], 0, v[82:83]
	v_lshlrev_b64 v[84:85], 13, v[80:81]
	v_lshl_add_u64 v[82:83], v[82:83], 0, v[138:139]
	v_lshl_add_u64 v[84:85], s[2:3], 0, v[84:85]
	global_store_dwordx4 v[82:83], v[72:75], off sc1
	v_lshl_add_u64 v[84:85], v[84:85], 0, v[138:139]
	s_waitcnt vmcnt(1)
	v_lshlrev_b32_e32 v72, 16, v76
	v_and_b32_e32 v73, 0xffff0000, v76
	v_lshlrev_b32_e32 v74, 16, v77
	v_and_b32_e32 v75, 0xffff0000, v77
	v_lshlrev_b32_e32 v76, 16, v78
	v_and_b32_e32 v77, 0xffff0000, v78
	v_lshlrev_b32_e32 v78, 16, v79
	v_and_b32_e32 v79, 0xffff0000, v79
	v_pk_mul_f32 v[70:71], v[70:71], v[74:75]
	v_pk_mul_f32 v[68:69], v[68:69], v[72:73]
	v_pk_mul_f32 v[72:73], v[66:67], v[78:79]
	v_pk_mul_f32 v[66:67], v[64:65], v[76:77]
	v_cvt_pk_bf16_f32 v64, v68, v69
	v_cvt_pk_bf16_f32 v65, v70, v71
	s_nop 0
	v_cvt_pk_bf16_f32 v66, v66, v67
	v_cvt_pk_bf16_f32 v67, v72, v73
	global_load_dwordx4 v[68:71], v[84:85], off
	s_nop 0
	global_store_dwordx4 v[82:83], v[64:67], off offset:256 sc1
	s_waitcnt vmcnt(1)
	s_nop 0
	v_lshlrev_b32_e32 v64, 16, v68
	v_and_b32_e32 v65, 0xffff0000, v68
	v_lshlrev_b32_e32 v66, 16, v69
	v_and_b32_e32 v67, 0xffff0000, v69
	v_lshlrev_b32_e32 v68, 16, v70
	v_and_b32_e32 v69, 0xffff0000, v70
	v_lshlrev_b32_e32 v70, 16, v71
	v_and_b32_e32 v71, 0xffff0000, v71
	v_pk_mul_f32 v[62:63], v[62:63], v[66:67]
	v_pk_mul_f32 v[60:61], v[60:61], v[64:65]
	v_pk_mul_f32 v[64:65], v[58:59], v[70:71]
	v_pk_mul_f32 v[58:59], v[56:57], v[68:69]
	v_cvt_pk_bf16_f32 v56, v60, v61
	v_cvt_pk_bf16_f32 v57, v62, v63
	v_lshlrev_b64 v[66:67], 12, v[80:81]
	v_cvt_pk_bf16_f32 v58, v58, v59
	v_cvt_pk_bf16_f32 v59, v64, v65
	global_load_dwordx4 v[60:63], v[84:85], off offset:256
	v_add_u32_e32 v64, 0x90, v140
	v_ashrrev_i32_e32 v65, 31, v64
	v_lshl_add_u64 v[66:67], s[62:63], 0, v[66:67]
	v_lshlrev_b64 v[68:69], 13, v[64:65]
	v_lshl_add_u64 v[66:67], v[66:67], 0, v[138:139]
	v_lshl_add_u64 v[68:69], s[2:3], 0, v[68:69]
	global_store_dwordx4 v[66:67], v[56:59], off sc1
	v_lshl_add_u64 v[68:69], v[68:69], 0, v[138:139]
	s_waitcnt vmcnt(1)
	v_lshlrev_b32_e32 v56, 16, v60
	v_and_b32_e32 v57, 0xffff0000, v60
	v_lshlrev_b32_e32 v58, 16, v61
	v_and_b32_e32 v59, 0xffff0000, v61
	v_lshlrev_b32_e32 v60, 16, v62
	v_and_b32_e32 v61, 0xffff0000, v62
	v_lshlrev_b32_e32 v62, 16, v63
	v_and_b32_e32 v63, 0xffff0000, v63
	v_pk_mul_f32 v[50:51], v[50:51], v[58:59]
	v_pk_mul_f32 v[48:49], v[48:49], v[56:57]
	v_pk_mul_f32 v[56:57], v[46:47], v[62:63]
	v_pk_mul_f32 v[46:47], v[44:45], v[60:61]
	v_cvt_pk_bf16_f32 v44, v48, v49
	v_cvt_pk_bf16_f32 v45, v50, v51
	s_nop 0
	v_cvt_pk_bf16_f32 v46, v46, v47
	v_cvt_pk_bf16_f32 v47, v56, v57
	global_load_dwordx4 v[48:51], v[68:69], off
	s_nop 0
	global_store_dwordx4 v[66:67], v[44:47], off offset:256 sc1
	s_waitcnt vmcnt(1)
	s_nop 0
	v_lshlrev_b32_e32 v44, 16, v48
	v_and_b32_e32 v45, 0xffff0000, v48
	v_lshlrev_b32_e32 v46, 16, v49
	v_and_b32_e32 v47, 0xffff0000, v49
	v_lshlrev_b32_e32 v48, 16, v50
	v_and_b32_e32 v49, 0xffff0000, v50
	v_lshlrev_b32_e32 v50, 16, v51
	v_and_b32_e32 v51, 0xffff0000, v51
	v_pk_mul_f32 v[46:47], v[54:55], v[46:47]
	v_pk_mul_f32 v[44:45], v[52:53], v[44:45]
	v_pk_mul_f32 v[50:51], v[42:43], v[50:51]
	v_pk_mul_f32 v[42:43], v[40:41], v[48:49]
	v_cvt_pk_bf16_f32 v40, v44, v45
	v_cvt_pk_bf16_f32 v41, v46, v47
	v_add_u32_e32 v48, 0xa0, v140
	v_cvt_pk_bf16_f32 v42, v42, v43
	v_cvt_pk_bf16_f32 v43, v50, v51
	global_load_dwordx4 v[44:47], v[68:69], off offset:256
	v_lshlrev_b64 v[50:51], 12, v[64:65]
	v_ashrrev_i32_e32 v49, 31, v48
	v_lshl_add_u64 v[50:51], s[62:63], 0, v[50:51]
	v_lshlrev_b64 v[52:53], 13, v[48:49]
	v_lshl_add_u64 v[50:51], v[50:51], 0, v[138:139]
	v_lshl_add_u64 v[52:53], s[2:3], 0, v[52:53]
	global_store_dwordx4 v[50:51], v[40:43], off sc1
	v_lshl_add_u64 v[52:53], v[52:53], 0, v[138:139]
	s_waitcnt vmcnt(1)
	v_lshlrev_b32_e32 v40, 16, v44
	v_and_b32_e32 v41, 0xffff0000, v44
	v_lshlrev_b32_e32 v42, 16, v45
	v_and_b32_e32 v43, 0xffff0000, v45
	v_lshlrev_b32_e32 v44, 16, v46
	v_and_b32_e32 v45, 0xffff0000, v46
	v_lshlrev_b32_e32 v46, 16, v47
	v_and_b32_e32 v47, 0xffff0000, v47
	v_pk_mul_f32 v[34:35], v[34:35], v[42:43]
	v_pk_mul_f32 v[32:33], v[32:33], v[40:41]
	v_pk_mul_f32 v[40:41], v[30:31], v[46:47]
	v_pk_mul_f32 v[30:31], v[28:29], v[44:45]
	v_cvt_pk_bf16_f32 v28, v32, v33
	v_cvt_pk_bf16_f32 v29, v34, v35
	s_nop 0
	v_cvt_pk_bf16_f32 v30, v30, v31
	v_cvt_pk_bf16_f32 v31, v40, v41
	global_load_dwordx4 v[32:35], v[52:53], off
	s_nop 0
	global_store_dwordx4 v[50:51], v[28:31], off offset:256 sc1
	s_waitcnt vmcnt(1)
	s_nop 0
	v_lshlrev_b32_e32 v28, 16, v32
	v_and_b32_e32 v29, 0xffff0000, v32
	v_lshlrev_b32_e32 v30, 16, v33
	v_and_b32_e32 v31, 0xffff0000, v33
	v_lshlrev_b32_e32 v32, 16, v34
	v_and_b32_e32 v33, 0xffff0000, v34
	v_lshlrev_b32_e32 v34, 16, v35
	v_and_b32_e32 v35, 0xffff0000, v35
	v_pk_mul_f32 v[30:31], v[38:39], v[30:31]
	v_pk_mul_f32 v[28:29], v[36:37], v[28:29]
	v_pk_mul_f32 v[34:35], v[26:27], v[34:35]
	v_pk_mul_f32 v[26:27], v[24:25], v[32:33]
	v_cvt_pk_bf16_f32 v24, v28, v29
	v_cvt_pk_bf16_f32 v25, v30, v31
	v_add_u32_e32 v32, 0xb0, v140
	v_cvt_pk_bf16_f32 v26, v26, v27
	v_cvt_pk_bf16_f32 v27, v34, v35
	global_load_dwordx4 v[28:31], v[52:53], off offset:256
	v_lshlrev_b64 v[34:35], 12, v[48:49]
	v_ashrrev_i32_e32 v33, 31, v32
	v_lshl_add_u64 v[34:35], s[62:63], 0, v[34:35]
	v_lshlrev_b64 v[36:37], 13, v[32:33]
	v_lshl_add_u64 v[34:35], v[34:35], 0, v[138:139]
	v_lshl_add_u64 v[36:37], s[2:3], 0, v[36:37]
	global_store_dwordx4 v[34:35], v[24:27], off sc1
	v_lshl_add_u64 v[36:37], v[36:37], 0, v[138:139]
	s_waitcnt vmcnt(1)
	v_lshlrev_b32_e32 v24, 16, v28
	v_and_b32_e32 v25, 0xffff0000, v28
	v_lshlrev_b32_e32 v26, 16, v29
	v_and_b32_e32 v27, 0xffff0000, v29
	v_lshlrev_b32_e32 v28, 16, v30
	v_and_b32_e32 v29, 0xffff0000, v30
	v_lshlrev_b32_e32 v30, 16, v31
	v_and_b32_e32 v31, 0xffff0000, v31
	v_pk_mul_f32 v[18:19], v[18:19], v[26:27]
	v_pk_mul_f32 v[16:17], v[16:17], v[24:25]
	v_pk_mul_f32 v[24:25], v[14:15], v[30:31]
	v_pk_mul_f32 v[14:15], v[12:13], v[28:29]
	v_cvt_pk_bf16_f32 v12, v16, v17
	v_cvt_pk_bf16_f32 v13, v18, v19
	s_nop 0
	v_cvt_pk_bf16_f32 v14, v14, v15
	v_cvt_pk_bf16_f32 v15, v24, v25
	global_load_dwordx4 v[16:19], v[36:37], off
	s_nop 0
	global_store_dwordx4 v[34:35], v[12:15], off offset:256 sc1
	s_waitcnt vmcnt(1)
	s_nop 0
	v_lshlrev_b32_e32 v12, 16, v16
	v_and_b32_e32 v13, 0xffff0000, v16
	v_lshlrev_b32_e32 v14, 16, v17
	v_and_b32_e32 v15, 0xffff0000, v17
	v_lshlrev_b32_e32 v16, 16, v18
	v_and_b32_e32 v17, 0xffff0000, v18
	v_lshlrev_b32_e32 v18, 16, v19
	v_and_b32_e32 v19, 0xffff0000, v19
	v_pk_mul_f32 v[14:15], v[22:23], v[14:15]
	v_pk_mul_f32 v[12:13], v[20:21], v[12:13]
	v_pk_mul_f32 v[18:19], v[10:11], v[18:19]
	v_pk_mul_f32 v[10:11], v[8:9], v[16:17]
	v_cvt_pk_bf16_f32 v8, v12, v13
	v_cvt_pk_bf16_f32 v9, v14, v15
	v_lshlrev_b64 v[16:17], 12, v[32:33]
	v_cvt_pk_bf16_f32 v10, v10, v11
	v_cvt_pk_bf16_f32 v11, v18, v19
	global_load_dwordx4 v[12:15], v[36:37], off offset:256
	v_lshl_add_u64 v[16:17], s[62:63], 0, v[16:17]
	v_lshl_add_u64 v[16:17], v[16:17], 0, v[138:139]
	global_store_dwordx4 v[16:17], v[8:11], off sc1
	s_waitcnt vmcnt(1)
	s_nop 0
	v_lshlrev_b32_e32 v8, 16, v12
	v_and_b32_e32 v9, 0xffff0000, v12
	v_lshlrev_b32_e32 v10, 16, v13
	v_and_b32_e32 v11, 0xffff0000, v13
	v_lshlrev_b32_e32 v12, 16, v14
	v_and_b32_e32 v13, 0xffff0000, v14
	v_lshlrev_b32_e32 v14, 16, v15
	v_and_b32_e32 v15, 0xffff0000, v15
	v_pk_mul_f32 v[4:5], v[4:5], v[8:9]
	v_pk_mul_f32 v[8:9], v[2:3], v[14:15]
	v_pk_mul_f32 v[2:3], v[0:1], v[12:13]
	v_pk_mul_f32 v[6:7], v[6:7], v[10:11]
	v_cvt_pk_bf16_f32 v0, v4, v5
	s_nop 0
	v_cvt_pk_bf16_f32 v1, v6, v7
	v_cvt_pk_bf16_f32 v2, v2, v3
	v_cvt_pk_bf16_f32 v3, v8, v9
	global_store_dwordx4 v[16:17], v[0:3], off offset:256 sc1
	s_cbranch_vccnz .LBB0_797
	s_andn2_b64 vcc, exec, s[0:1]
	s_cbranch_vccnz .LBB0_796
	s_barrier
	s_branch .LBB0_796

.LBB0_825:
	v_lshl_or_b32 v154, s41, 8, v151
	s_ashr_i32 s41, s40, 31
	s_lshl_b64 s[6:7], s[40:41], 21
	v_readlane_b32 s24, v250, 6
	v_readlane_b32 s25, v250, 7
	s_add_u32 s6, s24, s6
	v_ashrrev_i32_e32 v155, 31, v154
	s_addc_u32 s7, s25, s7
	v_lshl_add_u64 v[154:155], v[154:155], 2, s[6:7]
	v_lshl_add_u64 v[156:157], v[154:155], 0, v[134:135]
	global_store_dwordx4 v[156:157], v[124:127], off sc1
	global_store_dwordx4 v[156:157], v[120:123], off offset:16 sc1
	global_store_dwordx4 v[156:157], v[100:103], off offset:512 sc1
	global_store_dwordx4 v[156:157], v[92:95], off offset:528 sc1
	v_readlane_b32 s90, v255, 34
	v_readlane_b32 s62, v255, 40
	v_lshl_add_u64 v[92:93], v[154:155], 0, v[136:137]
	global_store_dwordx4 v[92:93], v[116:119], off sc1
	global_store_dwordx4 v[92:93], v[112:115], off offset:16 sc1
	global_store_dwordx4 v[92:93], v[84:87], off offset:512 sc1
	global_store_dwordx4 v[92:93], v[80:83], off offset:528 sc1
	s_andn2_b64 vcc, exec, s[18:19]
	s_mov_b64 s[6:7], -1
	v_lshl_add_u64 v[80:81], v[154:155], 0, v[138:139]
	global_store_dwordx4 v[80:81], v[108:111], off sc1
	global_store_dwordx4 v[80:81], v[104:107], off offset:16 sc1
	global_store_dwordx4 v[80:81], v[76:79], off offset:512 sc1
	global_store_dwordx4 v[80:81], v[72:75], off offset:528 sc1
	v_readlane_b32 s91, v255, 35
	v_readlane_b32 s63, v255, 41
	v_lshl_add_u64 v[72:73], v[154:155], 0, v[140:141]
	global_store_dwordx4 v[72:73], v[96:99], off sc1
	global_store_dwordx4 v[72:73], v[88:91], off offset:16 sc1
	global_store_dwordx4 v[72:73], v[68:71], off offset:512 sc1
	global_store_dwordx4 v[72:73], v[64:67], off offset:528 sc1
	v_readlane_b32 s48, v252, 42
	s_nop 0
	v_lshl_add_u64 v[64:65], v[154:155], 0, v[142:143]
	global_store_dwordx4 v[64:65], v[60:63], off sc1
	global_store_dwordx4 v[64:65], v[56:59], off offset:16 sc1
	global_store_dwordx4 v[64:65], v[36:39], off offset:512 sc1
	global_store_dwordx4 v[64:65], v[28:31], off offset:528 sc1
	s_nop 1
	v_lshl_add_u64 v[28:29], v[154:155], 0, v[144:145]
	global_store_dwordx4 v[28:29], v[52:55], off sc1
	global_store_dwordx4 v[28:29], v[48:51], off offset:16 sc1
	global_store_dwordx4 v[28:29], v[20:23], off offset:512 sc1
	global_store_dwordx4 v[28:29], v[16:19], off offset:528 sc1
	s_nop 1
	v_lshl_add_u64 v[16:17], v[154:155], 0, v[146:147]
	global_store_dwordx4 v[16:17], v[44:47], off sc1
	global_store_dwordx4 v[16:17], v[40:43], off offset:16 sc1
	global_store_dwordx4 v[16:17], v[12:15], off offset:512 sc1
	global_store_dwordx4 v[16:17], v[8:11], off offset:528 sc1
	s_nop 1
	v_lshl_add_u64 v[8:9], v[154:155], 0, v[148:149]
	global_store_dwordx4 v[8:9], v[32:35], off sc1
	global_store_dwordx4 v[8:9], v[24:27], off offset:16 sc1
	global_store_dwordx4 v[8:9], v[4:7], off offset:512 sc1
	global_store_dwordx4 v[8:9], v[0:3], off offset:528 sc1
	s_cbranch_vccnz .LBB0_818
	s_andn2_b64 vcc, exec, s[0:1]
	s_cbranch_vccnz .LBB0_817
	s_barrier
	s_branch .LBB0_817

.LBB0_845:
	v_lshl_add_u32 v142, s53, 8, v146
	v_ashrrev_i32_e32 v143, 31, v142
	v_lshl_or_b32 v140, s52, 8, v148
	v_lshlrev_b64 v[138:139], 13, v[142:143]
	v_lshl_add_u64 v[138:139], s[2:3], 0, v[138:139]
	s_mov_b64 s[24:25], 0x1000
	v_ashrrev_i32_e32 v141, 31, v140
	v_lshl_add_u64 v[158:159], v[138:139], 0, s[24:25]
	v_lshlrev_b64 v[138:139], 1, v[140:141]
	v_lshl_add_u64 v[144:145], v[158:159], 0, v[138:139]
	global_load_dwordx4 v[150:153], v[144:145], off
	v_lshlrev_b64 v[144:145], 12, v[142:143]
	v_lshl_add_u64 v[144:145], s[62:63], 0, v[144:145]
	v_lshl_add_u64 v[144:145], v[144:145], 0, v[138:139]
	global_load_dwordx4 v[154:157], v[144:145], off
	v_or_b32_e32 v140, 0x80, v140
	v_ashrrev_i32_e32 v141, 31, v140
	v_lshlrev_b64 v[140:141], 1, v[140:141]
	v_lshl_add_u64 v[158:159], v[158:159], 0, v[140:141]
	s_andn2_b64 vcc, exec, s[38:39]
	s_mov_b64 s[30:31], -1
	s_waitcnt vmcnt(0)
	v_lshlrev_b32_e32 v160, 16, v150
	v_and_b32_e32 v161, 0xffff0000, v150
	v_lshlrev_b32_e32 v150, 16, v151
	v_and_b32_e32 v151, 0xffff0000, v151
	v_lshlrev_b32_e32 v162, 16, v152
	v_and_b32_e32 v163, 0xffff0000, v152
	v_lshlrev_b32_e32 v152, 16, v153
	v_and_b32_e32 v153, 0xffff0000, v153
	v_lshlrev_b32_e32 v164, 16, v154
	v_and_b32_e32 v165, 0xffff0000, v154
	v_lshlrev_b32_e32 v154, 16, v155
	v_and_b32_e32 v155, 0xffff0000, v155
	v_lshlrev_b32_e32 v166, 16, v156
	v_and_b32_e32 v167, 0xffff0000, v156
	v_lshlrev_b32_e32 v156, 16, v157
	v_and_b32_e32 v157, 0xffff0000, v157
	v_pk_fma_f32 v[126:127], v[126:127], v[150:151], v[154:155]
	v_pk_fma_f32 v[124:125], v[124:125], v[160:161], v[164:165]
	v_pk_fma_f32 v[150:151], v[122:123], v[152:153], v[156:157]
	v_pk_fma_f32 v[122:123], v[120:121], v[162:163], v[166:167]
	v_cvt_pk_bf16_f32 v120, v124, v125
	v_cvt_pk_bf16_f32 v121, v126, v127
	v_or_b32_e32 v154, 16, v142
	v_cvt_pk_bf16_f32 v122, v122, v123
	v_cvt_pk_bf16_f32 v123, v150, v151
	global_load_dwordx4 v[124:127], v[158:159], off
	global_load_dwordx4 v[150:153], v[144:145], off offset:256
	v_ashrrev_i32_e32 v155, 31, v154
	global_store_dwordx4 v[144:145], v[120:123], off sc1
	v_lshlrev_b64 v[156:157], 13, v[154:155]
	v_lshl_add_u64 v[156:157], s[2:3], 0, v[156:157]
	v_lshl_add_u64 v[156:157], v[156:157], 0, s[24:25]
	v_lshl_add_u64 v[158:159], v[156:157], 0, v[138:139]
	s_waitcnt vmcnt(2)
	v_lshlrev_b32_e32 v120, 16, v124
	v_and_b32_e32 v121, 0xffff0000, v124
	v_lshlrev_b32_e32 v122, 16, v125
	v_and_b32_e32 v123, 0xffff0000, v125
	v_lshlrev_b32_e32 v124, 16, v126
	v_and_b32_e32 v125, 0xffff0000, v126
	v_lshlrev_b32_e32 v126, 16, v127
	v_and_b32_e32 v127, 0xffff0000, v127
	s_waitcnt vmcnt(1)
	v_lshlrev_b32_e32 v160, 16, v150
	v_and_b32_e32 v161, 0xffff0000, v150
	v_lshlrev_b32_e32 v162, 16, v152
	v_and_b32_e32 v163, 0xffff0000, v152
	v_lshlrev_b32_e32 v152, 16, v153
	v_and_b32_e32 v153, 0xffff0000, v153
	v_lshlrev_b32_e32 v150, 16, v151
	v_and_b32_e32 v151, 0xffff0000, v151
	v_pk_fma_f32 v[116:117], v[116:117], v[120:121], v[160:161]
	v_pk_fma_f32 v[120:121], v[114:115], v[126:127], v[152:153]
	v_pk_fma_f32 v[114:115], v[112:113], v[124:125], v[162:163]
	v_pk_fma_f32 v[118:119], v[118:119], v[122:123], v[150:151]
	v_cvt_pk_bf16_f32 v112, v116, v117
	v_lshl_add_u64 v[126:127], v[156:157], 0, v[140:141]
	v_cvt_pk_bf16_f32 v113, v118, v119
	v_cvt_pk_bf16_f32 v114, v114, v115
	v_cvt_pk_bf16_f32 v115, v120, v121
	v_lshlrev_b64 v[120:121], 12, v[154:155]
	v_lshl_add_u64 v[120:121], s[62:63], 0, v[120:121]
	v_lshl_add_u64 v[124:125], v[120:121], 0, v[138:139]
	global_load_dwordx4 v[116:119], v[158:159], off
	global_load_dwordx4 v[120:123], v[124:125], off
	s_waitcnt vmcnt(0)
	v_lshlrev_b32_e32 v150, 16, v122
	global_store_dwordx4 v[144:145], v[112:115], off offset:256 sc1
	v_lshlrev_b32_e32 v144, 16, v120
	v_and_b32_e32 v145, 0xffff0000, v120
	v_lshlrev_b32_e32 v112, 16, v116
	v_and_b32_e32 v113, 0xffff0000, v116
	v_lshlrev_b32_e32 v114, 16, v117
	v_and_b32_e32 v115, 0xffff0000, v117
	v_lshlrev_b32_e32 v116, 16, v118
	v_and_b32_e32 v117, 0xffff0000, v118
	v_lshlrev_b32_e32 v118, 16, v119
	v_and_b32_e32 v119, 0xffff0000, v119
	v_lshlrev_b32_e32 v120, 16, v121
	v_and_b32_e32 v121, 0xffff0000, v121
	v_and_b32_e32 v151, 0xffff0000, v122
	v_lshlrev_b32_e32 v122, 16, v123
	v_and_b32_e32 v123, 0xffff0000, v123
	v_pk_fma_f32 v[110:111], v[110:111], v[114:115], v[120:121]
	v_pk_fma_f32 v[108:109], v[108:109], v[112:113], v[144:145]
	v_pk_fma_f32 v[112:113], v[106:107], v[118:119], v[122:123]
	v_pk_fma_f32 v[106:107], v[104:105], v[116:117], v[150:151]
	v_cvt_pk_bf16_f32 v104, v108, v109
	v_cvt_pk_bf16_f32 v105, v110, v111
	v_or_b32_e32 v116, 32, v142
	v_cvt_pk_bf16_f32 v106, v106, v107
	v_cvt_pk_bf16_f32 v107, v112, v113
	global_load_dwordx4 v[108:111], v[126:127], off
	global_load_dwordx4 v[112:115], v[124:125], off offset:256
	v_ashrrev_i32_e32 v117, 31, v116
	global_store_dwordx4 v[124:125], v[104:107], off sc1
	v_lshlrev_b64 v[118:119], 13, v[116:117]
	v_lshl_add_u64 v[118:119], s[2:3], 0, v[118:119]
	v_lshl_add_u64 v[118:119], v[118:119], 0, s[24:25]
	v_lshl_add_u64 v[120:121], v[118:119], 0, v[138:139]
	s_waitcnt vmcnt(2)
	v_lshlrev_b32_e32 v104, 16, v108
	v_and_b32_e32 v105, 0xffff0000, v108
	v_lshlrev_b32_e32 v106, 16, v109
	v_and_b32_e32 v107, 0xffff0000, v109
	v_lshlrev_b32_e32 v108, 16, v110
	v_and_b32_e32 v109, 0xffff0000, v110
	v_lshlrev_b32_e32 v110, 16, v111
	v_and_b32_e32 v111, 0xffff0000, v111
	s_waitcnt vmcnt(1)
	v_lshlrev_b32_e32 v122, 16, v112
	v_and_b32_e32 v123, 0xffff0000, v112
	v_lshlrev_b32_e32 v126, 16, v114
	v_and_b32_e32 v127, 0xffff0000, v114
	v_lshlrev_b32_e32 v114, 16, v115
	v_and_b32_e32 v115, 0xffff0000, v115
	v_lshlrev_b32_e32 v112, 16, v113
	v_and_b32_e32 v113, 0xffff0000, v113
	v_pk_fma_f32 v[100:101], v[100:101], v[104:105], v[122:123]
	v_pk_fma_f32 v[104:105], v[98:99], v[110:111], v[114:115]
	v_pk_fma_f32 v[98:99], v[96:97], v[108:109], v[126:127]
	v_pk_fma_f32 v[102:103], v[102:103], v[106:107], v[112:113]
	v_cvt_pk_bf16_f32 v96, v100, v101
	v_lshl_add_u64 v[110:111], v[118:119], 0, v[140:141]
	v_cvt_pk_bf16_f32 v97, v102, v103
	v_cvt_pk_bf16_f32 v98, v98, v99
	v_cvt_pk_bf16_f32 v99, v104, v105
	v_lshlrev_b64 v[104:105], 12, v[116:117]
	v_lshl_add_u64 v[104:105], s[62:63], 0, v[104:105]
	v_lshl_add_u64 v[108:109], v[104:105], 0, v[138:139]
	global_load_dwordx4 v[100:103], v[120:121], off
	global_load_dwordx4 v[104:107], v[108:109], off
	s_waitcnt vmcnt(0)
	v_lshlrev_b32_e32 v112, 16, v104
	global_store_dwordx4 v[124:125], v[96:99], off offset:256 sc1
	v_and_b32_e32 v113, 0xffff0000, v104
	v_lshlrev_b32_e32 v104, 16, v105
	v_lshlrev_b32_e32 v96, 16, v100
	v_and_b32_e32 v97, 0xffff0000, v100
	v_lshlrev_b32_e32 v98, 16, v101
	v_and_b32_e32 v99, 0xffff0000, v101
	v_lshlrev_b32_e32 v100, 16, v102
	v_and_b32_e32 v101, 0xffff0000, v102
	v_lshlrev_b32_e32 v102, 16, v103
	v_and_b32_e32 v103, 0xffff0000, v103
	v_and_b32_e32 v105, 0xffff0000, v105
	v_lshlrev_b32_e32 v114, 16, v106
	v_and_b32_e32 v115, 0xffff0000, v106
	v_lshlrev_b32_e32 v106, 16, v107
	v_and_b32_e32 v107, 0xffff0000, v107
	v_pk_fma_f32 v[94:95], v[94:95], v[98:99], v[104:105]
	v_pk_fma_f32 v[92:93], v[92:93], v[96:97], v[112:113]
	v_pk_fma_f32 v[96:97], v[90:91], v[102:103], v[106:107]
	v_pk_fma_f32 v[90:91], v[88:89], v[100:101], v[114:115]
	v_cvt_pk_bf16_f32 v88, v92, v93
	v_cvt_pk_bf16_f32 v89, v94, v95
	v_or_b32_e32 v100, 48, v142
	v_cvt_pk_bf16_f32 v90, v90, v91
	v_cvt_pk_bf16_f32 v91, v96, v97
	global_load_dwordx4 v[92:95], v[110:111], off
	global_load_dwordx4 v[96:99], v[108:109], off offset:256
	v_ashrrev_i32_e32 v101, 31, v100
	global_store_dwordx4 v[108:109], v[88:91], off sc1
	v_lshlrev_b64 v[102:103], 13, v[100:101]
	v_lshl_add_u64 v[102:103], s[2:3], 0, v[102:103]
	v_lshl_add_u64 v[102:103], v[102:103], 0, s[24:25]
	v_lshl_add_u64 v[104:105], v[102:103], 0, v[138:139]
	s_waitcnt vmcnt(2)
	v_lshlrev_b32_e32 v88, 16, v92
	v_and_b32_e32 v89, 0xffff0000, v92
	v_lshlrev_b32_e32 v90, 16, v93
	v_and_b32_e32 v91, 0xffff0000, v93
	v_lshlrev_b32_e32 v92, 16, v94
	v_and_b32_e32 v93, 0xffff0000, v94
	v_lshlrev_b32_e32 v94, 16, v95
	v_and_b32_e32 v95, 0xffff0000, v95
	s_waitcnt vmcnt(1)
	v_lshlrev_b32_e32 v106, 16, v96
	v_and_b32_e32 v107, 0xffff0000, v96
	v_lshlrev_b32_e32 v110, 16, v98
	v_and_b32_e32 v111, 0xffff0000, v98
	v_lshlrev_b32_e32 v98, 16, v99
	v_and_b32_e32 v99, 0xffff0000, v99
	v_lshlrev_b32_e32 v96, 16, v97
	v_and_b32_e32 v97, 0xffff0000, v97
	v_pk_fma_f32 v[84:85], v[84:85], v[88:89], v[106:107]
	v_pk_fma_f32 v[88:89], v[82:83], v[94:95], v[98:99]
	v_pk_fma_f32 v[82:83], v[80:81], v[92:93], v[110:111]
	v_pk_fma_f32 v[86:87], v[86:87], v[90:91], v[96:97]
	v_cvt_pk_bf16_f32 v80, v84, v85
	v_lshl_add_u64 v[94:95], v[102:103], 0, v[140:141]
	v_cvt_pk_bf16_f32 v81, v86, v87
	v_cvt_pk_bf16_f32 v82, v82, v83
	v_cvt_pk_bf16_f32 v83, v88, v89
	v_lshlrev_b64 v[88:89], 12, v[100:101]
	v_lshl_add_u64 v[88:89], s[62:63], 0, v[88:89]
	v_lshl_add_u64 v[92:93], v[88:89], 0, v[138:139]
	global_load_dwordx4 v[84:87], v[104:105], off
	global_load_dwordx4 v[88:91], v[92:93], off
	s_waitcnt vmcnt(0)
	v_lshlrev_b32_e32 v96, 16, v88
	global_store_dwordx4 v[108:109], v[80:83], off offset:256 sc1
	v_and_b32_e32 v97, 0xffff0000, v88
	v_lshlrev_b32_e32 v88, 16, v89
	v_lshlrev_b32_e32 v80, 16, v84
	v_and_b32_e32 v81, 0xffff0000, v84
	v_lshlrev_b32_e32 v82, 16, v85
	v_and_b32_e32 v83, 0xffff0000, v85
	v_lshlrev_b32_e32 v84, 16, v86
	v_and_b32_e32 v85, 0xffff0000, v86
	v_lshlrev_b32_e32 v86, 16, v87
	v_and_b32_e32 v87, 0xffff0000, v87
	v_and_b32_e32 v89, 0xffff0000, v89
	v_lshlrev_b32_e32 v98, 16, v90
	v_and_b32_e32 v99, 0xffff0000, v90
	v_lshlrev_b32_e32 v90, 16, v91
	v_and_b32_e32 v91, 0xffff0000, v91
	v_pk_fma_f32 v[78:79], v[78:79], v[82:83], v[88:89]
	v_pk_fma_f32 v[76:77], v[76:77], v[80:81], v[96:97]
	v_pk_fma_f32 v[80:81], v[74:75], v[86:87], v[90:91]
	v_pk_fma_f32 v[74:75], v[72:73], v[84:85], v[98:99]
	v_cvt_pk_bf16_f32 v72, v76, v77
	v_cvt_pk_bf16_f32 v73, v78, v79
	v_add_u32_e32 v84, 0x80, v142
	v_cvt_pk_bf16_f32 v74, v74, v75
	v_cvt_pk_bf16_f32 v75, v80, v81
	global_load_dwordx4 v[76:79], v[94:95], off
	global_load_dwordx4 v[80:83], v[92:93], off offset:256
	v_ashrrev_i32_e32 v85, 31, v84
	global_store_dwordx4 v[92:93], v[72:75], off sc1
	v_lshlrev_b64 v[86:87], 13, v[84:85]
	v_lshl_add_u64 v[86:87], s[2:3], 0, v[86:87]
	v_lshl_add_u64 v[86:87], v[86:87], 0, s[24:25]
	v_lshl_add_u64 v[88:89], v[86:87], 0, v[138:139]
	s_waitcnt vmcnt(2)
	v_lshlrev_b32_e32 v72, 16, v76
	v_and_b32_e32 v73, 0xffff0000, v76
	v_lshlrev_b32_e32 v74, 16, v77
	v_and_b32_e32 v75, 0xffff0000, v77
	v_lshlrev_b32_e32 v76, 16, v78
	v_and_b32_e32 v77, 0xffff0000, v78
	v_lshlrev_b32_e32 v78, 16, v79
	v_and_b32_e32 v79, 0xffff0000, v79
	s_waitcnt vmcnt(1)
	v_lshlrev_b32_e32 v90, 16, v80
	v_and_b32_e32 v91, 0xffff0000, v80
	v_lshlrev_b32_e32 v94, 16, v82
	v_and_b32_e32 v95, 0xffff0000, v82
	v_lshlrev_b32_e32 v82, 16, v83
	v_and_b32_e32 v83, 0xffff0000, v83
	v_lshlrev_b32_e32 v80, 16, v81
	v_and_b32_e32 v81, 0xffff0000, v81
	v_pk_fma_f32 v[68:69], v[68:69], v[72:73], v[90:91]
	v_pk_fma_f32 v[72:73], v[66:67], v[78:79], v[82:83]
	v_pk_fma_f32 v[66:67], v[64:65], v[76:77], v[94:95]
	v_pk_fma_f32 v[70:71], v[70:71], v[74:75], v[80:81]
	v_cvt_pk_bf16_f32 v64, v68, v69
	v_lshl_add_u64 v[78:79], v[86:87], 0, v[140:141]
	v_cvt_pk_bf16_f32 v65, v70, v71
	v_cvt_pk_bf16_f32 v66, v66, v67
	v_cvt_pk_bf16_f32 v67, v72, v73
	v_lshlrev_b64 v[72:73], 12, v[84:85]
	v_lshl_add_u64 v[72:73], s[62:63], 0, v[72:73]
	v_lshl_add_u64 v[76:77], v[72:73], 0, v[138:139]
	global_load_dwordx4 v[68:71], v[88:89], off
	global_load_dwordx4 v[72:75], v[76:77], off
	s_waitcnt vmcnt(0)
	v_lshlrev_b32_e32 v80, 16, v72
	global_store_dwordx4 v[92:93], v[64:67], off offset:256 sc1
	v_and_b32_e32 v81, 0xffff0000, v72
	v_lshlrev_b32_e32 v72, 16, v73
	v_lshlrev_b32_e32 v64, 16, v68
	v_and_b32_e32 v65, 0xffff0000, v68
	v_lshlrev_b32_e32 v66, 16, v69
	v_and_b32_e32 v67, 0xffff0000, v69
	v_lshlrev_b32_e32 v68, 16, v70
	v_and_b32_e32 v69, 0xffff0000, v70
	v_lshlrev_b32_e32 v70, 16, v71
	v_and_b32_e32 v71, 0xffff0000, v71
	v_and_b32_e32 v73, 0xffff0000, v73
	v_lshlrev_b32_e32 v82, 16, v74
	v_and_b32_e32 v83, 0xffff0000, v74
	v_lshlrev_b32_e32 v74, 16, v75
	v_and_b32_e32 v75, 0xffff0000, v75
	v_pk_fma_f32 v[62:63], v[62:63], v[66:67], v[72:73]
	v_pk_fma_f32 v[60:61], v[60:61], v[64:65], v[80:81]
	v_pk_fma_f32 v[64:65], v[58:59], v[70:71], v[74:75]
	v_pk_fma_f32 v[58:59], v[56:57], v[68:69], v[82:83]
	v_cvt_pk_bf16_f32 v56, v60, v61
	v_cvt_pk_bf16_f32 v57, v62, v63
	v_add_u32_e32 v68, 0x90, v142
	v_cvt_pk_bf16_f32 v58, v58, v59
	v_cvt_pk_bf16_f32 v59, v64, v65
	global_load_dwordx4 v[60:63], v[78:79], off
	global_load_dwordx4 v[64:67], v[76:77], off offset:256
	v_ashrrev_i32_e32 v69, 31, v68
	global_store_dwordx4 v[76:77], v[56:59], off sc1
	v_lshlrev_b64 v[70:71], 13, v[68:69]
	v_lshl_add_u64 v[70:71], s[2:3], 0, v[70:71]
	v_lshl_add_u64 v[70:71], v[70:71], 0, s[24:25]
	v_lshl_add_u64 v[72:73], v[70:71], 0, v[138:139]
	s_waitcnt vmcnt(2)
	v_lshlrev_b32_e32 v56, 16, v60
	v_and_b32_e32 v57, 0xffff0000, v60
	v_lshlrev_b32_e32 v58, 16, v61
	v_and_b32_e32 v59, 0xffff0000, v61
	v_lshlrev_b32_e32 v60, 16, v62
	v_and_b32_e32 v61, 0xffff0000, v62
	v_lshlrev_b32_e32 v62, 16, v63
	v_and_b32_e32 v63, 0xffff0000, v63
	s_waitcnt vmcnt(1)
	v_lshlrev_b32_e32 v74, 16, v64
	v_and_b32_e32 v75, 0xffff0000, v64
	v_lshlrev_b32_e32 v78, 16, v66
	v_and_b32_e32 v79, 0xffff0000, v66
	v_lshlrev_b32_e32 v66, 16, v67
	v_and_b32_e32 v67, 0xffff0000, v67
	v_lshlrev_b32_e32 v64, 16, v65
	v_and_b32_e32 v65, 0xffff0000, v65
	v_pk_fma_f32 v[52:53], v[52:53], v[56:57], v[74:75]
	v_pk_fma_f32 v[56:57], v[50:51], v[62:63], v[66:67]
	v_pk_fma_f32 v[50:51], v[48:49], v[60:61], v[78:79]
	v_pk_fma_f32 v[54:55], v[54:55], v[58:59], v[64:65]
	v_cvt_pk_bf16_f32 v48, v52, v53
	v_lshl_add_u64 v[62:63], v[70:71], 0, v[140:141]
	v_cvt_pk_bf16_f32 v49, v54, v55
	v_cvt_pk_bf16_f32 v50, v50, v51
	v_cvt_pk_bf16_f32 v51, v56, v57
	v_lshlrev_b64 v[56:57], 12, v[68:69]
	v_lshl_add_u64 v[56:57], s[62:63], 0, v[56:57]
	v_lshl_add_u64 v[60:61], v[56:57], 0, v[138:139]
	global_load_dwordx4 v[52:55], v[72:73], off
	global_load_dwordx4 v[56:59], v[60:61], off
	s_waitcnt vmcnt(0)
	v_lshlrev_b32_e32 v64, 16, v56
	global_store_dwordx4 v[76:77], v[48:51], off offset:256 sc1
	v_and_b32_e32 v65, 0xffff0000, v56
	v_lshlrev_b32_e32 v56, 16, v57
	v_lshlrev_b32_e32 v48, 16, v52
	v_and_b32_e32 v49, 0xffff0000, v52
	v_lshlrev_b32_e32 v50, 16, v53
	v_and_b32_e32 v51, 0xffff0000, v53
	v_lshlrev_b32_e32 v52, 16, v54
	v_and_b32_e32 v53, 0xffff0000, v54
	v_lshlrev_b32_e32 v54, 16, v55
	v_and_b32_e32 v55, 0xffff0000, v55
	v_and_b32_e32 v57, 0xffff0000, v57
	v_lshlrev_b32_e32 v66, 16, v58
	v_and_b32_e32 v67, 0xffff0000, v58
	v_lshlrev_b32_e32 v58, 16, v59
	v_and_b32_e32 v59, 0xffff0000, v59
	v_pk_fma_f32 v[46:47], v[46:47], v[50:51], v[56:57]
	v_pk_fma_f32 v[44:45], v[44:45], v[48:49], v[64:65]
	v_pk_fma_f32 v[48:49], v[42:43], v[54:55], v[58:59]
	v_pk_fma_f32 v[42:43], v[40:41], v[52:53], v[66:67]
	v_cvt_pk_bf16_f32 v40, v44, v45
	v_cvt_pk_bf16_f32 v41, v46, v47
	v_add_u32_e32 v52, 0xa0, v142
	v_cvt_pk_bf16_f32 v42, v42, v43
	v_cvt_pk_bf16_f32 v43, v48, v49
	global_load_dwordx4 v[44:47], v[62:63], off
	global_load_dwordx4 v[48:51], v[60:61], off offset:256
	v_ashrrev_i32_e32 v53, 31, v52
	global_store_dwordx4 v[60:61], v[40:43], off sc1
	v_lshlrev_b64 v[54:55], 13, v[52:53]
	v_lshl_add_u64 v[54:55], s[2:3], 0, v[54:55]
	v_lshl_add_u64 v[54:55], v[54:55], 0, s[24:25]
	v_lshl_add_u64 v[56:57], v[54:55], 0, v[138:139]
	s_waitcnt vmcnt(2)
	v_lshlrev_b32_e32 v40, 16, v44
	v_and_b32_e32 v41, 0xffff0000, v44
	v_lshlrev_b32_e32 v42, 16, v45
	v_and_b32_e32 v43, 0xffff0000, v45
	v_lshlrev_b32_e32 v44, 16, v46
	v_and_b32_e32 v45, 0xffff0000, v46
	v_lshlrev_b32_e32 v46, 16, v47
	v_and_b32_e32 v47, 0xffff0000, v47
	s_waitcnt vmcnt(1)
	v_lshlrev_b32_e32 v58, 16, v48
	v_and_b32_e32 v59, 0xffff0000, v48
	v_lshlrev_b32_e32 v62, 16, v50
	v_and_b32_e32 v63, 0xffff0000, v50
	v_lshlrev_b32_e32 v50, 16, v51
	v_and_b32_e32 v51, 0xffff0000, v51
	v_lshlrev_b32_e32 v48, 16, v49
	v_and_b32_e32 v49, 0xffff0000, v49
	v_pk_fma_f32 v[36:37], v[36:37], v[40:41], v[58:59]
	v_pk_fma_f32 v[40:41], v[34:35], v[46:47], v[50:51]
	v_pk_fma_f32 v[34:35], v[32:33], v[44:45], v[62:63]
	v_pk_fma_f32 v[38:39], v[38:39], v[42:43], v[48:49]
	v_cvt_pk_bf16_f32 v32, v36, v37
	v_lshl_add_u64 v[46:47], v[54:55], 0, v[140:141]
	v_cvt_pk_bf16_f32 v33, v38, v39
	v_cvt_pk_bf16_f32 v34, v34, v35
	v_cvt_pk_bf16_f32 v35, v40, v41
	v_lshlrev_b64 v[40:41], 12, v[52:53]
	v_lshl_add_u64 v[40:41], s[62:63], 0, v[40:41]
	v_lshl_add_u64 v[44:45], v[40:41], 0, v[138:139]
	global_load_dwordx4 v[36:39], v[56:57], off
	global_load_dwordx4 v[40:43], v[44:45], off
	s_waitcnt vmcnt(0)
	v_lshlrev_b32_e32 v48, 16, v40
	global_store_dwordx4 v[60:61], v[32:35], off offset:256 sc1
	v_and_b32_e32 v49, 0xffff0000, v40
	v_lshlrev_b32_e32 v40, 16, v41
	v_lshlrev_b32_e32 v32, 16, v36
	v_and_b32_e32 v33, 0xffff0000, v36
	v_lshlrev_b32_e32 v34, 16, v37
	v_and_b32_e32 v35, 0xffff0000, v37
	v_lshlrev_b32_e32 v36, 16, v38
	v_and_b32_e32 v37, 0xffff0000, v38
	v_lshlrev_b32_e32 v38, 16, v39
	v_and_b32_e32 v39, 0xffff0000, v39
	v_and_b32_e32 v41, 0xffff0000, v41
	v_lshlrev_b32_e32 v50, 16, v42
	v_and_b32_e32 v51, 0xffff0000, v42
	v_lshlrev_b32_e32 v42, 16, v43
	v_and_b32_e32 v43, 0xffff0000, v43
	v_pk_fma_f32 v[30:31], v[30:31], v[34:35], v[40:41]
	v_pk_fma_f32 v[28:29], v[28:29], v[32:33], v[48:49]
	v_pk_fma_f32 v[32:33], v[26:27], v[38:39], v[42:43]
	v_pk_fma_f32 v[26:27], v[24:25], v[36:37], v[50:51]
	v_cvt_pk_bf16_f32 v24, v28, v29
	v_cvt_pk_bf16_f32 v25, v30, v31
	v_add_u32_e32 v36, 0xb0, v142
	v_cvt_pk_bf16_f32 v26, v26, v27
	v_cvt_pk_bf16_f32 v27, v32, v33
	global_load_dwordx4 v[28:31], v[46:47], off
	global_load_dwordx4 v[32:35], v[44:45], off offset:256
	v_ashrrev_i32_e32 v37, 31, v36
	global_store_dwordx4 v[44:45], v[24:27], off sc1
	v_lshlrev_b64 v[38:39], 13, v[36:37]
	v_lshl_add_u64 v[38:39], s[2:3], 0, v[38:39]
	v_lshl_add_u64 v[38:39], v[38:39], 0, s[24:25]
	v_lshl_add_u64 v[40:41], v[38:39], 0, v[138:139]
	s_waitcnt vmcnt(2)
	v_lshlrev_b32_e32 v24, 16, v28
	v_and_b32_e32 v25, 0xffff0000, v28
	v_lshlrev_b32_e32 v26, 16, v29
	v_and_b32_e32 v27, 0xffff0000, v29
	v_lshlrev_b32_e32 v28, 16, v30
	v_and_b32_e32 v29, 0xffff0000, v30
	v_lshlrev_b32_e32 v30, 16, v31
	v_and_b32_e32 v31, 0xffff0000, v31
	s_waitcnt vmcnt(1)
	v_lshlrev_b32_e32 v42, 16, v32
	v_and_b32_e32 v43, 0xffff0000, v32
	v_lshlrev_b32_e32 v46, 16, v34
	v_and_b32_e32 v47, 0xffff0000, v34
	v_lshlrev_b32_e32 v34, 16, v35
	v_and_b32_e32 v35, 0xffff0000, v35
	v_lshlrev_b32_e32 v32, 16, v33
	v_and_b32_e32 v33, 0xffff0000, v33
	v_pk_fma_f32 v[20:21], v[20:21], v[24:25], v[42:43]
	v_pk_fma_f32 v[24:25], v[18:19], v[30:31], v[34:35]
	v_pk_fma_f32 v[18:19], v[16:17], v[28:29], v[46:47]
	v_pk_fma_f32 v[22:23], v[22:23], v[26:27], v[32:33]
	v_cvt_pk_bf16_f32 v16, v20, v21
	v_lshl_add_u64 v[30:31], v[38:39], 0, v[140:141]
	v_cvt_pk_bf16_f32 v17, v22, v23
	v_cvt_pk_bf16_f32 v18, v18, v19
	v_cvt_pk_bf16_f32 v19, v24, v25
	v_lshlrev_b64 v[24:25], 12, v[36:37]
	v_lshl_add_u64 v[24:25], s[62:63], 0, v[24:25]
	v_lshl_add_u64 v[28:29], v[24:25], 0, v[138:139]
	global_load_dwordx4 v[20:23], v[40:41], off
	global_load_dwordx4 v[24:27], v[28:29], off
	s_waitcnt vmcnt(0)
	v_lshlrev_b32_e32 v32, 16, v24
	global_store_dwordx4 v[44:45], v[16:19], off offset:256 sc1
	v_and_b32_e32 v33, 0xffff0000, v24
	v_lshlrev_b32_e32 v24, 16, v25
	v_lshlrev_b32_e32 v16, 16, v20
	v_and_b32_e32 v17, 0xffff0000, v20
	v_lshlrev_b32_e32 v18, 16, v21
	v_and_b32_e32 v19, 0xffff0000, v21
	v_lshlrev_b32_e32 v20, 16, v22
	v_and_b32_e32 v21, 0xffff0000, v22
	v_lshlrev_b32_e32 v22, 16, v23
	v_and_b32_e32 v23, 0xffff0000, v23
	v_and_b32_e32 v25, 0xffff0000, v25
	v_lshlrev_b32_e32 v34, 16, v26
	v_and_b32_e32 v35, 0xffff0000, v26
	v_lshlrev_b32_e32 v26, 16, v27
	v_and_b32_e32 v27, 0xffff0000, v27
	v_pk_fma_f32 v[14:15], v[14:15], v[18:19], v[24:25]
	v_pk_fma_f32 v[12:13], v[12:13], v[16:17], v[32:33]
	v_pk_fma_f32 v[16:17], v[10:11], v[22:23], v[26:27]
	v_pk_fma_f32 v[10:11], v[8:9], v[20:21], v[34:35]
	v_cvt_pk_bf16_f32 v8, v12, v13
	v_cvt_pk_bf16_f32 v9, v14, v15
	s_nop 0
	v_cvt_pk_bf16_f32 v10, v10, v11
	v_cvt_pk_bf16_f32 v11, v16, v17
	global_load_dwordx4 v[12:15], v[30:31], off
	global_load_dwordx4 v[16:19], v[28:29], off offset:256
	s_waitcnt vmcnt(0)
	v_lshlrev_b32_e32 v20, 16, v16
	global_store_dwordx4 v[28:29], v[8:11], off sc1
	v_and_b32_e32 v21, 0xffff0000, v16
	v_lshlrev_b32_e32 v22, 16, v18
	v_lshlrev_b32_e32 v8, 16, v12
	v_and_b32_e32 v9, 0xffff0000, v12
	v_lshlrev_b32_e32 v10, 16, v13
	v_and_b32_e32 v11, 0xffff0000, v13
	v_lshlrev_b32_e32 v12, 16, v14
	v_and_b32_e32 v13, 0xffff0000, v14
	v_lshlrev_b32_e32 v14, 16, v15
	v_and_b32_e32 v15, 0xffff0000, v15
	v_and_b32_e32 v23, 0xffff0000, v18
	v_lshlrev_b32_e32 v18, 16, v19
	v_and_b32_e32 v19, 0xffff0000, v19
	v_lshlrev_b32_e32 v16, 16, v17
	v_and_b32_e32 v17, 0xffff0000, v17
	v_pk_fma_f32 v[4:5], v[4:5], v[8:9], v[20:21]
	v_pk_fma_f32 v[8:9], v[2:3], v[14:15], v[18:19]
	v_pk_fma_f32 v[2:3], v[0:1], v[12:13], v[22:23]
	v_pk_fma_f32 v[6:7], v[6:7], v[10:11], v[16:17]
	v_cvt_pk_bf16_f32 v0, v4, v5
	s_nop 0
	v_cvt_pk_bf16_f32 v1, v6, v7
	v_cvt_pk_bf16_f32 v2, v2, v3
	v_cvt_pk_bf16_f32 v3, v8, v9
	global_store_dwordx4 v[28:29], v[0:3], off offset:256 sc1
	s_cbranch_vccnz .LBB0_834
	s_andn2_b64 vcc, exec, s[0:1]
	s_cbranch_vccnz .LBB0_833
	s_barrier
	s_branch .LBB0_833

.LBB0_862:
	v_lshl_or_b32 v154, s37, 8, v151
	s_ashr_i32 s37, s36, 31
	s_lshl_b64 s[6:7], s[36:37], 21
	v_readlane_b32 s11, v252, 40
	s_add_u32 s6, s11, s6
	v_readlane_b32 s11, v252, 41
	v_ashrrev_i32_e32 v155, 31, v154
	s_addc_u32 s7, s11, s7
	v_lshl_add_u64 v[154:155], v[154:155], 2, s[6:7]
	v_lshl_add_u64 v[156:157], v[154:155], 0, v[134:135]
	global_store_dwordx4 v[156:157], v[124:127], off sc1
	global_store_dwordx4 v[156:157], v[120:123], off offset:16 sc1
	global_store_dwordx4 v[156:157], v[100:103], off offset:512 sc1
	global_store_dwordx4 v[156:157], v[92:95], off offset:528 sc1
	v_readlane_b32 s90, v255, 34
	v_readlane_b32 s94, v255, 36
	v_lshl_add_u64 v[92:93], v[154:155], 0, v[136:137]
	global_store_dwordx4 v[92:93], v[116:119], off sc1
	global_store_dwordx4 v[92:93], v[112:115], off offset:16 sc1
	global_store_dwordx4 v[92:93], v[84:87], off offset:512 sc1
	global_store_dwordx4 v[92:93], v[80:83], off offset:528 sc1
	v_readlane_b32 s62, v255, 40
	s_andn2_b64 vcc, exec, s[18:19]
	v_lshl_add_u64 v[80:81], v[154:155], 0, v[138:139]
	global_store_dwordx4 v[80:81], v[108:111], off sc1
	global_store_dwordx4 v[80:81], v[104:107], off offset:16 sc1
	global_store_dwordx4 v[80:81], v[76:79], off offset:512 sc1
	global_store_dwordx4 v[80:81], v[72:75], off offset:528 sc1
	s_mov_b64 s[6:7], -1
	v_readlane_b32 s91, v255, 35
	v_lshl_add_u64 v[72:73], v[154:155], 0, v[140:141]
	global_store_dwordx4 v[72:73], v[96:99], off sc1
	global_store_dwordx4 v[72:73], v[88:91], off offset:16 sc1
	global_store_dwordx4 v[72:73], v[68:71], off offset:512 sc1
	global_store_dwordx4 v[72:73], v[64:67], off offset:528 sc1
	v_readlane_b32 s95, v255, 37
	v_readlane_b32 s63, v255, 41
	v_lshl_add_u64 v[64:65], v[154:155], 0, v[142:143]
	global_store_dwordx4 v[64:65], v[60:63], off sc1
	global_store_dwordx4 v[64:65], v[56:59], off offset:16 sc1
	global_store_dwordx4 v[64:65], v[36:39], off offset:512 sc1
	global_store_dwordx4 v[64:65], v[28:31], off offset:528 sc1
	v_readlane_b32 s48, v252, 42
	s_nop 0
	v_lshl_add_u64 v[28:29], v[154:155], 0, v[144:145]
	global_store_dwordx4 v[28:29], v[52:55], off sc1
	global_store_dwordx4 v[28:29], v[48:51], off offset:16 sc1
	global_store_dwordx4 v[28:29], v[20:23], off offset:512 sc1
	global_store_dwordx4 v[28:29], v[16:19], off offset:528 sc1
	s_nop 1
	v_lshl_add_u64 v[16:17], v[154:155], 0, v[146:147]
	global_store_dwordx4 v[16:17], v[44:47], off sc1
	global_store_dwordx4 v[16:17], v[40:43], off offset:16 sc1
	global_store_dwordx4 v[16:17], v[12:15], off offset:512 sc1
	global_store_dwordx4 v[16:17], v[8:11], off offset:528 sc1
	s_nop 1
	v_lshl_add_u64 v[8:9], v[154:155], 0, v[148:149]
	global_store_dwordx4 v[8:9], v[32:35], off sc1
	global_store_dwordx4 v[8:9], v[24:27], off offset:16 sc1
	global_store_dwordx4 v[8:9], v[4:7], off offset:512 sc1
	global_store_dwordx4 v[8:9], v[0:3], off offset:528 sc1
	s_cbranch_vccnz .LBB0_855
	s_andn2_b64 vcc, exec, s[0:1]
	s_cbranch_vccnz .LBB0_854
	s_barrier
	s_branch .LBB0_854

.LBB0_923:
	v_ashrrev_i32_e32 v0, 31, v4
	v_lshrrev_b32_e32 v0, 23, v0
	v_add_u32_e32 v0, v4, v0
	v_ashrrev_i32_e32 v2, 9, v0
	s_waitcnt vmcnt(0)
	v_mul_i32_i24_e32 v1, 0x200, v2
	v_ashrrev_i32_e32 v3, 31, v2
	v_lshlrev_b32_e32 v6, 2, v1
	v_add_u32_e32 v0, 0x4000, v2
	v_lshlrev_b64 v[2:3], 13, v[2:3]
	v_sub_u32_e32 v6, v5, v6
	v_lshl_add_u64 v[2:3], s[10:11], 0, v[2:3]
	v_ashrrev_i32_e32 v7, 31, v6
	v_lshl_add_u64 v[10:11], v[6:7], 2, v[2:3]
	s_mov_b32 s8, 0x200000
	v_add_co_u32_e32 v12, vcc, s8, v10
	s_mov_b32 s8, 0x1000000
	s_nop 0
	v_addc_co_u32_e32 v13, vcc, 0, v11, vcc
	v_add_co_u32_e32 v14, vcc, s13, v10
	v_ashrrev_i32_e32 v1, 31, v0
	s_nop 0
	v_addc_co_u32_e32 v15, vcc, 0, v11, vcc
	v_add_co_u32_e32 v18, vcc, s14, v10
	v_lshlrev_b64 v[8:9], 13, v[0:1]
	s_nop 0
	v_addc_co_u32_e32 v19, vcc, 0, v11, vcc
	v_add_co_u32_e32 v30, vcc, s12, v10
	v_lshl_add_u64 v[8:9], s[2:3], 0, v[8:9]
	s_nop 0
	v_addc_co_u32_e32 v31, vcc, 0, v11, vcc
	v_add_co_u32_e32 v34, vcc, s15, v10
	v_lshlrev_b64 v[2:3], 1, v[6:7]
	s_nop 0
	v_addc_co_u32_e32 v35, vcc, 0, v11, vcc
	v_add_co_u32_e32 v38, vcc, s16, v10
	v_lshl_add_u64 v[52:53], v[8:9], 0, v[2:3]
	s_nop 0
	v_addc_co_u32_e32 v39, vcc, 0, v11, vcc
	v_add_co_u32_e32 v50, vcc, s17, v10
	v_lshlrev_b64 v[0:1], 12, v[0:1]
	s_nop 0
	v_addc_co_u32_e32 v51, vcc, 0, v11, vcc
	v_add_co_u32_e32 v22, vcc, s8, v10
	s_mov_b32 s8, 0x1200000
	s_nop 0
	v_addc_co_u32_e32 v23, vcc, 0, v11, vcc
	v_add_co_u32_e32 v26, vcc, s8, v10
	s_mov_b32 s8, 0x1400000
	s_nop 0
	v_addc_co_u32_e32 v27, vcc, 0, v11, vcc
	v_add_co_u32_e32 v42, vcc, s8, v10
	v_lshl_add_u64 v[0:1], s[62:63], 0, v[0:1]
	s_nop 0
	v_addc_co_u32_e32 v43, vcc, 0, v11, vcc
	v_add_co_u32_e32 v46, vcc, s18, v10
	v_lshl_add_u64 v[0:1], v[0:1], 0, v[2:3]
	s_nop 0
	v_addc_co_u32_e32 v47, vcc, 0, v11, vcc
	global_load_dwordx4 v[6:9], v[10:11], off
	s_nop 0
	global_load_dwordx4 v[10:13], v[12:13], off
	s_nop 0
	global_load_dwordx4 v[14:17], v[14:15], off
	s_nop 0
	global_load_dwordx4 v[18:21], v[18:19], off
	s_nop 0
	global_load_dwordx4 v[22:25], v[22:23], off
	s_nop 0
	global_load_dwordx4 v[26:29], v[26:27], off
	s_nop 0
	global_load_dwordx4 v[30:33], v[30:31], off
	s_nop 0
	global_load_dwordx4 v[34:37], v[34:35], off
	s_nop 0
	global_load_dwordx2 v[54:55], v[52:53], off
	s_nop 0
	global_load_dwordx4 v[38:41], v[38:39], off
	s_nop 0
	global_load_dwordx4 v[42:45], v[42:43], off
	s_nop 0
	global_load_dwordx4 v[46:49], v[46:47], off
	v_add_co_u32_e32 v52, vcc, s9, v52
	v_add_u32_e32 v4, s48, v4
	s_nop 0
	v_addc_co_u32_e32 v53, vcc, 0, v53, vcc
	global_load_dwordx2 v[56:57], v[52:53], off
	s_nop 0
	global_load_dwordx4 v[50:53], v[50:51], off
	s_mov_b32 s8, 0x1ffff
	v_cmp_lt_i32_e32 vcc, s8, v4
	s_or_b64 s[6:7], vcc, s[6:7]
	v_add_u32_e32 v5, s4, v5
	s_waitcnt vmcnt(12)
	v_pk_add_f32 v[2:3], v[8:9], v[12:13]
	v_pk_add_f32 v[6:7], v[6:7], v[10:11]
	s_waitcnt vmcnt(11)
	v_pk_add_f32 v[2:3], v[2:3], v[16:17]
	v_pk_add_f32 v[6:7], v[6:7], v[14:15]
	s_waitcnt vmcnt(10)
	v_pk_add_f32 v[2:3], v[2:3], v[20:21]
	v_pk_add_f32 v[6:7], v[6:7], v[18:19]
	s_waitcnt vmcnt(8)
	v_pk_add_f32 v[8:9], v[24:25], v[28:29]
	v_pk_add_f32 v[10:11], v[22:23], v[26:27]
	s_waitcnt vmcnt(7)
	v_pk_add_f32 v[2:3], v[2:3], v[32:33]
	v_pk_add_f32 v[6:7], v[6:7], v[30:31]
	s_waitcnt vmcnt(3)
	v_pk_add_f32 v[8:9], v[8:9], v[44:45]
	v_pk_add_f32 v[10:11], v[10:11], v[42:43]
	v_pk_add_f32 v[2:3], v[2:3], v[36:37]
	v_pk_add_f32 v[6:7], v[6:7], v[34:35]
	s_waitcnt vmcnt(2)
	v_pk_add_f32 v[8:9], v[8:9], v[48:49]
	s_waitcnt vmcnt(1)
	v_lshlrev_b32_e32 v14, 16, v56
	v_and_b32_e32 v15, 0xffff0000, v56
	v_lshlrev_b32_e32 v16, 16, v57
	v_and_b32_e32 v17, 0xffff0000, v57
	v_pk_add_f32 v[10:11], v[10:11], v[46:47]
	v_pk_add_f32 v[2:3], v[2:3], v[40:41]
	v_pk_add_f32 v[6:7], v[6:7], v[38:39]
	v_lshlrev_b32_e32 v12, 16, v54
	v_and_b32_e32 v13, 0xffff0000, v54
	v_lshlrev_b32_e32 v22, 16, v55
	v_and_b32_e32 v23, 0xffff0000, v55
	v_pk_mul_f32 v[10:11], v[10:11], v[14:15]
	v_pk_mul_f32 v[8:9], v[8:9], v[16:17]
	s_waitcnt vmcnt(0)
	v_pk_add_f32 v[2:3], v[2:3], v[52:53]
	v_pk_add_f32 v[6:7], v[6:7], v[50:51]
	v_pk_fma_f32 v[2:3], v[2:3], v[22:23], v[8:9]
	v_pk_fma_f32 v[6:7], v[6:7], v[12:13], v[10:11]
	v_bfe_u32 v10, v2, 16, 1
	v_bfe_u32 v8, v6, 16, 1
	v_bfe_u32 v9, v7, 16, 1
	v_bfe_u32 v11, v3, 16, 1
	v_add3_u32 v6, v6, v8, s33
	v_add3_u32 v2, v2, v10, s33
	v_add3_u32 v7, v7, v9, s33
	v_add3_u32 v3, v3, v11, s33
	v_lshrrev_b32_e32 v6, 16, v6
	v_lshrrev_b32_e32 v8, 16, v2
	v_and_or_b32 v2, v7, s96, v6
	v_and_or_b32 v3, v3, s96, v8
	global_store_dwordx2 v[0:1], v[2:3], off sc1
	s_andn2_b64 exec, exec, s[6:7]
	s_cbranch_execnz .LBB0_923

.LBB0_999:
	v_readlane_b32 s28, v249, 60
	s_waitcnt vmcnt(0)
	v_pk_fma_f32 v[146:147], v[142:143], v[62:63], v[146:147]
	v_pk_fma_f32 v[144:145], v[140:141], v[60:61], v[144:145]
	v_pk_fma_f32 v[148:149], v[136:137], v[56:57], v[148:149]
	v_readlane_b32 s29, v249, 61
	v_cvt_pk_bf16_f32 v144, v144, v145
	v_cvt_pk_bf16_f32 v145, v146, v147
	v_cvt_pk_bf16_f32 v146, v148, v149
	s_mov_b64 s[42:43], 0
	v_pk_fma_f32 v[150:151], v[138:139], v[58:59], v[150:151]
	v_lshl_add_u64 v[148:149], v[166:167], 1, s[28:29]
	v_cvt_pk_bf16_f32 v147, v150, v151
	global_store_dwordx4 v[148:149], v[144:147], off sc1
.LBB0_1000:
	v_readlane_b32 s28, v255, 49
	s_nop 0
	v_lshlrev_b64 v[144:145], 2, v[166:167]
	v_readlane_b32 s29, v255, 50
	s_and_b64 vcc, exec, s[42:43]
	s_nop 0
	v_lshl_add_u64 v[146:147], s[28:29], 0, v[144:145]
	v_readlane_b32 s28, v249, 58
	v_readlane_b32 s29, v249, 59
	s_nop 1
	v_lshl_add_u64 v[144:145], s[28:29], 0, v[144:145]
	s_cbranch_vccz .LBB0_1002
	global_load_dwordx4 v[148:151], v[146:147], off
	s_waitcnt vmcnt(0)
	v_pk_fma_f32 v[142:143], v[142:143], v[62:63], v[150:151]
	v_pk_fma_f32 v[140:141], v[140:141], v[60:61], v[148:149]
	global_store_dwordx4 v[144:145], v[140:143], off sc1
	global_load_dwordx4 v[140:143], v[146:147], off offset:16
	s_waitcnt vmcnt(0)
	v_pk_fma_f32 v[138:139], v[138:139], v[58:59], v[142:143]
	v_pk_fma_f32 v[136:137], v[136:137], v[56:57], v[140:141]
	global_store_dwordx4 v[144:145], v[136:139], off offset:16 sc1

.LBB0_1007:
	s_waitcnt vmcnt(0)
	v_pk_fma_f32 v[138:139], v[134:135], v[46:47], v[138:139]
	v_pk_fma_f32 v[136:137], v[132:133], v[44:45], v[136:137]
	s_mov_b64 s[44:45], 0
	v_pk_fma_f32 v[142:143], v[130:131], v[42:43], v[142:143]
	v_pk_fma_f32 v[140:141], v[128:129], v[40:41], v[140:141]
	v_cvt_pk_bf16_f32 v136, v136, v137
	v_cvt_pk_bf16_f32 v137, v138, v139
	s_nop 0
	v_cvt_pk_bf16_f32 v138, v140, v141
	v_cvt_pk_bf16_f32 v139, v142, v143
	global_store_dwordx4 v[148:149], v[136:139], off offset:256 sc1
.LBB0_1008:
	s_and_b64 vcc, exec, s[44:45]
	s_cbranch_vccz .LBB0_1010
	global_load_dwordx4 v[136:139], v[146:147], off offset:512
	s_waitcnt vmcnt(0)
	v_pk_fma_f32 v[134:135], v[134:135], v[46:47], v[138:139]
	v_pk_fma_f32 v[132:133], v[132:133], v[44:45], v[136:137]
	global_store_dwordx4 v[144:145], v[132:135], off offset:512 sc1
	global_load_dwordx4 v[132:135], v[146:147], off offset:528
	s_waitcnt vmcnt(0)
	v_pk_fma_f32 v[130:131], v[130:131], v[42:43], v[134:135]
	v_pk_fma_f32 v[128:129], v[128:129], v[40:41], v[132:133]
	global_store_dwordx4 v[144:145], v[128:131], off offset:528 sc1

.LBB0_1015:
	v_readlane_b32 s28, v249, 60
	s_waitcnt vmcnt(0)
	v_pk_fma_f32 v[130:131], v[126:127], v[62:63], v[130:131]
	v_pk_fma_f32 v[128:129], v[124:125], v[60:61], v[128:129]
	v_pk_fma_f32 v[132:133], v[120:121], v[56:57], v[132:133]
	v_readlane_b32 s29, v249, 61
	v_cvt_pk_bf16_f32 v128, v128, v129
	v_cvt_pk_bf16_f32 v129, v130, v131
	v_cvt_pk_bf16_f32 v130, v132, v133
	s_mov_b64 s[44:45], 0
	v_pk_fma_f32 v[134:135], v[122:123], v[58:59], v[134:135]
	v_lshl_add_u64 v[132:133], v[136:137], 1, s[28:29]
	v_cvt_pk_bf16_f32 v131, v134, v135
	global_store_dwordx4 v[132:133], v[128:131], off sc1
.LBB0_1016:
	v_readlane_b32 s28, v255, 49
	s_nop 0
	v_lshlrev_b64 v[128:129], 2, v[136:137]
	v_readlane_b32 s29, v255, 50
	s_and_b64 vcc, exec, s[44:45]
	s_nop 0
	v_lshl_add_u64 v[130:131], s[28:29], 0, v[128:129]
	v_readlane_b32 s28, v249, 58
	v_readlane_b32 s29, v249, 59
	s_nop 1
	v_lshl_add_u64 v[128:129], s[28:29], 0, v[128:129]
	s_cbranch_vccz .LBB0_1083
	global_load_dwordx4 v[132:135], v[130:131], off
	s_waitcnt vmcnt(0)
	v_pk_fma_f32 v[126:127], v[126:127], v[62:63], v[134:135]
	v_pk_fma_f32 v[124:125], v[124:125], v[60:61], v[132:133]
	global_store_dwordx4 v[128:129], v[124:127], off sc1
	global_load_dwordx4 v[124:127], v[130:131], off offset:16
	s_waitcnt vmcnt(0)
	v_pk_fma_f32 v[122:123], v[122:123], v[58:59], v[126:127]
	v_pk_fma_f32 v[120:121], v[120:121], v[56:57], v[124:125]
	global_store_dwordx4 v[128:129], v[120:123], off offset:16 sc1
	s_and_b64 vcc, exec, s[42:43]
	s_mov_b64 s[44:45], -1
	s_cbranch_vccz .LBB0_1084
.LBB0_1018:
	s_and_b64 vcc, exec, s[44:45]
	s_cbranch_vccz .LBB0_1020
	global_load_dwordx4 v[120:123], v[130:131], off offset:512
	s_waitcnt vmcnt(0)
	v_pk_fma_f32 v[118:119], v[118:119], v[46:47], v[122:123]
	v_pk_fma_f32 v[116:117], v[116:117], v[44:45], v[120:121]
	global_store_dwordx4 v[128:129], v[116:119], off offset:512 sc1
	global_load_dwordx4 v[116:119], v[130:131], off offset:528
	s_waitcnt vmcnt(0)
	v_pk_fma_f32 v[114:115], v[114:115], v[42:43], v[118:119]
	v_pk_fma_f32 v[112:113], v[112:113], v[40:41], v[116:117]
	global_store_dwordx4 v[128:129], v[112:115], off offset:528 sc1

.LBB0_1025:
	v_readlane_b32 s28, v249, 60
	s_waitcnt vmcnt(0)
	v_pk_fma_f32 v[114:115], v[110:111], v[62:63], v[114:115]
	v_pk_fma_f32 v[112:113], v[108:109], v[60:61], v[112:113]
	v_pk_fma_f32 v[116:117], v[104:105], v[56:57], v[116:117]
	v_readlane_b32 s29, v249, 61
	v_cvt_pk_bf16_f32 v112, v112, v113
	v_cvt_pk_bf16_f32 v113, v114, v115
	v_cvt_pk_bf16_f32 v114, v116, v117
	s_mov_b64 s[44:45], 0
	v_pk_fma_f32 v[118:119], v[106:107], v[58:59], v[118:119]
	v_lshl_add_u64 v[116:117], v[120:121], 1, s[28:29]
	v_cvt_pk_bf16_f32 v115, v118, v119
	global_store_dwordx4 v[116:117], v[112:115], off sc1
.LBB0_1026:
	v_readlane_b32 s28, v255, 49
	s_nop 0
	v_lshlrev_b64 v[112:113], 2, v[120:121]
	v_readlane_b32 s29, v255, 50
	s_and_b64 vcc, exec, s[44:45]
	s_nop 0
	v_lshl_add_u64 v[114:115], s[28:29], 0, v[112:113]
	v_readlane_b32 s28, v249, 58
	v_readlane_b32 s29, v249, 59
	s_nop 1
	v_lshl_add_u64 v[112:113], s[28:29], 0, v[112:113]
	s_cbranch_vccz .LBB0_1089
	global_load_dwordx4 v[116:119], v[114:115], off
	s_waitcnt vmcnt(0)
	v_pk_fma_f32 v[110:111], v[110:111], v[62:63], v[118:119]
	v_pk_fma_f32 v[108:109], v[108:109], v[60:61], v[116:117]
	global_store_dwordx4 v[112:113], v[108:111], off sc1
	global_load_dwordx4 v[108:111], v[114:115], off offset:16
	s_waitcnt vmcnt(0)
	v_pk_fma_f32 v[106:107], v[106:107], v[58:59], v[110:111]
	v_pk_fma_f32 v[104:105], v[104:105], v[56:57], v[108:109]
	global_store_dwordx4 v[112:113], v[104:107], off offset:16 sc1
	s_and_b64 vcc, exec, s[42:43]
	s_mov_b64 s[44:45], -1
	s_cbranch_vccz .LBB0_1090
.LBB0_1028:
	s_and_b64 vcc, exec, s[44:45]
	s_cbranch_vccz .LBB0_1030
	global_load_dwordx4 v[104:107], v[114:115], off offset:512
	s_waitcnt vmcnt(0)
	v_pk_fma_f32 v[102:103], v[102:103], v[46:47], v[106:107]
	v_pk_fma_f32 v[100:101], v[100:101], v[44:45], v[104:105]
	global_store_dwordx4 v[112:113], v[100:103], off offset:512 sc1
	global_load_dwordx4 v[100:103], v[114:115], off offset:528
	s_waitcnt vmcnt(0)
	v_pk_fma_f32 v[98:99], v[98:99], v[42:43], v[102:103]
	v_pk_fma_f32 v[96:97], v[96:97], v[40:41], v[100:101]
	global_store_dwordx4 v[112:113], v[96:99], off offset:528 sc1

.LBB0_1035:
	v_readlane_b32 s28, v249, 60
	s_waitcnt vmcnt(0)
	v_pk_fma_f32 v[98:99], v[94:95], v[62:63], v[98:99]
	v_pk_fma_f32 v[96:97], v[92:93], v[60:61], v[96:97]
	v_pk_fma_f32 v[100:101], v[88:89], v[56:57], v[100:101]
	v_readlane_b32 s29, v249, 61
	v_cvt_pk_bf16_f32 v96, v96, v97
	v_cvt_pk_bf16_f32 v97, v98, v99
	v_cvt_pk_bf16_f32 v98, v100, v101
	s_mov_b64 s[44:45], 0
	v_pk_fma_f32 v[102:103], v[90:91], v[58:59], v[102:103]
	v_lshl_add_u64 v[100:101], v[104:105], 1, s[28:29]
	v_cvt_pk_bf16_f32 v99, v102, v103
	global_store_dwordx4 v[100:101], v[96:99], off sc1
.LBB0_1036:
	v_readlane_b32 s28, v255, 49
	s_nop 0
	v_lshlrev_b64 v[96:97], 2, v[104:105]
	v_readlane_b32 s29, v255, 50
	s_and_b64 vcc, exec, s[44:45]
	s_nop 0
	v_lshl_add_u64 v[98:99], s[28:29], 0, v[96:97]
	v_readlane_b32 s28, v249, 58
	v_readlane_b32 s29, v249, 59
	s_nop 1
	v_lshl_add_u64 v[96:97], s[28:29], 0, v[96:97]
	s_cbranch_vccz .LBB0_1095
	global_load_dwordx4 v[100:103], v[98:99], off
	s_waitcnt vmcnt(0)
	v_pk_fma_f32 v[94:95], v[94:95], v[62:63], v[102:103]
	v_pk_fma_f32 v[92:93], v[92:93], v[60:61], v[100:101]
	global_store_dwordx4 v[96:97], v[92:95], off sc1
	global_load_dwordx4 v[92:95], v[98:99], off offset:16
	s_waitcnt vmcnt(0)
	v_pk_fma_f32 v[90:91], v[90:91], v[58:59], v[94:95]
	v_pk_fma_f32 v[88:89], v[88:89], v[56:57], v[92:93]
	global_store_dwordx4 v[96:97], v[88:91], off offset:16 sc1
	s_and_b64 vcc, exec, s[42:43]
	s_mov_b64 s[44:45], -1
	s_cbranch_vccz .LBB0_1096
.LBB0_1038:
	s_and_b64 vcc, exec, s[44:45]
	s_cbranch_vccz .LBB0_1040
	global_load_dwordx4 v[88:91], v[98:99], off offset:512
	s_waitcnt vmcnt(0)
	v_pk_fma_f32 v[86:87], v[86:87], v[46:47], v[90:91]
	v_pk_fma_f32 v[84:85], v[84:85], v[44:45], v[88:89]
	global_store_dwordx4 v[96:97], v[84:87], off offset:512 sc1
	global_load_dwordx4 v[84:87], v[98:99], off offset:528
	s_waitcnt vmcnt(0)
	v_pk_fma_f32 v[82:83], v[82:83], v[42:43], v[86:87]
	v_pk_fma_f32 v[80:81], v[80:81], v[40:41], v[84:85]
	global_store_dwordx4 v[96:97], v[80:83], off offset:528 sc1

.LBB0_1045:
	v_readlane_b32 s28, v249, 60
	s_waitcnt vmcnt(0)
	v_pk_fma_f32 v[82:83], v[78:79], v[62:63], v[82:83]
	v_pk_fma_f32 v[80:81], v[76:77], v[60:61], v[80:81]
	v_pk_fma_f32 v[84:85], v[72:73], v[56:57], v[84:85]
	v_readlane_b32 s29, v249, 61
	v_cvt_pk_bf16_f32 v80, v80, v81
	v_cvt_pk_bf16_f32 v81, v82, v83
	v_cvt_pk_bf16_f32 v82, v84, v85
	s_mov_b64 s[44:45], 0
	v_pk_fma_f32 v[86:87], v[74:75], v[58:59], v[86:87]
	v_lshl_add_u64 v[84:85], v[88:89], 1, s[28:29]
	v_cvt_pk_bf16_f32 v83, v86, v87
	global_store_dwordx4 v[84:85], v[80:83], off sc1
.LBB0_1046:
	v_readlane_b32 s28, v255, 49
	s_nop 0
	v_lshlrev_b64 v[80:81], 2, v[88:89]
	v_readlane_b32 s29, v255, 50
	s_and_b64 vcc, exec, s[44:45]
	s_nop 0
	v_lshl_add_u64 v[82:83], s[28:29], 0, v[80:81]
	v_readlane_b32 s28, v249, 58
	v_readlane_b32 s29, v249, 59
	s_nop 1
	v_lshl_add_u64 v[80:81], s[28:29], 0, v[80:81]
	s_cbranch_vccz .LBB0_1101
	global_load_dwordx4 v[84:87], v[82:83], off
	s_waitcnt vmcnt(0)
	v_pk_fma_f32 v[78:79], v[78:79], v[62:63], v[86:87]
	v_pk_fma_f32 v[76:77], v[76:77], v[60:61], v[84:85]
	global_store_dwordx4 v[80:81], v[76:79], off sc1
	global_load_dwordx4 v[76:79], v[82:83], off offset:16
	s_waitcnt vmcnt(0)
	v_pk_fma_f32 v[74:75], v[74:75], v[58:59], v[78:79]
	v_pk_fma_f32 v[72:73], v[72:73], v[56:57], v[76:77]
	global_store_dwordx4 v[80:81], v[72:75], off offset:16 sc1
	s_and_b64 vcc, exec, s[42:43]
	s_mov_b64 s[44:45], -1
	s_cbranch_vccz .LBB0_1102
.LBB0_1048:
	s_and_b64 vcc, exec, s[44:45]
	s_cbranch_vccz .LBB0_1050
	global_load_dwordx4 v[72:75], v[82:83], off offset:512
	s_waitcnt vmcnt(0)
	v_pk_fma_f32 v[70:71], v[70:71], v[46:47], v[74:75]
	v_pk_fma_f32 v[68:69], v[68:69], v[44:45], v[72:73]
	global_store_dwordx4 v[80:81], v[68:71], off offset:512 sc1
	global_load_dwordx4 v[68:71], v[82:83], off offset:528
	s_waitcnt vmcnt(0)
	v_pk_fma_f32 v[66:67], v[66:67], v[42:43], v[70:71]
	v_pk_fma_f32 v[64:65], v[64:65], v[40:41], v[68:69]
	global_store_dwordx4 v[80:81], v[64:67], off offset:528 sc1

.LBB0_1055:
	v_readlane_b32 s28, v249, 60
	s_waitcnt vmcnt(0)
	v_pk_fma_f32 v[66:67], v[54:55], v[62:63], v[66:67]
	v_pk_fma_f32 v[64:65], v[52:53], v[60:61], v[64:65]
	v_pk_fma_f32 v[68:69], v[48:49], v[56:57], v[68:69]
	v_readlane_b32 s29, v249, 61
	v_cvt_pk_bf16_f32 v64, v64, v65
	v_cvt_pk_bf16_f32 v65, v66, v67
	v_cvt_pk_bf16_f32 v66, v68, v69
	s_mov_b64 s[44:45], 0
	v_pk_fma_f32 v[70:71], v[50:51], v[58:59], v[70:71]
	v_lshl_add_u64 v[68:69], v[72:73], 1, s[28:29]
	v_cvt_pk_bf16_f32 v67, v70, v71
	global_store_dwordx4 v[68:69], v[64:67], off sc1
.LBB0_1056:
	v_readlane_b32 s28, v255, 49
	s_nop 0
	v_lshlrev_b64 v[64:65], 2, v[72:73]
	v_readlane_b32 s29, v255, 50
	s_and_b64 vcc, exec, s[44:45]
	s_nop 0
	v_lshl_add_u64 v[66:67], s[28:29], 0, v[64:65]
	v_readlane_b32 s28, v249, 58
	v_readlane_b32 s29, v249, 59
	s_nop 1
	v_lshl_add_u64 v[64:65], s[28:29], 0, v[64:65]
	s_cbranch_vccz .LBB0_1107
	global_load_dwordx4 v[68:71], v[66:67], off
	s_waitcnt vmcnt(0)
	v_pk_fma_f32 v[54:55], v[54:55], v[62:63], v[70:71]
	v_pk_fma_f32 v[52:53], v[52:53], v[60:61], v[68:69]
	global_store_dwordx4 v[64:65], v[52:55], off sc1
	global_load_dwordx4 v[52:55], v[66:67], off offset:16
	s_waitcnt vmcnt(0)
	v_pk_fma_f32 v[50:51], v[50:51], v[58:59], v[54:55]
	v_pk_fma_f32 v[48:49], v[48:49], v[56:57], v[52:53]
	global_store_dwordx4 v[64:65], v[48:51], off offset:16 sc1
	s_and_b64 vcc, exec, s[42:43]
	s_mov_b64 s[44:45], -1
	s_cbranch_vccz .LBB0_1108
.LBB0_1058:
	s_and_b64 vcc, exec, s[44:45]
	s_cbranch_vccz .LBB0_1060
	global_load_dwordx4 v[48:51], v[66:67], off offset:512
	s_waitcnt vmcnt(0)
	v_pk_fma_f32 v[38:39], v[38:39], v[46:47], v[50:51]
	v_pk_fma_f32 v[36:37], v[36:37], v[44:45], v[48:49]
	global_store_dwordx4 v[64:65], v[36:39], off offset:512 sc1
	global_load_dwordx4 v[36:39], v[66:67], off offset:528
	s_waitcnt vmcnt(0)
	v_pk_fma_f32 v[34:35], v[34:35], v[42:43], v[38:39]
	v_pk_fma_f32 v[32:33], v[32:33], v[40:41], v[36:37]
	global_store_dwordx4 v[64:65], v[32:35], off offset:528 sc1

.LBB0_1065:
	v_readlane_b32 s28, v249, 60
	s_waitcnt vmcnt(0)
	v_pk_fma_f32 v[34:35], v[30:31], v[62:63], v[34:35]
	v_pk_fma_f32 v[32:33], v[28:29], v[60:61], v[32:33]
	v_pk_fma_f32 v[36:37], v[24:25], v[56:57], v[36:37]
	v_readlane_b32 s29, v249, 61
	v_cvt_pk_bf16_f32 v32, v32, v33
	v_cvt_pk_bf16_f32 v33, v34, v35
	v_cvt_pk_bf16_f32 v34, v36, v37
	s_mov_b64 s[44:45], 0
	v_pk_fma_f32 v[38:39], v[26:27], v[58:59], v[38:39]
	v_lshl_add_u64 v[36:37], v[48:49], 1, s[28:29]
	v_cvt_pk_bf16_f32 v35, v38, v39
	global_store_dwordx4 v[36:37], v[32:35], off sc1
.LBB0_1066:
	v_readlane_b32 s28, v255, 49
	s_nop 0
	v_lshlrev_b64 v[32:33], 2, v[48:49]
	v_readlane_b32 s29, v255, 50
	s_and_b64 vcc, exec, s[44:45]
	s_nop 0
	v_lshl_add_u64 v[34:35], s[28:29], 0, v[32:33]
	v_readlane_b32 s28, v249, 58
	v_readlane_b32 s29, v249, 59
	s_nop 1
	v_lshl_add_u64 v[32:33], s[28:29], 0, v[32:33]
	s_cbranch_vccz .LBB0_1113
	global_load_dwordx4 v[36:39], v[34:35], off
	s_waitcnt vmcnt(0)
	v_pk_fma_f32 v[30:31], v[30:31], v[62:63], v[38:39]
	v_pk_fma_f32 v[28:29], v[28:29], v[60:61], v[36:37]
	global_store_dwordx4 v[32:33], v[28:31], off sc1
	global_load_dwordx4 v[28:31], v[34:35], off offset:16
	s_waitcnt vmcnt(0)
	v_pk_fma_f32 v[26:27], v[26:27], v[58:59], v[30:31]
	v_pk_fma_f32 v[24:25], v[24:25], v[56:57], v[28:29]
	global_store_dwordx4 v[32:33], v[24:27], off offset:16 sc1
	s_and_b64 vcc, exec, s[42:43]
	s_mov_b64 s[44:45], -1
	s_cbranch_vccz .LBB0_1114
.LBB0_1068:
	s_and_b64 vcc, exec, s[44:45]
	s_cbranch_vccz .LBB0_1070
	global_load_dwordx4 v[24:27], v[34:35], off offset:512
	s_waitcnt vmcnt(0)
	v_pk_fma_f32 v[22:23], v[22:23], v[46:47], v[26:27]
	v_pk_fma_f32 v[20:21], v[20:21], v[44:45], v[24:25]
	global_store_dwordx4 v[32:33], v[20:23], off offset:512 sc1
	global_load_dwordx4 v[20:23], v[34:35], off offset:528
	s_waitcnt vmcnt(0)
	v_pk_fma_f32 v[18:19], v[18:19], v[42:43], v[22:23]
	v_pk_fma_f32 v[16:17], v[16:17], v[40:41], v[20:21]
	global_store_dwordx4 v[32:33], v[16:19], off offset:528 sc1

.LBB0_1075:
	v_readlane_b32 s28, v249, 60
	s_waitcnt vmcnt(0)
	v_pk_fma_f32 v[18:19], v[14:15], v[62:63], v[18:19]
	v_pk_fma_f32 v[16:17], v[12:13], v[60:61], v[16:17]
	v_pk_fma_f32 v[20:21], v[8:9], v[56:57], v[20:21]
	v_readlane_b32 s29, v249, 61
	v_cvt_pk_bf16_f32 v16, v16, v17
	v_cvt_pk_bf16_f32 v17, v18, v19
	v_cvt_pk_bf16_f32 v18, v20, v21
	s_mov_b64 s[44:45], 0
	v_pk_fma_f32 v[22:23], v[10:11], v[58:59], v[22:23]
	v_lshl_add_u64 v[20:21], v[24:25], 1, s[28:29]
	v_cvt_pk_bf16_f32 v19, v22, v23
	global_store_dwordx4 v[20:21], v[16:19], off sc1
.LBB0_1076:
	v_readlane_b32 s28, v255, 49
	s_nop 0
	v_lshlrev_b64 v[16:17], 2, v[24:25]
	v_readlane_b32 s29, v255, 50
	s_and_b64 vcc, exec, s[44:45]
	s_nop 0
	v_lshl_add_u64 v[18:19], s[28:29], 0, v[16:17]
	v_readlane_b32 s28, v249, 58
	v_readlane_b32 s29, v249, 59
	s_nop 1
	v_lshl_add_u64 v[16:17], s[28:29], 0, v[16:17]
	s_cbranch_vccz .LBB0_1119
	global_load_dwordx4 v[20:23], v[18:19], off
	s_waitcnt vmcnt(0)
	v_pk_fma_f32 v[14:15], v[14:15], v[62:63], v[22:23]
	v_pk_fma_f32 v[12:13], v[12:13], v[60:61], v[20:21]
	global_store_dwordx4 v[16:17], v[12:15], off sc1
	global_load_dwordx4 v[12:15], v[18:19], off offset:16
	s_waitcnt vmcnt(0)
	v_pk_fma_f32 v[10:11], v[10:11], v[58:59], v[14:15]
	v_pk_fma_f32 v[8:9], v[8:9], v[56:57], v[12:13]
	global_store_dwordx4 v[16:17], v[8:11], off offset:16 sc1
	s_and_b64 vcc, exec, s[42:43]
	s_mov_b64 s[42:43], -1
	s_cbranch_vccz .LBB0_1120
.LBB0_1078:
	s_and_b64 vcc, exec, s[42:43]
	s_cbranch_vccz .LBB0_1080
	global_load_dwordx4 v[8:11], v[18:19], off offset:512
	s_waitcnt vmcnt(0)
	v_pk_fma_f32 v[6:7], v[6:7], v[46:47], v[10:11]
	v_pk_fma_f32 v[4:5], v[4:5], v[44:45], v[8:9]
	global_store_dwordx4 v[16:17], v[4:7], off offset:512 sc1
	global_load_dwordx4 v[4:7], v[18:19], off offset:528
	s_waitcnt vmcnt(0)
	v_pk_fma_f32 v[2:3], v[2:3], v[42:43], v[6:7]
	v_pk_fma_f32 v[0:1], v[0:1], v[40:41], v[4:5]
	global_store_dwordx4 v[16:17], v[0:3], off offset:528 sc1

.LBB0_1088:
	s_waitcnt vmcnt(0)
	v_pk_fma_f32 v[122:123], v[118:119], v[46:47], v[122:123]
	v_pk_fma_f32 v[120:121], v[116:117], v[44:45], v[120:121]
	v_pk_fma_f32 v[126:127], v[114:115], v[42:43], v[126:127]
	v_pk_fma_f32 v[124:125], v[112:113], v[40:41], v[124:125]
	v_cvt_pk_bf16_f32 v120, v120, v121
	v_cvt_pk_bf16_f32 v121, v122, v123
	s_nop 0
	v_cvt_pk_bf16_f32 v122, v124, v125
	v_cvt_pk_bf16_f32 v123, v126, v127
	global_store_dwordx4 v[132:133], v[120:123], off offset:256 sc1
	s_branch .LBB0_1020

.LBB0_1094:
	s_waitcnt vmcnt(0)
	v_pk_fma_f32 v[106:107], v[102:103], v[46:47], v[106:107]
	v_pk_fma_f32 v[104:105], v[100:101], v[44:45], v[104:105]
	v_pk_fma_f32 v[110:111], v[98:99], v[42:43], v[110:111]
	v_pk_fma_f32 v[108:109], v[96:97], v[40:41], v[108:109]
	v_cvt_pk_bf16_f32 v104, v104, v105
	v_cvt_pk_bf16_f32 v105, v106, v107
	s_nop 0
	v_cvt_pk_bf16_f32 v106, v108, v109
	v_cvt_pk_bf16_f32 v107, v110, v111
	global_store_dwordx4 v[116:117], v[104:107], off offset:256 sc1
	s_branch .LBB0_1030

.LBB0_1100:
	s_waitcnt vmcnt(0)
	v_pk_fma_f32 v[90:91], v[86:87], v[46:47], v[90:91]
	v_pk_fma_f32 v[88:89], v[84:85], v[44:45], v[88:89]
	v_pk_fma_f32 v[94:95], v[82:83], v[42:43], v[94:95]
	v_pk_fma_f32 v[92:93], v[80:81], v[40:41], v[92:93]
	v_cvt_pk_bf16_f32 v88, v88, v89
	v_cvt_pk_bf16_f32 v89, v90, v91
	s_nop 0
	v_cvt_pk_bf16_f32 v90, v92, v93
	v_cvt_pk_bf16_f32 v91, v94, v95
	global_store_dwordx4 v[100:101], v[88:91], off offset:256 sc1
	s_branch .LBB0_1040

.LBB0_1106:
	s_waitcnt vmcnt(0)
	v_pk_fma_f32 v[74:75], v[70:71], v[46:47], v[74:75]
	v_pk_fma_f32 v[72:73], v[68:69], v[44:45], v[72:73]
	v_pk_fma_f32 v[78:79], v[66:67], v[42:43], v[78:79]
	v_pk_fma_f32 v[76:77], v[64:65], v[40:41], v[76:77]
	v_cvt_pk_bf16_f32 v72, v72, v73
	v_cvt_pk_bf16_f32 v73, v74, v75
	s_nop 0
	v_cvt_pk_bf16_f32 v74, v76, v77
	v_cvt_pk_bf16_f32 v75, v78, v79
	global_store_dwordx4 v[84:85], v[72:75], off offset:256 sc1
	s_branch .LBB0_1050

.LBB0_1112:
	s_waitcnt vmcnt(0)
	v_pk_fma_f32 v[50:51], v[38:39], v[46:47], v[50:51]
	v_pk_fma_f32 v[48:49], v[36:37], v[44:45], v[48:49]
	v_pk_fma_f32 v[54:55], v[34:35], v[42:43], v[54:55]
	v_pk_fma_f32 v[52:53], v[32:33], v[40:41], v[52:53]
	v_cvt_pk_bf16_f32 v48, v48, v49
	v_cvt_pk_bf16_f32 v49, v50, v51
	s_nop 0
	v_cvt_pk_bf16_f32 v50, v52, v53
	v_cvt_pk_bf16_f32 v51, v54, v55
	global_store_dwordx4 v[68:69], v[48:51], off offset:256 sc1
	s_branch .LBB0_1060

.LBB0_1118:
	s_waitcnt vmcnt(0)
	v_pk_fma_f32 v[26:27], v[22:23], v[46:47], v[26:27]
	v_pk_fma_f32 v[24:25], v[20:21], v[44:45], v[24:25]
	v_pk_fma_f32 v[30:31], v[18:19], v[42:43], v[30:31]
	v_pk_fma_f32 v[28:29], v[16:17], v[40:41], v[28:29]
	v_cvt_pk_bf16_f32 v24, v24, v25
	v_cvt_pk_bf16_f32 v25, v26, v27
	s_nop 0
	v_cvt_pk_bf16_f32 v26, v28, v29
	v_cvt_pk_bf16_f32 v27, v30, v31
	global_store_dwordx4 v[36:37], v[24:27], off offset:256 sc1
	s_branch .LBB0_1070

.LBB0_1124:
	s_waitcnt vmcnt(0)
	v_pk_fma_f32 v[10:11], v[6:7], v[46:47], v[10:11]
	v_pk_fma_f32 v[8:9], v[4:5], v[44:45], v[8:9]
	v_pk_fma_f32 v[14:15], v[2:3], v[42:43], v[14:15]
	v_pk_fma_f32 v[12:13], v[0:1], v[40:41], v[12:13]
	v_cvt_pk_bf16_f32 v8, v8, v9
	v_cvt_pk_bf16_f32 v9, v10, v11
	s_nop 0
	v_cvt_pk_bf16_f32 v10, v12, v13
	v_cvt_pk_bf16_f32 v11, v14, v15
	global_store_dwordx4 v[20:21], v[8:11], off offset:256 sc1
	s_branch .LBB0_1080

.LBB0_1139:
	v_lshl_or_b32 v112, s41, 8, v169
	v_ashrrev_i32_e32 v113, 31, v112
	v_lshlrev_b64 v[166:167], 2, v[112:113]
	v_lshl_add_u64 v[124:125], s[0:1], 0, v[166:167]
	global_load_dwordx4 v[116:119], v[124:125], off offset:16
	global_load_dwordx4 v[132:135], v[124:125], off
	global_load_dwordx4 v[112:115], v[124:125], off offset:528
	s_nop 0
	global_load_dwordx4 v[124:127], v[124:125], off offset:512
	s_ashr_i32 s41, s40, 31
	s_lshl_b64 s[28:29], s[40:41], 21
	v_readlane_b32 s38, v250, 6
	v_readlane_b32 s39, v250, 7
	s_add_u32 s28, s38, s28
	s_addc_u32 s29, s39, s29
	v_lshl_add_u64 v[166:167], s[28:29], 0, v[166:167]
	v_lshl_add_u64 v[172:173], v[166:167], 0, v[150:151]
	v_readlane_b32 s90, v255, 34
	v_readlane_b32 s94, v255, 36
	s_mov_b64 s[38:39], -1
	s_andn2_b64 vcc, exec, s[18:19]
	v_readlane_b32 s91, v255, 35
	v_readlane_b32 s95, v255, 37
	s_movk_i32 s25, 0x1000
	s_mov_b32 s48, 0x1600000
	s_waitcnt vmcnt(0)
	v_pk_mul_f32 v[138:139], v[138:139], v[118:119]
	v_pk_mul_f32 v[142:143], v[142:143], v[134:135]
	v_pk_mul_f32 v[122:123], v[122:123], v[114:115]
	v_pk_mul_f32 v[120:121], v[120:121], v[112:113]
	global_store_dwordx4 v[172:173], v[120:123], off offset:528 sc1
	v_pk_mul_f32 v[98:99], v[98:99], v[114:115]
	v_pk_mul_f32 v[96:97], v[96:97], v[112:113]
	v_lshl_add_u64 v[120:121], v[166:167], 0, v[152:153]
	global_store_dwordx4 v[120:121], v[96:99], off offset:528 sc1
	v_pk_mul_f32 v[82:83], v[82:83], v[114:115]
	v_pk_mul_f32 v[80:81], v[80:81], v[112:113]
	v_lshl_add_u64 v[96:97], v[166:167], 0, v[154:155]
	global_store_dwordx4 v[96:97], v[80:83], off offset:528 sc1
	v_pk_mul_f32 v[66:67], v[66:67], v[114:115]
	v_pk_mul_f32 v[64:65], v[64:65], v[112:113]
	v_lshl_add_u64 v[80:81], v[166:167], 0, v[156:157]
	global_store_dwordx4 v[80:81], v[64:67], off offset:528 sc1
	v_pk_mul_f32 v[50:51], v[50:51], v[114:115]
	v_pk_mul_f32 v[48:49], v[48:49], v[112:113]
	v_lshl_add_u64 v[64:65], v[166:167], 0, v[158:159]
	global_store_dwordx4 v[64:65], v[48:51], off offset:528 sc1
	v_pk_mul_f32 v[34:35], v[34:35], v[126:127]
	v_pk_mul_f32 v[32:33], v[32:33], v[124:125]
	v_lshl_add_u64 v[48:49], v[166:167], 0, v[160:161]
	global_store_dwordx4 v[48:49], v[32:35], off offset:512 sc1
	v_pk_mul_f32 v[26:27], v[26:27], v[114:115]
	v_pk_mul_f32 v[24:25], v[24:25], v[112:113]
	v_lshl_add_u64 v[32:33], v[166:167], 0, v[162:163]
	v_pk_mul_f32 v[18:19], v[18:19], v[126:127]
	v_pk_mul_f32 v[16:17], v[16:17], v[124:125]
	v_pk_mul_f32 v[10:11], v[10:11], v[114:115]
	v_pk_mul_f32 v[8:9], v[8:9], v[112:113]
	global_store_dwordx4 v[48:49], v[24:27], off offset:528 sc1
	global_store_dwordx4 v[32:33], v[16:19], off offset:512 sc1
	global_store_dwordx4 v[32:33], v[8:11], off offset:528 sc1
	v_pk_mul_f32 v[26:27], v[38:39], v[134:135]
	v_pk_mul_f32 v[24:25], v[36:37], v[132:133]
	v_lshl_add_u64 v[16:17], v[166:167], 0, v[164:165]
	v_pk_mul_f32 v[10:11], v[22:23], v[134:135]
	v_pk_mul_f32 v[8:9], v[20:21], v[132:133]
	v_pk_mul_f32 v[140:141], v[140:141], v[132:133]
	v_pk_mul_f32 v[136:137], v[136:137], v[116:117]
	v_pk_mul_f32 v[130:131], v[130:131], v[126:127]
	v_pk_mul_f32 v[128:129], v[128:129], v[124:125]
	v_pk_mul_f32 v[110:111], v[110:111], v[134:135]
	v_pk_mul_f32 v[108:109], v[108:109], v[132:133]
	v_pk_mul_f32 v[106:107], v[106:107], v[118:119]
	v_pk_mul_f32 v[104:105], v[104:105], v[116:117]
	v_pk_mul_f32 v[102:103], v[102:103], v[126:127]
	v_pk_mul_f32 v[100:101], v[100:101], v[124:125]
	v_pk_mul_f32 v[94:95], v[94:95], v[134:135]
	v_pk_mul_f32 v[92:93], v[92:93], v[132:133]
	v_pk_mul_f32 v[90:91], v[90:91], v[118:119]
	v_pk_mul_f32 v[88:89], v[88:89], v[116:117]
	v_pk_mul_f32 v[86:87], v[86:87], v[126:127]
	v_pk_mul_f32 v[84:85], v[84:85], v[124:125]
	v_pk_mul_f32 v[78:79], v[78:79], v[134:135]
	v_pk_mul_f32 v[76:77], v[76:77], v[132:133]
	v_pk_mul_f32 v[74:75], v[74:75], v[118:119]
	v_pk_mul_f32 v[72:73], v[72:73], v[116:117]
	v_pk_mul_f32 v[70:71], v[70:71], v[126:127]
	v_pk_mul_f32 v[68:69], v[68:69], v[124:125]
	v_pk_mul_f32 v[62:63], v[62:63], v[134:135]
	v_pk_mul_f32 v[60:61], v[60:61], v[132:133]
	v_pk_mul_f32 v[58:59], v[58:59], v[118:119]
	v_pk_mul_f32 v[56:57], v[56:57], v[116:117]
	v_pk_mul_f32 v[54:55], v[54:55], v[126:127]
	v_pk_mul_f32 v[52:53], v[52:53], v[124:125]
	v_pk_mul_f32 v[46:47], v[46:47], v[134:135]
	v_pk_mul_f32 v[44:45], v[44:45], v[132:133]
	v_pk_mul_f32 v[42:43], v[42:43], v[118:119]
	v_pk_mul_f32 v[40:41], v[40:41], v[116:117]
	global_store_dwordx4 v[32:33], v[24:27], off sc1
	global_store_dwordx4 v[16:17], v[8:11], off sc1
	v_pk_mul_f32 v[6:7], v[6:7], v[126:127]
	v_pk_mul_f32 v[26:27], v[30:31], v[118:119]
	v_pk_mul_f32 v[24:25], v[28:29], v[116:117]
	v_pk_mul_f32 v[10:11], v[14:15], v[118:119]
	v_pk_mul_f32 v[8:9], v[12:13], v[116:117]
	v_pk_mul_f32 v[4:5], v[4:5], v[124:125]
	v_pk_mul_f32 v[2:3], v[2:3], v[114:115]
	v_pk_mul_f32 v[0:1], v[0:1], v[112:113]
	global_store_dwordx4 v[172:173], v[140:143], off sc1
	global_store_dwordx4 v[172:173], v[136:139], off offset:16 sc1
	global_store_dwordx4 v[172:173], v[128:131], off offset:512 sc1
	global_store_dwordx4 v[120:121], v[108:111], off sc1
	global_store_dwordx4 v[120:121], v[104:107], off offset:16 sc1
	global_store_dwordx4 v[120:121], v[100:103], off offset:512 sc1
	global_store_dwordx4 v[96:97], v[92:95], off sc1
	global_store_dwordx4 v[96:97], v[88:91], off offset:16 sc1
	global_store_dwordx4 v[96:97], v[84:87], off offset:512 sc1
	global_store_dwordx4 v[80:81], v[76:79], off sc1
	global_store_dwordx4 v[80:81], v[72:75], off offset:16 sc1
	global_store_dwordx4 v[80:81], v[68:71], off offset:512 sc1
	global_store_dwordx4 v[64:65], v[60:63], off sc1
	global_store_dwordx4 v[64:65], v[56:59], off offset:16 sc1
	global_store_dwordx4 v[64:65], v[52:55], off offset:512 sc1
	global_store_dwordx4 v[48:49], v[44:47], off sc1
	global_store_dwordx4 v[48:49], v[40:43], off offset:16 sc1
	global_store_dwordx4 v[32:33], v[24:27], off offset:16 sc1
	global_store_dwordx4 v[16:17], v[8:11], off offset:16 sc1
	global_store_dwordx4 v[16:17], v[4:7], off offset:512 sc1
	global_store_dwordx4 v[16:17], v[0:3], off offset:528 sc1
	s_cbranch_vccnz .LBB0_1132
	s_andn2_b64 vcc, exec, s[6:7]
	s_cbranch_vccnz .LBB0_1131
	s_barrier
	s_branch .LBB0_1131

.LBB0_1204:
	s_add_i32 s10, s88, s50
	s_cmpk_lt_i32 s10, 0x4000
	s_cselect_b64 s[78:79], -1, 0
	s_and_b64 s[0:1], s[78:79], exec
	v_readlane_b32 s0, v255, 21
	s_cselect_b32 s30, s10, s50
	s_add_i32 s10, s0, s50
	s_cmpk_lt_i32 s10, 0x4000
	v_readlane_b32 s1, v255, 22
	s_cselect_b64 s[16:17], -1, 0
	s_and_b64 s[0:1], s[16:17], exec
	v_readlane_b32 s0, v255, 29
	s_cselect_b32 s14, s10, s50
	s_add_i32 s12, s0, s50
	s_cmpk_lt_i32 s12, 0x4000
	s_cselect_b64 s[0:1], -1, 0
	s_and_b64 s[10:11], s[0:1], exec
	v_lshl_add_u64 v[0:1], s[22:23], 0, v[30:31]
	s_mov_b32 s11, 0x3ce00000
	v_add_co_u32_e32 v2, vcc, s11, v0
	s_cselect_b32 s10, s12, s50
	s_nop 0
	v_addc_co_u32_e32 v3, vcc, 0, v1, vcc
	global_load_dwordx2 v[16:17], v[2:3], off
	global_load_dwordx2 v[14:15], v[2:3], off offset:512
	global_load_dwordx2 v[12:13], v[2:3], off offset:1024
	global_load_dwordx2 v[10:11], v[2:3], off offset:1536
	global_load_dwordx2 v[8:9], v[2:3], off offset:2048
	global_load_dwordx2 v[6:7], v[2:3], off offset:2560
	global_load_dwordx2 v[4:5], v[2:3], off offset:3072
	s_nop 0
	global_load_dwordx2 v[2:3], v[2:3], off offset:3584
	s_ashr_i32 s31, s30, 31
	s_lshl_b64 s[58:59], s[30:31], 12
	s_ashr_i32 s15, s14, 31
	v_lshl_add_u64 v[18:19], v[26:27], 0, s[58:59]
	s_lshl_b64 s[18:19], s[14:15], 12
	s_ashr_i32 s11, s10, 31
	global_load_dwordx2 v[78:79], v[18:19], off
	global_load_dwordx2 v[76:77], v[18:19], off offset:512
	global_load_dwordx2 v[74:75], v[18:19], off offset:1024
	global_load_dwordx2 v[72:73], v[18:19], off offset:1536
	global_load_dwordx2 v[70:71], v[18:19], off offset:2048
	global_load_dwordx2 v[68:69], v[18:19], off offset:2560
	global_load_dwordx2 v[66:67], v[18:19], off offset:3072
	global_load_dwordx2 v[64:65], v[18:19], off offset:3584
	v_lshl_add_u64 v[18:19], v[26:27], 0, s[18:19]
	s_lshl_b64 s[12:13], s[10:11], 12
	global_load_dwordx2 v[62:63], v[18:19], off
	global_load_dwordx2 v[60:61], v[18:19], off offset:512
	global_load_dwordx2 v[58:59], v[18:19], off offset:1024
	global_load_dwordx2 v[56:57], v[18:19], off offset:1536
	global_load_dwordx2 v[54:55], v[18:19], off offset:2048
	global_load_dwordx2 v[52:53], v[18:19], off offset:2560
	global_load_dwordx2 v[50:51], v[18:19], off offset:3072
	global_load_dwordx2 v[48:49], v[18:19], off offset:3584
	v_lshl_add_u64 v[18:19], v[26:27], 0, s[12:13]
	global_load_dwordx2 v[46:47], v[18:19], off
	global_load_dwordx2 v[44:45], v[18:19], off offset:512
	global_load_dwordx2 v[42:43], v[18:19], off offset:1024
	global_load_dwordx2 v[40:41], v[18:19], off offset:1536
	global_load_dwordx2 v[38:39], v[18:19], off offset:2048
	global_load_dwordx2 v[36:37], v[18:19], off offset:2560
	global_load_dwordx2 v[34:35], v[18:19], off offset:3072
	global_load_dwordx2 v[32:33], v[18:19], off offset:3584
	s_mov_b32 s20, 0xf800000
	s_waitcnt vmcnt(31)
	v_lshlrev_b32_e32 v18, 16, v16
	v_and_b32_e32 v19, 0xffff0000, v16
	v_lshlrev_b32_e32 v16, 16, v17
	v_and_b32_e32 v17, 0xffff0000, v17
	s_waitcnt vmcnt(30)
	v_and_b32_e32 v103, 0xffff0000, v14
	v_and_b32_e32 v101, 0xffff0000, v15
	v_lshlrev_b32_e32 v102, 16, v14
	s_waitcnt vmcnt(24)
	v_lshlrev_b32_e32 v82, 16, v2
	v_and_b32_e32 v83, 0xffff0000, v2
	v_lshlrev_b32_e32 v80, 16, v3
	v_and_b32_e32 v81, 0xffff0000, v3
	v_mul_f32_e32 v2, v19, v19
	v_mul_f32_e32 v3, v17, v17
	v_fmac_f32_e32 v2, v18, v18
	v_fmac_f32_e32 v3, v16, v16
	v_lshlrev_b32_e32 v100, 16, v15
	v_lshlrev_b32_e32 v84, 16, v4
	v_and_b32_e32 v85, 0xffff0000, v4
	v_add_f32_e32 v2, v2, v3
	v_mul_f32_e32 v3, v103, v103
	v_mul_f32_e32 v4, v101, v101
	v_fmac_f32_e32 v3, v102, v102
	v_fmac_f32_e32 v4, v100, v100
	v_and_b32_e32 v113, 0xffff0000, v12
	v_and_b32_e32 v109, 0xffff0000, v13
	v_add_f32_e32 v3, v3, v4
	v_lshlrev_b32_e32 v112, 16, v12
	v_lshlrev_b32_e32 v108, 16, v13
	v_add_f32_e32 v2, v2, v3
	v_mul_f32_e32 v3, v113, v113
	v_mul_f32_e32 v4, v109, v109
	v_fmac_f32_e32 v3, v112, v112
	v_fmac_f32_e32 v4, v108, v108
	v_and_b32_e32 v21, 0xffff0000, v10
	v_and_b32_e32 v23, 0xffff0000, v11
	v_add_f32_e32 v3, v3, v4
	v_lshlrev_b32_e32 v20, 16, v10
	v_lshlrev_b32_e32 v22, 16, v11
	v_add_f32_e32 v2, v2, v3
	v_mul_f32_e32 v3, v21, v21
	v_mul_f32_e32 v4, v23, v23
	v_fmac_f32_e32 v3, v20, v20
	v_fmac_f32_e32 v4, v22, v22
	v_and_b32_e32 v99, 0xffff0000, v8
	v_and_b32_e32 v97, 0xffff0000, v9
	v_add_f32_e32 v3, v3, v4
	v_lshlrev_b32_e32 v98, 16, v8
	v_lshlrev_b32_e32 v96, 16, v9
	v_add_f32_e32 v2, v2, v3
	v_mul_f32_e32 v3, v99, v99
	v_mul_f32_e32 v4, v97, v97
	v_fmac_f32_e32 v3, v98, v98
	v_fmac_f32_e32 v4, v96, v96
	v_and_b32_e32 v95, 0xffff0000, v6
	v_and_b32_e32 v93, 0xffff0000, v7
	v_add_f32_e32 v3, v3, v4
	v_lshlrev_b32_e32 v94, 16, v6
	v_lshlrev_b32_e32 v92, 16, v7
	v_add_f32_e32 v2, v2, v3
	v_mul_f32_e32 v3, v95, v95
	v_mul_f32_e32 v4, v93, v93
	v_fmac_f32_e32 v3, v94, v94
	v_fmac_f32_e32 v4, v92, v92
	v_and_b32_e32 v87, 0xffff0000, v5
	v_add_f32_e32 v3, v3, v4
	v_lshlrev_b32_e32 v86, 16, v5
	v_add_f32_e32 v2, v2, v3
	v_mul_f32_e32 v3, v85, v85
	v_mul_f32_e32 v4, v87, v87
	v_fmac_f32_e32 v3, v84, v84
	v_fmac_f32_e32 v4, v86, v86
	v_add_f32_e32 v3, v3, v4
	v_add_f32_e32 v2, v2, v3
	v_mul_f32_e32 v3, v83, v83
	v_mul_f32_e32 v4, v81, v81
	v_fmac_f32_e32 v3, v82, v82
	v_fmac_f32_e32 v4, v80, v80
	v_add_f32_e32 v3, v3, v4
	v_add_f32_e32 v2, v2, v3
	s_nop 1
	v_add_f32_dpp v2, v2, v2 quad_perm:[1,0,3,2] row_mask:0xf bank_mask:0xf bound_ctrl:1
	s_nop 1
	v_add_f32_dpp v2, v2, v2 quad_perm:[2,3,0,1] row_mask:0xf bank_mask:0xf bound_ctrl:1
	s_nop 1
	v_add_f32_dpp v2, v2, v2 row_half_mirror row_mask:0xf bank_mask:0xf bound_ctrl:1
	s_nop 1
	v_add_f32_dpp v2, v2, v2 row_mirror row_mask:0xf bank_mask:0xf bound_ctrl:1
	ds_swizzle_b32 v3, v2 offset:swizzle(SWAP,16)
	s_waitcnt lgkmcnt(0)
	v_add_f32_e32 v2, v2, v3
	v_mov_b32_e32 v3, v2
	s_nop 1
	v_permlane32_swap_b32_e32 v2, v3
	v_add_f32_e32 v2, v2, v3
	v_fmamk_f32 v2, v2, 0x3a000000, v212
	v_cmp_gt_f32_e32 vcc, s20, v2
	v_mul_f32_e32 v3, 0x4f800000, v2
	s_nop 0
	v_cndmask_b32_e32 v2, v2, v3, vcc
	v_sqrt_f32_e32 v3, v2
	s_nop 0
	v_add_u32_e32 v4, -1, v3
	v_fma_f32 v5, -v4, v3, v2
	v_cmp_ge_f32_e64 s[40:41], 0, v5
	v_add_u32_e32 v5, 1, v3
	s_nop 0
	v_cndmask_b32_e64 v4, v3, v4, s[40:41]
	v_fma_f32 v3, -v5, v3, v2
	v_cmp_lt_f32_e64 s[40:41], 0, v3
	s_nop 1
	v_cndmask_b32_e64 v3, v4, v5, s[40:41]
	v_mul_f32_e32 v4, 0x37800000, v3
	v_cndmask_b32_e32 v3, v3, v4, vcc
	v_cmp_class_f32_e32 vcc, v2, v213
	s_nop 1
	v_cndmask_b32_e32 v2, v3, v2, vcc
	v_div_scale_f32 v3, s[20:21], v2, v2, 1.0
	v_rcp_f32_e32 v4, v3
	s_mov_b32 s20, 0x1b800000
	v_fma_f32 v5, -v3, v4, 1.0
	v_fmac_f32_e32 v4, v5, v4
	v_div_scale_f32 v5, vcc, 1.0, v2, 1.0
	v_mul_f32_e32 v6, v5, v4
	v_fma_f32 v7, -v3, v6, v5
	v_fmac_f32_e32 v6, v7, v4
	v_fma_f32 v3, -v3, v6, v5
	v_div_fmas_f32 v3, v3, v4, v6
	v_div_fixup_f32 v88, v3, v2, 1.0
	ds_read_b128 v[2:5], v139
	ds_read_b128 v[6:9], v139 offset:16384
	v_pk_mul_f32 v[12:13], v[18:19], v[88:89] op_sel_hi:[1,0]
	v_pk_mul_f32 v[10:11], v[16:17], v[88:89] op_sel_hi:[1,0]
	v_add_co_u32_e32 v90, vcc, s20, v0
	s_waitcnt lgkmcnt(0)
	v_pk_fma_f32 v[120:121], v[2:3], v[12:13], v[6:7]
	v_pk_fma_f32 v[114:115], v[4:5], v[10:11], v[8:9]
	v_and_b32_sdwa v3, v120, v214 dst_sel:DWORD dst_unused:UNUSED_PAD src0_sel:WORD_1 src1_sel:DWORD
	v_add3_u32 v4, v120, v3, s33
	v_and_b32_sdwa v3, v115, v214 dst_sel:DWORD dst_unused:UNUSED_PAD src0_sel:WORD_1 src1_sel:DWORD
	v_and_b32_sdwa v5, v121, v214 dst_sel:DWORD dst_unused:UNUSED_PAD src0_sel:WORD_1 src1_sel:DWORD
	v_and_b32_sdwa v2, v114, v214 dst_sel:DWORD dst_unused:UNUSED_PAD src0_sel:WORD_1 src1_sel:DWORD
	v_add3_u32 v3, v115, v3, s33
	v_add3_u32 v5, v121, v5, s33
	v_add3_u32 v2, v114, v2, s33
	v_and_b32_e32 v3, 0xffff0000, v3
	v_and_b32_e32 v5, 0xffff0000, v5
	v_or_b32_sdwa v3, v3, v2 dst_sel:DWORD dst_unused:UNUSED_PAD src0_sel:DWORD src1_sel:WORD_1
	v_or_b32_sdwa v2, v5, v4 dst_sel:DWORD dst_unused:UNUSED_PAD src0_sel:DWORD src1_sel:WORD_1
	v_addc_co_u32_e32 v91, vcc, 0, v1, vcc
	global_store_dwordx2 v[90:91], v[2:3], off sc1
	ds_read_b128 v[104:107], v139 offset:32768
	ds_read_b128 v[116:119], v139 offset:40960
	ds_read_b128 v[126:129], v139 offset:49152
	ds_read_b128 v[16:19], v139 offset:57344
	ds_read_b128 v[12:15], v140 offset:32768
	ds_read_b128 v[8:11], v140 offset:40960
	ds_read_b128 v[4:7], v140 offset:49152
	ds_read_b128 v[0:3], v140 offset:57344
	ds_read_b128 v[130:133], v139 offset:1024
	ds_read_b128 v[134:137], v139 offset:17408
	v_pk_mul_f32 v[102:103], v[102:103], v[88:89] op_sel_hi:[1,0]
	v_pk_mul_f32 v[100:101], v[100:101], v[88:89] op_sel_hi:[1,0]
	s_waitcnt lgkmcnt(9)
	v_mov_b32_e32 v110, v104
	v_mov_b32_e32 v104, v105
	s_waitcnt lgkmcnt(0)
	v_pk_fma_f32 v[122:123], v[100:101], v[132:133], v[136:137]
	v_pk_fma_f32 v[124:125], v[102:103], v[130:131], v[134:135]
	v_and_b32_sdwa v101, v123, v214 dst_sel:DWORD dst_unused:UNUSED_PAD src0_sel:WORD_1 src1_sel:DWORD
	v_and_b32_sdwa v102, v125, v214 dst_sel:DWORD dst_unused:UNUSED_PAD src0_sel:WORD_1 src1_sel:DWORD
	v_and_b32_sdwa v89, v122, v214 dst_sel:DWORD dst_unused:UNUSED_PAD src0_sel:WORD_1 src1_sel:DWORD
	v_and_b32_sdwa v100, v124, v214 dst_sel:DWORD dst_unused:UNUSED_PAD src0_sel:WORD_1 src1_sel:DWORD
	v_add3_u32 v101, v123, v101, s33
	v_add3_u32 v102, v125, v102, s33
	v_add3_u32 v100, v124, v100, s33
	v_add3_u32 v89, v122, v89, s33
	v_and_b32_e32 v101, 0xffff0000, v101
	v_and_b32_e32 v102, 0xffff0000, v102
	v_or_b32_sdwa v101, v101, v89 dst_sel:DWORD dst_unused:UNUSED_PAD src0_sel:DWORD src1_sel:WORD_1
	v_or_b32_sdwa v100, v102, v100 dst_sel:DWORD dst_unused:UNUSED_PAD src0_sel:DWORD src1_sel:WORD_1
	global_store_dwordx2 v[90:91], v[100:101], off offset:512 sc1
	ds_read_b128 v[100:103], v139 offset:33792
	v_mov_b32_e32 v105, v125
	v_mov_b32_e32 v111, v124
	v_mov_b32_e32 v130, v120
	s_mov_b32 s20, 0xff61b1e6
	s_waitcnt lgkmcnt(0)
	v_mov_b32_e32 v131, v100
	v_mov_b32_e32 v100, v121
	v_pk_mul_f32 v[100:101], v[104:105], v[100:101]
	v_mov_b32_e32 v104, v106
	v_pk_fma_f32 v[100:101], v[110:111], v[130:131], v[100:101]
	v_mov_b32_e32 v111, v102
	v_mov_b32_e32 v106, v107
	v_mov_b32_e32 v107, v123
	v_mov_b32_e32 v102, v115
	v_mov_b32_e32 v105, v122
	v_mov_b32_e32 v110, v114
	v_pk_mul_f32 v[102:103], v[106:107], v[102:103]
	v_mov_b32_e32 v106, v116
	v_pk_fma_f32 v[102:103], v[104:105], v[110:111], v[102:103]
	v_mov_b32_e32 v116, v117
	v_pk_add_f32 v[100:101], v[100:101], v[102:103]
	v_mov_b32_e32 v117, v125
	v_add_f32_e32 v89, 0, v100
	v_add_f32_e32 v104, v89, v101
	ds_read_b128 v[100:103], v139 offset:41984
	v_mov_b32_e32 v107, v124
	v_mov_b32_e32 v110, v120
	s_waitcnt lgkmcnt(0)
	v_mov_b32_e32 v111, v100
	v_mov_b32_e32 v100, v121
	v_pk_mul_f32 v[100:101], v[116:117], v[100:101]
	v_mov_b32_e32 v116, v119
	v_pk_fma_f32 v[100:101], v[106:107], v[110:111], v[100:101]
	v_mov_b32_e32 v111, v102
	v_mov_b32_e32 v117, v123
	v_mov_b32_e32 v102, v115
	v_mov_b32_e32 v106, v118
	v_mov_b32_e32 v107, v122
	v_mov_b32_e32 v110, v114
	v_pk_mul_f32 v[102:103], v[116:117], v[102:103]
	v_mov_b32_e32 v118, v127
	v_pk_fma_f32 v[102:103], v[106:107], v[110:111], v[102:103]
	v_mov_b32_e32 v119, v125
	v_pk_add_f32 v[100:101], v[100:101], v[102:103]
	v_mov_b32_e32 v110, v126
	v_add_f32_e32 v89, 0, v100
	v_add_f32_e32 v106, v89, v101
	ds_read_b128 v[100:103], v139 offset:50176
	v_mov_b32_e32 v111, v124
	v_mov_b32_e32 v116, v120
	s_waitcnt lgkmcnt(0)
	v_mov_b32_e32 v117, v100
	v_mov_b32_e32 v100, v121
	v_pk_mul_f32 v[100:101], v[118:119], v[100:101]
	v_mov_b32_e32 v118, v129
	v_pk_fma_f32 v[100:101], v[110:111], v[116:117], v[100:101]
	v_mov_b32_e32 v117, v102
	v_mov_b32_e32 v119, v123
	v_mov_b32_e32 v102, v115
	v_mov_b32_e32 v110, v128
	v_mov_b32_e32 v111, v122
	v_mov_b32_e32 v116, v114
	v_pk_mul_f32 v[102:103], v[118:119], v[102:103]
	s_nop 0
	v_pk_fma_f32 v[102:103], v[110:111], v[116:117], v[102:103]
	ds_read_b128 v[116:119], v139 offset:58368
	v_pk_add_f32 v[100:101], v[100:101], v[102:103]
	v_mov_b32_e32 v110, v120
	v_add_f32_e32 v89, 0, v100
	v_mov_b32_e32 v100, v16
	s_waitcnt lgkmcnt(0)
	v_mov_b32_e32 v111, v116
	v_mov_b32_e32 v16, v17
	v_mov_b32_e32 v17, v125
	v_mov_b32_e32 v116, v121
	v_add_f32_e32 v102, v89, v101
	v_mov_b32_e32 v101, v124
	v_pk_mul_f32 v[16:17], v[16:17], v[116:117]
	v_pk_mul_f32 v[98:99], v[98:99], v[88:89] op_sel_hi:[1,0]
	v_pk_fma_f32 v[16:17], v[100:101], v[110:111], v[16:17]
	v_mov_b32_e32 v100, v18
	v_mov_b32_e32 v111, v118
	v_mov_b32_e32 v18, v19
	v_mov_b32_e32 v19, v123
	v_mov_b32_e32 v118, v115
	v_mov_b32_e32 v101, v122
	v_mov_b32_e32 v110, v114
	v_pk_mul_f32 v[18:19], v[18:19], v[118:119]
	v_pk_mul_f32 v[96:97], v[96:97], v[88:89] op_sel_hi:[1,0]
	v_pk_fma_f32 v[18:19], v[100:101], v[110:111], v[18:19]
	v_mov_b32_e32 v100, v12
	v_pk_add_f32 v[16:17], v[16:17], v[18:19]
	v_mov_b32_e32 v12, v13
	v_add_f32_e32 v16, 0, v16
	v_add_f32_e32 v118, v16, v17
	ds_read_b128 v[16:19], v141 offset:32768
	v_mov_b32_e32 v13, v125
	v_mov_b32_e32 v101, v124
	v_mov_b32_e32 v110, v120
	s_waitcnt lgkmcnt(0)
	v_mov_b32_e32 v111, v16
	v_mov_b32_e32 v16, v121
	v_pk_mul_f32 v[12:13], v[12:13], v[16:17]
	v_mov_b32_e32 v16, v14
	v_pk_fma_f32 v[12:13], v[100:101], v[110:111], v[12:13]
	v_mov_b32_e32 v101, v18
	v_mov_b32_e32 v14, v15
	v_mov_b32_e32 v15, v123
	v_mov_b32_e32 v18, v115
	v_mov_b32_e32 v17, v122
	v_mov_b32_e32 v100, v114
	v_pk_mul_f32 v[14:15], v[14:15], v[18:19]
	v_mov_b32_e32 v18, v120
	v_pk_fma_f32 v[14:15], v[16:17], v[100:101], v[14:15]
	v_mov_b32_e32 v16, v8
	v_pk_add_f32 v[12:13], v[12:13], v[14:15]
	v_mov_b32_e32 v8, v9
	v_add_f32_e32 v12, 0, v12
	v_add_f32_e32 v100, v12, v13
	ds_read_b128 v[12:15], v141 offset:40960
	v_mov_b32_e32 v9, v125
	v_mov_b32_e32 v17, v124
	s_waitcnt lgkmcnt(0)
	v_mov_b32_e32 v19, v12
	v_mov_b32_e32 v12, v121
	v_pk_mul_f32 v[8:9], v[8:9], v[12:13]
	v_mov_b32_e32 v12, v10
	v_pk_fma_f32 v[8:9], v[16:17], v[18:19], v[8:9]
	v_mov_b32_e32 v17, v14
	v_mov_b32_e32 v10, v11
	v_mov_b32_e32 v11, v123
	v_mov_b32_e32 v14, v115
	v_mov_b32_e32 v13, v122
	v_mov_b32_e32 v16, v114
	v_pk_mul_f32 v[10:11], v[10:11], v[14:15]
	v_mov_b32_e32 v14, v120
	v_pk_fma_f32 v[10:11], v[12:13], v[16:17], v[10:11]
	v_mov_b32_e32 v12, v4
	v_pk_add_f32 v[8:9], v[8:9], v[10:11]
	v_mov_b32_e32 v4, v5
	v_add_f32_e32 v8, 0, v8
	v_add_f32_e32 v116, v8, v9
	ds_read_b128 v[8:11], v141 offset:49152
	v_mov_b32_e32 v5, v125
	v_mov_b32_e32 v13, v124
	s_waitcnt lgkmcnt(0)
	v_mov_b32_e32 v15, v8
	v_mov_b32_e32 v8, v121
	v_pk_mul_f32 v[4:5], v[4:5], v[8:9]
	v_mov_b32_e32 v8, v6
	v_pk_fma_f32 v[4:5], v[12:13], v[14:15], v[4:5]
	v_mov_b32_e32 v13, v10
	v_mov_b32_e32 v6, v7
	v_mov_b32_e32 v7, v123
	v_mov_b32_e32 v10, v115
	v_mov_b32_e32 v9, v122
	v_mov_b32_e32 v12, v114
	v_pk_mul_f32 v[6:7], v[6:7], v[10:11]
	v_mov_b32_e32 v10, v120
	v_pk_fma_f32 v[6:7], v[8:9], v[12:13], v[6:7]
	v_mov_b32_e32 v9, v124
	v_pk_add_f32 v[4:5], v[4:5], v[6:7]
	v_mov_b32_e32 v124, v1
	v_add_f32_e32 v4, 0, v4
	v_add_f32_e32 v110, v4, v5
	ds_read_b128 v[4:7], v141 offset:57344
	v_mov_b32_e32 v8, v0
	s_waitcnt lgkmcnt(0)
	v_mov_b32_e32 v11, v4
	v_mov_b32_e32 v4, v121
	v_pk_mul_f32 v[0:1], v[124:125], v[4:5]
	v_mov_b32_e32 v5, v122
	v_pk_fma_f32 v[0:1], v[8:9], v[10:11], v[0:1]
	v_mov_b32_e32 v9, v6
	v_mov_b32_e32 v122, v3
	v_mov_b32_e32 v6, v115
	v_mov_b32_e32 v4, v2
	v_mov_b32_e32 v8, v114
	v_pk_mul_f32 v[2:3], v[122:123], v[6:7]
	v_pk_mul_f32 v[10:11], v[112:113], v[88:89] op_sel_hi:[1,0]
	v_pk_fma_f32 v[2:3], v[4:5], v[8:9], v[2:3]
	s_nop 0
	v_pk_add_f32 v[0:1], v[0:1], v[2:3]
	ds_read_b128 v[2:5], v139 offset:2048
	ds_read_b128 v[6:9], v139 offset:18432
	v_add_f32_e32 v0, 0, v0
	v_add_f32_e32 v114, v0, v1
	v_pk_mul_f32 v[0:1], v[108:109], v[88:89] op_sel_hi:[1,0]
	s_waitcnt lgkmcnt(0)
	v_pk_fma_f32 v[2:3], v[10:11], v[2:3], v[6:7]
	v_pk_fma_f32 v[0:1], v[0:1], v[4:5], v[8:9]
	v_and_b32_sdwa v5, v2, v214 dst_sel:DWORD dst_unused:UNUSED_PAD src0_sel:WORD_1 src1_sel:DWORD
	v_add3_u32 v6, v2, v5, s33
	v_and_b32_sdwa v5, v1, v214 dst_sel:DWORD dst_unused:UNUSED_PAD src0_sel:WORD_1 src1_sel:DWORD
	v_and_b32_sdwa v7, v3, v214 dst_sel:DWORD dst_unused:UNUSED_PAD src0_sel:WORD_1 src1_sel:DWORD
	v_and_b32_sdwa v4, v0, v214 dst_sel:DWORD dst_unused:UNUSED_PAD src0_sel:WORD_1 src1_sel:DWORD
	v_add3_u32 v5, v1, v5, s33
	v_add3_u32 v7, v3, v7, s33
	v_add3_u32 v4, v0, v4, s33
	v_and_b32_e32 v5, 0xffff0000, v5
	v_and_b32_e32 v7, 0xffff0000, v7
	v_or_b32_sdwa v5, v5, v4 dst_sel:DWORD dst_unused:UNUSED_PAD src0_sel:DWORD src1_sel:WORD_1
	v_or_b32_sdwa v4, v7, v6 dst_sel:DWORD dst_unused:UNUSED_PAD src0_sel:DWORD src1_sel:WORD_1
	global_store_dwordx2 v[90:91], v[4:5], off offset:1024 sc1
	ds_read_b128 v[4:7], v139 offset:34816
	v_pk_mul_f32 v[10:11], v[20:21], v[88:89] op_sel_hi:[1,0]
	s_waitcnt lgkmcnt(0)
	v_pk_mul_f32 v[4:5], v[2:3], v[4:5]
	v_pk_mul_f32 v[6:7], v[0:1], v[6:7]
	s_nop 0
	v_pk_mov_b32 v[8:9], v[4:5], v[6:7] op_sel:[1,0]
	v_mov_b32_e32 v5, v7
	v_pk_add_f32 v[112:113], v[8:9], v[4:5]
	ds_read_b128 v[4:7], v139 offset:43008
	s_waitcnt lgkmcnt(0)
	v_pk_mul_f32 v[4:5], v[2:3], v[4:5]
	v_pk_mul_f32 v[6:7], v[0:1], v[6:7]
	s_nop 0
	v_pk_mov_b32 v[8:9], v[4:5], v[6:7] op_sel:[1,0]
	v_mov_b32_e32 v5, v7
	v_pk_add_f32 v[108:109], v[8:9], v[4:5]
	ds_read_b128 v[4:7], v139 offset:51200
	s_waitcnt lgkmcnt(0)
	v_pk_mul_f32 v[4:5], v[2:3], v[4:5]
	v_pk_mul_f32 v[6:7], v[0:1], v[6:7]
	s_nop 0
	v_pk_mov_b32 v[8:9], v[4:5], v[6:7] op_sel:[1,0]
	v_mov_b32_e32 v5, v7
	v_pk_add_f32 v[136:137], v[8:9], v[4:5]
	ds_read_b128 v[4:7], v139 offset:59392
	s_waitcnt lgkmcnt(0)
	v_pk_mul_f32 v[4:5], v[2:3], v[4:5]
	v_pk_mul_f32 v[6:7], v[0:1], v[6:7]
	s_nop 0
	v_pk_mov_b32 v[8:9], v[4:5], v[6:7] op_sel:[1,0]
	v_mov_b32_e32 v5, v7
	v_pk_add_f32 v[134:135], v[8:9], v[4:5]
	ds_read_b128 v[4:7], v142 offset:32768
	s_waitcnt lgkmcnt(0)
	v_pk_mul_f32 v[4:5], v[2:3], v[4:5]
	v_pk_mul_f32 v[6:7], v[0:1], v[6:7]
	s_nop 0
	v_pk_mov_b32 v[8:9], v[4:5], v[6:7] op_sel:[1,0]
	v_mov_b32_e32 v5, v7
	v_pk_add_f32 v[132:133], v[8:9], v[4:5]
	ds_read_b128 v[4:7], v142 offset:40960
	s_waitcnt lgkmcnt(0)
	v_pk_mul_f32 v[4:5], v[2:3], v[4:5]
	v_pk_mul_f32 v[6:7], v[0:1], v[6:7]
	s_nop 0
	v_pk_mov_b32 v[8:9], v[4:5], v[6:7] op_sel:[1,0]
	v_mov_b32_e32 v5, v7
	v_pk_add_f32 v[128:129], v[8:9], v[4:5]
	ds_read_b128 v[4:7], v142 offset:49152
	s_waitcnt lgkmcnt(0)
	v_pk_mul_f32 v[4:5], v[2:3], v[4:5]
	v_pk_mul_f32 v[6:7], v[0:1], v[6:7]
	s_nop 0
	v_pk_mov_b32 v[8:9], v[4:5], v[6:7] op_sel:[1,0]
	v_mov_b32_e32 v5, v7
	v_pk_add_f32 v[126:127], v[8:9], v[4:5]
	ds_read_b128 v[4:7], v142 offset:57344
	v_pk_mul_f32 v[8:9], v[22:23], v[88:89] op_sel_hi:[1,0]
	s_waitcnt lgkmcnt(0)
	v_pk_mul_f32 v[2:3], v[2:3], v[4:5]
	v_pk_mul_f32 v[0:1], v[0:1], v[6:7]
	s_nop 0
	v_pk_mov_b32 v[4:5], v[2:3], v[0:1] op_sel:[1,0]
	v_mov_b32_e32 v3, v1
	v_pk_add_f32 v[120:121], v[4:5], v[2:3]
	ds_read_b128 v[0:3], v139 offset:3072
	ds_read_b128 v[4:7], v139 offset:19456
	s_waitcnt lgkmcnt(0)
	v_pk_fma_f32 v[122:123], v[10:11], v[0:1], v[4:5]
	v_pk_fma_f32 v[124:125], v[8:9], v[2:3], v[6:7]
	v_and_b32_sdwa v1, v122, v214 dst_sel:DWORD dst_unused:UNUSED_PAD src0_sel:WORD_1 src1_sel:DWORD
	v_add3_u32 v2, v122, v1, s33
	v_and_b32_sdwa v1, v125, v214 dst_sel:DWORD dst_unused:UNUSED_PAD src0_sel:WORD_1 src1_sel:DWORD
	v_and_b32_sdwa v3, v123, v214 dst_sel:DWORD dst_unused:UNUSED_PAD src0_sel:WORD_1 src1_sel:DWORD
	v_and_b32_sdwa v0, v124, v214 dst_sel:DWORD dst_unused:UNUSED_PAD src0_sel:WORD_1 src1_sel:DWORD
	v_add3_u32 v1, v125, v1, s33
	v_add3_u32 v3, v123, v3, s33
	v_add3_u32 v0, v124, v0, s33
	v_and_b32_e32 v1, 0xffff0000, v1
	v_and_b32_e32 v3, 0xffff0000, v3
	v_or_b32_sdwa v1, v1, v0 dst_sel:DWORD dst_unused:UNUSED_PAD src0_sel:DWORD src1_sel:WORD_1
	v_or_b32_sdwa v0, v3, v2 dst_sel:DWORD dst_unused:UNUSED_PAD src0_sel:DWORD src1_sel:WORD_1
	global_store_dwordx2 v[90:91], v[0:1], off offset:1536 sc1
	ds_read_b128 v[148:151], v139 offset:35840
	ds_read_b128 v[152:155], v139 offset:44032
	ds_read_b128 v[20:23], v139 offset:52224
	ds_read_b128 v[16:19], v139 offset:60416
	ds_read_b128 v[12:15], v143 offset:32768
	ds_read_b128 v[8:11], v143 offset:40960
	ds_read_b128 v[4:7], v143 offset:49152
	ds_read_b128 v[0:3], v143 offset:57344
	ds_read_b128 v[156:159], v139 offset:4096
	ds_read_b128 v[160:163], v139 offset:20480
	s_waitcnt lgkmcnt(0)
	v_pk_fma_f32 v[96:97], v[96:97], v[158:159], v[162:163]
	v_pk_fma_f32 v[130:131], v[98:99], v[156:157], v[160:161]
	ds_read_b128 v[156:159], v139 offset:36864
	v_and_b32_sdwa v99, v97, v214 dst_sel:DWORD dst_unused:UNUSED_PAD src0_sel:WORD_1 src1_sel:DWORD
	v_and_b32_sdwa v101, v131, v214 dst_sel:DWORD dst_unused:UNUSED_PAD src0_sel:WORD_1 src1_sel:DWORD
	v_and_b32_sdwa v89, v96, v214 dst_sel:DWORD dst_unused:UNUSED_PAD src0_sel:WORD_1 src1_sel:DWORD
	v_and_b32_sdwa v98, v130, v214 dst_sel:DWORD dst_unused:UNUSED_PAD src0_sel:WORD_1 src1_sel:DWORD
	v_add3_u32 v99, v97, v99, s33
	v_add3_u32 v101, v131, v101, s33
	v_add3_u32 v98, v130, v98, s33
	v_add3_u32 v89, v96, v89, s33
	v_and_b32_e32 v99, 0xffff0000, v99
	v_and_b32_e32 v101, 0xffff0000, v101
	v_or_b32_sdwa v99, v99, v89 dst_sel:DWORD dst_unused:UNUSED_PAD src0_sel:DWORD src1_sel:WORD_1
	v_or_b32_sdwa v98, v101, v98 dst_sel:DWORD dst_unused:UNUSED_PAD src0_sel:DWORD src1_sel:WORD_1
	global_store_dwordx2 v[90:91], v[98:99], off offset:2048 sc1
	s_waitcnt lgkmcnt(0)
	v_mul_f32_e32 v89, v131, v157
	v_pk_add_f32 v[98:99], v[112:113], v[112:113] op_sel:[0,1] op_sel_hi:[1,0]
	v_mul_f32_e32 v105, v130, v156
	v_mov_b32_e32 v99, v89
	v_pk_add_f32 v[98:99], v[104:105], v[98:99]
	v_mul_f32_e32 v104, v123, v149
	v_mul_f32_e32 v112, v125, v151
	v_pk_fma_f32 v[104:105], v[122:123], v[148:149], v[104:105] op_sel_hi:[1,1,0]
	v_pk_fma_f32 v[112:113], v[124:125], v[150:151], v[112:113] op_sel_hi:[1,1,0]
	ds_read_b128 v[148:151], v139 offset:45056
	v_mul_f32_e32 v101, v96, v158
	v_mul_f32_e32 v103, v97, v159
	v_mov_b32_e32 v105, v101
	v_mov_b32_e32 v113, v103
	v_pk_add_f32 v[104:105], v[104:105], v[112:113]
	s_waitcnt lgkmcnt(0)
	v_mul_f32_e32 v89, v131, v149
	v_pk_add_f32 v[112:113], v[98:99], v[104:105]
	v_pk_add_f32 v[98:99], v[108:109], v[108:109] op_sel:[0,1] op_sel_hi:[1,0]
	v_mul_f32_e32 v107, v130, v148
	v_mov_b32_e32 v99, v89
	v_pk_add_f32 v[98:99], v[106:107], v[98:99]
	v_mul_f32_e32 v104, v123, v153
	v_mul_f32_e32 v106, v125, v155
	v_mul_f32_e32 v101, v96, v150
	v_mul_f32_e32 v103, v97, v151
	v_pk_fma_f32 v[104:105], v[122:123], v[152:153], v[104:105] op_sel_hi:[1,1,0]
	v_pk_fma_f32 v[106:107], v[124:125], v[154:155], v[106:107] op_sel_hi:[1,1,0]
	v_mov_b32_e32 v105, v101
	v_mov_b32_e32 v107, v103
	v_pk_add_f32 v[104:105], v[104:105], v[106:107]
	s_nop 0
	v_pk_add_f32 v[108:109], v[98:99], v[104:105]
	ds_read_b128 v[104:107], v139 offset:53248
	v_pk_add_f32 v[98:99], v[136:137], v[136:137] op_sel:[0,1] op_sel_hi:[1,0]
	s_waitcnt lgkmcnt(0)
	v_mul_f32_e32 v89, v131, v105
	v_mul_f32_e32 v103, v130, v104
	v_mov_b32_e32 v99, v89
	v_pk_add_f32 v[98:99], v[102:103], v[98:99]
	v_mul_f32_e32 v102, v123, v21
	v_pk_fma_f32 v[20:21], v[122:123], v[20:21], v[102:103] op_sel_hi:[1,1,0]
	v_mul_f32_e32 v102, v125, v23
	v_mul_f32_e32 v101, v96, v106
	v_mul_f32_e32 v104, v97, v107
	v_pk_fma_f32 v[22:23], v[124:125], v[22:23], v[102:103] op_sel_hi:[1,1,0]
	v_mov_b32_e32 v21, v101
	v_mov_b32_e32 v23, v104
	v_pk_add_f32 v[20:21], v[20:21], v[22:23]
	s_nop 0
	v_pk_add_f32 v[106:107], v[98:99], v[20:21]
	ds_read_b128 v[20:23], v139 offset:61440
	s_waitcnt lgkmcnt(0)
	v_mul_f32_e32 v98, v96, v22
	v_mul_f32_e32 v23, v97, v23
	v_mul_f32_e32 v22, v123, v17
	v_pk_fma_f32 v[16:17], v[122:123], v[16:17], v[22:23] op_sel_hi:[1,1,0]
	v_mul_f32_e32 v22, v125, v19
	v_mul_f32_e32 v119, v130, v20
	v_mul_f32_e32 v89, v131, v21
	v_pk_add_f32 v[20:21], v[134:135], v[134:135] op_sel:[0,1] op_sel_hi:[1,0]
	v_pk_fma_f32 v[18:19], v[124:125], v[18:19], v[22:23] op_sel_hi:[1,1,0]
	v_mov_b32_e32 v21, v89
	v_mov_b32_e32 v17, v98
	v_mov_b32_e32 v19, v23
	v_pk_add_f32 v[20:21], v[118:119], v[20:21]
	v_pk_add_f32 v[16:17], v[16:17], v[18:19]
	v_pk_mul_f32 v[82:83], v[82:83], v[88:89] op_sel_hi:[1,0]
	v_pk_add_f32 v[104:105], v[20:21], v[16:17]
	ds_read_b128 v[16:19], v144 offset:32768
	v_pk_mul_f32 v[80:81], v[80:81], v[88:89] op_sel_hi:[1,0]
	s_waitcnt lgkmcnt(0)
	v_mul_f32_e32 v21, v96, v18
	v_mul_f32_e32 v19, v97, v19
	v_mul_f32_e32 v18, v123, v13
	v_pk_fma_f32 v[12:13], v[122:123], v[12:13], v[18:19] op_sel_hi:[1,1,0]
	v_mul_f32_e32 v18, v125, v15
	v_mul_f32_e32 v101, v130, v16
	v_mul_f32_e32 v20, v131, v17
	v_pk_add_f32 v[16:17], v[132:133], v[132:133] op_sel:[0,1] op_sel_hi:[1,0]
	v_pk_fma_f32 v[14:15], v[124:125], v[14:15], v[18:19] op_sel_hi:[1,1,0]
	v_mov_b32_e32 v17, v20
	v_mov_b32_e32 v13, v21
	v_mov_b32_e32 v15, v19
	v_pk_add_f32 v[16:17], v[100:101], v[16:17]
	v_pk_add_f32 v[12:13], v[12:13], v[14:15]
	s_nop 0
	v_pk_add_f32 v[102:103], v[16:17], v[12:13]
	ds_read_b128 v[12:15], v144 offset:40960
	s_waitcnt lgkmcnt(0)
	v_mul_f32_e32 v17, v96, v14
	v_mul_f32_e32 v15, v97, v15
	v_mul_f32_e32 v14, v123, v9
	v_pk_fma_f32 v[8:9], v[122:123], v[8:9], v[14:15] op_sel_hi:[1,1,0]
	v_mul_f32_e32 v14, v125, v11
	v_mul_f32_e32 v117, v130, v12
	v_mul_f32_e32 v16, v131, v13
	v_pk_add_f32 v[12:13], v[128:129], v[128:129] op_sel:[0,1] op_sel_hi:[1,0]
	v_pk_fma_f32 v[10:11], v[124:125], v[10:11], v[14:15] op_sel_hi:[1,1,0]
	v_mov_b32_e32 v13, v16
	v_mov_b32_e32 v9, v17
	v_mov_b32_e32 v11, v15
	v_pk_add_f32 v[12:13], v[116:117], v[12:13]
	v_pk_add_f32 v[8:9], v[8:9], v[10:11]
	s_nop 0
	v_pk_add_f32 v[100:101], v[12:13], v[8:9]
	ds_read_b128 v[8:11], v144 offset:49152
	s_waitcnt lgkmcnt(0)
	v_mul_f32_e32 v13, v96, v10
	v_mul_f32_e32 v11, v97, v11
	v_mul_f32_e32 v10, v123, v5
	v_pk_fma_f32 v[4:5], v[122:123], v[4:5], v[10:11] op_sel_hi:[1,1,0]
	v_mul_f32_e32 v10, v125, v7
	v_mul_f32_e32 v111, v130, v8
	v_mul_f32_e32 v12, v131, v9
	v_pk_add_f32 v[8:9], v[126:127], v[126:127] op_sel:[0,1] op_sel_hi:[1,0]
	v_pk_fma_f32 v[6:7], v[124:125], v[6:7], v[10:11] op_sel_hi:[1,1,0]
	v_mov_b32_e32 v9, v12
	v_mov_b32_e32 v5, v13
	v_mov_b32_e32 v7, v11
	v_pk_add_f32 v[8:9], v[110:111], v[8:9]
	v_pk_add_f32 v[4:5], v[4:5], v[6:7]
	v_pk_mul_f32 v[10:11], v[94:95], v[88:89] op_sel_hi:[1,0]
	v_pk_add_f32 v[98:99], v[8:9], v[4:5]
	ds_read_b128 v[4:7], v144 offset:57344
	s_waitcnt lgkmcnt(0)
	v_mul_f32_e32 v9, v96, v6
	v_mul_f32_e32 v7, v97, v7
	v_mul_f32_e32 v6, v123, v1
	v_pk_fma_f32 v[0:1], v[122:123], v[0:1], v[6:7] op_sel_hi:[1,1,0]
	v_mul_f32_e32 v6, v125, v3
	v_mul_f32_e32 v115, v130, v4
	v_mul_f32_e32 v8, v131, v5
	v_pk_add_f32 v[4:5], v[120:121], v[120:121] op_sel:[0,1] op_sel_hi:[1,0]
	v_pk_fma_f32 v[2:3], v[124:125], v[2:3], v[6:7] op_sel_hi:[1,1,0]
	v_mov_b32_e32 v5, v8
	v_mov_b32_e32 v1, v9
	v_mov_b32_e32 v3, v7
	v_pk_add_f32 v[4:5], v[114:115], v[4:5]
	v_pk_add_f32 v[0:1], v[0:1], v[2:3]
	s_nop 0
	v_pk_add_f32 v[96:97], v[4:5], v[0:1]
	ds_read_b128 v[2:5], v139 offset:5120
	ds_read_b128 v[6:9], v139 offset:21504
	v_pk_mul_f32 v[0:1], v[92:93], v[88:89] op_sel_hi:[1,0]
	s_waitcnt lgkmcnt(0)
	v_pk_fma_f32 v[2:3], v[10:11], v[2:3], v[6:7]
	v_pk_fma_f32 v[0:1], v[0:1], v[4:5], v[8:9]
	v_and_b32_sdwa v5, v2, v214 dst_sel:DWORD dst_unused:UNUSED_PAD src0_sel:WORD_1 src1_sel:DWORD
	v_add3_u32 v6, v2, v5, s33
	v_and_b32_sdwa v5, v1, v214 dst_sel:DWORD dst_unused:UNUSED_PAD src0_sel:WORD_1 src1_sel:DWORD
	v_and_b32_sdwa v7, v3, v214 dst_sel:DWORD dst_unused:UNUSED_PAD src0_sel:WORD_1 src1_sel:DWORD
	v_and_b32_sdwa v4, v0, v214 dst_sel:DWORD dst_unused:UNUSED_PAD src0_sel:WORD_1 src1_sel:DWORD
	v_add3_u32 v5, v1, v5, s33
	v_add3_u32 v7, v3, v7, s33
	v_add3_u32 v4, v0, v4, s33
	v_and_b32_e32 v5, 0xffff0000, v5
	v_and_b32_e32 v7, 0xffff0000, v7
	v_or_b32_sdwa v5, v5, v4 dst_sel:DWORD dst_unused:UNUSED_PAD src0_sel:DWORD src1_sel:WORD_1
	v_or_b32_sdwa v4, v7, v6 dst_sel:DWORD dst_unused:UNUSED_PAD src0_sel:DWORD src1_sel:WORD_1
	global_store_dwordx2 v[90:91], v[4:5], off offset:2560 sc1
	ds_read_b128 v[4:7], v139 offset:37888
	v_pk_mul_f32 v[10:11], v[84:85], v[88:89] op_sel_hi:[1,0]
	s_waitcnt lgkmcnt(0)
	v_pk_mul_f32 v[4:5], v[2:3], v[4:5]
	v_pk_mul_f32 v[6:7], v[0:1], v[6:7]
	s_nop 0
	v_pk_mov_b32 v[8:9], v[4:5], v[6:7] op_sel:[1,0]
	v_mov_b32_e32 v5, v7
	v_pk_add_f32 v[122:123], v[8:9], v[4:5]
	ds_read_b128 v[4:7], v139 offset:46080
	s_waitcnt lgkmcnt(0)
	v_pk_mul_f32 v[4:5], v[2:3], v[4:5]
	v_pk_mul_f32 v[6:7], v[0:1], v[6:7]
	s_nop 0
	v_pk_mov_b32 v[8:9], v[4:5], v[6:7] op_sel:[1,0]
	v_mov_b32_e32 v5, v7
	v_pk_add_f32 v[120:121], v[8:9], v[4:5]
	ds_read_b128 v[4:7], v139 offset:54272
	s_waitcnt lgkmcnt(0)
	v_pk_mul_f32 v[4:5], v[2:3], v[4:5]
	v_pk_mul_f32 v[6:7], v[0:1], v[6:7]
	s_nop 0
	v_pk_mov_b32 v[8:9], v[4:5], v[6:7] op_sel:[1,0]
	v_mov_b32_e32 v5, v7
	v_pk_add_f32 v[118:119], v[8:9], v[4:5]
	ds_read_b128 v[4:7], v139 offset:62464
	s_waitcnt lgkmcnt(0)
	v_pk_mul_f32 v[4:5], v[2:3], v[4:5]
	v_pk_mul_f32 v[6:7], v[0:1], v[6:7]
	s_nop 0
	v_pk_mov_b32 v[8:9], v[4:5], v[6:7] op_sel:[1,0]
	v_mov_b32_e32 v5, v7
	v_pk_add_f32 v[116:117], v[8:9], v[4:5]
	ds_read_b128 v[4:7], v145 offset:32768
	s_waitcnt lgkmcnt(0)
	v_pk_mul_f32 v[4:5], v[2:3], v[4:5]
	v_pk_mul_f32 v[6:7], v[0:1], v[6:7]
	s_nop 0
	v_pk_mov_b32 v[8:9], v[4:5], v[6:7] op_sel:[1,0]
	v_mov_b32_e32 v5, v7
	v_pk_add_f32 v[114:115], v[8:9], v[4:5]
	ds_read_b128 v[4:7], v145 offset:40960
	s_waitcnt lgkmcnt(0)
	v_pk_mul_f32 v[4:5], v[2:3], v[4:5]
	v_pk_mul_f32 v[6:7], v[0:1], v[6:7]
	s_nop 0
	v_pk_mov_b32 v[8:9], v[4:5], v[6:7] op_sel:[1,0]
	v_mov_b32_e32 v5, v7
	v_pk_add_f32 v[110:111], v[8:9], v[4:5]
	ds_read_b128 v[4:7], v145 offset:49152
	s_waitcnt lgkmcnt(0)
	v_pk_mul_f32 v[4:5], v[2:3], v[4:5]
	v_pk_mul_f32 v[6:7], v[0:1], v[6:7]
	s_nop 0
	v_pk_mov_b32 v[8:9], v[4:5], v[6:7] op_sel:[1,0]
	v_mov_b32_e32 v5, v7
	v_pk_add_f32 v[94:95], v[8:9], v[4:5]
	ds_read_b128 v[4:7], v145 offset:57344
	v_pk_mul_f32 v[8:9], v[86:87], v[88:89] op_sel_hi:[1,0]
	s_waitcnt lgkmcnt(0)
	v_pk_mul_f32 v[2:3], v[2:3], v[4:5]
	v_pk_mul_f32 v[0:1], v[0:1], v[6:7]
	s_nop 0
	v_pk_mov_b32 v[4:5], v[2:3], v[0:1] op_sel:[1,0]
	v_mov_b32_e32 v3, v1
	v_pk_add_f32 v[92:93], v[4:5], v[2:3]
	ds_read_b128 v[0:3], v139 offset:6144
	ds_read_b128 v[4:7], v139 offset:22528
	s_waitcnt lgkmcnt(0)
	v_pk_fma_f32 v[84:85], v[10:11], v[0:1], v[4:5]
	v_pk_fma_f32 v[86:87], v[8:9], v[2:3], v[6:7]
	v_and_b32_sdwa v1, v84, v214 dst_sel:DWORD dst_unused:UNUSED_PAD src0_sel:WORD_1 src1_sel:DWORD
	v_add3_u32 v2, v84, v1, s33
	v_and_b32_sdwa v1, v87, v214 dst_sel:DWORD dst_unused:UNUSED_PAD src0_sel:WORD_1 src1_sel:DWORD
	v_and_b32_sdwa v3, v85, v214 dst_sel:DWORD dst_unused:UNUSED_PAD src0_sel:WORD_1 src1_sel:DWORD
	v_and_b32_sdwa v0, v86, v214 dst_sel:DWORD dst_unused:UNUSED_PAD src0_sel:WORD_1 src1_sel:DWORD
	v_add3_u32 v1, v87, v1, s33
	v_add3_u32 v3, v85, v3, s33
	v_add3_u32 v0, v86, v0, s33
	v_and_b32_e32 v1, 0xffff0000, v1
	v_and_b32_e32 v3, 0xffff0000, v3
	v_or_b32_sdwa v1, v1, v0 dst_sel:DWORD dst_unused:UNUSED_PAD src0_sel:DWORD src1_sel:WORD_1
	v_or_b32_sdwa v0, v3, v2 dst_sel:DWORD dst_unused:UNUSED_PAD src0_sel:DWORD src1_sel:WORD_1
	global_store_dwordx2 v[90:91], v[0:1], off offset:3072 sc1
	ds_read_b128 v[124:127], v139 offset:38912
	ds_read_b128 v[128:131], v139 offset:47104
	ds_read_b128 v[20:23], v139 offset:55296
	ds_read_b128 v[16:19], v139 offset:63488
	ds_read_b128 v[12:15], v146 offset:32768
	ds_read_b128 v[8:11], v146 offset:40960
	ds_read_b128 v[4:7], v146 offset:49152
	ds_read_b128 v[0:3], v146 offset:57344
	ds_read_b128 v[132:135], v139 offset:7168
	ds_read_b128 v[148:151], v139 offset:23552
	s_waitcnt lgkmcnt(0)
	v_pk_fma_f32 v[82:83], v[82:83], v[132:133], v[148:149]
	v_pk_fma_f32 v[80:81], v[80:81], v[134:135], v[150:151]
	v_and_b32_sdwa v89, v82, v214 dst_sel:DWORD dst_unused:UNUSED_PAD src0_sel:WORD_1 src1_sel:DWORD
	v_add3_u32 v132, v82, v89, s33
	v_and_b32_sdwa v89, v81, v214 dst_sel:DWORD dst_unused:UNUSED_PAD src0_sel:WORD_1 src1_sel:DWORD
	v_and_b32_sdwa v133, v83, v214 dst_sel:DWORD dst_unused:UNUSED_PAD src0_sel:WORD_1 src1_sel:DWORD
	v_and_b32_sdwa v88, v80, v214 dst_sel:DWORD dst_unused:UNUSED_PAD src0_sel:WORD_1 src1_sel:DWORD
	v_add3_u32 v89, v81, v89, s33
	v_add3_u32 v133, v83, v133, s33
	v_add3_u32 v88, v80, v88, s33
	v_and_b32_e32 v89, 0xffff0000, v89
	v_and_b32_e32 v133, 0xffff0000, v133
	v_or_b32_sdwa v89, v89, v88 dst_sel:DWORD dst_unused:UNUSED_PAD src0_sel:DWORD src1_sel:WORD_1
	v_or_b32_sdwa v88, v133, v132 dst_sel:DWORD dst_unused:UNUSED_PAD src0_sel:DWORD src1_sel:WORD_1
	global_store_dwordx2 v[90:91], v[88:89], off offset:3584 sc1
	ds_read_b128 v[88:91], v139 offset:39936
	s_waitcnt lgkmcnt(0)
	v_mul_f32_e32 v132, v82, v88
	v_mul_f32_e32 v133, v83, v89
	v_mul_f32_e32 v134, v80, v90
	v_mul_f32_e32 v135, v81, v91
	v_pk_add_f32 v[88:89], v[112:113], v[112:113] op_sel:[0,1] op_sel_hi:[1,0]
	v_pk_add_f32 v[90:91], v[122:123], v[122:123] op_sel:[0,1] op_sel_hi:[1,0]
	v_mov_b32_e32 v89, v132
	v_mov_b32_e32 v91, v133
	v_pk_add_f32 v[88:89], v[88:89], v[90:91]
	v_mul_f32_e32 v90, v85, v125
	v_pk_fma_f32 v[90:91], v[84:85], v[124:125], v[90:91] op_sel_hi:[1,1,0]
	v_mul_f32_e32 v112, v87, v127
	ds_read_b128 v[122:125], v139 offset:48128
	v_pk_fma_f32 v[112:113], v[86:87], v[126:127], v[112:113] op_sel_hi:[1,1,0]
	v_mov_b32_e32 v91, v134
	v_mov_b32_e32 v113, v135
	v_pk_add_f32 v[90:91], v[90:91], v[112:113]
	s_waitcnt lgkmcnt(0)
	v_mul_f32_e32 v112, v83, v123
	v_pk_add_f32 v[88:89], v[88:89], v[90:91]
	v_pk_add_f32 v[90:91], v[108:109], v[108:109] op_sel:[0,1] op_sel_hi:[1,0]
	v_add_f32_e32 v88, v88, v89
	v_mul_f32_e32 v89, v82, v122
	v_pk_add_f32 v[108:109], v[120:121], v[120:121] op_sel:[0,1] op_sel_hi:[1,0]
	v_mov_b32_e32 v91, v89
	v_mov_b32_e32 v109, v112
	v_pk_add_f32 v[90:91], v[90:91], v[108:109]
	v_mul_f32_e32 v108, v85, v129
	v_mul_f32_e32 v113, v80, v124
	v_pk_fma_f32 v[108:109], v[84:85], v[128:129], v[108:109] op_sel_hi:[1,1,0]
	v_mul_f32_e32 v112, v87, v131
	v_mul_f32_e32 v122, v81, v125
	v_mov_b32_e32 v109, v113
	v_pk_fma_f32 v[112:113], v[86:87], v[130:131], v[112:113] op_sel_hi:[1,1,0]
	s_nop 0
	v_mov_b32_e32 v113, v122
	ds_read_b128 v[120:123], v139 offset:56320
	v_pk_add_f32 v[108:109], v[108:109], v[112:113]
	s_waitcnt lgkmcnt(0)
	v_mul_f32_e32 v112, v80, v122
	v_pk_add_f32 v[90:91], v[90:91], v[108:109]
	v_mul_f32_e32 v108, v82, v120
	v_add_f32_e32 v89, v90, v91
	v_mul_f32_e32 v109, v83, v121
	v_pk_add_f32 v[90:91], v[106:107], v[106:107] op_sel:[0,1] op_sel_hi:[1,0]
	v_pk_add_f32 v[106:107], v[118:119], v[118:119] op_sel:[0,1] op_sel_hi:[1,0]
	v_mov_b32_e32 v91, v108
	v_mov_b32_e32 v107, v109
	v_pk_add_f32 v[90:91], v[90:91], v[106:107]
	v_mul_f32_e32 v106, v85, v21
	v_pk_fma_f32 v[20:21], v[84:85], v[20:21], v[106:107] op_sel_hi:[1,1,0]
	v_mul_f32_e32 v106, v87, v23
	v_pk_fma_f32 v[22:23], v[86:87], v[22:23], v[106:107] op_sel_hi:[1,1,0]
	ds_read_b128 v[106:109], v139 offset:64512
	v_mul_f32_e32 v113, v81, v123
	v_mov_b32_e32 v21, v112
	v_mov_b32_e32 v23, v113
	v_pk_add_f32 v[20:21], v[20:21], v[22:23]
	v_pk_add_f32 v[22:23], v[104:105], v[104:105] op_sel:[0,1] op_sel_hi:[1,0]
	v_pk_add_f32 v[20:21], v[90:91], v[20:21]
	v_pk_add_f32 v[90:91], v[116:117], v[116:117] op_sel:[0,1] op_sel_hi:[1,0]
	v_add_f32_e32 v20, v20, v21
	s_waitcnt lgkmcnt(0)
	v_mul_f32_e32 v21, v82, v106
	v_mul_f32_e32 v106, v83, v107
	v_mov_b32_e32 v23, v21
	v_mov_b32_e32 v91, v106
	v_pk_add_f32 v[22:23], v[22:23], v[90:91]
	v_mul_f32_e32 v90, v85, v17
	v_pk_fma_f32 v[16:17], v[84:85], v[16:17], v[90:91] op_sel_hi:[1,1,0]
	v_mul_f32_e32 v90, v87, v19
	v_mul_f32_e32 v107, v80, v108
	v_mul_f32_e32 v108, v81, v109
	v_pk_fma_f32 v[18:19], v[86:87], v[18:19], v[90:91] op_sel_hi:[1,1,0]
	v_mov_b32_e32 v17, v107
	v_mov_b32_e32 v19, v108
	v_pk_add_f32 v[16:17], v[16:17], v[18:19]
	s_nop 0
	v_pk_add_f32 v[16:17], v[22:23], v[16:17]
	s_nop 0
	v_add_f32_e32 v21, v16, v17
	ds_read_b128 v[16:19], v147 offset:32768
	s_waitcnt lgkmcnt(0)
	v_mul_f32_e32 v22, v82, v16
	v_mul_f32_e32 v23, v83, v17
	v_mul_f32_e32 v90, v80, v18
	v_mul_f32_e32 v91, v81, v19
	v_pk_add_f32 v[16:17], v[102:103], v[102:103] op_sel:[0,1] op_sel_hi:[1,0]
	v_pk_add_f32 v[18:19], v[114:115], v[114:115] op_sel:[0,1] op_sel_hi:[1,0]
	v_mov_b32_e32 v17, v22
	v_mov_b32_e32 v19, v23
	v_pk_add_f32 v[16:17], v[16:17], v[18:19]
	v_mul_f32_e32 v18, v85, v13
	v_pk_fma_f32 v[12:13], v[84:85], v[12:13], v[18:19] op_sel_hi:[1,1,0]
	v_mul_f32_e32 v18, v87, v15
	v_pk_fma_f32 v[14:15], v[86:87], v[14:15], v[18:19] op_sel_hi:[1,1,0]
	v_mov_b32_e32 v13, v90
	v_mov_b32_e32 v15, v91
	v_pk_add_f32 v[12:13], v[12:13], v[14:15]
	s_nop 0
	v_pk_add_f32 v[12:13], v[16:17], v[12:13]
	s_nop 0
	v_add_f32_e32 v16, v12, v13
	ds_read_b128 v[12:15], v147 offset:40960
	s_waitcnt lgkmcnt(0)
	v_mul_f32_e32 v17, v82, v12
	v_mul_f32_e32 v18, v83, v13
	v_mul_f32_e32 v19, v80, v14
	v_mul_f32_e32 v22, v81, v15
	v_pk_add_f32 v[12:13], v[100:101], v[100:101] op_sel:[0,1] op_sel_hi:[1,0]
	v_pk_add_f32 v[14:15], v[110:111], v[110:111] op_sel:[0,1] op_sel_hi:[1,0]
	v_mov_b32_e32 v13, v17
	v_mov_b32_e32 v15, v18
	v_pk_add_f32 v[12:13], v[12:13], v[14:15]
	v_mul_f32_e32 v14, v85, v9
	v_pk_fma_f32 v[8:9], v[84:85], v[8:9], v[14:15] op_sel_hi:[1,1,0]
	v_mul_f32_e32 v14, v87, v11
	v_pk_fma_f32 v[10:11], v[86:87], v[10:11], v[14:15] op_sel_hi:[1,1,0]
	v_mov_b32_e32 v9, v19
	v_mov_b32_e32 v11, v22
	v_pk_add_f32 v[8:9], v[8:9], v[10:11]
	s_nop 0
	v_pk_add_f32 v[8:9], v[12:13], v[8:9]
	s_nop 0
	v_add_f32_e32 v12, v8, v9
	ds_read_b128 v[8:11], v147 offset:49152
	s_waitcnt lgkmcnt(0)
	v_mul_f32_e32 v13, v82, v8
	v_mul_f32_e32 v14, v83, v9
	v_mul_f32_e32 v15, v80, v10
	v_mul_f32_e32 v17, v81, v11
	v_pk_add_f32 v[8:9], v[98:99], v[98:99] op_sel:[0,1] op_sel_hi:[1,0]
	v_pk_add_f32 v[10:11], v[94:95], v[94:95] op_sel:[0,1] op_sel_hi:[1,0]
	v_mov_b32_e32 v9, v13
	v_mov_b32_e32 v11, v14
	v_pk_add_f32 v[8:9], v[8:9], v[10:11]
	v_mul_f32_e32 v10, v85, v5
	v_pk_fma_f32 v[4:5], v[84:85], v[4:5], v[10:11] op_sel_hi:[1,1,0]
	v_mul_f32_e32 v10, v87, v7
	v_pk_fma_f32 v[6:7], v[86:87], v[6:7], v[10:11] op_sel_hi:[1,1,0]
	v_mov_b32_e32 v5, v15
	v_mov_b32_e32 v7, v17
	v_pk_add_f32 v[4:5], v[4:5], v[6:7]
	s_nop 0
	v_pk_add_f32 v[4:5], v[8:9], v[4:5]
	s_nop 0
	v_add_f32_e32 v8, v4, v5
	ds_read_b128 v[4:7], v147 offset:57344
	s_waitcnt lgkmcnt(0)
	v_mul_f32_e32 v9, v82, v4
	v_mul_f32_e32 v10, v83, v5
	v_mul_f32_e32 v11, v80, v6
	v_mul_f32_e32 v13, v81, v7
	v_pk_add_f32 v[4:5], v[96:97], v[96:97] op_sel:[0,1] op_sel_hi:[1,0]
	v_pk_add_f32 v[6:7], v[92:93], v[92:93] op_sel:[0,1] op_sel_hi:[1,0]
	v_mov_b32_e32 v5, v9
	v_mov_b32_e32 v7, v10
	v_pk_add_f32 v[4:5], v[4:5], v[6:7]
	v_mul_f32_e32 v6, v85, v1
	v_pk_fma_f32 v[0:1], v[84:85], v[0:1], v[6:7] op_sel_hi:[1,1,0]
	v_mul_f32_e32 v6, v87, v3
	v_pk_fma_f32 v[2:3], v[86:87], v[2:3], v[6:7] op_sel_hi:[1,1,0]
	v_mov_b32_e32 v1, v11
	v_mov_b32_e32 v3, v13
	v_pk_add_f32 v[0:1], v[0:1], v[2:3]
	s_nop 0
	v_pk_add_f32 v[0:1], v[4:5], v[0:1]
	s_nop 0
	v_add_f32_e32 v6, v0, v1
	v_add_f32_dpp v0, v88, v88 quad_perm:[1,0,3,2] row_mask:0xf bank_mask:0xf bound_ctrl:1
	s_nop 1
	v_add_f32_dpp v0, v0, v0 quad_perm:[2,3,0,1] row_mask:0xf bank_mask:0xf bound_ctrl:1
	s_nop 1
	v_add_f32_dpp v0, v0, v0 row_half_mirror row_mask:0xf bank_mask:0xf bound_ctrl:1
	s_nop 1
	v_add_f32_dpp v0, v0, v0 row_mirror row_mask:0xf bank_mask:0xf bound_ctrl:1
	ds_swizzle_b32 v1, v0 offset:swizzle(SWAP,16)
	s_waitcnt lgkmcnt(0)
	v_add_f32_e32 v1, v0, v1
	v_add_f32_dpp v0, v89, v89 quad_perm:[1,0,3,2] row_mask:0xf bank_mask:0xf bound_ctrl:1
	v_mov_b32_e32 v3, v1
	s_nop 1
	v_permlane32_swap_b32_e32 v1, v3
	v_add_f32_dpp v0, v0, v0 quad_perm:[2,3,0,1] row_mask:0xf bank_mask:0xf bound_ctrl:1
	s_nop 1
	v_add_f32_dpp v0, v0, v0 row_half_mirror row_mask:0xf bank_mask:0xf bound_ctrl:1
	s_nop 1
	v_add_f32_dpp v0, v0, v0 row_mirror row_mask:0xf bank_mask:0xf bound_ctrl:1
	ds_swizzle_b32 v2, v0 offset:swizzle(SWAP,16)
	s_waitcnt lgkmcnt(0)
	v_add_f32_e32 v0, v0, v2
	v_mov_b32_e32 v2, v0
	s_nop 1
	v_permlane32_swap_b32_e32 v0, v2
	v_pk_add_f32 v[4:5], v[0:1], v[2:3]
	s_nop 0
	v_add_f32_dpp v0, v20, v20 quad_perm:[1,0,3,2] row_mask:0xf bank_mask:0xf bound_ctrl:1
	v_cmp_gt_f32_e32 vcc, v4, v5
	v_cmp_nlt_f32_e64 s[46:47], s20, v5
	v_add_f32_dpp v0, v0, v0 quad_perm:[2,3,0,1] row_mask:0xf bank_mask:0xf bound_ctrl:1
	v_cndmask_b32_e64 v3, 0, 1, vcc
	s_nop 0
	v_add_f32_dpp v0, v0, v0 row_half_mirror row_mask:0xf bank_mask:0xf bound_ctrl:1
	s_nop 1
	v_add_f32_dpp v0, v0, v0 row_mirror row_mask:0xf bank_mask:0xf bound_ctrl:1
	ds_swizzle_b32 v1, v0 offset:swizzle(SWAP,16)
	s_waitcnt lgkmcnt(0)
	v_add_f32_e32 v0, v0, v1
	v_mov_b32_e32 v1, v0
	s_nop 1
	v_permlane32_swap_b32_e32 v0, v1
	v_add_f32_e32 v2, v0, v1
	s_nop 0
	v_add_f32_dpp v0, v21, v21 quad_perm:[1,0,3,2] row_mask:0xf bank_mask:0xf bound_ctrl:1
	s_nop 1
	v_add_f32_dpp v0, v0, v0 quad_perm:[2,3,0,1] row_mask:0xf bank_mask:0xf bound_ctrl:1
	s_nop 1
	v_add_f32_dpp v0, v0, v0 row_half_mirror row_mask:0xf bank_mask:0xf bound_ctrl:1
	s_nop 1
	v_add_f32_dpp v0, v0, v0 row_mirror row_mask:0xf bank_mask:0xf bound_ctrl:1
	ds_swizzle_b32 v1, v0 offset:swizzle(SWAP,16)
	s_waitcnt lgkmcnt(0)
	v_add_f32_e32 v0, v0, v1
	v_mov_b32_e32 v1, v0
	s_nop 1
	v_permlane32_swap_b32_e32 v0, v1
	v_add_f32_e32 v7, v0, v1
	s_nop 0
	v_add_f32_dpp v0, v16, v16 quad_perm:[1,0,3,2] row_mask:0xf bank_mask:0xf bound_ctrl:1
	s_nop 1
	v_add_f32_dpp v0, v0, v0 quad_perm:[2,3,0,1] row_mask:0xf bank_mask:0xf bound_ctrl:1
	s_nop 1
	v_add_f32_dpp v0, v0, v0 row_half_mirror row_mask:0xf bank_mask:0xf bound_ctrl:1
	s_nop 1
	v_add_f32_dpp v0, v0, v0 row_mirror row_mask:0xf bank_mask:0xf bound_ctrl:1
	ds_swizzle_b32 v1, v0 offset:swizzle(SWAP,16)
	s_waitcnt lgkmcnt(0)
	v_add_f32_e32 v0, v0, v1
	v_mov_b32_e32 v1, v0
	s_nop 1
	v_permlane32_swap_b32_e32 v0, v1
	v_add_f32_e32 v9, v0, v1
	s_nop 0
	v_add_f32_dpp v0, v12, v12 quad_perm:[1,0,3,2] row_mask:0xf bank_mask:0xf bound_ctrl:1
	s_nop 1
	v_add_f32_dpp v0, v0, v0 quad_perm:[2,3,0,1] row_mask:0xf bank_mask:0xf bound_ctrl:1
	s_nop 1
	v_add_f32_dpp v0, v0, v0 row_half_mirror row_mask:0xf bank_mask:0xf bound_ctrl:1
	s_nop 1
	v_add_f32_dpp v0, v0, v0 row_mirror row_mask:0xf bank_mask:0xf bound_ctrl:1
	ds_swizzle_b32 v1, v0 offset:swizzle(SWAP,16)
	s_waitcnt lgkmcnt(0)
	v_add_f32_e32 v0, v0, v1
	v_mov_b32_e32 v1, v0
	s_nop 1
	v_permlane32_swap_b32_e32 v0, v1
	v_add_f32_e32 v10, v0, v1
	s_nop 0
	v_add_f32_dpp v0, v8, v8 quad_perm:[1,0,3,2] row_mask:0xf bank_mask:0xf bound_ctrl:1
	s_nop 1
	v_add_f32_dpp v0, v0, v0 quad_perm:[2,3,0,1] row_mask:0xf bank_mask:0xf bound_ctrl:1
	s_nop 1
	v_add_f32_dpp v0, v0, v0 row_half_mirror row_mask:0xf bank_mask:0xf bound_ctrl:1
	s_nop 1
	v_add_f32_dpp v0, v0, v0 row_mirror row_mask:0xf bank_mask:0xf bound_ctrl:1
	ds_swizzle_b32 v1, v0 offset:swizzle(SWAP,16)
	s_waitcnt lgkmcnt(0)
	v_add_f32_e32 v0, v0, v1
	v_mov_b32_e32 v1, v0
	s_nop 1
	v_permlane32_swap_b32_e32 v0, v1
	v_add_f32_e32 v8, v0, v1
	s_nop 0
	v_add_f32_dpp v0, v6, v6 quad_perm:[1,0,3,2] row_mask:0xf bank_mask:0xf bound_ctrl:1
	s_nop 1
	v_add_f32_dpp v0, v0, v0 quad_perm:[2,3,0,1] row_mask:0xf bank_mask:0xf bound_ctrl:1
	s_nop 1
	v_add_f32_dpp v0, v0, v0 row_half_mirror row_mask:0xf bank_mask:0xf bound_ctrl:1
	s_nop 1
	v_add_f32_dpp v0, v0, v0 row_mirror row_mask:0xf bank_mask:0xf bound_ctrl:1
	ds_swizzle_b32 v1, v0 offset:swizzle(SWAP,16)
	s_waitcnt lgkmcnt(0)
	v_add_f32_e32 v0, v0, v1
	v_mov_b32_e32 v1, v0
	s_nop 1
	v_permlane32_swap_b32_e32 v0, v1
	v_add_f32_e32 v1, v0, v1
	v_cndmask_b32_e32 v0, v5, v4, vcc
	v_cmp_gt_f32_e32 vcc, v2, v0
	s_nop 1
	v_cndmask_b32_e32 v0, v0, v2, vcc
	v_cndmask_b32_e64 v3, v3, 2, vcc
	v_cmp_gt_f32_e32 vcc, v7, v0
	s_nop 1
	v_cndmask_b32_e32 v0, v0, v7, vcc
	v_cndmask_b32_e64 v3, v3, 3, vcc
	v_cmp_gt_f32_e32 vcc, v9, v0
	s_nop 1
	v_cndmask_b32_e32 v0, v0, v9, vcc
	v_cndmask_b32_e64 v3, v3, 4, vcc
	v_cmp_gt_f32_e32 vcc, v10, v0
	s_nop 1
	v_cndmask_b32_e32 v0, v0, v10, vcc
	v_cndmask_b32_e64 v6, v3, 5, vcc
	v_cmp_ngt_f32_e32 vcc, v8, v0
	s_nop 1
	v_cndmask_b32_e32 v3, v8, v0, vcc
	v_cndmask_b32_e32 v0, 6, v6, vcc
	v_cmp_gt_f32_e64 s[42:43], v1, v3
	s_or_b64 s[20:21], vcc, s[42:43]
	v_cmp_ngt_f32_e64 s[40:41], v1, v3
	v_cndmask_b32_e64 v0, v0, 7, s[42:43]
	v_cmp_eq_u32_e64 s[44:45], 0, v0
	s_or_b64 s[44:45], s[44:45], s[46:47]
	s_nop 0
	v_cndmask_b32_e64 v5, v5, v222, s[44:45]
	v_cndmask_b32_e64 v6, 0, -1, s[44:45]
	v_cmp_ne_u32_e64 s[44:45], 1, v0
	v_cmp_gt_f32_e64 s[46:47], v4, v5
	s_and_b64 s[44:45], s[44:45], s[46:47]
	v_cndmask_b32_e64 v4, v5, v4, s[44:45]
	v_cndmask_b32_e64 v5, v6, 1, s[44:45]
	v_cmp_ne_u32_e64 s[44:45], 2, v0
	v_cmp_gt_f32_e64 s[46:47], v2, v4
	s_and_b64 s[44:45], s[44:45], s[46:47]
	v_cndmask_b32_e64 v2, v4, v2, s[44:45]
	v_cndmask_b32_e64 v4, v5, 2, s[44:45]
	v_cmp_ne_u32_e64 s[44:45], 3, v0
	v_cmp_gt_f32_e64 s[46:47], v7, v2
	s_and_b64 s[44:45], s[44:45], s[46:47]
	v_cndmask_b32_e64 v2, v2, v7, s[44:45]
	v_cndmask_b32_e64 v4, v4, 3, s[44:45]
	v_cmp_ne_u32_e64 s[44:45], 4, v0
	v_cmp_gt_f32_e64 s[46:47], v9, v2
	s_and_b64 s[44:45], s[44:45], s[46:47]
	v_cndmask_b32_e64 v2, v2, v9, s[44:45]
	v_cndmask_b32_e64 v4, v4, 4, s[44:45]
	v_cmp_ne_u32_e64 s[44:45], 5, v0
	v_cmp_gt_f32_e64 s[46:47], v10, v2
	s_and_b64 s[44:45], s[44:45], s[46:47]
	v_cndmask_b32_e64 v2, v2, v10, s[44:45]
	v_cmp_gt_f32_e32 vcc, v8, v2
	v_cndmask_b32_e64 v5, v4, 5, s[44:45]
	s_and_b64 vcc, s[20:21], vcc
	v_cndmask_b32_e32 v4, v2, v8, vcc
	v_cndmask_b32_e64 v2, v5, 6, vcc
	s_and_saveexec_b64 s[42:43], s[40:41]
	s_cbranch_execz .LBB0_1208
	v_cmp_gt_f32_e32 vcc, v1, v4
	s_and_saveexec_b64 s[40:41], vcc
	v_mov_b32_e32 v2, 7
	v_mov_b32_e32 v4, v1
	s_or_b64 exec, exec, s[40:41]
	v_mov_b32_e32 v1, v3
.LBB0_1208:
	s_or_b64 exec, exec, s[42:43]
	s_and_saveexec_b64 s[40:41], s[38:39]
	s_cbranch_execz .LBB0_1213
	v_sub_f32_e32 v1, v4, v1
	v_mul_f32_e32 v1, 0x3fb8aa3b, v1
	v_exp_f32_e32 v1, v1
	s_cmp_gt_i32 s4, 31
	s_mov_b64 s[42:43], -1
	v_add_f32_e32 v1, 1.0, v1
	v_div_scale_f32 v3, s[20:21], v1, v1, 1.0
	v_rcp_f32_e32 v4, v3
	v_div_scale_f32 v5, vcc, 1.0, v1, 1.0
	v_fma_f32 v6, -v3, v4, 1.0
	v_fmac_f32_e32 v4, v6, v4
	v_mul_f32_e32 v6, v5, v4
	v_fma_f32 v7, -v3, v6, v5
	v_fmac_f32_e32 v6, v7, v4
	v_fma_f32 v3, -v3, v6, v5
	v_div_fmas_f32 v3, v3, v4, v6
	v_div_fixup_f32 v4, v3, v1, 1.0
	v_sub_f32_e32 v5, 1.0, v4
	s_cbranch_scc0 .LBB0_1211
	v_readlane_b32 s20, v252, 53
	v_lshlrev_b32_e32 v184, 6, v0
	v_readlane_b32 s21, v252, 54
	s_mov_b64 s[42:43], 0
	s_nop 0
	v_lshl_add_u64 v[6:7], v[184:185], 2, s[20:21]
	global_atomic_add v1, v[6:7], v214, off sc0
	v_lshlrev_b32_e32 v6, 6, v2
	v_ashrrev_i32_e32 v7, 31, v6
	v_lshl_add_u64 v[6:7], v[6:7], 2, s[20:21]
	global_atomic_add v3, v[6:7], v214, off sc0
	s_add_u32 s20, s22, s8
	s_addc_u32 s21, s23, s9
	s_waitcnt vmcnt(0)
	global_store_dwordx4 v185, v[0:3], s[20:21] sc1
	s_add_u32 s20, s22, s6
	s_addc_u32 s21, s23, s7
	global_store_dwordx2 v185, v[4:5], s[20:21] sc1

.LBB0_1213:
	s_or_b64 exec, exec, s[40:41]
	s_andn2_b64 vcc, exec, s[78:79]
	s_cbranch_vccnz .LBB0_1224
	s_waitcnt vmcnt(31)
	v_and_b32_e32 v9, 0xffff0000, v78
	v_and_b32_e32 v11, 0xffff0000, v79
	v_lshlrev_b32_e32 v8, 16, v78
	v_lshlrev_b32_e32 v10, 16, v79
	v_mul_f32_e32 v0, v9, v9
	v_mul_f32_e32 v1, v11, v11
	s_waitcnt vmcnt(30)
	v_and_b32_e32 v95, 0xffff0000, v76
	v_and_b32_e32 v107, 0xffff0000, v77
	v_fmac_f32_e32 v0, v8, v8
	v_fmac_f32_e32 v1, v10, v10
	v_lshlrev_b32_e32 v94, 16, v76
	v_lshlrev_b32_e32 v106, 16, v77
	v_add_f32_e32 v0, v0, v1
	v_mul_f32_e32 v1, v95, v95
	v_mul_f32_e32 v2, v107, v107
	v_fmac_f32_e32 v1, v94, v94
	v_fmac_f32_e32 v2, v106, v106
	s_waitcnt vmcnt(29)
	v_and_b32_e32 v97, 0xffff0000, v74
	v_and_b32_e32 v93, 0xffff0000, v75
	v_add_f32_e32 v1, v1, v2
	v_lshlrev_b32_e32 v96, 16, v74
	v_lshlrev_b32_e32 v92, 16, v75
	v_add_f32_e32 v0, v0, v1
	v_mul_f32_e32 v1, v97, v97
	v_mul_f32_e32 v2, v93, v93
	v_fmac_f32_e32 v1, v96, v96
	v_fmac_f32_e32 v2, v92, v92
	s_waitcnt vmcnt(28)
	v_and_b32_e32 v21, 0xffff0000, v72
	v_and_b32_e32 v23, 0xffff0000, v73
	v_add_f32_e32 v1, v1, v2
	v_lshlrev_b32_e32 v20, 16, v72
	v_lshlrev_b32_e32 v22, 16, v73
	v_add_f32_e32 v0, v0, v1
	v_mul_f32_e32 v1, v21, v21
	v_mul_f32_e32 v2, v23, v23
	v_fmac_f32_e32 v1, v20, v20
	v_fmac_f32_e32 v2, v22, v22
	s_waitcnt vmcnt(27)
	v_and_b32_e32 v83, 0xffff0000, v70
	v_and_b32_e32 v81, 0xffff0000, v71
	v_add_f32_e32 v1, v1, v2
	v_lshlrev_b32_e32 v82, 16, v70
	v_lshlrev_b32_e32 v80, 16, v71
	v_add_f32_e32 v0, v0, v1
	v_mul_f32_e32 v1, v83, v83
	v_mul_f32_e32 v2, v81, v81
	v_fmac_f32_e32 v1, v82, v82
	v_fmac_f32_e32 v2, v80, v80
	s_waitcnt vmcnt(26)
	v_and_b32_e32 v79, 0xffff0000, v68
	v_and_b32_e32 v77, 0xffff0000, v69
	v_add_f32_e32 v1, v1, v2
	v_lshlrev_b32_e32 v78, 16, v68
	v_lshlrev_b32_e32 v76, 16, v69
	v_add_f32_e32 v0, v0, v1
	v_mul_f32_e32 v1, v79, v79
	v_mul_f32_e32 v2, v77, v77
	v_fmac_f32_e32 v1, v78, v78
	v_fmac_f32_e32 v2, v76, v76
	s_waitcnt vmcnt(25)
	v_and_b32_e32 v69, 0xffff0000, v66
	v_and_b32_e32 v71, 0xffff0000, v67
	v_add_f32_e32 v1, v1, v2
	v_lshlrev_b32_e32 v68, 16, v66
	v_lshlrev_b32_e32 v70, 16, v67
	v_add_f32_e32 v0, v0, v1
	v_mul_f32_e32 v1, v69, v69
	v_mul_f32_e32 v2, v71, v71
	v_fmac_f32_e32 v1, v68, v68
	v_fmac_f32_e32 v2, v70, v70
	s_waitcnt vmcnt(24)
	v_lshlrev_b32_e32 v66, 16, v64
	v_and_b32_e32 v67, 0xffff0000, v64
	v_lshlrev_b32_e32 v64, 16, v65
	v_and_b32_e32 v65, 0xffff0000, v65
	v_add_f32_e32 v1, v1, v2
	v_add_f32_e32 v0, v0, v1
	v_mul_f32_e32 v1, v67, v67
	v_mul_f32_e32 v2, v65, v65
	v_fmac_f32_e32 v1, v66, v66
	v_fmac_f32_e32 v2, v64, v64
	v_add_f32_e32 v1, v1, v2
	v_add_f32_e32 v0, v0, v1
	s_mov_b32 s20, 0xf800000
	v_lshl_add_u64 v[74:75], v[28:29], 0, s[58:59]
	v_add_f32_dpp v0, v0, v0 quad_perm:[1,0,3,2] row_mask:0xf bank_mask:0xf bound_ctrl:1
	s_nop 1
	v_add_f32_dpp v0, v0, v0 quad_perm:[2,3,0,1] row_mask:0xf bank_mask:0xf bound_ctrl:1
	s_nop 1
	v_add_f32_dpp v0, v0, v0 row_half_mirror row_mask:0xf bank_mask:0xf bound_ctrl:1
	s_nop 1
	v_add_f32_dpp v0, v0, v0 row_mirror row_mask:0xf bank_mask:0xf bound_ctrl:1
	ds_swizzle_b32 v1, v0 offset:swizzle(SWAP,16)
	s_waitcnt lgkmcnt(0)
	v_add_f32_e32 v0, v0, v1
	v_mov_b32_e32 v1, v0
	s_nop 1
	v_permlane32_swap_b32_e32 v0, v1
	v_add_f32_e32 v0, v0, v1
	v_fmamk_f32 v0, v0, 0x3a000000, v212
	v_cmp_gt_f32_e32 vcc, s20, v0
	v_mul_f32_e32 v1, 0x4f800000, v0
	s_nop 0
	v_cndmask_b32_e32 v0, v0, v1, vcc
	v_sqrt_f32_e32 v1, v0
	s_nop 0
	v_add_u32_e32 v2, -1, v1
	v_fma_f32 v3, -v2, v1, v0
	v_cmp_ge_f32_e64 s[40:41], 0, v3
	v_add_u32_e32 v3, 1, v1
	s_nop 0
	v_cndmask_b32_e64 v2, v1, v2, s[40:41]
	v_fma_f32 v1, -v3, v1, v0
	v_cmp_lt_f32_e64 s[40:41], 0, v1
	s_nop 1
	v_cndmask_b32_e64 v1, v2, v3, s[40:41]
	v_mul_f32_e32 v2, 0x37800000, v1
	v_cndmask_b32_e32 v1, v1, v2, vcc
	v_cmp_class_f32_e32 vcc, v0, v213
	s_nop 1
	v_cndmask_b32_e32 v0, v1, v0, vcc
	v_div_scale_f32 v1, s[20:21], v0, v0, 1.0
	v_rcp_f32_e32 v2, v1
	s_mov_b32 s20, 0xff61b1e6
	v_fma_f32 v3, -v1, v2, 1.0
	v_fmac_f32_e32 v2, v3, v2
	v_div_scale_f32 v3, vcc, 1.0, v0, 1.0
	v_mul_f32_e32 v4, v3, v2
	v_fma_f32 v5, -v1, v4, v3
	v_fmac_f32_e32 v4, v5, v2
	v_fma_f32 v1, -v1, v4, v3
	v_div_fmas_f32 v1, v1, v2, v4
	v_div_fixup_f32 v72, v1, v0, 1.0
	ds_read_b128 v[0:3], v139
	ds_read_b128 v[4:7], v139 offset:16384
	v_pk_mul_f32 v[8:9], v[8:9], v[72:73] op_sel_hi:[1,0]
	v_pk_mul_f32 v[10:11], v[10:11], v[72:73] op_sel_hi:[1,0]
	v_pk_mul_f32 v[94:95], v[94:95], v[72:73] op_sel_hi:[1,0]
	v_pk_mul_f32 v[106:107], v[106:107], v[72:73] op_sel_hi:[1,0]
	s_waitcnt lgkmcnt(0)
	v_pk_fma_f32 v[104:105], v[0:1], v[8:9], v[4:5]
	v_pk_fma_f32 v[98:99], v[2:3], v[10:11], v[6:7]
	v_and_b32_sdwa v1, v104, v214 dst_sel:DWORD dst_unused:UNUSED_PAD src0_sel:WORD_1 src1_sel:DWORD
	v_add3_u32 v2, v104, v1, s33
	v_and_b32_sdwa v1, v99, v214 dst_sel:DWORD dst_unused:UNUSED_PAD src0_sel:WORD_1 src1_sel:DWORD
	v_and_b32_sdwa v3, v105, v214 dst_sel:DWORD dst_unused:UNUSED_PAD src0_sel:WORD_1 src1_sel:DWORD
	v_and_b32_sdwa v0, v98, v214 dst_sel:DWORD dst_unused:UNUSED_PAD src0_sel:WORD_1 src1_sel:DWORD
	v_add3_u32 v1, v99, v1, s33
	v_add3_u32 v3, v105, v3, s33
	v_add3_u32 v0, v98, v0, s33
	v_and_b32_e32 v1, 0xffff0000, v1
	v_and_b32_e32 v3, 0xffff0000, v3
	v_or_b32_sdwa v1, v1, v0 dst_sel:DWORD dst_unused:UNUSED_PAD src0_sel:DWORD src1_sel:WORD_1
	v_or_b32_sdwa v0, v3, v2 dst_sel:DWORD dst_unused:UNUSED_PAD src0_sel:DWORD src1_sel:WORD_1
	global_store_dwordx2 v[74:75], v[0:1], off sc1
	ds_read_b128 v[84:87], v139 offset:32768
	ds_read_b128 v[100:103], v139 offset:40960
	ds_read_b128 v[110:113], v139 offset:49152
	ds_read_b128 v[16:19], v139 offset:57344
	ds_read_b128 v[12:15], v140 offset:32768
	ds_read_b128 v[8:11], v140 offset:40960
	ds_read_b128 v[4:7], v140 offset:49152
	ds_read_b128 v[0:3], v140 offset:57344
	ds_read_b128 v[88:91], v139 offset:1024
	ds_read_b128 v[114:117], v139 offset:17408
	s_waitcnt lgkmcnt(0)
	v_pk_fma_f32 v[106:107], v[106:107], v[90:91], v[116:117]
	v_pk_fma_f32 v[108:109], v[94:95], v[88:89], v[114:115]
	v_and_b32_sdwa v89, v107, v214 dst_sel:DWORD dst_unused:UNUSED_PAD src0_sel:WORD_1 src1_sel:DWORD
	v_and_b32_sdwa v90, v109, v214 dst_sel:DWORD dst_unused:UNUSED_PAD src0_sel:WORD_1 src1_sel:DWORD
	v_and_b32_sdwa v73, v106, v214 dst_sel:DWORD dst_unused:UNUSED_PAD src0_sel:WORD_1 src1_sel:DWORD
	v_and_b32_sdwa v88, v108, v214 dst_sel:DWORD dst_unused:UNUSED_PAD src0_sel:WORD_1 src1_sel:DWORD
	v_add3_u32 v89, v107, v89, s33
	v_add3_u32 v90, v109, v90, s33
	v_add3_u32 v88, v108, v88, s33
	v_add3_u32 v73, v106, v73, s33
	v_and_b32_e32 v89, 0xffff0000, v89
	v_and_b32_e32 v90, 0xffff0000, v90
	v_or_b32_sdwa v89, v89, v73 dst_sel:DWORD dst_unused:UNUSED_PAD src0_sel:DWORD src1_sel:WORD_1
	v_or_b32_sdwa v88, v90, v88 dst_sel:DWORD dst_unused:UNUSED_PAD src0_sel:DWORD src1_sel:WORD_1
	global_store_dwordx2 v[74:75], v[88:89], off offset:512 sc1
	ds_read_b128 v[88:91], v139 offset:33792
	v_mov_b32_e32 v94, v84
	v_mov_b32_e32 v84, v85
	v_mov_b32_e32 v85, v109
	v_mov_b32_e32 v95, v108
	s_waitcnt lgkmcnt(0)
	v_mov_b32_e32 v115, v88
	v_mov_b32_e32 v88, v105
	v_mov_b32_e32 v114, v104
	v_pk_mul_f32 v[84:85], v[84:85], v[88:89]
	v_mov_b32_e32 v88, v86
	v_pk_fma_f32 v[84:85], v[94:95], v[114:115], v[84:85]
	v_mov_b32_e32 v95, v90
	v_mov_b32_e32 v86, v87
	v_mov_b32_e32 v87, v107
	v_mov_b32_e32 v90, v99
	v_mov_b32_e32 v89, v106
	v_mov_b32_e32 v94, v98
	v_pk_mul_f32 v[86:87], v[86:87], v[90:91]
	v_mov_b32_e32 v90, v100
	v_pk_fma_f32 v[86:87], v[88:89], v[94:95], v[86:87]
	v_mov_b32_e32 v100, v101
	v_pk_add_f32 v[84:85], v[84:85], v[86:87]
	v_mov_b32_e32 v101, v109
	v_add_f32_e32 v73, 0, v84
	v_add_f32_e32 v88, v73, v85
	ds_read_b128 v[84:87], v139 offset:41984
	v_mov_b32_e32 v91, v108
	v_mov_b32_e32 v94, v104
	s_waitcnt lgkmcnt(0)
	v_mov_b32_e32 v95, v84
	v_mov_b32_e32 v84, v105
	v_pk_mul_f32 v[84:85], v[100:101], v[84:85]
	v_mov_b32_e32 v100, v103
	v_pk_fma_f32 v[84:85], v[90:91], v[94:95], v[84:85]
	v_mov_b32_e32 v95, v86
	v_mov_b32_e32 v101, v107
	v_mov_b32_e32 v86, v99
	v_mov_b32_e32 v90, v102
	v_mov_b32_e32 v91, v106
	v_mov_b32_e32 v94, v98
	v_pk_mul_f32 v[86:87], v[100:101], v[86:87]
	v_mov_b32_e32 v102, v111
	v_pk_fma_f32 v[86:87], v[90:91], v[94:95], v[86:87]
	v_mov_b32_e32 v103, v109
	v_pk_add_f32 v[84:85], v[84:85], v[86:87]
	v_mov_b32_e32 v94, v110
	v_add_f32_e32 v73, 0, v84
	v_add_f32_e32 v90, v73, v85
	ds_read_b128 v[84:87], v139 offset:50176
	v_mov_b32_e32 v95, v108
	v_mov_b32_e32 v100, v104
	s_waitcnt lgkmcnt(0)
	v_mov_b32_e32 v101, v84
	v_mov_b32_e32 v84, v105
	v_pk_mul_f32 v[84:85], v[102:103], v[84:85]
	v_mov_b32_e32 v102, v113
	v_pk_fma_f32 v[84:85], v[94:95], v[100:101], v[84:85]
	v_mov_b32_e32 v101, v86
	v_mov_b32_e32 v103, v107
	v_mov_b32_e32 v86, v99
	v_mov_b32_e32 v94, v112
	v_mov_b32_e32 v95, v106
	v_mov_b32_e32 v100, v98
	v_pk_mul_f32 v[86:87], v[102:103], v[86:87]
	s_nop 0
	v_pk_fma_f32 v[86:87], v[94:95], v[100:101], v[86:87]
	ds_read_b128 v[100:103], v139 offset:58368
	v_pk_add_f32 v[84:85], v[84:85], v[86:87]
	v_mov_b32_e32 v94, v104
	v_add_f32_e32 v73, 0, v84
	v_mov_b32_e32 v84, v16
	s_waitcnt lgkmcnt(0)
	v_mov_b32_e32 v95, v100
	v_mov_b32_e32 v16, v17
	v_mov_b32_e32 v17, v109
	v_mov_b32_e32 v100, v105
	v_add_f32_e32 v86, v73, v85
	v_mov_b32_e32 v85, v108
	v_pk_mul_f32 v[16:17], v[16:17], v[100:101]
	v_pk_mul_f32 v[82:83], v[82:83], v[72:73] op_sel_hi:[1,0]
	v_pk_fma_f32 v[16:17], v[84:85], v[94:95], v[16:17]
	v_mov_b32_e32 v84, v18
	v_mov_b32_e32 v95, v102
	v_mov_b32_e32 v18, v19
	v_mov_b32_e32 v19, v107
	v_mov_b32_e32 v102, v99
	v_mov_b32_e32 v85, v106
	v_mov_b32_e32 v94, v98
	v_pk_mul_f32 v[18:19], v[18:19], v[102:103]
	v_pk_mul_f32 v[80:81], v[80:81], v[72:73] op_sel_hi:[1,0]
	v_pk_fma_f32 v[18:19], v[84:85], v[94:95], v[18:19]
	v_mov_b32_e32 v84, v12
	v_pk_add_f32 v[16:17], v[16:17], v[18:19]
	v_mov_b32_e32 v12, v13
	v_add_f32_e32 v16, 0, v16
	v_add_f32_e32 v102, v16, v17
	ds_read_b128 v[16:19], v141 offset:32768
	v_mov_b32_e32 v13, v109
	v_mov_b32_e32 v85, v108
	v_mov_b32_e32 v94, v104
	s_waitcnt lgkmcnt(0)
	v_mov_b32_e32 v95, v16
	v_mov_b32_e32 v16, v105
	v_pk_mul_f32 v[12:13], v[12:13], v[16:17]
	v_mov_b32_e32 v16, v14
	v_pk_fma_f32 v[12:13], v[84:85], v[94:95], v[12:13]
	v_mov_b32_e32 v85, v18
	v_mov_b32_e32 v14, v15
	v_mov_b32_e32 v15, v107
	v_mov_b32_e32 v18, v99
	v_mov_b32_e32 v17, v106
	v_mov_b32_e32 v84, v98
	v_pk_mul_f32 v[14:15], v[14:15], v[18:19]
	v_mov_b32_e32 v18, v104
	v_pk_fma_f32 v[14:15], v[16:17], v[84:85], v[14:15]
	v_mov_b32_e32 v16, v8
	v_pk_add_f32 v[12:13], v[12:13], v[14:15]
	v_mov_b32_e32 v8, v9
	v_add_f32_e32 v12, 0, v12
	v_add_f32_e32 v84, v12, v13
	ds_read_b128 v[12:15], v141 offset:40960
	v_mov_b32_e32 v9, v109
	v_mov_b32_e32 v17, v108
	s_waitcnt lgkmcnt(0)
	v_mov_b32_e32 v19, v12
	v_mov_b32_e32 v12, v105
	v_pk_mul_f32 v[8:9], v[8:9], v[12:13]
	v_mov_b32_e32 v12, v10
	v_pk_fma_f32 v[8:9], v[16:17], v[18:19], v[8:9]
	v_mov_b32_e32 v17, v14
	v_mov_b32_e32 v10, v11
	v_mov_b32_e32 v11, v107
	v_mov_b32_e32 v14, v99
	v_mov_b32_e32 v13, v106
	v_mov_b32_e32 v16, v98
	v_pk_mul_f32 v[10:11], v[10:11], v[14:15]
	v_mov_b32_e32 v14, v104
	v_pk_fma_f32 v[10:11], v[12:13], v[16:17], v[10:11]
	v_mov_b32_e32 v12, v4
	v_pk_add_f32 v[8:9], v[8:9], v[10:11]
	v_mov_b32_e32 v4, v5
	v_add_f32_e32 v8, 0, v8
	v_add_f32_e32 v100, v8, v9
	ds_read_b128 v[8:11], v141 offset:49152
	v_mov_b32_e32 v5, v109
	v_mov_b32_e32 v13, v108
	s_waitcnt lgkmcnt(0)
	v_mov_b32_e32 v15, v8
	v_mov_b32_e32 v8, v105
	v_pk_mul_f32 v[4:5], v[4:5], v[8:9]
	v_mov_b32_e32 v8, v6
	v_pk_fma_f32 v[4:5], v[12:13], v[14:15], v[4:5]
	v_mov_b32_e32 v13, v10
	v_mov_b32_e32 v6, v7
	v_mov_b32_e32 v7, v107
	v_mov_b32_e32 v10, v99
	v_mov_b32_e32 v9, v106
	v_mov_b32_e32 v12, v98
	v_pk_mul_f32 v[6:7], v[6:7], v[10:11]
	v_mov_b32_e32 v10, v104
	v_pk_fma_f32 v[6:7], v[8:9], v[12:13], v[6:7]
	v_mov_b32_e32 v9, v108
	v_pk_add_f32 v[4:5], v[4:5], v[6:7]
	v_mov_b32_e32 v108, v1
	v_add_f32_e32 v4, 0, v4
	v_add_f32_e32 v94, v4, v5
	ds_read_b128 v[4:7], v141 offset:57344
	v_mov_b32_e32 v8, v0
	s_waitcnt lgkmcnt(0)
	v_mov_b32_e32 v11, v4
	v_mov_b32_e32 v4, v105
	v_pk_mul_f32 v[0:1], v[108:109], v[4:5]
	v_mov_b32_e32 v5, v106
	v_pk_fma_f32 v[0:1], v[8:9], v[10:11], v[0:1]
	v_mov_b32_e32 v9, v6
	v_mov_b32_e32 v106, v3
	v_mov_b32_e32 v6, v99
	v_mov_b32_e32 v4, v2
	v_mov_b32_e32 v8, v98
	v_pk_mul_f32 v[2:3], v[106:107], v[6:7]
	v_pk_mul_f32 v[10:11], v[96:97], v[72:73] op_sel_hi:[1,0]
	v_pk_fma_f32 v[2:3], v[4:5], v[8:9], v[2:3]
	s_nop 0
	v_pk_add_f32 v[0:1], v[0:1], v[2:3]
	ds_read_b128 v[2:5], v139 offset:2048
	ds_read_b128 v[6:9], v139 offset:18432
	v_add_f32_e32 v0, 0, v0
	v_add_f32_e32 v98, v0, v1
	v_pk_mul_f32 v[0:1], v[92:93], v[72:73] op_sel_hi:[1,0]
	s_waitcnt lgkmcnt(0)
	v_pk_fma_f32 v[2:3], v[10:11], v[2:3], v[6:7]
	v_pk_fma_f32 v[0:1], v[0:1], v[4:5], v[8:9]
	v_and_b32_sdwa v5, v2, v214 dst_sel:DWORD dst_unused:UNUSED_PAD src0_sel:WORD_1 src1_sel:DWORD
	v_add3_u32 v6, v2, v5, s33
	v_and_b32_sdwa v5, v1, v214 dst_sel:DWORD dst_unused:UNUSED_PAD src0_sel:WORD_1 src1_sel:DWORD
	v_and_b32_sdwa v7, v3, v214 dst_sel:DWORD dst_unused:UNUSED_PAD src0_sel:WORD_1 src1_sel:DWORD
	v_and_b32_sdwa v4, v0, v214 dst_sel:DWORD dst_unused:UNUSED_PAD src0_sel:WORD_1 src1_sel:DWORD
	v_add3_u32 v5, v1, v5, s33
	v_add3_u32 v7, v3, v7, s33
	v_add3_u32 v4, v0, v4, s33
	v_and_b32_e32 v5, 0xffff0000, v5
	v_and_b32_e32 v7, 0xffff0000, v7
	v_or_b32_sdwa v5, v5, v4 dst_sel:DWORD dst_unused:UNUSED_PAD src0_sel:DWORD src1_sel:WORD_1
	v_or_b32_sdwa v4, v7, v6 dst_sel:DWORD dst_unused:UNUSED_PAD src0_sel:DWORD src1_sel:WORD_1
	global_store_dwordx2 v[74:75], v[4:5], off offset:1024 sc1
	ds_read_b128 v[4:7], v139 offset:34816
	v_pk_mul_f32 v[10:11], v[20:21], v[72:73] op_sel_hi:[1,0]
	s_waitcnt lgkmcnt(0)
	v_pk_mul_f32 v[4:5], v[2:3], v[4:5]
	v_pk_mul_f32 v[6:7], v[0:1], v[6:7]
	s_nop 0
	v_pk_mov_b32 v[8:9], v[4:5], v[6:7] op_sel:[1,0]
	v_mov_b32_e32 v5, v7
	v_pk_add_f32 v[96:97], v[8:9], v[4:5]
	ds_read_b128 v[4:7], v139 offset:43008
	s_waitcnt lgkmcnt(0)
	v_pk_mul_f32 v[4:5], v[2:3], v[4:5]
	v_pk_mul_f32 v[6:7], v[0:1], v[6:7]
	s_nop 0
	v_pk_mov_b32 v[8:9], v[4:5], v[6:7] op_sel:[1,0]
	v_mov_b32_e32 v5, v7
	v_pk_add_f32 v[92:93], v[8:9], v[4:5]
	ds_read_b128 v[4:7], v139 offset:51200
	s_waitcnt lgkmcnt(0)
	v_pk_mul_f32 v[4:5], v[2:3], v[4:5]
	v_pk_mul_f32 v[6:7], v[0:1], v[6:7]
	s_nop 0
	v_pk_mov_b32 v[8:9], v[4:5], v[6:7] op_sel:[1,0]
	v_mov_b32_e32 v5, v7
	v_pk_add_f32 v[120:121], v[8:9], v[4:5]
	ds_read_b128 v[4:7], v139 offset:59392
	s_waitcnt lgkmcnt(0)
	v_pk_mul_f32 v[4:5], v[2:3], v[4:5]
	v_pk_mul_f32 v[6:7], v[0:1], v[6:7]
	s_nop 0
	v_pk_mov_b32 v[8:9], v[4:5], v[6:7] op_sel:[1,0]
	v_mov_b32_e32 v5, v7
	v_pk_add_f32 v[118:119], v[8:9], v[4:5]
	ds_read_b128 v[4:7], v142 offset:32768
	s_waitcnt lgkmcnt(0)
	v_pk_mul_f32 v[4:5], v[2:3], v[4:5]
	v_pk_mul_f32 v[6:7], v[0:1], v[6:7]
	s_nop 0
	v_pk_mov_b32 v[8:9], v[4:5], v[6:7] op_sel:[1,0]
	v_mov_b32_e32 v5, v7
	v_pk_add_f32 v[116:117], v[8:9], v[4:5]
	ds_read_b128 v[4:7], v142 offset:40960
	s_waitcnt lgkmcnt(0)
	v_pk_mul_f32 v[4:5], v[2:3], v[4:5]
	v_pk_mul_f32 v[6:7], v[0:1], v[6:7]
	s_nop 0
	v_pk_mov_b32 v[8:9], v[4:5], v[6:7] op_sel:[1,0]
	v_mov_b32_e32 v5, v7
	v_pk_add_f32 v[112:113], v[8:9], v[4:5]
	ds_read_b128 v[4:7], v142 offset:49152
	s_waitcnt lgkmcnt(0)
	v_pk_mul_f32 v[4:5], v[2:3], v[4:5]
	v_pk_mul_f32 v[6:7], v[0:1], v[6:7]
	s_nop 0
	v_pk_mov_b32 v[8:9], v[4:5], v[6:7] op_sel:[1,0]
	v_mov_b32_e32 v5, v7
	v_pk_add_f32 v[110:111], v[8:9], v[4:5]
	ds_read_b128 v[4:7], v142 offset:57344
	v_pk_mul_f32 v[8:9], v[22:23], v[72:73] op_sel_hi:[1,0]
	s_waitcnt lgkmcnt(0)
	v_pk_mul_f32 v[2:3], v[2:3], v[4:5]
	v_pk_mul_f32 v[0:1], v[0:1], v[6:7]
	s_nop 0
	v_pk_mov_b32 v[4:5], v[2:3], v[0:1] op_sel:[1,0]
	v_mov_b32_e32 v3, v1
	v_pk_add_f32 v[104:105], v[4:5], v[2:3]
	ds_read_b128 v[0:3], v139 offset:3072
	ds_read_b128 v[4:7], v139 offset:19456
	s_waitcnt lgkmcnt(0)
	v_pk_fma_f32 v[106:107], v[10:11], v[0:1], v[4:5]
	v_pk_fma_f32 v[108:109], v[8:9], v[2:3], v[6:7]
	v_and_b32_sdwa v1, v106, v214 dst_sel:DWORD dst_unused:UNUSED_PAD src0_sel:WORD_1 src1_sel:DWORD
	v_add3_u32 v2, v106, v1, s33
	v_and_b32_sdwa v1, v109, v214 dst_sel:DWORD dst_unused:UNUSED_PAD src0_sel:WORD_1 src1_sel:DWORD
	v_and_b32_sdwa v3, v107, v214 dst_sel:DWORD dst_unused:UNUSED_PAD src0_sel:WORD_1 src1_sel:DWORD
	v_and_b32_sdwa v0, v108, v214 dst_sel:DWORD dst_unused:UNUSED_PAD src0_sel:WORD_1 src1_sel:DWORD
	v_add3_u32 v1, v109, v1, s33
	v_add3_u32 v3, v107, v3, s33
	v_add3_u32 v0, v108, v0, s33
	v_and_b32_e32 v1, 0xffff0000, v1
	v_and_b32_e32 v3, 0xffff0000, v3
	v_or_b32_sdwa v1, v1, v0 dst_sel:DWORD dst_unused:UNUSED_PAD src0_sel:DWORD src1_sel:WORD_1
	v_or_b32_sdwa v0, v3, v2 dst_sel:DWORD dst_unused:UNUSED_PAD src0_sel:DWORD src1_sel:WORD_1
	global_store_dwordx2 v[74:75], v[0:1], off offset:1536 sc1
	ds_read_b128 v[122:125], v139 offset:35840
	ds_read_b128 v[126:129], v139 offset:44032
	ds_read_b128 v[20:23], v139 offset:52224
	ds_read_b128 v[16:19], v139 offset:60416
	ds_read_b128 v[12:15], v143 offset:32768
	ds_read_b128 v[8:11], v143 offset:40960
	ds_read_b128 v[4:7], v143 offset:49152
	ds_read_b128 v[0:3], v143 offset:57344
	ds_read_b128 v[130:133], v139 offset:4096
	ds_read_b128 v[134:137], v139 offset:20480
	s_waitcnt lgkmcnt(0)
	v_pk_fma_f32 v[80:81], v[80:81], v[132:133], v[136:137]
	v_pk_fma_f32 v[114:115], v[82:83], v[130:131], v[134:135]
	ds_read_b128 v[130:133], v139 offset:36864
	v_and_b32_sdwa v83, v81, v214 dst_sel:DWORD dst_unused:UNUSED_PAD src0_sel:WORD_1 src1_sel:DWORD
	v_and_b32_sdwa v85, v115, v214 dst_sel:DWORD dst_unused:UNUSED_PAD src0_sel:WORD_1 src1_sel:DWORD
	v_and_b32_sdwa v73, v80, v214 dst_sel:DWORD dst_unused:UNUSED_PAD src0_sel:WORD_1 src1_sel:DWORD
	v_and_b32_sdwa v82, v114, v214 dst_sel:DWORD dst_unused:UNUSED_PAD src0_sel:WORD_1 src1_sel:DWORD
	v_add3_u32 v83, v81, v83, s33
	v_add3_u32 v85, v115, v85, s33
	v_add3_u32 v82, v114, v82, s33
	v_add3_u32 v73, v80, v73, s33
	v_and_b32_e32 v83, 0xffff0000, v83
	v_and_b32_e32 v85, 0xffff0000, v85
	v_or_b32_sdwa v83, v83, v73 dst_sel:DWORD dst_unused:UNUSED_PAD src0_sel:DWORD src1_sel:WORD_1
	v_or_b32_sdwa v82, v85, v82 dst_sel:DWORD dst_unused:UNUSED_PAD src0_sel:DWORD src1_sel:WORD_1
	global_store_dwordx2 v[74:75], v[82:83], off offset:2048 sc1
	s_waitcnt lgkmcnt(0)
	v_mul_f32_e32 v73, v115, v131
	v_pk_add_f32 v[82:83], v[96:97], v[96:97] op_sel:[0,1] op_sel_hi:[1,0]
	v_mul_f32_e32 v89, v114, v130
	v_mov_b32_e32 v83, v73
	v_pk_add_f32 v[82:83], v[88:89], v[82:83]
	v_mul_f32_e32 v88, v107, v123
	v_mul_f32_e32 v96, v109, v125
	v_pk_fma_f32 v[88:89], v[106:107], v[122:123], v[88:89] op_sel_hi:[1,1,0]
	v_pk_fma_f32 v[96:97], v[108:109], v[124:125], v[96:97] op_sel_hi:[1,1,0]
	ds_read_b128 v[122:125], v139 offset:45056
	v_mul_f32_e32 v85, v80, v132
	v_mul_f32_e32 v87, v81, v133
	v_mov_b32_e32 v89, v85
	v_mov_b32_e32 v97, v87
	v_pk_add_f32 v[88:89], v[88:89], v[96:97]
	s_waitcnt lgkmcnt(0)
	v_mul_f32_e32 v73, v115, v123
	v_pk_add_f32 v[96:97], v[82:83], v[88:89]
	v_pk_add_f32 v[82:83], v[92:93], v[92:93] op_sel:[0,1] op_sel_hi:[1,0]
	v_mul_f32_e32 v91, v114, v122
	v_mov_b32_e32 v83, v73
	v_pk_add_f32 v[82:83], v[90:91], v[82:83]
	v_mul_f32_e32 v88, v107, v127
	v_mul_f32_e32 v90, v109, v129
	v_mul_f32_e32 v85, v80, v124
	v_mul_f32_e32 v87, v81, v125
	v_pk_fma_f32 v[88:89], v[106:107], v[126:127], v[88:89] op_sel_hi:[1,1,0]
	v_pk_fma_f32 v[90:91], v[108:109], v[128:129], v[90:91] op_sel_hi:[1,1,0]
	v_mov_b32_e32 v89, v85
	v_mov_b32_e32 v91, v87
	v_pk_add_f32 v[88:89], v[88:89], v[90:91]
	s_nop 0
	v_pk_add_f32 v[92:93], v[82:83], v[88:89]
	ds_read_b128 v[88:91], v139 offset:53248
	v_pk_add_f32 v[82:83], v[120:121], v[120:121] op_sel:[0,1] op_sel_hi:[1,0]
	s_waitcnt lgkmcnt(0)
	v_mul_f32_e32 v73, v115, v89
	v_mul_f32_e32 v87, v114, v88
	v_mov_b32_e32 v83, v73
	v_pk_add_f32 v[82:83], v[86:87], v[82:83]
	v_mul_f32_e32 v86, v107, v21
	v_pk_fma_f32 v[20:21], v[106:107], v[20:21], v[86:87] op_sel_hi:[1,1,0]
	v_mul_f32_e32 v86, v109, v23
	v_mul_f32_e32 v85, v80, v90
	v_mul_f32_e32 v88, v81, v91
	v_pk_fma_f32 v[22:23], v[108:109], v[22:23], v[86:87] op_sel_hi:[1,1,0]
	v_mov_b32_e32 v21, v85
	v_mov_b32_e32 v23, v88
	v_pk_add_f32 v[20:21], v[20:21], v[22:23]
	s_nop 0
	v_pk_add_f32 v[90:91], v[82:83], v[20:21]
	ds_read_b128 v[20:23], v139 offset:61440
	s_waitcnt lgkmcnt(0)
	v_mul_f32_e32 v82, v80, v22
	v_mul_f32_e32 v23, v81, v23
	v_mul_f32_e32 v22, v107, v17
	v_pk_fma_f32 v[16:17], v[106:107], v[16:17], v[22:23] op_sel_hi:[1,1,0]
	v_mul_f32_e32 v22, v109, v19
	v_mul_f32_e32 v103, v114, v20
	v_mul_f32_e32 v73, v115, v21
	v_pk_add_f32 v[20:21], v[118:119], v[118:119] op_sel:[0,1] op_sel_hi:[1,0]
	v_pk_fma_f32 v[18:19], v[108:109], v[18:19], v[22:23] op_sel_hi:[1,1,0]
	v_mov_b32_e32 v21, v73
	v_mov_b32_e32 v17, v82
	v_mov_b32_e32 v19, v23
	v_pk_add_f32 v[20:21], v[102:103], v[20:21]
	v_pk_add_f32 v[16:17], v[16:17], v[18:19]
	v_pk_mul_f32 v[66:67], v[66:67], v[72:73] op_sel_hi:[1,0]
	v_pk_add_f32 v[88:89], v[20:21], v[16:17]
	ds_read_b128 v[16:19], v144 offset:32768
	v_pk_mul_f32 v[64:65], v[64:65], v[72:73] op_sel_hi:[1,0]
	s_waitcnt lgkmcnt(0)
	v_mul_f32_e32 v21, v80, v18
	v_mul_f32_e32 v19, v81, v19
	v_mul_f32_e32 v18, v107, v13
	v_pk_fma_f32 v[12:13], v[106:107], v[12:13], v[18:19] op_sel_hi:[1,1,0]
	v_mul_f32_e32 v18, v109, v15
	v_mul_f32_e32 v85, v114, v16
	v_mul_f32_e32 v20, v115, v17
	v_pk_add_f32 v[16:17], v[116:117], v[116:117] op_sel:[0,1] op_sel_hi:[1,0]
	v_pk_fma_f32 v[14:15], v[108:109], v[14:15], v[18:19] op_sel_hi:[1,1,0]
	v_mov_b32_e32 v17, v20
	v_mov_b32_e32 v13, v21
	v_mov_b32_e32 v15, v19
	v_pk_add_f32 v[16:17], v[84:85], v[16:17]
	v_pk_add_f32 v[12:13], v[12:13], v[14:15]
	s_nop 0
	v_pk_add_f32 v[86:87], v[16:17], v[12:13]
	ds_read_b128 v[12:15], v144 offset:40960
	s_waitcnt lgkmcnt(0)
	v_mul_f32_e32 v17, v80, v14
	v_mul_f32_e32 v15, v81, v15
	v_mul_f32_e32 v14, v107, v9
	v_pk_fma_f32 v[8:9], v[106:107], v[8:9], v[14:15] op_sel_hi:[1,1,0]
	v_mul_f32_e32 v14, v109, v11
	v_mul_f32_e32 v101, v114, v12
	v_mul_f32_e32 v16, v115, v13
	v_pk_add_f32 v[12:13], v[112:113], v[112:113] op_sel:[0,1] op_sel_hi:[1,0]
	v_pk_fma_f32 v[10:11], v[108:109], v[10:11], v[14:15] op_sel_hi:[1,1,0]
	v_mov_b32_e32 v13, v16
	v_mov_b32_e32 v9, v17
	v_mov_b32_e32 v11, v15
	v_pk_add_f32 v[12:13], v[100:101], v[12:13]
	v_pk_add_f32 v[8:9], v[8:9], v[10:11]
	s_nop 0
	v_pk_add_f32 v[84:85], v[12:13], v[8:9]
	ds_read_b128 v[8:11], v144 offset:49152
	s_waitcnt lgkmcnt(0)
	v_mul_f32_e32 v13, v80, v10
	v_mul_f32_e32 v11, v81, v11
	v_mul_f32_e32 v10, v107, v5
	v_pk_fma_f32 v[4:5], v[106:107], v[4:5], v[10:11] op_sel_hi:[1,1,0]
	v_mul_f32_e32 v10, v109, v7
	v_mul_f32_e32 v95, v114, v8
	v_mul_f32_e32 v12, v115, v9
	v_pk_add_f32 v[8:9], v[110:111], v[110:111] op_sel:[0,1] op_sel_hi:[1,0]
	v_pk_fma_f32 v[6:7], v[108:109], v[6:7], v[10:11] op_sel_hi:[1,1,0]
	v_mov_b32_e32 v9, v12
	v_mov_b32_e32 v5, v13
	v_mov_b32_e32 v7, v11
	v_pk_add_f32 v[8:9], v[94:95], v[8:9]
	v_pk_add_f32 v[4:5], v[4:5], v[6:7]
	v_pk_mul_f32 v[10:11], v[78:79], v[72:73] op_sel_hi:[1,0]
	v_pk_add_f32 v[82:83], v[8:9], v[4:5]
	ds_read_b128 v[4:7], v144 offset:57344
	s_waitcnt lgkmcnt(0)
	v_mul_f32_e32 v9, v80, v6
	v_mul_f32_e32 v7, v81, v7
	v_mul_f32_e32 v6, v107, v1
	v_pk_fma_f32 v[0:1], v[106:107], v[0:1], v[6:7] op_sel_hi:[1,1,0]
	v_mul_f32_e32 v6, v109, v3
	v_mul_f32_e32 v99, v114, v4
	v_mul_f32_e32 v8, v115, v5
	v_pk_add_f32 v[4:5], v[104:105], v[104:105] op_sel:[0,1] op_sel_hi:[1,0]
	v_pk_fma_f32 v[2:3], v[108:109], v[2:3], v[6:7] op_sel_hi:[1,1,0]
	v_mov_b32_e32 v5, v8
	v_mov_b32_e32 v1, v9
	v_mov_b32_e32 v3, v7
	v_pk_add_f32 v[4:5], v[98:99], v[4:5]
	v_pk_add_f32 v[0:1], v[0:1], v[2:3]
	s_nop 0
	v_pk_add_f32 v[80:81], v[4:5], v[0:1]
	ds_read_b128 v[2:5], v139 offset:5120
	ds_read_b128 v[6:9], v139 offset:21504
	v_pk_mul_f32 v[0:1], v[76:77], v[72:73] op_sel_hi:[1,0]
	s_waitcnt lgkmcnt(0)
	v_pk_fma_f32 v[2:3], v[10:11], v[2:3], v[6:7]
	v_pk_fma_f32 v[0:1], v[0:1], v[4:5], v[8:9]
	v_and_b32_sdwa v5, v2, v214 dst_sel:DWORD dst_unused:UNUSED_PAD src0_sel:WORD_1 src1_sel:DWORD
	v_add3_u32 v6, v2, v5, s33
	v_and_b32_sdwa v5, v1, v214 dst_sel:DWORD dst_unused:UNUSED_PAD src0_sel:WORD_1 src1_sel:DWORD
	v_and_b32_sdwa v7, v3, v214 dst_sel:DWORD dst_unused:UNUSED_PAD src0_sel:WORD_1 src1_sel:DWORD
	v_and_b32_sdwa v4, v0, v214 dst_sel:DWORD dst_unused:UNUSED_PAD src0_sel:WORD_1 src1_sel:DWORD
	v_add3_u32 v5, v1, v5, s33
	v_add3_u32 v7, v3, v7, s33
	v_add3_u32 v4, v0, v4, s33
	v_and_b32_e32 v5, 0xffff0000, v5
	v_and_b32_e32 v7, 0xffff0000, v7
	v_or_b32_sdwa v5, v5, v4 dst_sel:DWORD dst_unused:UNUSED_PAD src0_sel:DWORD src1_sel:WORD_1
	v_or_b32_sdwa v4, v7, v6 dst_sel:DWORD dst_unused:UNUSED_PAD src0_sel:DWORD src1_sel:WORD_1
	global_store_dwordx2 v[74:75], v[4:5], off offset:2560 sc1
	ds_read_b128 v[4:7], v139 offset:37888
	v_pk_mul_f32 v[10:11], v[68:69], v[72:73] op_sel_hi:[1,0]
	s_waitcnt lgkmcnt(0)
	v_pk_mul_f32 v[4:5], v[2:3], v[4:5]
	v_pk_mul_f32 v[6:7], v[0:1], v[6:7]
	s_nop 0
	v_pk_mov_b32 v[8:9], v[4:5], v[6:7] op_sel:[1,0]
	v_mov_b32_e32 v5, v7
	v_pk_add_f32 v[106:107], v[8:9], v[4:5]
	ds_read_b128 v[4:7], v139 offset:46080
	s_waitcnt lgkmcnt(0)
	v_pk_mul_f32 v[4:5], v[2:3], v[4:5]
	v_pk_mul_f32 v[6:7], v[0:1], v[6:7]
	s_nop 0
	v_pk_mov_b32 v[8:9], v[4:5], v[6:7] op_sel:[1,0]
	v_mov_b32_e32 v5, v7
	v_pk_add_f32 v[104:105], v[8:9], v[4:5]
	ds_read_b128 v[4:7], v139 offset:54272
	s_waitcnt lgkmcnt(0)
	v_pk_mul_f32 v[4:5], v[2:3], v[4:5]
	v_pk_mul_f32 v[6:7], v[0:1], v[6:7]
	s_nop 0
	v_pk_mov_b32 v[8:9], v[4:5], v[6:7] op_sel:[1,0]
	v_mov_b32_e32 v5, v7
	v_pk_add_f32 v[102:103], v[8:9], v[4:5]
	ds_read_b128 v[4:7], v139 offset:62464
	s_waitcnt lgkmcnt(0)
	v_pk_mul_f32 v[4:5], v[2:3], v[4:5]
	v_pk_mul_f32 v[6:7], v[0:1], v[6:7]
	s_nop 0
	v_pk_mov_b32 v[8:9], v[4:5], v[6:7] op_sel:[1,0]
	v_mov_b32_e32 v5, v7
	v_pk_add_f32 v[100:101], v[8:9], v[4:5]
	ds_read_b128 v[4:7], v145 offset:32768
	s_waitcnt lgkmcnt(0)
	v_pk_mul_f32 v[4:5], v[2:3], v[4:5]
	v_pk_mul_f32 v[6:7], v[0:1], v[6:7]
	s_nop 0
	v_pk_mov_b32 v[8:9], v[4:5], v[6:7] op_sel:[1,0]
	v_mov_b32_e32 v5, v7
	v_pk_add_f32 v[98:99], v[8:9], v[4:5]
	ds_read_b128 v[4:7], v145 offset:40960
	s_waitcnt lgkmcnt(0)
	v_pk_mul_f32 v[4:5], v[2:3], v[4:5]
	v_pk_mul_f32 v[6:7], v[0:1], v[6:7]
	s_nop 0
	v_pk_mov_b32 v[8:9], v[4:5], v[6:7] op_sel:[1,0]
	v_mov_b32_e32 v5, v7
	v_pk_add_f32 v[94:95], v[8:9], v[4:5]
	ds_read_b128 v[4:7], v145 offset:49152
	s_waitcnt lgkmcnt(0)
	v_pk_mul_f32 v[4:5], v[2:3], v[4:5]
	v_pk_mul_f32 v[6:7], v[0:1], v[6:7]
	s_nop 0
	v_pk_mov_b32 v[8:9], v[4:5], v[6:7] op_sel:[1,0]
	v_mov_b32_e32 v5, v7
	v_pk_add_f32 v[78:79], v[8:9], v[4:5]
	ds_read_b128 v[4:7], v145 offset:57344
	v_pk_mul_f32 v[8:9], v[70:71], v[72:73] op_sel_hi:[1,0]
	s_waitcnt lgkmcnt(0)
	v_pk_mul_f32 v[2:3], v[2:3], v[4:5]
	v_pk_mul_f32 v[0:1], v[0:1], v[6:7]
	s_nop 0
	v_pk_mov_b32 v[4:5], v[2:3], v[0:1] op_sel:[1,0]
	v_mov_b32_e32 v3, v1
	v_pk_add_f32 v[76:77], v[4:5], v[2:3]
	ds_read_b128 v[0:3], v139 offset:6144
	ds_read_b128 v[4:7], v139 offset:22528
	s_waitcnt lgkmcnt(0)
	v_pk_fma_f32 v[68:69], v[10:11], v[0:1], v[4:5]
	v_pk_fma_f32 v[70:71], v[8:9], v[2:3], v[6:7]
	v_and_b32_sdwa v1, v68, v214 dst_sel:DWORD dst_unused:UNUSED_PAD src0_sel:WORD_1 src1_sel:DWORD
	v_add3_u32 v2, v68, v1, s33
	v_and_b32_sdwa v1, v71, v214 dst_sel:DWORD dst_unused:UNUSED_PAD src0_sel:WORD_1 src1_sel:DWORD
	v_and_b32_sdwa v3, v69, v214 dst_sel:DWORD dst_unused:UNUSED_PAD src0_sel:WORD_1 src1_sel:DWORD
	v_and_b32_sdwa v0, v70, v214 dst_sel:DWORD dst_unused:UNUSED_PAD src0_sel:WORD_1 src1_sel:DWORD
	v_add3_u32 v1, v71, v1, s33
	v_add3_u32 v3, v69, v3, s33
	v_add3_u32 v0, v70, v0, s33
	v_and_b32_e32 v1, 0xffff0000, v1
	v_and_b32_e32 v3, 0xffff0000, v3
	v_or_b32_sdwa v1, v1, v0 dst_sel:DWORD dst_unused:UNUSED_PAD src0_sel:DWORD src1_sel:WORD_1
	v_or_b32_sdwa v0, v3, v2 dst_sel:DWORD dst_unused:UNUSED_PAD src0_sel:DWORD src1_sel:WORD_1
	global_store_dwordx2 v[74:75], v[0:1], off offset:3072 sc1
	ds_read_b128 v[108:111], v139 offset:38912
	ds_read_b128 v[112:115], v139 offset:47104
	ds_read_b128 v[20:23], v139 offset:55296
	ds_read_b128 v[16:19], v139 offset:63488
	ds_read_b128 v[12:15], v146 offset:32768
	ds_read_b128 v[8:11], v146 offset:40960
	ds_read_b128 v[4:7], v146 offset:49152
	ds_read_b128 v[0:3], v146 offset:57344
	ds_read_b128 v[116:119], v139 offset:7168
	ds_read_b128 v[120:123], v139 offset:23552
	s_waitcnt lgkmcnt(0)
	v_pk_fma_f32 v[66:67], v[66:67], v[116:117], v[120:121]
	v_pk_fma_f32 v[64:65], v[64:65], v[118:119], v[122:123]
	v_and_b32_sdwa v73, v66, v214 dst_sel:DWORD dst_unused:UNUSED_PAD src0_sel:WORD_1 src1_sel:DWORD
	v_add3_u32 v116, v66, v73, s33
	v_and_b32_sdwa v73, v65, v214 dst_sel:DWORD dst_unused:UNUSED_PAD src0_sel:WORD_1 src1_sel:DWORD
	v_and_b32_sdwa v117, v67, v214 dst_sel:DWORD dst_unused:UNUSED_PAD src0_sel:WORD_1 src1_sel:DWORD
	v_and_b32_sdwa v72, v64, v214 dst_sel:DWORD dst_unused:UNUSED_PAD src0_sel:WORD_1 src1_sel:DWORD
	v_add3_u32 v73, v65, v73, s33
	v_add3_u32 v117, v67, v117, s33
	v_add3_u32 v72, v64, v72, s33
	v_and_b32_e32 v73, 0xffff0000, v73
	v_and_b32_e32 v117, 0xffff0000, v117
	v_or_b32_sdwa v73, v73, v72 dst_sel:DWORD dst_unused:UNUSED_PAD src0_sel:DWORD src1_sel:WORD_1
	v_or_b32_sdwa v72, v117, v116 dst_sel:DWORD dst_unused:UNUSED_PAD src0_sel:DWORD src1_sel:WORD_1
	global_store_dwordx2 v[74:75], v[72:73], off offset:3584 sc1
	ds_read_b128 v[72:75], v139 offset:39936
	s_waitcnt lgkmcnt(0)
	v_mul_f32_e32 v116, v66, v72
	v_mul_f32_e32 v117, v67, v73
	v_mul_f32_e32 v118, v64, v74
	v_mul_f32_e32 v119, v65, v75
	v_pk_add_f32 v[72:73], v[96:97], v[96:97] op_sel:[0,1] op_sel_hi:[1,0]
	v_pk_add_f32 v[74:75], v[106:107], v[106:107] op_sel:[0,1] op_sel_hi:[1,0]
	v_mov_b32_e32 v73, v116
	v_mov_b32_e32 v75, v117
	v_pk_add_f32 v[72:73], v[72:73], v[74:75]
	v_mul_f32_e32 v74, v69, v109
	v_pk_fma_f32 v[74:75], v[68:69], v[108:109], v[74:75] op_sel_hi:[1,1,0]
	v_mul_f32_e32 v96, v71, v111
	ds_read_b128 v[106:109], v139 offset:48128
	v_pk_fma_f32 v[96:97], v[70:71], v[110:111], v[96:97] op_sel_hi:[1,1,0]
	v_mov_b32_e32 v75, v118
	v_mov_b32_e32 v97, v119
	v_pk_add_f32 v[74:75], v[74:75], v[96:97]
	s_waitcnt lgkmcnt(0)
	v_mul_f32_e32 v96, v67, v107
	v_pk_add_f32 v[72:73], v[72:73], v[74:75]
	v_pk_add_f32 v[74:75], v[92:93], v[92:93] op_sel:[0,1] op_sel_hi:[1,0]
	v_add_f32_e32 v72, v72, v73
	v_mul_f32_e32 v73, v66, v106
	v_pk_add_f32 v[92:93], v[104:105], v[104:105] op_sel:[0,1] op_sel_hi:[1,0]
	v_mov_b32_e32 v75, v73
	v_mov_b32_e32 v93, v96
	v_pk_add_f32 v[74:75], v[74:75], v[92:93]
	v_mul_f32_e32 v92, v69, v113
	v_mul_f32_e32 v97, v64, v108
	v_pk_fma_f32 v[92:93], v[68:69], v[112:113], v[92:93] op_sel_hi:[1,1,0]
	v_mul_f32_e32 v96, v71, v115
	v_mul_f32_e32 v106, v65, v109
	v_mov_b32_e32 v93, v97
	v_pk_fma_f32 v[96:97], v[70:71], v[114:115], v[96:97] op_sel_hi:[1,1,0]
	s_nop 0
	v_mov_b32_e32 v97, v106
	ds_read_b128 v[104:107], v139 offset:56320
	v_pk_add_f32 v[92:93], v[92:93], v[96:97]
	s_waitcnt lgkmcnt(0)
	v_mul_f32_e32 v96, v64, v106
	v_pk_add_f32 v[74:75], v[74:75], v[92:93]
	v_mul_f32_e32 v92, v66, v104
	v_add_f32_e32 v73, v74, v75
	v_mul_f32_e32 v93, v67, v105
	v_pk_add_f32 v[74:75], v[90:91], v[90:91] op_sel:[0,1] op_sel_hi:[1,0]
	v_pk_add_f32 v[90:91], v[102:103], v[102:103] op_sel:[0,1] op_sel_hi:[1,0]
	v_mov_b32_e32 v75, v92
	v_mov_b32_e32 v91, v93
	v_pk_add_f32 v[74:75], v[74:75], v[90:91]
	v_mul_f32_e32 v90, v69, v21
	v_pk_fma_f32 v[20:21], v[68:69], v[20:21], v[90:91] op_sel_hi:[1,1,0]
	v_mul_f32_e32 v90, v71, v23
	v_pk_fma_f32 v[22:23], v[70:71], v[22:23], v[90:91] op_sel_hi:[1,1,0]
	ds_read_b128 v[90:93], v139 offset:64512
	v_mul_f32_e32 v97, v65, v107
	v_mov_b32_e32 v21, v96
	v_mov_b32_e32 v23, v97
	v_pk_add_f32 v[20:21], v[20:21], v[22:23]
	v_pk_add_f32 v[22:23], v[88:89], v[88:89] op_sel:[0,1] op_sel_hi:[1,0]
	v_pk_add_f32 v[20:21], v[74:75], v[20:21]
	v_pk_add_f32 v[74:75], v[100:101], v[100:101] op_sel:[0,1] op_sel_hi:[1,0]
	v_add_f32_e32 v20, v20, v21
	s_waitcnt lgkmcnt(0)
	v_mul_f32_e32 v21, v66, v90
	v_mul_f32_e32 v90, v67, v91
	v_mov_b32_e32 v23, v21
	v_mov_b32_e32 v75, v90
	v_pk_add_f32 v[22:23], v[22:23], v[74:75]
	v_mul_f32_e32 v74, v69, v17
	v_pk_fma_f32 v[16:17], v[68:69], v[16:17], v[74:75] op_sel_hi:[1,1,0]
	v_mul_f32_e32 v74, v71, v19
	v_mul_f32_e32 v91, v64, v92
	v_mul_f32_e32 v92, v65, v93
	v_pk_fma_f32 v[18:19], v[70:71], v[18:19], v[74:75] op_sel_hi:[1,1,0]
	v_mov_b32_e32 v17, v91
	v_mov_b32_e32 v19, v92
	v_pk_add_f32 v[16:17], v[16:17], v[18:19]
	s_nop 0
	v_pk_add_f32 v[16:17], v[22:23], v[16:17]
	s_nop 0
	v_add_f32_e32 v21, v16, v17
	ds_read_b128 v[16:19], v147 offset:32768
	s_waitcnt lgkmcnt(0)
	v_mul_f32_e32 v22, v66, v16
	v_mul_f32_e32 v23, v67, v17
	v_mul_f32_e32 v74, v64, v18
	v_mul_f32_e32 v75, v65, v19
	v_pk_add_f32 v[16:17], v[86:87], v[86:87] op_sel:[0,1] op_sel_hi:[1,0]
	v_pk_add_f32 v[18:19], v[98:99], v[98:99] op_sel:[0,1] op_sel_hi:[1,0]
	v_mov_b32_e32 v17, v22
	v_mov_b32_e32 v19, v23
	v_pk_add_f32 v[16:17], v[16:17], v[18:19]
	v_mul_f32_e32 v18, v69, v13
	v_pk_fma_f32 v[12:13], v[68:69], v[12:13], v[18:19] op_sel_hi:[1,1,0]
	v_mul_f32_e32 v18, v71, v15
	v_pk_fma_f32 v[14:15], v[70:71], v[14:15], v[18:19] op_sel_hi:[1,1,0]
	v_mov_b32_e32 v13, v74
	v_mov_b32_e32 v15, v75
	v_pk_add_f32 v[12:13], v[12:13], v[14:15]
	s_nop 0
	v_pk_add_f32 v[12:13], v[16:17], v[12:13]
	s_nop 0
	v_add_f32_e32 v16, v12, v13
	ds_read_b128 v[12:15], v147 offset:40960
	s_waitcnt lgkmcnt(0)
	v_mul_f32_e32 v17, v66, v12
	v_mul_f32_e32 v18, v67, v13
	v_mul_f32_e32 v19, v64, v14
	v_mul_f32_e32 v22, v65, v15
	v_pk_add_f32 v[12:13], v[84:85], v[84:85] op_sel:[0,1] op_sel_hi:[1,0]
	v_pk_add_f32 v[14:15], v[94:95], v[94:95] op_sel:[0,1] op_sel_hi:[1,0]
	v_mov_b32_e32 v13, v17
	v_mov_b32_e32 v15, v18
	v_pk_add_f32 v[12:13], v[12:13], v[14:15]
	v_mul_f32_e32 v14, v69, v9
	v_pk_fma_f32 v[8:9], v[68:69], v[8:9], v[14:15] op_sel_hi:[1,1,0]
	v_mul_f32_e32 v14, v71, v11
	v_pk_fma_f32 v[10:11], v[70:71], v[10:11], v[14:15] op_sel_hi:[1,1,0]
	v_mov_b32_e32 v9, v19
	v_mov_b32_e32 v11, v22
	v_pk_add_f32 v[8:9], v[8:9], v[10:11]
	s_nop 0
	v_pk_add_f32 v[8:9], v[12:13], v[8:9]
	s_nop 0
	v_add_f32_e32 v12, v8, v9
	ds_read_b128 v[8:11], v147 offset:49152
	s_waitcnt lgkmcnt(0)
	v_mul_f32_e32 v13, v66, v8
	v_mul_f32_e32 v14, v67, v9
	v_mul_f32_e32 v15, v64, v10
	v_mul_f32_e32 v17, v65, v11
	v_pk_add_f32 v[8:9], v[82:83], v[82:83] op_sel:[0,1] op_sel_hi:[1,0]
	v_pk_add_f32 v[10:11], v[78:79], v[78:79] op_sel:[0,1] op_sel_hi:[1,0]
	v_mov_b32_e32 v9, v13
	v_mov_b32_e32 v11, v14
	v_pk_add_f32 v[8:9], v[8:9], v[10:11]
	v_mul_f32_e32 v10, v69, v5
	v_pk_fma_f32 v[4:5], v[68:69], v[4:5], v[10:11] op_sel_hi:[1,1,0]
	v_mul_f32_e32 v10, v71, v7
	v_pk_fma_f32 v[6:7], v[70:71], v[6:7], v[10:11] op_sel_hi:[1,1,0]
	v_mov_b32_e32 v5, v15
	v_mov_b32_e32 v7, v17
	v_pk_add_f32 v[4:5], v[4:5], v[6:7]
	s_nop 0
	v_pk_add_f32 v[4:5], v[8:9], v[4:5]
	s_nop 0
	v_add_f32_e32 v8, v4, v5
	ds_read_b128 v[4:7], v147 offset:57344
	s_waitcnt lgkmcnt(0)
	v_mul_f32_e32 v9, v66, v4
	v_mul_f32_e32 v10, v67, v5
	v_mul_f32_e32 v11, v64, v6
	v_mul_f32_e32 v13, v65, v7
	v_pk_add_f32 v[4:5], v[80:81], v[80:81] op_sel:[0,1] op_sel_hi:[1,0]
	v_pk_add_f32 v[6:7], v[76:77], v[76:77] op_sel:[0,1] op_sel_hi:[1,0]
	v_mov_b32_e32 v5, v9
	v_mov_b32_e32 v7, v10
	v_pk_add_f32 v[4:5], v[4:5], v[6:7]
	v_mul_f32_e32 v6, v69, v1
	v_pk_fma_f32 v[0:1], v[68:69], v[0:1], v[6:7] op_sel_hi:[1,1,0]
	v_mul_f32_e32 v6, v71, v3
	v_pk_fma_f32 v[2:3], v[70:71], v[2:3], v[6:7] op_sel_hi:[1,1,0]
	v_mov_b32_e32 v1, v11
	v_mov_b32_e32 v3, v13
	v_pk_add_f32 v[0:1], v[0:1], v[2:3]
	s_nop 0
	v_pk_add_f32 v[0:1], v[4:5], v[0:1]
	s_nop 0
	v_add_f32_e32 v6, v0, v1
	v_add_f32_dpp v0, v72, v72 quad_perm:[1,0,3,2] row_mask:0xf bank_mask:0xf bound_ctrl:1
	s_nop 1
	v_add_f32_dpp v0, v0, v0 quad_perm:[2,3,0,1] row_mask:0xf bank_mask:0xf bound_ctrl:1
	s_nop 1
	v_add_f32_dpp v0, v0, v0 row_half_mirror row_mask:0xf bank_mask:0xf bound_ctrl:1
	s_nop 1
	v_add_f32_dpp v0, v0, v0 row_mirror row_mask:0xf bank_mask:0xf bound_ctrl:1
	ds_swizzle_b32 v1, v0 offset:swizzle(SWAP,16)
	s_waitcnt lgkmcnt(0)
	v_add_f32_e32 v1, v0, v1
	v_add_f32_dpp v0, v73, v73 quad_perm:[1,0,3,2] row_mask:0xf bank_mask:0xf bound_ctrl:1
	v_mov_b32_e32 v3, v1
	s_nop 1
	v_permlane32_swap_b32_e32 v1, v3
	v_add_f32_dpp v0, v0, v0 quad_perm:[2,3,0,1] row_mask:0xf bank_mask:0xf bound_ctrl:1
	s_nop 1
	v_add_f32_dpp v0, v0, v0 row_half_mirror row_mask:0xf bank_mask:0xf bound_ctrl:1
	s_nop 1
	v_add_f32_dpp v0, v0, v0 row_mirror row_mask:0xf bank_mask:0xf bound_ctrl:1
	ds_swizzle_b32 v2, v0 offset:swizzle(SWAP,16)
	s_waitcnt lgkmcnt(0)
	v_add_f32_e32 v0, v0, v2
	v_mov_b32_e32 v2, v0
	s_nop 1
	v_permlane32_swap_b32_e32 v0, v2
	v_pk_add_f32 v[4:5], v[0:1], v[2:3]
	s_nop 0
	v_add_f32_dpp v0, v20, v20 quad_perm:[1,0,3,2] row_mask:0xf bank_mask:0xf bound_ctrl:1
	v_cmp_gt_f32_e32 vcc, v4, v5
	v_cmp_nlt_f32_e64 s[46:47], s20, v5
	v_add_f32_dpp v0, v0, v0 quad_perm:[2,3,0,1] row_mask:0xf bank_mask:0xf bound_ctrl:1
	v_cndmask_b32_e64 v3, 0, 1, vcc
	s_nop 0
	v_add_f32_dpp v0, v0, v0 row_half_mirror row_mask:0xf bank_mask:0xf bound_ctrl:1
	s_nop 1
	v_add_f32_dpp v0, v0, v0 row_mirror row_mask:0xf bank_mask:0xf bound_ctrl:1
	ds_swizzle_b32 v1, v0 offset:swizzle(SWAP,16)
	s_waitcnt lgkmcnt(0)
	v_add_f32_e32 v0, v0, v1
	v_mov_b32_e32 v1, v0
	s_nop 1
	v_permlane32_swap_b32_e32 v0, v1
	v_add_f32_e32 v2, v0, v1
	s_nop 0
	v_add_f32_dpp v0, v21, v21 quad_perm:[1,0,3,2] row_mask:0xf bank_mask:0xf bound_ctrl:1
	s_nop 1
	v_add_f32_dpp v0, v0, v0 quad_perm:[2,3,0,1] row_mask:0xf bank_mask:0xf bound_ctrl:1
	s_nop 1
	v_add_f32_dpp v0, v0, v0 row_half_mirror row_mask:0xf bank_mask:0xf bound_ctrl:1
	s_nop 1
	v_add_f32_dpp v0, v0, v0 row_mirror row_mask:0xf bank_mask:0xf bound_ctrl:1
	ds_swizzle_b32 v1, v0 offset:swizzle(SWAP,16)
	s_waitcnt lgkmcnt(0)
	v_add_f32_e32 v0, v0, v1
	v_mov_b32_e32 v1, v0
	s_nop 1
	v_permlane32_swap_b32_e32 v0, v1
	v_add_f32_e32 v7, v0, v1
	s_nop 0
	v_add_f32_dpp v0, v16, v16 quad_perm:[1,0,3,2] row_mask:0xf bank_mask:0xf bound_ctrl:1
	s_nop 1
	v_add_f32_dpp v0, v0, v0 quad_perm:[2,3,0,1] row_mask:0xf bank_mask:0xf bound_ctrl:1
	s_nop 1
	v_add_f32_dpp v0, v0, v0 row_half_mirror row_mask:0xf bank_mask:0xf bound_ctrl:1
	s_nop 1
	v_add_f32_dpp v0, v0, v0 row_mirror row_mask:0xf bank_mask:0xf bound_ctrl:1
	ds_swizzle_b32 v1, v0 offset:swizzle(SWAP,16)
	s_waitcnt lgkmcnt(0)
	v_add_f32_e32 v0, v0, v1
	v_mov_b32_e32 v1, v0
	s_nop 1
	v_permlane32_swap_b32_e32 v0, v1
	v_add_f32_e32 v9, v0, v1
	s_nop 0
	v_add_f32_dpp v0, v12, v12 quad_perm:[1,0,3,2] row_mask:0xf bank_mask:0xf bound_ctrl:1
	s_nop 1
	v_add_f32_dpp v0, v0, v0 quad_perm:[2,3,0,1] row_mask:0xf bank_mask:0xf bound_ctrl:1
	s_nop 1
	v_add_f32_dpp v0, v0, v0 row_half_mirror row_mask:0xf bank_mask:0xf bound_ctrl:1
	s_nop 1
	v_add_f32_dpp v0, v0, v0 row_mirror row_mask:0xf bank_mask:0xf bound_ctrl:1
	ds_swizzle_b32 v1, v0 offset:swizzle(SWAP,16)
	s_waitcnt lgkmcnt(0)
	v_add_f32_e32 v0, v0, v1
	v_mov_b32_e32 v1, v0
	s_nop 1
	v_permlane32_swap_b32_e32 v0, v1
	v_add_f32_e32 v10, v0, v1
	s_nop 0
	v_add_f32_dpp v0, v8, v8 quad_perm:[1,0,3,2] row_mask:0xf bank_mask:0xf bound_ctrl:1
	s_nop 1
	v_add_f32_dpp v0, v0, v0 quad_perm:[2,3,0,1] row_mask:0xf bank_mask:0xf bound_ctrl:1
	s_nop 1
	v_add_f32_dpp v0, v0, v0 row_half_mirror row_mask:0xf bank_mask:0xf bound_ctrl:1
	s_nop 1
	v_add_f32_dpp v0, v0, v0 row_mirror row_mask:0xf bank_mask:0xf bound_ctrl:1
	ds_swizzle_b32 v1, v0 offset:swizzle(SWAP,16)
	s_waitcnt lgkmcnt(0)
	v_add_f32_e32 v0, v0, v1
	v_mov_b32_e32 v1, v0
	s_nop 1
	v_permlane32_swap_b32_e32 v0, v1
	v_add_f32_e32 v8, v0, v1
	s_nop 0
	v_add_f32_dpp v0, v6, v6 quad_perm:[1,0,3,2] row_mask:0xf bank_mask:0xf bound_ctrl:1
	s_nop 1
	v_add_f32_dpp v0, v0, v0 quad_perm:[2,3,0,1] row_mask:0xf bank_mask:0xf bound_ctrl:1
	s_nop 1
	v_add_f32_dpp v0, v0, v0 row_half_mirror row_mask:0xf bank_mask:0xf bound_ctrl:1
	s_nop 1
	v_add_f32_dpp v0, v0, v0 row_mirror row_mask:0xf bank_mask:0xf bound_ctrl:1
	ds_swizzle_b32 v1, v0 offset:swizzle(SWAP,16)
	s_waitcnt lgkmcnt(0)
	v_add_f32_e32 v0, v0, v1
	v_mov_b32_e32 v1, v0
	s_nop 1
	v_permlane32_swap_b32_e32 v0, v1
	v_add_f32_e32 v1, v0, v1
	v_cndmask_b32_e32 v0, v5, v4, vcc
	v_cmp_gt_f32_e32 vcc, v2, v0
	s_nop 1
	v_cndmask_b32_e32 v0, v0, v2, vcc
	v_cndmask_b32_e64 v3, v3, 2, vcc
	v_cmp_gt_f32_e32 vcc, v7, v0
	s_nop 1
	v_cndmask_b32_e32 v0, v0, v7, vcc
	v_cndmask_b32_e64 v3, v3, 3, vcc
	v_cmp_gt_f32_e32 vcc, v9, v0
	s_nop 1
	v_cndmask_b32_e32 v0, v0, v9, vcc
	v_cndmask_b32_e64 v3, v3, 4, vcc
	v_cmp_gt_f32_e32 vcc, v10, v0
	s_nop 1
	v_cndmask_b32_e32 v0, v0, v10, vcc
	v_cndmask_b32_e64 v6, v3, 5, vcc
	v_cmp_ngt_f32_e32 vcc, v8, v0
	s_nop 1
	v_cndmask_b32_e32 v3, v8, v0, vcc
	v_cndmask_b32_e32 v0, 6, v6, vcc
	v_cmp_gt_f32_e64 s[42:43], v1, v3
	s_or_b64 s[20:21], vcc, s[42:43]
	v_cmp_ngt_f32_e64 s[40:41], v1, v3
	v_cndmask_b32_e64 v0, v0, 7, s[42:43]
	v_cmp_eq_u32_e64 s[44:45], 0, v0
	s_or_b64 s[44:45], s[44:45], s[46:47]
	s_nop 0
	v_cndmask_b32_e64 v5, v5, v222, s[44:45]
	v_cndmask_b32_e64 v6, 0, -1, s[44:45]
	v_cmp_ne_u32_e64 s[44:45], 1, v0
	v_cmp_gt_f32_e64 s[46:47], v4, v5
	s_and_b64 s[44:45], s[44:45], s[46:47]
	v_cndmask_b32_e64 v4, v5, v4, s[44:45]
	v_cndmask_b32_e64 v5, v6, 1, s[44:45]
	v_cmp_ne_u32_e64 s[44:45], 2, v0
	v_cmp_gt_f32_e64 s[46:47], v2, v4
	s_and_b64 s[44:45], s[44:45], s[46:47]
	v_cndmask_b32_e64 v2, v4, v2, s[44:45]
	v_cndmask_b32_e64 v4, v5, 2, s[44:45]
	v_cmp_ne_u32_e64 s[44:45], 3, v0
	v_cmp_gt_f32_e64 s[46:47], v7, v2
	s_and_b64 s[44:45], s[44:45], s[46:47]
	v_cndmask_b32_e64 v2, v2, v7, s[44:45]
	v_cndmask_b32_e64 v4, v4, 3, s[44:45]
	v_cmp_ne_u32_e64 s[44:45], 4, v0
	v_cmp_gt_f32_e64 s[46:47], v9, v2
	s_and_b64 s[44:45], s[44:45], s[46:47]
	v_cndmask_b32_e64 v2, v2, v9, s[44:45]
	v_cndmask_b32_e64 v4, v4, 4, s[44:45]
	v_cmp_ne_u32_e64 s[44:45], 5, v0
	v_cmp_gt_f32_e64 s[46:47], v10, v2
	s_and_b64 s[44:45], s[44:45], s[46:47]
	v_cndmask_b32_e64 v2, v2, v10, s[44:45]
	v_cmp_gt_f32_e32 vcc, v8, v2
	v_cndmask_b32_e64 v5, v4, 5, s[44:45]
	s_and_b64 vcc, s[20:21], vcc
	v_cndmask_b32_e32 v4, v2, v8, vcc
	v_cndmask_b32_e64 v2, v5, 6, vcc
	s_and_saveexec_b64 s[42:43], s[40:41]
	s_cbranch_execz .LBB0_1218
	v_cmp_gt_f32_e32 vcc, v1, v4
	s_and_saveexec_b64 s[40:41], vcc
	v_mov_b32_e32 v2, 7
	v_mov_b32_e32 v4, v1
	s_or_b64 exec, exec, s[40:41]
	v_mov_b32_e32 v1, v3
.LBB0_1218:
	s_or_b64 exec, exec, s[42:43]
	s_and_saveexec_b64 s[40:41], s[38:39]
	s_cbranch_execz .LBB0_1223
	v_sub_f32_e32 v1, v4, v1
	v_mul_f32_e32 v1, 0x3fb8aa3b, v1
	v_exp_f32_e32 v1, v1
	s_cmp_gt_i32 s4, 30
	s_mov_b64 s[42:43], -1
	v_add_f32_e32 v1, 1.0, v1
	v_div_scale_f32 v3, s[20:21], v1, v1, 1.0
	v_rcp_f32_e32 v4, v3
	v_div_scale_f32 v5, vcc, 1.0, v1, 1.0
	v_fma_f32 v6, -v3, v4, 1.0
	v_fmac_f32_e32 v4, v6, v4
	v_mul_f32_e32 v6, v5, v4
	v_fma_f32 v7, -v3, v6, v5
	v_fmac_f32_e32 v6, v7, v4
	v_fma_f32 v3, -v3, v6, v5
	v_div_fmas_f32 v3, v3, v4, v6
	v_div_fixup_f32 v4, v3, v1, 1.0
	v_sub_f32_e32 v5, 1.0, v4
	s_cbranch_scc0 .LBB0_1221
	v_readlane_b32 s20, v252, 53
	v_lshlrev_b32_e32 v184, 6, v0
	v_readlane_b32 s21, v252, 54
	v_readlane_b32 s24, v250, 0
	v_readlane_b32 s25, v250, 1
	v_lshl_add_u64 v[6:7], v[184:185], 2, s[20:21]
	global_atomic_add v1, v[6:7], v214, off sc0
	v_lshlrev_b32_e32 v6, 6, v2
	v_ashrrev_i32_e32 v7, 31, v6
	v_lshl_add_u64 v[6:7], v[6:7], 2, s[20:21]
	global_atomic_add v3, v[6:7], v214, off sc0
	s_lshl_b64 s[20:21], s[30:31], 4
	s_add_u32 s20, s24, s20
	s_addc_u32 s21, s25, s21
	v_readlane_b32 s24, v250, 2
	v_readlane_b32 s25, v250, 3
	s_mov_b64 s[42:43], 0
	s_waitcnt vmcnt(0)
	global_store_dwordx4 v185, v[0:3], s[20:21] sc1
	s_lshl_b64 s[20:21], s[30:31], 3
	s_add_u32 s20, s24, s20
	s_addc_u32 s21, s25, s21
	global_store_dwordx2 v185, v[4:5], s[20:21] sc1

.LBB0_1225:
	s_waitcnt vmcnt(23)
	v_and_b32_e32 v9, 0xffff0000, v62
	v_and_b32_e32 v11, 0xffff0000, v63
	v_lshlrev_b32_e32 v8, 16, v62
	v_lshlrev_b32_e32 v10, 16, v63
	v_mul_f32_e32 v0, v9, v9
	v_mul_f32_e32 v1, v11, v11
	s_waitcnt vmcnt(22)
	v_and_b32_e32 v79, 0xffff0000, v60
	v_and_b32_e32 v91, 0xffff0000, v61
	v_fmac_f32_e32 v0, v8, v8
	v_fmac_f32_e32 v1, v10, v10
	v_lshlrev_b32_e32 v78, 16, v60
	v_lshlrev_b32_e32 v90, 16, v61
	v_add_f32_e32 v0, v0, v1
	v_mul_f32_e32 v1, v79, v79
	v_mul_f32_e32 v2, v91, v91
	v_fmac_f32_e32 v1, v78, v78
	v_fmac_f32_e32 v2, v90, v90
	s_waitcnt vmcnt(21)
	v_and_b32_e32 v81, 0xffff0000, v58
	v_and_b32_e32 v77, 0xffff0000, v59
	v_add_f32_e32 v1, v1, v2
	v_lshlrev_b32_e32 v80, 16, v58
	v_lshlrev_b32_e32 v76, 16, v59
	v_add_f32_e32 v0, v0, v1
	v_mul_f32_e32 v1, v81, v81
	v_mul_f32_e32 v2, v77, v77
	v_fmac_f32_e32 v1, v80, v80
	v_fmac_f32_e32 v2, v76, v76
	s_waitcnt vmcnt(20)
	v_and_b32_e32 v21, 0xffff0000, v56
	v_and_b32_e32 v23, 0xffff0000, v57
	v_add_f32_e32 v1, v1, v2
	v_lshlrev_b32_e32 v20, 16, v56
	v_lshlrev_b32_e32 v22, 16, v57
	v_add_f32_e32 v0, v0, v1
	v_mul_f32_e32 v1, v21, v21
	v_mul_f32_e32 v2, v23, v23
	v_fmac_f32_e32 v1, v20, v20
	v_fmac_f32_e32 v2, v22, v22
	s_waitcnt vmcnt(19)
	v_and_b32_e32 v67, 0xffff0000, v54
	v_and_b32_e32 v65, 0xffff0000, v55
	v_add_f32_e32 v1, v1, v2
	v_lshlrev_b32_e32 v66, 16, v54
	v_lshlrev_b32_e32 v64, 16, v55
	v_add_f32_e32 v0, v0, v1
	v_mul_f32_e32 v1, v67, v67
	v_mul_f32_e32 v2, v65, v65
	v_fmac_f32_e32 v1, v66, v66
	v_fmac_f32_e32 v2, v64, v64
	s_waitcnt vmcnt(18)
	v_and_b32_e32 v63, 0xffff0000, v52
	v_and_b32_e32 v61, 0xffff0000, v53
	v_add_f32_e32 v1, v1, v2
	v_lshlrev_b32_e32 v62, 16, v52
	v_lshlrev_b32_e32 v60, 16, v53
	v_add_f32_e32 v0, v0, v1
	v_mul_f32_e32 v1, v63, v63
	v_mul_f32_e32 v2, v61, v61
	v_fmac_f32_e32 v1, v62, v62
	v_fmac_f32_e32 v2, v60, v60
	s_waitcnt vmcnt(17)
	v_and_b32_e32 v53, 0xffff0000, v50
	v_and_b32_e32 v55, 0xffff0000, v51
	v_add_f32_e32 v1, v1, v2
	v_lshlrev_b32_e32 v52, 16, v50
	v_lshlrev_b32_e32 v54, 16, v51
	v_add_f32_e32 v0, v0, v1
	v_mul_f32_e32 v1, v53, v53
	v_mul_f32_e32 v2, v55, v55
	v_fmac_f32_e32 v1, v52, v52
	v_fmac_f32_e32 v2, v54, v54
	s_waitcnt vmcnt(16)
	v_lshlrev_b32_e32 v50, 16, v48
	v_and_b32_e32 v51, 0xffff0000, v48
	v_lshlrev_b32_e32 v48, 16, v49
	v_and_b32_e32 v49, 0xffff0000, v49
	v_add_f32_e32 v1, v1, v2
	v_add_f32_e32 v0, v0, v1
	v_mul_f32_e32 v1, v51, v51
	v_mul_f32_e32 v2, v49, v49
	v_fmac_f32_e32 v1, v50, v50
	v_fmac_f32_e32 v2, v48, v48
	v_add_f32_e32 v1, v1, v2
	v_add_f32_e32 v0, v0, v1
	s_mov_b32 s16, 0xf800000
	v_lshl_add_u64 v[58:59], v[28:29], 0, s[18:19]
	v_add_f32_dpp v0, v0, v0 quad_perm:[1,0,3,2] row_mask:0xf bank_mask:0xf bound_ctrl:1
	s_nop 1
	v_add_f32_dpp v0, v0, v0 quad_perm:[2,3,0,1] row_mask:0xf bank_mask:0xf bound_ctrl:1
	s_nop 1
	v_add_f32_dpp v0, v0, v0 row_half_mirror row_mask:0xf bank_mask:0xf bound_ctrl:1
	s_nop 1
	v_add_f32_dpp v0, v0, v0 row_mirror row_mask:0xf bank_mask:0xf bound_ctrl:1
	ds_swizzle_b32 v1, v0 offset:swizzle(SWAP,16)
	s_waitcnt lgkmcnt(0)
	v_add_f32_e32 v0, v0, v1
	v_mov_b32_e32 v1, v0
	s_nop 1
	v_permlane32_swap_b32_e32 v0, v1
	v_add_f32_e32 v0, v0, v1
	v_fmamk_f32 v0, v0, 0x3a000000, v212
	v_cmp_gt_f32_e32 vcc, s16, v0
	v_mul_f32_e32 v1, 0x4f800000, v0
	s_nop 0
	v_cndmask_b32_e32 v0, v0, v1, vcc
	v_sqrt_f32_e32 v1, v0
	s_nop 0
	v_add_u32_e32 v2, -1, v1
	v_fma_f32 v3, -v2, v1, v0
	v_cmp_ge_f32_e64 s[40:41], 0, v3
	v_add_u32_e32 v3, 1, v1
	s_nop 0
	v_cndmask_b32_e64 v2, v1, v2, s[40:41]
	v_fma_f32 v1, -v3, v1, v0
	v_cmp_lt_f32_e64 s[40:41], 0, v1
	s_nop 1
	v_cndmask_b32_e64 v1, v2, v3, s[40:41]
	v_mul_f32_e32 v2, 0x37800000, v1
	v_cndmask_b32_e32 v1, v1, v2, vcc
	v_cmp_class_f32_e32 vcc, v0, v213
	s_nop 1
	v_cndmask_b32_e32 v0, v1, v0, vcc
	v_div_scale_f32 v1, s[16:17], v0, v0, 1.0
	v_rcp_f32_e32 v2, v1
	s_mov_b32 s16, 0xff61b1e6
	v_fma_f32 v3, -v1, v2, 1.0
	v_fmac_f32_e32 v2, v3, v2
	v_div_scale_f32 v3, vcc, 1.0, v0, 1.0
	v_mul_f32_e32 v4, v3, v2
	v_fma_f32 v5, -v1, v4, v3
	v_fmac_f32_e32 v4, v5, v2
	v_fma_f32 v1, -v1, v4, v3
	v_div_fmas_f32 v1, v1, v2, v4
	v_div_fixup_f32 v56, v1, v0, 1.0
	ds_read_b128 v[0:3], v139
	ds_read_b128 v[4:7], v139 offset:16384
	v_pk_mul_f32 v[8:9], v[8:9], v[56:57] op_sel_hi:[1,0]
	v_pk_mul_f32 v[10:11], v[10:11], v[56:57] op_sel_hi:[1,0]
	v_pk_mul_f32 v[78:79], v[78:79], v[56:57] op_sel_hi:[1,0]
	v_pk_mul_f32 v[90:91], v[90:91], v[56:57] op_sel_hi:[1,0]
	s_waitcnt lgkmcnt(0)
	v_pk_fma_f32 v[88:89], v[0:1], v[8:9], v[4:5]
	v_pk_fma_f32 v[82:83], v[2:3], v[10:11], v[6:7]
	v_and_b32_sdwa v1, v88, v214 dst_sel:DWORD dst_unused:UNUSED_PAD src0_sel:WORD_1 src1_sel:DWORD
	v_add3_u32 v2, v88, v1, s33
	v_and_b32_sdwa v1, v83, v214 dst_sel:DWORD dst_unused:UNUSED_PAD src0_sel:WORD_1 src1_sel:DWORD
	v_and_b32_sdwa v3, v89, v214 dst_sel:DWORD dst_unused:UNUSED_PAD src0_sel:WORD_1 src1_sel:DWORD
	v_and_b32_sdwa v0, v82, v214 dst_sel:DWORD dst_unused:UNUSED_PAD src0_sel:WORD_1 src1_sel:DWORD
	v_add3_u32 v1, v83, v1, s33
	v_add3_u32 v3, v89, v3, s33
	v_add3_u32 v0, v82, v0, s33
	v_and_b32_e32 v1, 0xffff0000, v1
	v_and_b32_e32 v3, 0xffff0000, v3
	v_or_b32_sdwa v1, v1, v0 dst_sel:DWORD dst_unused:UNUSED_PAD src0_sel:DWORD src1_sel:WORD_1
	v_or_b32_sdwa v0, v3, v2 dst_sel:DWORD dst_unused:UNUSED_PAD src0_sel:DWORD src1_sel:WORD_1
	global_store_dwordx2 v[58:59], v[0:1], off sc1
	ds_read_b128 v[68:71], v139 offset:32768
	ds_read_b128 v[84:87], v139 offset:40960
	ds_read_b128 v[94:97], v139 offset:49152
	ds_read_b128 v[16:19], v139 offset:57344
	ds_read_b128 v[12:15], v140 offset:32768
	ds_read_b128 v[8:11], v140 offset:40960
	ds_read_b128 v[4:7], v140 offset:49152
	ds_read_b128 v[0:3], v140 offset:57344
	ds_read_b128 v[72:75], v139 offset:1024
	ds_read_b128 v[98:101], v139 offset:17408
	s_waitcnt lgkmcnt(0)
	v_pk_fma_f32 v[90:91], v[90:91], v[74:75], v[100:101]
	v_pk_fma_f32 v[92:93], v[78:79], v[72:73], v[98:99]
	v_and_b32_sdwa v73, v91, v214 dst_sel:DWORD dst_unused:UNUSED_PAD src0_sel:WORD_1 src1_sel:DWORD
	v_and_b32_sdwa v74, v93, v214 dst_sel:DWORD dst_unused:UNUSED_PAD src0_sel:WORD_1 src1_sel:DWORD
	v_and_b32_sdwa v57, v90, v214 dst_sel:DWORD dst_unused:UNUSED_PAD src0_sel:WORD_1 src1_sel:DWORD
	v_and_b32_sdwa v72, v92, v214 dst_sel:DWORD dst_unused:UNUSED_PAD src0_sel:WORD_1 src1_sel:DWORD
	v_add3_u32 v73, v91, v73, s33
	v_add3_u32 v74, v93, v74, s33
	v_add3_u32 v72, v92, v72, s33
	v_add3_u32 v57, v90, v57, s33
	v_and_b32_e32 v73, 0xffff0000, v73
	v_and_b32_e32 v74, 0xffff0000, v74
	v_or_b32_sdwa v73, v73, v57 dst_sel:DWORD dst_unused:UNUSED_PAD src0_sel:DWORD src1_sel:WORD_1
	v_or_b32_sdwa v72, v74, v72 dst_sel:DWORD dst_unused:UNUSED_PAD src0_sel:DWORD src1_sel:WORD_1
	global_store_dwordx2 v[58:59], v[72:73], off offset:512 sc1
	ds_read_b128 v[72:75], v139 offset:33792
	v_mov_b32_e32 v78, v68
	v_mov_b32_e32 v68, v69
	v_mov_b32_e32 v69, v93
	v_mov_b32_e32 v79, v92
	s_waitcnt lgkmcnt(0)
	v_mov_b32_e32 v99, v72
	v_mov_b32_e32 v72, v89
	v_mov_b32_e32 v98, v88
	v_pk_mul_f32 v[68:69], v[68:69], v[72:73]
	v_mov_b32_e32 v72, v70
	v_pk_fma_f32 v[68:69], v[78:79], v[98:99], v[68:69]
	v_mov_b32_e32 v79, v74
	v_mov_b32_e32 v70, v71
	v_mov_b32_e32 v71, v91
	v_mov_b32_e32 v74, v83
	v_mov_b32_e32 v73, v90
	v_mov_b32_e32 v78, v82
	v_pk_mul_f32 v[70:71], v[70:71], v[74:75]
	v_mov_b32_e32 v74, v84
	v_pk_fma_f32 v[70:71], v[72:73], v[78:79], v[70:71]
	v_mov_b32_e32 v84, v85
	v_pk_add_f32 v[68:69], v[68:69], v[70:71]
	v_mov_b32_e32 v85, v93
	v_add_f32_e32 v57, 0, v68
	v_add_f32_e32 v72, v57, v69
	ds_read_b128 v[68:71], v139 offset:41984
	v_mov_b32_e32 v75, v92
	v_mov_b32_e32 v78, v88
	s_waitcnt lgkmcnt(0)
	v_mov_b32_e32 v79, v68
	v_mov_b32_e32 v68, v89
	v_pk_mul_f32 v[68:69], v[84:85], v[68:69]
	v_mov_b32_e32 v84, v87
	v_pk_fma_f32 v[68:69], v[74:75], v[78:79], v[68:69]
	v_mov_b32_e32 v79, v70
	v_mov_b32_e32 v85, v91
	v_mov_b32_e32 v70, v83
	v_mov_b32_e32 v74, v86
	v_mov_b32_e32 v75, v90
	v_mov_b32_e32 v78, v82
	v_pk_mul_f32 v[70:71], v[84:85], v[70:71]
	v_mov_b32_e32 v86, v95
	v_pk_fma_f32 v[70:71], v[74:75], v[78:79], v[70:71]
	v_mov_b32_e32 v87, v93
	v_pk_add_f32 v[68:69], v[68:69], v[70:71]
	v_mov_b32_e32 v78, v94
	v_add_f32_e32 v57, 0, v68
	v_add_f32_e32 v74, v57, v69
	ds_read_b128 v[68:71], v139 offset:50176
	v_mov_b32_e32 v79, v92
	v_mov_b32_e32 v84, v88
	s_waitcnt lgkmcnt(0)
	v_mov_b32_e32 v85, v68
	v_mov_b32_e32 v68, v89
	v_pk_mul_f32 v[68:69], v[86:87], v[68:69]
	v_mov_b32_e32 v86, v97
	v_pk_fma_f32 v[68:69], v[78:79], v[84:85], v[68:69]
	v_mov_b32_e32 v85, v70
	v_mov_b32_e32 v87, v91
	v_mov_b32_e32 v70, v83
	v_mov_b32_e32 v78, v96
	v_mov_b32_e32 v79, v90
	v_mov_b32_e32 v84, v82
	v_pk_mul_f32 v[70:71], v[86:87], v[70:71]
	s_nop 0
	v_pk_fma_f32 v[70:71], v[78:79], v[84:85], v[70:71]
	ds_read_b128 v[84:87], v139 offset:58368
	v_pk_add_f32 v[68:69], v[68:69], v[70:71]
	v_mov_b32_e32 v78, v88
	v_add_f32_e32 v57, 0, v68
	v_mov_b32_e32 v68, v16
	s_waitcnt lgkmcnt(0)
	v_mov_b32_e32 v79, v84
	v_mov_b32_e32 v16, v17
	v_mov_b32_e32 v17, v93
	v_mov_b32_e32 v84, v89
	v_add_f32_e32 v70, v57, v69
	v_mov_b32_e32 v69, v92
	v_pk_mul_f32 v[16:17], v[16:17], v[84:85]
	v_pk_mul_f32 v[66:67], v[66:67], v[56:57] op_sel_hi:[1,0]
	v_pk_fma_f32 v[16:17], v[68:69], v[78:79], v[16:17]
	v_mov_b32_e32 v68, v18
	v_mov_b32_e32 v79, v86
	v_mov_b32_e32 v18, v19
	v_mov_b32_e32 v19, v91
	v_mov_b32_e32 v86, v83
	v_mov_b32_e32 v69, v90
	v_mov_b32_e32 v78, v82
	v_pk_mul_f32 v[18:19], v[18:19], v[86:87]
	v_pk_mul_f32 v[64:65], v[64:65], v[56:57] op_sel_hi:[1,0]
	v_pk_fma_f32 v[18:19], v[68:69], v[78:79], v[18:19]
	v_mov_b32_e32 v68, v12
	v_pk_add_f32 v[16:17], v[16:17], v[18:19]
	v_mov_b32_e32 v12, v13
	v_add_f32_e32 v16, 0, v16
	v_add_f32_e32 v86, v16, v17
	ds_read_b128 v[16:19], v141 offset:32768
	v_mov_b32_e32 v13, v93
	v_mov_b32_e32 v69, v92
	v_mov_b32_e32 v78, v88
	s_waitcnt lgkmcnt(0)
	v_mov_b32_e32 v79, v16
	v_mov_b32_e32 v16, v89
	v_pk_mul_f32 v[12:13], v[12:13], v[16:17]
	v_mov_b32_e32 v16, v14
	v_pk_fma_f32 v[12:13], v[68:69], v[78:79], v[12:13]
	v_mov_b32_e32 v69, v18
	v_mov_b32_e32 v14, v15
	v_mov_b32_e32 v15, v91
	v_mov_b32_e32 v18, v83
	v_mov_b32_e32 v17, v90
	v_mov_b32_e32 v68, v82
	v_pk_mul_f32 v[14:15], v[14:15], v[18:19]
	v_mov_b32_e32 v18, v88
	v_pk_fma_f32 v[14:15], v[16:17], v[68:69], v[14:15]
	v_mov_b32_e32 v16, v8
	v_pk_add_f32 v[12:13], v[12:13], v[14:15]
	v_mov_b32_e32 v8, v9
	v_add_f32_e32 v12, 0, v12
	v_add_f32_e32 v68, v12, v13
	ds_read_b128 v[12:15], v141 offset:40960
	v_mov_b32_e32 v9, v93
	v_mov_b32_e32 v17, v92
	s_waitcnt lgkmcnt(0)
	v_mov_b32_e32 v19, v12
	v_mov_b32_e32 v12, v89
	v_pk_mul_f32 v[8:9], v[8:9], v[12:13]
	v_mov_b32_e32 v12, v10
	v_pk_fma_f32 v[8:9], v[16:17], v[18:19], v[8:9]
	v_mov_b32_e32 v17, v14
	v_mov_b32_e32 v10, v11
	v_mov_b32_e32 v11, v91
	v_mov_b32_e32 v14, v83
	v_mov_b32_e32 v13, v90
	v_mov_b32_e32 v16, v82
	v_pk_mul_f32 v[10:11], v[10:11], v[14:15]
	v_mov_b32_e32 v14, v88
	v_pk_fma_f32 v[10:11], v[12:13], v[16:17], v[10:11]
	v_mov_b32_e32 v12, v4
	v_pk_add_f32 v[8:9], v[8:9], v[10:11]
	v_mov_b32_e32 v4, v5
	v_add_f32_e32 v8, 0, v8
	v_add_f32_e32 v84, v8, v9
	ds_read_b128 v[8:11], v141 offset:49152
	v_mov_b32_e32 v5, v93
	v_mov_b32_e32 v13, v92
	s_waitcnt lgkmcnt(0)
	v_mov_b32_e32 v15, v8
	v_mov_b32_e32 v8, v89
	v_pk_mul_f32 v[4:5], v[4:5], v[8:9]
	v_mov_b32_e32 v8, v6
	v_pk_fma_f32 v[4:5], v[12:13], v[14:15], v[4:5]
	v_mov_b32_e32 v13, v10
	v_mov_b32_e32 v6, v7
	v_mov_b32_e32 v7, v91
	v_mov_b32_e32 v10, v83
	v_mov_b32_e32 v9, v90
	v_mov_b32_e32 v12, v82
	v_pk_mul_f32 v[6:7], v[6:7], v[10:11]
	v_mov_b32_e32 v10, v88
	v_pk_fma_f32 v[6:7], v[8:9], v[12:13], v[6:7]
	v_mov_b32_e32 v9, v92
	v_pk_add_f32 v[4:5], v[4:5], v[6:7]
	v_mov_b32_e32 v92, v1
	v_add_f32_e32 v4, 0, v4
	v_add_f32_e32 v78, v4, v5
	ds_read_b128 v[4:7], v141 offset:57344
	v_mov_b32_e32 v8, v0
	s_waitcnt lgkmcnt(0)
	v_mov_b32_e32 v11, v4
	v_mov_b32_e32 v4, v89
	v_pk_mul_f32 v[0:1], v[92:93], v[4:5]
	v_mov_b32_e32 v5, v90
	v_pk_fma_f32 v[0:1], v[8:9], v[10:11], v[0:1]
	v_mov_b32_e32 v9, v6
	v_mov_b32_e32 v90, v3
	v_mov_b32_e32 v6, v83
	v_mov_b32_e32 v4, v2
	v_mov_b32_e32 v8, v82
	v_pk_mul_f32 v[2:3], v[90:91], v[6:7]
	v_pk_mul_f32 v[10:11], v[80:81], v[56:57] op_sel_hi:[1,0]
	v_pk_fma_f32 v[2:3], v[4:5], v[8:9], v[2:3]
	s_nop 0
	v_pk_add_f32 v[0:1], v[0:1], v[2:3]
	ds_read_b128 v[2:5], v139 offset:2048
	ds_read_b128 v[6:9], v139 offset:18432
	v_add_f32_e32 v0, 0, v0
	v_add_f32_e32 v82, v0, v1
	v_pk_mul_f32 v[0:1], v[76:77], v[56:57] op_sel_hi:[1,0]
	s_waitcnt lgkmcnt(0)
	v_pk_fma_f32 v[2:3], v[10:11], v[2:3], v[6:7]
	v_pk_fma_f32 v[0:1], v[0:1], v[4:5], v[8:9]
	v_and_b32_sdwa v5, v2, v214 dst_sel:DWORD dst_unused:UNUSED_PAD src0_sel:WORD_1 src1_sel:DWORD
	v_add3_u32 v6, v2, v5, s33
	v_and_b32_sdwa v5, v1, v214 dst_sel:DWORD dst_unused:UNUSED_PAD src0_sel:WORD_1 src1_sel:DWORD
	v_and_b32_sdwa v7, v3, v214 dst_sel:DWORD dst_unused:UNUSED_PAD src0_sel:WORD_1 src1_sel:DWORD
	v_and_b32_sdwa v4, v0, v214 dst_sel:DWORD dst_unused:UNUSED_PAD src0_sel:WORD_1 src1_sel:DWORD
	v_add3_u32 v5, v1, v5, s33
	v_add3_u32 v7, v3, v7, s33
	v_add3_u32 v4, v0, v4, s33
	v_and_b32_e32 v5, 0xffff0000, v5
	v_and_b32_e32 v7, 0xffff0000, v7
	v_or_b32_sdwa v5, v5, v4 dst_sel:DWORD dst_unused:UNUSED_PAD src0_sel:DWORD src1_sel:WORD_1
	v_or_b32_sdwa v4, v7, v6 dst_sel:DWORD dst_unused:UNUSED_PAD src0_sel:DWORD src1_sel:WORD_1
	global_store_dwordx2 v[58:59], v[4:5], off offset:1024 sc1
	ds_read_b128 v[4:7], v139 offset:34816
	v_pk_mul_f32 v[10:11], v[20:21], v[56:57] op_sel_hi:[1,0]
	s_waitcnt lgkmcnt(0)
	v_pk_mul_f32 v[4:5], v[2:3], v[4:5]
	v_pk_mul_f32 v[6:7], v[0:1], v[6:7]
	s_nop 0
	v_pk_mov_b32 v[8:9], v[4:5], v[6:7] op_sel:[1,0]
	v_mov_b32_e32 v5, v7
	v_pk_add_f32 v[80:81], v[8:9], v[4:5]
	ds_read_b128 v[4:7], v139 offset:43008
	s_waitcnt lgkmcnt(0)
	v_pk_mul_f32 v[4:5], v[2:3], v[4:5]
	v_pk_mul_f32 v[6:7], v[0:1], v[6:7]
	s_nop 0
	v_pk_mov_b32 v[8:9], v[4:5], v[6:7] op_sel:[1,0]
	v_mov_b32_e32 v5, v7
	v_pk_add_f32 v[76:77], v[8:9], v[4:5]
	ds_read_b128 v[4:7], v139 offset:51200
	s_waitcnt lgkmcnt(0)
	v_pk_mul_f32 v[4:5], v[2:3], v[4:5]
	v_pk_mul_f32 v[6:7], v[0:1], v[6:7]
	s_nop 0
	v_pk_mov_b32 v[8:9], v[4:5], v[6:7] op_sel:[1,0]
	v_mov_b32_e32 v5, v7
	v_pk_add_f32 v[104:105], v[8:9], v[4:5]
	ds_read_b128 v[4:7], v139 offset:59392
	s_waitcnt lgkmcnt(0)
	v_pk_mul_f32 v[4:5], v[2:3], v[4:5]
	v_pk_mul_f32 v[6:7], v[0:1], v[6:7]
	s_nop 0
	v_pk_mov_b32 v[8:9], v[4:5], v[6:7] op_sel:[1,0]
	v_mov_b32_e32 v5, v7
	v_pk_add_f32 v[102:103], v[8:9], v[4:5]
	ds_read_b128 v[4:7], v142 offset:32768
	s_waitcnt lgkmcnt(0)
	v_pk_mul_f32 v[4:5], v[2:3], v[4:5]
	v_pk_mul_f32 v[6:7], v[0:1], v[6:7]
	s_nop 0
	v_pk_mov_b32 v[8:9], v[4:5], v[6:7] op_sel:[1,0]
	v_mov_b32_e32 v5, v7
	v_pk_add_f32 v[100:101], v[8:9], v[4:5]
	ds_read_b128 v[4:7], v142 offset:40960
	s_waitcnt lgkmcnt(0)
	v_pk_mul_f32 v[4:5], v[2:3], v[4:5]
	v_pk_mul_f32 v[6:7], v[0:1], v[6:7]
	s_nop 0
	v_pk_mov_b32 v[8:9], v[4:5], v[6:7] op_sel:[1,0]
	v_mov_b32_e32 v5, v7
	v_pk_add_f32 v[96:97], v[8:9], v[4:5]
	ds_read_b128 v[4:7], v142 offset:49152
	s_waitcnt lgkmcnt(0)
	v_pk_mul_f32 v[4:5], v[2:3], v[4:5]
	v_pk_mul_f32 v[6:7], v[0:1], v[6:7]
	s_nop 0
	v_pk_mov_b32 v[8:9], v[4:5], v[6:7] op_sel:[1,0]
	v_mov_b32_e32 v5, v7
	v_pk_add_f32 v[94:95], v[8:9], v[4:5]
	ds_read_b128 v[4:7], v142 offset:57344
	v_pk_mul_f32 v[8:9], v[22:23], v[56:57] op_sel_hi:[1,0]
	s_waitcnt lgkmcnt(0)
	v_pk_mul_f32 v[2:3], v[2:3], v[4:5]
	v_pk_mul_f32 v[0:1], v[0:1], v[6:7]
	s_nop 0
	v_pk_mov_b32 v[4:5], v[2:3], v[0:1] op_sel:[1,0]
	v_mov_b32_e32 v3, v1
	v_pk_add_f32 v[88:89], v[4:5], v[2:3]
	ds_read_b128 v[0:3], v139 offset:3072
	ds_read_b128 v[4:7], v139 offset:19456
	s_waitcnt lgkmcnt(0)
	v_pk_fma_f32 v[90:91], v[10:11], v[0:1], v[4:5]
	v_pk_fma_f32 v[92:93], v[8:9], v[2:3], v[6:7]
	v_and_b32_sdwa v1, v90, v214 dst_sel:DWORD dst_unused:UNUSED_PAD src0_sel:WORD_1 src1_sel:DWORD
	v_add3_u32 v2, v90, v1, s33
	v_and_b32_sdwa v1, v93, v214 dst_sel:DWORD dst_unused:UNUSED_PAD src0_sel:WORD_1 src1_sel:DWORD
	v_and_b32_sdwa v3, v91, v214 dst_sel:DWORD dst_unused:UNUSED_PAD src0_sel:WORD_1 src1_sel:DWORD
	v_and_b32_sdwa v0, v92, v214 dst_sel:DWORD dst_unused:UNUSED_PAD src0_sel:WORD_1 src1_sel:DWORD
	v_add3_u32 v1, v93, v1, s33
	v_add3_u32 v3, v91, v3, s33
	v_add3_u32 v0, v92, v0, s33
	v_and_b32_e32 v1, 0xffff0000, v1
	v_and_b32_e32 v3, 0xffff0000, v3
	v_or_b32_sdwa v1, v1, v0 dst_sel:DWORD dst_unused:UNUSED_PAD src0_sel:DWORD src1_sel:WORD_1
	v_or_b32_sdwa v0, v3, v2 dst_sel:DWORD dst_unused:UNUSED_PAD src0_sel:DWORD src1_sel:WORD_1
	global_store_dwordx2 v[58:59], v[0:1], off offset:1536 sc1
	ds_read_b128 v[106:109], v139 offset:35840
	ds_read_b128 v[110:113], v139 offset:44032
	ds_read_b128 v[20:23], v139 offset:52224
	ds_read_b128 v[16:19], v139 offset:60416
	ds_read_b128 v[12:15], v143 offset:32768
	ds_read_b128 v[8:11], v143 offset:40960
	ds_read_b128 v[4:7], v143 offset:49152
	ds_read_b128 v[0:3], v143 offset:57344
	ds_read_b128 v[114:117], v139 offset:4096
	ds_read_b128 v[118:121], v139 offset:20480
	s_waitcnt lgkmcnt(0)
	v_pk_fma_f32 v[64:65], v[64:65], v[116:117], v[120:121]
	v_pk_fma_f32 v[98:99], v[66:67], v[114:115], v[118:119]
	ds_read_b128 v[114:117], v139 offset:36864
	v_and_b32_sdwa v67, v65, v214 dst_sel:DWORD dst_unused:UNUSED_PAD src0_sel:WORD_1 src1_sel:DWORD
	v_and_b32_sdwa v69, v99, v214 dst_sel:DWORD dst_unused:UNUSED_PAD src0_sel:WORD_1 src1_sel:DWORD
	v_and_b32_sdwa v57, v64, v214 dst_sel:DWORD dst_unused:UNUSED_PAD src0_sel:WORD_1 src1_sel:DWORD
	v_and_b32_sdwa v66, v98, v214 dst_sel:DWORD dst_unused:UNUSED_PAD src0_sel:WORD_1 src1_sel:DWORD
	v_add3_u32 v67, v65, v67, s33
	v_add3_u32 v69, v99, v69, s33
	v_add3_u32 v66, v98, v66, s33
	v_add3_u32 v57, v64, v57, s33
	v_and_b32_e32 v67, 0xffff0000, v67
	v_and_b32_e32 v69, 0xffff0000, v69
	v_or_b32_sdwa v67, v67, v57 dst_sel:DWORD dst_unused:UNUSED_PAD src0_sel:DWORD src1_sel:WORD_1
	v_or_b32_sdwa v66, v69, v66 dst_sel:DWORD dst_unused:UNUSED_PAD src0_sel:DWORD src1_sel:WORD_1
	global_store_dwordx2 v[58:59], v[66:67], off offset:2048 sc1
	s_waitcnt lgkmcnt(0)
	v_mul_f32_e32 v57, v99, v115
	v_pk_add_f32 v[66:67], v[80:81], v[80:81] op_sel:[0,1] op_sel_hi:[1,0]
	v_mul_f32_e32 v73, v98, v114
	v_mov_b32_e32 v67, v57
	v_pk_add_f32 v[66:67], v[72:73], v[66:67]
	v_mul_f32_e32 v72, v91, v107
	v_mul_f32_e32 v80, v93, v109
	v_pk_fma_f32 v[72:73], v[90:91], v[106:107], v[72:73] op_sel_hi:[1,1,0]
	v_pk_fma_f32 v[80:81], v[92:93], v[108:109], v[80:81] op_sel_hi:[1,1,0]
	ds_read_b128 v[106:109], v139 offset:45056
	v_mul_f32_e32 v69, v64, v116
	v_mul_f32_e32 v71, v65, v117
	v_mov_b32_e32 v73, v69
	v_mov_b32_e32 v81, v71
	v_pk_add_f32 v[72:73], v[72:73], v[80:81]
	s_waitcnt lgkmcnt(0)
	v_mul_f32_e32 v57, v99, v107
	v_pk_add_f32 v[80:81], v[66:67], v[72:73]
	v_pk_add_f32 v[66:67], v[76:77], v[76:77] op_sel:[0,1] op_sel_hi:[1,0]
	v_mul_f32_e32 v75, v98, v106
	v_mov_b32_e32 v67, v57
	v_pk_add_f32 v[66:67], v[74:75], v[66:67]
	v_mul_f32_e32 v72, v91, v111
	v_mul_f32_e32 v74, v93, v113
	v_mul_f32_e32 v69, v64, v108
	v_mul_f32_e32 v71, v65, v109
	v_pk_fma_f32 v[72:73], v[90:91], v[110:111], v[72:73] op_sel_hi:[1,1,0]
	v_pk_fma_f32 v[74:75], v[92:93], v[112:113], v[74:75] op_sel_hi:[1,1,0]
	v_mov_b32_e32 v73, v69
	v_mov_b32_e32 v75, v71
	v_pk_add_f32 v[72:73], v[72:73], v[74:75]
	s_nop 0
	v_pk_add_f32 v[76:77], v[66:67], v[72:73]
	ds_read_b128 v[72:75], v139 offset:53248
	v_pk_add_f32 v[66:67], v[104:105], v[104:105] op_sel:[0,1] op_sel_hi:[1,0]
	s_waitcnt lgkmcnt(0)
	v_mul_f32_e32 v57, v99, v73
	v_mul_f32_e32 v71, v98, v72
	v_mov_b32_e32 v67, v57
	v_pk_add_f32 v[66:67], v[70:71], v[66:67]
	v_mul_f32_e32 v70, v91, v21
	v_pk_fma_f32 v[20:21], v[90:91], v[20:21], v[70:71] op_sel_hi:[1,1,0]
	v_mul_f32_e32 v70, v93, v23
	v_mul_f32_e32 v69, v64, v74
	v_mul_f32_e32 v72, v65, v75
	v_pk_fma_f32 v[22:23], v[92:93], v[22:23], v[70:71] op_sel_hi:[1,1,0]
	v_mov_b32_e32 v21, v69
	v_mov_b32_e32 v23, v72
	v_pk_add_f32 v[20:21], v[20:21], v[22:23]
	s_nop 0
	v_pk_add_f32 v[74:75], v[66:67], v[20:21]
	ds_read_b128 v[20:23], v139 offset:61440
	s_waitcnt lgkmcnt(0)
	v_mul_f32_e32 v66, v64, v22
	v_mul_f32_e32 v23, v65, v23
	v_mul_f32_e32 v22, v91, v17
	v_pk_fma_f32 v[16:17], v[90:91], v[16:17], v[22:23] op_sel_hi:[1,1,0]
	v_mul_f32_e32 v22, v93, v19
	v_mul_f32_e32 v87, v98, v20
	v_mul_f32_e32 v57, v99, v21
	v_pk_add_f32 v[20:21], v[102:103], v[102:103] op_sel:[0,1] op_sel_hi:[1,0]
	v_pk_fma_f32 v[18:19], v[92:93], v[18:19], v[22:23] op_sel_hi:[1,1,0]
	v_mov_b32_e32 v21, v57
	v_mov_b32_e32 v17, v66
	v_mov_b32_e32 v19, v23
	v_pk_add_f32 v[20:21], v[86:87], v[20:21]
	v_pk_add_f32 v[16:17], v[16:17], v[18:19]
	v_pk_mul_f32 v[50:51], v[50:51], v[56:57] op_sel_hi:[1,0]
	v_pk_add_f32 v[72:73], v[20:21], v[16:17]
	ds_read_b128 v[16:19], v144 offset:32768
	v_pk_mul_f32 v[48:49], v[48:49], v[56:57] op_sel_hi:[1,0]
	s_waitcnt lgkmcnt(0)
	v_mul_f32_e32 v21, v64, v18
	v_mul_f32_e32 v19, v65, v19
	v_mul_f32_e32 v18, v91, v13
	v_pk_fma_f32 v[12:13], v[90:91], v[12:13], v[18:19] op_sel_hi:[1,1,0]
	v_mul_f32_e32 v18, v93, v15
	v_mul_f32_e32 v69, v98, v16
	v_mul_f32_e32 v20, v99, v17
	v_pk_add_f32 v[16:17], v[100:101], v[100:101] op_sel:[0,1] op_sel_hi:[1,0]
	v_pk_fma_f32 v[14:15], v[92:93], v[14:15], v[18:19] op_sel_hi:[1,1,0]
	v_mov_b32_e32 v17, v20
	v_mov_b32_e32 v13, v21
	v_mov_b32_e32 v15, v19
	v_pk_add_f32 v[16:17], v[68:69], v[16:17]
	v_pk_add_f32 v[12:13], v[12:13], v[14:15]
	s_nop 0
	v_pk_add_f32 v[70:71], v[16:17], v[12:13]
	ds_read_b128 v[12:15], v144 offset:40960
	s_waitcnt lgkmcnt(0)
	v_mul_f32_e32 v17, v64, v14
	v_mul_f32_e32 v15, v65, v15
	v_mul_f32_e32 v14, v91, v9
	v_pk_fma_f32 v[8:9], v[90:91], v[8:9], v[14:15] op_sel_hi:[1,1,0]
	v_mul_f32_e32 v14, v93, v11
	v_mul_f32_e32 v85, v98, v12
	v_mul_f32_e32 v16, v99, v13
	v_pk_add_f32 v[12:13], v[96:97], v[96:97] op_sel:[0,1] op_sel_hi:[1,0]
	v_pk_fma_f32 v[10:11], v[92:93], v[10:11], v[14:15] op_sel_hi:[1,1,0]
	v_mov_b32_e32 v13, v16
	v_mov_b32_e32 v9, v17
	v_mov_b32_e32 v11, v15
	v_pk_add_f32 v[12:13], v[84:85], v[12:13]
	v_pk_add_f32 v[8:9], v[8:9], v[10:11]
	s_nop 0
	v_pk_add_f32 v[68:69], v[12:13], v[8:9]
	ds_read_b128 v[8:11], v144 offset:49152
	s_waitcnt lgkmcnt(0)
	v_mul_f32_e32 v13, v64, v10
	v_mul_f32_e32 v11, v65, v11
	v_mul_f32_e32 v10, v91, v5
	v_pk_fma_f32 v[4:5], v[90:91], v[4:5], v[10:11] op_sel_hi:[1,1,0]
	v_mul_f32_e32 v10, v93, v7
	v_mul_f32_e32 v79, v98, v8
	v_mul_f32_e32 v12, v99, v9
	v_pk_add_f32 v[8:9], v[94:95], v[94:95] op_sel:[0,1] op_sel_hi:[1,0]
	v_pk_fma_f32 v[6:7], v[92:93], v[6:7], v[10:11] op_sel_hi:[1,1,0]
	v_mov_b32_e32 v9, v12
	v_mov_b32_e32 v5, v13
	v_mov_b32_e32 v7, v11
	v_pk_add_f32 v[8:9], v[78:79], v[8:9]
	v_pk_add_f32 v[4:5], v[4:5], v[6:7]
	v_pk_mul_f32 v[10:11], v[62:63], v[56:57] op_sel_hi:[1,0]
	v_pk_add_f32 v[66:67], v[8:9], v[4:5]
	ds_read_b128 v[4:7], v144 offset:57344
	s_waitcnt lgkmcnt(0)
	v_mul_f32_e32 v9, v64, v6
	v_mul_f32_e32 v7, v65, v7
	v_mul_f32_e32 v6, v91, v1
	v_pk_fma_f32 v[0:1], v[90:91], v[0:1], v[6:7] op_sel_hi:[1,1,0]
	v_mul_f32_e32 v6, v93, v3
	v_mul_f32_e32 v83, v98, v4
	v_mul_f32_e32 v8, v99, v5
	v_pk_add_f32 v[4:5], v[88:89], v[88:89] op_sel:[0,1] op_sel_hi:[1,0]
	v_pk_fma_f32 v[2:3], v[92:93], v[2:3], v[6:7] op_sel_hi:[1,1,0]
	v_mov_b32_e32 v5, v8
	v_mov_b32_e32 v1, v9
	v_mov_b32_e32 v3, v7
	v_pk_add_f32 v[4:5], v[82:83], v[4:5]
	v_pk_add_f32 v[0:1], v[0:1], v[2:3]
	s_nop 0
	v_pk_add_f32 v[64:65], v[4:5], v[0:1]
	ds_read_b128 v[2:5], v139 offset:5120
	ds_read_b128 v[6:9], v139 offset:21504
	v_pk_mul_f32 v[0:1], v[60:61], v[56:57] op_sel_hi:[1,0]
	s_waitcnt lgkmcnt(0)
	v_pk_fma_f32 v[2:3], v[10:11], v[2:3], v[6:7]
	v_pk_fma_f32 v[0:1], v[0:1], v[4:5], v[8:9]
	v_and_b32_sdwa v5, v2, v214 dst_sel:DWORD dst_unused:UNUSED_PAD src0_sel:WORD_1 src1_sel:DWORD
	v_add3_u32 v6, v2, v5, s33
	v_and_b32_sdwa v5, v1, v214 dst_sel:DWORD dst_unused:UNUSED_PAD src0_sel:WORD_1 src1_sel:DWORD
	v_and_b32_sdwa v7, v3, v214 dst_sel:DWORD dst_unused:UNUSED_PAD src0_sel:WORD_1 src1_sel:DWORD
	v_and_b32_sdwa v4, v0, v214 dst_sel:DWORD dst_unused:UNUSED_PAD src0_sel:WORD_1 src1_sel:DWORD
	v_add3_u32 v5, v1, v5, s33
	v_add3_u32 v7, v3, v7, s33
	v_add3_u32 v4, v0, v4, s33
	v_and_b32_e32 v5, 0xffff0000, v5
	v_and_b32_e32 v7, 0xffff0000, v7
	v_or_b32_sdwa v5, v5, v4 dst_sel:DWORD dst_unused:UNUSED_PAD src0_sel:DWORD src1_sel:WORD_1
	v_or_b32_sdwa v4, v7, v6 dst_sel:DWORD dst_unused:UNUSED_PAD src0_sel:DWORD src1_sel:WORD_1
	global_store_dwordx2 v[58:59], v[4:5], off offset:2560 sc1
	ds_read_b128 v[4:7], v139 offset:37888
	v_pk_mul_f32 v[10:11], v[52:53], v[56:57] op_sel_hi:[1,0]
	s_waitcnt lgkmcnt(0)
	v_pk_mul_f32 v[4:5], v[2:3], v[4:5]
	v_pk_mul_f32 v[6:7], v[0:1], v[6:7]
	s_nop 0
	v_pk_mov_b32 v[8:9], v[4:5], v[6:7] op_sel:[1,0]
	v_mov_b32_e32 v5, v7
	v_pk_add_f32 v[90:91], v[8:9], v[4:5]
	ds_read_b128 v[4:7], v139 offset:46080
	s_waitcnt lgkmcnt(0)
	v_pk_mul_f32 v[4:5], v[2:3], v[4:5]
	v_pk_mul_f32 v[6:7], v[0:1], v[6:7]
	s_nop 0
	v_pk_mov_b32 v[8:9], v[4:5], v[6:7] op_sel:[1,0]
	v_mov_b32_e32 v5, v7
	v_pk_add_f32 v[88:89], v[8:9], v[4:5]
	ds_read_b128 v[4:7], v139 offset:54272
	s_waitcnt lgkmcnt(0)
	v_pk_mul_f32 v[4:5], v[2:3], v[4:5]
	v_pk_mul_f32 v[6:7], v[0:1], v[6:7]
	s_nop 0
	v_pk_mov_b32 v[8:9], v[4:5], v[6:7] op_sel:[1,0]
	v_mov_b32_e32 v5, v7
	v_pk_add_f32 v[86:87], v[8:9], v[4:5]
	ds_read_b128 v[4:7], v139 offset:62464
	s_waitcnt lgkmcnt(0)
	v_pk_mul_f32 v[4:5], v[2:3], v[4:5]
	v_pk_mul_f32 v[6:7], v[0:1], v[6:7]
	s_nop 0
	v_pk_mov_b32 v[8:9], v[4:5], v[6:7] op_sel:[1,0]
	v_mov_b32_e32 v5, v7
	v_pk_add_f32 v[84:85], v[8:9], v[4:5]
	ds_read_b128 v[4:7], v145 offset:32768
	s_waitcnt lgkmcnt(0)
	v_pk_mul_f32 v[4:5], v[2:3], v[4:5]
	v_pk_mul_f32 v[6:7], v[0:1], v[6:7]
	s_nop 0
	v_pk_mov_b32 v[8:9], v[4:5], v[6:7] op_sel:[1,0]
	v_mov_b32_e32 v5, v7
	v_pk_add_f32 v[82:83], v[8:9], v[4:5]
	ds_read_b128 v[4:7], v145 offset:40960
	s_waitcnt lgkmcnt(0)
	v_pk_mul_f32 v[4:5], v[2:3], v[4:5]
	v_pk_mul_f32 v[6:7], v[0:1], v[6:7]
	s_nop 0
	v_pk_mov_b32 v[8:9], v[4:5], v[6:7] op_sel:[1,0]
	v_mov_b32_e32 v5, v7
	v_pk_add_f32 v[78:79], v[8:9], v[4:5]
	ds_read_b128 v[4:7], v145 offset:49152
	s_waitcnt lgkmcnt(0)
	v_pk_mul_f32 v[4:5], v[2:3], v[4:5]
	v_pk_mul_f32 v[6:7], v[0:1], v[6:7]
	s_nop 0
	v_pk_mov_b32 v[8:9], v[4:5], v[6:7] op_sel:[1,0]
	v_mov_b32_e32 v5, v7
	v_pk_add_f32 v[62:63], v[8:9], v[4:5]
	ds_read_b128 v[4:7], v145 offset:57344
	v_pk_mul_f32 v[8:9], v[54:55], v[56:57] op_sel_hi:[1,0]
	s_waitcnt lgkmcnt(0)
	v_pk_mul_f32 v[2:3], v[2:3], v[4:5]
	v_pk_mul_f32 v[0:1], v[0:1], v[6:7]
	s_nop 0
	v_pk_mov_b32 v[4:5], v[2:3], v[0:1] op_sel:[1,0]
	v_mov_b32_e32 v3, v1
	v_pk_add_f32 v[60:61], v[4:5], v[2:3]
	ds_read_b128 v[0:3], v139 offset:6144
	ds_read_b128 v[4:7], v139 offset:22528
	s_waitcnt lgkmcnt(0)
	v_pk_fma_f32 v[52:53], v[10:11], v[0:1], v[4:5]
	v_pk_fma_f32 v[54:55], v[8:9], v[2:3], v[6:7]
	v_and_b32_sdwa v1, v52, v214 dst_sel:DWORD dst_unused:UNUSED_PAD src0_sel:WORD_1 src1_sel:DWORD
	v_add3_u32 v2, v52, v1, s33
	v_and_b32_sdwa v1, v55, v214 dst_sel:DWORD dst_unused:UNUSED_PAD src0_sel:WORD_1 src1_sel:DWORD
	v_and_b32_sdwa v3, v53, v214 dst_sel:DWORD dst_unused:UNUSED_PAD src0_sel:WORD_1 src1_sel:DWORD
	v_and_b32_sdwa v0, v54, v214 dst_sel:DWORD dst_unused:UNUSED_PAD src0_sel:WORD_1 src1_sel:DWORD
	v_add3_u32 v1, v55, v1, s33
	v_add3_u32 v3, v53, v3, s33
	v_add3_u32 v0, v54, v0, s33
	v_and_b32_e32 v1, 0xffff0000, v1
	v_and_b32_e32 v3, 0xffff0000, v3
	v_or_b32_sdwa v1, v1, v0 dst_sel:DWORD dst_unused:UNUSED_PAD src0_sel:DWORD src1_sel:WORD_1
	v_or_b32_sdwa v0, v3, v2 dst_sel:DWORD dst_unused:UNUSED_PAD src0_sel:DWORD src1_sel:WORD_1
	global_store_dwordx2 v[58:59], v[0:1], off offset:3072 sc1
	ds_read_b128 v[92:95], v139 offset:38912
	ds_read_b128 v[96:99], v139 offset:47104
	ds_read_b128 v[20:23], v139 offset:55296
	ds_read_b128 v[16:19], v139 offset:63488
	ds_read_b128 v[12:15], v146 offset:32768
	ds_read_b128 v[8:11], v146 offset:40960
	ds_read_b128 v[4:7], v146 offset:49152
	ds_read_b128 v[0:3], v146 offset:57344
	ds_read_b128 v[100:103], v139 offset:7168
	ds_read_b128 v[104:107], v139 offset:23552
	s_waitcnt lgkmcnt(0)
	v_pk_fma_f32 v[50:51], v[50:51], v[100:101], v[104:105]
	v_pk_fma_f32 v[48:49], v[48:49], v[102:103], v[106:107]
	v_and_b32_sdwa v57, v50, v214 dst_sel:DWORD dst_unused:UNUSED_PAD src0_sel:WORD_1 src1_sel:DWORD
	v_add3_u32 v100, v50, v57, s33
	v_and_b32_sdwa v57, v49, v214 dst_sel:DWORD dst_unused:UNUSED_PAD src0_sel:WORD_1 src1_sel:DWORD
	v_and_b32_sdwa v101, v51, v214 dst_sel:DWORD dst_unused:UNUSED_PAD src0_sel:WORD_1 src1_sel:DWORD
	v_and_b32_sdwa v56, v48, v214 dst_sel:DWORD dst_unused:UNUSED_PAD src0_sel:WORD_1 src1_sel:DWORD
	v_add3_u32 v57, v49, v57, s33
	v_add3_u32 v101, v51, v101, s33
	v_add3_u32 v56, v48, v56, s33
	v_and_b32_e32 v57, 0xffff0000, v57
	v_and_b32_e32 v101, 0xffff0000, v101
	v_or_b32_sdwa v57, v57, v56 dst_sel:DWORD dst_unused:UNUSED_PAD src0_sel:DWORD src1_sel:WORD_1
	v_or_b32_sdwa v56, v101, v100 dst_sel:DWORD dst_unused:UNUSED_PAD src0_sel:DWORD src1_sel:WORD_1
	global_store_dwordx2 v[58:59], v[56:57], off offset:3584 sc1
	ds_read_b128 v[56:59], v139 offset:39936
	s_waitcnt lgkmcnt(0)
	v_mul_f32_e32 v100, v50, v56
	v_mul_f32_e32 v101, v51, v57
	v_mul_f32_e32 v102, v48, v58
	v_mul_f32_e32 v103, v49, v59
	v_pk_add_f32 v[56:57], v[80:81], v[80:81] op_sel:[0,1] op_sel_hi:[1,0]
	v_pk_add_f32 v[58:59], v[90:91], v[90:91] op_sel:[0,1] op_sel_hi:[1,0]
	v_mov_b32_e32 v57, v100
	v_mov_b32_e32 v59, v101
	v_pk_add_f32 v[56:57], v[56:57], v[58:59]
	v_mul_f32_e32 v58, v53, v93
	v_pk_fma_f32 v[58:59], v[52:53], v[92:93], v[58:59] op_sel_hi:[1,1,0]
	v_mul_f32_e32 v80, v55, v95
	ds_read_b128 v[90:93], v139 offset:48128
	v_pk_fma_f32 v[80:81], v[54:55], v[94:95], v[80:81] op_sel_hi:[1,1,0]
	v_mov_b32_e32 v59, v102
	v_mov_b32_e32 v81, v103
	v_pk_add_f32 v[58:59], v[58:59], v[80:81]
	s_waitcnt lgkmcnt(0)
	v_mul_f32_e32 v80, v51, v91
	v_pk_add_f32 v[56:57], v[56:57], v[58:59]
	v_pk_add_f32 v[58:59], v[76:77], v[76:77] op_sel:[0,1] op_sel_hi:[1,0]
	v_add_f32_e32 v56, v56, v57
	v_mul_f32_e32 v57, v50, v90
	v_pk_add_f32 v[76:77], v[88:89], v[88:89] op_sel:[0,1] op_sel_hi:[1,0]
	v_mov_b32_e32 v59, v57
	v_mov_b32_e32 v77, v80
	v_pk_add_f32 v[58:59], v[58:59], v[76:77]
	v_mul_f32_e32 v76, v53, v97
	v_mul_f32_e32 v81, v48, v92
	v_pk_fma_f32 v[76:77], v[52:53], v[96:97], v[76:77] op_sel_hi:[1,1,0]
	v_mul_f32_e32 v80, v55, v99
	v_mul_f32_e32 v90, v49, v93
	v_mov_b32_e32 v77, v81
	v_pk_fma_f32 v[80:81], v[54:55], v[98:99], v[80:81] op_sel_hi:[1,1,0]
	s_nop 0
	v_mov_b32_e32 v81, v90
	ds_read_b128 v[88:91], v139 offset:56320
	v_pk_add_f32 v[76:77], v[76:77], v[80:81]
	s_waitcnt lgkmcnt(0)
	v_mul_f32_e32 v80, v48, v90
	v_pk_add_f32 v[58:59], v[58:59], v[76:77]
	v_mul_f32_e32 v76, v50, v88
	v_add_f32_e32 v57, v58, v59
	v_mul_f32_e32 v77, v51, v89
	v_pk_add_f32 v[58:59], v[74:75], v[74:75] op_sel:[0,1] op_sel_hi:[1,0]
	v_pk_add_f32 v[74:75], v[86:87], v[86:87] op_sel:[0,1] op_sel_hi:[1,0]
	v_mov_b32_e32 v59, v76
	v_mov_b32_e32 v75, v77
	v_pk_add_f32 v[58:59], v[58:59], v[74:75]
	v_mul_f32_e32 v74, v53, v21
	v_pk_fma_f32 v[20:21], v[52:53], v[20:21], v[74:75] op_sel_hi:[1,1,0]
	v_mul_f32_e32 v74, v55, v23
	v_pk_fma_f32 v[22:23], v[54:55], v[22:23], v[74:75] op_sel_hi:[1,1,0]
	ds_read_b128 v[74:77], v139 offset:64512
	v_mul_f32_e32 v81, v49, v91
	v_mov_b32_e32 v21, v80
	v_mov_b32_e32 v23, v81
	v_pk_add_f32 v[20:21], v[20:21], v[22:23]
	v_pk_add_f32 v[22:23], v[72:73], v[72:73] op_sel:[0,1] op_sel_hi:[1,0]
	v_pk_add_f32 v[20:21], v[58:59], v[20:21]
	v_pk_add_f32 v[58:59], v[84:85], v[84:85] op_sel:[0,1] op_sel_hi:[1,0]
	v_add_f32_e32 v20, v20, v21
	s_waitcnt lgkmcnt(0)
	v_mul_f32_e32 v21, v50, v74
	v_mul_f32_e32 v74, v51, v75
	v_mov_b32_e32 v23, v21
	v_mov_b32_e32 v59, v74
	v_pk_add_f32 v[22:23], v[22:23], v[58:59]
	v_mul_f32_e32 v58, v53, v17
	v_pk_fma_f32 v[16:17], v[52:53], v[16:17], v[58:59] op_sel_hi:[1,1,0]
	v_mul_f32_e32 v58, v55, v19
	v_mul_f32_e32 v75, v48, v76
	v_mul_f32_e32 v76, v49, v77
	v_pk_fma_f32 v[18:19], v[54:55], v[18:19], v[58:59] op_sel_hi:[1,1,0]
	v_mov_b32_e32 v17, v75
	v_mov_b32_e32 v19, v76
	v_pk_add_f32 v[16:17], v[16:17], v[18:19]
	s_nop 0
	v_pk_add_f32 v[16:17], v[22:23], v[16:17]
	s_nop 0
	v_add_f32_e32 v21, v16, v17
	ds_read_b128 v[16:19], v147 offset:32768
	s_waitcnt lgkmcnt(0)
	v_mul_f32_e32 v22, v50, v16
	v_mul_f32_e32 v23, v51, v17
	v_mul_f32_e32 v58, v48, v18
	v_mul_f32_e32 v59, v49, v19
	v_pk_add_f32 v[16:17], v[70:71], v[70:71] op_sel:[0,1] op_sel_hi:[1,0]
	v_pk_add_f32 v[18:19], v[82:83], v[82:83] op_sel:[0,1] op_sel_hi:[1,0]
	v_mov_b32_e32 v17, v22
	v_mov_b32_e32 v19, v23
	v_pk_add_f32 v[16:17], v[16:17], v[18:19]
	v_mul_f32_e32 v18, v53, v13
	v_pk_fma_f32 v[12:13], v[52:53], v[12:13], v[18:19] op_sel_hi:[1,1,0]
	v_mul_f32_e32 v18, v55, v15
	v_pk_fma_f32 v[14:15], v[54:55], v[14:15], v[18:19] op_sel_hi:[1,1,0]
	v_mov_b32_e32 v13, v58
	v_mov_b32_e32 v15, v59
	v_pk_add_f32 v[12:13], v[12:13], v[14:15]
	s_nop 0
	v_pk_add_f32 v[12:13], v[16:17], v[12:13]
	s_nop 0
	v_add_f32_e32 v16, v12, v13
	ds_read_b128 v[12:15], v147 offset:40960
	s_waitcnt lgkmcnt(0)
	v_mul_f32_e32 v17, v50, v12
	v_mul_f32_e32 v18, v51, v13
	v_mul_f32_e32 v19, v48, v14
	v_mul_f32_e32 v22, v49, v15
	v_pk_add_f32 v[12:13], v[68:69], v[68:69] op_sel:[0,1] op_sel_hi:[1,0]
	v_pk_add_f32 v[14:15], v[78:79], v[78:79] op_sel:[0,1] op_sel_hi:[1,0]
	v_mov_b32_e32 v13, v17
	v_mov_b32_e32 v15, v18
	v_pk_add_f32 v[12:13], v[12:13], v[14:15]
	v_mul_f32_e32 v14, v53, v9
	v_pk_fma_f32 v[8:9], v[52:53], v[8:9], v[14:15] op_sel_hi:[1,1,0]
	v_mul_f32_e32 v14, v55, v11
	v_pk_fma_f32 v[10:11], v[54:55], v[10:11], v[14:15] op_sel_hi:[1,1,0]
	v_mov_b32_e32 v9, v19
	v_mov_b32_e32 v11, v22
	v_pk_add_f32 v[8:9], v[8:9], v[10:11]
	s_nop 0
	v_pk_add_f32 v[8:9], v[12:13], v[8:9]
	s_nop 0
	v_add_f32_e32 v12, v8, v9
	ds_read_b128 v[8:11], v147 offset:49152
	s_waitcnt lgkmcnt(0)
	v_mul_f32_e32 v13, v50, v8
	v_mul_f32_e32 v14, v51, v9
	v_mul_f32_e32 v15, v48, v10
	v_mul_f32_e32 v17, v49, v11
	v_pk_add_f32 v[8:9], v[66:67], v[66:67] op_sel:[0,1] op_sel_hi:[1,0]
	v_pk_add_f32 v[10:11], v[62:63], v[62:63] op_sel:[0,1] op_sel_hi:[1,0]
	v_mov_b32_e32 v9, v13
	v_mov_b32_e32 v11, v14
	v_pk_add_f32 v[8:9], v[8:9], v[10:11]
	v_mul_f32_e32 v10, v53, v5
	v_pk_fma_f32 v[4:5], v[52:53], v[4:5], v[10:11] op_sel_hi:[1,1,0]
	v_mul_f32_e32 v10, v55, v7
	v_pk_fma_f32 v[6:7], v[54:55], v[6:7], v[10:11] op_sel_hi:[1,1,0]
	v_mov_b32_e32 v5, v15
	v_mov_b32_e32 v7, v17
	v_pk_add_f32 v[4:5], v[4:5], v[6:7]
	s_nop 0
	v_pk_add_f32 v[4:5], v[8:9], v[4:5]
	s_nop 0
	v_add_f32_e32 v8, v4, v5
	ds_read_b128 v[4:7], v147 offset:57344
	s_waitcnt lgkmcnt(0)
	v_mul_f32_e32 v9, v50, v4
	v_mul_f32_e32 v10, v51, v5
	v_mul_f32_e32 v11, v48, v6
	v_mul_f32_e32 v13, v49, v7
	v_pk_add_f32 v[4:5], v[64:65], v[64:65] op_sel:[0,1] op_sel_hi:[1,0]
	v_pk_add_f32 v[6:7], v[60:61], v[60:61] op_sel:[0,1] op_sel_hi:[1,0]
	v_mov_b32_e32 v5, v9
	v_mov_b32_e32 v7, v10
	v_pk_add_f32 v[4:5], v[4:5], v[6:7]
	v_mul_f32_e32 v6, v53, v1
	v_pk_fma_f32 v[0:1], v[52:53], v[0:1], v[6:7] op_sel_hi:[1,1,0]
	v_mul_f32_e32 v6, v55, v3
	v_pk_fma_f32 v[2:3], v[54:55], v[2:3], v[6:7] op_sel_hi:[1,1,0]
	v_mov_b32_e32 v1, v11
	v_mov_b32_e32 v3, v13
	v_pk_add_f32 v[0:1], v[0:1], v[2:3]
	s_nop 0
	v_pk_add_f32 v[0:1], v[4:5], v[0:1]
	s_nop 0
	v_add_f32_e32 v6, v0, v1
	v_add_f32_dpp v0, v56, v56 quad_perm:[1,0,3,2] row_mask:0xf bank_mask:0xf bound_ctrl:1
	s_nop 1
	v_add_f32_dpp v0, v0, v0 quad_perm:[2,3,0,1] row_mask:0xf bank_mask:0xf bound_ctrl:1
	s_nop 1
	v_add_f32_dpp v0, v0, v0 row_half_mirror row_mask:0xf bank_mask:0xf bound_ctrl:1
	s_nop 1
	v_add_f32_dpp v0, v0, v0 row_mirror row_mask:0xf bank_mask:0xf bound_ctrl:1
	ds_swizzle_b32 v1, v0 offset:swizzle(SWAP,16)
	s_waitcnt lgkmcnt(0)
	v_add_f32_e32 v1, v0, v1
	v_add_f32_dpp v0, v57, v57 quad_perm:[1,0,3,2] row_mask:0xf bank_mask:0xf bound_ctrl:1
	v_mov_b32_e32 v3, v1
	s_nop 1
	v_permlane32_swap_b32_e32 v1, v3
	v_add_f32_dpp v0, v0, v0 quad_perm:[2,3,0,1] row_mask:0xf bank_mask:0xf bound_ctrl:1
	s_nop 1
	v_add_f32_dpp v0, v0, v0 row_half_mirror row_mask:0xf bank_mask:0xf bound_ctrl:1
	s_nop 1
	v_add_f32_dpp v0, v0, v0 row_mirror row_mask:0xf bank_mask:0xf bound_ctrl:1
	ds_swizzle_b32 v2, v0 offset:swizzle(SWAP,16)
	s_waitcnt lgkmcnt(0)
	v_add_f32_e32 v0, v0, v2
	v_mov_b32_e32 v2, v0
	s_nop 1
	v_permlane32_swap_b32_e32 v0, v2
	v_pk_add_f32 v[4:5], v[0:1], v[2:3]
	s_nop 0
	v_add_f32_dpp v0, v20, v20 quad_perm:[1,0,3,2] row_mask:0xf bank_mask:0xf bound_ctrl:1
	v_cmp_gt_f32_e32 vcc, v4, v5
	v_cmp_nlt_f32_e64 s[46:47], s16, v5
	v_add_f32_dpp v0, v0, v0 quad_perm:[2,3,0,1] row_mask:0xf bank_mask:0xf bound_ctrl:1
	v_cndmask_b32_e64 v3, 0, 1, vcc
	s_nop 0
	v_add_f32_dpp v0, v0, v0 row_half_mirror row_mask:0xf bank_mask:0xf bound_ctrl:1
	s_nop 1
	v_add_f32_dpp v0, v0, v0 row_mirror row_mask:0xf bank_mask:0xf bound_ctrl:1
	ds_swizzle_b32 v1, v0 offset:swizzle(SWAP,16)
	s_waitcnt lgkmcnt(0)
	v_add_f32_e32 v0, v0, v1
	v_mov_b32_e32 v1, v0
	s_nop 1
	v_permlane32_swap_b32_e32 v0, v1
	v_add_f32_e32 v2, v0, v1
	s_nop 0
	v_add_f32_dpp v0, v21, v21 quad_perm:[1,0,3,2] row_mask:0xf bank_mask:0xf bound_ctrl:1
	s_nop 1
	v_add_f32_dpp v0, v0, v0 quad_perm:[2,3,0,1] row_mask:0xf bank_mask:0xf bound_ctrl:1
	s_nop 1
	v_add_f32_dpp v0, v0, v0 row_half_mirror row_mask:0xf bank_mask:0xf bound_ctrl:1
	s_nop 1
	v_add_f32_dpp v0, v0, v0 row_mirror row_mask:0xf bank_mask:0xf bound_ctrl:1
	ds_swizzle_b32 v1, v0 offset:swizzle(SWAP,16)
	s_waitcnt lgkmcnt(0)
	v_add_f32_e32 v0, v0, v1
	v_mov_b32_e32 v1, v0
	s_nop 1
	v_permlane32_swap_b32_e32 v0, v1
	v_add_f32_e32 v7, v0, v1
	s_nop 0
	v_add_f32_dpp v0, v16, v16 quad_perm:[1,0,3,2] row_mask:0xf bank_mask:0xf bound_ctrl:1
	s_nop 1
	v_add_f32_dpp v0, v0, v0 quad_perm:[2,3,0,1] row_mask:0xf bank_mask:0xf bound_ctrl:1
	s_nop 1
	v_add_f32_dpp v0, v0, v0 row_half_mirror row_mask:0xf bank_mask:0xf bound_ctrl:1
	s_nop 1
	v_add_f32_dpp v0, v0, v0 row_mirror row_mask:0xf bank_mask:0xf bound_ctrl:1
	ds_swizzle_b32 v1, v0 offset:swizzle(SWAP,16)
	s_waitcnt lgkmcnt(0)
	v_add_f32_e32 v0, v0, v1
	v_mov_b32_e32 v1, v0
	s_nop 1
	v_permlane32_swap_b32_e32 v0, v1
	v_add_f32_e32 v9, v0, v1
	s_nop 0
	v_add_f32_dpp v0, v12, v12 quad_perm:[1,0,3,2] row_mask:0xf bank_mask:0xf bound_ctrl:1
	s_nop 1
	v_add_f32_dpp v0, v0, v0 quad_perm:[2,3,0,1] row_mask:0xf bank_mask:0xf bound_ctrl:1
	s_nop 1
	v_add_f32_dpp v0, v0, v0 row_half_mirror row_mask:0xf bank_mask:0xf bound_ctrl:1
	s_nop 1
	v_add_f32_dpp v0, v0, v0 row_mirror row_mask:0xf bank_mask:0xf bound_ctrl:1
	ds_swizzle_b32 v1, v0 offset:swizzle(SWAP,16)
	s_waitcnt lgkmcnt(0)
	v_add_f32_e32 v0, v0, v1
	v_mov_b32_e32 v1, v0
	s_nop 1
	v_permlane32_swap_b32_e32 v0, v1
	v_add_f32_e32 v10, v0, v1
	s_nop 0
	v_add_f32_dpp v0, v8, v8 quad_perm:[1,0,3,2] row_mask:0xf bank_mask:0xf bound_ctrl:1
	s_nop 1
	v_add_f32_dpp v0, v0, v0 quad_perm:[2,3,0,1] row_mask:0xf bank_mask:0xf bound_ctrl:1
	s_nop 1
	v_add_f32_dpp v0, v0, v0 row_half_mirror row_mask:0xf bank_mask:0xf bound_ctrl:1
	s_nop 1
	v_add_f32_dpp v0, v0, v0 row_mirror row_mask:0xf bank_mask:0xf bound_ctrl:1
	ds_swizzle_b32 v1, v0 offset:swizzle(SWAP,16)
	s_waitcnt lgkmcnt(0)
	v_add_f32_e32 v0, v0, v1
	v_mov_b32_e32 v1, v0
	s_nop 1
	v_permlane32_swap_b32_e32 v0, v1
	v_add_f32_e32 v8, v0, v1
	s_nop 0
	v_add_f32_dpp v0, v6, v6 quad_perm:[1,0,3,2] row_mask:0xf bank_mask:0xf bound_ctrl:1
	s_nop 1
	v_add_f32_dpp v0, v0, v0 quad_perm:[2,3,0,1] row_mask:0xf bank_mask:0xf bound_ctrl:1
	s_nop 1
	v_add_f32_dpp v0, v0, v0 row_half_mirror row_mask:0xf bank_mask:0xf bound_ctrl:1
	s_nop 1
	v_add_f32_dpp v0, v0, v0 row_mirror row_mask:0xf bank_mask:0xf bound_ctrl:1
	ds_swizzle_b32 v1, v0 offset:swizzle(SWAP,16)
	s_waitcnt lgkmcnt(0)
	v_add_f32_e32 v0, v0, v1
	v_mov_b32_e32 v1, v0
	s_nop 1
	v_permlane32_swap_b32_e32 v0, v1
	v_add_f32_e32 v1, v0, v1
	v_cndmask_b32_e32 v0, v5, v4, vcc
	v_cmp_gt_f32_e32 vcc, v2, v0
	s_nop 1
	v_cndmask_b32_e32 v0, v0, v2, vcc
	v_cndmask_b32_e64 v3, v3, 2, vcc
	v_cmp_gt_f32_e32 vcc, v7, v0
	s_nop 1
	v_cndmask_b32_e32 v0, v0, v7, vcc
	v_cndmask_b32_e64 v3, v3, 3, vcc
	v_cmp_gt_f32_e32 vcc, v9, v0
	s_nop 1
	v_cndmask_b32_e32 v0, v0, v9, vcc
	v_cndmask_b32_e64 v3, v3, 4, vcc
	v_cmp_gt_f32_e32 vcc, v10, v0
	s_nop 1
	v_cndmask_b32_e32 v0, v0, v10, vcc
	v_cndmask_b32_e64 v6, v3, 5, vcc
	v_cmp_ngt_f32_e32 vcc, v8, v0
	s_nop 1
	v_cndmask_b32_e32 v3, v8, v0, vcc
	v_cndmask_b32_e32 v0, 6, v6, vcc
	v_cmp_gt_f32_e64 s[42:43], v1, v3
	s_or_b64 s[16:17], vcc, s[42:43]
	v_cmp_ngt_f32_e64 s[40:41], v1, v3
	v_cndmask_b32_e64 v0, v0, 7, s[42:43]
	v_cmp_eq_u32_e64 s[44:45], 0, v0
	s_or_b64 s[44:45], s[44:45], s[46:47]
	s_nop 0
	v_cndmask_b32_e64 v5, v5, v222, s[44:45]
	v_cndmask_b32_e64 v6, 0, -1, s[44:45]
	v_cmp_ne_u32_e64 s[44:45], 1, v0
	v_cmp_gt_f32_e64 s[46:47], v4, v5
	s_and_b64 s[44:45], s[44:45], s[46:47]
	v_cndmask_b32_e64 v4, v5, v4, s[44:45]
	v_cndmask_b32_e64 v5, v6, 1, s[44:45]
	v_cmp_ne_u32_e64 s[44:45], 2, v0
	v_cmp_gt_f32_e64 s[46:47], v2, v4
	s_and_b64 s[44:45], s[44:45], s[46:47]
	v_cndmask_b32_e64 v2, v4, v2, s[44:45]
	v_cndmask_b32_e64 v4, v5, 2, s[44:45]
	v_cmp_ne_u32_e64 s[44:45], 3, v0
	v_cmp_gt_f32_e64 s[46:47], v7, v2
	s_and_b64 s[44:45], s[44:45], s[46:47]
	v_cndmask_b32_e64 v2, v2, v7, s[44:45]
	v_cndmask_b32_e64 v4, v4, 3, s[44:45]
	v_cmp_ne_u32_e64 s[44:45], 4, v0
	v_cmp_gt_f32_e64 s[46:47], v9, v2
	s_and_b64 s[44:45], s[44:45], s[46:47]
	v_cndmask_b32_e64 v2, v2, v9, s[44:45]
	v_cndmask_b32_e64 v4, v4, 4, s[44:45]
	v_cmp_ne_u32_e64 s[44:45], 5, v0
	v_cmp_gt_f32_e64 s[46:47], v10, v2
	s_and_b64 s[44:45], s[44:45], s[46:47]
	v_cndmask_b32_e64 v2, v2, v10, s[44:45]
	v_cmp_gt_f32_e32 vcc, v8, v2
	v_cndmask_b32_e64 v5, v4, 5, s[44:45]
	s_and_b64 vcc, s[16:17], vcc
	v_cndmask_b32_e32 v4, v2, v8, vcc
	v_cndmask_b32_e64 v2, v5, 6, vcc
	s_and_saveexec_b64 s[16:17], s[40:41]
	s_cbranch_execz .LBB0_1229
	v_cmp_gt_f32_e32 vcc, v1, v4
	s_and_saveexec_b64 s[18:19], vcc
	v_mov_b32_e32 v2, 7
	v_mov_b32_e32 v4, v1
	s_or_b64 exec, exec, s[18:19]
	v_mov_b32_e32 v1, v3
.LBB0_1229:
	s_or_b64 exec, exec, s[16:17]
	s_and_saveexec_b64 s[16:17], s[38:39]
	s_cbranch_execz .LBB0_1234
	v_sub_f32_e32 v1, v4, v1
	v_mul_f32_e32 v1, 0x3fb8aa3b, v1
	v_exp_f32_e32 v1, v1
	s_cmp_gt_i32 s4, 31
	v_add_f32_e32 v1, 1.0, v1
	v_div_scale_f32 v3, s[18:19], v1, v1, 1.0
	v_rcp_f32_e32 v4, v3
	v_div_scale_f32 v5, vcc, 1.0, v1, 1.0
	s_mov_b64 s[18:19], -1
	v_fma_f32 v6, -v3, v4, 1.0
	v_fmac_f32_e32 v4, v6, v4
	v_mul_f32_e32 v6, v5, v4
	v_fma_f32 v7, -v3, v6, v5
	v_fmac_f32_e32 v6, v7, v4
	v_fma_f32 v3, -v3, v6, v5
	v_div_fmas_f32 v3, v3, v4, v6
	v_div_fixup_f32 v4, v3, v1, 1.0
	v_sub_f32_e32 v5, 1.0, v4
	s_cbranch_scc0 .LBB0_1232
	v_readlane_b32 s18, v252, 53
	v_lshlrev_b32_e32 v184, 6, v0
	v_readlane_b32 s19, v252, 54
	v_readlane_b32 s20, v250, 0
	v_readlane_b32 s21, v250, 1
	v_lshl_add_u64 v[6:7], v[184:185], 2, s[18:19]
	global_atomic_add v1, v[6:7], v214, off sc0
	v_lshlrev_b32_e32 v6, 6, v2
	v_ashrrev_i32_e32 v7, 31, v6
	v_lshl_add_u64 v[6:7], v[6:7], 2, s[18:19]
	global_atomic_add v3, v[6:7], v214, off sc0
	s_lshl_b64 s[18:19], s[14:15], 4
	s_add_u32 s18, s20, s18
	s_addc_u32 s19, s21, s19
	s_lshl_b64 s[14:15], s[14:15], 3
	s_waitcnt vmcnt(0)
	global_store_dwordx4 v185, v[0:3], s[18:19] sc1
	v_readlane_b32 s18, v250, 2
	v_readlane_b32 s19, v250, 3
	s_add_u32 s14, s18, s14
	s_addc_u32 s15, s19, s15
	global_store_dwordx2 v185, v[4:5], s[14:15] sc1
	s_mov_b64 s[18:19], 0

.LBB0_1235:
	s_andn2_b64 vcc, exec, s[0:1]
	s_cbranch_vccnz .LBB0_1203
	s_waitcnt vmcnt(15)
	v_and_b32_e32 v9, 0xffff0000, v46
	v_and_b32_e32 v11, 0xffff0000, v47
	v_lshlrev_b32_e32 v8, 16, v46
	v_lshlrev_b32_e32 v10, 16, v47
	v_mul_f32_e32 v0, v9, v9
	v_mul_f32_e32 v1, v11, v11
	s_waitcnt vmcnt(14)
	v_and_b32_e32 v63, 0xffff0000, v44
	v_and_b32_e32 v75, 0xffff0000, v45
	v_fmac_f32_e32 v0, v8, v8
	v_fmac_f32_e32 v1, v10, v10
	v_lshlrev_b32_e32 v62, 16, v44
	v_lshlrev_b32_e32 v74, 16, v45
	v_add_f32_e32 v0, v0, v1
	v_mul_f32_e32 v1, v63, v63
	v_mul_f32_e32 v2, v75, v75
	v_fmac_f32_e32 v1, v62, v62
	v_fmac_f32_e32 v2, v74, v74
	s_waitcnt vmcnt(13)
	v_and_b32_e32 v65, 0xffff0000, v42
	v_and_b32_e32 v61, 0xffff0000, v43
	v_add_f32_e32 v1, v1, v2
	v_lshlrev_b32_e32 v64, 16, v42
	v_lshlrev_b32_e32 v60, 16, v43
	v_add_f32_e32 v0, v0, v1
	v_mul_f32_e32 v1, v65, v65
	v_mul_f32_e32 v2, v61, v61
	v_fmac_f32_e32 v1, v64, v64
	v_fmac_f32_e32 v2, v60, v60
	s_waitcnt vmcnt(12)
	v_and_b32_e32 v21, 0xffff0000, v40
	v_and_b32_e32 v23, 0xffff0000, v41
	v_add_f32_e32 v1, v1, v2
	v_lshlrev_b32_e32 v20, 16, v40
	v_lshlrev_b32_e32 v22, 16, v41
	v_add_f32_e32 v0, v0, v1
	v_mul_f32_e32 v1, v21, v21
	v_mul_f32_e32 v2, v23, v23
	v_fmac_f32_e32 v1, v20, v20
	v_fmac_f32_e32 v2, v22, v22
	s_waitcnt vmcnt(11)
	v_and_b32_e32 v51, 0xffff0000, v38
	v_and_b32_e32 v49, 0xffff0000, v39
	v_add_f32_e32 v1, v1, v2
	v_lshlrev_b32_e32 v50, 16, v38
	v_lshlrev_b32_e32 v48, 16, v39
	v_add_f32_e32 v0, v0, v1
	v_mul_f32_e32 v1, v51, v51
	v_mul_f32_e32 v2, v49, v49
	v_fmac_f32_e32 v1, v50, v50
	v_fmac_f32_e32 v2, v48, v48
	s_waitcnt vmcnt(10)
	v_and_b32_e32 v47, 0xffff0000, v36
	v_and_b32_e32 v45, 0xffff0000, v37
	v_add_f32_e32 v1, v1, v2
	v_lshlrev_b32_e32 v46, 16, v36
	v_lshlrev_b32_e32 v44, 16, v37
	v_add_f32_e32 v0, v0, v1
	v_mul_f32_e32 v1, v47, v47
	v_mul_f32_e32 v2, v45, v45
	v_fmac_f32_e32 v1, v46, v46
	v_fmac_f32_e32 v2, v44, v44
	s_waitcnt vmcnt(9)
	v_and_b32_e32 v37, 0xffff0000, v34
	v_and_b32_e32 v39, 0xffff0000, v35
	v_add_f32_e32 v1, v1, v2
	v_lshlrev_b32_e32 v36, 16, v34
	v_lshlrev_b32_e32 v38, 16, v35
	v_add_f32_e32 v0, v0, v1
	v_mul_f32_e32 v1, v37, v37
	v_mul_f32_e32 v2, v39, v39
	v_fmac_f32_e32 v1, v36, v36
	v_fmac_f32_e32 v2, v38, v38
	s_waitcnt vmcnt(8)
	v_lshlrev_b32_e32 v34, 16, v32
	v_and_b32_e32 v35, 0xffff0000, v32
	v_lshlrev_b32_e32 v32, 16, v33
	v_and_b32_e32 v33, 0xffff0000, v33
	v_add_f32_e32 v1, v1, v2
	v_add_f32_e32 v0, v0, v1
	v_mul_f32_e32 v1, v35, v35
	v_mul_f32_e32 v2, v33, v33
	v_fmac_f32_e32 v1, v34, v34
	v_fmac_f32_e32 v2, v32, v32
	v_add_f32_e32 v1, v1, v2
	v_add_f32_e32 v0, v0, v1
	s_mov_b32 s0, 0xf800000
	v_lshl_add_u64 v[42:43], v[28:29], 0, s[12:13]
	v_add_f32_dpp v0, v0, v0 quad_perm:[1,0,3,2] row_mask:0xf bank_mask:0xf bound_ctrl:1
	s_nop 1
	v_add_f32_dpp v0, v0, v0 quad_perm:[2,3,0,1] row_mask:0xf bank_mask:0xf bound_ctrl:1
	s_nop 1
	v_add_f32_dpp v0, v0, v0 row_half_mirror row_mask:0xf bank_mask:0xf bound_ctrl:1
	s_nop 1
	v_add_f32_dpp v0, v0, v0 row_mirror row_mask:0xf bank_mask:0xf bound_ctrl:1
	ds_swizzle_b32 v1, v0 offset:swizzle(SWAP,16)
	s_waitcnt lgkmcnt(0)
	v_add_f32_e32 v0, v0, v1
	v_mov_b32_e32 v1, v0
	s_nop 1
	v_permlane32_swap_b32_e32 v0, v1
	v_add_f32_e32 v0, v0, v1
	v_fmamk_f32 v0, v0, 0x3a000000, v212
	v_cmp_gt_f32_e32 vcc, s0, v0
	v_mul_f32_e32 v1, 0x4f800000, v0
	s_nop 0
	v_cndmask_b32_e32 v0, v0, v1, vcc
	v_sqrt_f32_e32 v1, v0
	s_nop 0
	v_add_u32_e32 v2, -1, v1
	v_fma_f32 v3, -v2, v1, v0
	v_cmp_ge_f32_e64 s[40:41], 0, v3
	v_add_u32_e32 v3, 1, v1
	s_nop 0
	v_cndmask_b32_e64 v2, v1, v2, s[40:41]
	v_fma_f32 v1, -v3, v1, v0
	v_cmp_lt_f32_e64 s[40:41], 0, v1
	s_nop 1
	v_cndmask_b32_e64 v1, v2, v3, s[40:41]
	v_mul_f32_e32 v2, 0x37800000, v1
	v_cndmask_b32_e32 v1, v1, v2, vcc
	v_cmp_class_f32_e32 vcc, v0, v213
	s_nop 1
	v_cndmask_b32_e32 v0, v1, v0, vcc
	v_div_scale_f32 v1, s[0:1], v0, v0, 1.0
	v_rcp_f32_e32 v2, v1
	s_mov_b32 s0, 0xff61b1e6
	v_fma_f32 v3, -v1, v2, 1.0
	v_fmac_f32_e32 v2, v3, v2
	v_div_scale_f32 v3, vcc, 1.0, v0, 1.0
	v_mul_f32_e32 v4, v3, v2
	v_fma_f32 v5, -v1, v4, v3
	v_fmac_f32_e32 v4, v5, v2
	v_fma_f32 v1, -v1, v4, v3
	v_div_fmas_f32 v1, v1, v2, v4
	v_div_fixup_f32 v40, v1, v0, 1.0
	ds_read_b128 v[0:3], v139
	ds_read_b128 v[4:7], v139 offset:16384
	v_pk_mul_f32 v[8:9], v[8:9], v[40:41] op_sel_hi:[1,0]
	v_pk_mul_f32 v[10:11], v[10:11], v[40:41] op_sel_hi:[1,0]
	v_pk_mul_f32 v[62:63], v[62:63], v[40:41] op_sel_hi:[1,0]
	v_pk_mul_f32 v[74:75], v[74:75], v[40:41] op_sel_hi:[1,0]
	s_waitcnt lgkmcnt(0)
	v_pk_fma_f32 v[72:73], v[0:1], v[8:9], v[4:5]
	v_pk_fma_f32 v[66:67], v[2:3], v[10:11], v[6:7]
	v_and_b32_sdwa v1, v72, v214 dst_sel:DWORD dst_unused:UNUSED_PAD src0_sel:WORD_1 src1_sel:DWORD
	v_add3_u32 v2, v72, v1, s33
	v_and_b32_sdwa v1, v67, v214 dst_sel:DWORD dst_unused:UNUSED_PAD src0_sel:WORD_1 src1_sel:DWORD
	v_and_b32_sdwa v3, v73, v214 dst_sel:DWORD dst_unused:UNUSED_PAD src0_sel:WORD_1 src1_sel:DWORD
	v_and_b32_sdwa v0, v66, v214 dst_sel:DWORD dst_unused:UNUSED_PAD src0_sel:WORD_1 src1_sel:DWORD
	v_add3_u32 v1, v67, v1, s33
	v_add3_u32 v3, v73, v3, s33
	v_add3_u32 v0, v66, v0, s33
	v_and_b32_e32 v1, 0xffff0000, v1
	v_and_b32_e32 v3, 0xffff0000, v3
	v_or_b32_sdwa v1, v1, v0 dst_sel:DWORD dst_unused:UNUSED_PAD src0_sel:DWORD src1_sel:WORD_1
	v_or_b32_sdwa v0, v3, v2 dst_sel:DWORD dst_unused:UNUSED_PAD src0_sel:DWORD src1_sel:WORD_1
	global_store_dwordx2 v[42:43], v[0:1], off sc1
	ds_read_b128 v[52:55], v139 offset:32768
	ds_read_b128 v[68:71], v139 offset:40960
	ds_read_b128 v[78:81], v139 offset:49152
	ds_read_b128 v[16:19], v139 offset:57344
	ds_read_b128 v[12:15], v140 offset:32768
	ds_read_b128 v[8:11], v140 offset:40960
	ds_read_b128 v[4:7], v140 offset:49152
	ds_read_b128 v[0:3], v140 offset:57344
	ds_read_b128 v[56:59], v139 offset:1024
	ds_read_b128 v[82:85], v139 offset:17408
	s_waitcnt lgkmcnt(0)
	v_pk_fma_f32 v[74:75], v[74:75], v[58:59], v[84:85]
	v_pk_fma_f32 v[76:77], v[62:63], v[56:57], v[82:83]
	v_and_b32_sdwa v57, v75, v214 dst_sel:DWORD dst_unused:UNUSED_PAD src0_sel:WORD_1 src1_sel:DWORD
	v_and_b32_sdwa v58, v77, v214 dst_sel:DWORD dst_unused:UNUSED_PAD src0_sel:WORD_1 src1_sel:DWORD
	v_and_b32_sdwa v41, v74, v214 dst_sel:DWORD dst_unused:UNUSED_PAD src0_sel:WORD_1 src1_sel:DWORD
	v_and_b32_sdwa v56, v76, v214 dst_sel:DWORD dst_unused:UNUSED_PAD src0_sel:WORD_1 src1_sel:DWORD
	v_add3_u32 v57, v75, v57, s33
	v_add3_u32 v58, v77, v58, s33
	v_add3_u32 v56, v76, v56, s33
	v_add3_u32 v41, v74, v41, s33
	v_and_b32_e32 v57, 0xffff0000, v57
	v_and_b32_e32 v58, 0xffff0000, v58
	v_or_b32_sdwa v57, v57, v41 dst_sel:DWORD dst_unused:UNUSED_PAD src0_sel:DWORD src1_sel:WORD_1
	v_or_b32_sdwa v56, v58, v56 dst_sel:DWORD dst_unused:UNUSED_PAD src0_sel:DWORD src1_sel:WORD_1
	global_store_dwordx2 v[42:43], v[56:57], off offset:512 sc1
	ds_read_b128 v[56:59], v139 offset:33792
	v_mov_b32_e32 v62, v52
	v_mov_b32_e32 v52, v53
	v_mov_b32_e32 v53, v77
	v_mov_b32_e32 v63, v76
	s_waitcnt lgkmcnt(0)
	v_mov_b32_e32 v83, v56
	v_mov_b32_e32 v56, v73
	v_mov_b32_e32 v82, v72
	v_pk_mul_f32 v[52:53], v[52:53], v[56:57]
	v_mov_b32_e32 v56, v54
	v_pk_fma_f32 v[52:53], v[62:63], v[82:83], v[52:53]
	v_mov_b32_e32 v63, v58
	v_mov_b32_e32 v54, v55
	v_mov_b32_e32 v55, v75
	v_mov_b32_e32 v58, v67
	v_mov_b32_e32 v57, v74
	v_mov_b32_e32 v62, v66
	v_pk_mul_f32 v[54:55], v[54:55], v[58:59]
	v_mov_b32_e32 v58, v68
	v_pk_fma_f32 v[54:55], v[56:57], v[62:63], v[54:55]
	v_mov_b32_e32 v68, v69
	v_pk_add_f32 v[52:53], v[52:53], v[54:55]
	v_mov_b32_e32 v69, v77
	v_add_f32_e32 v41, 0, v52
	v_add_f32_e32 v56, v41, v53
	ds_read_b128 v[52:55], v139 offset:41984
	v_mov_b32_e32 v59, v76
	v_mov_b32_e32 v62, v72
	s_waitcnt lgkmcnt(0)
	v_mov_b32_e32 v63, v52
	v_mov_b32_e32 v52, v73
	v_pk_mul_f32 v[52:53], v[68:69], v[52:53]
	v_mov_b32_e32 v68, v71
	v_pk_fma_f32 v[52:53], v[58:59], v[62:63], v[52:53]
	v_mov_b32_e32 v63, v54
	v_mov_b32_e32 v69, v75
	v_mov_b32_e32 v54, v67
	v_mov_b32_e32 v58, v70
	v_mov_b32_e32 v59, v74
	v_mov_b32_e32 v62, v66
	v_pk_mul_f32 v[54:55], v[68:69], v[54:55]
	v_mov_b32_e32 v70, v79
	v_pk_fma_f32 v[54:55], v[58:59], v[62:63], v[54:55]
	v_mov_b32_e32 v71, v77
	v_pk_add_f32 v[52:53], v[52:53], v[54:55]
	v_mov_b32_e32 v62, v78
	v_add_f32_e32 v41, 0, v52
	v_add_f32_e32 v58, v41, v53
	ds_read_b128 v[52:55], v139 offset:50176
	v_mov_b32_e32 v63, v76
	v_mov_b32_e32 v68, v72
	s_waitcnt lgkmcnt(0)
	v_mov_b32_e32 v69, v52
	v_mov_b32_e32 v52, v73
	v_pk_mul_f32 v[52:53], v[70:71], v[52:53]
	v_mov_b32_e32 v70, v81
	v_pk_fma_f32 v[52:53], v[62:63], v[68:69], v[52:53]
	v_mov_b32_e32 v69, v54
	v_mov_b32_e32 v71, v75
	v_mov_b32_e32 v54, v67
	v_mov_b32_e32 v62, v80
	v_mov_b32_e32 v63, v74
	v_mov_b32_e32 v68, v66
	v_pk_mul_f32 v[54:55], v[70:71], v[54:55]
	s_nop 0
	v_pk_fma_f32 v[54:55], v[62:63], v[68:69], v[54:55]
	ds_read_b128 v[68:71], v139 offset:58368
	v_pk_add_f32 v[52:53], v[52:53], v[54:55]
	v_mov_b32_e32 v62, v72
	v_add_f32_e32 v41, 0, v52
	v_mov_b32_e32 v52, v16
	s_waitcnt lgkmcnt(0)
	v_mov_b32_e32 v63, v68
	v_mov_b32_e32 v16, v17
	v_mov_b32_e32 v17, v77
	v_mov_b32_e32 v68, v73
	v_add_f32_e32 v54, v41, v53
	v_mov_b32_e32 v53, v76
	v_pk_mul_f32 v[16:17], v[16:17], v[68:69]
	v_pk_mul_f32 v[50:51], v[50:51], v[40:41] op_sel_hi:[1,0]
	v_pk_fma_f32 v[16:17], v[52:53], v[62:63], v[16:17]
	v_mov_b32_e32 v52, v18
	v_mov_b32_e32 v63, v70
	v_mov_b32_e32 v18, v19
	v_mov_b32_e32 v19, v75
	v_mov_b32_e32 v70, v67
	v_mov_b32_e32 v53, v74
	v_mov_b32_e32 v62, v66
	v_pk_mul_f32 v[18:19], v[18:19], v[70:71]
	v_pk_mul_f32 v[48:49], v[48:49], v[40:41] op_sel_hi:[1,0]
	v_pk_fma_f32 v[18:19], v[52:53], v[62:63], v[18:19]
	v_mov_b32_e32 v52, v12
	v_pk_add_f32 v[16:17], v[16:17], v[18:19]
	v_mov_b32_e32 v12, v13
	v_add_f32_e32 v16, 0, v16
	v_add_f32_e32 v70, v16, v17
	ds_read_b128 v[16:19], v141 offset:32768
	v_mov_b32_e32 v13, v77
	v_mov_b32_e32 v53, v76
	v_mov_b32_e32 v62, v72
	s_waitcnt lgkmcnt(0)
	v_mov_b32_e32 v63, v16
	v_mov_b32_e32 v16, v73
	v_pk_mul_f32 v[12:13], v[12:13], v[16:17]
	v_mov_b32_e32 v16, v14
	v_pk_fma_f32 v[12:13], v[52:53], v[62:63], v[12:13]
	v_mov_b32_e32 v53, v18
	v_mov_b32_e32 v14, v15
	v_mov_b32_e32 v15, v75
	v_mov_b32_e32 v18, v67
	v_mov_b32_e32 v17, v74
	v_mov_b32_e32 v52, v66
	v_pk_mul_f32 v[14:15], v[14:15], v[18:19]
	v_mov_b32_e32 v18, v72
	v_pk_fma_f32 v[14:15], v[16:17], v[52:53], v[14:15]
	v_mov_b32_e32 v16, v8
	v_pk_add_f32 v[12:13], v[12:13], v[14:15]
	v_mov_b32_e32 v8, v9
	v_add_f32_e32 v12, 0, v12
	v_add_f32_e32 v52, v12, v13
	ds_read_b128 v[12:15], v141 offset:40960
	v_mov_b32_e32 v9, v77
	v_mov_b32_e32 v17, v76
	s_waitcnt lgkmcnt(0)
	v_mov_b32_e32 v19, v12
	v_mov_b32_e32 v12, v73
	v_pk_mul_f32 v[8:9], v[8:9], v[12:13]
	v_mov_b32_e32 v12, v10
	v_pk_fma_f32 v[8:9], v[16:17], v[18:19], v[8:9]
	v_mov_b32_e32 v17, v14
	v_mov_b32_e32 v10, v11
	v_mov_b32_e32 v11, v75
	v_mov_b32_e32 v14, v67
	v_mov_b32_e32 v13, v74
	v_mov_b32_e32 v16, v66
	v_pk_mul_f32 v[10:11], v[10:11], v[14:15]
	v_mov_b32_e32 v14, v72
	v_pk_fma_f32 v[10:11], v[12:13], v[16:17], v[10:11]
	v_mov_b32_e32 v12, v4
	v_pk_add_f32 v[8:9], v[8:9], v[10:11]
	v_mov_b32_e32 v4, v5
	v_add_f32_e32 v8, 0, v8
	v_add_f32_e32 v68, v8, v9
	ds_read_b128 v[8:11], v141 offset:49152
	v_mov_b32_e32 v5, v77
	v_mov_b32_e32 v13, v76
	s_waitcnt lgkmcnt(0)
	v_mov_b32_e32 v15, v8
	v_mov_b32_e32 v8, v73
	v_pk_mul_f32 v[4:5], v[4:5], v[8:9]
	v_mov_b32_e32 v8, v6
	v_pk_fma_f32 v[4:5], v[12:13], v[14:15], v[4:5]
	v_mov_b32_e32 v13, v10
	v_mov_b32_e32 v6, v7
	v_mov_b32_e32 v7, v75
	v_mov_b32_e32 v10, v67
	v_mov_b32_e32 v9, v74
	v_mov_b32_e32 v12, v66
	v_pk_mul_f32 v[6:7], v[6:7], v[10:11]
	v_mov_b32_e32 v10, v72
	v_pk_fma_f32 v[6:7], v[8:9], v[12:13], v[6:7]
	v_mov_b32_e32 v9, v76
	v_pk_add_f32 v[4:5], v[4:5], v[6:7]
	v_mov_b32_e32 v76, v1
	v_add_f32_e32 v4, 0, v4
	v_add_f32_e32 v62, v4, v5
	ds_read_b128 v[4:7], v141 offset:57344
	v_mov_b32_e32 v8, v0
	s_waitcnt lgkmcnt(0)
	v_mov_b32_e32 v11, v4
	v_mov_b32_e32 v4, v73
	v_pk_mul_f32 v[0:1], v[76:77], v[4:5]
	v_mov_b32_e32 v5, v74
	v_pk_fma_f32 v[0:1], v[8:9], v[10:11], v[0:1]
	v_mov_b32_e32 v9, v6
	v_mov_b32_e32 v74, v3
	v_mov_b32_e32 v6, v67
	v_mov_b32_e32 v4, v2
	v_mov_b32_e32 v8, v66
	v_pk_mul_f32 v[2:3], v[74:75], v[6:7]
	v_pk_mul_f32 v[10:11], v[64:65], v[40:41] op_sel_hi:[1,0]
	v_pk_fma_f32 v[2:3], v[4:5], v[8:9], v[2:3]
	s_nop 0
	v_pk_add_f32 v[0:1], v[0:1], v[2:3]
	ds_read_b128 v[2:5], v139 offset:2048
	ds_read_b128 v[6:9], v139 offset:18432
	v_add_f32_e32 v0, 0, v0
	v_add_f32_e32 v66, v0, v1
	v_pk_mul_f32 v[0:1], v[60:61], v[40:41] op_sel_hi:[1,0]
	s_waitcnt lgkmcnt(0)
	v_pk_fma_f32 v[2:3], v[10:11], v[2:3], v[6:7]
	v_pk_fma_f32 v[0:1], v[0:1], v[4:5], v[8:9]
	v_and_b32_sdwa v5, v2, v214 dst_sel:DWORD dst_unused:UNUSED_PAD src0_sel:WORD_1 src1_sel:DWORD
	v_add3_u32 v6, v2, v5, s33
	v_and_b32_sdwa v5, v1, v214 dst_sel:DWORD dst_unused:UNUSED_PAD src0_sel:WORD_1 src1_sel:DWORD
	v_and_b32_sdwa v7, v3, v214 dst_sel:DWORD dst_unused:UNUSED_PAD src0_sel:WORD_1 src1_sel:DWORD
	v_and_b32_sdwa v4, v0, v214 dst_sel:DWORD dst_unused:UNUSED_PAD src0_sel:WORD_1 src1_sel:DWORD
	v_add3_u32 v5, v1, v5, s33
	v_add3_u32 v7, v3, v7, s33
	v_add3_u32 v4, v0, v4, s33
	v_and_b32_e32 v5, 0xffff0000, v5
	v_and_b32_e32 v7, 0xffff0000, v7
	v_or_b32_sdwa v5, v5, v4 dst_sel:DWORD dst_unused:UNUSED_PAD src0_sel:DWORD src1_sel:WORD_1
	v_or_b32_sdwa v4, v7, v6 dst_sel:DWORD dst_unused:UNUSED_PAD src0_sel:DWORD src1_sel:WORD_1
	global_store_dwordx2 v[42:43], v[4:5], off offset:1024 sc1
	ds_read_b128 v[4:7], v139 offset:34816
	v_pk_mul_f32 v[10:11], v[20:21], v[40:41] op_sel_hi:[1,0]
	s_waitcnt lgkmcnt(0)
	v_pk_mul_f32 v[4:5], v[2:3], v[4:5]
	v_pk_mul_f32 v[6:7], v[0:1], v[6:7]
	s_nop 0
	v_pk_mov_b32 v[8:9], v[4:5], v[6:7] op_sel:[1,0]
	v_mov_b32_e32 v5, v7
	v_pk_add_f32 v[64:65], v[8:9], v[4:5]
	ds_read_b128 v[4:7], v139 offset:43008
	s_waitcnt lgkmcnt(0)
	v_pk_mul_f32 v[4:5], v[2:3], v[4:5]
	v_pk_mul_f32 v[6:7], v[0:1], v[6:7]
	s_nop 0
	v_pk_mov_b32 v[8:9], v[4:5], v[6:7] op_sel:[1,0]
	v_mov_b32_e32 v5, v7
	v_pk_add_f32 v[60:61], v[8:9], v[4:5]
	ds_read_b128 v[4:7], v139 offset:51200
	s_waitcnt lgkmcnt(0)
	v_pk_mul_f32 v[4:5], v[2:3], v[4:5]
	v_pk_mul_f32 v[6:7], v[0:1], v[6:7]
	s_nop 0
	v_pk_mov_b32 v[8:9], v[4:5], v[6:7] op_sel:[1,0]
	v_mov_b32_e32 v5, v7
	v_pk_add_f32 v[88:89], v[8:9], v[4:5]
	ds_read_b128 v[4:7], v139 offset:59392
	s_waitcnt lgkmcnt(0)
	v_pk_mul_f32 v[4:5], v[2:3], v[4:5]
	v_pk_mul_f32 v[6:7], v[0:1], v[6:7]
	s_nop 0
	v_pk_mov_b32 v[8:9], v[4:5], v[6:7] op_sel:[1,0]
	v_mov_b32_e32 v5, v7
	v_pk_add_f32 v[86:87], v[8:9], v[4:5]
	ds_read_b128 v[4:7], v142 offset:32768
	s_waitcnt lgkmcnt(0)
	v_pk_mul_f32 v[4:5], v[2:3], v[4:5]
	v_pk_mul_f32 v[6:7], v[0:1], v[6:7]
	s_nop 0
	v_pk_mov_b32 v[8:9], v[4:5], v[6:7] op_sel:[1,0]
	v_mov_b32_e32 v5, v7
	v_pk_add_f32 v[84:85], v[8:9], v[4:5]
	ds_read_b128 v[4:7], v142 offset:40960
	s_waitcnt lgkmcnt(0)
	v_pk_mul_f32 v[4:5], v[2:3], v[4:5]
	v_pk_mul_f32 v[6:7], v[0:1], v[6:7]
	s_nop 0
	v_pk_mov_b32 v[8:9], v[4:5], v[6:7] op_sel:[1,0]
	v_mov_b32_e32 v5, v7
	v_pk_add_f32 v[80:81], v[8:9], v[4:5]
	ds_read_b128 v[4:7], v142 offset:49152
	s_waitcnt lgkmcnt(0)
	v_pk_mul_f32 v[4:5], v[2:3], v[4:5]
	v_pk_mul_f32 v[6:7], v[0:1], v[6:7]
	s_nop 0
	v_pk_mov_b32 v[8:9], v[4:5], v[6:7] op_sel:[1,0]
	v_mov_b32_e32 v5, v7
	v_pk_add_f32 v[78:79], v[8:9], v[4:5]
	ds_read_b128 v[4:7], v142 offset:57344
	v_pk_mul_f32 v[8:9], v[22:23], v[40:41] op_sel_hi:[1,0]
	s_waitcnt lgkmcnt(0)
	v_pk_mul_f32 v[2:3], v[2:3], v[4:5]
	v_pk_mul_f32 v[0:1], v[0:1], v[6:7]
	s_nop 0
	v_pk_mov_b32 v[4:5], v[2:3], v[0:1] op_sel:[1,0]
	v_mov_b32_e32 v3, v1
	v_pk_add_f32 v[72:73], v[4:5], v[2:3]
	ds_read_b128 v[0:3], v139 offset:3072
	ds_read_b128 v[4:7], v139 offset:19456
	s_waitcnt lgkmcnt(0)
	v_pk_fma_f32 v[74:75], v[10:11], v[0:1], v[4:5]
	v_pk_fma_f32 v[76:77], v[8:9], v[2:3], v[6:7]
	v_and_b32_sdwa v1, v74, v214 dst_sel:DWORD dst_unused:UNUSED_PAD src0_sel:WORD_1 src1_sel:DWORD
	v_add3_u32 v2, v74, v1, s33
	v_and_b32_sdwa v1, v77, v214 dst_sel:DWORD dst_unused:UNUSED_PAD src0_sel:WORD_1 src1_sel:DWORD
	v_and_b32_sdwa v3, v75, v214 dst_sel:DWORD dst_unused:UNUSED_PAD src0_sel:WORD_1 src1_sel:DWORD
	v_and_b32_sdwa v0, v76, v214 dst_sel:DWORD dst_unused:UNUSED_PAD src0_sel:WORD_1 src1_sel:DWORD
	v_add3_u32 v1, v77, v1, s33
	v_add3_u32 v3, v75, v3, s33
	v_add3_u32 v0, v76, v0, s33
	v_and_b32_e32 v1, 0xffff0000, v1
	v_and_b32_e32 v3, 0xffff0000, v3
	v_or_b32_sdwa v1, v1, v0 dst_sel:DWORD dst_unused:UNUSED_PAD src0_sel:DWORD src1_sel:WORD_1
	v_or_b32_sdwa v0, v3, v2 dst_sel:DWORD dst_unused:UNUSED_PAD src0_sel:DWORD src1_sel:WORD_1
	global_store_dwordx2 v[42:43], v[0:1], off offset:1536 sc1
	ds_read_b128 v[90:93], v139 offset:35840
	ds_read_b128 v[94:97], v139 offset:44032
	ds_read_b128 v[20:23], v139 offset:52224
	ds_read_b128 v[16:19], v139 offset:60416
	ds_read_b128 v[12:15], v143 offset:32768
	ds_read_b128 v[8:11], v143 offset:40960
	ds_read_b128 v[4:7], v143 offset:49152
	ds_read_b128 v[0:3], v143 offset:57344
	ds_read_b128 v[98:101], v139 offset:4096
	ds_read_b128 v[102:105], v139 offset:20480
	s_waitcnt lgkmcnt(0)
	v_pk_fma_f32 v[48:49], v[48:49], v[100:101], v[104:105]
	v_pk_fma_f32 v[82:83], v[50:51], v[98:99], v[102:103]
	ds_read_b128 v[98:101], v139 offset:36864
	v_and_b32_sdwa v51, v49, v214 dst_sel:DWORD dst_unused:UNUSED_PAD src0_sel:WORD_1 src1_sel:DWORD
	v_and_b32_sdwa v53, v83, v214 dst_sel:DWORD dst_unused:UNUSED_PAD src0_sel:WORD_1 src1_sel:DWORD
	v_and_b32_sdwa v41, v48, v214 dst_sel:DWORD dst_unused:UNUSED_PAD src0_sel:WORD_1 src1_sel:DWORD
	v_and_b32_sdwa v50, v82, v214 dst_sel:DWORD dst_unused:UNUSED_PAD src0_sel:WORD_1 src1_sel:DWORD
	v_add3_u32 v51, v49, v51, s33
	v_add3_u32 v53, v83, v53, s33
	v_add3_u32 v50, v82, v50, s33
	v_add3_u32 v41, v48, v41, s33
	v_and_b32_e32 v51, 0xffff0000, v51
	v_and_b32_e32 v53, 0xffff0000, v53
	v_or_b32_sdwa v51, v51, v41 dst_sel:DWORD dst_unused:UNUSED_PAD src0_sel:DWORD src1_sel:WORD_1
	v_or_b32_sdwa v50, v53, v50 dst_sel:DWORD dst_unused:UNUSED_PAD src0_sel:DWORD src1_sel:WORD_1
	global_store_dwordx2 v[42:43], v[50:51], off offset:2048 sc1
	s_waitcnt lgkmcnt(0)
	v_mul_f32_e32 v41, v83, v99
	v_pk_add_f32 v[50:51], v[64:65], v[64:65] op_sel:[0,1] op_sel_hi:[1,0]
	v_mul_f32_e32 v57, v82, v98
	v_mov_b32_e32 v51, v41
	v_pk_add_f32 v[50:51], v[56:57], v[50:51]
	v_mul_f32_e32 v56, v75, v91
	v_mul_f32_e32 v64, v77, v93
	v_pk_fma_f32 v[56:57], v[74:75], v[90:91], v[56:57] op_sel_hi:[1,1,0]
	v_pk_fma_f32 v[64:65], v[76:77], v[92:93], v[64:65] op_sel_hi:[1,1,0]
	ds_read_b128 v[90:93], v139 offset:45056
	v_mul_f32_e32 v53, v48, v100
	v_mul_f32_e32 v55, v49, v101
	v_mov_b32_e32 v57, v53
	v_mov_b32_e32 v65, v55
	v_pk_add_f32 v[56:57], v[56:57], v[64:65]
	s_waitcnt lgkmcnt(0)
	v_mul_f32_e32 v41, v83, v91
	v_pk_add_f32 v[64:65], v[50:51], v[56:57]
	v_pk_add_f32 v[50:51], v[60:61], v[60:61] op_sel:[0,1] op_sel_hi:[1,0]
	v_mul_f32_e32 v59, v82, v90
	v_mov_b32_e32 v51, v41
	v_pk_add_f32 v[50:51], v[58:59], v[50:51]
	v_mul_f32_e32 v56, v75, v95
	v_mul_f32_e32 v58, v77, v97
	v_mul_f32_e32 v53, v48, v92
	v_mul_f32_e32 v55, v49, v93
	v_pk_fma_f32 v[56:57], v[74:75], v[94:95], v[56:57] op_sel_hi:[1,1,0]
	v_pk_fma_f32 v[58:59], v[76:77], v[96:97], v[58:59] op_sel_hi:[1,1,0]
	v_mov_b32_e32 v57, v53
	v_mov_b32_e32 v59, v55
	v_pk_add_f32 v[56:57], v[56:57], v[58:59]
	s_nop 0
	v_pk_add_f32 v[60:61], v[50:51], v[56:57]
	ds_read_b128 v[56:59], v139 offset:53248
	v_pk_add_f32 v[50:51], v[88:89], v[88:89] op_sel:[0,1] op_sel_hi:[1,0]
	s_waitcnt lgkmcnt(0)
	v_mul_f32_e32 v41, v83, v57
	v_mul_f32_e32 v55, v82, v56
	v_mov_b32_e32 v51, v41
	v_pk_add_f32 v[50:51], v[54:55], v[50:51]
	v_mul_f32_e32 v54, v75, v21
	v_pk_fma_f32 v[20:21], v[74:75], v[20:21], v[54:55] op_sel_hi:[1,1,0]
	v_mul_f32_e32 v54, v77, v23
	v_mul_f32_e32 v53, v48, v58
	v_mul_f32_e32 v56, v49, v59
	v_pk_fma_f32 v[22:23], v[76:77], v[22:23], v[54:55] op_sel_hi:[1,1,0]
	v_mov_b32_e32 v21, v53
	v_mov_b32_e32 v23, v56
	v_pk_add_f32 v[20:21], v[20:21], v[22:23]
	s_nop 0
	v_pk_add_f32 v[58:59], v[50:51], v[20:21]
	ds_read_b128 v[20:23], v139 offset:61440
	s_waitcnt lgkmcnt(0)
	v_mul_f32_e32 v50, v48, v22
	v_mul_f32_e32 v23, v49, v23
	v_mul_f32_e32 v22, v75, v17
	v_pk_fma_f32 v[16:17], v[74:75], v[16:17], v[22:23] op_sel_hi:[1,1,0]
	v_mul_f32_e32 v22, v77, v19
	v_mul_f32_e32 v71, v82, v20
	v_mul_f32_e32 v41, v83, v21
	v_pk_add_f32 v[20:21], v[86:87], v[86:87] op_sel:[0,1] op_sel_hi:[1,0]
	v_pk_fma_f32 v[18:19], v[76:77], v[18:19], v[22:23] op_sel_hi:[1,1,0]
	v_mov_b32_e32 v21, v41
	v_mov_b32_e32 v17, v50
	v_mov_b32_e32 v19, v23
	v_pk_add_f32 v[20:21], v[70:71], v[20:21]
	v_pk_add_f32 v[16:17], v[16:17], v[18:19]
	v_pk_mul_f32 v[34:35], v[34:35], v[40:41] op_sel_hi:[1,0]
	v_pk_add_f32 v[56:57], v[20:21], v[16:17]
	ds_read_b128 v[16:19], v144 offset:32768
	v_pk_mul_f32 v[32:33], v[32:33], v[40:41] op_sel_hi:[1,0]
	s_waitcnt lgkmcnt(0)
	v_mul_f32_e32 v21, v48, v18
	v_mul_f32_e32 v19, v49, v19
	v_mul_f32_e32 v18, v75, v13
	v_pk_fma_f32 v[12:13], v[74:75], v[12:13], v[18:19] op_sel_hi:[1,1,0]
	v_mul_f32_e32 v18, v77, v15
	v_mul_f32_e32 v53, v82, v16
	v_mul_f32_e32 v20, v83, v17
	v_pk_add_f32 v[16:17], v[84:85], v[84:85] op_sel:[0,1] op_sel_hi:[1,0]
	v_pk_fma_f32 v[14:15], v[76:77], v[14:15], v[18:19] op_sel_hi:[1,1,0]
	v_mov_b32_e32 v17, v20
	v_mov_b32_e32 v13, v21
	v_mov_b32_e32 v15, v19
	v_pk_add_f32 v[16:17], v[52:53], v[16:17]
	v_pk_add_f32 v[12:13], v[12:13], v[14:15]
	s_nop 0
	v_pk_add_f32 v[54:55], v[16:17], v[12:13]
	ds_read_b128 v[12:15], v144 offset:40960
	s_waitcnt lgkmcnt(0)
	v_mul_f32_e32 v17, v48, v14
	v_mul_f32_e32 v15, v49, v15
	v_mul_f32_e32 v14, v75, v9
	v_pk_fma_f32 v[8:9], v[74:75], v[8:9], v[14:15] op_sel_hi:[1,1,0]
	v_mul_f32_e32 v14, v77, v11
	v_mul_f32_e32 v69, v82, v12
	v_mul_f32_e32 v16, v83, v13
	v_pk_add_f32 v[12:13], v[80:81], v[80:81] op_sel:[0,1] op_sel_hi:[1,0]
	v_pk_fma_f32 v[10:11], v[76:77], v[10:11], v[14:15] op_sel_hi:[1,1,0]
	v_mov_b32_e32 v13, v16
	v_mov_b32_e32 v9, v17
	v_mov_b32_e32 v11, v15
	v_pk_add_f32 v[12:13], v[68:69], v[12:13]
	v_pk_add_f32 v[8:9], v[8:9], v[10:11]
	s_nop 0
	v_pk_add_f32 v[52:53], v[12:13], v[8:9]
	ds_read_b128 v[8:11], v144 offset:49152
	s_waitcnt lgkmcnt(0)
	v_mul_f32_e32 v13, v48, v10
	v_mul_f32_e32 v11, v49, v11
	v_mul_f32_e32 v10, v75, v5
	v_pk_fma_f32 v[4:5], v[74:75], v[4:5], v[10:11] op_sel_hi:[1,1,0]
	v_mul_f32_e32 v10, v77, v7
	v_mul_f32_e32 v63, v82, v8
	v_mul_f32_e32 v12, v83, v9
	v_pk_add_f32 v[8:9], v[78:79], v[78:79] op_sel:[0,1] op_sel_hi:[1,0]
	v_pk_fma_f32 v[6:7], v[76:77], v[6:7], v[10:11] op_sel_hi:[1,1,0]
	v_mov_b32_e32 v9, v12
	v_mov_b32_e32 v5, v13
	v_mov_b32_e32 v7, v11
	v_pk_add_f32 v[8:9], v[62:63], v[8:9]
	v_pk_add_f32 v[4:5], v[4:5], v[6:7]
	v_pk_mul_f32 v[10:11], v[46:47], v[40:41] op_sel_hi:[1,0]
	v_pk_add_f32 v[50:51], v[8:9], v[4:5]
	ds_read_b128 v[4:7], v144 offset:57344
	s_waitcnt lgkmcnt(0)
	v_mul_f32_e32 v9, v48, v6
	v_mul_f32_e32 v7, v49, v7
	v_mul_f32_e32 v6, v75, v1
	v_pk_fma_f32 v[0:1], v[74:75], v[0:1], v[6:7] op_sel_hi:[1,1,0]
	v_mul_f32_e32 v6, v77, v3
	v_mul_f32_e32 v67, v82, v4
	v_mul_f32_e32 v8, v83, v5
	v_pk_add_f32 v[4:5], v[72:73], v[72:73] op_sel:[0,1] op_sel_hi:[1,0]
	v_pk_fma_f32 v[2:3], v[76:77], v[2:3], v[6:7] op_sel_hi:[1,1,0]
	v_mov_b32_e32 v5, v8
	v_mov_b32_e32 v1, v9
	v_mov_b32_e32 v3, v7
	v_pk_add_f32 v[4:5], v[66:67], v[4:5]
	v_pk_add_f32 v[0:1], v[0:1], v[2:3]
	s_nop 0
	v_pk_add_f32 v[48:49], v[4:5], v[0:1]
	ds_read_b128 v[2:5], v139 offset:5120
	ds_read_b128 v[6:9], v139 offset:21504
	v_pk_mul_f32 v[0:1], v[44:45], v[40:41] op_sel_hi:[1,0]
	s_waitcnt lgkmcnt(0)
	v_pk_fma_f32 v[2:3], v[10:11], v[2:3], v[6:7]
	v_pk_fma_f32 v[0:1], v[0:1], v[4:5], v[8:9]
	v_and_b32_sdwa v5, v2, v214 dst_sel:DWORD dst_unused:UNUSED_PAD src0_sel:WORD_1 src1_sel:DWORD
	v_add3_u32 v6, v2, v5, s33
	v_and_b32_sdwa v5, v1, v214 dst_sel:DWORD dst_unused:UNUSED_PAD src0_sel:WORD_1 src1_sel:DWORD
	v_and_b32_sdwa v7, v3, v214 dst_sel:DWORD dst_unused:UNUSED_PAD src0_sel:WORD_1 src1_sel:DWORD
	v_and_b32_sdwa v4, v0, v214 dst_sel:DWORD dst_unused:UNUSED_PAD src0_sel:WORD_1 src1_sel:DWORD
	v_add3_u32 v5, v1, v5, s33
	v_add3_u32 v7, v3, v7, s33
	v_add3_u32 v4, v0, v4, s33
	v_and_b32_e32 v5, 0xffff0000, v5
	v_and_b32_e32 v7, 0xffff0000, v7
	v_or_b32_sdwa v5, v5, v4 dst_sel:DWORD dst_unused:UNUSED_PAD src0_sel:DWORD src1_sel:WORD_1
	v_or_b32_sdwa v4, v7, v6 dst_sel:DWORD dst_unused:UNUSED_PAD src0_sel:DWORD src1_sel:WORD_1
	global_store_dwordx2 v[42:43], v[4:5], off offset:2560 sc1
	ds_read_b128 v[4:7], v139 offset:37888
	v_pk_mul_f32 v[10:11], v[36:37], v[40:41] op_sel_hi:[1,0]
	s_waitcnt lgkmcnt(0)
	v_pk_mul_f32 v[4:5], v[2:3], v[4:5]
	v_pk_mul_f32 v[6:7], v[0:1], v[6:7]
	s_nop 0
	v_pk_mov_b32 v[8:9], v[4:5], v[6:7] op_sel:[1,0]
	v_mov_b32_e32 v5, v7
	v_pk_add_f32 v[74:75], v[8:9], v[4:5]
	ds_read_b128 v[4:7], v139 offset:46080
	s_waitcnt lgkmcnt(0)
	v_pk_mul_f32 v[4:5], v[2:3], v[4:5]
	v_pk_mul_f32 v[6:7], v[0:1], v[6:7]
	s_nop 0
	v_pk_mov_b32 v[8:9], v[4:5], v[6:7] op_sel:[1,0]
	v_mov_b32_e32 v5, v7
	v_pk_add_f32 v[72:73], v[8:9], v[4:5]
	ds_read_b128 v[4:7], v139 offset:54272
	s_waitcnt lgkmcnt(0)
	v_pk_mul_f32 v[4:5], v[2:3], v[4:5]
	v_pk_mul_f32 v[6:7], v[0:1], v[6:7]
	s_nop 0
	v_pk_mov_b32 v[8:9], v[4:5], v[6:7] op_sel:[1,0]
	v_mov_b32_e32 v5, v7
	v_pk_add_f32 v[70:71], v[8:9], v[4:5]
	ds_read_b128 v[4:7], v139 offset:62464
	s_waitcnt lgkmcnt(0)
	v_pk_mul_f32 v[4:5], v[2:3], v[4:5]
	v_pk_mul_f32 v[6:7], v[0:1], v[6:7]
	s_nop 0
	v_pk_mov_b32 v[8:9], v[4:5], v[6:7] op_sel:[1,0]
	v_mov_b32_e32 v5, v7
	v_pk_add_f32 v[68:69], v[8:9], v[4:5]
	ds_read_b128 v[4:7], v145 offset:32768
	s_waitcnt lgkmcnt(0)
	v_pk_mul_f32 v[4:5], v[2:3], v[4:5]
	v_pk_mul_f32 v[6:7], v[0:1], v[6:7]
	s_nop 0
	v_pk_mov_b32 v[8:9], v[4:5], v[6:7] op_sel:[1,0]
	v_mov_b32_e32 v5, v7
	v_pk_add_f32 v[66:67], v[8:9], v[4:5]
	ds_read_b128 v[4:7], v145 offset:40960
	s_waitcnt lgkmcnt(0)
	v_pk_mul_f32 v[4:5], v[2:3], v[4:5]
	v_pk_mul_f32 v[6:7], v[0:1], v[6:7]
	s_nop 0
	v_pk_mov_b32 v[8:9], v[4:5], v[6:7] op_sel:[1,0]
	v_mov_b32_e32 v5, v7
	v_pk_add_f32 v[62:63], v[8:9], v[4:5]
	ds_read_b128 v[4:7], v145 offset:49152
	s_waitcnt lgkmcnt(0)
	v_pk_mul_f32 v[4:5], v[2:3], v[4:5]
	v_pk_mul_f32 v[6:7], v[0:1], v[6:7]
	s_nop 0
	v_pk_mov_b32 v[8:9], v[4:5], v[6:7] op_sel:[1,0]
	v_mov_b32_e32 v5, v7
	v_pk_add_f32 v[46:47], v[8:9], v[4:5]
	ds_read_b128 v[4:7], v145 offset:57344
	v_pk_mul_f32 v[8:9], v[38:39], v[40:41] op_sel_hi:[1,0]
	s_waitcnt lgkmcnt(0)
	v_pk_mul_f32 v[2:3], v[2:3], v[4:5]
	v_pk_mul_f32 v[0:1], v[0:1], v[6:7]
	s_nop 0
	v_pk_mov_b32 v[4:5], v[2:3], v[0:1] op_sel:[1,0]
	v_mov_b32_e32 v3, v1
	v_pk_add_f32 v[44:45], v[4:5], v[2:3]
	ds_read_b128 v[0:3], v139 offset:6144
	ds_read_b128 v[4:7], v139 offset:22528
	s_waitcnt lgkmcnt(0)
	v_pk_fma_f32 v[36:37], v[10:11], v[0:1], v[4:5]
	v_pk_fma_f32 v[38:39], v[8:9], v[2:3], v[6:7]
	v_and_b32_sdwa v1, v36, v214 dst_sel:DWORD dst_unused:UNUSED_PAD src0_sel:WORD_1 src1_sel:DWORD
	v_add3_u32 v2, v36, v1, s33
	v_and_b32_sdwa v1, v39, v214 dst_sel:DWORD dst_unused:UNUSED_PAD src0_sel:WORD_1 src1_sel:DWORD
	v_and_b32_sdwa v3, v37, v214 dst_sel:DWORD dst_unused:UNUSED_PAD src0_sel:WORD_1 src1_sel:DWORD
	v_and_b32_sdwa v0, v38, v214 dst_sel:DWORD dst_unused:UNUSED_PAD src0_sel:WORD_1 src1_sel:DWORD
	v_add3_u32 v1, v39, v1, s33
	v_add3_u32 v3, v37, v3, s33
	v_add3_u32 v0, v38, v0, s33
	v_and_b32_e32 v1, 0xffff0000, v1
	v_and_b32_e32 v3, 0xffff0000, v3
	v_or_b32_sdwa v1, v1, v0 dst_sel:DWORD dst_unused:UNUSED_PAD src0_sel:DWORD src1_sel:WORD_1
	v_or_b32_sdwa v0, v3, v2 dst_sel:DWORD dst_unused:UNUSED_PAD src0_sel:DWORD src1_sel:WORD_1
	global_store_dwordx2 v[42:43], v[0:1], off offset:3072 sc1
	ds_read_b128 v[76:79], v139 offset:38912
	ds_read_b128 v[80:83], v139 offset:47104
	ds_read_b128 v[20:23], v139 offset:55296
	ds_read_b128 v[16:19], v139 offset:63488
	ds_read_b128 v[12:15], v146 offset:32768
	ds_read_b128 v[8:11], v146 offset:40960
	ds_read_b128 v[4:7], v146 offset:49152
	ds_read_b128 v[0:3], v146 offset:57344
	ds_read_b128 v[84:87], v139 offset:7168
	ds_read_b128 v[88:91], v139 offset:23552
	s_waitcnt lgkmcnt(0)
	v_pk_fma_f32 v[34:35], v[34:35], v[84:85], v[88:89]
	v_pk_fma_f32 v[32:33], v[32:33], v[86:87], v[90:91]
	v_and_b32_sdwa v41, v34, v214 dst_sel:DWORD dst_unused:UNUSED_PAD src0_sel:WORD_1 src1_sel:DWORD
	v_add3_u32 v84, v34, v41, s33
	v_and_b32_sdwa v41, v33, v214 dst_sel:DWORD dst_unused:UNUSED_PAD src0_sel:WORD_1 src1_sel:DWORD
	v_and_b32_sdwa v85, v35, v214 dst_sel:DWORD dst_unused:UNUSED_PAD src0_sel:WORD_1 src1_sel:DWORD
	v_and_b32_sdwa v40, v32, v214 dst_sel:DWORD dst_unused:UNUSED_PAD src0_sel:WORD_1 src1_sel:DWORD
	v_add3_u32 v41, v33, v41, s33
	v_add3_u32 v85, v35, v85, s33
	v_add3_u32 v40, v32, v40, s33
	v_and_b32_e32 v41, 0xffff0000, v41
	v_and_b32_e32 v85, 0xffff0000, v85
	v_or_b32_sdwa v41, v41, v40 dst_sel:DWORD dst_unused:UNUSED_PAD src0_sel:DWORD src1_sel:WORD_1
	v_or_b32_sdwa v40, v85, v84 dst_sel:DWORD dst_unused:UNUSED_PAD src0_sel:DWORD src1_sel:WORD_1
	global_store_dwordx2 v[42:43], v[40:41], off offset:3584 sc1
	ds_read_b128 v[40:43], v139 offset:39936
	s_waitcnt lgkmcnt(0)
	v_mul_f32_e32 v84, v34, v40
	v_mul_f32_e32 v85, v35, v41
	v_mul_f32_e32 v86, v32, v42
	v_mul_f32_e32 v87, v33, v43
	v_pk_add_f32 v[40:41], v[64:65], v[64:65] op_sel:[0,1] op_sel_hi:[1,0]
	v_pk_add_f32 v[42:43], v[74:75], v[74:75] op_sel:[0,1] op_sel_hi:[1,0]
	v_mov_b32_e32 v41, v84
	v_mov_b32_e32 v43, v85
	v_pk_add_f32 v[40:41], v[40:41], v[42:43]
	v_mul_f32_e32 v42, v37, v77
	v_pk_fma_f32 v[42:43], v[36:37], v[76:77], v[42:43] op_sel_hi:[1,1,0]
	v_mul_f32_e32 v64, v39, v79
	ds_read_b128 v[74:77], v139 offset:48128
	v_pk_fma_f32 v[64:65], v[38:39], v[78:79], v[64:65] op_sel_hi:[1,1,0]
	v_mov_b32_e32 v43, v86
	v_mov_b32_e32 v65, v87
	v_pk_add_f32 v[42:43], v[42:43], v[64:65]
	s_waitcnt lgkmcnt(0)
	v_mul_f32_e32 v64, v35, v75
	v_pk_add_f32 v[40:41], v[40:41], v[42:43]
	v_pk_add_f32 v[42:43], v[60:61], v[60:61] op_sel:[0,1] op_sel_hi:[1,0]
	v_add_f32_e32 v40, v40, v41
	v_mul_f32_e32 v41, v34, v74
	v_pk_add_f32 v[60:61], v[72:73], v[72:73] op_sel:[0,1] op_sel_hi:[1,0]
	v_mov_b32_e32 v43, v41
	v_mov_b32_e32 v61, v64
	v_pk_add_f32 v[42:43], v[42:43], v[60:61]
	v_mul_f32_e32 v60, v37, v81
	v_mul_f32_e32 v65, v32, v76
	v_pk_fma_f32 v[60:61], v[36:37], v[80:81], v[60:61] op_sel_hi:[1,1,0]
	v_mul_f32_e32 v64, v39, v83
	v_mul_f32_e32 v74, v33, v77
	v_mov_b32_e32 v61, v65
	v_pk_fma_f32 v[64:65], v[38:39], v[82:83], v[64:65] op_sel_hi:[1,1,0]
	s_nop 0
	v_mov_b32_e32 v65, v74
	ds_read_b128 v[72:75], v139 offset:56320
	v_pk_add_f32 v[60:61], v[60:61], v[64:65]
	s_waitcnt lgkmcnt(0)
	v_mul_f32_e32 v64, v32, v74
	v_pk_add_f32 v[42:43], v[42:43], v[60:61]
	v_mul_f32_e32 v60, v34, v72
	v_add_f32_e32 v41, v42, v43
	v_mul_f32_e32 v61, v35, v73
	v_pk_add_f32 v[42:43], v[58:59], v[58:59] op_sel:[0,1] op_sel_hi:[1,0]
	v_pk_add_f32 v[58:59], v[70:71], v[70:71] op_sel:[0,1] op_sel_hi:[1,0]
	v_mov_b32_e32 v43, v60
	v_mov_b32_e32 v59, v61
	v_pk_add_f32 v[42:43], v[42:43], v[58:59]
	v_mul_f32_e32 v58, v37, v21
	v_pk_fma_f32 v[20:21], v[36:37], v[20:21], v[58:59] op_sel_hi:[1,1,0]
	v_mul_f32_e32 v58, v39, v23
	v_pk_fma_f32 v[22:23], v[38:39], v[22:23], v[58:59] op_sel_hi:[1,1,0]
	ds_read_b128 v[58:61], v139 offset:64512
	v_mul_f32_e32 v65, v33, v75
	v_mov_b32_e32 v21, v64
	v_mov_b32_e32 v23, v65
	v_pk_add_f32 v[20:21], v[20:21], v[22:23]
	v_pk_add_f32 v[22:23], v[56:57], v[56:57] op_sel:[0,1] op_sel_hi:[1,0]
	v_pk_add_f32 v[20:21], v[42:43], v[20:21]
	v_pk_add_f32 v[42:43], v[68:69], v[68:69] op_sel:[0,1] op_sel_hi:[1,0]
	v_add_f32_e32 v20, v20, v21
	s_waitcnt lgkmcnt(0)
	v_mul_f32_e32 v21, v34, v58
	v_mul_f32_e32 v58, v35, v59
	v_mov_b32_e32 v23, v21
	v_mov_b32_e32 v43, v58
	v_pk_add_f32 v[22:23], v[22:23], v[42:43]
	v_mul_f32_e32 v42, v37, v17
	v_pk_fma_f32 v[16:17], v[36:37], v[16:17], v[42:43] op_sel_hi:[1,1,0]
	v_mul_f32_e32 v42, v39, v19
	v_mul_f32_e32 v59, v32, v60
	v_mul_f32_e32 v60, v33, v61
	v_pk_fma_f32 v[18:19], v[38:39], v[18:19], v[42:43] op_sel_hi:[1,1,0]
	v_mov_b32_e32 v17, v59
	v_mov_b32_e32 v19, v60
	v_pk_add_f32 v[16:17], v[16:17], v[18:19]
	s_nop 0
	v_pk_add_f32 v[16:17], v[22:23], v[16:17]
	s_nop 0
	v_add_f32_e32 v21, v16, v17
	ds_read_b128 v[16:19], v147 offset:32768
	s_waitcnt lgkmcnt(0)
	v_mul_f32_e32 v22, v34, v16
	v_mul_f32_e32 v23, v35, v17
	v_mul_f32_e32 v42, v32, v18
	v_mul_f32_e32 v43, v33, v19
	v_pk_add_f32 v[16:17], v[54:55], v[54:55] op_sel:[0,1] op_sel_hi:[1,0]
	v_pk_add_f32 v[18:19], v[66:67], v[66:67] op_sel:[0,1] op_sel_hi:[1,0]
	v_mov_b32_e32 v17, v22
	v_mov_b32_e32 v19, v23
	v_pk_add_f32 v[16:17], v[16:17], v[18:19]
	v_mul_f32_e32 v18, v37, v13
	v_pk_fma_f32 v[12:13], v[36:37], v[12:13], v[18:19] op_sel_hi:[1,1,0]
	v_mul_f32_e32 v18, v39, v15
	v_pk_fma_f32 v[14:15], v[38:39], v[14:15], v[18:19] op_sel_hi:[1,1,0]
	v_mov_b32_e32 v13, v42
	v_mov_b32_e32 v15, v43
	v_pk_add_f32 v[12:13], v[12:13], v[14:15]
	s_nop 0
	v_pk_add_f32 v[12:13], v[16:17], v[12:13]
	s_nop 0
	v_add_f32_e32 v16, v12, v13
	ds_read_b128 v[12:15], v147 offset:40960
	s_waitcnt lgkmcnt(0)
	v_mul_f32_e32 v17, v34, v12
	v_mul_f32_e32 v18, v35, v13
	v_mul_f32_e32 v19, v32, v14
	v_mul_f32_e32 v22, v33, v15
	v_pk_add_f32 v[12:13], v[52:53], v[52:53] op_sel:[0,1] op_sel_hi:[1,0]
	v_pk_add_f32 v[14:15], v[62:63], v[62:63] op_sel:[0,1] op_sel_hi:[1,0]
	v_mov_b32_e32 v13, v17
	v_mov_b32_e32 v15, v18
	v_pk_add_f32 v[12:13], v[12:13], v[14:15]
	v_mul_f32_e32 v14, v37, v9
	v_pk_fma_f32 v[8:9], v[36:37], v[8:9], v[14:15] op_sel_hi:[1,1,0]
	v_mul_f32_e32 v14, v39, v11
	v_pk_fma_f32 v[10:11], v[38:39], v[10:11], v[14:15] op_sel_hi:[1,1,0]
	v_mov_b32_e32 v9, v19
	v_mov_b32_e32 v11, v22
	v_pk_add_f32 v[8:9], v[8:9], v[10:11]
	s_nop 0
	v_pk_add_f32 v[8:9], v[12:13], v[8:9]
	s_nop 0
	v_add_f32_e32 v12, v8, v9
	ds_read_b128 v[8:11], v147 offset:49152
	s_waitcnt lgkmcnt(0)
	v_mul_f32_e32 v13, v34, v8
	v_mul_f32_e32 v14, v35, v9
	v_mul_f32_e32 v15, v32, v10
	v_mul_f32_e32 v17, v33, v11
	v_pk_add_f32 v[8:9], v[50:51], v[50:51] op_sel:[0,1] op_sel_hi:[1,0]
	v_pk_add_f32 v[10:11], v[46:47], v[46:47] op_sel:[0,1] op_sel_hi:[1,0]
	v_mov_b32_e32 v9, v13
	v_mov_b32_e32 v11, v14
	v_pk_add_f32 v[8:9], v[8:9], v[10:11]
	v_mul_f32_e32 v10, v37, v5
	v_pk_fma_f32 v[4:5], v[36:37], v[4:5], v[10:11] op_sel_hi:[1,1,0]
	v_mul_f32_e32 v10, v39, v7
	v_pk_fma_f32 v[6:7], v[38:39], v[6:7], v[10:11] op_sel_hi:[1,1,0]
	v_mov_b32_e32 v5, v15
	v_mov_b32_e32 v7, v17
	v_pk_add_f32 v[4:5], v[4:5], v[6:7]
	s_nop 0
	v_pk_add_f32 v[4:5], v[8:9], v[4:5]
	s_nop 0
	v_add_f32_e32 v8, v4, v5
	ds_read_b128 v[4:7], v147 offset:57344
	s_waitcnt lgkmcnt(0)
	v_mul_f32_e32 v9, v34, v4
	v_mul_f32_e32 v10, v35, v5
	v_mul_f32_e32 v11, v32, v6
	v_mul_f32_e32 v13, v33, v7
	v_pk_add_f32 v[4:5], v[48:49], v[48:49] op_sel:[0,1] op_sel_hi:[1,0]
	v_pk_add_f32 v[6:7], v[44:45], v[44:45] op_sel:[0,1] op_sel_hi:[1,0]
	v_mov_b32_e32 v5, v9
	v_mov_b32_e32 v7, v10
	v_pk_add_f32 v[4:5], v[4:5], v[6:7]
	v_mul_f32_e32 v6, v37, v1
	v_pk_fma_f32 v[0:1], v[36:37], v[0:1], v[6:7] op_sel_hi:[1,1,0]
	v_mul_f32_e32 v6, v39, v3
	v_pk_fma_f32 v[2:3], v[38:39], v[2:3], v[6:7] op_sel_hi:[1,1,0]
	v_mov_b32_e32 v1, v11
	v_mov_b32_e32 v3, v13
	v_pk_add_f32 v[0:1], v[0:1], v[2:3]
	s_nop 0
	v_pk_add_f32 v[0:1], v[4:5], v[0:1]
	s_nop 0
	v_add_f32_e32 v6, v0, v1
	v_add_f32_dpp v0, v40, v40 quad_perm:[1,0,3,2] row_mask:0xf bank_mask:0xf bound_ctrl:1
	s_nop 1
	v_add_f32_dpp v0, v0, v0 quad_perm:[2,3,0,1] row_mask:0xf bank_mask:0xf bound_ctrl:1
	s_nop 1
	v_add_f32_dpp v0, v0, v0 row_half_mirror row_mask:0xf bank_mask:0xf bound_ctrl:1
	s_nop 1
	v_add_f32_dpp v0, v0, v0 row_mirror row_mask:0xf bank_mask:0xf bound_ctrl:1
	ds_swizzle_b32 v1, v0 offset:swizzle(SWAP,16)
	s_waitcnt lgkmcnt(0)
	v_add_f32_e32 v1, v0, v1
	v_add_f32_dpp v0, v41, v41 quad_perm:[1,0,3,2] row_mask:0xf bank_mask:0xf bound_ctrl:1
	v_mov_b32_e32 v3, v1
	s_nop 1
	v_permlane32_swap_b32_e32 v1, v3
	v_add_f32_dpp v0, v0, v0 quad_perm:[2,3,0,1] row_mask:0xf bank_mask:0xf bound_ctrl:1
	s_nop 1
	v_add_f32_dpp v0, v0, v0 row_half_mirror row_mask:0xf bank_mask:0xf bound_ctrl:1
	s_nop 1
	v_add_f32_dpp v0, v0, v0 row_mirror row_mask:0xf bank_mask:0xf bound_ctrl:1
	ds_swizzle_b32 v2, v0 offset:swizzle(SWAP,16)
	s_waitcnt lgkmcnt(0)
	v_add_f32_e32 v0, v0, v2
	v_mov_b32_e32 v2, v0
	s_nop 1
	v_permlane32_swap_b32_e32 v0, v2
	v_pk_add_f32 v[4:5], v[0:1], v[2:3]
	s_nop 0
	v_add_f32_dpp v0, v20, v20 quad_perm:[1,0,3,2] row_mask:0xf bank_mask:0xf bound_ctrl:1
	v_cmp_gt_f32_e32 vcc, v4, v5
	v_cmp_nlt_f32_e64 s[46:47], s0, v5
	v_add_f32_dpp v0, v0, v0 quad_perm:[2,3,0,1] row_mask:0xf bank_mask:0xf bound_ctrl:1
	v_cndmask_b32_e64 v3, 0, 1, vcc
	s_nop 0
	v_add_f32_dpp v0, v0, v0 row_half_mirror row_mask:0xf bank_mask:0xf bound_ctrl:1
	s_nop 1
	v_add_f32_dpp v0, v0, v0 row_mirror row_mask:0xf bank_mask:0xf bound_ctrl:1
	ds_swizzle_b32 v1, v0 offset:swizzle(SWAP,16)
	s_waitcnt lgkmcnt(0)
	v_add_f32_e32 v0, v0, v1
	v_mov_b32_e32 v1, v0
	s_nop 1
	v_permlane32_swap_b32_e32 v0, v1
	v_add_f32_e32 v2, v0, v1
	s_nop 0
	v_add_f32_dpp v0, v21, v21 quad_perm:[1,0,3,2] row_mask:0xf bank_mask:0xf bound_ctrl:1
	s_nop 1
	v_add_f32_dpp v0, v0, v0 quad_perm:[2,3,0,1] row_mask:0xf bank_mask:0xf bound_ctrl:1
	s_nop 1
	v_add_f32_dpp v0, v0, v0 row_half_mirror row_mask:0xf bank_mask:0xf bound_ctrl:1
	s_nop 1
	v_add_f32_dpp v0, v0, v0 row_mirror row_mask:0xf bank_mask:0xf bound_ctrl:1
	ds_swizzle_b32 v1, v0 offset:swizzle(SWAP,16)
	s_waitcnt lgkmcnt(0)
	v_add_f32_e32 v0, v0, v1
	v_mov_b32_e32 v1, v0
	s_nop 1
	v_permlane32_swap_b32_e32 v0, v1
	v_add_f32_e32 v7, v0, v1
	s_nop 0
	v_add_f32_dpp v0, v16, v16 quad_perm:[1,0,3,2] row_mask:0xf bank_mask:0xf bound_ctrl:1
	s_nop 1
	v_add_f32_dpp v0, v0, v0 quad_perm:[2,3,0,1] row_mask:0xf bank_mask:0xf bound_ctrl:1
	s_nop 1
	v_add_f32_dpp v0, v0, v0 row_half_mirror row_mask:0xf bank_mask:0xf bound_ctrl:1
	s_nop 1
	v_add_f32_dpp v0, v0, v0 row_mirror row_mask:0xf bank_mask:0xf bound_ctrl:1
	ds_swizzle_b32 v1, v0 offset:swizzle(SWAP,16)
	s_waitcnt lgkmcnt(0)
	v_add_f32_e32 v0, v0, v1
	v_mov_b32_e32 v1, v0
	s_nop 1
	v_permlane32_swap_b32_e32 v0, v1
	v_add_f32_e32 v9, v0, v1
	s_nop 0
	v_add_f32_dpp v0, v12, v12 quad_perm:[1,0,3,2] row_mask:0xf bank_mask:0xf bound_ctrl:1
	s_nop 1
	v_add_f32_dpp v0, v0, v0 quad_perm:[2,3,0,1] row_mask:0xf bank_mask:0xf bound_ctrl:1
	s_nop 1
	v_add_f32_dpp v0, v0, v0 row_half_mirror row_mask:0xf bank_mask:0xf bound_ctrl:1
	s_nop 1
	v_add_f32_dpp v0, v0, v0 row_mirror row_mask:0xf bank_mask:0xf bound_ctrl:1
	ds_swizzle_b32 v1, v0 offset:swizzle(SWAP,16)
	s_waitcnt lgkmcnt(0)
	v_add_f32_e32 v0, v0, v1
	v_mov_b32_e32 v1, v0
	s_nop 1
	v_permlane32_swap_b32_e32 v0, v1
	v_add_f32_e32 v10, v0, v1
	s_nop 0
	v_add_f32_dpp v0, v8, v8 quad_perm:[1,0,3,2] row_mask:0xf bank_mask:0xf bound_ctrl:1
	s_nop 1
	v_add_f32_dpp v0, v0, v0 quad_perm:[2,3,0,1] row_mask:0xf bank_mask:0xf bound_ctrl:1
	s_nop 1
	v_add_f32_dpp v0, v0, v0 row_half_mirror row_mask:0xf bank_mask:0xf bound_ctrl:1
	s_nop 1
	v_add_f32_dpp v0, v0, v0 row_mirror row_mask:0xf bank_mask:0xf bound_ctrl:1
	ds_swizzle_b32 v1, v0 offset:swizzle(SWAP,16)
	s_waitcnt lgkmcnt(0)
	v_add_f32_e32 v0, v0, v1
	v_mov_b32_e32 v1, v0
	s_nop 1
	v_permlane32_swap_b32_e32 v0, v1
	v_add_f32_e32 v8, v0, v1
	s_nop 0
	v_add_f32_dpp v0, v6, v6 quad_perm:[1,0,3,2] row_mask:0xf bank_mask:0xf bound_ctrl:1
	s_nop 1
	v_add_f32_dpp v0, v0, v0 quad_perm:[2,3,0,1] row_mask:0xf bank_mask:0xf bound_ctrl:1
	s_nop 1
	v_add_f32_dpp v0, v0, v0 row_half_mirror row_mask:0xf bank_mask:0xf bound_ctrl:1
	s_nop 1
	v_add_f32_dpp v0, v0, v0 row_mirror row_mask:0xf bank_mask:0xf bound_ctrl:1
	ds_swizzle_b32 v1, v0 offset:swizzle(SWAP,16)
	s_waitcnt lgkmcnt(0)
	v_add_f32_e32 v0, v0, v1
	v_mov_b32_e32 v1, v0
	s_nop 1
	v_permlane32_swap_b32_e32 v0, v1
	v_add_f32_e32 v1, v0, v1
	v_cndmask_b32_e32 v0, v5, v4, vcc
	v_cmp_gt_f32_e32 vcc, v2, v0
	s_nop 1
	v_cndmask_b32_e32 v0, v0, v2, vcc
	v_cndmask_b32_e64 v3, v3, 2, vcc
	v_cmp_gt_f32_e32 vcc, v7, v0
	s_nop 1
	v_cndmask_b32_e32 v0, v0, v7, vcc
	v_cndmask_b32_e64 v3, v3, 3, vcc
	v_cmp_gt_f32_e32 vcc, v9, v0
	s_nop 1
	v_cndmask_b32_e32 v0, v0, v9, vcc
	v_cndmask_b32_e64 v3, v3, 4, vcc
	v_cmp_gt_f32_e32 vcc, v10, v0
	s_nop 1
	v_cndmask_b32_e32 v0, v0, v10, vcc
	v_cndmask_b32_e64 v6, v3, 5, vcc
	v_cmp_ngt_f32_e32 vcc, v8, v0
	s_nop 1
	v_cndmask_b32_e32 v3, v8, v0, vcc
	v_cndmask_b32_e32 v0, 6, v6, vcc
	v_cmp_gt_f32_e64 s[42:43], v1, v3
	s_or_b64 s[0:1], vcc, s[42:43]
	v_cmp_ngt_f32_e64 s[40:41], v1, v3
	v_cndmask_b32_e64 v0, v0, 7, s[42:43]
	v_cmp_eq_u32_e64 s[44:45], 0, v0
	s_or_b64 s[44:45], s[44:45], s[46:47]
	s_nop 0
	v_cndmask_b32_e64 v5, v5, v222, s[44:45]
	v_cndmask_b32_e64 v6, 0, -1, s[44:45]
	v_cmp_ne_u32_e64 s[44:45], 1, v0
	v_cmp_gt_f32_e64 s[46:47], v4, v5
	s_and_b64 s[44:45], s[44:45], s[46:47]
	v_cndmask_b32_e64 v4, v5, v4, s[44:45]
	v_cndmask_b32_e64 v5, v6, 1, s[44:45]
	v_cmp_ne_u32_e64 s[44:45], 2, v0
	v_cmp_gt_f32_e64 s[46:47], v2, v4
	s_and_b64 s[44:45], s[44:45], s[46:47]
	v_cndmask_b32_e64 v2, v4, v2, s[44:45]
	v_cndmask_b32_e64 v4, v5, 2, s[44:45]
	v_cmp_ne_u32_e64 s[44:45], 3, v0
	v_cmp_gt_f32_e64 s[46:47], v7, v2
	s_and_b64 s[44:45], s[44:45], s[46:47]
	v_cndmask_b32_e64 v2, v2, v7, s[44:45]
	v_cndmask_b32_e64 v4, v4, 3, s[44:45]
	v_cmp_ne_u32_e64 s[44:45], 4, v0
	v_cmp_gt_f32_e64 s[46:47], v9, v2
	s_and_b64 s[44:45], s[44:45], s[46:47]
	v_cndmask_b32_e64 v2, v2, v9, s[44:45]
	v_cndmask_b32_e64 v4, v4, 4, s[44:45]
	v_cmp_ne_u32_e64 s[44:45], 5, v0
	v_cmp_gt_f32_e64 s[46:47], v10, v2
	s_and_b64 s[44:45], s[44:45], s[46:47]
	v_cndmask_b32_e64 v2, v2, v10, s[44:45]
	v_cmp_gt_f32_e32 vcc, v8, v2
	v_cndmask_b32_e64 v5, v4, 5, s[44:45]
	s_and_b64 vcc, s[0:1], vcc
	v_cndmask_b32_e32 v4, v2, v8, vcc
	v_cndmask_b32_e64 v2, v5, 6, vcc
	s_and_saveexec_b64 s[0:1], s[40:41]
	s_cbranch_execz .LBB0_1240
	v_cmp_gt_f32_e32 vcc, v1, v4
	s_and_saveexec_b64 s[12:13], vcc
	v_mov_b32_e32 v2, 7
	v_mov_b32_e32 v4, v1
	s_or_b64 exec, exec, s[12:13]
	v_mov_b32_e32 v1, v3
.LBB0_1240:
	s_or_b64 exec, exec, s[0:1]
	s_and_saveexec_b64 s[0:1], s[38:39]
	s_cbranch_execz .LBB0_1202
	v_sub_f32_e32 v1, v4, v1
	v_mul_f32_e32 v1, 0x3fb8aa3b, v1
	v_exp_f32_e32 v1, v1
	s_cmp_gt_i32 s4, 31
	v_add_f32_e32 v1, 1.0, v1
	v_div_scale_f32 v3, s[12:13], v1, v1, 1.0
	v_rcp_f32_e32 v4, v3
	v_div_scale_f32 v5, vcc, 1.0, v1, 1.0
	s_mov_b64 s[12:13], -1
	v_fma_f32 v6, -v3, v4, 1.0
	v_fmac_f32_e32 v4, v6, v4
	v_mul_f32_e32 v6, v5, v4
	v_fma_f32 v7, -v3, v6, v5
	v_fmac_f32_e32 v6, v7, v4
	v_fma_f32 v3, -v3, v6, v5
	v_div_fmas_f32 v3, v3, v4, v6
	v_div_fixup_f32 v4, v3, v1, 1.0
	v_sub_f32_e32 v5, 1.0, v4
	s_cbranch_scc0 .LBB0_1243
	v_readlane_b32 s12, v252, 53
	v_lshlrev_b32_e32 v184, 6, v0
	v_readlane_b32 s13, v252, 54
	v_readlane_b32 s14, v250, 0
	v_readlane_b32 s15, v250, 1
	v_lshl_add_u64 v[6:7], v[184:185], 2, s[12:13]
	global_atomic_add v1, v[6:7], v214, off sc0
	v_lshlrev_b32_e32 v6, 6, v2
	v_ashrrev_i32_e32 v7, 31, v6
	v_lshl_add_u64 v[6:7], v[6:7], 2, s[12:13]
	global_atomic_add v3, v[6:7], v214, off sc0
	s_lshl_b64 s[12:13], s[10:11], 4
	s_add_u32 s12, s14, s12
	s_addc_u32 s13, s15, s13
	s_lshl_b64 s[10:11], s[10:11], 3
	s_waitcnt vmcnt(0)
	global_store_dwordx4 v185, v[0:3], s[12:13] sc1
	v_readlane_b32 s12, v250, 2
	v_readlane_b32 s13, v250, 3
	s_add_u32 s10, s12, s10
	s_addc_u32 s11, s13, s11
	global_store_dwordx2 v185, v[4:5], s[10:11] sc1
	s_mov_b64 s[12:13], 0

.LBB0_1248:
	s_or_b64 exec, exec, s[0:1]
	s_waitcnt lgkmcnt(0)
	s_barrier
	s_and_saveexec_b64 s[0:1], s[6:7]
	s_cbranch_execz .LBB0_1250
	v_readlane_b32 s4, v252, 55
	v_readlane_b32 s6, v254, 62
	v_mul_lo_u32 v4, v25, s88
	v_lshl_add_u32 v0, v25, 4, s4
	ds_read_b128 v[0:3], v0
	s_add_i32 s4, 0, 0x18020
	v_readlane_b32 s7, v254, 63
	v_add_u32_e32 v4, s6, v4
	v_readlane_b32 s6, v250, 0
	s_waitcnt lgkmcnt(0)
	v_lshl_add_u32 v5, v0, 2, s4
	ds_read_b32 v5, v5
	v_readlane_b32 s7, v250, 1
	s_waitcnt lgkmcnt(0)
	v_add_u32_e32 v1, v5, v1
	v_lshl_add_u32 v5, v2, 2, s4
	ds_read_b32 v5, v5
	v_readlane_b32 s4, v252, 56
	s_waitcnt lgkmcnt(0)
	v_add_u32_e32 v3, v5, v3
	v_ashrrev_i32_e32 v5, 31, v4
	v_lshl_add_u64 v[6:7], v[4:5], 4, s[6:7]
	global_store_dwordx4 v[6:7], v[0:3], off sc1
	v_readlane_b32 s6, v250, 2
	v_readlane_b32 s7, v250, 3
	v_lshl_add_u32 v0, v25, 3, s4
	ds_read_b64 v[0:1], v0
	v_lshl_add_u64 v[2:3], v[4:5], 3, s[6:7]
	s_waitcnt lgkmcnt(0)
	global_store_dwordx2 v[2:3], v[0:1], off sc1

.LBB0_1254:
	s_or_b64 exec, exec, s[8:9]
	s_waitcnt lgkmcnt(0)
	s_barrier
	ds_read_b128 v[10:13], v185 offset:32768
	ds_read_b128 v[14:17], v185 offset:32784
	s_mov_b32 s8, 0xf800000
	s_waitcnt lgkmcnt(0)
	s_barrier
	v_add_f32_e32 v10, 0, v10
	v_add_f32_e32 v10, v10, v11
	v_add_f32_e32 v10, v10, v12
	v_add_f32_e32 v10, v10, v13
	v_add_f32_e32 v10, v10, v14
	v_add_f32_e32 v10, v10, v15
	v_add_f32_e32 v10, v10, v16
	v_add_f32_e32 v10, v10, v17
	v_fmamk_f32 v10, v10, 0x3a000000, v212
	v_cmp_gt_f32_e32 vcc, s8, v10
	v_mul_f32_e32 v11, 0x4f800000, v10
	s_nop 0
	v_cndmask_b32_e32 v10, v10, v11, vcc
	v_sqrt_f32_e32 v11, v10
	s_nop 0
	v_add_u32_e32 v12, -1, v11
	v_fma_f32 v13, -v12, v11, v10
	v_cmp_ge_f32_e64 s[38:39], 0, v13
	v_add_u32_e32 v13, 1, v11
	s_nop 0
	v_cndmask_b32_e64 v12, v11, v12, s[38:39]
	v_fma_f32 v11, -v13, v11, v10
	v_cmp_lt_f32_e64 s[38:39], 0, v11
	s_nop 1
	v_cndmask_b32_e64 v11, v12, v13, s[38:39]
	v_mul_f32_e32 v12, 0x37800000, v11
	v_cndmask_b32_e32 v11, v11, v12, vcc
	v_cmp_class_f32_e32 vcc, v10, v213
	s_nop 1
	v_cndmask_b32_e32 v10, v11, v10, vcc
	v_div_scale_f32 v11, s[8:9], v10, v10, 1.0
	v_rcp_f32_e32 v12, v11
	s_add_i32 s8, s4, 0x4000
	s_ashr_i32 s9, s8, 31
	s_lshl_b64 s[8:9], s[8:9], 12
	v_fma_f32 v13, -v11, v12, 1.0
	v_fmac_f32_e32 v12, v13, v12
	v_div_scale_f32 v13, vcc, 1.0, v10, 1.0
	v_mul_f32_e32 v14, v13, v12
	v_fma_f32 v15, -v11, v14, v13
	v_fmac_f32_e32 v14, v15, v12
	v_fma_f32 v11, -v11, v14, v13
	v_div_fmas_f32 v11, v11, v12, v14
	v_div_fixup_f32 v18, v11, v10, 1.0
	ds_read_b128 v[10:13], v9 offset:8192
	ds_read_b128 v[14:17], v9 offset:24576
	v_pk_mul_f32 v[0:1], v[0:1], v[18:19] op_sel_hi:[1,0]
	v_pk_mul_f32 v[2:3], v[2:3], v[18:19] op_sel_hi:[1,0]
	s_add_i32 s4, s4, s94
	s_waitcnt lgkmcnt(0)
	v_pk_fma_f32 v[0:1], v[10:11], v[0:1], v[14:15]
	s_nop 0
	v_bfe_u32 v10, v0, 16, 1
	v_add3_u32 v0, v0, v10, s33
	v_bfe_u32 v10, v1, 16, 1
	v_pk_fma_f32 v[2:3], v[12:13], v[2:3], v[16:17]
	v_lshrrev_b32_e32 v0, 16, v0
	v_add3_u32 v1, v1, v10, s33
	v_and_or_b32 v0, v1, s96, v0
	v_bfe_u32 v1, v2, 16, 1
	v_add3_u32 v1, v2, v1, s33
	v_bfe_u32 v2, v3, 16, 1
	v_lshrrev_b32_e32 v1, 16, v1
	v_add3_u32 v2, v3, v2, s33
	v_and_or_b32 v1, v2, s96, v1
	v_lshl_add_u64 v[2:3], v[4:5], 0, s[8:9]
	v_readlane_b32 s8, v254, 42
	v_readlane_b32 s9, v254, 43
	s_add_u32 s6, s6, s8
	s_addc_u32 s7, s7, s9
	s_add_u32 s0, s0, s8
	s_addc_u32 s1, s1, s9
	s_cmpk_gt_i32 s4, 0xff
	global_store_dwordx2 v[2:3], v[0:1], off sc1
	s_cbranch_scc1 .LBB0_1257
.LBB0_1255:
	v_lshl_add_u64 v[42:43], s[6:7], 0, v[6:7]
	v_add_co_u32_e32 v10, vcc, 0x3a400000, v42
	v_lshl_add_u64 v[0:1], s[0:1], 0, v[6:7]
	s_nop 0
	v_addc_co_u32_e32 v11, vcc, 0, v43, vcc
	v_add_co_u32_e32 v14, vcc, 0x3a600000, v42
	global_load_dwordx4 v[0:3], v[0:1], off
	s_nop 0
	v_addc_co_u32_e32 v15, vcc, 0, v43, vcc
	v_add_co_u32_e32 v18, vcc, 0x3a800000, v42
	global_load_dwordx4 v[10:13], v[10:11], off
	s_nop 0
	global_load_dwordx4 v[14:17], v[14:15], off
	v_addc_co_u32_e32 v19, vcc, 0, v43, vcc
	v_add_co_u32_e32 v22, vcc, 0x3aa00000, v42
	s_mov_b32 s8, 0x3a100000
	s_nop 0
	v_addc_co_u32_e32 v23, vcc, 0, v43, vcc
	v_add_co_u32_e32 v26, vcc, 0x3ac00000, v42
	global_load_dwordx4 v[18:21], v[18:19], off
	s_nop 0
	global_load_dwordx4 v[22:25], v[22:23], off
	v_addc_co_u32_e32 v27, vcc, 0, v43, vcc
	v_add_co_u32_e32 v30, vcc, 0x3ae00000, v42
	s_waitcnt vmcnt(3)
	v_pk_add_f32 v[2:3], v[2:3], v[12:13]
	v_addc_co_u32_e32 v31, vcc, 0, v43, vcc
	v_add_co_u32_e32 v34, vcc, 0x3b000000, v42
	global_load_dwordx4 v[26:29], v[26:27], off
	s_nop 0
	global_load_dwordx4 v[30:33], v[30:31], off
	v_addc_co_u32_e32 v35, vcc, 0, v43, vcc
	v_add_co_u32_e32 v38, vcc, 0x3b200000, v42
	global_load_dwordx4 v[34:37], v[34:35], off
	s_nop 0
	v_addc_co_u32_e32 v39, vcc, 0, v43, vcc
	global_load_dwordx4 v[38:41], v[38:39], off
	v_pk_add_f32 v[0:1], v[0:1], v[10:11]
	s_waitcnt vmcnt(6)
	v_pk_add_f32 v[2:3], v[2:3], v[16:17]
	v_pk_add_f32 v[0:1], v[0:1], v[14:15]
	s_waitcnt vmcnt(5)
	v_pk_add_f32 v[2:3], v[2:3], v[20:21]
	v_pk_add_f32 v[0:1], v[0:1], v[18:19]
	s_waitcnt vmcnt(4)
	v_pk_add_f32 v[2:3], v[2:3], v[24:25]
	v_pk_add_f32 v[0:1], v[0:1], v[22:23]
	s_waitcnt vmcnt(3)
	v_pk_add_f32 v[2:3], v[2:3], v[28:29]
	v_pk_add_f32 v[0:1], v[0:1], v[26:27]
	s_waitcnt vmcnt(2)
	v_pk_add_f32 v[2:3], v[2:3], v[32:33]
	v_pk_add_f32 v[0:1], v[0:1], v[30:31]
	s_waitcnt vmcnt(1)
	v_pk_add_f32 v[2:3], v[2:3], v[36:37]
	v_pk_add_f32 v[0:1], v[0:1], v[34:35]
	s_waitcnt vmcnt(0)
	v_pk_add_f32 v[2:3], v[2:3], v[40:41]
	v_pk_add_f32 v[0:1], v[0:1], v[38:39]
	v_mul_f32_e32 v11, v3, v3
	v_mul_f32_e32 v10, v1, v1
	v_fmac_f32_e32 v10, v0, v0
	v_fmac_f32_e32 v11, v2, v2
	v_add_f32_e32 v10, v10, v11
	s_nop 1
	v_add_f32_dpp v10, v10, v10 quad_perm:[1,0,3,2] row_mask:0xf bank_mask:0xf bound_ctrl:1
	s_nop 1
	v_add_f32_dpp v10, v10, v10 quad_perm:[2,3,0,1] row_mask:0xf bank_mask:0xf bound_ctrl:1
	s_nop 1
	v_add_f32_dpp v10, v10, v10 row_half_mirror row_mask:0xf bank_mask:0xf bound_ctrl:1
	s_nop 1
	v_add_f32_dpp v12, v10, v10 row_mirror row_mask:0xf bank_mask:0xf bound_ctrl:1
	ds_swizzle_b32 v13, v12 offset:swizzle(SWAP,16)
	v_add_co_u32_e32 v10, vcc, s8, v42
	s_nop 1
	v_addc_co_u32_e32 v11, vcc, 0, v43, vcc
	global_store_dwordx4 v[10:11], v[0:3], off sc1
	s_waitcnt lgkmcnt(0)
	v_add_f32_e32 v10, v12, v13
	v_mov_b32_e32 v11, v10
	s_nop 1
	v_permlane32_swap_b32_e32 v10, v11
	s_and_saveexec_b64 s[8:9], s[36:37]
	s_cbranch_execz .LBB0_1254
	v_add_f32_e32 v10, v10, v11
	v_mov_b32_e32 v11, s12
	ds_write_b32 v11, v10 offset:32768
	s_branch .LBB0_1254

.LBB0_1260:
	global_load_dwordx2 v[78:79], v[136:137], off
	global_load_dwordx2 v[76:77], v[136:137], off offset:512
	global_load_dwordx2 v[74:75], v[136:137], off offset:1024
	global_load_dwordx2 v[72:73], v[136:137], off offset:1536
	global_load_dwordx2 v[70:71], v[136:137], off offset:2048
	global_load_dwordx2 v[68:69], v[136:137], off offset:2560
	global_load_dwordx2 v[66:67], v[136:137], off offset:3072
	global_load_dwordx2 v[64:65], v[136:137], off offset:3584
	s_add_i32 s4, s88, s30
	s_cmpk_lt_i32 s4, 0x4000
	s_cselect_b64 s[0:1], -1, 0
	v_cndmask_b32_e64 v184, 0, 1, s[0:1]
	s_and_b64 s[0:1], s[0:1], exec
	v_readlane_b32 s0, v255, 21
	s_cselect_b32 s24, s4, s30
	s_add_i32 s4, s0, s30
	s_cmpk_lt_i32 s4, 0x4000
	v_readlane_b32 s1, v255, 22
	s_cselect_b64 s[12:13], -1, 0
	s_and_b64 s[0:1], s[12:13], exec
	v_readlane_b32 s0, v255, 29
	s_cselect_b32 s14, s4, s30
	s_add_i32 s4, s0, s30
	s_cmpk_lt_i32 s4, 0x4000
	s_cselect_b64 s[6:7], -1, 0
	s_and_b64 s[0:1], s[6:7], exec
	s_cselect_b32 s8, s4, s30
	s_ashr_i32 s25, s24, 31
	s_ashr_i32 s15, s14, 31
	s_lshl_b64 s[16:17], s[24:25], 12
	s_lshl_b64 s[10:11], s[14:15], 12
	v_lshl_add_u64 v[88:89], v[128:129], 0, s[16:17]
	v_lshl_add_u64 v[90:91], v[128:129], 0, s[10:11]
	global_load_dwordx2 v[86:87], v[88:89], off
	global_load_dwordx2 v[84:85], v[88:89], off offset:512
	global_load_dwordx2 v[80:81], v[88:89], off offset:1024
	global_load_dwordx2 v[82:83], v[88:89], off offset:1536
	global_load_dwordx2 v[102:103], v[88:89], off offset:2048
	global_load_dwordx2 v[100:101], v[88:89], off offset:2560
	global_load_dwordx2 v[98:99], v[88:89], off offset:3072
	global_load_dwordx2 v[96:97], v[88:89], off offset:3584
	global_load_dwordx2 v[160:161], v[90:91], off
	global_load_dwordx2 v[158:159], v[90:91], off offset:512
	global_load_dwordx2 v[156:157], v[90:91], off offset:1024
	global_load_dwordx2 v[154:155], v[90:91], off offset:1536
	s_mov_b32 s4, 0xf800000
	s_ashr_i32 s9, s8, 31
	s_lshl_b64 s[0:1], s[8:9], 12
	global_load_dwordx2 v[168:169], v[90:91], off offset:2048
	global_load_dwordx2 v[166:167], v[90:91], off offset:2560
	global_load_dwordx2 v[164:165], v[90:91], off offset:3072
	global_load_dwordx2 v[162:163], v[90:91], off offset:3584
	v_lshl_add_u64 v[90:91], v[128:129], 0, s[0:1]
	global_load_dwordx2 v[150:151], v[90:91], off
	global_load_dwordx2 v[146:147], v[90:91], off offset:512
	global_load_dwordx2 v[142:143], v[90:91], off offset:1024
	global_load_dwordx2 v[138:139], v[90:91], off offset:1536
	global_load_dwordx2 v[152:153], v[90:91], off offset:2048
	global_load_dwordx2 v[148:149], v[90:91], off offset:2560
	global_load_dwordx2 v[144:145], v[90:91], off offset:3072
	global_load_dwordx2 v[140:141], v[90:91], off offset:3584
	s_cmpk_gt_i32 s24, 0x3fff
	s_waitcnt vmcnt(31)
	v_lshlrev_b32_e32 v88, 16, v78
	v_and_b32_e32 v89, 0xffff0000, v78
	v_lshlrev_b32_e32 v78, 16, v79
	v_and_b32_e32 v79, 0xffff0000, v79
	s_waitcnt vmcnt(30)
	v_lshlrev_b32_e32 v92, 16, v76
	v_and_b32_e32 v93, 0xffff0000, v76
	v_lshlrev_b32_e32 v76, 16, v77
	v_and_b32_e32 v77, 0xffff0000, v77
	v_mul_f32_e32 v114, v89, v89
	v_mul_f32_e32 v115, v79, v79
	v_mul_f32_e32 v116, v93, v93
	v_mul_f32_e32 v117, v77, v77
	v_fmac_f32_e32 v114, v88, v88
	v_fmac_f32_e32 v115, v78, v78
	v_fmac_f32_e32 v116, v92, v92
	v_fmac_f32_e32 v117, v76, v76
	s_waitcnt vmcnt(29)
	v_lshlrev_b32_e32 v94, 16, v74
	v_and_b32_e32 v95, 0xffff0000, v74
	v_lshlrev_b32_e32 v74, 16, v75
	v_and_b32_e32 v75, 0xffff0000, v75
	v_add_f32_e32 v114, v114, v115
	v_add_f32_e32 v115, v116, v117
	v_add_f32_e32 v114, v114, v115
	v_mul_f32_e32 v115, v95, v95
	v_mul_f32_e32 v116, v75, v75
	v_fmac_f32_e32 v115, v94, v94
	v_fmac_f32_e32 v116, v74, v74
	s_waitcnt vmcnt(28)
	v_lshlrev_b32_e32 v104, 16, v72
	v_and_b32_e32 v105, 0xffff0000, v72
	v_lshlrev_b32_e32 v72, 16, v73
	v_and_b32_e32 v73, 0xffff0000, v73
	v_add_f32_e32 v115, v115, v116
	v_add_f32_e32 v114, v115, v114
	v_mul_f32_e32 v115, v105, v105
	v_mul_f32_e32 v116, v73, v73
	v_fmac_f32_e32 v115, v104, v104
	v_fmac_f32_e32 v116, v72, v72
	s_waitcnt vmcnt(27)
	v_lshlrev_b32_e32 v106, 16, v70
	v_and_b32_e32 v107, 0xffff0000, v70
	v_lshlrev_b32_e32 v70, 16, v71
	v_and_b32_e32 v71, 0xffff0000, v71
	v_add_f32_e32 v115, v115, v116
	v_add_f32_e32 v114, v115, v114
	v_mul_f32_e32 v115, v107, v107
	v_mul_f32_e32 v116, v71, v71
	v_fmac_f32_e32 v115, v106, v106
	v_fmac_f32_e32 v116, v70, v70
	s_waitcnt vmcnt(26)
	v_lshlrev_b32_e32 v108, 16, v68
	v_and_b32_e32 v109, 0xffff0000, v68
	v_lshlrev_b32_e32 v68, 16, v69
	v_and_b32_e32 v69, 0xffff0000, v69
	v_add_f32_e32 v115, v115, v116
	v_add_f32_e32 v114, v115, v114
	v_mul_f32_e32 v115, v109, v109
	v_mul_f32_e32 v116, v69, v69
	v_fmac_f32_e32 v115, v108, v108
	v_fmac_f32_e32 v116, v68, v68
	s_waitcnt vmcnt(25)
	v_lshlrev_b32_e32 v110, 16, v66
	v_and_b32_e32 v111, 0xffff0000, v66
	v_lshlrev_b32_e32 v66, 16, v67
	v_and_b32_e32 v67, 0xffff0000, v67
	v_add_f32_e32 v115, v115, v116
	v_add_f32_e32 v114, v115, v114
	v_mul_f32_e32 v115, v111, v111
	v_mul_f32_e32 v116, v67, v67
	v_fmac_f32_e32 v115, v110, v110
	v_fmac_f32_e32 v116, v66, v66
	s_waitcnt vmcnt(24)
	v_lshlrev_b32_e32 v112, 16, v64
	v_and_b32_e32 v113, 0xffff0000, v64
	v_lshlrev_b32_e32 v64, 16, v65
	v_and_b32_e32 v65, 0xffff0000, v65
	v_add_f32_e32 v115, v115, v116
	v_add_f32_e32 v114, v115, v114
	v_mul_f32_e32 v115, v113, v113
	v_mul_f32_e32 v116, v65, v65
	v_fmac_f32_e32 v115, v112, v112
	v_fmac_f32_e32 v116, v64, v64
	v_add_f32_e32 v115, v115, v116
	v_add_f32_e32 v114, v115, v114
	s_nop 1
	v_add_f32_dpp v114, v114, v114 quad_perm:[1,0,3,2] row_mask:0xf bank_mask:0xf bound_ctrl:1
	s_nop 1
	v_add_f32_dpp v114, v114, v114 quad_perm:[2,3,0,1] row_mask:0xf bank_mask:0xf bound_ctrl:1
	s_nop 1
	v_add_f32_dpp v114, v114, v114 row_half_mirror row_mask:0xf bank_mask:0xf bound_ctrl:1
	s_nop 1
	v_add_f32_dpp v114, v114, v114 row_mirror row_mask:0xf bank_mask:0xf bound_ctrl:1
	ds_swizzle_b32 v115, v114 offset:swizzle(SWAP,16)
	s_waitcnt lgkmcnt(0)
	v_add_f32_e32 v114, v114, v115
	v_mov_b32_e32 v115, v114
	s_nop 1
	v_permlane32_swap_b32_e32 v114, v115
	v_add_f32_e32 v114, v114, v115
	v_fmamk_f32 v114, v114, 0x3a000000, v212
	v_mul_f32_e32 v115, 0x4f800000, v114
	v_cmp_gt_f32_e32 vcc, s4, v114
	s_mov_b32 s4, 0xdea00000
	s_nop 0
	v_cndmask_b32_e32 v114, v114, v115, vcc
	v_sqrt_f32_e32 v115, v114
	s_nop 0
	v_add_u32_e32 v116, -1, v115
	v_fma_f32 v117, -v116, v115, v114
	v_cmp_ge_f32_e64 s[36:37], 0, v117
	v_add_u32_e32 v117, 1, v115
	s_nop 0
	v_cndmask_b32_e64 v116, v115, v116, s[36:37]
	v_fma_f32 v115, -v117, v115, v114
	v_cmp_lt_f32_e64 s[36:37], 0, v115
	s_nop 1
	v_cndmask_b32_e64 v115, v116, v117, s[36:37]
	v_mul_f32_e32 v116, 0x37800000, v115
	v_cndmask_b32_e32 v115, v115, v116, vcc
	v_cmp_class_f32_e32 vcc, v114, v213
	s_nop 1
	v_cndmask_b32_e32 v114, v115, v114, vcc
	v_div_scale_f32 v115, s[18:19], v114, v114, 1.0
	v_rcp_f32_e32 v116, v115
	s_cselect_b64 s[18:19], -1, 0
	s_cmpk_lt_i32 s24, 0x4000
	v_fma_f32 v90, -v115, v116, 1.0
	v_fmac_f32_e32 v116, v90, v116
	v_div_scale_f32 v90, vcc, 1.0, v114, 1.0
	v_mul_f32_e32 v91, v90, v116
	v_fma_f32 v117, -v115, v91, v90
	v_fmac_f32_e32 v91, v117, v116
	v_fma_f32 v90, -v115, v91, v90
	v_div_fmas_f32 v90, v90, v116, v91
	v_div_fixup_f32 v90, v90, v114, 1.0
	v_pk_mul_f32 v[88:89], v[88:89], v[90:91] op_sel_hi:[1,0]
	v_pk_mul_f32 v[78:79], v[78:79], v[90:91] op_sel_hi:[1,0]
	v_pk_fma_f32 v[88:89], v[0:1], v[88:89], v[8:9]
	v_pk_fma_f32 v[78:79], v[2:3], v[78:79], v[10:11]
	v_bfe_u32 v91, v89, 16, 1
	v_add3_u32 v89, v89, v91, s33
	v_bfe_u32 v91, v88, 16, 1
	v_add3_u32 v88, v88, v91, s33
	v_lshrrev_b32_e32 v88, 16, v88
	v_and_or_b32 v88, v89, s96, v88
	v_bfe_u32 v89, v79, 16, 1
	v_add3_u32 v79, v79, v89, s33
	v_bfe_u32 v89, v78, 16, 1
	v_add3_u32 v78, v78, v89, s33
	v_lshrrev_b32_e32 v78, 16, v78
	v_and_or_b32 v89, v79, s96, v78
	v_add_co_u32_e32 v78, vcc, s4, v136
	v_pk_mul_f32 v[76:77], v[76:77], v[90:91] op_sel_hi:[1,0]
	s_nop 0
	v_addc_co_u32_e32 v79, vcc, -1, v137, vcc
	global_store_dwordx2 v[78:79], v[88:89], off sc1
	v_pk_mul_f32 v[78:79], v[92:93], v[90:91] op_sel_hi:[1,0]
	v_pk_fma_f32 v[76:77], v[6:7], v[76:77], v[14:15]
	v_pk_fma_f32 v[78:79], v[4:5], v[78:79], v[12:13]
	s_mov_b32 s4, 0xdea01000
	v_bfe_u32 v88, v79, 16, 1
	v_add3_u32 v79, v79, v88, s33
	v_bfe_u32 v88, v78, 16, 1
	v_add3_u32 v78, v78, v88, s33
	v_lshrrev_b32_e32 v78, 16, v78
	v_and_or_b32 v78, v79, s96, v78
	v_bfe_u32 v79, v77, 16, 1
	v_add3_u32 v77, v77, v79, s33
	v_bfe_u32 v79, v76, 16, 1
	v_add3_u32 v76, v76, v79, s33
	v_lshrrev_b32_e32 v76, 16, v76
	v_and_or_b32 v79, v77, s96, v76
	v_add_co_u32_e32 v76, vcc, s4, v136
	v_pk_mul_f32 v[74:75], v[74:75], v[90:91] op_sel_hi:[1,0]
	s_nop 0
	v_addc_co_u32_e32 v77, vcc, -1, v137, vcc
	global_store_dwordx2 v[76:77], v[78:79], off offset:-3584 sc1
	v_pk_mul_f32 v[78:79], v[94:95], v[90:91] op_sel_hi:[1,0]
	v_pk_fma_f32 v[74:75], v[18:19], v[74:75], v[26:27]
	v_pk_fma_f32 v[78:79], v[16:17], v[78:79], v[24:25]
	v_pk_mul_f32 v[72:73], v[72:73], v[90:91] op_sel_hi:[1,0]
	v_bfe_u32 v88, v79, 16, 1
	v_add3_u32 v79, v79, v88, s33
	v_bfe_u32 v88, v78, 16, 1
	v_add3_u32 v78, v78, v88, s33
	v_lshrrev_b32_e32 v78, 16, v78
	v_and_or_b32 v78, v79, s96, v78
	v_bfe_u32 v79, v75, 16, 1
	v_add3_u32 v75, v75, v79, s33
	v_bfe_u32 v79, v74, 16, 1
	v_add3_u32 v74, v74, v79, s33
	v_lshrrev_b32_e32 v74, 16, v74
	v_and_or_b32 v79, v75, s96, v74
	v_pk_mul_f32 v[74:75], v[104:105], v[90:91] op_sel_hi:[1,0]
	global_store_dwordx2 v[76:77], v[78:79], off offset:-3072 sc1
	v_pk_fma_f32 v[74:75], v[74:75], v[20:21], v[28:29]
	v_pk_fma_f32 v[72:73], v[72:73], v[22:23], v[30:31]
	v_bfe_u32 v78, v75, 16, 1
	v_add3_u32 v75, v75, v78, s33
	v_bfe_u32 v78, v74, 16, 1
	v_add3_u32 v74, v74, v78, s33
	v_lshrrev_b32_e32 v74, 16, v74
	v_and_or_b32 v74, v75, s96, v74
	v_bfe_u32 v75, v73, 16, 1
	v_add3_u32 v73, v73, v75, s33
	v_bfe_u32 v75, v72, 16, 1
	v_add3_u32 v72, v72, v75, s33
	v_lshrrev_b32_e32 v72, 16, v72
	v_and_or_b32 v75, v73, s96, v72
	v_pk_mul_f32 v[72:73], v[106:107], v[90:91] op_sel_hi:[1,0]
	global_store_dwordx2 v[76:77], v[74:75], off offset:-2560 sc1
	v_pk_fma_f32 v[72:73], v[72:73], v[32:33], v[40:41]
	v_pk_mul_f32 v[70:71], v[70:71], v[90:91] op_sel_hi:[1,0]
	v_bfe_u32 v74, v73, 16, 1
	v_add3_u32 v73, v73, v74, s33
	v_bfe_u32 v74, v72, 16, 1
	v_add3_u32 v72, v72, v74, s33
	v_pk_fma_f32 v[70:71], v[70:71], v[34:35], v[42:43]
	v_lshrrev_b32_e32 v72, 16, v72
	v_and_or_b32 v72, v73, s96, v72
	v_bfe_u32 v73, v71, 16, 1
	v_add3_u32 v71, v71, v73, s33
	v_bfe_u32 v73, v70, 16, 1
	v_add3_u32 v70, v70, v73, s33
	v_lshrrev_b32_e32 v70, 16, v70
	v_and_or_b32 v73, v71, s96, v70
	v_pk_mul_f32 v[70:71], v[108:109], v[90:91] op_sel_hi:[1,0]
	global_store_dwordx2 v[76:77], v[72:73], off offset:-2048 sc1
	v_pk_fma_f32 v[70:71], v[70:71], v[36:37], v[44:45]
	v_pk_mul_f32 v[68:69], v[68:69], v[90:91] op_sel_hi:[1,0]
	v_bfe_u32 v72, v71, 16, 1
	v_add3_u32 v71, v71, v72, s33
	v_bfe_u32 v72, v70, 16, 1
	v_add3_u32 v70, v70, v72, s33
	v_pk_fma_f32 v[68:69], v[68:69], v[38:39], v[46:47]
	v_lshrrev_b32_e32 v70, 16, v70
	v_and_or_b32 v70, v71, s96, v70
	v_bfe_u32 v71, v69, 16, 1
	v_add3_u32 v69, v69, v71, s33
	v_bfe_u32 v71, v68, 16, 1
	v_add3_u32 v68, v68, v71, s33
	v_lshrrev_b32_e32 v68, 16, v68
	v_and_or_b32 v71, v69, s96, v68
	v_pk_mul_f32 v[68:69], v[110:111], v[90:91] op_sel_hi:[1,0]
	global_store_dwordx2 v[76:77], v[70:71], off offset:-1536 sc1
	v_pk_fma_f32 v[68:69], v[68:69], v[48:49], v[56:57]
	v_pk_mul_f32 v[66:67], v[66:67], v[90:91] op_sel_hi:[1,0]
	v_bfe_u32 v70, v69, 16, 1
	v_add3_u32 v69, v69, v70, s33
	v_bfe_u32 v70, v68, 16, 1
	v_add3_u32 v68, v68, v70, s33
	v_pk_fma_f32 v[66:67], v[66:67], v[50:51], v[58:59]
	v_lshrrev_b32_e32 v68, 16, v68
	v_and_or_b32 v68, v69, s96, v68
	v_bfe_u32 v69, v67, 16, 1
	v_add3_u32 v67, v67, v69, s33
	v_bfe_u32 v69, v66, 16, 1
	v_add3_u32 v66, v66, v69, s33
	v_lshrrev_b32_e32 v66, 16, v66
	v_and_or_b32 v69, v67, s96, v66
	v_pk_mul_f32 v[66:67], v[112:113], v[90:91] op_sel_hi:[1,0]
	global_store_dwordx2 v[76:77], v[68:69], off offset:-1024 sc1
	v_pk_fma_f32 v[66:67], v[66:67], v[52:53], v[60:61]
	v_pk_mul_f32 v[64:65], v[64:65], v[90:91] op_sel_hi:[1,0]
	v_bfe_u32 v68, v67, 16, 1
	v_add3_u32 v67, v67, v68, s33
	v_bfe_u32 v68, v66, 16, 1
	v_add3_u32 v66, v66, v68, s33
	v_pk_fma_f32 v[64:65], v[64:65], v[54:55], v[62:63]
	v_lshrrev_b32_e32 v66, 16, v66
	v_and_or_b32 v66, v67, s96, v66
	v_bfe_u32 v67, v65, 16, 1
	v_add3_u32 v65, v65, v67, s33
	v_bfe_u32 v67, v64, 16, 1
	v_add3_u32 v64, v64, v67, s33
	v_lshrrev_b32_e32 v64, 16, v64
	v_and_or_b32 v67, v65, s96, v64
	global_store_dwordx2 v[76:77], v[66:67], off offset:-512 sc1
	s_waitcnt vmcnt(31)
	v_lshlrev_b32_e32 v92, 16, v86
	v_and_b32_e32 v93, 0xffff0000, v86
	v_lshlrev_b32_e32 v94, 16, v87
	v_and_b32_e32 v95, 0xffff0000, v87
	s_waitcnt vmcnt(30)
	v_lshlrev_b32_e32 v88, 16, v84
	v_and_b32_e32 v89, 0xffff0000, v84
	v_lshlrev_b32_e32 v90, 16, v85
	v_and_b32_e32 v91, 0xffff0000, v85
	s_waitcnt vmcnt(29)
	v_lshlrev_b32_e32 v84, 16, v80
	v_and_b32_e32 v85, 0xffff0000, v80
	v_lshlrev_b32_e32 v86, 16, v81
	v_and_b32_e32 v87, 0xffff0000, v81
	s_waitcnt vmcnt(28)
	v_lshlrev_b32_e32 v80, 16, v82
	v_and_b32_e32 v81, 0xffff0000, v82
	v_lshlrev_b32_e32 v82, 16, v83
	v_and_b32_e32 v83, 0xffff0000, v83
	s_waitcnt vmcnt(27)
	v_lshlrev_b32_e32 v76, 16, v102
	v_and_b32_e32 v77, 0xffff0000, v102
	v_lshlrev_b32_e32 v78, 16, v103
	v_and_b32_e32 v79, 0xffff0000, v103
	s_waitcnt vmcnt(26)
	v_lshlrev_b32_e32 v72, 16, v100
	v_and_b32_e32 v73, 0xffff0000, v100
	v_lshlrev_b32_e32 v74, 16, v101
	v_and_b32_e32 v75, 0xffff0000, v101
	s_waitcnt vmcnt(25)
	v_lshlrev_b32_e32 v68, 16, v98
	v_and_b32_e32 v69, 0xffff0000, v98
	v_lshlrev_b32_e32 v70, 16, v99
	v_and_b32_e32 v71, 0xffff0000, v99
	s_waitcnt vmcnt(24)
	v_lshlrev_b32_e32 v64, 16, v96
	v_and_b32_e32 v65, 0xffff0000, v96
	v_lshlrev_b32_e32 v66, 16, v97
	v_and_b32_e32 v67, 0xffff0000, v97
	s_cbranch_scc1 .LBB0_1263
	s_add_i32 s4, s24, 0xffffc000
	s_lshl_b64 s[20:21], s[4:5], 13
	v_lshl_add_u64 v[96:97], v[130:131], 0, s[20:21]
	v_add_co_u32_e32 v126, vcc, 0x200000, v96
	global_load_dwordx4 v[98:101], v[96:97], off
	s_nop 0
	v_addc_co_u32_e32 v127, vcc, 0, v97, vcc
	global_load_dwordx4 v[102:105], v[126:127], off
	global_load_dwordx4 v[106:109], v[96:97], off offset:1024
	global_load_dwordx4 v[110:113], v[126:127], off offset:1024
	global_load_dwordx4 v[114:117], v[96:97], off offset:2048
	global_load_dwordx4 v[118:121], v[126:127], off offset:2048
	global_load_dwordx4 v[122:125], v[96:97], off offset:3072
	global_load_dwordx4 v[170:173], v[126:127], off offset:3072
	v_add_co_u32_e32 v126, vcc, s26, v96
	s_mov_b32 s9, 0x201000
	s_nop 0
	v_addc_co_u32_e32 v127, vcc, 0, v97, vcc
	global_load_dwordx4 v[174:177], v[126:127], off
	v_add_co_u32_e32 v182, vcc, s9, v96
	s_mov_b32 s25, 0x400000
	s_nop 0
	v_addc_co_u32_e32 v183, vcc, 0, v97, vcc
	global_load_dwordx4 v[178:181], v[182:183], off
	global_load_dwordx4 v[194:197], v[126:127], off offset:1024
	global_load_dwordx4 v[198:201], v[182:183], off offset:1024
	global_load_dwordx4 v[202:205], v[126:127], off offset:2048
	global_load_dwordx4 v[206:209], v[182:183], off offset:2048
	global_load_dwordx4 v[226:229], v[126:127], off offset:3072
	global_load_dwordx4 v[230:233], v[182:183], off offset:3072
	s_mov_b32 s9, 0x401000
	s_mov_b32 s27, 0x600000
	s_mov_b32 s24, 0x800000
	s_mov_b32 s28, 0xa00000
	s_mov_b32 s29, 0xc00000
	s_mov_b32 s31, 0xe00000
	s_waitcnt vmcnt(13)
	v_pk_add_f32 v[90:91], v[90:91], v[108:109]
	v_pk_add_f32 v[88:89], v[88:89], v[106:107]
	v_pk_add_f32 v[92:93], v[92:93], v[98:99]
	v_pk_add_f32 v[94:95], v[94:95], v[100:101]
	s_waitcnt vmcnt(9)
	v_pk_add_f32 v[80:81], v[80:81], v[122:123]
	v_pk_add_f32 v[86:87], v[86:87], v[116:117]
	s_waitcnt vmcnt(8)
	v_pk_add_f32 v[80:81], v[80:81], v[170:171]
	v_pk_add_f32 v[84:85], v[84:85], v[114:115]
	v_pk_add_f32 v[82:83], v[82:83], v[124:125]
	v_pk_add_f32 v[92:93], v[92:93], v[102:103]
	v_pk_add_f32 v[94:95], v[94:95], v[104:105]
	s_waitcnt vmcnt(7)
	v_pk_add_f32 v[78:79], v[78:79], v[176:177]
	v_pk_add_f32 v[98:99], v[76:77], v[174:175]
	s_waitcnt vmcnt(6)
	v_pk_add_f32 v[76:77], v[78:79], v[180:181]
	v_pk_add_f32 v[78:79], v[98:99], v[178:179]
	s_waitcnt vmcnt(5)
	v_pk_add_f32 v[74:75], v[74:75], v[196:197]
	v_pk_add_f32 v[98:99], v[72:73], v[194:195]
	s_waitcnt vmcnt(4)
	v_pk_add_f32 v[72:73], v[74:75], v[200:201]
	v_pk_add_f32 v[74:75], v[98:99], v[198:199]
	s_waitcnt vmcnt(3)
	v_pk_add_f32 v[70:71], v[70:71], v[204:205]
	v_pk_add_f32 v[98:99], v[68:69], v[202:203]
	s_waitcnt vmcnt(2)
	v_pk_add_f32 v[68:69], v[70:71], v[208:209]
	v_pk_add_f32 v[70:71], v[98:99], v[206:207]
	s_waitcnt vmcnt(1)
	v_pk_add_f32 v[66:67], v[66:67], v[228:229]
	v_pk_add_f32 v[98:99], v[64:65], v[226:227]
	s_waitcnt vmcnt(0)
	v_pk_add_f32 v[64:65], v[66:67], v[232:233]
	v_pk_add_f32 v[66:67], v[98:99], v[230:231]
	v_add_co_u32_e32 v98, vcc, s25, v96
	v_pk_add_f32 v[88:89], v[88:89], v[110:111]
	s_nop 0
	v_addc_co_u32_e32 v99, vcc, 0, v97, vcc
	v_add_co_u32_e32 v182, vcc, s9, v96
	s_mov_b32 s9, 0x601000
	s_nop 0
	v_addc_co_u32_e32 v183, vcc, 0, v97, vcc
	v_add_co_u32_e32 v170, vcc, s27, v96
	v_pk_add_f32 v[90:91], v[90:91], v[112:113]
	s_nop 0
	v_addc_co_u32_e32 v171, vcc, 0, v97, vcc
	v_add_co_u32_e32 v210, vcc, s9, v96
	v_pk_add_f32 v[84:85], v[84:85], v[118:119]
	s_nop 0
	v_addc_co_u32_e32 v211, vcc, 0, v97, vcc
	v_pk_add_f32 v[86:87], v[86:87], v[120:121]
	v_pk_add_f32 v[82:83], v[82:83], v[172:173]
	global_load_dwordx4 v[100:103], v[182:183], off offset:-4096
	global_load_dwordx4 v[104:107], v[210:211], off offset:-4096
	global_load_dwordx4 v[108:111], v[98:99], off offset:1024
	global_load_dwordx4 v[112:115], v[170:171], off offset:1024
	global_load_dwordx4 v[116:119], v[98:99], off offset:2048
	global_load_dwordx4 v[120:123], v[170:171], off offset:2048
	global_load_dwordx4 v[124:127], v[98:99], off offset:3072
	s_nop 0
	global_load_dwordx4 v[170:173], v[170:171], off offset:3072
	s_nop 0
	global_load_dwordx4 v[174:177], v[182:183], off
	global_load_dwordx4 v[178:181], v[210:211], off
	global_load_dwordx4 v[194:197], v[182:183], off offset:1024
	global_load_dwordx4 v[198:201], v[210:211], off offset:1024
	global_load_dwordx4 v[202:205], v[182:183], off offset:2048
	global_load_dwordx4 v[206:209], v[210:211], off offset:2048
	global_load_dwordx4 v[226:229], v[182:183], off offset:3072
	global_load_dwordx4 v[230:233], v[210:211], off offset:3072
	s_mov_b32 s9, 0x801000
	s_waitcnt vmcnt(13)
	v_pk_add_f32 v[88:89], v[88:89], v[108:109]
	s_waitcnt vmcnt(12)
	v_pk_add_f32 v[218:219], v[88:89], v[112:113]
	v_add_co_u32_e32 v88, vcc, s24, v96
	s_waitcnt vmcnt(11)
	v_pk_add_f32 v[86:87], v[86:87], v[118:119]
	v_addc_co_u32_e32 v89, vcc, 0, v97, vcc
	s_waitcnt vmcnt(10)
	v_pk_add_f32 v[234:235], v[86:87], v[122:123]
	v_add_co_u32_e32 v122, vcc, s9, v96
	s_waitcnt vmcnt(9)
	v_pk_add_f32 v[82:83], v[82:83], v[126:127]
	v_addc_co_u32_e32 v123, vcc, 0, v97, vcc
	s_waitcnt vmcnt(1)
	v_pk_add_f32 v[64:65], v[64:65], v[228:229]
	v_pk_add_f32 v[66:67], v[66:67], v[226:227]
	s_waitcnt vmcnt(0)
	v_pk_add_f32 v[232:233], v[64:65], v[232:233]
	v_pk_add_f32 v[230:231], v[66:67], v[230:231]
	global_load_dwordx4 v[64:67], v[122:123], off offset:-4096
	v_pk_add_f32 v[92:93], v[92:93], v[100:101]
	v_pk_add_f32 v[76:77], v[76:77], v[176:177]
	v_pk_add_f32 v[210:211], v[92:93], v[104:105]
	v_add_co_u32_e32 v92, vcc, s28, v96
	s_mov_b32 s9, 0xa01000
	s_nop 0
	v_addc_co_u32_e32 v93, vcc, 0, v97, vcc
	v_pk_add_f32 v[126:127], v[82:83], v[172:173]
	v_pk_add_f32 v[172:173], v[76:77], v[180:181]
	v_add_co_u32_e32 v180, vcc, s9, v96
	v_pk_add_f32 v[94:95], v[94:95], v[102:103]
	v_pk_add_f32 v[90:91], v[90:91], v[110:111]
	v_pk_add_f32 v[84:85], v[84:85], v[116:117]
	v_pk_add_f32 v[80:81], v[80:81], v[124:125]
	v_pk_add_f32 v[78:79], v[78:79], v[174:175]
	v_pk_add_f32 v[72:73], v[72:73], v[196:197]
	v_pk_add_f32 v[74:75], v[74:75], v[194:195]
	v_pk_add_f32 v[68:69], v[68:69], v[204:205]
	v_pk_add_f32 v[70:71], v[70:71], v[202:203]
	v_addc_co_u32_e32 v181, vcc, 0, v97, vcc
	v_pk_add_f32 v[182:183], v[94:95], v[106:107]
	v_pk_add_f32 v[216:217], v[90:91], v[114:115]
	v_pk_add_f32 v[236:237], v[84:85], v[120:121]
	v_pk_add_f32 v[170:171], v[80:81], v[170:171]
	v_pk_add_f32 v[174:175], v[78:79], v[178:179]
	v_pk_add_f32 v[176:177], v[72:73], v[200:201]
	v_pk_add_f32 v[178:179], v[74:75], v[198:199]
	v_pk_add_f32 v[238:239], v[68:69], v[208:209]
	v_pk_add_f32 v[240:241], v[70:71], v[206:207]
	global_load_dwordx4 v[68:71], v[180:181], off offset:-4096
	global_load_dwordx4 v[72:75], v[88:89], off offset:1024
	global_load_dwordx4 v[76:79], v[92:93], off offset:1024
	global_load_dwordx4 v[80:83], v[88:89], off offset:2048
	global_load_dwordx4 v[84:87], v[92:93], off offset:2048
	s_nop 0
	global_load_dwordx4 v[88:91], v[88:89], off offset:3072
	s_nop 0
	global_load_dwordx4 v[92:95], v[92:93], off offset:3072
	s_nop 0
	global_load_dwordx4 v[98:101], v[122:123], off
	global_load_dwordx4 v[102:105], v[180:181], off
	global_load_dwordx4 v[106:109], v[122:123], off offset:1024
	global_load_dwordx4 v[110:113], v[180:181], off offset:1024
	global_load_dwordx4 v[114:117], v[122:123], off offset:2048
	global_load_dwordx4 v[118:121], v[180:181], off offset:2048
	s_nop 0
	global_load_dwordx4 v[122:125], v[122:123], off offset:3072
	s_nop 0
	global_load_dwordx4 v[226:229], v[180:181], off offset:3072
	s_mov_b32 s9, 0xc01000
	s_waitcnt vmcnt(15)
	v_pk_add_f32 v[64:65], v[210:211], v[64:65]
	v_pk_add_f32 v[66:67], v[182:183], v[66:67]
	s_waitcnt vmcnt(14)
	v_pk_add_f32 v[210:211], v[64:65], v[68:69]
	s_waitcnt vmcnt(13)
	v_pk_add_f32 v[64:65], v[216:217], v[74:75]
	v_pk_add_f32 v[208:209], v[66:67], v[70:71]
	v_pk_add_f32 v[66:67], v[218:219], v[72:73]
	s_waitcnt vmcnt(12)
	v_pk_add_f32 v[204:205], v[64:65], v[78:79]
	s_waitcnt vmcnt(11)
	v_pk_add_f32 v[64:65], v[234:235], v[82:83]
	v_pk_add_f32 v[206:207], v[66:67], v[76:77]
	v_pk_add_f32 v[66:67], v[236:237], v[80:81]
	s_waitcnt vmcnt(10)
	v_pk_add_f32 v[200:201], v[64:65], v[86:87]
	s_waitcnt vmcnt(9)
	v_pk_add_f32 v[64:65], v[126:127], v[90:91]
	v_pk_add_f32 v[202:203], v[66:67], v[84:85]
	v_pk_add_f32 v[66:67], v[170:171], v[88:89]
	s_waitcnt vmcnt(8)
	v_pk_add_f32 v[196:197], v[64:65], v[94:95]
	s_waitcnt vmcnt(7)
	v_pk_add_f32 v[64:65], v[172:173], v[100:101]
	v_pk_add_f32 v[198:199], v[66:67], v[92:93]
	v_pk_add_f32 v[66:67], v[174:175], v[98:99]
	s_waitcnt vmcnt(6)
	v_pk_add_f32 v[182:183], v[64:65], v[104:105]
	s_waitcnt vmcnt(5)
	v_pk_add_f32 v[64:65], v[176:177], v[108:109]
	v_pk_add_f32 v[194:195], v[66:67], v[102:103]
	v_pk_add_f32 v[66:67], v[178:179], v[106:107]
	s_waitcnt vmcnt(4)
	v_pk_add_f32 v[178:179], v[64:65], v[112:113]
	s_waitcnt vmcnt(3)
	v_pk_add_f32 v[64:65], v[238:239], v[116:117]
	v_pk_add_f32 v[180:181], v[66:67], v[110:111]
	s_waitcnt vmcnt(2)
	v_pk_add_f32 v[174:175], v[64:65], v[120:121]
	s_waitcnt vmcnt(1)
	v_pk_add_f32 v[64:65], v[232:233], v[124:125]
	v_pk_add_f32 v[66:67], v[240:241], v[114:115]
	s_waitcnt vmcnt(0)
	v_pk_add_f32 v[170:171], v[64:65], v[228:229]
	v_add_co_u32_e32 v64, vcc, s29, v96
	v_pk_add_f32 v[176:177], v[66:67], v[118:119]
	v_pk_add_f32 v[66:67], v[230:231], v[122:123]
	v_addc_co_u32_e32 v65, vcc, 0, v97, vcc
	v_pk_add_f32 v[172:173], v[66:67], v[226:227]
	v_add_co_u32_e32 v66, vcc, s9, v96
	s_mov_b32 s9, 0xe01000
	s_nop 0
	v_addc_co_u32_e32 v67, vcc, 0, v97, vcc
	global_load_dwordx4 v[68:71], v[66:67], off offset:-4096
	v_add_co_u32_e32 v72, vcc, s31, v96
	s_waitcnt vmcnt(0)
	v_pk_add_f32 v[68:69], v[210:211], v[68:69]
	v_addc_co_u32_e32 v73, vcc, 0, v97, vcc
	v_add_co_u32_e32 v96, vcc, s9, v96
	v_pk_add_f32 v[70:71], v[208:209], v[70:71]
	s_nop 0
	v_addc_co_u32_e32 v97, vcc, 0, v97, vcc
	global_load_dwordx4 v[92:95], v[96:97], off offset:-4096
	global_load_dwordx4 v[84:87], v[64:65], off offset:1024
	global_load_dwordx4 v[88:91], v[72:73], off offset:1024
	global_load_dwordx4 v[120:123], v[64:65], off offset:2048
	global_load_dwordx4 v[124:127], v[72:73], off offset:2048
	global_load_dwordx4 v[80:83], v[64:65], off offset:3072
	global_load_dwordx4 v[116:119], v[72:73], off offset:3072
	global_load_dwordx4 v[76:79], v[66:67], off
	global_load_dwordx4 v[112:115], v[96:97], off
	s_nop 0
	global_load_dwordx4 v[72:75], v[66:67], off offset:1024
	global_load_dwordx4 v[108:111], v[96:97], off offset:1024
	global_load_dwordx4 v[100:103], v[66:67], off offset:2048
	global_load_dwordx4 v[104:107], v[96:97], off offset:2048
	s_nop 0
	global_load_dwordx4 v[64:67], v[66:67], off offset:3072
	s_nop 0
	global_load_dwordx4 v[96:99], v[96:97], off offset:3072
	v_cmp_ne_u32_e32 vcc, 1, v184
	s_and_b64 vcc, exec, vcc
	s_waitcnt vmcnt(14)
	v_pk_add_f32 v[92:93], v[68:69], v[92:93]
	s_waitcnt vmcnt(13)
	v_pk_add_f32 v[68:69], v[204:205], v[86:87]
	v_pk_add_f32 v[94:95], v[70:71], v[94:95]
	v_pk_add_f32 v[70:71], v[206:207], v[84:85]
	s_waitcnt vmcnt(12)
	v_pk_add_f32 v[90:91], v[68:69], v[90:91]
	s_waitcnt vmcnt(11)
	v_pk_add_f32 v[68:69], v[200:201], v[122:123]
	v_pk_add_f32 v[88:89], v[70:71], v[88:89]
	v_pk_add_f32 v[70:71], v[202:203], v[120:121]
	s_waitcnt vmcnt(10)
	v_pk_add_f32 v[86:87], v[68:69], v[126:127]
	s_waitcnt vmcnt(9)
	v_pk_add_f32 v[68:69], v[196:197], v[82:83]
	v_pk_add_f32 v[84:85], v[70:71], v[124:125]
	v_pk_add_f32 v[70:71], v[198:199], v[80:81]
	s_waitcnt vmcnt(8)
	v_pk_add_f32 v[82:83], v[68:69], v[118:119]
	s_waitcnt vmcnt(7)
	v_pk_add_f32 v[68:69], v[182:183], v[78:79]
	v_pk_add_f32 v[80:81], v[70:71], v[116:117]
	v_pk_add_f32 v[70:71], v[194:195], v[76:77]
	s_waitcnt vmcnt(6)
	v_pk_add_f32 v[78:79], v[68:69], v[114:115]
	s_waitcnt vmcnt(5)
	v_pk_add_f32 v[68:69], v[178:179], v[74:75]
	v_pk_add_f32 v[76:77], v[70:71], v[112:113]
	v_pk_add_f32 v[70:71], v[180:181], v[72:73]
	s_waitcnt vmcnt(4)
	v_pk_add_f32 v[74:75], v[68:69], v[110:111]
	s_waitcnt vmcnt(3)
	v_pk_add_f32 v[68:69], v[174:175], v[102:103]
	v_pk_add_f32 v[100:101], v[176:177], v[100:101]
	s_waitcnt vmcnt(1)
	v_pk_add_f32 v[66:67], v[170:171], v[66:67]
	v_pk_add_f32 v[64:65], v[172:173], v[64:65]
	v_pk_add_f32 v[72:73], v[70:71], v[108:109]
	v_pk_add_f32 v[70:71], v[68:69], v[106:107]
	v_pk_add_f32 v[68:69], v[100:101], v[104:105]
	s_waitcnt vmcnt(0)
	v_pk_add_f32 v[66:67], v[66:67], v[98:99]
	v_pk_add_f32 v[64:65], v[64:65], v[96:97]
	s_cbranch_vccnz .LBB0_1264
	s_lshl_b64 s[20:21], s[4:5], 11
	v_lshl_add_u64 v[96:97], s[20:21], 2, v[132:133]
	global_store_dwordx4 v[96:97], v[92:95], off sc1
	global_store_dwordx4 v[96:97], v[88:91], off offset:1024 sc1
	global_store_dwordx4 v[96:97], v[84:87], off offset:2048 sc1
	global_store_dwordx4 v[96:97], v[80:83], off offset:3072 sc1
	v_add_co_u32_e32 v96, vcc, 0x1000, v96
	s_nop 1
	v_addc_co_u32_e32 v97, vcc, 0, v97, vcc
	global_store_dwordx4 v[96:97], v[76:79], off sc1
	global_store_dwordx4 v[96:97], v[72:75], off offset:1024 sc1
	global_store_dwordx4 v[96:97], v[68:71], off offset:2048 sc1
	global_store_dwordx4 v[96:97], v[64:67], off offset:3072 sc1
	s_branch .LBB0_1264

.LBB0_1264:
	v_mul_f32_e32 v96, v93, v93
	v_mul_f32_e32 v97, v95, v95
	v_fmac_f32_e32 v96, v92, v92
	v_fmac_f32_e32 v97, v94, v94
	v_add_f32_e32 v96, v96, v97
	v_mul_f32_e32 v97, v89, v89
	v_mul_f32_e32 v98, v91, v91
	v_fmac_f32_e32 v97, v88, v88
	v_fmac_f32_e32 v98, v90, v90
	v_add_f32_e32 v97, v97, v98
	v_add_f32_e32 v96, v96, v97
	v_mul_f32_e32 v97, v85, v85
	v_mul_f32_e32 v98, v87, v87
	v_fmac_f32_e32 v97, v84, v84
	v_fmac_f32_e32 v98, v86, v86
	v_add_f32_e32 v97, v97, v98
	v_add_f32_e32 v96, v97, v96
	v_mul_f32_e32 v97, v81, v81
	v_mul_f32_e32 v98, v83, v83
	v_fmac_f32_e32 v97, v80, v80
	v_fmac_f32_e32 v98, v82, v82
	v_add_f32_e32 v97, v97, v98
	v_add_f32_e32 v96, v97, v96
	v_mul_f32_e32 v97, v77, v77
	v_mul_f32_e32 v98, v79, v79
	v_fmac_f32_e32 v97, v76, v76
	v_fmac_f32_e32 v98, v78, v78
	v_add_f32_e32 v97, v97, v98
	v_add_f32_e32 v96, v97, v96
	v_mul_f32_e32 v97, v73, v73
	v_mul_f32_e32 v98, v75, v75
	v_fmac_f32_e32 v97, v72, v72
	v_fmac_f32_e32 v98, v74, v74
	v_add_f32_e32 v97, v97, v98
	v_add_f32_e32 v96, v97, v96
	v_mul_f32_e32 v97, v69, v69
	v_mul_f32_e32 v98, v71, v71
	v_fmac_f32_e32 v97, v68, v68
	v_fmac_f32_e32 v98, v70, v70
	v_add_f32_e32 v97, v97, v98
	v_add_f32_e32 v96, v97, v96
	v_mul_f32_e32 v97, v65, v65
	v_mul_f32_e32 v98, v67, v67
	v_fmac_f32_e32 v97, v64, v64
	v_fmac_f32_e32 v98, v66, v66
	v_add_f32_e32 v97, v97, v98
	v_add_f32_e32 v96, v97, v96
	v_cmp_ne_u32_e32 vcc, 1, v184
	s_and_b64 vcc, exec, vcc
	v_add_f32_dpp v96, v96, v96 quad_perm:[1,0,3,2] row_mask:0xf bank_mask:0xf bound_ctrl:1
	s_nop 1
	v_add_f32_dpp v96, v96, v96 quad_perm:[2,3,0,1] row_mask:0xf bank_mask:0xf bound_ctrl:1
	s_nop 1
	v_add_f32_dpp v96, v96, v96 row_half_mirror row_mask:0xf bank_mask:0xf bound_ctrl:1
	s_nop 1
	v_add_f32_dpp v96, v96, v96 row_mirror row_mask:0xf bank_mask:0xf bound_ctrl:1
	ds_swizzle_b32 v97, v96 offset:swizzle(SWAP,16)
	s_waitcnt lgkmcnt(0)
	v_add_f32_e32 v96, v96, v97
	v_mov_b32_e32 v97, v96
	s_nop 1
	v_permlane32_swap_b32_e32 v96, v97
	s_cbranch_vccnz .LBB0_1266
	v_add_f32_e32 v96, v96, v97
	v_fmamk_f32 v96, v96, 0x3a000000, v212
	s_mov_b32 s9, 0xf800000
	v_cmp_gt_f32_e32 vcc, s9, v96
	v_mul_f32_e32 v97, 0x4f800000, v96
	s_and_b64 s[18:19], s[18:19], exec
	v_cndmask_b32_e32 v96, v96, v97, vcc
	v_sqrt_f32_e32 v97, v96
	s_cselect_b32 s4, 0x2000, 0
	v_add_u32_e32 v98, -1, v97
	v_fma_f32 v99, -v98, v97, v96
	v_cmp_ge_f32_e64 s[36:37], 0, v99
	v_add_u32_e32 v99, 1, v97
	s_nop 0
	v_cndmask_b32_e64 v98, v97, v98, s[36:37]
	v_fma_f32 v97, -v99, v97, v96
	v_cmp_lt_f32_e64 s[36:37], 0, v97
	s_nop 1
	v_cndmask_b32_e64 v97, v98, v99, s[36:37]
	v_mul_f32_e32 v98, 0x37800000, v97
	v_cndmask_b32_e32 v97, v97, v98, vcc
	v_cmp_class_f32_e32 vcc, v96, v213
	s_nop 1
	v_cndmask_b32_e32 v96, v97, v96, vcc
	v_div_scale_f32 v97, s[18:19], v96, v96, 1.0
	v_rcp_f32_e32 v98, v97
	s_nop 0
	v_fma_f32 v99, -v97, v98, 1.0
	v_fmac_f32_e32 v98, v99, v98
	v_div_scale_f32 v99, vcc, 1.0, v96, 1.0
	v_mul_f32_e32 v100, v99, v98
	v_fma_f32 v101, -v97, v100, v99
	v_fmac_f32_e32 v100, v101, v98
	v_fma_f32 v97, -v97, v100, v99
	v_div_fmas_f32 v97, v97, v98, v100
	v_div_fixup_f32 v98, v97, v96, 1.0
	v_pk_mul_f32 v[108:109], v[92:93], v[98:99] op_sel_hi:[1,0]
	v_add_u32_e32 v92, s4, v224
	ds_read_b128 v[100:103], v92
	ds_read_b128 v[104:107], v92 offset:16384
	v_pk_mul_f32 v[94:95], v[94:95], v[98:99] op_sel_hi:[1,0]
	v_lshl_add_u64 v[96:97], v[134:135], 0, s[16:17]
	s_waitcnt lgkmcnt(0)
	v_pk_fma_f32 v[100:101], v[108:109], v[100:101], v[104:105]
	s_nop 0
	v_bfe_u32 v99, v100, 16, 1
	v_bfe_u32 v93, v101, 16, 1
	v_add3_u32 v99, v100, v99, s33
	v_pk_fma_f32 v[94:95], v[94:95], v[102:103], v[106:107]
	v_add3_u32 v93, v101, v93, s33
	v_lshrrev_b32_e32 v99, 16, v99
	v_and_or_b32 v100, v93, s96, v99
	v_bfe_u32 v93, v95, 16, 1
	v_add3_u32 v93, v95, v93, s33
	v_bfe_u32 v95, v94, 16, 1
	v_add3_u32 v94, v94, v95, s33
	v_lshrrev_b32_e32 v94, 16, v94
	v_and_or_b32 v101, v93, s96, v94
	global_store_dwordx2 v[96:97], v[100:101], off sc1
	v_pk_mul_f32 v[94:95], v[88:89], v[98:99] op_sel_hi:[1,0]
	v_pk_mul_f32 v[104:105], v[90:91], v[98:99] op_sel_hi:[1,0]
	ds_read_b128 v[88:91], v92 offset:1024
	ds_read_b128 v[100:103], v92 offset:17408
	s_waitcnt lgkmcnt(0)
	v_pk_fma_f32 v[88:89], v[94:95], v[88:89], v[100:101]
	s_nop 0
	v_bfe_u32 v93, v89, 16, 1
	v_add3_u32 v89, v89, v93, s33
	v_bfe_u32 v93, v88, 16, 1
	v_add3_u32 v88, v88, v93, s33
	v_pk_fma_f32 v[90:91], v[104:105], v[90:91], v[102:103]
	v_lshrrev_b32_e32 v88, 16, v88
	v_and_or_b32 v88, v89, s96, v88
	v_bfe_u32 v89, v91, 16, 1
	v_add3_u32 v89, v91, v89, s33
	v_bfe_u32 v91, v90, 16, 1
	v_add3_u32 v90, v90, v91, s33
	v_lshrrev_b32_e32 v90, 16, v90
	v_and_or_b32 v89, v89, s96, v90
	global_store_dwordx2 v[96:97], v[88:89], off offset:512 sc1
	v_pk_mul_f32 v[94:95], v[84:85], v[98:99] op_sel_hi:[1,0]
	v_pk_mul_f32 v[100:101], v[86:87], v[98:99] op_sel_hi:[1,0]
	ds_read_b128 v[84:87], v92 offset:2048
	ds_read_b128 v[88:91], v92 offset:18432
	s_waitcnt lgkmcnt(0)
	v_pk_fma_f32 v[84:85], v[94:95], v[84:85], v[88:89]
	s_nop 0
	v_bfe_u32 v88, v85, 16, 1
	v_add3_u32 v85, v85, v88, s33
	v_bfe_u32 v88, v84, 16, 1
	v_add3_u32 v84, v84, v88, s33
	v_pk_fma_f32 v[86:87], v[100:101], v[86:87], v[90:91]
	v_lshrrev_b32_e32 v84, 16, v84
	v_and_or_b32 v84, v85, s96, v84
	v_bfe_u32 v85, v87, 16, 1
	v_add3_u32 v85, v87, v85, s33
	v_bfe_u32 v87, v86, 16, 1
	v_add3_u32 v86, v86, v87, s33
	v_lshrrev_b32_e32 v86, 16, v86
	v_and_or_b32 v85, v85, s96, v86
	global_store_dwordx2 v[96:97], v[84:85], off offset:1024 sc1
	v_pk_mul_f32 v[88:89], v[80:81], v[98:99] op_sel_hi:[1,0]
	v_pk_mul_f32 v[90:91], v[82:83], v[98:99] op_sel_hi:[1,0]
	ds_read_b128 v[80:83], v92 offset:3072
	ds_read_b128 v[84:87], v92 offset:19456
	s_waitcnt lgkmcnt(0)
	v_pk_fma_f32 v[80:81], v[88:89], v[80:81], v[84:85]
	s_nop 0
	v_bfe_u32 v84, v81, 16, 1
	v_add3_u32 v81, v81, v84, s33
	v_bfe_u32 v84, v80, 16, 1
	v_add3_u32 v80, v80, v84, s33
	v_pk_fma_f32 v[82:83], v[90:91], v[82:83], v[86:87]
	v_lshrrev_b32_e32 v80, 16, v80
	v_and_or_b32 v80, v81, s96, v80
	v_bfe_u32 v81, v83, 16, 1
	v_add3_u32 v81, v83, v81, s33
	v_bfe_u32 v83, v82, 16, 1
	v_add3_u32 v82, v82, v83, s33
	v_lshrrev_b32_e32 v82, 16, v82
	v_and_or_b32 v81, v81, s96, v82
	global_store_dwordx2 v[96:97], v[80:81], off offset:1536 sc1
	v_pk_mul_f32 v[84:85], v[76:77], v[98:99] op_sel_hi:[1,0]
	v_pk_mul_f32 v[86:87], v[78:79], v[98:99] op_sel_hi:[1,0]
	ds_read_b128 v[76:79], v92 offset:4096
	ds_read_b128 v[80:83], v92 offset:20480
	s_waitcnt lgkmcnt(0)
	v_pk_fma_f32 v[76:77], v[84:85], v[76:77], v[80:81]
	s_nop 0
	v_bfe_u32 v80, v77, 16, 1
	v_add3_u32 v77, v77, v80, s33
	v_bfe_u32 v80, v76, 16, 1
	v_add3_u32 v76, v76, v80, s33
	v_pk_fma_f32 v[78:79], v[86:87], v[78:79], v[82:83]
	v_lshrrev_b32_e32 v76, 16, v76
	v_and_or_b32 v76, v77, s96, v76
	v_bfe_u32 v77, v79, 16, 1
	v_add3_u32 v77, v79, v77, s33
	v_bfe_u32 v79, v78, 16, 1
	v_add3_u32 v78, v78, v79, s33
	v_lshrrev_b32_e32 v78, 16, v78
	v_and_or_b32 v77, v77, s96, v78
	global_store_dwordx2 v[96:97], v[76:77], off offset:2048 sc1
	v_pk_mul_f32 v[80:81], v[72:73], v[98:99] op_sel_hi:[1,0]
	v_pk_mul_f32 v[82:83], v[74:75], v[98:99] op_sel_hi:[1,0]
	ds_read_b128 v[72:75], v92 offset:5120
	ds_read_b128 v[76:79], v92 offset:21504
	s_waitcnt lgkmcnt(0)
	v_pk_fma_f32 v[72:73], v[80:81], v[72:73], v[76:77]
	s_nop 0
	v_bfe_u32 v76, v73, 16, 1
	v_add3_u32 v73, v73, v76, s33
	v_bfe_u32 v76, v72, 16, 1
	v_add3_u32 v72, v72, v76, s33
	v_pk_fma_f32 v[74:75], v[82:83], v[74:75], v[78:79]
	v_lshrrev_b32_e32 v72, 16, v72
	v_and_or_b32 v72, v73, s96, v72
	v_bfe_u32 v73, v75, 16, 1
	v_add3_u32 v73, v75, v73, s33
	v_bfe_u32 v75, v74, 16, 1
	v_add3_u32 v74, v74, v75, s33
	v_lshrrev_b32_e32 v74, 16, v74
	v_and_or_b32 v73, v73, s96, v74
	global_store_dwordx2 v[96:97], v[72:73], off offset:2560 sc1
	v_pk_mul_f32 v[76:77], v[68:69], v[98:99] op_sel_hi:[1,0]
	v_pk_mul_f32 v[78:79], v[70:71], v[98:99] op_sel_hi:[1,0]
	ds_read_b128 v[68:71], v92 offset:6144
	ds_read_b128 v[72:75], v92 offset:22528
	s_waitcnt lgkmcnt(0)
	v_pk_fma_f32 v[68:69], v[76:77], v[68:69], v[72:73]
	s_nop 0
	v_bfe_u32 v72, v69, 16, 1
	v_add3_u32 v69, v69, v72, s33
	v_bfe_u32 v72, v68, 16, 1
	v_add3_u32 v68, v68, v72, s33
	v_pk_fma_f32 v[70:71], v[78:79], v[70:71], v[74:75]
	v_lshrrev_b32_e32 v68, 16, v68
	v_and_or_b32 v68, v69, s96, v68
	v_bfe_u32 v69, v71, 16, 1
	v_add3_u32 v69, v71, v69, s33
	v_bfe_u32 v71, v70, 16, 1
	v_add3_u32 v70, v70, v71, s33
	v_lshrrev_b32_e32 v70, 16, v70
	v_and_or_b32 v69, v69, s96, v70
	global_store_dwordx2 v[96:97], v[68:69], off offset:3072 sc1
	v_pk_mul_f32 v[72:73], v[64:65], v[98:99] op_sel_hi:[1,0]
	v_pk_mul_f32 v[74:75], v[66:67], v[98:99] op_sel_hi:[1,0]
	ds_read_b128 v[64:67], v92 offset:7168
	ds_read_b128 v[68:71], v92 offset:23552
	s_waitcnt lgkmcnt(0)
	v_pk_fma_f32 v[64:65], v[72:73], v[64:65], v[68:69]
	s_nop 0
	v_bfe_u32 v68, v65, 16, 1
	v_add3_u32 v65, v65, v68, s33
	v_bfe_u32 v68, v64, 16, 1
	v_add3_u32 v64, v64, v68, s33
	v_pk_fma_f32 v[66:67], v[74:75], v[66:67], v[70:71]
	v_lshrrev_b32_e32 v64, 16, v64
	v_and_or_b32 v64, v65, s96, v64
	v_bfe_u32 v65, v67, 16, 1
	v_add3_u32 v65, v67, v65, s33
	v_bfe_u32 v67, v66, 16, 1
	v_add3_u32 v66, v66, v67, s33
	v_lshrrev_b32_e32 v66, 16, v66
	v_and_or_b32 v65, v65, s96, v66
	global_store_dwordx2 v[96:97], v[64:65], off offset:3584 sc1
.LBB0_1266:
	s_cmpk_gt_i32 s14, 0x3fff
	s_waitcnt vmcnt(23)
	v_lshlrev_b32_e32 v92, 16, v160
	v_and_b32_e32 v93, 0xffff0000, v160
	v_lshlrev_b32_e32 v94, 16, v161
	v_and_b32_e32 v95, 0xffff0000, v161
	s_waitcnt vmcnt(22)
	v_lshlrev_b32_e32 v88, 16, v158
	v_and_b32_e32 v89, 0xffff0000, v158
	v_lshlrev_b32_e32 v90, 16, v159
	v_and_b32_e32 v91, 0xffff0000, v159
	s_waitcnt vmcnt(21)
	v_lshlrev_b32_e32 v84, 16, v156
	v_and_b32_e32 v85, 0xffff0000, v156
	v_lshlrev_b32_e32 v86, 16, v157
	v_and_b32_e32 v87, 0xffff0000, v157
	s_waitcnt vmcnt(20)
	v_lshlrev_b32_e32 v80, 16, v154
	v_and_b32_e32 v81, 0xffff0000, v154
	v_lshlrev_b32_e32 v82, 16, v155
	v_and_b32_e32 v83, 0xffff0000, v155
	s_waitcnt vmcnt(19)
	v_lshlrev_b32_e32 v76, 16, v168
	v_and_b32_e32 v77, 0xffff0000, v168
	v_lshlrev_b32_e32 v78, 16, v169
	v_and_b32_e32 v79, 0xffff0000, v169
	s_waitcnt vmcnt(18)
	v_lshlrev_b32_e32 v72, 16, v166
	v_and_b32_e32 v73, 0xffff0000, v166
	v_lshlrev_b32_e32 v74, 16, v167
	v_and_b32_e32 v75, 0xffff0000, v167
	s_waitcnt vmcnt(17)
	v_lshlrev_b32_e32 v68, 16, v164
	v_and_b32_e32 v69, 0xffff0000, v164
	v_lshlrev_b32_e32 v70, 16, v165
	v_and_b32_e32 v71, 0xffff0000, v165
	s_waitcnt vmcnt(16)
	v_lshlrev_b32_e32 v64, 16, v162
	v_and_b32_e32 v65, 0xffff0000, v162
	v_lshlrev_b32_e32 v66, 16, v163
	v_and_b32_e32 v67, 0xffff0000, v163
	s_cselect_b64 s[16:17], -1, 0
	s_cmpk_lt_i32 s14, 0x4000
	v_cndmask_b32_e64 v184, 0, 1, s[12:13]
	s_cbranch_scc1 .LBB0_1269
	s_add_i32 s4, s14, 0xffffc000
	s_lshl_b64 s[14:15], s[4:5], 13
	v_lshl_add_u64 v[96:97], v[130:131], 0, s[14:15]
	v_add_co_u32_e32 v126, vcc, 0x200000, v96
	global_load_dwordx4 v[98:101], v[96:97], off
	s_nop 0
	v_addc_co_u32_e32 v127, vcc, 0, v97, vcc
	global_load_dwordx4 v[102:105], v[126:127], off
	global_load_dwordx4 v[106:109], v[96:97], off offset:1024
	global_load_dwordx4 v[110:113], v[126:127], off offset:1024
	global_load_dwordx4 v[114:117], v[96:97], off offset:2048
	global_load_dwordx4 v[118:121], v[126:127], off offset:2048
	global_load_dwordx4 v[122:125], v[96:97], off offset:3072
	global_load_dwordx4 v[154:157], v[126:127], off offset:3072
	v_add_co_u32_e32 v126, vcc, s26, v96
	s_mov_b32 s9, 0x201000
	s_nop 0
	v_addc_co_u32_e32 v127, vcc, 0, v97, vcc
	global_load_dwordx4 v[158:161], v[126:127], off
	v_add_co_u32_e32 v182, vcc, s9, v96
	s_mov_b32 s9, 0x401000
	s_nop 0
	v_addc_co_u32_e32 v183, vcc, 0, v97, vcc
	global_load_dwordx4 v[162:165], v[182:183], off
	global_load_dwordx4 v[166:169], v[126:127], off offset:1024
	global_load_dwordx4 v[170:173], v[182:183], off offset:1024
	global_load_dwordx4 v[174:177], v[126:127], off offset:2048
	global_load_dwordx4 v[178:181], v[182:183], off offset:2048
	global_load_dwordx4 v[194:197], v[126:127], off offset:3072
	global_load_dwordx4 v[198:201], v[182:183], off offset:3072
	s_waitcnt vmcnt(13)
	v_pk_add_f32 v[90:91], v[90:91], v[108:109]
	v_pk_add_f32 v[88:89], v[88:89], v[106:107]
	v_pk_add_f32 v[92:93], v[92:93], v[98:99]
	v_pk_add_f32 v[94:95], v[94:95], v[100:101]
	s_waitcnt vmcnt(9)
	v_pk_add_f32 v[80:81], v[80:81], v[122:123]
	v_pk_add_f32 v[86:87], v[86:87], v[116:117]
	s_waitcnt vmcnt(8)
	v_pk_add_f32 v[80:81], v[80:81], v[154:155]
	v_pk_add_f32 v[84:85], v[84:85], v[114:115]
	v_pk_add_f32 v[82:83], v[82:83], v[124:125]
	v_pk_add_f32 v[92:93], v[92:93], v[102:103]
	v_pk_add_f32 v[94:95], v[94:95], v[104:105]
	s_waitcnt vmcnt(7)
	v_pk_add_f32 v[78:79], v[78:79], v[160:161]
	v_pk_add_f32 v[98:99], v[76:77], v[158:159]
	s_waitcnt vmcnt(6)
	v_pk_add_f32 v[76:77], v[78:79], v[164:165]
	v_pk_add_f32 v[78:79], v[98:99], v[162:163]
	s_waitcnt vmcnt(5)
	v_pk_add_f32 v[74:75], v[74:75], v[168:169]
	v_pk_add_f32 v[98:99], v[72:73], v[166:167]
	s_waitcnt vmcnt(4)
	v_pk_add_f32 v[72:73], v[74:75], v[172:173]
	v_pk_add_f32 v[74:75], v[98:99], v[170:171]
	s_waitcnt vmcnt(3)
	v_pk_add_f32 v[70:71], v[70:71], v[176:177]
	v_pk_add_f32 v[98:99], v[68:69], v[174:175]
	s_waitcnt vmcnt(2)
	v_pk_add_f32 v[68:69], v[70:71], v[180:181]
	v_pk_add_f32 v[70:71], v[98:99], v[178:179]
	s_waitcnt vmcnt(1)
	v_pk_add_f32 v[66:67], v[66:67], v[196:197]
	v_pk_add_f32 v[98:99], v[64:65], v[194:195]
	s_waitcnt vmcnt(0)
	v_pk_add_f32 v[64:65], v[66:67], v[200:201]
	v_pk_add_f32 v[66:67], v[98:99], v[198:199]
	v_add_co_u32_e32 v98, vcc, s25, v96
	v_pk_add_f32 v[88:89], v[88:89], v[110:111]
	s_nop 0
	v_addc_co_u32_e32 v99, vcc, 0, v97, vcc
	v_add_co_u32_e32 v182, vcc, s9, v96
	s_mov_b32 s9, 0x601000
	s_nop 0
	v_addc_co_u32_e32 v183, vcc, 0, v97, vcc
	v_add_co_u32_e32 v154, vcc, s27, v96
	v_pk_add_f32 v[90:91], v[90:91], v[112:113]
	s_nop 0
	v_addc_co_u32_e32 v155, vcc, 0, v97, vcc
	v_add_co_u32_e32 v198, vcc, s9, v96
	v_pk_add_f32 v[84:85], v[84:85], v[118:119]
	s_nop 0
	v_addc_co_u32_e32 v199, vcc, 0, v97, vcc
	v_pk_add_f32 v[86:87], v[86:87], v[120:121]
	v_pk_add_f32 v[82:83], v[82:83], v[156:157]
	global_load_dwordx4 v[100:103], v[182:183], off offset:-4096
	global_load_dwordx4 v[104:107], v[198:199], off offset:-4096
	global_load_dwordx4 v[108:111], v[98:99], off offset:1024
	global_load_dwordx4 v[112:115], v[154:155], off offset:1024
	global_load_dwordx4 v[116:119], v[98:99], off offset:2048
	global_load_dwordx4 v[120:123], v[154:155], off offset:2048
	global_load_dwordx4 v[124:127], v[98:99], off offset:3072
	s_nop 0
	global_load_dwordx4 v[154:157], v[154:155], off offset:3072
	s_nop 0
	global_load_dwordx4 v[158:161], v[182:183], off
	global_load_dwordx4 v[162:165], v[198:199], off
	global_load_dwordx4 v[166:169], v[182:183], off offset:1024
	global_load_dwordx4 v[170:173], v[198:199], off offset:1024
	global_load_dwordx4 v[174:177], v[182:183], off offset:2048
	global_load_dwordx4 v[178:181], v[198:199], off offset:2048
	global_load_dwordx4 v[194:197], v[182:183], off offset:3072
	s_nop 0
	global_load_dwordx4 v[198:201], v[198:199], off offset:3072
	s_mov_b32 s9, 0x801000
	s_waitcnt vmcnt(13)
	v_pk_add_f32 v[88:89], v[88:89], v[108:109]
	s_waitcnt vmcnt(12)
	v_pk_add_f32 v[206:207], v[88:89], v[112:113]
	v_add_co_u32_e32 v88, vcc, s24, v96
	s_waitcnt vmcnt(11)
	v_pk_add_f32 v[86:87], v[86:87], v[118:119]
	v_addc_co_u32_e32 v89, vcc, 0, v97, vcc
	s_waitcnt vmcnt(10)
	v_pk_add_f32 v[208:209], v[86:87], v[122:123]
	v_add_co_u32_e32 v122, vcc, s9, v96
	s_waitcnt vmcnt(9)
	v_pk_add_f32 v[82:83], v[82:83], v[126:127]
	v_addc_co_u32_e32 v123, vcc, 0, v97, vcc
	s_waitcnt vmcnt(1)
	v_pk_add_f32 v[64:65], v[64:65], v[196:197]
	v_pk_add_f32 v[66:67], v[66:67], v[194:195]
	s_waitcnt vmcnt(0)
	v_pk_add_f32 v[200:201], v[64:65], v[200:201]
	v_pk_add_f32 v[226:227], v[66:67], v[198:199]
	global_load_dwordx4 v[64:67], v[122:123], off offset:-4096
	v_pk_add_f32 v[92:93], v[92:93], v[100:101]
	v_pk_add_f32 v[76:77], v[76:77], v[160:161]
	v_pk_add_f32 v[202:203], v[92:93], v[104:105]
	v_add_co_u32_e32 v92, vcc, s28, v96
	s_mov_b32 s9, 0xa01000
	s_nop 0
	v_addc_co_u32_e32 v93, vcc, 0, v97, vcc
	v_pk_add_f32 v[126:127], v[82:83], v[156:157]
	v_pk_add_f32 v[156:157], v[76:77], v[164:165]
	v_add_co_u32_e32 v164, vcc, s9, v96
	v_pk_add_f32 v[94:95], v[94:95], v[102:103]
	v_pk_add_f32 v[90:91], v[90:91], v[110:111]
	v_pk_add_f32 v[84:85], v[84:85], v[116:117]
	v_pk_add_f32 v[80:81], v[80:81], v[124:125]
	v_pk_add_f32 v[78:79], v[78:79], v[158:159]
	v_pk_add_f32 v[72:73], v[72:73], v[168:169]
	v_pk_add_f32 v[74:75], v[74:75], v[166:167]
	v_pk_add_f32 v[68:69], v[68:69], v[176:177]
	v_pk_add_f32 v[70:71], v[70:71], v[174:175]
	v_addc_co_u32_e32 v165, vcc, 0, v97, vcc
	v_pk_add_f32 v[182:183], v[94:95], v[106:107]
	v_pk_add_f32 v[204:205], v[90:91], v[114:115]
	v_pk_add_f32 v[210:211], v[84:85], v[120:121]
	v_pk_add_f32 v[154:155], v[80:81], v[154:155]
	v_pk_add_f32 v[158:159], v[78:79], v[162:163]
	v_pk_add_f32 v[160:161], v[72:73], v[172:173]
	v_pk_add_f32 v[162:163], v[74:75], v[170:171]
	v_pk_add_f32 v[216:217], v[68:69], v[180:181]
	v_pk_add_f32 v[218:219], v[70:71], v[178:179]
	global_load_dwordx4 v[68:71], v[164:165], off offset:-4096
	global_load_dwordx4 v[72:75], v[88:89], off offset:1024
	global_load_dwordx4 v[76:79], v[92:93], off offset:1024
	global_load_dwordx4 v[80:83], v[88:89], off offset:2048
	global_load_dwordx4 v[84:87], v[92:93], off offset:2048
	s_nop 0
	global_load_dwordx4 v[88:91], v[88:89], off offset:3072
	s_nop 0
	global_load_dwordx4 v[92:95], v[92:93], off offset:3072
	s_nop 0
	global_load_dwordx4 v[98:101], v[122:123], off
	global_load_dwordx4 v[102:105], v[164:165], off
	global_load_dwordx4 v[106:109], v[122:123], off offset:1024
	global_load_dwordx4 v[110:113], v[164:165], off offset:1024
	global_load_dwordx4 v[114:117], v[122:123], off offset:2048
	global_load_dwordx4 v[118:121], v[164:165], off offset:2048
	s_nop 0
	global_load_dwordx4 v[122:125], v[122:123], off offset:3072
	s_nop 0
	global_load_dwordx4 v[196:199], v[164:165], off offset:3072
	s_mov_b32 s9, 0xc01000
	s_waitcnt vmcnt(15)
	v_pk_add_f32 v[64:65], v[202:203], v[64:65]
	v_pk_add_f32 v[66:67], v[182:183], v[66:67]
	s_waitcnt vmcnt(14)
	v_pk_add_f32 v[194:195], v[64:65], v[68:69]
	s_waitcnt vmcnt(13)
	v_pk_add_f32 v[64:65], v[204:205], v[74:75]
	v_pk_add_f32 v[182:183], v[66:67], v[70:71]
	v_pk_add_f32 v[66:67], v[206:207], v[72:73]
	s_waitcnt vmcnt(12)
	v_pk_add_f32 v[178:179], v[64:65], v[78:79]
	s_waitcnt vmcnt(11)
	v_pk_add_f32 v[64:65], v[208:209], v[82:83]
	v_pk_add_f32 v[180:181], v[66:67], v[76:77]
	v_pk_add_f32 v[66:67], v[210:211], v[80:81]
	s_waitcnt vmcnt(10)
	v_pk_add_f32 v[174:175], v[64:65], v[86:87]
	s_waitcnt vmcnt(9)
	v_pk_add_f32 v[64:65], v[126:127], v[90:91]
	v_pk_add_f32 v[176:177], v[66:67], v[84:85]
	v_pk_add_f32 v[66:67], v[154:155], v[88:89]
	s_waitcnt vmcnt(8)
	v_pk_add_f32 v[170:171], v[64:65], v[94:95]
	s_waitcnt vmcnt(7)
	v_pk_add_f32 v[64:65], v[156:157], v[100:101]
	v_pk_add_f32 v[172:173], v[66:67], v[92:93]
	v_pk_add_f32 v[66:67], v[158:159], v[98:99]
	s_waitcnt vmcnt(6)
	v_pk_add_f32 v[166:167], v[64:65], v[104:105]
	s_waitcnt vmcnt(5)
	v_pk_add_f32 v[64:65], v[160:161], v[108:109]
	v_pk_add_f32 v[168:169], v[66:67], v[102:103]
	v_pk_add_f32 v[66:67], v[162:163], v[106:107]
	s_waitcnt vmcnt(4)
	v_pk_add_f32 v[162:163], v[64:65], v[112:113]
	s_waitcnt vmcnt(3)
	v_pk_add_f32 v[64:65], v[216:217], v[116:117]
	v_pk_add_f32 v[164:165], v[66:67], v[110:111]
	s_waitcnt vmcnt(2)
	v_pk_add_f32 v[158:159], v[64:65], v[120:121]
	s_waitcnt vmcnt(1)
	v_pk_add_f32 v[64:65], v[200:201], v[124:125]
	v_pk_add_f32 v[66:67], v[218:219], v[114:115]
	s_waitcnt vmcnt(0)
	v_pk_add_f32 v[154:155], v[64:65], v[198:199]
	v_add_co_u32_e32 v64, vcc, s29, v96
	v_pk_add_f32 v[160:161], v[66:67], v[118:119]
	v_pk_add_f32 v[66:67], v[226:227], v[122:123]
	v_addc_co_u32_e32 v65, vcc, 0, v97, vcc
	v_pk_add_f32 v[156:157], v[66:67], v[196:197]
	v_add_co_u32_e32 v66, vcc, s9, v96
	s_mov_b32 s9, 0xe01000
	s_nop 0
	v_addc_co_u32_e32 v67, vcc, 0, v97, vcc
	global_load_dwordx4 v[72:75], v[66:67], off offset:-4096
	v_add_co_u32_e32 v68, vcc, s31, v96
	s_waitcnt vmcnt(0)
	v_pk_add_f32 v[72:73], v[194:195], v[72:73]
	v_addc_co_u32_e32 v69, vcc, 0, v97, vcc
	v_add_co_u32_e32 v96, vcc, s9, v96
	v_pk_add_f32 v[74:75], v[182:183], v[74:75]
	s_nop 0
	v_addc_co_u32_e32 v97, vcc, 0, v97, vcc
	global_load_dwordx4 v[92:95], v[96:97], off offset:-4096
	global_load_dwordx4 v[84:87], v[64:65], off offset:1024
	global_load_dwordx4 v[88:91], v[68:69], off offset:1024
	global_load_dwordx4 v[120:123], v[64:65], off offset:2048
	global_load_dwordx4 v[124:127], v[68:69], off offset:2048
	global_load_dwordx4 v[80:83], v[64:65], off offset:3072
	global_load_dwordx4 v[116:119], v[68:69], off offset:3072
	global_load_dwordx4 v[76:79], v[66:67], off
	global_load_dwordx4 v[112:115], v[96:97], off
	global_load_dwordx4 v[104:107], v[66:67], off offset:1024
	global_load_dwordx4 v[108:111], v[96:97], off offset:1024
	s_nop 0
	global_load_dwordx4 v[68:71], v[66:67], off offset:2048
	global_load_dwordx4 v[100:103], v[96:97], off offset:2048
	s_nop 0
	global_load_dwordx4 v[64:67], v[66:67], off offset:3072
	s_nop 0
	global_load_dwordx4 v[96:99], v[96:97], off offset:3072
	s_andn2_b64 vcc, exec, s[12:13]
	s_waitcnt vmcnt(14)
	v_pk_add_f32 v[92:93], v[72:73], v[92:93]
	s_waitcnt vmcnt(13)
	v_pk_add_f32 v[72:73], v[178:179], v[86:87]
	v_pk_add_f32 v[94:95], v[74:75], v[94:95]
	v_pk_add_f32 v[74:75], v[180:181], v[84:85]
	s_waitcnt vmcnt(12)
	v_pk_add_f32 v[90:91], v[72:73], v[90:91]
	s_waitcnt vmcnt(11)
	v_pk_add_f32 v[72:73], v[174:175], v[122:123]
	v_pk_add_f32 v[88:89], v[74:75], v[88:89]
	v_pk_add_f32 v[74:75], v[176:177], v[120:121]
	s_waitcnt vmcnt(10)
	v_pk_add_f32 v[86:87], v[72:73], v[126:127]
	s_waitcnt vmcnt(9)
	v_pk_add_f32 v[72:73], v[170:171], v[82:83]
	v_pk_add_f32 v[84:85], v[74:75], v[124:125]
	v_pk_add_f32 v[74:75], v[172:173], v[80:81]
	s_waitcnt vmcnt(8)
	v_pk_add_f32 v[82:83], v[72:73], v[118:119]
	s_waitcnt vmcnt(7)
	v_pk_add_f32 v[72:73], v[166:167], v[78:79]
	v_pk_add_f32 v[80:81], v[74:75], v[116:117]
	v_pk_add_f32 v[74:75], v[168:169], v[76:77]
	s_waitcnt vmcnt(6)
	v_pk_add_f32 v[78:79], v[72:73], v[114:115]
	s_waitcnt vmcnt(5)
	v_pk_add_f32 v[72:73], v[162:163], v[106:107]
	v_pk_add_f32 v[104:105], v[164:165], v[104:105]
	s_waitcnt vmcnt(3)
	v_pk_add_f32 v[70:71], v[158:159], v[70:71]
	v_pk_add_f32 v[68:69], v[160:161], v[68:69]
	s_waitcnt vmcnt(1)
	v_pk_add_f32 v[66:67], v[154:155], v[66:67]
	v_pk_add_f32 v[64:65], v[156:157], v[64:65]
	v_pk_add_f32 v[76:77], v[74:75], v[112:113]
	v_pk_add_f32 v[74:75], v[72:73], v[110:111]
	v_pk_add_f32 v[72:73], v[104:105], v[108:109]
	v_pk_add_f32 v[70:71], v[70:71], v[102:103]
	v_pk_add_f32 v[68:69], v[68:69], v[100:101]
	s_waitcnt vmcnt(0)
	v_pk_add_f32 v[66:67], v[66:67], v[98:99]
	v_pk_add_f32 v[64:65], v[64:65], v[96:97]
	s_cbranch_vccnz .LBB0_1269
	s_lshl_b64 s[12:13], s[4:5], 11
	v_lshl_add_u64 v[96:97], s[12:13], 2, v[132:133]
	global_store_dwordx4 v[96:97], v[92:95], off sc1
	global_store_dwordx4 v[96:97], v[88:91], off offset:1024 sc1
	global_store_dwordx4 v[96:97], v[84:87], off offset:2048 sc1
	global_store_dwordx4 v[96:97], v[80:83], off offset:3072 sc1
	v_add_co_u32_e32 v96, vcc, 0x1000, v96
	s_nop 1
	v_addc_co_u32_e32 v97, vcc, 0, v97, vcc
	global_store_dwordx4 v[96:97], v[76:79], off sc1
	global_store_dwordx4 v[96:97], v[72:75], off offset:1024 sc1
	global_store_dwordx4 v[96:97], v[68:71], off offset:2048 sc1
	global_store_dwordx4 v[96:97], v[64:67], off offset:3072 sc1
.LBB0_1269:
	v_mul_f32_e32 v96, v93, v93
	v_mul_f32_e32 v97, v95, v95
	v_fmac_f32_e32 v96, v92, v92
	v_fmac_f32_e32 v97, v94, v94
	v_add_f32_e32 v96, v96, v97
	v_mul_f32_e32 v97, v89, v89
	v_mul_f32_e32 v98, v91, v91
	v_fmac_f32_e32 v97, v88, v88
	v_fmac_f32_e32 v98, v90, v90
	v_add_f32_e32 v97, v97, v98
	v_add_f32_e32 v96, v96, v97
	v_mul_f32_e32 v97, v85, v85
	v_mul_f32_e32 v98, v87, v87
	v_fmac_f32_e32 v97, v84, v84
	v_fmac_f32_e32 v98, v86, v86
	v_add_f32_e32 v97, v97, v98
	v_add_f32_e32 v96, v97, v96
	v_mul_f32_e32 v97, v81, v81
	v_mul_f32_e32 v98, v83, v83
	v_fmac_f32_e32 v97, v80, v80
	v_fmac_f32_e32 v98, v82, v82
	v_add_f32_e32 v97, v97, v98
	v_add_f32_e32 v96, v97, v96
	v_mul_f32_e32 v97, v77, v77
	v_mul_f32_e32 v98, v79, v79
	v_fmac_f32_e32 v97, v76, v76
	v_fmac_f32_e32 v98, v78, v78
	v_add_f32_e32 v97, v97, v98
	v_add_f32_e32 v96, v97, v96
	v_mul_f32_e32 v97, v73, v73
	v_mul_f32_e32 v98, v75, v75
	v_fmac_f32_e32 v97, v72, v72
	v_fmac_f32_e32 v98, v74, v74
	v_add_f32_e32 v97, v97, v98
	v_add_f32_e32 v96, v97, v96
	v_mul_f32_e32 v97, v69, v69
	v_mul_f32_e32 v98, v71, v71
	v_fmac_f32_e32 v97, v68, v68
	v_fmac_f32_e32 v98, v70, v70
	v_add_f32_e32 v97, v97, v98
	v_add_f32_e32 v96, v97, v96
	v_mul_f32_e32 v97, v65, v65
	v_mul_f32_e32 v98, v67, v67
	v_fmac_f32_e32 v97, v64, v64
	v_fmac_f32_e32 v98, v66, v66
	v_add_f32_e32 v97, v97, v98
	v_add_f32_e32 v96, v97, v96
	v_cmp_ne_u32_e32 vcc, 1, v184
	s_and_b64 vcc, exec, vcc
	v_add_f32_dpp v96, v96, v96 quad_perm:[1,0,3,2] row_mask:0xf bank_mask:0xf bound_ctrl:1
	s_nop 1
	v_add_f32_dpp v96, v96, v96 quad_perm:[2,3,0,1] row_mask:0xf bank_mask:0xf bound_ctrl:1
	s_nop 1
	v_add_f32_dpp v96, v96, v96 row_half_mirror row_mask:0xf bank_mask:0xf bound_ctrl:1
	s_nop 1
	v_add_f32_dpp v96, v96, v96 row_mirror row_mask:0xf bank_mask:0xf bound_ctrl:1
	ds_swizzle_b32 v97, v96 offset:swizzle(SWAP,16)
	s_waitcnt lgkmcnt(0)
	v_add_f32_e32 v96, v96, v97
	v_mov_b32_e32 v97, v96
	s_nop 1
	v_permlane32_swap_b32_e32 v96, v97
	s_cbranch_vccnz .LBB0_1271
	v_add_f32_e32 v96, v96, v97
	v_fmamk_f32 v96, v96, 0x3a000000, v212
	s_mov_b32 s9, 0xf800000
	v_cmp_gt_f32_e32 vcc, s9, v96
	v_mul_f32_e32 v97, 0x4f800000, v96
	s_and_b64 s[12:13], s[16:17], exec
	v_cndmask_b32_e32 v96, v96, v97, vcc
	v_sqrt_f32_e32 v97, v96
	s_cselect_b32 s4, 0x2000, 0
	v_add_u32_e32 v98, -1, v97
	v_fma_f32 v99, -v98, v97, v96
	v_cmp_ge_f32_e64 s[36:37], 0, v99
	v_add_u32_e32 v99, 1, v97
	s_nop 0
	v_cndmask_b32_e64 v98, v97, v98, s[36:37]
	v_fma_f32 v97, -v99, v97, v96
	v_cmp_lt_f32_e64 s[36:37], 0, v97
	s_nop 1
	v_cndmask_b32_e64 v97, v98, v99, s[36:37]
	v_mul_f32_e32 v98, 0x37800000, v97
	v_cndmask_b32_e32 v97, v97, v98, vcc
	v_cmp_class_f32_e32 vcc, v96, v213
	s_nop 1
	v_cndmask_b32_e32 v96, v97, v96, vcc
	v_div_scale_f32 v97, s[12:13], v96, v96, 1.0
	v_rcp_f32_e32 v98, v97
	s_nop 0
	v_fma_f32 v99, -v97, v98, 1.0
	v_fmac_f32_e32 v98, v99, v98
	v_div_scale_f32 v99, vcc, 1.0, v96, 1.0
	v_mul_f32_e32 v100, v99, v98
	v_fma_f32 v101, -v97, v100, v99
	v_fmac_f32_e32 v100, v101, v98
	v_fma_f32 v97, -v97, v100, v99
	v_div_fmas_f32 v97, v97, v98, v100
	v_div_fixup_f32 v98, v97, v96, 1.0
	v_pk_mul_f32 v[108:109], v[92:93], v[98:99] op_sel_hi:[1,0]
	v_add_u32_e32 v92, s4, v224
	ds_read_b128 v[100:103], v92
	ds_read_b128 v[104:107], v92 offset:16384
	v_pk_mul_f32 v[94:95], v[94:95], v[98:99] op_sel_hi:[1,0]
	v_lshl_add_u64 v[96:97], v[134:135], 0, s[10:11]
	s_waitcnt lgkmcnt(0)
	v_pk_fma_f32 v[100:101], v[108:109], v[100:101], v[104:105]
	s_nop 0
	v_bfe_u32 v99, v100, 16, 1
	v_bfe_u32 v93, v101, 16, 1
	v_add3_u32 v99, v100, v99, s33
	v_pk_fma_f32 v[94:95], v[94:95], v[102:103], v[106:107]
	v_add3_u32 v93, v101, v93, s33
	v_lshrrev_b32_e32 v99, 16, v99
	v_and_or_b32 v100, v93, s96, v99
	v_bfe_u32 v93, v95, 16, 1
	v_add3_u32 v93, v95, v93, s33
	v_bfe_u32 v95, v94, 16, 1
	v_add3_u32 v94, v94, v95, s33
	v_lshrrev_b32_e32 v94, 16, v94
	v_and_or_b32 v101, v93, s96, v94
	global_store_dwordx2 v[96:97], v[100:101], off sc1
	v_pk_mul_f32 v[94:95], v[88:89], v[98:99] op_sel_hi:[1,0]
	v_pk_mul_f32 v[104:105], v[90:91], v[98:99] op_sel_hi:[1,0]
	ds_read_b128 v[88:91], v92 offset:1024
	ds_read_b128 v[100:103], v92 offset:17408
	s_waitcnt lgkmcnt(0)
	v_pk_fma_f32 v[88:89], v[94:95], v[88:89], v[100:101]
	s_nop 0
	v_bfe_u32 v93, v89, 16, 1
	v_add3_u32 v89, v89, v93, s33
	v_bfe_u32 v93, v88, 16, 1
	v_add3_u32 v88, v88, v93, s33
	v_pk_fma_f32 v[90:91], v[104:105], v[90:91], v[102:103]
	v_lshrrev_b32_e32 v88, 16, v88
	v_and_or_b32 v88, v89, s96, v88
	v_bfe_u32 v89, v91, 16, 1
	v_add3_u32 v89, v91, v89, s33
	v_bfe_u32 v91, v90, 16, 1
	v_add3_u32 v90, v90, v91, s33
	v_lshrrev_b32_e32 v90, 16, v90
	v_and_or_b32 v89, v89, s96, v90
	global_store_dwordx2 v[96:97], v[88:89], off offset:512 sc1
	v_pk_mul_f32 v[94:95], v[84:85], v[98:99] op_sel_hi:[1,0]
	v_pk_mul_f32 v[100:101], v[86:87], v[98:99] op_sel_hi:[1,0]
	ds_read_b128 v[84:87], v92 offset:2048
	ds_read_b128 v[88:91], v92 offset:18432
	s_waitcnt lgkmcnt(0)
	v_pk_fma_f32 v[84:85], v[94:95], v[84:85], v[88:89]
	s_nop 0
	v_bfe_u32 v88, v85, 16, 1
	v_add3_u32 v85, v85, v88, s33
	v_bfe_u32 v88, v84, 16, 1
	v_add3_u32 v84, v84, v88, s33
	v_pk_fma_f32 v[86:87], v[100:101], v[86:87], v[90:91]
	v_lshrrev_b32_e32 v84, 16, v84
	v_and_or_b32 v84, v85, s96, v84
	v_bfe_u32 v85, v87, 16, 1
	v_add3_u32 v85, v87, v85, s33
	v_bfe_u32 v87, v86, 16, 1
	v_add3_u32 v86, v86, v87, s33
	v_lshrrev_b32_e32 v86, 16, v86
	v_and_or_b32 v85, v85, s96, v86
	global_store_dwordx2 v[96:97], v[84:85], off offset:1024 sc1
	v_pk_mul_f32 v[88:89], v[80:81], v[98:99] op_sel_hi:[1,0]
	v_pk_mul_f32 v[90:91], v[82:83], v[98:99] op_sel_hi:[1,0]
	ds_read_b128 v[80:83], v92 offset:3072
	ds_read_b128 v[84:87], v92 offset:19456
	s_waitcnt lgkmcnt(0)
	v_pk_fma_f32 v[80:81], v[88:89], v[80:81], v[84:85]
	s_nop 0
	v_bfe_u32 v84, v81, 16, 1
	v_add3_u32 v81, v81, v84, s33
	v_bfe_u32 v84, v80, 16, 1
	v_add3_u32 v80, v80, v84, s33
	v_pk_fma_f32 v[82:83], v[90:91], v[82:83], v[86:87]
	v_lshrrev_b32_e32 v80, 16, v80
	v_and_or_b32 v80, v81, s96, v80
	v_bfe_u32 v81, v83, 16, 1
	v_add3_u32 v81, v83, v81, s33
	v_bfe_u32 v83, v82, 16, 1
	v_add3_u32 v82, v82, v83, s33
	v_lshrrev_b32_e32 v82, 16, v82
	v_and_or_b32 v81, v81, s96, v82
	global_store_dwordx2 v[96:97], v[80:81], off offset:1536 sc1
	v_pk_mul_f32 v[84:85], v[76:77], v[98:99] op_sel_hi:[1,0]
	v_pk_mul_f32 v[86:87], v[78:79], v[98:99] op_sel_hi:[1,0]
	ds_read_b128 v[76:79], v92 offset:4096
	ds_read_b128 v[80:83], v92 offset:20480
	s_waitcnt lgkmcnt(0)
	v_pk_fma_f32 v[76:77], v[84:85], v[76:77], v[80:81]
	s_nop 0
	v_bfe_u32 v80, v77, 16, 1
	v_add3_u32 v77, v77, v80, s33
	v_bfe_u32 v80, v76, 16, 1
	v_add3_u32 v76, v76, v80, s33
	v_pk_fma_f32 v[78:79], v[86:87], v[78:79], v[82:83]
	v_lshrrev_b32_e32 v76, 16, v76
	v_and_or_b32 v76, v77, s96, v76
	v_bfe_u32 v77, v79, 16, 1
	v_add3_u32 v77, v79, v77, s33
	v_bfe_u32 v79, v78, 16, 1
	v_add3_u32 v78, v78, v79, s33
	v_lshrrev_b32_e32 v78, 16, v78
	v_and_or_b32 v77, v77, s96, v78
	global_store_dwordx2 v[96:97], v[76:77], off offset:2048 sc1
	v_pk_mul_f32 v[80:81], v[72:73], v[98:99] op_sel_hi:[1,0]
	v_pk_mul_f32 v[82:83], v[74:75], v[98:99] op_sel_hi:[1,0]
	ds_read_b128 v[72:75], v92 offset:5120
	ds_read_b128 v[76:79], v92 offset:21504
	s_waitcnt lgkmcnt(0)
	v_pk_fma_f32 v[72:73], v[80:81], v[72:73], v[76:77]
	s_nop 0
	v_bfe_u32 v76, v73, 16, 1
	v_add3_u32 v73, v73, v76, s33
	v_bfe_u32 v76, v72, 16, 1
	v_add3_u32 v72, v72, v76, s33
	v_pk_fma_f32 v[74:75], v[82:83], v[74:75], v[78:79]
	v_lshrrev_b32_e32 v72, 16, v72
	v_and_or_b32 v72, v73, s96, v72
	v_bfe_u32 v73, v75, 16, 1
	v_add3_u32 v73, v75, v73, s33
	v_bfe_u32 v75, v74, 16, 1
	v_add3_u32 v74, v74, v75, s33
	v_lshrrev_b32_e32 v74, 16, v74
	v_and_or_b32 v73, v73, s96, v74
	global_store_dwordx2 v[96:97], v[72:73], off offset:2560 sc1
	v_pk_mul_f32 v[76:77], v[68:69], v[98:99] op_sel_hi:[1,0]
	v_pk_mul_f32 v[78:79], v[70:71], v[98:99] op_sel_hi:[1,0]
	ds_read_b128 v[68:71], v92 offset:6144
	ds_read_b128 v[72:75], v92 offset:22528
	s_waitcnt lgkmcnt(0)
	v_pk_fma_f32 v[68:69], v[76:77], v[68:69], v[72:73]
	s_nop 0
	v_bfe_u32 v72, v69, 16, 1
	v_add3_u32 v69, v69, v72, s33
	v_bfe_u32 v72, v68, 16, 1
	v_add3_u32 v68, v68, v72, s33
	v_pk_fma_f32 v[70:71], v[78:79], v[70:71], v[74:75]
	v_lshrrev_b32_e32 v68, 16, v68
	v_and_or_b32 v68, v69, s96, v68
	v_bfe_u32 v69, v71, 16, 1
	v_add3_u32 v69, v71, v69, s33
	v_bfe_u32 v71, v70, 16, 1
	v_add3_u32 v70, v70, v71, s33
	v_lshrrev_b32_e32 v70, 16, v70
	v_and_or_b32 v69, v69, s96, v70
	global_store_dwordx2 v[96:97], v[68:69], off offset:3072 sc1
	v_pk_mul_f32 v[72:73], v[64:65], v[98:99] op_sel_hi:[1,0]
	v_pk_mul_f32 v[74:75], v[66:67], v[98:99] op_sel_hi:[1,0]
	ds_read_b128 v[64:67], v92 offset:7168
	ds_read_b128 v[68:71], v92 offset:23552
	s_waitcnt lgkmcnt(0)
	v_pk_fma_f32 v[64:65], v[72:73], v[64:65], v[68:69]
	s_nop 0
	v_bfe_u32 v68, v65, 16, 1
	v_add3_u32 v65, v65, v68, s33
	v_bfe_u32 v68, v64, 16, 1
	v_add3_u32 v64, v64, v68, s33
	v_pk_fma_f32 v[66:67], v[74:75], v[66:67], v[70:71]
	v_lshrrev_b32_e32 v64, 16, v64
	v_and_or_b32 v64, v65, s96, v64
	v_bfe_u32 v65, v67, 16, 1
	v_add3_u32 v65, v67, v65, s33
	v_bfe_u32 v67, v66, 16, 1
	v_add3_u32 v66, v66, v67, s33
	v_lshrrev_b32_e32 v66, 16, v66
	v_and_or_b32 v65, v65, s96, v66
	global_store_dwordx2 v[96:97], v[64:65], off offset:3584 sc1
.LBB0_1271:
	s_cmpk_gt_i32 s8, 0x3fff
	s_waitcnt vmcnt(15)
	v_lshlrev_b32_e32 v92, 16, v150
	v_and_b32_e32 v93, 0xffff0000, v150
	v_lshlrev_b32_e32 v94, 16, v151
	v_and_b32_e32 v95, 0xffff0000, v151
	s_waitcnt vmcnt(14)
	v_lshlrev_b32_e32 v88, 16, v146
	v_and_b32_e32 v89, 0xffff0000, v146
	v_lshlrev_b32_e32 v90, 16, v147
	v_and_b32_e32 v91, 0xffff0000, v147
	s_waitcnt vmcnt(13)
	v_lshlrev_b32_e32 v84, 16, v142
	v_and_b32_e32 v85, 0xffff0000, v142
	v_lshlrev_b32_e32 v86, 16, v143
	v_and_b32_e32 v87, 0xffff0000, v143
	s_waitcnt vmcnt(12)
	v_lshlrev_b32_e32 v80, 16, v138
	v_and_b32_e32 v81, 0xffff0000, v138
	v_lshlrev_b32_e32 v82, 16, v139
	v_and_b32_e32 v83, 0xffff0000, v139
	s_waitcnt vmcnt(11)
	v_lshlrev_b32_e32 v76, 16, v152
	v_and_b32_e32 v77, 0xffff0000, v152
	v_lshlrev_b32_e32 v78, 16, v153
	v_and_b32_e32 v79, 0xffff0000, v153
	s_waitcnt vmcnt(10)
	v_lshlrev_b32_e32 v72, 16, v148
	v_and_b32_e32 v73, 0xffff0000, v148
	v_lshlrev_b32_e32 v74, 16, v149
	v_and_b32_e32 v75, 0xffff0000, v149
	s_waitcnt vmcnt(9)
	v_lshlrev_b32_e32 v68, 16, v144
	v_and_b32_e32 v69, 0xffff0000, v144
	v_lshlrev_b32_e32 v70, 16, v145
	v_and_b32_e32 v71, 0xffff0000, v145
	s_waitcnt vmcnt(8)
	v_lshlrev_b32_e32 v64, 16, v140
	v_and_b32_e32 v65, 0xffff0000, v140
	v_lshlrev_b32_e32 v66, 16, v141
	v_and_b32_e32 v67, 0xffff0000, v141
	s_cselect_b64 s[10:11], -1, 0
	s_cmpk_lt_i32 s8, 0x4000
	v_cndmask_b32_e64 v170, 0, 1, s[6:7]
	s_cbranch_scc1 .LBB0_1274
	s_add_i32 s4, s8, 0xffffc000
	s_lshl_b64 s[8:9], s[4:5], 13
	v_lshl_add_u64 v[96:97], v[130:131], 0, s[8:9]
	v_add_co_u32_e32 v126, vcc, 0x200000, v96
	global_load_dwordx4 v[98:101], v[96:97], off
	s_nop 0
	v_addc_co_u32_e32 v127, vcc, 0, v97, vcc
	global_load_dwordx4 v[102:105], v[126:127], off
	global_load_dwordx4 v[106:109], v[96:97], off offset:1024
	global_load_dwordx4 v[110:113], v[126:127], off offset:1024
	global_load_dwordx4 v[114:117], v[96:97], off offset:2048
	global_load_dwordx4 v[118:121], v[126:127], off offset:2048
	global_load_dwordx4 v[122:125], v[96:97], off offset:3072
	global_load_dwordx4 v[138:141], v[126:127], off offset:3072
	v_add_co_u32_e32 v126, vcc, s26, v96
	s_mov_b32 s8, 0x201000
	s_nop 0
	v_addc_co_u32_e32 v127, vcc, 0, v97, vcc
	global_load_dwordx4 v[142:145], v[126:127], off
	v_add_co_u32_e32 v172, vcc, s8, v96
	s_mov_b32 s8, 0x401000
	s_nop 0
	v_addc_co_u32_e32 v173, vcc, 0, v97, vcc
	global_load_dwordx4 v[146:149], v[172:173], off
	global_load_dwordx4 v[150:153], v[126:127], off offset:1024
	global_load_dwordx4 v[154:157], v[172:173], off offset:1024
	global_load_dwordx4 v[158:161], v[126:127], off offset:2048
	global_load_dwordx4 v[162:165], v[172:173], off offset:2048
	global_load_dwordx4 v[166:169], v[126:127], off offset:3072
	s_nop 0
	global_load_dwordx4 v[172:175], v[172:173], off offset:3072
	s_waitcnt vmcnt(13)
	v_pk_add_f32 v[90:91], v[90:91], v[108:109]
	v_pk_add_f32 v[88:89], v[88:89], v[106:107]
	v_pk_add_f32 v[92:93], v[92:93], v[98:99]
	v_pk_add_f32 v[94:95], v[94:95], v[100:101]
	s_waitcnt vmcnt(9)
	v_pk_add_f32 v[80:81], v[80:81], v[122:123]
	v_pk_add_f32 v[86:87], v[86:87], v[116:117]
	s_waitcnt vmcnt(8)
	v_pk_add_f32 v[80:81], v[80:81], v[138:139]
	v_pk_add_f32 v[84:85], v[84:85], v[114:115]
	v_pk_add_f32 v[82:83], v[82:83], v[124:125]
	v_pk_add_f32 v[92:93], v[92:93], v[102:103]
	v_pk_add_f32 v[94:95], v[94:95], v[104:105]
	s_waitcnt vmcnt(7)
	v_pk_add_f32 v[78:79], v[78:79], v[144:145]
	v_pk_add_f32 v[98:99], v[76:77], v[142:143]
	s_waitcnt vmcnt(6)
	v_pk_add_f32 v[76:77], v[78:79], v[148:149]
	v_pk_add_f32 v[78:79], v[98:99], v[146:147]
	s_waitcnt vmcnt(5)
	v_pk_add_f32 v[74:75], v[74:75], v[152:153]
	v_pk_add_f32 v[98:99], v[72:73], v[150:151]
	s_waitcnt vmcnt(4)
	v_pk_add_f32 v[72:73], v[74:75], v[156:157]
	v_pk_add_f32 v[74:75], v[98:99], v[154:155]
	s_waitcnt vmcnt(3)
	v_pk_add_f32 v[70:71], v[70:71], v[160:161]
	v_pk_add_f32 v[98:99], v[68:69], v[158:159]
	s_waitcnt vmcnt(2)
	v_pk_add_f32 v[68:69], v[70:71], v[164:165]
	v_pk_add_f32 v[70:71], v[98:99], v[162:163]
	s_waitcnt vmcnt(1)
	v_pk_add_f32 v[66:67], v[66:67], v[168:169]
	v_pk_add_f32 v[98:99], v[64:65], v[166:167]
	s_waitcnt vmcnt(0)
	v_pk_add_f32 v[64:65], v[66:67], v[174:175]
	v_pk_add_f32 v[66:67], v[98:99], v[172:173]
	v_add_co_u32_e32 v98, vcc, s25, v96
	v_pk_add_f32 v[88:89], v[88:89], v[110:111]
	s_nop 0
	v_addc_co_u32_e32 v99, vcc, 0, v97, vcc
	v_add_co_u32_e32 v166, vcc, s8, v96
	s_mov_b32 s8, 0x601000
	s_nop 0
	v_addc_co_u32_e32 v167, vcc, 0, v97, vcc
	v_add_co_u32_e32 v138, vcc, s27, v96
	v_pk_add_f32 v[90:91], v[90:91], v[112:113]
	s_nop 0
	v_addc_co_u32_e32 v139, vcc, 0, v97, vcc
	v_add_co_u32_e32 v172, vcc, s8, v96
	v_pk_add_f32 v[84:85], v[84:85], v[118:119]
	s_nop 0
	v_addc_co_u32_e32 v173, vcc, 0, v97, vcc
	v_pk_add_f32 v[86:87], v[86:87], v[120:121]
	v_pk_add_f32 v[82:83], v[82:83], v[140:141]
	global_load_dwordx4 v[100:103], v[166:167], off offset:-4096
	global_load_dwordx4 v[104:107], v[172:173], off offset:-4096
	global_load_dwordx4 v[108:111], v[98:99], off offset:1024
	global_load_dwordx4 v[112:115], v[138:139], off offset:1024
	global_load_dwordx4 v[116:119], v[98:99], off offset:2048
	global_load_dwordx4 v[120:123], v[138:139], off offset:2048
	global_load_dwordx4 v[124:127], v[98:99], off offset:3072
	s_nop 0
	global_load_dwordx4 v[138:141], v[138:139], off offset:3072
	s_nop 0
	global_load_dwordx4 v[142:145], v[166:167], off
	global_load_dwordx4 v[146:149], v[172:173], off
	global_load_dwordx4 v[150:153], v[166:167], off offset:1024
	global_load_dwordx4 v[154:157], v[172:173], off offset:1024
	global_load_dwordx4 v[158:161], v[166:167], off offset:2048
	global_load_dwordx4 v[162:165], v[172:173], off offset:2048
	s_nop 0
	global_load_dwordx4 v[166:169], v[166:167], off offset:3072
	s_nop 0
	global_load_dwordx4 v[172:175], v[172:173], off offset:3072
	s_mov_b32 s8, 0x801000
	s_waitcnt vmcnt(13)
	v_pk_add_f32 v[88:89], v[88:89], v[108:109]
	s_waitcnt vmcnt(12)
	v_pk_add_f32 v[182:183], v[88:89], v[112:113]
	v_add_co_u32_e32 v88, vcc, s24, v96
	s_waitcnt vmcnt(11)
	v_pk_add_f32 v[86:87], v[86:87], v[118:119]
	v_addc_co_u32_e32 v89, vcc, 0, v97, vcc
	s_waitcnt vmcnt(10)
	v_pk_add_f32 v[194:195], v[86:87], v[122:123]
	v_add_co_u32_e32 v122, vcc, s8, v96
	s_waitcnt vmcnt(9)
	v_pk_add_f32 v[82:83], v[82:83], v[126:127]
	v_addc_co_u32_e32 v123, vcc, 0, v97, vcc
	s_waitcnt vmcnt(1)
	v_pk_add_f32 v[64:65], v[64:65], v[168:169]
	v_pk_add_f32 v[66:67], v[66:67], v[166:167]
	s_waitcnt vmcnt(0)
	v_pk_add_f32 v[202:203], v[64:65], v[174:175]
	v_pk_add_f32 v[204:205], v[66:67], v[172:173]
	global_load_dwordx4 v[64:67], v[122:123], off offset:-4096
	v_pk_add_f32 v[92:93], v[92:93], v[100:101]
	v_pk_add_f32 v[76:77], v[76:77], v[144:145]
	v_pk_add_f32 v[178:179], v[92:93], v[104:105]
	v_add_co_u32_e32 v92, vcc, s28, v96
	s_mov_b32 s8, 0xa01000
	s_nop 0
	v_addc_co_u32_e32 v93, vcc, 0, v97, vcc
	v_pk_add_f32 v[126:127], v[82:83], v[140:141]
	v_pk_add_f32 v[140:141], v[76:77], v[148:149]
	v_add_co_u32_e32 v148, vcc, s8, v96
	v_pk_add_f32 v[94:95], v[94:95], v[102:103]
	v_pk_add_f32 v[90:91], v[90:91], v[110:111]
	v_pk_add_f32 v[84:85], v[84:85], v[116:117]
	v_pk_add_f32 v[80:81], v[80:81], v[124:125]
	v_pk_add_f32 v[78:79], v[78:79], v[142:143]
	v_pk_add_f32 v[72:73], v[72:73], v[152:153]
	v_pk_add_f32 v[74:75], v[74:75], v[150:151]
	v_pk_add_f32 v[68:69], v[68:69], v[160:161]
	v_pk_add_f32 v[70:71], v[70:71], v[158:159]
	v_addc_co_u32_e32 v149, vcc, 0, v97, vcc
	v_pk_add_f32 v[176:177], v[94:95], v[106:107]
	v_pk_add_f32 v[180:181], v[90:91], v[114:115]
	v_pk_add_f32 v[196:197], v[84:85], v[120:121]
	v_pk_add_f32 v[138:139], v[80:81], v[138:139]
	v_pk_add_f32 v[142:143], v[78:79], v[146:147]
	v_pk_add_f32 v[144:145], v[72:73], v[156:157]
	v_pk_add_f32 v[146:147], v[74:75], v[154:155]
	v_pk_add_f32 v[198:199], v[68:69], v[164:165]
	v_pk_add_f32 v[200:201], v[70:71], v[162:163]
	global_load_dwordx4 v[68:71], v[148:149], off offset:-4096
	global_load_dwordx4 v[72:75], v[88:89], off offset:1024
	global_load_dwordx4 v[76:79], v[92:93], off offset:1024
	global_load_dwordx4 v[80:83], v[88:89], off offset:2048
	global_load_dwordx4 v[84:87], v[92:93], off offset:2048
	s_nop 0
	global_load_dwordx4 v[88:91], v[88:89], off offset:3072
	s_nop 0
	global_load_dwordx4 v[92:95], v[92:93], off offset:3072
	s_nop 0
	global_load_dwordx4 v[98:101], v[122:123], off
	global_load_dwordx4 v[102:105], v[148:149], off
	global_load_dwordx4 v[106:109], v[122:123], off offset:1024
	global_load_dwordx4 v[110:113], v[148:149], off offset:1024
	global_load_dwordx4 v[114:117], v[122:123], off offset:2048
	global_load_dwordx4 v[118:121], v[148:149], off offset:2048
	s_nop 0
	global_load_dwordx4 v[122:125], v[122:123], off offset:3072
	s_nop 0
	global_load_dwordx4 v[172:175], v[148:149], off offset:3072
	s_mov_b32 s8, 0xc01000
	s_waitcnt vmcnt(15)
	v_pk_add_f32 v[64:65], v[178:179], v[64:65]
	v_pk_add_f32 v[66:67], v[176:177], v[66:67]
	s_waitcnt vmcnt(14)
	v_pk_add_f32 v[168:169], v[64:65], v[68:69]
	s_waitcnt vmcnt(13)
	v_pk_add_f32 v[64:65], v[180:181], v[74:75]
	v_pk_add_f32 v[166:167], v[66:67], v[70:71]
	v_pk_add_f32 v[66:67], v[182:183], v[72:73]
	s_waitcnt vmcnt(12)
	v_pk_add_f32 v[162:163], v[64:65], v[78:79]
	s_waitcnt vmcnt(11)
	v_pk_add_f32 v[64:65], v[194:195], v[82:83]
	v_pk_add_f32 v[164:165], v[66:67], v[76:77]
	v_pk_add_f32 v[66:67], v[196:197], v[80:81]
	s_waitcnt vmcnt(10)
	v_pk_add_f32 v[158:159], v[64:65], v[86:87]
	s_waitcnt vmcnt(9)
	v_pk_add_f32 v[64:65], v[126:127], v[90:91]
	v_pk_add_f32 v[160:161], v[66:67], v[84:85]
	v_pk_add_f32 v[66:67], v[138:139], v[88:89]
	s_waitcnt vmcnt(8)
	v_pk_add_f32 v[154:155], v[64:65], v[94:95]
	s_waitcnt vmcnt(7)
	v_pk_add_f32 v[64:65], v[140:141], v[100:101]
	v_pk_add_f32 v[156:157], v[66:67], v[92:93]
	v_pk_add_f32 v[66:67], v[142:143], v[98:99]
	s_waitcnt vmcnt(6)
	v_pk_add_f32 v[150:151], v[64:65], v[104:105]
	s_waitcnt vmcnt(5)
	v_pk_add_f32 v[64:65], v[144:145], v[108:109]
	v_pk_add_f32 v[152:153], v[66:67], v[102:103]
	v_pk_add_f32 v[66:67], v[146:147], v[106:107]
	s_waitcnt vmcnt(4)
	v_pk_add_f32 v[146:147], v[64:65], v[112:113]
	s_waitcnt vmcnt(3)
	v_pk_add_f32 v[64:65], v[198:199], v[116:117]
	v_pk_add_f32 v[148:149], v[66:67], v[110:111]
	s_waitcnt vmcnt(2)
	v_pk_add_f32 v[142:143], v[64:65], v[120:121]
	s_waitcnt vmcnt(1)
	v_pk_add_f32 v[64:65], v[202:203], v[124:125]
	v_pk_add_f32 v[66:67], v[200:201], v[114:115]
	s_waitcnt vmcnt(0)
	v_pk_add_f32 v[138:139], v[64:65], v[174:175]
	v_add_co_u32_e32 v64, vcc, s29, v96
	v_pk_add_f32 v[144:145], v[66:67], v[118:119]
	v_pk_add_f32 v[66:67], v[204:205], v[122:123]
	v_addc_co_u32_e32 v65, vcc, 0, v97, vcc
	v_pk_add_f32 v[140:141], v[66:67], v[172:173]
	v_add_co_u32_e32 v66, vcc, s8, v96
	s_mov_b32 s8, 0xe01000
	s_nop 0
	v_addc_co_u32_e32 v67, vcc, 0, v97, vcc
	global_load_dwordx4 v[72:75], v[66:67], off offset:-4096
	v_add_co_u32_e32 v68, vcc, s31, v96
	s_waitcnt vmcnt(0)
	v_pk_add_f32 v[72:73], v[168:169], v[72:73]
	v_addc_co_u32_e32 v69, vcc, 0, v97, vcc
	v_add_co_u32_e32 v96, vcc, s8, v96
	v_pk_add_f32 v[74:75], v[166:167], v[74:75]
	s_nop 0
	v_addc_co_u32_e32 v97, vcc, 0, v97, vcc
	global_load_dwordx4 v[92:95], v[96:97], off offset:-4096
	global_load_dwordx4 v[84:87], v[64:65], off offset:1024
	global_load_dwordx4 v[88:91], v[68:69], off offset:1024
	global_load_dwordx4 v[120:123], v[64:65], off offset:2048
	global_load_dwordx4 v[124:127], v[68:69], off offset:2048
	global_load_dwordx4 v[80:83], v[64:65], off offset:3072
	global_load_dwordx4 v[116:119], v[68:69], off offset:3072
	global_load_dwordx4 v[76:79], v[66:67], off
	global_load_dwordx4 v[112:115], v[96:97], off
	global_load_dwordx4 v[104:107], v[66:67], off offset:1024
	global_load_dwordx4 v[108:111], v[96:97], off offset:1024
	s_nop 0
	global_load_dwordx4 v[68:71], v[66:67], off offset:2048
	global_load_dwordx4 v[100:103], v[96:97], off offset:2048
	s_nop 0
	global_load_dwordx4 v[64:67], v[66:67], off offset:3072
	s_nop 0
	global_load_dwordx4 v[96:99], v[96:97], off offset:3072
	s_andn2_b64 vcc, exec, s[6:7]
	s_waitcnt vmcnt(14)
	v_pk_add_f32 v[92:93], v[72:73], v[92:93]
	s_waitcnt vmcnt(13)
	v_pk_add_f32 v[72:73], v[162:163], v[86:87]
	v_pk_add_f32 v[94:95], v[74:75], v[94:95]
	v_pk_add_f32 v[74:75], v[164:165], v[84:85]
	s_waitcnt vmcnt(12)
	v_pk_add_f32 v[90:91], v[72:73], v[90:91]
	s_waitcnt vmcnt(11)
	v_pk_add_f32 v[72:73], v[158:159], v[122:123]
	v_pk_add_f32 v[88:89], v[74:75], v[88:89]
	v_pk_add_f32 v[74:75], v[160:161], v[120:121]
	s_waitcnt vmcnt(10)
	v_pk_add_f32 v[86:87], v[72:73], v[126:127]
	s_waitcnt vmcnt(9)
	v_pk_add_f32 v[72:73], v[154:155], v[82:83]
	v_pk_add_f32 v[84:85], v[74:75], v[124:125]
	v_pk_add_f32 v[74:75], v[156:157], v[80:81]
	s_waitcnt vmcnt(8)
	v_pk_add_f32 v[82:83], v[72:73], v[118:119]
	s_waitcnt vmcnt(7)
	v_pk_add_f32 v[72:73], v[150:151], v[78:79]
	v_pk_add_f32 v[80:81], v[74:75], v[116:117]
	v_pk_add_f32 v[74:75], v[152:153], v[76:77]
	s_waitcnt vmcnt(6)
	v_pk_add_f32 v[78:79], v[72:73], v[114:115]
	s_waitcnt vmcnt(5)
	v_pk_add_f32 v[72:73], v[146:147], v[106:107]
	v_pk_add_f32 v[104:105], v[148:149], v[104:105]
	s_waitcnt vmcnt(3)
	v_pk_add_f32 v[70:71], v[142:143], v[70:71]
	v_pk_add_f32 v[68:69], v[144:145], v[68:69]
	s_waitcnt vmcnt(1)
	v_pk_add_f32 v[66:67], v[138:139], v[66:67]
	v_pk_add_f32 v[64:65], v[140:141], v[64:65]
	v_pk_add_f32 v[76:77], v[74:75], v[112:113]
	v_pk_add_f32 v[74:75], v[72:73], v[110:111]
	v_pk_add_f32 v[72:73], v[104:105], v[108:109]
	v_pk_add_f32 v[70:71], v[70:71], v[102:103]
	v_pk_add_f32 v[68:69], v[68:69], v[100:101]
	s_waitcnt vmcnt(0)
	v_pk_add_f32 v[66:67], v[66:67], v[98:99]
	v_pk_add_f32 v[64:65], v[64:65], v[96:97]
	s_cbranch_vccnz .LBB0_1274
	s_lshl_b64 s[6:7], s[4:5], 11
	v_lshl_add_u64 v[96:97], s[6:7], 2, v[132:133]
	global_store_dwordx4 v[96:97], v[92:95], off sc1
	global_store_dwordx4 v[96:97], v[88:91], off offset:1024 sc1
	global_store_dwordx4 v[96:97], v[84:87], off offset:2048 sc1
	global_store_dwordx4 v[96:97], v[80:83], off offset:3072 sc1
	v_add_co_u32_e32 v96, vcc, 0x1000, v96
	s_nop 1
	v_addc_co_u32_e32 v97, vcc, 0, v97, vcc
	global_store_dwordx4 v[96:97], v[76:79], off sc1
	global_store_dwordx4 v[96:97], v[72:75], off offset:1024 sc1
	global_store_dwordx4 v[96:97], v[68:71], off offset:2048 sc1
	global_store_dwordx4 v[96:97], v[64:67], off offset:3072 sc1
.LBB0_1274:
	v_mul_f32_e32 v96, v93, v93
	v_mul_f32_e32 v97, v95, v95
	v_fmac_f32_e32 v96, v92, v92
	v_fmac_f32_e32 v97, v94, v94
	v_add_f32_e32 v96, v96, v97
	v_mul_f32_e32 v97, v89, v89
	v_mul_f32_e32 v98, v91, v91
	v_fmac_f32_e32 v97, v88, v88
	v_fmac_f32_e32 v98, v90, v90
	v_add_f32_e32 v97, v97, v98
	v_add_f32_e32 v96, v96, v97
	v_mul_f32_e32 v97, v85, v85
	v_mul_f32_e32 v98, v87, v87
	v_fmac_f32_e32 v97, v84, v84
	v_fmac_f32_e32 v98, v86, v86
	v_add_f32_e32 v97, v97, v98
	v_add_f32_e32 v96, v97, v96
	v_mul_f32_e32 v97, v81, v81
	v_mul_f32_e32 v98, v83, v83
	v_fmac_f32_e32 v97, v80, v80
	v_fmac_f32_e32 v98, v82, v82
	v_add_f32_e32 v97, v97, v98
	v_add_f32_e32 v96, v97, v96
	v_mul_f32_e32 v97, v77, v77
	v_mul_f32_e32 v98, v79, v79
	v_fmac_f32_e32 v97, v76, v76
	v_fmac_f32_e32 v98, v78, v78
	v_add_f32_e32 v97, v97, v98
	v_add_f32_e32 v96, v97, v96
	v_mul_f32_e32 v97, v73, v73
	v_mul_f32_e32 v98, v75, v75
	v_fmac_f32_e32 v97, v72, v72
	v_fmac_f32_e32 v98, v74, v74
	v_add_f32_e32 v97, v97, v98
	v_add_f32_e32 v96, v97, v96
	v_mul_f32_e32 v97, v69, v69
	v_mul_f32_e32 v98, v71, v71
	v_fmac_f32_e32 v97, v68, v68
	v_fmac_f32_e32 v98, v70, v70
	v_add_f32_e32 v97, v97, v98
	v_add_f32_e32 v96, v97, v96
	v_mul_f32_e32 v97, v65, v65
	v_mul_f32_e32 v98, v67, v67
	v_fmac_f32_e32 v97, v64, v64
	v_fmac_f32_e32 v98, v66, v66
	v_add_f32_e32 v97, v97, v98
	v_add_f32_e32 v96, v97, v96
	v_cmp_ne_u32_e32 vcc, 1, v170
	s_and_b64 vcc, exec, vcc
	v_add_f32_dpp v96, v96, v96 quad_perm:[1,0,3,2] row_mask:0xf bank_mask:0xf bound_ctrl:1
	s_nop 1
	v_add_f32_dpp v96, v96, v96 quad_perm:[2,3,0,1] row_mask:0xf bank_mask:0xf bound_ctrl:1
	s_nop 1
	v_add_f32_dpp v96, v96, v96 row_half_mirror row_mask:0xf bank_mask:0xf bound_ctrl:1
	s_nop 1
	v_add_f32_dpp v96, v96, v96 row_mirror row_mask:0xf bank_mask:0xf bound_ctrl:1
	ds_swizzle_b32 v97, v96 offset:swizzle(SWAP,16)
	s_waitcnt lgkmcnt(0)
	v_add_f32_e32 v96, v96, v97
	v_mov_b32_e32 v97, v96
	s_nop 1
	v_permlane32_swap_b32_e32 v96, v97
	s_cbranch_vccnz .LBB0_1259
	s_and_b64 s[6:7], s[10:11], exec
	v_add_f32_e32 v96, v96, v97
	v_fmamk_f32 v96, v96, 0x3a000000, v212
	s_mov_b32 s6, 0xf800000
	v_cmp_gt_f32_e32 vcc, s6, v96
	v_mul_f32_e32 v97, 0x4f800000, v96
	s_cselect_b32 s4, 0x2000, 0
	v_cndmask_b32_e32 v96, v96, v97, vcc
	v_sqrt_f32_e32 v97, v96
	s_nop 0
	v_add_u32_e32 v98, -1, v97
	v_fma_f32 v99, -v98, v97, v96
	v_cmp_ge_f32_e64 s[36:37], 0, v99
	v_add_u32_e32 v99, 1, v97
	s_nop 0
	v_cndmask_b32_e64 v98, v97, v98, s[36:37]
	v_fma_f32 v97, -v99, v97, v96
	v_cmp_lt_f32_e64 s[36:37], 0, v97
	s_nop 1
	v_cndmask_b32_e64 v97, v98, v99, s[36:37]
	v_mul_f32_e32 v98, 0x37800000, v97
	v_cndmask_b32_e32 v97, v97, v98, vcc
	v_cmp_class_f32_e32 vcc, v96, v213
	s_nop 1
	v_cndmask_b32_e32 v96, v97, v96, vcc
	v_div_scale_f32 v97, s[6:7], v96, v96, 1.0
	v_rcp_f32_e32 v98, v97
	s_nop 0
	v_fma_f32 v99, -v97, v98, 1.0
	v_fmac_f32_e32 v98, v99, v98
	v_div_scale_f32 v99, vcc, 1.0, v96, 1.0
	v_mul_f32_e32 v100, v99, v98
	v_fma_f32 v101, -v97, v100, v99
	v_fmac_f32_e32 v100, v101, v98
	v_fma_f32 v97, -v97, v100, v99
	v_div_fmas_f32 v97, v97, v98, v100
	v_div_fixup_f32 v98, v97, v96, 1.0
	v_pk_mul_f32 v[108:109], v[92:93], v[98:99] op_sel_hi:[1,0]
	v_add_u32_e32 v92, s4, v224
	ds_read_b128 v[100:103], v92
	ds_read_b128 v[104:107], v92 offset:16384
	v_pk_mul_f32 v[94:95], v[94:95], v[98:99] op_sel_hi:[1,0]
	v_lshl_add_u64 v[96:97], v[134:135], 0, s[0:1]
	s_waitcnt lgkmcnt(0)
	v_pk_fma_f32 v[100:101], v[108:109], v[100:101], v[104:105]
	s_nop 0
	v_bfe_u32 v99, v100, 16, 1
	v_bfe_u32 v93, v101, 16, 1
	v_add3_u32 v99, v100, v99, s33
	v_pk_fma_f32 v[94:95], v[94:95], v[102:103], v[106:107]
	v_add3_u32 v93, v101, v93, s33
	v_lshrrev_b32_e32 v99, 16, v99
	v_and_or_b32 v100, v93, s96, v99
	v_bfe_u32 v93, v95, 16, 1
	v_add3_u32 v93, v95, v93, s33
	v_bfe_u32 v95, v94, 16, 1
	v_add3_u32 v94, v94, v95, s33
	v_lshrrev_b32_e32 v94, 16, v94
	v_and_or_b32 v101, v93, s96, v94
	global_store_dwordx2 v[96:97], v[100:101], off sc1
	v_pk_mul_f32 v[94:95], v[88:89], v[98:99] op_sel_hi:[1,0]
	v_pk_mul_f32 v[104:105], v[90:91], v[98:99] op_sel_hi:[1,0]
	ds_read_b128 v[88:91], v92 offset:1024
	ds_read_b128 v[100:103], v92 offset:17408
	s_waitcnt lgkmcnt(0)
	v_pk_fma_f32 v[88:89], v[94:95], v[88:89], v[100:101]
	s_nop 0
	v_bfe_u32 v93, v89, 16, 1
	v_add3_u32 v89, v89, v93, s33
	v_bfe_u32 v93, v88, 16, 1
	v_add3_u32 v88, v88, v93, s33
	v_pk_fma_f32 v[90:91], v[104:105], v[90:91], v[102:103]
	v_lshrrev_b32_e32 v88, 16, v88
	v_and_or_b32 v88, v89, s96, v88
	v_bfe_u32 v89, v91, 16, 1
	v_add3_u32 v89, v91, v89, s33
	v_bfe_u32 v91, v90, 16, 1
	v_add3_u32 v90, v90, v91, s33
	v_lshrrev_b32_e32 v90, 16, v90
	v_and_or_b32 v89, v89, s96, v90
	global_store_dwordx2 v[96:97], v[88:89], off offset:512 sc1
	v_pk_mul_f32 v[94:95], v[84:85], v[98:99] op_sel_hi:[1,0]
	v_pk_mul_f32 v[100:101], v[86:87], v[98:99] op_sel_hi:[1,0]
	ds_read_b128 v[84:87], v92 offset:2048
	ds_read_b128 v[88:91], v92 offset:18432
	s_waitcnt lgkmcnt(0)
	v_pk_fma_f32 v[84:85], v[94:95], v[84:85], v[88:89]
	s_nop 0
	v_bfe_u32 v88, v85, 16, 1
	v_add3_u32 v85, v85, v88, s33
	v_bfe_u32 v88, v84, 16, 1
	v_add3_u32 v84, v84, v88, s33
	v_pk_fma_f32 v[86:87], v[100:101], v[86:87], v[90:91]
	v_lshrrev_b32_e32 v84, 16, v84
	v_and_or_b32 v84, v85, s96, v84
	v_bfe_u32 v85, v87, 16, 1
	v_add3_u32 v85, v87, v85, s33
	v_bfe_u32 v87, v86, 16, 1
	v_add3_u32 v86, v86, v87, s33
	v_lshrrev_b32_e32 v86, 16, v86
	v_and_or_b32 v85, v85, s96, v86
	global_store_dwordx2 v[96:97], v[84:85], off offset:1024 sc1
	v_pk_mul_f32 v[88:89], v[80:81], v[98:99] op_sel_hi:[1,0]
	v_pk_mul_f32 v[90:91], v[82:83], v[98:99] op_sel_hi:[1,0]
	ds_read_b128 v[80:83], v92 offset:3072
	ds_read_b128 v[84:87], v92 offset:19456
	s_waitcnt lgkmcnt(0)
	v_pk_fma_f32 v[80:81], v[88:89], v[80:81], v[84:85]
	s_nop 0
	v_bfe_u32 v84, v81, 16, 1
	v_add3_u32 v81, v81, v84, s33
	v_bfe_u32 v84, v80, 16, 1
	v_add3_u32 v80, v80, v84, s33
	v_pk_fma_f32 v[82:83], v[90:91], v[82:83], v[86:87]
	v_lshrrev_b32_e32 v80, 16, v80
	v_and_or_b32 v80, v81, s96, v80
	v_bfe_u32 v81, v83, 16, 1
	v_add3_u32 v81, v83, v81, s33
	v_bfe_u32 v83, v82, 16, 1
	v_add3_u32 v82, v82, v83, s33
	v_lshrrev_b32_e32 v82, 16, v82
	v_and_or_b32 v81, v81, s96, v82
	global_store_dwordx2 v[96:97], v[80:81], off offset:1536 sc1
	v_pk_mul_f32 v[84:85], v[76:77], v[98:99] op_sel_hi:[1,0]
	v_pk_mul_f32 v[86:87], v[78:79], v[98:99] op_sel_hi:[1,0]
	ds_read_b128 v[76:79], v92 offset:4096
	ds_read_b128 v[80:83], v92 offset:20480
	s_waitcnt lgkmcnt(0)
	v_pk_fma_f32 v[76:77], v[84:85], v[76:77], v[80:81]
	s_nop 0
	v_bfe_u32 v80, v77, 16, 1
	v_add3_u32 v77, v77, v80, s33
	v_bfe_u32 v80, v76, 16, 1
	v_add3_u32 v76, v76, v80, s33
	v_pk_fma_f32 v[78:79], v[86:87], v[78:79], v[82:83]
	v_lshrrev_b32_e32 v76, 16, v76
	v_and_or_b32 v76, v77, s96, v76
	v_bfe_u32 v77, v79, 16, 1
	v_add3_u32 v77, v79, v77, s33
	v_bfe_u32 v79, v78, 16, 1
	v_add3_u32 v78, v78, v79, s33
	v_lshrrev_b32_e32 v78, 16, v78
	v_and_or_b32 v77, v77, s96, v78
	global_store_dwordx2 v[96:97], v[76:77], off offset:2048 sc1
	v_pk_mul_f32 v[80:81], v[72:73], v[98:99] op_sel_hi:[1,0]
	v_pk_mul_f32 v[82:83], v[74:75], v[98:99] op_sel_hi:[1,0]
	ds_read_b128 v[72:75], v92 offset:5120
	ds_read_b128 v[76:79], v92 offset:21504
	s_waitcnt lgkmcnt(0)
	v_pk_fma_f32 v[72:73], v[80:81], v[72:73], v[76:77]
	s_nop 0
	v_bfe_u32 v76, v73, 16, 1
	v_add3_u32 v73, v73, v76, s33
	v_bfe_u32 v76, v72, 16, 1
	v_add3_u32 v72, v72, v76, s33
	v_pk_fma_f32 v[74:75], v[82:83], v[74:75], v[78:79]
	v_lshrrev_b32_e32 v72, 16, v72
	v_and_or_b32 v72, v73, s96, v72
	v_bfe_u32 v73, v75, 16, 1
	v_add3_u32 v73, v75, v73, s33
	v_bfe_u32 v75, v74, 16, 1
	v_add3_u32 v74, v74, v75, s33
	v_lshrrev_b32_e32 v74, 16, v74
	v_and_or_b32 v73, v73, s96, v74
	global_store_dwordx2 v[96:97], v[72:73], off offset:2560 sc1
	v_pk_mul_f32 v[76:77], v[68:69], v[98:99] op_sel_hi:[1,0]
	v_pk_mul_f32 v[78:79], v[70:71], v[98:99] op_sel_hi:[1,0]
	ds_read_b128 v[68:71], v92 offset:6144
	ds_read_b128 v[72:75], v92 offset:22528
	s_waitcnt lgkmcnt(0)
	v_pk_fma_f32 v[68:69], v[76:77], v[68:69], v[72:73]
	s_nop 0
	v_bfe_u32 v72, v69, 16, 1
	v_add3_u32 v69, v69, v72, s33
	v_bfe_u32 v72, v68, 16, 1
	v_add3_u32 v68, v68, v72, s33
	v_pk_fma_f32 v[70:71], v[78:79], v[70:71], v[74:75]
	v_lshrrev_b32_e32 v68, 16, v68
	v_and_or_b32 v68, v69, s96, v68
	v_bfe_u32 v69, v71, 16, 1
	v_add3_u32 v69, v71, v69, s33
	v_bfe_u32 v71, v70, 16, 1
	v_add3_u32 v70, v70, v71, s33
	v_lshrrev_b32_e32 v70, 16, v70
	v_and_or_b32 v69, v69, s96, v70
	global_store_dwordx2 v[96:97], v[68:69], off offset:3072 sc1
	v_pk_mul_f32 v[72:73], v[64:65], v[98:99] op_sel_hi:[1,0]
	v_pk_mul_f32 v[74:75], v[66:67], v[98:99] op_sel_hi:[1,0]
	ds_read_b128 v[64:67], v92 offset:7168
	ds_read_b128 v[68:71], v92 offset:23552
	s_waitcnt lgkmcnt(0)
	v_pk_fma_f32 v[64:65], v[72:73], v[64:65], v[68:69]
	s_nop 0
	v_bfe_u32 v68, v65, 16, 1
	v_add3_u32 v65, v65, v68, s33
	v_bfe_u32 v68, v64, 16, 1
	v_add3_u32 v64, v64, v68, s33
	v_pk_fma_f32 v[66:67], v[74:75], v[66:67], v[70:71]
	v_lshrrev_b32_e32 v64, 16, v64
	v_and_or_b32 v64, v65, s96, v64
	v_bfe_u32 v65, v67, 16, 1
	v_add3_u32 v65, v67, v65, s33
	v_bfe_u32 v67, v66, 16, 1
	v_add3_u32 v66, v66, v67, s33
	v_lshrrev_b32_e32 v66, 16, v66
	v_and_or_b32 v65, v65, s96, v66
	global_store_dwordx2 v[96:97], v[64:65], off offset:3584 sc1
	s_branch .LBB0_1259

.LBB0_1339:
	s_add_i32 s16, s88, s4
	s_cmpk_lt_i32 s16, 0x4000
	s_cselect_b64 s[10:11], -1, 0
	s_and_b64 s[12:13], s[10:11], exec
	s_cselect_b32 s12, s16, s4
	s_add_u32 s14, s22, s8
	s_addc_u32 s15, s23, s9
	global_load_dwordx4 v[4:7], v185, s[14:15]
	s_ashr_i32 s13, s12, 31
	s_lshl_b64 s[14:15], s[12:13], 4
	v_readlane_b32 s18, v250, 0
	v_readlane_b32 s19, v250, 1
	s_add_u32 s14, s18, s14
	s_addc_u32 s15, s19, s15
	global_load_dwordx4 v[0:3], v185, s[14:15]
	s_lshl_b64 s[12:13], s[12:13], 12
	v_lshl_add_u64 v[34:35], v[20:21], 0, s[12:13]
	s_mov_b32 s12, 0x1b800000
	s_cmpk_gt_i32 s16, 0x3fff
	s_waitcnt vmcnt(1)
	v_lshlrev_b32_e32 v4, 2, v4
	v_add_u32_e32 v4, 0, v4
	ds_read_b32 v4, v4
	v_lshlrev_b32_e32 v6, 2, v6
	v_add_u32_e32 v6, 0, v6
	ds_read_b32 v6, v6
	s_waitcnt vmcnt(0)
	v_lshlrev_b32_e32 v0, 2, v0
	v_lshlrev_b32_e32 v2, 2, v2
	v_add_u32_e32 v0, 0, v0
	v_add_u32_e32 v2, 0, v2
	ds_read_b32 v0, v0
	ds_read_b32 v2, v2
	s_waitcnt lgkmcnt(3)
	v_add_u32_e32 v26, v4, v5
	v_lshl_add_u64 v[4:5], s[22:23], 0, v[24:25]
	v_add_co_u32_e32 v8, vcc, s12, v4
	s_waitcnt lgkmcnt(2)
	v_add_u32_e32 v28, v6, v7
	v_addc_co_u32_e32 v9, vcc, 0, v5, vcc
	global_load_dwordx4 v[40:43], v[8:9], off
	global_load_dwordx4 v[12:15], v[34:35], off
	global_load_dwordx4 v[16:19], v[8:9], off offset:1024
	global_load_dwordx4 v[4:7], v[8:9], off offset:2048
	s_nop 0
	global_load_dwordx4 v[8:11], v[8:9], off offset:3072
	v_ashrrev_i32_e32 v27, 31, v26
	v_ashrrev_i32_e32 v29, 31, v28
	v_lshlrev_b64 v[30:31], 12, v[26:27]
	v_lshlrev_b64 v[32:33], 12, v[28:29]
	v_lshl_add_u64 v[38:39], v[22:23], 0, v[30:31]
	v_lshl_add_u64 v[36:37], v[22:23], 0, v[32:33]
	s_mov_b64 s[12:13], -1
	s_waitcnt vmcnt(4)
	global_store_dwordx4 v[38:39], v[40:43], off sc1
	global_store_dwordx4 v[36:37], v[40:43], off sc1
	s_cbranch_scc0 .LBB0_1341
	s_waitcnt vmcnt(4)
	global_store_dwordx4 v[38:39], v[16:19], off offset:1024 sc1
	global_store_dwordx4 v[36:37], v[16:19], off offset:1024 sc1
	s_mov_b64 s[12:13], 0
.LBB0_1341:
	s_waitcnt lgkmcnt(1)
	v_add_u32_e32 v0, v0, v1
	s_waitcnt lgkmcnt(0)
	v_add_u32_e32 v2, v2, v3
	s_andn2_b64 vcc, exec, s[12:13]
	s_mov_b64 s[12:13], 0x800
	s_cbranch_vccnz .LBB0_1343
	global_load_dwordx4 v[40:43], v[34:35], off offset:1024
	global_load_dwordx4 v[44:47], v[34:35], off offset:2048
	global_load_dwordx4 v[48:51], v[34:35], off offset:3072
	v_ashrrev_i32_e32 v3, 31, v2
	v_ashrrev_i32_e32 v1, 31, v0
	s_waitcnt vmcnt(7)
	global_store_dwordx4 v[38:39], v[16:19], off offset:1024 sc1
	global_store_dwordx4 v[36:37], v[16:19], off offset:1024 sc1
	s_waitcnt vmcnt(8)
	global_store_dwordx4 v[38:39], v[4:7], off offset:2048 sc1
	global_store_dwordx4 v[36:37], v[4:7], off offset:2048 sc1
	v_lshlrev_b64 v[32:33], 12, v[2:3]
	v_lshlrev_b64 v[30:31], 12, v[0:1]
	s_waitcnt vmcnt(9)
	v_mov_b64_e32 v[4:5], v[8:9]
	v_mov_b64_e32 v[6:7], v[10:11]
	v_lshl_add_u64 v[8:9], v[22:23], 0, v[32:33]
	v_lshl_add_u64 v[10:11], v[22:23], 0, v[30:31]
	s_mov_b64 s[12:13], 0xc00
	global_store_dwordx4 v[10:11], v[12:15], off sc1
	global_store_dwordx4 v[8:9], v[12:15], off sc1
	s_waitcnt vmcnt(8)
	global_store_dwordx4 v[10:11], v[40:43], off offset:1024 sc1
	global_store_dwordx4 v[8:9], v[40:43], off offset:1024 sc1
	s_waitcnt vmcnt(9)
	global_store_dwordx4 v[10:11], v[44:47], off offset:2048 sc1
	global_store_dwordx4 v[8:9], v[44:47], off offset:2048 sc1
	s_waitcnt vmcnt(10)
	v_mov_b64_e32 v[8:9], v[48:49]
	v_mov_b64_e32 v[10:11], v[50:51]
.LBB0_1343:
	s_waitcnt vmcnt(4)
	v_lshl_add_u64 v[16:17], v[38:39], 0, s[12:13]
	s_waitcnt vmcnt(3)
	global_store_dwordx4 v[16:17], v[4:7], off sc1
	v_lshl_add_u64 v[16:17], v[36:37], 0, s[12:13]
	v_lshl_add_u64 v[12:13], v[22:23], 0, v[32:33]
	v_lshl_add_u64 v[14:15], v[22:23], 0, v[30:31]
	global_store_dwordx4 v[16:17], v[4:7], off sc1
	s_waitcnt vmcnt(4)
	global_store_dwordx4 v[14:15], v[8:11], off offset:3072 sc1
	global_store_dwordx4 v[12:13], v[8:11], off offset:3072 sc1
	s_and_saveexec_b64 s[12:13], s[38:39]
	s_cbranch_execz .LBB0_1338
	s_add_u32 s14, s22, s0
	v_mov_b32_e32 v27, v28
	s_addc_u32 s15, s23, s1
	s_andn2_b64 vcc, exec, s[10:11]
	global_store_dwordx2 v185, v[26:27], s[14:15] sc1
	s_cbranch_vccnz .LBB0_1338
	s_add_u32 s10, s22, s6
	v_mov_b32_e32 v1, v2
	s_addc_u32 s11, s23, s7
	global_store_dwordx2 v185, v[0:1], s[10:11] sc1
	s_branch .LBB0_1338

.LBB0_1422:
	v_mul_f32_e32 v145, 0xbfb8aa3b, v124
	v_exp_f32_e32 v145, v145
	v_lshl_or_b32 v150, s16, 7, v148
	v_readlane_b32 s16, v249, 62
	v_readlane_b32 s17, v249, 63
	v_add_f32_e32 v145, 1.0, v145
	v_rcp_f32_e32 v145, v145
	v_lshl_add_u32 v144, s18, 8, v146
	v_ashrrev_i32_e32 v151, 31, v150
	s_movk_i32 s9, 0x1600
	v_mul_f32_e32 v124, v124, v145
	v_mul_f32_e32 v120, v124, v120
	v_mul_f32_e32 v124, 0xbfb8aa3b, v125
	v_exp_f32_e32 v124, v124
	s_andn2_b64 vcc, exec, s[38:39]
	s_mov_b32 s48, 0x1600000
	v_add_f32_e32 v124, 1.0, v124
	v_rcp_f32_e32 v124, v124
	s_nop 0
	v_mul_f32_e32 v124, v125, v124
	v_mul_f32_e32 v121, v124, v121
	v_mul_f32_e32 v124, 0xbfb8aa3b, v126
	v_exp_f32_e32 v124, v124
	s_nop 0
	v_add_f32_e32 v124, 1.0, v124
	v_rcp_f32_e32 v124, v124
	s_nop 0
	v_mul_f32_e32 v124, v126, v124
	v_mul_f32_e32 v122, v124, v122
	v_mul_f32_e32 v124, 0xbfb8aa3b, v127
	v_exp_f32_e32 v124, v124
	s_nop 0
	v_add_f32_e32 v124, 1.0, v124
	v_rcp_f32_e32 v124, v124
	s_nop 0
	v_mul_f32_e32 v124, v127, v124
	v_mul_f32_e32 v123, v124, v123
	v_mul_f32_e32 v124, 0xbfb8aa3b, v116
	v_exp_f32_e32 v124, v124
	s_nop 0
	v_add_f32_e32 v124, 1.0, v124
	v_rcp_f32_e32 v124, v124
	s_nop 0
	v_mul_f32_e32 v116, v116, v124
	v_mul_f32_e32 v112, v116, v112
	v_mul_f32_e32 v116, 0xbfb8aa3b, v117
	v_exp_f32_e32 v116, v116
	s_nop 0
	v_add_f32_e32 v116, 1.0, v116
	v_rcp_f32_e32 v116, v116
	s_nop 0
	v_mul_f32_e32 v116, v117, v116
	v_mul_f32_e32 v113, v116, v113
	v_mul_f32_e32 v116, 0xbfb8aa3b, v118
	v_exp_f32_e32 v116, v116
	s_nop 0
	v_add_f32_e32 v116, 1.0, v116
	v_rcp_f32_e32 v116, v116
	s_nop 0
	v_mul_f32_e32 v116, v118, v116
	v_mul_f32_e32 v114, v116, v114
	v_mul_f32_e32 v116, 0xbfb8aa3b, v119
	v_exp_f32_e32 v116, v116
	s_nop 0
	v_add_f32_e32 v116, 1.0, v116
	v_rcp_f32_e32 v116, v116
	s_nop 0
	v_mul_f32_e32 v116, v119, v116
	v_mul_f32_e32 v115, v116, v115
	v_cvt_pk_bf16_f32 v116, v120, v121
	v_cvt_pk_bf16_f32 v117, v122, v123
	v_cvt_pk_bf16_f32 v118, v112, v113
	v_mov_b64_e32 v[112:113], s[16:17]
	v_cvt_pk_bf16_f32 v119, v114, v115
	v_mad_i64_i32 v[120:121], s[16:17], v144, s9, v[112:113]
	v_lshlrev_b64 v[114:115], 1, v[150:151]
	v_lshl_add_u64 v[120:121], v[120:121], 0, v[114:115]
	global_store_dwordx4 v[120:121], v[116:119], off sc1
	s_nop 1
	v_mul_f32_e32 v116, 0xbfb8aa3b, v108
	v_exp_f32_e32 v116, v116
	s_nop 0
	v_add_f32_e32 v116, 1.0, v116
	v_rcp_f32_e32 v116, v116
	s_nop 0
	v_mul_f32_e32 v108, v108, v116
	v_mul_f32_e32 v104, v108, v104
	v_mul_f32_e32 v108, 0xbfb8aa3b, v109
	v_exp_f32_e32 v108, v108
	s_nop 0
	v_add_f32_e32 v108, 1.0, v108
	v_rcp_f32_e32 v108, v108
	s_nop 0
	v_mul_f32_e32 v108, v109, v108
	v_mul_f32_e32 v105, v108, v105
	v_mul_f32_e32 v108, 0xbfb8aa3b, v110
	v_exp_f32_e32 v108, v108
	s_nop 0
	v_add_f32_e32 v108, 1.0, v108
	v_rcp_f32_e32 v108, v108
	s_nop 0
	v_mul_f32_e32 v108, v110, v108
	v_mul_f32_e32 v106, v108, v106
	v_mul_f32_e32 v108, 0xbfb8aa3b, v111
	v_exp_f32_e32 v108, v108
	s_nop 0
	v_add_f32_e32 v108, 1.0, v108
	v_rcp_f32_e32 v108, v108
	s_nop 0
	v_mul_f32_e32 v108, v111, v108
	v_mul_f32_e32 v107, v108, v107
	v_mul_f32_e32 v108, 0xbfb8aa3b, v100
	v_exp_f32_e32 v108, v108
	s_nop 0
	v_add_f32_e32 v108, 1.0, v108
	v_rcp_f32_e32 v108, v108
	s_nop 0
	v_mul_f32_e32 v100, v100, v108
	v_mul_f32_e32 v100, v100, v96
	v_mul_f32_e32 v96, 0xbfb8aa3b, v101
	v_exp_f32_e32 v96, v96
	s_nop 0
	v_add_f32_e32 v96, 1.0, v96
	v_rcp_f32_e32 v96, v96
	s_nop 0
	v_mul_f32_e32 v96, v101, v96
	v_mul_f32_e32 v101, v96, v97
	v_mul_f32_e32 v96, 0xbfb8aa3b, v102
	v_exp_f32_e32 v96, v96
	s_nop 0
	v_add_f32_e32 v96, 1.0, v96
	v_rcp_f32_e32 v96, v96
	s_nop 0
	v_mul_f32_e32 v96, v102, v96
	v_mul_f32_e32 v102, v96, v98
	v_mul_f32_e32 v96, 0xbfb8aa3b, v103
	v_exp_f32_e32 v96, v96
	s_nop 0
	v_add_f32_e32 v96, 1.0, v96
	v_rcp_f32_e32 v96, v96
	s_nop 0
	v_mul_f32_e32 v96, v103, v96
	v_mul_f32_e32 v99, v96, v99
	v_cvt_pk_bf16_f32 v96, v104, v105
	v_cvt_pk_bf16_f32 v97, v106, v107
	v_cvt_pk_bf16_f32 v98, v100, v101
	v_or_b32_e32 v100, 16, v144
	v_mad_i64_i32 v[100:101], s[16:17], v100, s9, v[112:113]
	v_lshl_add_u64 v[100:101], v[100:101], 0, v[114:115]
	v_cvt_pk_bf16_f32 v99, v102, v99
	global_store_dwordx4 v[100:101], v[96:99], off sc1
	s_nop 1
	v_mul_f32_e32 v96, 0xbfb8aa3b, v92
	v_exp_f32_e32 v96, v96
	s_nop 0
	v_add_f32_e32 v96, 1.0, v96
	v_rcp_f32_e32 v96, v96
	s_nop 0
	v_mul_f32_e32 v92, v92, v96
	v_mul_f32_e32 v88, v92, v88
	v_mul_f32_e32 v92, 0xbfb8aa3b, v93
	v_exp_f32_e32 v92, v92
	s_nop 0
	v_add_f32_e32 v92, 1.0, v92
	v_rcp_f32_e32 v92, v92
	s_nop 0
	v_mul_f32_e32 v92, v93, v92
	v_mul_f32_e32 v89, v92, v89
	v_mul_f32_e32 v92, 0xbfb8aa3b, v94
	v_exp_f32_e32 v92, v92
	s_nop 0
	v_add_f32_e32 v92, 1.0, v92
	v_rcp_f32_e32 v92, v92
	s_nop 0
	v_mul_f32_e32 v92, v94, v92
	v_mul_f32_e32 v90, v92, v90
	v_mul_f32_e32 v92, 0xbfb8aa3b, v95
	v_exp_f32_e32 v92, v92
	s_nop 0
	v_add_f32_e32 v92, 1.0, v92
	v_rcp_f32_e32 v92, v92
	s_nop 0
	v_mul_f32_e32 v92, v95, v92
	v_mul_f32_e32 v91, v92, v91
	v_mul_f32_e32 v92, 0xbfb8aa3b, v84
	v_exp_f32_e32 v92, v92
	s_nop 0
	v_add_f32_e32 v92, 1.0, v92
	v_rcp_f32_e32 v92, v92
	s_nop 0
	v_mul_f32_e32 v84, v84, v92
	v_mul_f32_e32 v84, v84, v80
	v_mul_f32_e32 v80, 0xbfb8aa3b, v85
	v_exp_f32_e32 v80, v80
	s_nop 0
	v_add_f32_e32 v80, 1.0, v80
	v_rcp_f32_e32 v80, v80
	s_nop 0
	v_mul_f32_e32 v80, v85, v80
	v_mul_f32_e32 v85, v80, v81
	v_mul_f32_e32 v80, 0xbfb8aa3b, v86
	v_exp_f32_e32 v80, v80
	s_nop 0
	v_add_f32_e32 v80, 1.0, v80
	v_rcp_f32_e32 v80, v80
	s_nop 0
	v_mul_f32_e32 v80, v86, v80
	v_mul_f32_e32 v86, v80, v82
	v_mul_f32_e32 v80, 0xbfb8aa3b, v87
	v_exp_f32_e32 v80, v80
	s_nop 0
	v_add_f32_e32 v80, 1.0, v80
	v_rcp_f32_e32 v80, v80
	s_nop 0
	v_mul_f32_e32 v80, v87, v80
	v_mul_f32_e32 v83, v80, v83
	v_cvt_pk_bf16_f32 v80, v88, v89
	v_cvt_pk_bf16_f32 v81, v90, v91
	v_cvt_pk_bf16_f32 v82, v84, v85
	v_or_b32_e32 v84, 32, v144
	v_mad_i64_i32 v[84:85], s[16:17], v84, s9, v[112:113]
	v_lshl_add_u64 v[84:85], v[84:85], 0, v[114:115]
	v_cvt_pk_bf16_f32 v83, v86, v83
	global_store_dwordx4 v[84:85], v[80:83], off sc1
	s_nop 1
	v_mul_f32_e32 v80, 0xbfb8aa3b, v76
	v_exp_f32_e32 v80, v80
	s_nop 0
	v_add_f32_e32 v80, 1.0, v80
	v_rcp_f32_e32 v80, v80
	s_nop 0
	v_mul_f32_e32 v76, v76, v80
	v_mul_f32_e32 v72, v76, v72
	v_mul_f32_e32 v76, 0xbfb8aa3b, v77
	v_exp_f32_e32 v76, v76
	s_nop 0
	v_add_f32_e32 v76, 1.0, v76
	v_rcp_f32_e32 v76, v76
	s_nop 0
	v_mul_f32_e32 v76, v77, v76
	v_mul_f32_e32 v73, v76, v73
	v_mul_f32_e32 v76, 0xbfb8aa3b, v78
	v_exp_f32_e32 v76, v76
	s_nop 0
	v_add_f32_e32 v76, 1.0, v76
	v_rcp_f32_e32 v76, v76
	s_nop 0
	v_mul_f32_e32 v76, v78, v76
	v_mul_f32_e32 v74, v76, v74
	v_mul_f32_e32 v76, 0xbfb8aa3b, v79
	v_exp_f32_e32 v76, v76
	s_nop 0
	v_add_f32_e32 v76, 1.0, v76
	v_rcp_f32_e32 v76, v76
	s_nop 0
	v_mul_f32_e32 v76, v79, v76
	v_mul_f32_e32 v75, v76, v75
	v_mul_f32_e32 v76, 0xbfb8aa3b, v68
	v_exp_f32_e32 v76, v76
	s_nop 0
	v_add_f32_e32 v76, 1.0, v76
	v_rcp_f32_e32 v76, v76
	s_nop 0
	v_mul_f32_e32 v68, v68, v76
	v_mul_f32_e32 v68, v68, v64
	v_mul_f32_e32 v64, 0xbfb8aa3b, v69
	v_exp_f32_e32 v64, v64
	s_nop 0
	v_add_f32_e32 v64, 1.0, v64
	v_rcp_f32_e32 v64, v64
	s_nop 0
	v_mul_f32_e32 v64, v69, v64
	v_mul_f32_e32 v69, v64, v65
	v_mul_f32_e32 v64, 0xbfb8aa3b, v70
	v_exp_f32_e32 v64, v64
	s_nop 0
	v_add_f32_e32 v64, 1.0, v64
	v_rcp_f32_e32 v64, v64
	s_nop 0
	v_mul_f32_e32 v64, v70, v64
	v_mul_f32_e32 v70, v64, v66
	v_mul_f32_e32 v64, 0xbfb8aa3b, v71
	v_exp_f32_e32 v64, v64
	s_nop 0
	v_add_f32_e32 v64, 1.0, v64
	v_rcp_f32_e32 v64, v64
	s_nop 0
	v_mul_f32_e32 v64, v71, v64
	v_mul_f32_e32 v67, v64, v67
	v_cvt_pk_bf16_f32 v64, v72, v73
	v_cvt_pk_bf16_f32 v65, v74, v75
	v_cvt_pk_bf16_f32 v66, v68, v69
	v_or_b32_e32 v68, 48, v144
	v_mad_i64_i32 v[68:69], s[16:17], v68, s9, v[112:113]
	v_lshl_add_u64 v[68:69], v[68:69], 0, v[114:115]
	v_cvt_pk_bf16_f32 v67, v70, v67
	global_store_dwordx4 v[68:69], v[64:67], off sc1
	s_nop 1
	v_mul_f32_e32 v65, 0xbfb8aa3b, v60
	v_exp_f32_e32 v65, v65
	v_add_u32_e32 v64, 0x80, v144
	v_add_f32_e32 v65, 1.0, v65
	v_rcp_f32_e32 v65, v65
	s_nop 0
	v_mul_f32_e32 v60, v60, v65
	v_mul_f32_e32 v56, v60, v56
	v_mul_f32_e32 v60, 0xbfb8aa3b, v61
	v_exp_f32_e32 v60, v60
	s_nop 0
	v_add_f32_e32 v60, 1.0, v60
	v_rcp_f32_e32 v60, v60
	s_nop 0
	v_mul_f32_e32 v60, v61, v60
	v_mul_f32_e32 v57, v60, v57
	v_mul_f32_e32 v60, 0xbfb8aa3b, v62
	v_exp_f32_e32 v60, v60
	s_nop 0
	v_add_f32_e32 v60, 1.0, v60
	v_rcp_f32_e32 v60, v60
	s_nop 0
	v_mul_f32_e32 v60, v62, v60
	v_mul_f32_e32 v58, v60, v58
	v_mul_f32_e32 v60, 0xbfb8aa3b, v63
	v_exp_f32_e32 v60, v60
	s_nop 0
	v_add_f32_e32 v60, 1.0, v60
	v_rcp_f32_e32 v60, v60
	s_nop 0
	v_mul_f32_e32 v60, v63, v60
	v_mul_f32_e32 v59, v60, v59
	v_mul_f32_e32 v60, 0xbfb8aa3b, v52
	v_exp_f32_e32 v60, v60
	s_nop 0
	v_add_f32_e32 v60, 1.0, v60
	v_rcp_f32_e32 v60, v60
	s_nop 0
	v_mul_f32_e32 v52, v52, v60
	v_mul_f32_e32 v52, v52, v48
	v_mul_f32_e32 v48, 0xbfb8aa3b, v53
	v_exp_f32_e32 v48, v48
	s_nop 0
	v_add_f32_e32 v48, 1.0, v48
	v_rcp_f32_e32 v48, v48
	s_nop 0
	v_mul_f32_e32 v48, v53, v48
	v_mul_f32_e32 v53, v48, v49
	v_mul_f32_e32 v48, 0xbfb8aa3b, v54
	v_exp_f32_e32 v48, v48
	s_nop 0
	v_add_f32_e32 v48, 1.0, v48
	v_rcp_f32_e32 v48, v48
	s_nop 0
	v_mul_f32_e32 v48, v54, v48
	v_mul_f32_e32 v54, v48, v50
	v_mul_f32_e32 v48, 0xbfb8aa3b, v55
	v_exp_f32_e32 v48, v48
	s_nop 0
	v_add_f32_e32 v48, 1.0, v48
	v_rcp_f32_e32 v48, v48
	s_nop 0
	v_mul_f32_e32 v48, v55, v48
	v_mul_f32_e32 v51, v48, v51
	v_cvt_pk_bf16_f32 v48, v56, v57
	v_cvt_pk_bf16_f32 v49, v58, v59
	v_cvt_pk_bf16_f32 v50, v52, v53
	v_mad_i64_i32 v[52:53], s[16:17], v64, s9, v[112:113]
	v_lshl_add_u64 v[52:53], v[52:53], 0, v[114:115]
	v_cvt_pk_bf16_f32 v51, v54, v51
	global_store_dwordx4 v[52:53], v[48:51], off sc1
	s_nop 1
	v_mul_f32_e32 v48, 0xbfb8aa3b, v44
	v_exp_f32_e32 v48, v48
	s_nop 0
	v_add_f32_e32 v48, 1.0, v48
	v_rcp_f32_e32 v48, v48
	s_nop 0
	v_mul_f32_e32 v44, v44, v48
	v_mul_f32_e32 v40, v44, v40
	v_mul_f32_e32 v44, 0xbfb8aa3b, v45
	v_exp_f32_e32 v44, v44
	s_nop 0
	v_add_f32_e32 v44, 1.0, v44
	v_rcp_f32_e32 v44, v44
	s_nop 0
	v_mul_f32_e32 v44, v45, v44
	v_mul_f32_e32 v41, v44, v41
	v_mul_f32_e32 v44, 0xbfb8aa3b, v46
	v_exp_f32_e32 v44, v44
	s_nop 0
	v_add_f32_e32 v44, 1.0, v44
	v_rcp_f32_e32 v44, v44
	s_nop 0
	v_mul_f32_e32 v44, v46, v44
	v_mul_f32_e32 v42, v44, v42
	v_mul_f32_e32 v44, 0xbfb8aa3b, v47
	v_exp_f32_e32 v44, v44
	s_nop 0
	v_add_f32_e32 v44, 1.0, v44
	v_rcp_f32_e32 v44, v44
	s_nop 0
	v_mul_f32_e32 v44, v47, v44
	v_mul_f32_e32 v43, v44, v43
	v_mul_f32_e32 v44, 0xbfb8aa3b, v36
	v_exp_f32_e32 v44, v44
	s_nop 0
	v_add_f32_e32 v44, 1.0, v44
	v_rcp_f32_e32 v44, v44
	s_nop 0
	v_mul_f32_e32 v36, v36, v44
	v_mul_f32_e32 v36, v36, v32
	v_mul_f32_e32 v32, 0xbfb8aa3b, v37
	v_exp_f32_e32 v32, v32
	s_nop 0
	v_add_f32_e32 v32, 1.0, v32
	v_rcp_f32_e32 v32, v32
	s_nop 0
	v_mul_f32_e32 v32, v37, v32
	v_mul_f32_e32 v37, v32, v33
	v_mul_f32_e32 v32, 0xbfb8aa3b, v38
	v_exp_f32_e32 v32, v32
	s_nop 0
	v_add_f32_e32 v32, 1.0, v32
	v_rcp_f32_e32 v32, v32
	s_nop 0
	v_mul_f32_e32 v32, v38, v32
	v_mul_f32_e32 v38, v32, v34
	v_mul_f32_e32 v32, 0xbfb8aa3b, v39
	v_exp_f32_e32 v32, v32
	s_nop 0
	v_add_f32_e32 v32, 1.0, v32
	v_rcp_f32_e32 v32, v32
	s_nop 0
	v_mul_f32_e32 v32, v39, v32
	v_mul_f32_e32 v35, v32, v35
	v_cvt_pk_bf16_f32 v32, v40, v41
	v_cvt_pk_bf16_f32 v33, v42, v43
	v_cvt_pk_bf16_f32 v34, v36, v37
	v_add_u32_e32 v36, 0x90, v144
	v_mad_i64_i32 v[36:37], s[16:17], v36, s9, v[112:113]
	v_lshl_add_u64 v[36:37], v[36:37], 0, v[114:115]
	v_cvt_pk_bf16_f32 v35, v38, v35
	global_store_dwordx4 v[36:37], v[32:35], off sc1
	s_nop 1
	v_mul_f32_e32 v32, 0xbfb8aa3b, v28
	v_exp_f32_e32 v32, v32
	s_nop 0
	v_add_f32_e32 v32, 1.0, v32
	v_rcp_f32_e32 v32, v32
	s_nop 0
	v_mul_f32_e32 v28, v28, v32
	v_mul_f32_e32 v24, v28, v24
	v_mul_f32_e32 v28, 0xbfb8aa3b, v29
	v_exp_f32_e32 v28, v28
	s_nop 0
	v_add_f32_e32 v28, 1.0, v28
	v_rcp_f32_e32 v28, v28
	s_nop 0
	v_mul_f32_e32 v28, v29, v28
	v_mul_f32_e32 v25, v28, v25
	v_mul_f32_e32 v28, 0xbfb8aa3b, v30
	v_exp_f32_e32 v28, v28
	s_nop 0
	v_add_f32_e32 v28, 1.0, v28
	v_rcp_f32_e32 v28, v28
	s_nop 0
	v_mul_f32_e32 v28, v30, v28
	v_mul_f32_e32 v26, v28, v26
	v_mul_f32_e32 v28, 0xbfb8aa3b, v31
	v_exp_f32_e32 v28, v28
	s_nop 0
	v_add_f32_e32 v28, 1.0, v28
	v_rcp_f32_e32 v28, v28
	s_nop 0
	v_mul_f32_e32 v28, v31, v28
	v_mul_f32_e32 v27, v28, v27
	v_mul_f32_e32 v28, 0xbfb8aa3b, v20
	v_exp_f32_e32 v28, v28
	s_nop 0
	v_add_f32_e32 v28, 1.0, v28
	v_rcp_f32_e32 v28, v28
	s_nop 0
	v_mul_f32_e32 v20, v20, v28
	v_mul_f32_e32 v20, v20, v16
	v_mul_f32_e32 v16, 0xbfb8aa3b, v21
	v_exp_f32_e32 v16, v16
	s_nop 0
	v_add_f32_e32 v16, 1.0, v16
	v_rcp_f32_e32 v16, v16
	s_nop 0
	v_mul_f32_e32 v16, v21, v16
	v_mul_f32_e32 v21, v16, v17
	v_mul_f32_e32 v16, 0xbfb8aa3b, v22
	v_exp_f32_e32 v16, v16
	s_nop 0
	v_add_f32_e32 v16, 1.0, v16
	v_rcp_f32_e32 v16, v16
	s_nop 0
	v_mul_f32_e32 v16, v22, v16
	v_mul_f32_e32 v22, v16, v18
	v_mul_f32_e32 v16, 0xbfb8aa3b, v23
	v_exp_f32_e32 v16, v16
	s_nop 0
	v_add_f32_e32 v16, 1.0, v16
	v_rcp_f32_e32 v16, v16
	s_nop 0
	v_mul_f32_e32 v16, v23, v16
	v_mul_f32_e32 v19, v16, v19
	v_cvt_pk_bf16_f32 v16, v24, v25
	v_cvt_pk_bf16_f32 v17, v26, v27
	v_cvt_pk_bf16_f32 v18, v20, v21
	v_add_u32_e32 v20, 0xa0, v144
	v_mad_i64_i32 v[20:21], s[16:17], v20, s9, v[112:113]
	v_lshl_add_u64 v[20:21], v[20:21], 0, v[114:115]
	v_cvt_pk_bf16_f32 v19, v22, v19
	global_store_dwordx4 v[20:21], v[16:19], off sc1
	s_nop 1
	v_mul_f32_e32 v16, 0xbfb8aa3b, v12
	v_exp_f32_e32 v16, v16
	s_nop 0
	v_add_f32_e32 v16, 1.0, v16
	v_rcp_f32_e32 v16, v16
	s_nop 0
	v_mul_f32_e32 v12, v12, v16
	v_mul_f32_e32 v8, v12, v8
	v_mul_f32_e32 v12, 0xbfb8aa3b, v13
	v_exp_f32_e32 v12, v12
	s_nop 0
	v_add_f32_e32 v12, 1.0, v12
	v_rcp_f32_e32 v12, v12
	s_nop 0
	v_mul_f32_e32 v12, v13, v12
	v_mul_f32_e32 v9, v12, v9
	v_mul_f32_e32 v12, 0xbfb8aa3b, v14
	v_exp_f32_e32 v12, v12
	s_nop 0
	v_add_f32_e32 v12, 1.0, v12
	v_rcp_f32_e32 v12, v12
	s_nop 0
	v_mul_f32_e32 v12, v14, v12
	v_mul_f32_e32 v10, v12, v10
	v_mul_f32_e32 v12, 0xbfb8aa3b, v15
	v_exp_f32_e32 v12, v12
	s_nop 0
	v_add_f32_e32 v12, 1.0, v12
	v_rcp_f32_e32 v12, v12
	s_nop 0
	v_mul_f32_e32 v12, v15, v12
	v_mul_f32_e32 v11, v12, v11
	v_mul_f32_e32 v12, 0xbfb8aa3b, v4
	v_exp_f32_e32 v12, v12
	s_nop 0
	v_add_f32_e32 v12, 1.0, v12
	v_rcp_f32_e32 v12, v12
	s_nop 0
	v_mul_f32_e32 v4, v4, v12
	v_mul_f32_e32 v4, v4, v0
	v_mul_f32_e32 v0, 0xbfb8aa3b, v5
	v_exp_f32_e32 v0, v0
	s_nop 0
	v_add_f32_e32 v0, 1.0, v0
	v_rcp_f32_e32 v0, v0
	s_nop 0
	v_mul_f32_e32 v0, v5, v0
	v_mul_f32_e32 v5, v0, v1
	v_mul_f32_e32 v0, 0xbfb8aa3b, v6
	v_exp_f32_e32 v0, v0
	s_nop 0
	v_add_f32_e32 v0, 1.0, v0
	v_rcp_f32_e32 v0, v0
	s_nop 0
	v_mul_f32_e32 v0, v6, v0
	v_mul_f32_e32 v6, v0, v2
	v_mul_f32_e32 v0, 0xbfb8aa3b, v7
	v_exp_f32_e32 v0, v0
	s_nop 0
	v_add_f32_e32 v0, 1.0, v0
	v_rcp_f32_e32 v0, v0
	s_nop 0
	v_mul_f32_e32 v0, v7, v0
	v_mul_f32_e32 v3, v0, v3
	v_cvt_pk_bf16_f32 v0, v8, v9
	v_cvt_pk_bf16_f32 v1, v10, v11
	v_cvt_pk_bf16_f32 v2, v4, v5
	v_add_u32_e32 v4, 0xb0, v144
	v_mad_i64_i32 v[4:5], s[16:17], v4, s9, v[112:113]
	v_lshl_add_u64 v[4:5], v[4:5], 0, v[114:115]
	s_mov_b64 s[16:17], -1
	v_cvt_pk_bf16_f32 v3, v6, v3
	global_store_dwordx4 v[4:5], v[0:3], off sc1
	s_cbranch_vccnz .LBB0_1411
	s_andn2_b64 vcc, exec, s[0:1]
	s_cbranch_vccnz .LBB0_1410
	s_barrier
	s_branch .LBB0_1410

.LBB0_1494:
	v_lshl_add_u32 v150, s52, 8, v146
	v_lshl_or_b32 v144, s50, 8, v148
	v_ashrrev_i32_e32 v151, 31, v150
	v_readlane_b32 s12, v253, 45
	v_ashrrev_i32_e32 v145, 31, v144
	v_lshlrev_b64 v[152:153], 12, v[150:151]
	v_readlane_b32 s13, v253, 46
	v_lshlrev_b64 v[154:155], 1, v[144:145]
	v_cvt_pk_bf16_f32 v124, v124, v125
	v_cvt_pk_bf16_f32 v125, v126, v127
	v_cvt_pk_bf16_f32 v126, v120, v121
	v_cvt_pk_bf16_f32 v127, v122, v123
	s_nop 0
	v_lshl_add_u64 v[152:153], s[12:13], 0, v[152:153]
	v_lshl_add_u64 v[144:145], v[152:153], 0, v[154:155]
	global_store_dwordx4 v[144:145], v[124:127], off sc1
	v_cvt_pk_bf16_f32 v112, v112, v113
	v_cvt_pk_bf16_f32 v113, v114, v115
	v_cvt_pk_bf16_f32 v114, v104, v105
	v_or_b32_e32 v104, 16, v150
	v_ashrrev_i32_e32 v105, 31, v104
	v_lshlrev_b64 v[104:105], 12, v[104:105]
	v_lshl_add_u64 v[104:105], s[12:13], 0, v[104:105]
	v_cvt_pk_bf16_f32 v115, v106, v107
	global_store_dwordx4 v[144:145], v[112:115], off offset:256 sc1
	s_nop 1
	v_lshl_add_u64 v[112:113], v[104:105], 0, v[154:155]
	v_cvt_pk_bf16_f32 v104, v116, v117
	v_cvt_pk_bf16_f32 v105, v118, v119
	v_cvt_pk_bf16_f32 v106, v108, v109
	v_cvt_pk_bf16_f32 v107, v110, v111
	global_store_dwordx4 v[112:113], v[104:107], off sc1
	v_cvt_pk_bf16_f32 v96, v96, v97
	v_cvt_pk_bf16_f32 v97, v98, v99
	v_cvt_pk_bf16_f32 v98, v88, v89
	v_or_b32_e32 v88, 32, v150
	v_ashrrev_i32_e32 v89, 31, v88
	v_lshlrev_b64 v[88:89], 12, v[88:89]
	v_lshl_add_u64 v[88:89], s[12:13], 0, v[88:89]
	v_cvt_pk_bf16_f32 v99, v90, v91
	global_store_dwordx4 v[112:113], v[96:99], off offset:256 sc1
	s_nop 1
	v_lshl_add_u64 v[96:97], v[88:89], 0, v[154:155]
	v_cvt_pk_bf16_f32 v88, v100, v101
	v_cvt_pk_bf16_f32 v89, v102, v103
	v_cvt_pk_bf16_f32 v90, v92, v93
	v_cvt_pk_bf16_f32 v91, v94, v95
	global_store_dwordx4 v[96:97], v[88:91], off sc1
	v_cvt_pk_bf16_f32 v84, v84, v85
	v_cvt_pk_bf16_f32 v85, v86, v87
	v_cvt_pk_bf16_f32 v86, v76, v77
	v_or_b32_e32 v76, 48, v150
	v_ashrrev_i32_e32 v77, 31, v76
	v_lshlrev_b64 v[76:77], 12, v[76:77]
	v_lshl_add_u64 v[76:77], s[12:13], 0, v[76:77]
	v_cvt_pk_bf16_f32 v87, v78, v79
	global_store_dwordx4 v[96:97], v[84:87], off offset:256 sc1
	s_mov_b32 s12, 0x80000
	s_nop 0
	v_lshl_add_u64 v[84:85], v[76:77], 0, v[154:155]
	v_cvt_pk_bf16_f32 v76, v80, v81
	v_cvt_pk_bf16_f32 v77, v82, v83
	v_cvt_pk_bf16_f32 v78, v72, v73
	v_cvt_pk_bf16_f32 v79, v74, v75
	global_store_dwordx4 v[84:85], v[76:79], off sc1
	v_cvt_pk_bf16_f32 v68, v68, v69
	v_cvt_pk_bf16_f32 v69, v70, v71
	v_cvt_pk_bf16_f32 v70, v64, v65
	v_cvt_pk_bf16_f32 v71, v66, v67
	global_store_dwordx4 v[84:85], v[68:71], off offset:256 sc1
	v_cvt_pk_bf16_f32 v60, v60, v61
	v_cvt_pk_bf16_f32 v61, v62, v63
	v_cvt_pk_bf16_f32 v62, v56, v57
	v_add_co_u32_e32 v56, vcc, s12, v144
	v_lshl_add_u64 v[64:65], v[144:145], 0, s[48:49]
	s_nop 0
	v_addc_co_u32_e32 v57, vcc, 0, v145, vcc
	v_cvt_pk_bf16_f32 v63, v58, v59
	global_store_dwordx4 v[56:57], v[60:63], off sc1
	v_cvt_pk_bf16_f32 v48, v48, v49
	v_cvt_pk_bf16_f32 v49, v50, v51
	s_mov_b64 s[12:13], 0x90000
	v_cvt_pk_bf16_f32 v50, v40, v41
	v_cvt_pk_bf16_f32 v51, v42, v43
	global_store_dwordx4 v[64:65], v[48:51], off offset:256 sc1
	v_cvt_pk_bf16_f32 v40, v52, v53
	v_cvt_pk_bf16_f32 v41, v54, v55
	v_cvt_pk_bf16_f32 v42, v44, v45
	v_cvt_pk_bf16_f32 v43, v46, v47
	s_nop 1
	v_lshl_add_u64 v[48:49], v[144:145], 0, s[12:13]
	s_mov_b32 s12, 0x90000
	v_add_co_u32_e32 v44, vcc, s12, v144
	s_mov_b64 s[12:13], 0xa0000
	s_nop 0
	v_addc_co_u32_e32 v45, vcc, 0, v145, vcc
	global_store_dwordx4 v[44:45], v[40:43], off sc1
	v_cvt_pk_bf16_f32 v32, v32, v33
	v_cvt_pk_bf16_f32 v33, v34, v35
	v_cvt_pk_bf16_f32 v34, v24, v25
	v_cvt_pk_bf16_f32 v35, v26, v27
	global_store_dwordx4 v[48:49], v[32:35], off offset:256 sc1
	v_cvt_pk_bf16_f32 v24, v36, v37
	v_cvt_pk_bf16_f32 v25, v38, v39
	v_cvt_pk_bf16_f32 v26, v28, v29
	v_cvt_pk_bf16_f32 v27, v30, v31
	s_nop 1
	v_lshl_add_u64 v[32:33], v[144:145], 0, s[12:13]
	s_mov_b32 s12, 0xa0000
	v_add_co_u32_e32 v28, vcc, s12, v144
	s_mov_b32 s12, 0xb0000
	s_nop 0
	v_addc_co_u32_e32 v29, vcc, 0, v145, vcc
	global_store_dwordx4 v[28:29], v[24:27], off sc1
	v_cvt_pk_bf16_f32 v16, v16, v17
	v_cvt_pk_bf16_f32 v17, v18, v19
	v_cvt_pk_bf16_f32 v18, v8, v9
	v_cvt_pk_bf16_f32 v19, v10, v11
	global_store_dwordx4 v[32:33], v[16:19], off offset:256 sc1
	v_cvt_pk_bf16_f32 v8, v20, v21
	v_cvt_pk_bf16_f32 v9, v22, v23
	v_cvt_pk_bf16_f32 v10, v12, v13
	v_add_co_u32_e32 v12, vcc, s12, v144
	s_nop 0
	v_lshl_add_u64 v[16:17], v[144:145], 0, s[14:15]
	v_addc_co_u32_e32 v13, vcc, 0, v145, vcc
	s_andn2_b64 vcc, exec, s[38:39]
	s_mov_b64 s[12:13], -1
	v_cvt_pk_bf16_f32 v11, v14, v15
	global_store_dwordx4 v[12:13], v[8:11], off sc1
	v_cvt_pk_bf16_f32 v4, v4, v5
	v_cvt_pk_bf16_f32 v5, v6, v7
	v_cvt_pk_bf16_f32 v6, v0, v1
	v_cvt_pk_bf16_f32 v7, v2, v3
	global_store_dwordx4 v[16:17], v[4:7], off offset:256 sc1
	s_cbranch_vccnz .LBB0_1487
	s_andn2_b64 vcc, exec, s[0:1]
	s_cbranch_vccnz .LBB0_1486
	s_barrier
	s_branch .LBB0_1486

.LBB0_1555:
	s_add_i32 s8, s88, s4
	s_cmpk_gt_i32 s8, 0x3fff
	s_cselect_b64 s[6:7], -1, 0
	s_cmpk_lt_i32 s8, 0x4000
	s_cselect_b32 s8, s8, s4
	s_add_u32 s10, s22, s0
	s_addc_u32 s11, s23, s1
	s_ashr_i32 s9, s8, 31
	s_lshl_b64 s[12:13], s[8:9], 3
	v_mov_b32_e32 v0, 0x3a380000
	s_add_u32 s14, s18, s12
	global_load_dwordx2 v[0:1], v0, s[10:11]
	s_addc_u32 s15, s19, s13
	global_load_dwordx2 v[2:3], v185, s[14:15]
	global_load_dwordx2 v[126:127], v215, s[10:11]
	v_readlane_b32 s10, v250, 2
	s_add_u32 s10, s10, s12
	s_mov_b32 s12, 0x3ce00000
	v_readlane_b32 s11, v250, 3
	s_addc_u32 s11, s11, s13
	v_readlane_b32 s72, v249, 18
	v_readlane_b32 s84, v249, 30
	v_readlane_b32 s85, v249, 31
	v_readlane_b32 s86, v249, 32
	global_load_dwordx2 v[124:125], v185, s[10:11]
	v_readlane_b32 s87, v249, 33
	s_mov_b64 s[24:25], s[84:85]
	s_mov_b64 s[26:27], s[86:87]
	v_readlane_b32 s73, v249, 19
	v_readlane_b32 s74, v249, 20
	v_readlane_b32 s75, v249, 21
	v_readlane_b32 s76, v249, 22
	v_readlane_b32 s77, v249, 23
	v_readlane_b32 s78, v249, 24
	v_readlane_b32 s79, v249, 25
	v_readlane_b32 s80, v249, 26
	v_readlane_b32 s81, v249, 27
	v_readlane_b32 s82, v249, 28
	v_readlane_b32 s83, v249, 29
	s_waitcnt vmcnt(3)
	v_ashrrev_i32_e32 v7, 31, v1
	v_mov_b32_e32 v6, v1
	s_waitcnt vmcnt(2)
	v_ashrrev_i32_e32 v9, 31, v3
	v_mov_b32_e32 v8, v3
	v_ashrrev_i32_e32 v5, 31, v0
	v_mov_b32_e32 v4, v0
	v_lshlrev_b64 v[0:1], 12, v[6:7]
	v_ashrrev_i32_e32 v7, 31, v2
	v_mov_b32_e32 v6, v2
	v_lshlrev_b64 v[2:3], 12, v[8:9]
	v_lshl_add_u64 v[8:9], s[22:23], 0, v[112:113]
	v_lshlrev_b64 v[4:5], 12, v[4:5]
	v_add_co_u32_e32 v8, vcc, s12, v8
	v_lshl_add_u64 v[4:5], v[108:109], 0, v[4:5]
	s_nop 0
	v_addc_co_u32_e32 v9, vcc, 0, v9, vcc
	v_lshl_add_u64 v[0:1], v[108:109], 0, v[0:1]
	global_load_dwordx4 v[120:123], v[8:9], off nt
	global_load_dwordx4 v[134:137], v[4:5], off nt
	global_load_dwordx4 v[84:87], v[0:1], off nt
	s_lshl_b64 s[10:11], s[8:9], 12
	v_lshlrev_b64 v[6:7], 12, v[6:7]
	v_lshl_add_u64 v[10:11], v[110:111], 0, s[10:11]
	v_lshl_add_u64 v[6:7], v[108:109], 0, v[6:7]
	v_lshl_add_u64 v[2:3], v[108:109], 0, v[2:3]
	global_load_dwordx4 v[80:83], v[10:11], off nt
	global_load_dwordx4 v[76:79], v[6:7], off nt
	global_load_dwordx4 v[72:75], v[2:3], off nt
	global_load_dwordx4 v[48:51], v[8:9], off offset:1024 nt
	global_load_dwordx4 v[68:71], v[4:5], off offset:1024 nt
	global_load_dwordx4 v[64:67], v[0:1], off offset:1024 nt
	global_load_dwordx4 v[60:63], v[10:11], off offset:1024 nt
	global_load_dwordx4 v[56:59], v[6:7], off offset:1024 nt
	global_load_dwordx4 v[52:55], v[2:3], off offset:1024 nt
	global_load_dwordx4 v[44:47], v[8:9], off offset:2048 nt
	global_load_dwordx4 v[40:43], v[4:5], off offset:2048 nt
	global_load_dwordx4 v[36:39], v[0:1], off offset:2048 nt
	global_load_dwordx4 v[32:35], v[10:11], off offset:2048 nt
	global_load_dwordx4 v[28:31], v[6:7], off offset:2048 nt
	global_load_dwordx4 v[24:27], v[2:3], off offset:2048 nt
	global_load_dwordx4 v[20:23], v[8:9], off offset:3072 nt
	global_load_dwordx4 v[16:19], v[4:5], off offset:3072 nt
	global_load_dwordx4 v[12:15], v[0:1], off offset:3072 nt
	s_nop 0
	global_load_dwordx4 v[8:11], v[10:11], off offset:3072 nt
	s_nop 0
	global_load_dwordx4 v[4:7], v[6:7], off offset:3072 nt
	s_nop 0
	global_load_dwordx4 v[0:3], v[2:3], off offset:3072 nt
	s_nop 0
	global_load_dwordx4 v[138:141], v[90:91], off offset:16
	global_load_dwordx4 v[142:145], v[90:91], off
	s_mov_b32 s12, 0xf800000
	s_lshl_b64 s[8:9], s[8:9], 13
	s_add_u32 s8, s26, s8
	s_addc_u32 s9, s27, s9
	s_waitcnt vmcnt(25)
	v_lshlrev_b32_e32 v116, 16, v120
	v_and_b32_e32 v117, 0xffff0000, v120
	v_lshlrev_b32_e32 v118, 16, v121
	v_and_b32_e32 v119, 0xffff0000, v121
	s_waitcnt vmcnt(24)
	v_lshlrev_b32_e32 v120, 16, v134
	v_and_b32_e32 v121, 0xffff0000, v134
	v_lshlrev_b32_e32 v128, 16, v135
	v_and_b32_e32 v129, 0xffff0000, v135
	s_waitcnt vmcnt(23)
	v_lshlrev_b32_e32 v134, 16, v84
	v_and_b32_e32 v135, 0xffff0000, v84
	v_lshlrev_b32_e32 v84, 16, v85
	v_and_b32_e32 v85, 0xffff0000, v85
	v_pk_mul_f32 v[84:85], v[126:127], v[84:85] op_sel:[1,0]
	v_pk_mul_f32 v[134:135], v[126:127], v[134:135] op_sel:[1,0]
	v_pk_fma_f32 v[84:85], v[126:127], v[128:129], v[84:85] op_sel_hi:[0,1,1]
	v_pk_fma_f32 v[120:121], v[126:127], v[120:121], v[134:135] op_sel_hi:[0,1,1]
	s_waitcnt vmcnt(0)
	v_pk_fma_f32 v[118:119], v[84:85], v[144:145], v[118:119]
	v_pk_fma_f32 v[120:121], v[120:121], v[142:143], v[116:117]
	v_mul_f32_e32 v85, v119, v119
	v_mul_f32_e32 v84, v121, v121
	v_fmac_f32_e32 v84, v120, v120
	v_fmac_f32_e32 v85, v118, v118
	v_lshlrev_b32_e32 v128, 16, v72
	v_and_b32_e32 v129, 0xffff0000, v72
	v_lshlrev_b32_e32 v72, 16, v73
	v_and_b32_e32 v73, 0xffff0000, v73
	v_add_f32_e32 v133, v84, v85
	v_lshlrev_b32_e32 v84, 16, v76
	v_and_b32_e32 v85, 0xffff0000, v76
	v_lshlrev_b32_e32 v76, 16, v77
	v_and_b32_e32 v77, 0xffff0000, v77
	v_pk_mul_f32 v[72:73], v[124:125], v[72:73] op_sel:[1,0]
	v_pk_mul_f32 v[128:129], v[124:125], v[128:129] op_sel:[1,0]
	v_lshlrev_b32_e32 v116, 16, v80
	v_and_b32_e32 v117, 0xffff0000, v80
	v_lshlrev_b32_e32 v80, 16, v81
	v_and_b32_e32 v81, 0xffff0000, v81
	v_pk_fma_f32 v[128:129], v[124:125], v[84:85], v[128:129] op_sel_hi:[0,1,1]
	v_pk_fma_f32 v[72:73], v[124:125], v[76:77], v[72:73] op_sel_hi:[0,1,1]
	v_pk_fma_f32 v[84:85], v[72:73], v[144:145], v[80:81]
	v_pk_fma_f32 v[116:117], v[128:129], v[142:143], v[116:117]
	v_mul_f32_e32 v73, v85, v85
	v_mul_f32_e32 v72, v117, v117
	v_fmac_f32_e32 v72, v116, v116
	v_fmac_f32_e32 v73, v84, v84
	v_lshlrev_b32_e32 v128, 16, v86
	v_and_b32_e32 v129, 0xffff0000, v86
	v_lshlrev_b32_e32 v86, 16, v87
	v_and_b32_e32 v87, 0xffff0000, v87
	v_add_f32_e32 v134, v72, v73
	v_lshlrev_b32_e32 v72, 16, v122
	v_and_b32_e32 v73, 0xffff0000, v122
	v_lshlrev_b32_e32 v76, 16, v123
	v_and_b32_e32 v77, 0xffff0000, v123
	v_lshlrev_b32_e32 v80, 16, v136
	v_and_b32_e32 v81, 0xffff0000, v136
	v_lshlrev_b32_e32 v122, 16, v137
	v_and_b32_e32 v123, 0xffff0000, v137
	v_pk_mul_f32 v[86:87], v[126:127], v[86:87] op_sel:[1,0]
	v_pk_mul_f32 v[128:129], v[126:127], v[128:129] op_sel:[1,0]
	v_lshlrev_b32_e32 v136, 16, v68
	v_pk_fma_f32 v[128:129], v[126:127], v[80:81], v[128:129] op_sel_hi:[0,1,1]
	v_pk_fma_f32 v[80:81], v[126:127], v[122:123], v[86:87] op_sel_hi:[0,1,1]
	v_pk_fma_f32 v[80:81], v[80:81], v[140:141], v[76:77]
	v_pk_fma_f32 v[122:123], v[128:129], v[138:139], v[72:73]
	v_mul_f32_e32 v73, v81, v81
	v_mul_f32_e32 v72, v123, v123
	v_fmac_f32_e32 v72, v122, v122
	v_fmac_f32_e32 v73, v80, v80
	v_add_f32_e32 v72, v72, v73
	v_lshlrev_b32_e32 v86, 16, v74
	v_and_b32_e32 v87, 0xffff0000, v74
	v_lshlrev_b32_e32 v74, 16, v75
	v_and_b32_e32 v75, 0xffff0000, v75
	v_add_f32_e32 v133, v133, v72
	v_lshlrev_b32_e32 v72, 16, v82
	v_and_b32_e32 v73, 0xffff0000, v82
	v_lshlrev_b32_e32 v76, 16, v83
	v_and_b32_e32 v77, 0xffff0000, v83
	v_lshlrev_b32_e32 v82, 16, v78
	v_and_b32_e32 v83, 0xffff0000, v78
	v_lshlrev_b32_e32 v78, 16, v79
	v_and_b32_e32 v79, 0xffff0000, v79
	v_pk_mul_f32 v[74:75], v[124:125], v[74:75] op_sel:[1,0]
	v_pk_mul_f32 v[86:87], v[124:125], v[86:87] op_sel:[1,0]
	v_pk_fma_f32 v[74:75], v[124:125], v[78:79], v[74:75] op_sel_hi:[0,1,1]
	v_pk_fma_f32 v[86:87], v[124:125], v[82:83], v[86:87] op_sel_hi:[0,1,1]
	v_pk_fma_f32 v[82:83], v[74:75], v[140:141], v[76:77]
	v_pk_fma_f32 v[86:87], v[86:87], v[138:139], v[72:73]
	v_mul_f32_e32 v73, v83, v83
	v_mul_f32_e32 v72, v87, v87
	v_fmac_f32_e32 v72, v86, v86
	v_fmac_f32_e32 v73, v82, v82
	v_add_f32_e32 v72, v72, v73
	v_add_f32_e32 v134, v134, v72
	global_load_dwordx4 v[72:75], v[92:93], off offset:16
	global_load_dwordx4 v[76:79], v[92:93], off
	v_lshlrev_b32_e32 v138, 16, v64
	v_and_b32_e32 v139, 0xffff0000, v64
	v_lshlrev_b32_e32 v64, 16, v65
	v_and_b32_e32 v65, 0xffff0000, v65
	v_and_b32_e32 v137, 0xffff0000, v68
	v_lshlrev_b32_e32 v68, 16, v69
	v_and_b32_e32 v69, 0xffff0000, v69
	v_pk_mul_f32 v[64:65], v[126:127], v[64:65] op_sel:[1,0]
	v_pk_mul_f32 v[138:139], v[126:127], v[138:139] op_sel:[1,0]
	v_lshlrev_b32_e32 v128, 16, v48
	v_and_b32_e32 v129, 0xffff0000, v48
	v_lshlrev_b32_e32 v48, 16, v49
	v_and_b32_e32 v49, 0xffff0000, v49
	v_pk_fma_f32 v[136:137], v[126:127], v[136:137], v[138:139] op_sel_hi:[0,1,1]
	v_pk_fma_f32 v[64:65], v[126:127], v[68:69], v[64:65] op_sel_hi:[0,1,1]
	v_lshlrev_b32_e32 v68, 16, v56
	v_and_b32_e32 v69, 0xffff0000, v56
	v_lshlrev_b32_e32 v56, 16, v57
	v_and_b32_e32 v57, 0xffff0000, v57
	s_waitcnt vmcnt(0)
	v_pk_fma_f32 v[64:65], v[64:65], v[78:79], v[48:49]
	v_pk_fma_f32 v[128:129], v[136:137], v[76:77], v[128:129]
	v_mul_f32_e32 v49, v65, v65
	v_mul_f32_e32 v48, v129, v129
	v_fmac_f32_e32 v48, v128, v128
	v_fmac_f32_e32 v49, v64, v64
	v_lshlrev_b32_e32 v136, 16, v52
	v_and_b32_e32 v137, 0xffff0000, v52
	v_lshlrev_b32_e32 v52, 16, v53
	v_and_b32_e32 v53, 0xffff0000, v53
	v_add_f32_e32 v48, v48, v49
	v_pk_mul_f32 v[52:53], v[124:125], v[52:53] op_sel:[1,0]
	v_pk_mul_f32 v[136:137], v[124:125], v[136:137] op_sel:[1,0]
	v_add_f32_e32 v133, v133, v48
	v_lshlrev_b32_e32 v48, 16, v60
	v_and_b32_e32 v49, 0xffff0000, v60
	v_lshlrev_b32_e32 v60, 16, v61
	v_and_b32_e32 v61, 0xffff0000, v61
	v_pk_fma_f32 v[68:69], v[124:125], v[68:69], v[136:137] op_sel_hi:[0,1,1]
	v_pk_fma_f32 v[52:53], v[124:125], v[56:57], v[52:53] op_sel_hi:[0,1,1]
	v_pk_fma_f32 v[60:61], v[52:53], v[78:79], v[60:61]
	v_pk_fma_f32 v[68:69], v[68:69], v[76:77], v[48:49]
	v_mul_f32_e32 v49, v61, v61
	v_mul_f32_e32 v48, v69, v69
	v_fmac_f32_e32 v48, v68, v68
	v_fmac_f32_e32 v49, v60, v60
	v_lshlrev_b32_e32 v52, 16, v70
	v_and_b32_e32 v53, 0xffff0000, v70
	v_lshlrev_b32_e32 v56, 16, v71
	v_and_b32_e32 v57, 0xffff0000, v71
	v_lshlrev_b32_e32 v70, 16, v66
	v_and_b32_e32 v71, 0xffff0000, v66
	v_lshlrev_b32_e32 v66, 16, v67
	v_and_b32_e32 v67, 0xffff0000, v67
	v_add_f32_e32 v48, v48, v49
	v_pk_mul_f32 v[66:67], v[126:127], v[66:67] op_sel:[1,0]
	v_pk_mul_f32 v[70:71], v[126:127], v[70:71] op_sel:[1,0]
	v_add_f32_e32 v77, v134, v48
	v_lshlrev_b32_e32 v48, 16, v50
	v_and_b32_e32 v49, 0xffff0000, v50
	v_lshlrev_b32_e32 v50, 16, v51
	v_and_b32_e32 v51, 0xffff0000, v51
	v_pk_fma_f32 v[52:53], v[126:127], v[52:53], v[70:71] op_sel_hi:[0,1,1]
	v_pk_fma_f32 v[56:57], v[126:127], v[56:57], v[66:67] op_sel_hi:[0,1,1]
	v_pk_fma_f32 v[56:57], v[56:57], v[74:75], v[50:51]
	v_pk_fma_f32 v[66:67], v[52:53], v[72:73], v[48:49]
	v_mul_f32_e32 v49, v57, v57
	v_mul_f32_e32 v48, v67, v67
	v_fmac_f32_e32 v48, v66, v66
	v_fmac_f32_e32 v49, v56, v56
	v_add_f32_e32 v48, v48, v49
	v_add_f32_e32 v76, v133, v48
	v_lshlrev_b32_e32 v48, 16, v62
	v_and_b32_e32 v49, 0xffff0000, v62
	v_lshlrev_b32_e32 v50, 16, v63
	v_and_b32_e32 v51, 0xffff0000, v63
	v_lshlrev_b32_e32 v62, 16, v54
	v_and_b32_e32 v63, 0xffff0000, v54
	v_lshlrev_b32_e32 v54, 16, v55
	v_and_b32_e32 v55, 0xffff0000, v55
	v_lshlrev_b32_e32 v52, 16, v58
	v_and_b32_e32 v53, 0xffff0000, v58
	v_lshlrev_b32_e32 v58, 16, v59
	v_and_b32_e32 v59, 0xffff0000, v59
	v_pk_mul_f32 v[54:55], v[124:125], v[54:55] op_sel:[1,0]
	v_pk_mul_f32 v[62:63], v[124:125], v[62:63] op_sel:[1,0]
	v_pk_fma_f32 v[54:55], v[124:125], v[58:59], v[54:55] op_sel_hi:[0,1,1]
	v_pk_fma_f32 v[52:53], v[124:125], v[52:53], v[62:63] op_sel_hi:[0,1,1]
	v_pk_fma_f32 v[58:59], v[54:55], v[74:75], v[50:51]
	v_pk_fma_f32 v[62:63], v[52:53], v[72:73], v[48:49]
	v_mul_f32_e32 v49, v59, v59
	v_mul_f32_e32 v48, v63, v63
	v_fmac_f32_e32 v48, v62, v62
	v_fmac_f32_e32 v49, v58, v58
	v_add_f32_e32 v48, v48, v49
	v_add_f32_e32 v72, v77, v48
	global_load_dwordx4 v[48:51], v[94:95], off offset:16
	global_load_dwordx4 v[52:55], v[94:95], off
	v_lshlrev_b32_e32 v78, 16, v36
	v_and_b32_e32 v79, 0xffff0000, v36
	v_lshlrev_b32_e32 v36, 16, v37
	v_and_b32_e32 v37, 0xffff0000, v37
	v_lshlrev_b32_e32 v74, 16, v40
	v_and_b32_e32 v75, 0xffff0000, v40
	v_lshlrev_b32_e32 v40, 16, v41
	v_and_b32_e32 v41, 0xffff0000, v41
	v_pk_mul_f32 v[36:37], v[126:127], v[36:37] op_sel:[1,0]
	v_pk_mul_f32 v[78:79], v[126:127], v[78:79] op_sel:[1,0]
	v_lshlrev_b32_e32 v70, 16, v44
	v_and_b32_e32 v71, 0xffff0000, v44
	v_lshlrev_b32_e32 v44, 16, v45
	v_and_b32_e32 v45, 0xffff0000, v45
	v_pk_fma_f32 v[74:75], v[126:127], v[74:75], v[78:79] op_sel_hi:[0,1,1]
	v_pk_fma_f32 v[36:37], v[126:127], v[40:41], v[36:37] op_sel_hi:[0,1,1]
	v_lshlrev_b32_e32 v40, 16, v32
	v_and_b32_e32 v41, 0xffff0000, v32
	v_lshlrev_b32_e32 v32, 16, v33
	v_and_b32_e32 v33, 0xffff0000, v33
	s_waitcnt vmcnt(0)
	v_pk_fma_f32 v[44:45], v[36:37], v[54:55], v[44:45]
	v_pk_fma_f32 v[70:71], v[74:75], v[52:53], v[70:71]
	v_mul_f32_e32 v37, v45, v45
	v_mul_f32_e32 v36, v71, v71
	v_fmac_f32_e32 v36, v70, v70
	v_fmac_f32_e32 v37, v44, v44
	v_add_f32_e32 v36, v36, v37
	v_lshlrev_b32_e32 v74, 16, v24
	v_and_b32_e32 v75, 0xffff0000, v24
	v_lshlrev_b32_e32 v24, 16, v25
	v_and_b32_e32 v25, 0xffff0000, v25
	v_add_f32_e32 v73, v76, v36
	v_lshlrev_b32_e32 v36, 16, v28
	v_and_b32_e32 v37, 0xffff0000, v28
	v_lshlrev_b32_e32 v28, 16, v29
	v_and_b32_e32 v29, 0xffff0000, v29
	v_pk_mul_f32 v[24:25], v[124:125], v[24:25] op_sel:[1,0]
	v_pk_mul_f32 v[74:75], v[124:125], v[74:75] op_sel:[1,0]
	v_pk_fma_f32 v[24:25], v[124:125], v[28:29], v[24:25] op_sel_hi:[0,1,1]
	v_pk_fma_f32 v[74:75], v[124:125], v[36:37], v[74:75] op_sel_hi:[0,1,1]
	v_pk_fma_f32 v[36:37], v[24:25], v[54:55], v[32:33]
	v_pk_fma_f32 v[40:41], v[74:75], v[52:53], v[40:41]
	v_mul_f32_e32 v25, v37, v37
	v_mul_f32_e32 v24, v41, v41
	v_fmac_f32_e32 v24, v40, v40
	v_fmac_f32_e32 v25, v36, v36
	v_add_f32_e32 v24, v24, v25
	v_add_f32_e32 v52, v72, v24
	v_lshlrev_b32_e32 v24, 16, v46
	v_and_b32_e32 v25, 0xffff0000, v46
	v_lshlrev_b32_e32 v28, 16, v47
	v_and_b32_e32 v29, 0xffff0000, v47
	v_lshlrev_b32_e32 v46, 16, v38
	v_and_b32_e32 v47, 0xffff0000, v38
	v_lshlrev_b32_e32 v38, 16, v39
	v_and_b32_e32 v39, 0xffff0000, v39
	v_lshlrev_b32_e32 v32, 16, v42
	v_and_b32_e32 v33, 0xffff0000, v42
	v_lshlrev_b32_e32 v42, 16, v43
	v_and_b32_e32 v43, 0xffff0000, v43
	v_pk_mul_f32 v[38:39], v[126:127], v[38:39] op_sel:[1,0]
	v_pk_mul_f32 v[46:47], v[126:127], v[46:47] op_sel:[1,0]
	v_and_b32_e32 v53, 0xffff0000, v12
	v_pk_fma_f32 v[46:47], v[126:127], v[32:33], v[46:47] op_sel_hi:[0,1,1]
	v_pk_fma_f32 v[32:33], v[126:127], v[42:43], v[38:39] op_sel_hi:[0,1,1]
	v_pk_fma_f32 v[32:33], v[32:33], v[50:51], v[28:29]
	v_pk_fma_f32 v[42:43], v[46:47], v[48:49], v[24:25]
	v_mul_f32_e32 v25, v33, v33
	v_mul_f32_e32 v24, v43, v43
	v_fmac_f32_e32 v24, v42, v42
	v_fmac_f32_e32 v25, v32, v32
	v_add_f32_e32 v24, v24, v25
	v_lshlrev_b32_e32 v38, 16, v26
	v_and_b32_e32 v39, 0xffff0000, v26
	v_lshlrev_b32_e32 v26, 16, v27
	v_and_b32_e32 v27, 0xffff0000, v27
	v_add_f32_e32 v47, v73, v24
	v_lshlrev_b32_e32 v24, 16, v34
	v_and_b32_e32 v25, 0xffff0000, v34
	v_lshlrev_b32_e32 v28, 16, v35
	v_and_b32_e32 v29, 0xffff0000, v35
	v_lshlrev_b32_e32 v34, 16, v30
	v_and_b32_e32 v35, 0xffff0000, v30
	v_lshlrev_b32_e32 v30, 16, v31
	v_and_b32_e32 v31, 0xffff0000, v31
	v_pk_mul_f32 v[26:27], v[124:125], v[26:27] op_sel:[1,0]
	v_pk_mul_f32 v[38:39], v[124:125], v[38:39] op_sel:[1,0]
	v_pk_fma_f32 v[26:27], v[124:125], v[30:31], v[26:27] op_sel_hi:[0,1,1]
	v_pk_fma_f32 v[38:39], v[124:125], v[34:35], v[38:39] op_sel_hi:[0,1,1]
	v_pk_fma_f32 v[34:35], v[26:27], v[50:51], v[28:29]
	v_pk_fma_f32 v[38:39], v[38:39], v[48:49], v[24:25]
	v_mul_f32_e32 v25, v35, v35
	v_mul_f32_e32 v24, v39, v39
	v_fmac_f32_e32 v24, v38, v38
	v_fmac_f32_e32 v25, v34, v34
	v_add_f32_e32 v24, v24, v25
	v_add_f32_e32 v46, v52, v24
	global_load_dwordx4 v[24:27], v[96:97], off offset:16
	global_load_dwordx4 v[28:31], v[96:97], off
	v_lshlrev_b32_e32 v52, 16, v12
	v_lshlrev_b32_e32 v12, 16, v13
	v_and_b32_e32 v13, 0xffff0000, v13
	v_lshlrev_b32_e32 v50, 16, v16
	v_and_b32_e32 v51, 0xffff0000, v16
	v_lshlrev_b32_e32 v16, 16, v17
	v_and_b32_e32 v17, 0xffff0000, v17
	v_pk_mul_f32 v[12:13], v[126:127], v[12:13] op_sel:[1,0]
	v_pk_mul_f32 v[52:53], v[126:127], v[52:53] op_sel:[1,0]
	v_lshlrev_b32_e32 v48, 16, v20
	v_and_b32_e32 v49, 0xffff0000, v20
	v_lshlrev_b32_e32 v20, 16, v21
	v_and_b32_e32 v21, 0xffff0000, v21
	v_pk_fma_f32 v[50:51], v[126:127], v[50:51], v[52:53] op_sel_hi:[0,1,1]
	v_pk_fma_f32 v[12:13], v[126:127], v[16:17], v[12:13] op_sel_hi:[0,1,1]
	s_waitcnt vmcnt(0)
	v_pk_fma_f32 v[16:17], v[12:13], v[30:31], v[20:21]
	v_pk_fma_f32 v[20:21], v[50:51], v[28:29], v[48:49]
	v_mul_f32_e32 v13, v17, v17
	v_mul_f32_e32 v12, v21, v21
	v_fmac_f32_e32 v12, v20, v20
	v_fmac_f32_e32 v13, v16, v16
	v_lshlrev_b32_e32 v50, 16, v0
	v_and_b32_e32 v51, 0xffff0000, v0
	v_lshlrev_b32_e32 v0, 16, v1
	v_and_b32_e32 v1, 0xffff0000, v1
	v_add_f32_e32 v12, v12, v13
	v_lshlrev_b32_e32 v48, 16, v4
	v_and_b32_e32 v49, 0xffff0000, v4
	v_lshlrev_b32_e32 v4, 16, v5
	v_and_b32_e32 v5, 0xffff0000, v5
	v_pk_mul_f32 v[0:1], v[124:125], v[0:1] op_sel:[1,0]
	v_pk_mul_f32 v[50:51], v[124:125], v[50:51] op_sel:[1,0]
	v_add_f32_e32 v47, v47, v12
	v_lshlrev_b32_e32 v12, 16, v8
	v_and_b32_e32 v13, 0xffff0000, v8
	v_lshlrev_b32_e32 v8, 16, v9
	v_and_b32_e32 v9, 0xffff0000, v9
	v_pk_fma_f32 v[48:49], v[124:125], v[48:49], v[50:51] op_sel_hi:[0,1,1]
	v_pk_fma_f32 v[0:1], v[124:125], v[4:5], v[0:1] op_sel_hi:[0,1,1]
	v_pk_fma_f32 v[4:5], v[30:31], v[0:1], v[8:9]
	v_pk_fma_f32 v[12:13], v[28:29], v[48:49], v[12:13]
	v_mul_f32_e32 v1, v5, v5
	v_mul_f32_e32 v0, v13, v13
	v_fmac_f32_e32 v0, v12, v12
	v_fmac_f32_e32 v1, v4, v4
	v_add_f32_e32 v0, v0, v1
	v_lshlrev_b32_e32 v28, 16, v14
	v_and_b32_e32 v29, 0xffff0000, v14
	v_lshlrev_b32_e32 v14, 16, v15
	v_and_b32_e32 v15, 0xffff0000, v15
	v_add_f32_e32 v30, v46, v0
	v_lshlrev_b32_e32 v0, 16, v22
	v_and_b32_e32 v1, 0xffff0000, v22
	v_lshlrev_b32_e32 v8, 16, v23
	v_and_b32_e32 v9, 0xffff0000, v23
	v_lshlrev_b32_e32 v22, 16, v18
	v_and_b32_e32 v23, 0xffff0000, v18
	v_lshlrev_b32_e32 v18, 16, v19
	v_and_b32_e32 v19, 0xffff0000, v19
	v_pk_mul_f32 v[14:15], v[126:127], v[14:15] op_sel:[1,0]
	v_pk_mul_f32 v[28:29], v[126:127], v[28:29] op_sel:[1,0]
	v_pk_fma_f32 v[14:15], v[126:127], v[18:19], v[14:15] op_sel_hi:[0,1,1]
	v_pk_fma_f32 v[22:23], v[126:127], v[22:23], v[28:29] op_sel_hi:[0,1,1]
	v_pk_fma_f32 v[8:9], v[14:15], v[26:27], v[8:9]
	v_pk_fma_f32 v[14:15], v[22:23], v[24:25], v[0:1]
	v_mul_f32_e32 v1, v9, v9
	v_mul_f32_e32 v0, v15, v15
	v_fmac_f32_e32 v0, v14, v14
	v_fmac_f32_e32 v1, v8, v8
	v_lshlrev_b32_e32 v22, 16, v2
	v_and_b32_e32 v23, 0xffff0000, v2
	v_lshlrev_b32_e32 v2, 16, v3
	v_and_b32_e32 v3, 0xffff0000, v3
	v_add_f32_e32 v0, v0, v1
	v_lshlrev_b32_e32 v18, 16, v6
	v_and_b32_e32 v19, 0xffff0000, v6
	v_lshlrev_b32_e32 v6, 16, v7
	v_and_b32_e32 v7, 0xffff0000, v7
	v_pk_mul_f32 v[2:3], v[124:125], v[2:3] op_sel:[1,0]
	v_pk_mul_f32 v[22:23], v[124:125], v[22:23] op_sel:[1,0]
	v_add_f32_e32 v28, v47, v0
	v_lshlrev_b32_e32 v0, 16, v10
	v_and_b32_e32 v1, 0xffff0000, v10
	v_lshlrev_b32_e32 v10, 16, v11
	v_and_b32_e32 v11, 0xffff0000, v11
	v_pk_fma_f32 v[18:19], v[124:125], v[18:19], v[22:23] op_sel_hi:[0,1,1]
	v_pk_fma_f32 v[2:3], v[124:125], v[6:7], v[2:3] op_sel_hi:[0,1,1]
	v_pk_fma_f32 v[6:7], v[26:27], v[2:3], v[10:11]
	v_pk_fma_f32 v[10:11], v[24:25], v[18:19], v[0:1]
	v_mul_f32_e32 v1, v7, v7
	v_mul_f32_e32 v0, v11, v11
	v_fmac_f32_e32 v0, v10, v10
	v_fmac_f32_e32 v1, v6, v6
	v_add_f32_e32 v0, v0, v1
	v_add_f32_e32 v0, v0, v30
	v_add_f32_dpp v1, v28, v28 quad_perm:[1,0,3,2] row_mask:0xf bank_mask:0xf bound_ctrl:1
	s_nop 0
	v_add_f32_dpp v0, v0, v0 quad_perm:[1,0,3,2] row_mask:0xf bank_mask:0xf bound_ctrl:1
	v_add_f32_dpp v1, v1, v1 quad_perm:[2,3,0,1] row_mask:0xf bank_mask:0xf bound_ctrl:1
	s_nop 0
	v_add_f32_dpp v0, v0, v0 quad_perm:[2,3,0,1] row_mask:0xf bank_mask:0xf bound_ctrl:1
	v_add_f32_dpp v1, v1, v1 row_half_mirror row_mask:0xf bank_mask:0xf bound_ctrl:1
	s_nop 0
	v_add_f32_dpp v0, v0, v0 row_half_mirror row_mask:0xf bank_mask:0xf bound_ctrl:1
	v_add_f32_dpp v1, v1, v1 row_mirror row_mask:0xf bank_mask:0xf bound_ctrl:1
	ds_swizzle_b32 v2, v1 offset:swizzle(SWAP,16)
	v_add_f32_dpp v0, v0, v0 row_mirror row_mask:0xf bank_mask:0xf bound_ctrl:1
	s_waitcnt lgkmcnt(0)
	v_add_f32_e32 v1, v1, v2
	v_mov_b32_e32 v2, v1
	s_nop 1
	v_permlane32_swap_b32_e32 v1, v2
	v_add_f32_e32 v1, v1, v2
	v_fmamk_f32 v1, v1, 0x3a000000, v212
	v_cmp_gt_f32_e32 vcc, s12, v1
	v_mul_f32_e32 v2, 0x4f800000, v1
	s_nop 0
	v_cndmask_b32_e32 v1, v1, v2, vcc
	v_sqrt_f32_e32 v2, v1
	s_nop 0
	v_add_u32_e32 v3, -1, v2
	v_fma_f32 v18, -v3, v2, v1
	v_cmp_ge_f32_e64 s[40:41], 0, v18
	v_add_u32_e32 v18, 1, v2
	s_nop 0
	v_cndmask_b32_e64 v3, v2, v3, s[40:41]
	v_fma_f32 v2, -v18, v2, v1
	v_cmp_lt_f32_e64 s[40:41], 0, v2
	s_nop 1
	v_cndmask_b32_e64 v2, v3, v18, s[40:41]
	v_mul_f32_e32 v3, 0x37800000, v2
	v_cndmask_b32_e32 v2, v2, v3, vcc
	v_cmp_class_f32_e32 vcc, v1, v213
	s_nop 1
	v_cndmask_b32_e32 v1, v2, v1, vcc
	v_div_scale_f32 v2, s[10:11], v1, v1, 1.0
	v_rcp_f32_e32 v3, v2
	s_nop 0
	v_fma_f32 v18, -v2, v3, 1.0
	v_fmac_f32_e32 v3, v18, v3
	v_div_scale_f32 v18, vcc, 1.0, v1, 1.0
	v_mul_f32_e32 v19, v18, v3
	v_fma_f32 v22, -v2, v19, v18
	v_fmac_f32_e32 v19, v22, v3
	v_fma_f32 v2, -v2, v19, v18
	v_div_fmas_f32 v2, v2, v3, v19
	v_div_fixup_f32 v18, v2, v1, 1.0
	ds_swizzle_b32 v1, v0 offset:swizzle(SWAP,16)
	s_waitcnt lgkmcnt(0)
	v_add_f32_e32 v0, v0, v1
	v_mov_b32_e32 v1, v0
	s_nop 1
	v_permlane32_swap_b32_e32 v0, v1
	v_add_f32_e32 v0, v0, v1
	v_fmamk_f32 v0, v0, 0x3a000000, v212
	v_cmp_gt_f32_e32 vcc, s12, v0
	v_mul_f32_e32 v1, 0x4f800000, v0
	s_nop 0
	v_cndmask_b32_e32 v0, v0, v1, vcc
	v_sqrt_f32_e32 v1, v0
	s_nop 0
	v_add_u32_e32 v2, -1, v1
	v_fma_f32 v3, -v2, v1, v0
	v_cmp_ge_f32_e64 s[40:41], 0, v3
	v_add_u32_e32 v3, 1, v1
	s_nop 0
	v_cndmask_b32_e64 v2, v1, v2, s[40:41]
	v_fma_f32 v1, -v3, v1, v0
	v_cmp_lt_f32_e64 s[40:41], 0, v1
	s_nop 1
	v_cndmask_b32_e64 v1, v2, v3, s[40:41]
	v_mul_f32_e32 v2, 0x37800000, v1
	v_cndmask_b32_e32 v1, v1, v2, vcc
	v_cmp_class_f32_e32 vcc, v0, v213
	s_nop 1
	v_cndmask_b32_e32 v22, v1, v0, vcc
	v_div_scale_f32 v0, s[10:11], v22, v22, 1.0
	v_rcp_f32_e32 v1, v0
	s_mov_b64 s[10:11], -1
	v_fma_f32 v2, -v0, v1, 1.0
	v_fmac_f32_e32 v1, v2, v1
	v_div_scale_f32 v2, vcc, 1.0, v22, 1.0
	v_mul_f32_e32 v3, v2, v1
	v_fma_f32 v19, -v0, v3, v2
	v_fmac_f32_e32 v3, v19, v1
	v_fma_f32 v0, -v0, v3, v2
	v_div_fmas_f32 v23, v0, v1, v3
	global_load_dwordx4 v[0:3], v[98:99], off
	v_mov_b32_e32 v19, v18
	v_pk_mul_f32 v[24:25], v[118:119], v[18:19] op_sel_hi:[1,0]
	v_pk_mul_f32 v[26:27], v[120:121], v[18:19] op_sel_hi:[1,0]
	s_and_b64 vcc, exec, s[6:7]
	s_waitcnt vmcnt(0)
	v_pk_mul_f32 v[28:29], v[0:1], v[26:27]
	v_pk_mul_f32 v[24:25], v[2:3], v[24:25]
	s_nop 0
	v_cndmask_b32_e64 v27, v223, v25, s[38:39]
	v_cndmask_b32_e64 v26, v223, v24, s[38:39]
	v_cndmask_b32_e64 v25, v223, v29, s[38:39]
	v_cndmask_b32_e64 v24, v223, v28, s[38:39]
	global_store_dwordx4 v[114:115], v[24:27], off offset:-4096 sc1
	s_nop 1
	v_pk_mul_f32 v[24:25], v[122:123], v[18:19]
	s_cbranch_vccz .LBB0_1557
	global_load_dwordx4 v[26:29], v[98:99], off offset:16
	v_mov_b32_e32 v30, v18
	v_mov_b32_e32 v31, v18
	v_pk_mul_f32 v[30:31], v[80:81], v[30:31]
	s_mov_b64 s[10:11], 0
	s_waitcnt vmcnt(0)
	v_pk_mul_f32 v[28:29], v[30:31], v[28:29]
	v_pk_mul_f32 v[26:27], v[24:25], v[26:27]
	v_cndmask_b32_e64 v29, v223, v29, s[38:39]
	v_cndmask_b32_e64 v28, v223, v28, s[38:39]
	v_cndmask_b32_e64 v27, v223, v27, s[38:39]
	v_cndmask_b32_e64 v26, v223, v26, s[38:39]
	global_store_dwordx4 v[114:115], v[26:29], off offset:-4080 sc1
.LBB0_1557:
	v_div_fixup_f32 v22, v23, v22, 1.0
	v_mov_b32_e32 v23, v22
	s_andn2_b64 vcc, exec, s[10:11]
	v_lshlrev_b32_e32 v28, 2, v88
	s_cbranch_vccnz .LBB0_1559
	v_mov_b32_e32 v26, v22
	v_mov_b32_e32 v27, v22
	v_pk_mul_f32 v[30:31], v[84:85], v[26:27]
	v_pk_mul_f32 v[46:47], v[116:117], v[22:23]
	v_pk_mul_f32 v[2:3], v[2:3], v[30:31]
	v_pk_mul_f32 v[0:1], v[0:1], v[46:47]
	v_cndmask_b32_e64 v3, v223, v3, s[38:39]
	v_cndmask_b32_e64 v2, v223, v2, s[38:39]
	v_cndmask_b32_e64 v1, v223, v1, s[38:39]
	v_cndmask_b32_e64 v0, v223, v0, s[38:39]
	global_store_dwordx4 v28, v[0:3], s[8:9] sc1
	global_load_dwordx4 v[0:3], v[98:99], off offset:16
	v_mov_b32_e32 v30, v18
	v_mov_b32_e32 v31, v18
	v_pk_mul_f32 v[30:31], v[80:81], v[30:31]
	v_pk_mul_f32 v[46:47], v[86:87], v[22:23]
	v_pk_mul_f32 v[26:27], v[82:83], v[26:27]
	s_waitcnt vmcnt(0)
	v_pk_mul_f32 v[30:31], v[30:31], v[2:3]
	v_pk_mul_f32 v[24:25], v[24:25], v[0:1]
	v_pk_mul_f32 v[26:27], v[26:27], v[2:3]
	v_pk_mul_f32 v[46:47], v[46:47], v[0:1]
	v_cndmask_b32_e64 v3, v223, v31, s[38:39]
	v_cndmask_b32_e64 v2, v223, v30, s[38:39]
	v_cndmask_b32_e64 v1, v223, v25, s[38:39]
	v_cndmask_b32_e64 v0, v223, v24, s[38:39]
	v_cndmask_b32_e64 v27, v223, v27, s[38:39]
	v_cndmask_b32_e64 v26, v223, v26, s[38:39]
	v_cndmask_b32_e64 v25, v223, v47, s[38:39]
	v_cndmask_b32_e64 v24, v223, v46, s[38:39]
	global_store_dwordx4 v[114:115], v[0:3], off offset:-4080 sc1
	global_store_dwordx4 v28, v[24:27], s[8:9] offset:16 sc1
.LBB0_1559:
	global_load_dwordx4 v[0:3], v[98:99], off offset:2048
	s_nop 0
	v_mov_b32_e32 v26, v18
	v_mov_b32_e32 v27, v18
	v_pk_mul_f32 v[30:31], v[128:129], v[18:19]
	v_pk_mul_f32 v[46:47], v[64:65], v[26:27]
	s_mov_b64 s[10:11], -1
	s_and_b64 vcc, exec, s[6:7]
	v_pk_mul_f32 v[24:25], v[66:67], v[18:19]
	s_waitcnt vmcnt(0)
	v_pk_mul_f32 v[46:47], v[46:47], v[2:3]
	v_pk_mul_f32 v[30:31], v[30:31], v[0:1]
	v_cndmask_b32_e64 v49, v223, v47, s[38:39]
	v_cndmask_b32_e64 v48, v223, v46, s[38:39]
	v_cndmask_b32_e64 v47, v223, v31, s[38:39]
	v_cndmask_b32_e64 v46, v223, v30, s[38:39]
	global_store_dwordx4 v[114:115], v[46:49], off offset:-2048 sc1
	s_cbranch_vccz .LBB0_1561
	global_load_dwordx4 v[46:49], v[98:99], off offset:2064
	v_pk_mul_f32 v[26:27], v[56:57], v[26:27]
	s_mov_b64 s[10:11], 0
	s_waitcnt vmcnt(0)
	v_pk_mul_f32 v[26:27], v[26:27], v[48:49]
	v_pk_mul_f32 v[30:31], v[24:25], v[46:47]
	v_cndmask_b32_e64 v49, v223, v27, s[38:39]
	v_cndmask_b32_e64 v48, v223, v26, s[38:39]
	v_cndmask_b32_e64 v47, v223, v31, s[38:39]
	v_cndmask_b32_e64 v46, v223, v30, s[38:39]
	global_store_dwordx4 v[114:115], v[46:49], off offset:-2032 sc1
.LBB0_1561:
	s_andn2_b64 vcc, exec, s[10:11]
	s_cbranch_vccnz .LBB0_1563
	v_mov_b32_e32 v26, v22
	v_mov_b32_e32 v27, v22
	v_pk_mul_f32 v[30:31], v[60:61], v[26:27]
	v_pk_mul_f32 v[46:47], v[68:69], v[22:23]
	v_pk_mul_f32 v[2:3], v[30:31], v[2:3]
	v_pk_mul_f32 v[0:1], v[46:47], v[0:1]
	v_cndmask_b32_e64 v3, v223, v3, s[38:39]
	v_cndmask_b32_e64 v2, v223, v2, s[38:39]
	v_cndmask_b32_e64 v1, v223, v1, s[38:39]
	v_cndmask_b32_e64 v0, v223, v0, s[38:39]
	global_store_dwordx4 v28, v[0:3], s[8:9] offset:2048 sc1
	global_load_dwordx4 v[0:3], v[98:99], off offset:2064
	v_mov_b32_e32 v30, v18
	v_mov_b32_e32 v31, v18
	v_pk_mul_f32 v[30:31], v[56:57], v[30:31]
	v_pk_mul_f32 v[46:47], v[62:63], v[22:23]
	v_pk_mul_f32 v[26:27], v[58:59], v[26:27]
	s_waitcnt vmcnt(0)
	v_pk_mul_f32 v[30:31], v[30:31], v[2:3]
	v_pk_mul_f32 v[24:25], v[24:25], v[0:1]
	v_pk_mul_f32 v[26:27], v[26:27], v[2:3]
	v_pk_mul_f32 v[46:47], v[46:47], v[0:1]
	v_cndmask_b32_e64 v3, v223, v31, s[38:39]
	v_cndmask_b32_e64 v2, v223, v30, s[38:39]
	v_cndmask_b32_e64 v1, v223, v25, s[38:39]
	v_cndmask_b32_e64 v0, v223, v24, s[38:39]
	v_cndmask_b32_e64 v27, v223, v27, s[38:39]
	v_cndmask_b32_e64 v26, v223, v26, s[38:39]
	v_cndmask_b32_e64 v25, v223, v47, s[38:39]
	v_cndmask_b32_e64 v24, v223, v46, s[38:39]
	global_store_dwordx4 v[114:115], v[0:3], off offset:-2032 sc1
	global_store_dwordx4 v28, v[24:27], s[8:9] offset:2064 sc1
.LBB0_1563:
	global_load_dwordx4 v[0:3], v[100:101], off
	s_nop 0
	v_mov_b32_e32 v26, v18
	v_mov_b32_e32 v27, v18
	v_pk_mul_f32 v[28:29], v[70:71], v[18:19]
	v_pk_mul_f32 v[30:31], v[44:45], v[26:27]
	s_mov_b64 s[10:11], -1
	s_and_b64 vcc, exec, s[6:7]
	v_pk_mul_f32 v[24:25], v[42:43], v[18:19]
	s_waitcnt vmcnt(0)
	v_pk_mul_f32 v[30:31], v[30:31], v[2:3]
	v_pk_mul_f32 v[28:29], v[28:29], v[0:1]
	v_cndmask_b32_e64 v31, v223, v31, s[38:39]
	v_cndmask_b32_e64 v30, v223, v30, s[38:39]
	v_cndmask_b32_e64 v29, v223, v29, s[38:39]
	v_cndmask_b32_e64 v28, v223, v28, s[38:39]
	global_store_dwordx4 v[114:115], v[28:31], off sc1
	s_cbranch_vccz .LBB0_1565
	global_load_dwordx4 v[28:31], v[102:103], off
	v_pk_mul_f32 v[26:27], v[32:33], v[26:27]
	s_mov_b64 s[10:11], 0
	s_waitcnt vmcnt(0)
	v_pk_mul_f32 v[26:27], v[26:27], v[30:31]
	v_pk_mul_f32 v[30:31], v[24:25], v[28:29]
	v_cndmask_b32_e64 v29, v223, v27, s[38:39]
	v_cndmask_b32_e64 v28, v223, v26, s[38:39]
	v_cndmask_b32_e64 v27, v223, v31, s[38:39]
	v_cndmask_b32_e64 v26, v223, v30, s[38:39]
	global_store_dwordx4 v[114:115], v[26:29], off offset:16 sc1
.LBB0_1565:
	s_andn2_b64 vcc, exec, s[10:11]
	s_cbranch_vccnz .LBB0_1567
	v_mov_b32_e32 v26, v22
	v_mov_b32_e32 v27, v22
	v_pk_mul_f32 v[28:29], v[36:37], v[26:27]
	v_pk_mul_f32 v[30:31], v[40:41], v[22:23]
	v_pk_mul_f32 v[2:3], v[28:29], v[2:3]
	v_pk_mul_f32 v[0:1], v[30:31], v[0:1]
	v_cndmask_b32_e64 v3, v223, v3, s[38:39]
	v_cndmask_b32_e64 v2, v223, v2, s[38:39]
	v_cndmask_b32_e64 v1, v223, v1, s[38:39]
	v_cndmask_b32_e64 v0, v223, v0, s[38:39]
	global_store_dwordx4 v89, v[0:3], s[8:9] sc1
	global_load_dwordx4 v[0:3], v[102:103], off
	v_mov_b32_e32 v28, v18
	v_mov_b32_e32 v29, v18
	v_pk_mul_f32 v[28:29], v[32:33], v[28:29]
	v_pk_mul_f32 v[30:31], v[38:39], v[22:23]
	v_pk_mul_f32 v[26:27], v[34:35], v[26:27]
	s_waitcnt vmcnt(0)
	v_pk_mul_f32 v[28:29], v[28:29], v[2:3]
	v_pk_mul_f32 v[24:25], v[24:25], v[0:1]
	v_pk_mul_f32 v[26:27], v[26:27], v[2:3]
	v_pk_mul_f32 v[30:31], v[30:31], v[0:1]
	v_cndmask_b32_e64 v3, v223, v29, s[38:39]
	v_cndmask_b32_e64 v2, v223, v28, s[38:39]
	v_cndmask_b32_e64 v1, v223, v25, s[38:39]
	v_cndmask_b32_e64 v0, v223, v24, s[38:39]
	v_cndmask_b32_e64 v27, v223, v27, s[38:39]
	v_cndmask_b32_e64 v26, v223, v26, s[38:39]
	v_cndmask_b32_e64 v25, v223, v31, s[38:39]
	v_cndmask_b32_e64 v24, v223, v30, s[38:39]
	global_store_dwordx4 v[114:115], v[0:3], off offset:16 sc1
	global_store_dwordx4 v130, v[24:27], s[8:9] sc1
.LBB0_1567:
	global_load_dwordx4 v[0:3], v[104:105], off
	s_nop 0
	v_mov_b32_e32 v24, v18
	v_mov_b32_e32 v25, v18
	v_pk_mul_f32 v[20:21], v[20:21], v[18:19]
	v_pk_mul_f32 v[16:17], v[16:17], v[24:25]
	s_mov_b64 s[10:11], -1
	s_and_b64 vcc, exec, s[6:7]
	v_pk_mul_f32 v[14:15], v[14:15], v[18:19]
	s_waitcnt vmcnt(0)
	v_pk_mul_f32 v[16:17], v[16:17], v[2:3]
	v_pk_mul_f32 v[20:21], v[20:21], v[0:1]
	v_cndmask_b32_e64 v29, v223, v17, s[38:39]
	v_cndmask_b32_e64 v28, v223, v16, s[38:39]
	v_cndmask_b32_e64 v27, v223, v21, s[38:39]
	v_cndmask_b32_e64 v26, v223, v20, s[38:39]
	global_store_dwordx4 v[114:115], v[26:29], off offset:2048 sc1
	s_cbranch_vccz .LBB0_1569
	global_load_dwordx4 v[26:29], v[106:107], off
	v_pk_mul_f32 v[16:17], v[8:9], v[24:25]
	s_mov_b64 s[10:11], 0
	s_waitcnt vmcnt(0)
	v_pk_mul_f32 v[16:17], v[16:17], v[28:29]
	v_pk_mul_f32 v[20:21], v[14:15], v[26:27]
	v_cndmask_b32_e64 v27, v223, v17, s[38:39]
	v_cndmask_b32_e64 v26, v223, v16, s[38:39]
	v_cndmask_b32_e64 v25, v223, v21, s[38:39]
	v_cndmask_b32_e64 v24, v223, v20, s[38:39]
	global_store_dwordx4 v[114:115], v[24:27], off offset:2064 sc1
.LBB0_1569:
	s_andn2_b64 vcc, exec, s[10:11]
	s_cbranch_vccnz .LBB0_1554
	v_mov_b32_e32 v16, v22
	v_mov_b32_e32 v17, v22
	v_pk_mul_f32 v[4:5], v[4:5], v[16:17]
	v_pk_mul_f32 v[12:13], v[12:13], v[22:23]
	v_pk_mul_f32 v[2:3], v[4:5], v[2:3]
	v_pk_mul_f32 v[0:1], v[12:13], v[0:1]
	v_cndmask_b32_e64 v3, v223, v3, s[38:39]
	v_cndmask_b32_e64 v2, v223, v2, s[38:39]
	v_cndmask_b32_e64 v1, v223, v1, s[38:39]
	v_cndmask_b32_e64 v0, v223, v0, s[38:39]
	global_store_dwordx4 v131, v[0:3], s[8:9] sc1
	global_load_dwordx4 v[0:3], v[106:107], off
	v_mov_b32_e32 v19, v18
	v_pk_mul_f32 v[8:9], v[8:9], v[18:19]
	v_pk_mul_f32 v[4:5], v[10:11], v[22:23]
	v_pk_mul_f32 v[6:7], v[6:7], v[16:17]
	s_waitcnt vmcnt(0)
	v_pk_mul_f32 v[8:9], v[8:9], v[2:3]
	v_pk_mul_f32 v[10:11], v[14:15], v[0:1]
	v_pk_mul_f32 v[6:7], v[6:7], v[2:3]
	v_pk_mul_f32 v[4:5], v[4:5], v[0:1]
	v_cndmask_b32_e64 v3, v223, v9, s[38:39]
	v_cndmask_b32_e64 v2, v223, v8, s[38:39]
	v_cndmask_b32_e64 v1, v223, v11, s[38:39]
	v_cndmask_b32_e64 v0, v223, v10, s[38:39]
	v_cndmask_b32_e64 v7, v223, v7, s[38:39]
	v_cndmask_b32_e64 v6, v223, v6, s[38:39]
	v_cndmask_b32_e64 v5, v223, v5, s[38:39]
	v_cndmask_b32_e64 v4, v223, v4, s[38:39]
	global_store_dwordx4 v[114:115], v[0:3], off offset:2064 sc1
	global_store_dwordx4 v132, v[4:7], s[8:9] sc1
	s_branch .LBB0_1554

.LBB0_1590:
	v_mul_f32_e32 v143, 0xbfb8aa3b, v124
	v_exp_f32_e32 v143, v143
	v_readlane_b32 s24, v253, 45
	v_lshl_or_b32 v144, s43, 7, v140
	v_readlane_b32 s25, v253, 46
	v_add_f32_e32 v143, 1.0, v143
	v_rcp_f32_e32 v143, v143
	v_lshl_add_u32 v142, s44, 8, v138
	v_ashrrev_i32_e32 v145, 31, v144
	s_movk_i32 s9, 0x2c00
	v_mul_f32_e32 v124, v124, v143
	v_mul_f32_e32 v120, v124, v120
	v_mul_f32_e32 v124, 0xbfb8aa3b, v125
	v_exp_f32_e32 v124, v124
	s_andn2_b64 vcc, exec, s[36:37]
	v_add_f32_e32 v124, 1.0, v124
	v_rcp_f32_e32 v124, v124
	s_nop 0
	v_mul_f32_e32 v124, v125, v124
	v_mul_f32_e32 v121, v124, v121
	v_mul_f32_e32 v124, 0xbfb8aa3b, v126
	v_exp_f32_e32 v124, v124
	s_nop 0
	v_add_f32_e32 v124, 1.0, v124
	v_rcp_f32_e32 v124, v124
	s_nop 0
	v_mul_f32_e32 v124, v126, v124
	v_mul_f32_e32 v122, v124, v122
	v_mul_f32_e32 v124, 0xbfb8aa3b, v127
	v_exp_f32_e32 v124, v124
	s_nop 0
	v_add_f32_e32 v124, 1.0, v124
	v_rcp_f32_e32 v124, v124
	s_nop 0
	v_mul_f32_e32 v124, v127, v124
	v_mul_f32_e32 v123, v124, v123
	v_mul_f32_e32 v124, 0xbfb8aa3b, v116
	v_exp_f32_e32 v124, v124
	s_nop 0
	v_add_f32_e32 v124, 1.0, v124
	v_rcp_f32_e32 v124, v124
	s_nop 0
	v_mul_f32_e32 v116, v116, v124
	v_mul_f32_e32 v112, v116, v112
	v_mul_f32_e32 v116, 0xbfb8aa3b, v117
	v_exp_f32_e32 v116, v116
	s_nop 0
	v_add_f32_e32 v116, 1.0, v116
	v_rcp_f32_e32 v116, v116
	s_nop 0
	v_mul_f32_e32 v116, v117, v116
	v_mul_f32_e32 v113, v116, v113
	v_mul_f32_e32 v116, 0xbfb8aa3b, v118
	v_exp_f32_e32 v116, v116
	s_nop 0
	v_add_f32_e32 v116, 1.0, v116
	v_rcp_f32_e32 v116, v116
	s_nop 0
	v_mul_f32_e32 v116, v118, v116
	v_mul_f32_e32 v114, v116, v114
	v_mul_f32_e32 v116, 0xbfb8aa3b, v119
	v_exp_f32_e32 v116, v116
	s_nop 0
	v_add_f32_e32 v116, 1.0, v116
	v_rcp_f32_e32 v116, v116
	s_nop 0
	v_mul_f32_e32 v116, v119, v116
	v_mul_f32_e32 v115, v116, v115
	v_cvt_pk_bf16_f32 v116, v120, v121
	v_cvt_pk_bf16_f32 v117, v122, v123
	v_cvt_pk_bf16_f32 v118, v112, v113
	v_mov_b64_e32 v[112:113], s[24:25]
	v_cvt_pk_bf16_f32 v119, v114, v115
	v_mad_i64_i32 v[120:121], s[24:25], v142, s9, v[112:113]
	v_lshlrev_b64 v[114:115], 1, v[144:145]
	v_lshl_add_u64 v[120:121], v[120:121], 0, v[114:115]
	global_store_dwordx4 v[120:121], v[116:119], off sc1
	s_nop 1
	v_mul_f32_e32 v116, 0xbfb8aa3b, v108
	v_exp_f32_e32 v116, v116
	s_nop 0
	v_add_f32_e32 v116, 1.0, v116
	v_rcp_f32_e32 v116, v116
	s_nop 0
	v_mul_f32_e32 v108, v108, v116
	v_mul_f32_e32 v104, v108, v104
	v_mul_f32_e32 v108, 0xbfb8aa3b, v109
	v_exp_f32_e32 v108, v108
	s_nop 0
	v_add_f32_e32 v108, 1.0, v108
	v_rcp_f32_e32 v108, v108
	s_nop 0
	v_mul_f32_e32 v108, v109, v108
	v_mul_f32_e32 v105, v108, v105
	v_mul_f32_e32 v108, 0xbfb8aa3b, v110
	v_exp_f32_e32 v108, v108
	s_nop 0
	v_add_f32_e32 v108, 1.0, v108
	v_rcp_f32_e32 v108, v108
	s_nop 0
	v_mul_f32_e32 v108, v110, v108
	v_mul_f32_e32 v106, v108, v106
	v_mul_f32_e32 v108, 0xbfb8aa3b, v111
	v_exp_f32_e32 v108, v108
	s_nop 0
	v_add_f32_e32 v108, 1.0, v108
	v_rcp_f32_e32 v108, v108
	s_nop 0
	v_mul_f32_e32 v108, v111, v108
	v_mul_f32_e32 v107, v108, v107
	v_mul_f32_e32 v108, 0xbfb8aa3b, v100
	v_exp_f32_e32 v108, v108
	s_nop 0
	v_add_f32_e32 v108, 1.0, v108
	v_rcp_f32_e32 v108, v108
	s_nop 0
	v_mul_f32_e32 v100, v100, v108
	v_mul_f32_e32 v100, v100, v96
	v_mul_f32_e32 v96, 0xbfb8aa3b, v101
	v_exp_f32_e32 v96, v96
	s_nop 0
	v_add_f32_e32 v96, 1.0, v96
	v_rcp_f32_e32 v96, v96
	s_nop 0
	v_mul_f32_e32 v96, v101, v96
	v_mul_f32_e32 v101, v96, v97
	v_mul_f32_e32 v96, 0xbfb8aa3b, v102
	v_exp_f32_e32 v96, v96
	s_nop 0
	v_add_f32_e32 v96, 1.0, v96
	v_rcp_f32_e32 v96, v96
	s_nop 0
	v_mul_f32_e32 v96, v102, v96
	v_mul_f32_e32 v102, v96, v98
	v_mul_f32_e32 v96, 0xbfb8aa3b, v103
	v_exp_f32_e32 v96, v96
	s_nop 0
	v_add_f32_e32 v96, 1.0, v96
	v_rcp_f32_e32 v96, v96
	s_nop 0
	v_mul_f32_e32 v96, v103, v96
	v_mul_f32_e32 v99, v96, v99
	v_cvt_pk_bf16_f32 v96, v104, v105
	v_cvt_pk_bf16_f32 v97, v106, v107
	v_cvt_pk_bf16_f32 v98, v100, v101
	v_or_b32_e32 v100, 16, v142
	v_mad_i64_i32 v[100:101], s[24:25], v100, s9, v[112:113]
	v_lshl_add_u64 v[100:101], v[100:101], 0, v[114:115]
	v_cvt_pk_bf16_f32 v99, v102, v99
	global_store_dwordx4 v[100:101], v[96:99], off sc1
	s_nop 1
	v_mul_f32_e32 v96, 0xbfb8aa3b, v92
	v_exp_f32_e32 v96, v96
	s_nop 0
	v_add_f32_e32 v96, 1.0, v96
	v_rcp_f32_e32 v96, v96
	s_nop 0
	v_mul_f32_e32 v92, v92, v96
	v_mul_f32_e32 v88, v92, v88
	v_mul_f32_e32 v92, 0xbfb8aa3b, v93
	v_exp_f32_e32 v92, v92
	s_nop 0
	v_add_f32_e32 v92, 1.0, v92
	v_rcp_f32_e32 v92, v92
	s_nop 0
	v_mul_f32_e32 v92, v93, v92
	v_mul_f32_e32 v89, v92, v89
	v_mul_f32_e32 v92, 0xbfb8aa3b, v94
	v_exp_f32_e32 v92, v92
	s_nop 0
	v_add_f32_e32 v92, 1.0, v92
	v_rcp_f32_e32 v92, v92
	s_nop 0
	v_mul_f32_e32 v92, v94, v92
	v_mul_f32_e32 v90, v92, v90
	v_mul_f32_e32 v92, 0xbfb8aa3b, v95
	v_exp_f32_e32 v92, v92
	s_nop 0
	v_add_f32_e32 v92, 1.0, v92
	v_rcp_f32_e32 v92, v92
	s_nop 0
	v_mul_f32_e32 v92, v95, v92
	v_mul_f32_e32 v91, v92, v91
	v_mul_f32_e32 v92, 0xbfb8aa3b, v84
	v_exp_f32_e32 v92, v92
	s_nop 0
	v_add_f32_e32 v92, 1.0, v92
	v_rcp_f32_e32 v92, v92
	s_nop 0
	v_mul_f32_e32 v84, v84, v92
	v_mul_f32_e32 v84, v84, v80
	v_mul_f32_e32 v80, 0xbfb8aa3b, v85
	v_exp_f32_e32 v80, v80
	s_nop 0
	v_add_f32_e32 v80, 1.0, v80
	v_rcp_f32_e32 v80, v80
	s_nop 0
	v_mul_f32_e32 v80, v85, v80
	v_mul_f32_e32 v85, v80, v81
	v_mul_f32_e32 v80, 0xbfb8aa3b, v86
	v_exp_f32_e32 v80, v80
	s_nop 0
	v_add_f32_e32 v80, 1.0, v80
	v_rcp_f32_e32 v80, v80
	s_nop 0
	v_mul_f32_e32 v80, v86, v80
	v_mul_f32_e32 v86, v80, v82
	v_mul_f32_e32 v80, 0xbfb8aa3b, v87
	v_exp_f32_e32 v80, v80
	s_nop 0
	v_add_f32_e32 v80, 1.0, v80
	v_rcp_f32_e32 v80, v80
	s_nop 0
	v_mul_f32_e32 v80, v87, v80
	v_mul_f32_e32 v83, v80, v83
	v_cvt_pk_bf16_f32 v80, v88, v89
	v_cvt_pk_bf16_f32 v81, v90, v91
	v_cvt_pk_bf16_f32 v82, v84, v85
	v_or_b32_e32 v84, 32, v142
	v_mad_i64_i32 v[84:85], s[24:25], v84, s9, v[112:113]
	v_lshl_add_u64 v[84:85], v[84:85], 0, v[114:115]
	v_cvt_pk_bf16_f32 v83, v86, v83
	global_store_dwordx4 v[84:85], v[80:83], off sc1
	s_nop 1
	v_mul_f32_e32 v80, 0xbfb8aa3b, v76
	v_exp_f32_e32 v80, v80
	s_nop 0
	v_add_f32_e32 v80, 1.0, v80
	v_rcp_f32_e32 v80, v80
	s_nop 0
	v_mul_f32_e32 v76, v76, v80
	v_mul_f32_e32 v72, v76, v72
	v_mul_f32_e32 v76, 0xbfb8aa3b, v77
	v_exp_f32_e32 v76, v76
	s_nop 0
	v_add_f32_e32 v76, 1.0, v76
	v_rcp_f32_e32 v76, v76
	s_nop 0
	v_mul_f32_e32 v76, v77, v76
	v_mul_f32_e32 v73, v76, v73
	v_mul_f32_e32 v76, 0xbfb8aa3b, v78
	v_exp_f32_e32 v76, v76
	s_nop 0
	v_add_f32_e32 v76, 1.0, v76
	v_rcp_f32_e32 v76, v76
	s_nop 0
	v_mul_f32_e32 v76, v78, v76
	v_mul_f32_e32 v74, v76, v74
	v_mul_f32_e32 v76, 0xbfb8aa3b, v79
	v_exp_f32_e32 v76, v76
	s_nop 0
	v_add_f32_e32 v76, 1.0, v76
	v_rcp_f32_e32 v76, v76
	s_nop 0
	v_mul_f32_e32 v76, v79, v76
	v_mul_f32_e32 v75, v76, v75
	v_mul_f32_e32 v76, 0xbfb8aa3b, v68
	v_exp_f32_e32 v76, v76
	s_nop 0
	v_add_f32_e32 v76, 1.0, v76
	v_rcp_f32_e32 v76, v76
	s_nop 0
	v_mul_f32_e32 v68, v68, v76
	v_mul_f32_e32 v68, v68, v64
	v_mul_f32_e32 v64, 0xbfb8aa3b, v69
	v_exp_f32_e32 v64, v64
	s_nop 0
	v_add_f32_e32 v64, 1.0, v64
	v_rcp_f32_e32 v64, v64
	s_nop 0
	v_mul_f32_e32 v64, v69, v64
	v_mul_f32_e32 v69, v64, v65
	v_mul_f32_e32 v64, 0xbfb8aa3b, v70
	v_exp_f32_e32 v64, v64
	s_nop 0
	v_add_f32_e32 v64, 1.0, v64
	v_rcp_f32_e32 v64, v64
	s_nop 0
	v_mul_f32_e32 v64, v70, v64
	v_mul_f32_e32 v70, v64, v66
	v_mul_f32_e32 v64, 0xbfb8aa3b, v71
	v_exp_f32_e32 v64, v64
	s_nop 0
	v_add_f32_e32 v64, 1.0, v64
	v_rcp_f32_e32 v64, v64
	s_nop 0
	v_mul_f32_e32 v64, v71, v64
	v_mul_f32_e32 v67, v64, v67
	v_cvt_pk_bf16_f32 v64, v72, v73
	v_cvt_pk_bf16_f32 v65, v74, v75
	v_cvt_pk_bf16_f32 v66, v68, v69
	v_or_b32_e32 v68, 48, v142
	v_mad_i64_i32 v[68:69], s[24:25], v68, s9, v[112:113]
	v_lshl_add_u64 v[68:69], v[68:69], 0, v[114:115]
	v_cvt_pk_bf16_f32 v67, v70, v67
	global_store_dwordx4 v[68:69], v[64:67], off sc1
	s_nop 1
	v_mul_f32_e32 v65, 0xbfb8aa3b, v60
	v_exp_f32_e32 v65, v65
	v_add_u32_e32 v64, 0x80, v142
	v_add_f32_e32 v65, 1.0, v65
	v_rcp_f32_e32 v65, v65
	s_nop 0
	v_mul_f32_e32 v60, v60, v65
	v_mul_f32_e32 v56, v60, v56
	v_mul_f32_e32 v60, 0xbfb8aa3b, v61
	v_exp_f32_e32 v60, v60
	s_nop 0
	v_add_f32_e32 v60, 1.0, v60
	v_rcp_f32_e32 v60, v60
	s_nop 0
	v_mul_f32_e32 v60, v61, v60
	v_mul_f32_e32 v57, v60, v57
	v_mul_f32_e32 v60, 0xbfb8aa3b, v62
	v_exp_f32_e32 v60, v60
	s_nop 0
	v_add_f32_e32 v60, 1.0, v60
	v_rcp_f32_e32 v60, v60
	s_nop 0
	v_mul_f32_e32 v60, v62, v60
	v_mul_f32_e32 v58, v60, v58
	v_mul_f32_e32 v60, 0xbfb8aa3b, v63
	v_exp_f32_e32 v60, v60
	s_nop 0
	v_add_f32_e32 v60, 1.0, v60
	v_rcp_f32_e32 v60, v60
	s_nop 0
	v_mul_f32_e32 v60, v63, v60
	v_mul_f32_e32 v59, v60, v59
	v_mul_f32_e32 v60, 0xbfb8aa3b, v52
	v_exp_f32_e32 v60, v60
	s_nop 0
	v_add_f32_e32 v60, 1.0, v60
	v_rcp_f32_e32 v60, v60
	s_nop 0
	v_mul_f32_e32 v52, v52, v60
	v_mul_f32_e32 v52, v52, v48
	v_mul_f32_e32 v48, 0xbfb8aa3b, v53
	v_exp_f32_e32 v48, v48
	s_nop 0
	v_add_f32_e32 v48, 1.0, v48
	v_rcp_f32_e32 v48, v48
	s_nop 0
	v_mul_f32_e32 v48, v53, v48
	v_mul_f32_e32 v53, v48, v49
	v_mul_f32_e32 v48, 0xbfb8aa3b, v54
	v_exp_f32_e32 v48, v48
	s_nop 0
	v_add_f32_e32 v48, 1.0, v48
	v_rcp_f32_e32 v48, v48
	s_nop 0
	v_mul_f32_e32 v48, v54, v48
	v_mul_f32_e32 v54, v48, v50
	v_mul_f32_e32 v48, 0xbfb8aa3b, v55
	v_exp_f32_e32 v48, v48
	s_nop 0
	v_add_f32_e32 v48, 1.0, v48
	v_rcp_f32_e32 v48, v48
	s_nop 0
	v_mul_f32_e32 v48, v55, v48
	v_mul_f32_e32 v51, v48, v51
	v_cvt_pk_bf16_f32 v48, v56, v57
	v_cvt_pk_bf16_f32 v49, v58, v59
	v_cvt_pk_bf16_f32 v50, v52, v53
	v_mad_i64_i32 v[52:53], s[24:25], v64, s9, v[112:113]
	v_lshl_add_u64 v[52:53], v[52:53], 0, v[114:115]
	v_cvt_pk_bf16_f32 v51, v54, v51
	global_store_dwordx4 v[52:53], v[48:51], off sc1
	s_nop 1
	v_mul_f32_e32 v48, 0xbfb8aa3b, v44
	v_exp_f32_e32 v48, v48
	s_nop 0
	v_add_f32_e32 v48, 1.0, v48
	v_rcp_f32_e32 v48, v48
	s_nop 0
	v_mul_f32_e32 v44, v44, v48
	v_mul_f32_e32 v40, v44, v40
	v_mul_f32_e32 v44, 0xbfb8aa3b, v45
	v_exp_f32_e32 v44, v44
	s_nop 0
	v_add_f32_e32 v44, 1.0, v44
	v_rcp_f32_e32 v44, v44
	s_nop 0
	v_mul_f32_e32 v44, v45, v44
	v_mul_f32_e32 v41, v44, v41
	v_mul_f32_e32 v44, 0xbfb8aa3b, v46
	v_exp_f32_e32 v44, v44
	s_nop 0
	v_add_f32_e32 v44, 1.0, v44
	v_rcp_f32_e32 v44, v44
	s_nop 0
	v_mul_f32_e32 v44, v46, v44
	v_mul_f32_e32 v42, v44, v42
	v_mul_f32_e32 v44, 0xbfb8aa3b, v47
	v_exp_f32_e32 v44, v44
	s_nop 0
	v_add_f32_e32 v44, 1.0, v44
	v_rcp_f32_e32 v44, v44
	s_nop 0
	v_mul_f32_e32 v44, v47, v44
	v_mul_f32_e32 v43, v44, v43
	v_mul_f32_e32 v44, 0xbfb8aa3b, v36
	v_exp_f32_e32 v44, v44
	s_nop 0
	v_add_f32_e32 v44, 1.0, v44
	v_rcp_f32_e32 v44, v44
	s_nop 0
	v_mul_f32_e32 v36, v36, v44
	v_mul_f32_e32 v36, v36, v32
	v_mul_f32_e32 v32, 0xbfb8aa3b, v37
	v_exp_f32_e32 v32, v32
	s_nop 0
	v_add_f32_e32 v32, 1.0, v32
	v_rcp_f32_e32 v32, v32
	s_nop 0
	v_mul_f32_e32 v32, v37, v32
	v_mul_f32_e32 v37, v32, v33
	v_mul_f32_e32 v32, 0xbfb8aa3b, v38
	v_exp_f32_e32 v32, v32
	s_nop 0
	v_add_f32_e32 v32, 1.0, v32
	v_rcp_f32_e32 v32, v32
	s_nop 0
	v_mul_f32_e32 v32, v38, v32
	v_mul_f32_e32 v38, v32, v34
	v_mul_f32_e32 v32, 0xbfb8aa3b, v39
	v_exp_f32_e32 v32, v32
	s_nop 0
	v_add_f32_e32 v32, 1.0, v32
	v_rcp_f32_e32 v32, v32
	s_nop 0
	v_mul_f32_e32 v32, v39, v32
	v_mul_f32_e32 v35, v32, v35
	v_cvt_pk_bf16_f32 v32, v40, v41
	v_cvt_pk_bf16_f32 v33, v42, v43
	v_cvt_pk_bf16_f32 v34, v36, v37
	v_add_u32_e32 v36, 0x90, v142
	v_mad_i64_i32 v[36:37], s[24:25], v36, s9, v[112:113]
	v_lshl_add_u64 v[36:37], v[36:37], 0, v[114:115]
	v_cvt_pk_bf16_f32 v35, v38, v35
	global_store_dwordx4 v[36:37], v[32:35], off sc1
	s_nop 1
	v_mul_f32_e32 v32, 0xbfb8aa3b, v28
	v_exp_f32_e32 v32, v32
	s_nop 0
	v_add_f32_e32 v32, 1.0, v32
	v_rcp_f32_e32 v32, v32
	s_nop 0
	v_mul_f32_e32 v28, v28, v32
	v_mul_f32_e32 v24, v28, v24
	v_mul_f32_e32 v28, 0xbfb8aa3b, v29
	v_exp_f32_e32 v28, v28
	s_nop 0
	v_add_f32_e32 v28, 1.0, v28
	v_rcp_f32_e32 v28, v28
	s_nop 0
	v_mul_f32_e32 v28, v29, v28
	v_mul_f32_e32 v25, v28, v25
	v_mul_f32_e32 v28, 0xbfb8aa3b, v30
	v_exp_f32_e32 v28, v28
	s_nop 0
	v_add_f32_e32 v28, 1.0, v28
	v_rcp_f32_e32 v28, v28
	s_nop 0
	v_mul_f32_e32 v28, v30, v28
	v_mul_f32_e32 v26, v28, v26
	v_mul_f32_e32 v28, 0xbfb8aa3b, v31
	v_exp_f32_e32 v28, v28
	s_nop 0
	v_add_f32_e32 v28, 1.0, v28
	v_rcp_f32_e32 v28, v28
	s_nop 0
	v_mul_f32_e32 v28, v31, v28
	v_mul_f32_e32 v27, v28, v27
	v_mul_f32_e32 v28, 0xbfb8aa3b, v20
	v_exp_f32_e32 v28, v28
	s_nop 0
	v_add_f32_e32 v28, 1.0, v28
	v_rcp_f32_e32 v28, v28
	s_nop 0
	v_mul_f32_e32 v20, v20, v28
	v_mul_f32_e32 v20, v20, v16
	v_mul_f32_e32 v16, 0xbfb8aa3b, v21
	v_exp_f32_e32 v16, v16
	s_nop 0
	v_add_f32_e32 v16, 1.0, v16
	v_rcp_f32_e32 v16, v16
	s_nop 0
	v_mul_f32_e32 v16, v21, v16
	v_mul_f32_e32 v21, v16, v17
	v_mul_f32_e32 v16, 0xbfb8aa3b, v22
	v_exp_f32_e32 v16, v16
	s_nop 0
	v_add_f32_e32 v16, 1.0, v16
	v_rcp_f32_e32 v16, v16
	s_nop 0
	v_mul_f32_e32 v16, v22, v16
	v_mul_f32_e32 v22, v16, v18
	v_mul_f32_e32 v16, 0xbfb8aa3b, v23
	v_exp_f32_e32 v16, v16
	s_nop 0
	v_add_f32_e32 v16, 1.0, v16
	v_rcp_f32_e32 v16, v16
	s_nop 0
	v_mul_f32_e32 v16, v23, v16
	v_mul_f32_e32 v19, v16, v19
	v_cvt_pk_bf16_f32 v16, v24, v25
	v_cvt_pk_bf16_f32 v17, v26, v27
	v_cvt_pk_bf16_f32 v18, v20, v21
	v_add_u32_e32 v20, 0xa0, v142
	v_mad_i64_i32 v[20:21], s[24:25], v20, s9, v[112:113]
	v_lshl_add_u64 v[20:21], v[20:21], 0, v[114:115]
	v_cvt_pk_bf16_f32 v19, v22, v19
	global_store_dwordx4 v[20:21], v[16:19], off sc1
	s_nop 1
	v_mul_f32_e32 v16, 0xbfb8aa3b, v12
	v_exp_f32_e32 v16, v16
	s_nop 0
	v_add_f32_e32 v16, 1.0, v16
	v_rcp_f32_e32 v16, v16
	s_nop 0
	v_mul_f32_e32 v12, v12, v16
	v_mul_f32_e32 v8, v12, v8
	v_mul_f32_e32 v12, 0xbfb8aa3b, v13
	v_exp_f32_e32 v12, v12
	s_nop 0
	v_add_f32_e32 v12, 1.0, v12
	v_rcp_f32_e32 v12, v12
	s_nop 0
	v_mul_f32_e32 v12, v13, v12
	v_mul_f32_e32 v9, v12, v9
	v_mul_f32_e32 v12, 0xbfb8aa3b, v14
	v_exp_f32_e32 v12, v12
	s_nop 0
	v_add_f32_e32 v12, 1.0, v12
	v_rcp_f32_e32 v12, v12
	s_nop 0
	v_mul_f32_e32 v12, v14, v12
	v_mul_f32_e32 v10, v12, v10
	v_mul_f32_e32 v12, 0xbfb8aa3b, v15
	v_exp_f32_e32 v12, v12
	s_nop 0
	v_add_f32_e32 v12, 1.0, v12
	v_rcp_f32_e32 v12, v12
	s_nop 0
	v_mul_f32_e32 v12, v15, v12
	v_mul_f32_e32 v11, v12, v11
	v_mul_f32_e32 v12, 0xbfb8aa3b, v4
	v_exp_f32_e32 v12, v12
	s_nop 0
	v_add_f32_e32 v12, 1.0, v12
	v_rcp_f32_e32 v12, v12
	s_nop 0
	v_mul_f32_e32 v4, v4, v12
	v_mul_f32_e32 v4, v4, v0
	v_mul_f32_e32 v0, 0xbfb8aa3b, v5
	v_exp_f32_e32 v0, v0
	s_nop 0
	v_add_f32_e32 v0, 1.0, v0
	v_rcp_f32_e32 v0, v0
	s_nop 0
	v_mul_f32_e32 v0, v5, v0
	v_mul_f32_e32 v5, v0, v1
	v_mul_f32_e32 v0, 0xbfb8aa3b, v6
	v_exp_f32_e32 v0, v0
	s_nop 0
	v_add_f32_e32 v0, 1.0, v0
	v_rcp_f32_e32 v0, v0
	s_nop 0
	v_mul_f32_e32 v0, v6, v0
	v_mul_f32_e32 v6, v0, v2
	v_mul_f32_e32 v0, 0xbfb8aa3b, v7
	v_exp_f32_e32 v0, v0
	s_nop 0
	v_add_f32_e32 v0, 1.0, v0
	v_rcp_f32_e32 v0, v0
	s_nop 0
	v_mul_f32_e32 v0, v7, v0
	v_mul_f32_e32 v3, v0, v3
	v_cvt_pk_bf16_f32 v0, v8, v9
	v_cvt_pk_bf16_f32 v1, v10, v11
	v_cvt_pk_bf16_f32 v2, v4, v5
	v_add_u32_e32 v4, 0xb0, v142
	v_mad_i64_i32 v[4:5], s[24:25], v4, s9, v[112:113]
	v_lshl_add_u64 v[4:5], v[4:5], 0, v[114:115]
	s_mov_b64 s[24:25], -1
	v_cvt_pk_bf16_f32 v3, v6, v3
	global_store_dwordx4 v[4:5], v[0:3], off sc1
	s_cbranch_vccnz .LBB0_1579
	s_andn2_b64 vcc, exec, s[0:1]
	s_cbranch_vccnz .LBB0_1578
	s_barrier
	s_branch .LBB0_1578

.LBB0_1664:
	s_cmp_lt_i32 s50, 64
	s_cselect_b64 s[18:19], -1, 0
	s_lshl_b32 s24, s50, 8
	s_cmp_gt_i32 s50, 63
	s_cselect_b32 s25, s1, s41
	s_cselect_b32 s28, s0, s40
	v_lshl_or_b32 v154, s47, 8, v164
	v_mov_b32_e32 v64, s28
	v_mov_b32_e32 v65, s25
	v_ashrrev_i32_e32 v155, 31, v154
	v_lshl_add_u64 v[68:69], v[154:155], 2, v[64:65]
	global_load_dwordx4 v[80:83], v[68:69], off offset:16
	global_load_dwordx4 v[84:87], v[68:69], off
	global_load_dwordx4 v[64:67], v[68:69], off offset:528
	s_nop 0
	global_load_dwordx4 v[68:71], v[68:69], off offset:512
	s_cselect_b32 s24, 0, s24
	v_add_u32_e32 v156, s24, v162
	v_ashrrev_i32_e32 v157, 31, v156
	v_lshlrev_b64 v[158:159], 11, v[156:157]
	v_readlane_b32 s28, v249, 60
	v_lshl_add_u64 v[160:161], v[158:159], 0, v[154:155]
	v_readlane_b32 s29, v249, 61
	s_mov_b64 s[24:25], -1
	s_and_b64 vcc, exec, s[18:19]
	v_lshl_add_u64 v[158:159], v[160:161], 1, s[28:29]
	s_cbranch_vccz .LBB0_1666
	global_load_dwordx4 v[166:169], v[158:159], off
	s_mov_b64 s[24:25], 0
	s_waitcnt vmcnt(0)
	v_lshlrev_b32_e32 v170, 16, v166
	v_and_b32_e32 v171, 0xffff0000, v166
	v_lshlrev_b32_e32 v166, 16, v167
	v_and_b32_e32 v167, 0xffff0000, v167
	v_lshlrev_b32_e32 v172, 16, v168
	v_and_b32_e32 v173, 0xffff0000, v168
	v_lshlrev_b32_e32 v168, 16, v169
	v_and_b32_e32 v169, 0xffff0000, v169
	v_pk_fma_f32 v[174:175], v[142:143], v[86:87], v[166:167]
	v_pk_fma_f32 v[166:167], v[140:141], v[84:85], v[170:171]
	v_pk_fma_f32 v[170:171], v[138:139], v[82:83], v[168:169]
	v_pk_fma_f32 v[168:169], v[136:137], v[80:81], v[172:173]
	v_cvt_pk_bf16_f32 v166, v166, v167
	v_cvt_pk_bf16_f32 v167, v174, v175
	s_nop 0
	v_cvt_pk_bf16_f32 v168, v168, v169
	v_cvt_pk_bf16_f32 v169, v170, v171
	global_store_dwordx4 v[158:159], v[166:169], off sc1
.LBB0_1666:
	s_andn2_b64 vcc, exec, s[24:25]
	v_readlane_b32 s24, v249, 58
	v_readlane_b32 s25, v249, 59
	s_nop 1
	v_lshl_add_u64 v[160:161], v[160:161], 2, s[24:25]
	s_cbranch_vccnz .LBB0_1668
	global_load_dwordx4 v[166:169], v[160:161], off
	global_load_dwordx4 v[170:173], v[160:161], off offset:16
	s_waitcnt vmcnt(0)
	v_pk_fma_f32 v[142:143], v[142:143], v[86:87], v[168:169]
	v_pk_fma_f32 v[140:141], v[140:141], v[84:85], v[166:167]
	v_pk_fma_f32 v[138:139], v[138:139], v[82:83], v[172:173]
	v_pk_fma_f32 v[136:137], v[136:137], v[80:81], v[170:171]
	global_store_dwordx4 v[160:161], v[140:143], off sc1
	global_store_dwordx4 v[160:161], v[136:139], off offset:16 sc1
.LBB0_1668:
	s_nop 1
	v_cndmask_b32_e64 v136, 0, 1, s[18:19]
	v_cmp_ne_u32_e64 s[38:39], 1, v136
	s_andn2_b64 vcc, exec, s[18:19]
	s_mov_b64 s[18:19], -1
	s_cbranch_vccnz .LBB0_1670
	global_load_dwordx4 v[136:139], v[158:159], off offset:256
	s_mov_b64 s[18:19], 0
	s_waitcnt vmcnt(0)
	v_lshlrev_b32_e32 v140, 16, v136
	v_and_b32_e32 v141, 0xffff0000, v136
	v_lshlrev_b32_e32 v136, 16, v137
	v_and_b32_e32 v137, 0xffff0000, v137
	v_lshlrev_b32_e32 v142, 16, v138
	v_and_b32_e32 v143, 0xffff0000, v138
	v_lshlrev_b32_e32 v138, 16, v139
	v_and_b32_e32 v139, 0xffff0000, v139
	v_pk_fma_f32 v[166:167], v[134:135], v[70:71], v[136:137]
	v_pk_fma_f32 v[136:137], v[132:133], v[68:69], v[140:141]
	v_pk_fma_f32 v[140:141], v[130:131], v[66:67], v[138:139]
	v_pk_fma_f32 v[138:139], v[128:129], v[64:65], v[142:143]
	v_cvt_pk_bf16_f32 v136, v136, v137
	v_cvt_pk_bf16_f32 v137, v166, v167
	s_nop 0
	v_cvt_pk_bf16_f32 v138, v138, v139
	v_cvt_pk_bf16_f32 v139, v140, v141
	global_store_dwordx4 v[158:159], v[136:139], off offset:256 sc1
.LBB0_1670:
	s_andn2_b64 vcc, exec, s[18:19]
	s_cbranch_vccnz .LBB0_1672
	global_load_dwordx4 v[136:139], v[160:161], off offset:512
	global_load_dwordx4 v[140:143], v[160:161], off offset:528
	s_waitcnt vmcnt(0)
	v_pk_fma_f32 v[134:135], v[134:135], v[70:71], v[138:139]
	v_pk_fma_f32 v[132:133], v[132:133], v[68:69], v[136:137]
	v_pk_fma_f32 v[130:131], v[130:131], v[66:67], v[142:143]
	v_pk_fma_f32 v[128:129], v[128:129], v[64:65], v[140:141]
	global_store_dwordx4 v[160:161], v[132:135], off offset:512 sc1
	global_store_dwordx4 v[160:161], v[128:131], off offset:528 sc1
.LBB0_1672:
	s_nop 1
	v_or_b32_e32 v128, 16, v156
	v_ashrrev_i32_e32 v129, 31, v128
	v_lshlrev_b64 v[128:129], 11, v[128:129]
	v_readlane_b32 s24, v249, 60
	v_lshl_add_u64 v[130:131], v[128:129], 0, v[154:155]
	v_readlane_b32 s25, v249, 61
	s_mov_b64 s[18:19], -1
	s_and_b64 vcc, exec, s[38:39]
	v_lshl_add_u64 v[128:129], v[130:131], 1, s[24:25]
	s_cbranch_vccnz .LBB0_1674
	global_load_dwordx4 v[132:135], v[128:129], off
	s_mov_b64 s[18:19], 0
	s_waitcnt vmcnt(0)
	v_lshlrev_b32_e32 v136, 16, v132
	v_and_b32_e32 v137, 0xffff0000, v132
	v_lshlrev_b32_e32 v132, 16, v133
	v_and_b32_e32 v133, 0xffff0000, v133
	v_lshlrev_b32_e32 v138, 16, v134
	v_and_b32_e32 v139, 0xffff0000, v134
	v_lshlrev_b32_e32 v134, 16, v135
	v_and_b32_e32 v135, 0xffff0000, v135
	v_pk_fma_f32 v[140:141], v[126:127], v[86:87], v[132:133]
	v_pk_fma_f32 v[132:133], v[124:125], v[84:85], v[136:137]
	v_pk_fma_f32 v[136:137], v[122:123], v[82:83], v[134:135]
	v_pk_fma_f32 v[134:135], v[120:121], v[80:81], v[138:139]
	v_cvt_pk_bf16_f32 v132, v132, v133
	v_cvt_pk_bf16_f32 v133, v140, v141
	s_nop 0
	v_cvt_pk_bf16_f32 v134, v134, v135
	v_cvt_pk_bf16_f32 v135, v136, v137
	global_store_dwordx4 v[128:129], v[132:135], off sc1
.LBB0_1674:
	s_andn2_b64 vcc, exec, s[18:19]
	v_readlane_b32 s18, v249, 58
	v_readlane_b32 s19, v249, 59
	s_nop 1
	v_lshl_add_u64 v[130:131], v[130:131], 2, s[18:19]
	s_cbranch_vccnz .LBB0_1717
	global_load_dwordx4 v[132:135], v[130:131], off
	global_load_dwordx4 v[136:139], v[130:131], off offset:16
	s_waitcnt vmcnt(0)
	v_pk_fma_f32 v[126:127], v[126:127], v[86:87], v[134:135]
	v_pk_fma_f32 v[124:125], v[124:125], v[84:85], v[132:133]
	v_pk_fma_f32 v[122:123], v[122:123], v[82:83], v[138:139]
	v_pk_fma_f32 v[120:121], v[120:121], v[80:81], v[136:137]
	global_store_dwordx4 v[130:131], v[124:127], off sc1
	global_store_dwordx4 v[130:131], v[120:123], off offset:16 sc1
	s_and_b64 vcc, exec, s[38:39]
	s_mov_b64 s[18:19], -1
	s_cbranch_vccz .LBB0_1718

.LBB0_1677:
	global_load_dwordx4 v[120:123], v[130:131], off offset:512
	global_load_dwordx4 v[124:127], v[130:131], off offset:528
	s_waitcnt vmcnt(0)
	v_pk_fma_f32 v[118:119], v[118:119], v[70:71], v[122:123]
	v_pk_fma_f32 v[116:117], v[116:117], v[68:69], v[120:121]
	v_pk_fma_f32 v[114:115], v[114:115], v[66:67], v[126:127]
	v_pk_fma_f32 v[112:113], v[112:113], v[64:65], v[124:125]
	global_store_dwordx4 v[130:131], v[116:119], off offset:512 sc1
	global_store_dwordx4 v[130:131], v[112:115], off offset:528 sc1
.LBB0_1678:
	s_nop 1
	v_or_b32_e32 v112, 32, v156
	v_ashrrev_i32_e32 v113, 31, v112
	v_lshlrev_b64 v[112:113], 11, v[112:113]
	v_readlane_b32 s24, v249, 60
	v_lshl_add_u64 v[114:115], v[112:113], 0, v[154:155]
	v_readlane_b32 s25, v249, 61
	s_mov_b64 s[18:19], -1
	s_and_b64 vcc, exec, s[38:39]
	v_lshl_add_u64 v[112:113], v[114:115], 1, s[24:25]
	s_cbranch_vccnz .LBB0_1680
	global_load_dwordx4 v[116:119], v[112:113], off
	s_mov_b64 s[18:19], 0
	s_waitcnt vmcnt(0)
	v_lshlrev_b32_e32 v120, 16, v116
	v_and_b32_e32 v121, 0xffff0000, v116
	v_lshlrev_b32_e32 v116, 16, v117
	v_and_b32_e32 v117, 0xffff0000, v117
	v_lshlrev_b32_e32 v122, 16, v118
	v_and_b32_e32 v123, 0xffff0000, v118
	v_lshlrev_b32_e32 v118, 16, v119
	v_and_b32_e32 v119, 0xffff0000, v119
	v_pk_fma_f32 v[124:125], v[110:111], v[86:87], v[116:117]
	v_pk_fma_f32 v[116:117], v[108:109], v[84:85], v[120:121]
	v_pk_fma_f32 v[120:121], v[106:107], v[82:83], v[118:119]
	v_pk_fma_f32 v[118:119], v[104:105], v[80:81], v[122:123]
	v_cvt_pk_bf16_f32 v116, v116, v117
	v_cvt_pk_bf16_f32 v117, v124, v125
	s_nop 0
	v_cvt_pk_bf16_f32 v118, v118, v119
	v_cvt_pk_bf16_f32 v119, v120, v121
	global_store_dwordx4 v[112:113], v[116:119], off sc1
.LBB0_1680:
	s_andn2_b64 vcc, exec, s[18:19]
	v_readlane_b32 s18, v249, 58
	v_readlane_b32 s19, v249, 59
	s_nop 1
	v_lshl_add_u64 v[114:115], v[114:115], 2, s[18:19]
	s_cbranch_vccnz .LBB0_1719
	global_load_dwordx4 v[116:119], v[114:115], off
	global_load_dwordx4 v[120:123], v[114:115], off offset:16
	s_waitcnt vmcnt(0)
	v_pk_fma_f32 v[110:111], v[110:111], v[86:87], v[118:119]
	v_pk_fma_f32 v[108:109], v[108:109], v[84:85], v[116:117]
	v_pk_fma_f32 v[106:107], v[106:107], v[82:83], v[122:123]
	v_pk_fma_f32 v[104:105], v[104:105], v[80:81], v[120:121]
	global_store_dwordx4 v[114:115], v[108:111], off sc1
	global_store_dwordx4 v[114:115], v[104:107], off offset:16 sc1
	s_and_b64 vcc, exec, s[38:39]
	s_mov_b64 s[18:19], -1
	s_cbranch_vccz .LBB0_1720

.LBB0_1683:
	global_load_dwordx4 v[104:107], v[114:115], off offset:512
	global_load_dwordx4 v[108:111], v[114:115], off offset:528
	s_waitcnt vmcnt(0)
	v_pk_fma_f32 v[102:103], v[102:103], v[70:71], v[106:107]
	v_pk_fma_f32 v[100:101], v[100:101], v[68:69], v[104:105]
	v_pk_fma_f32 v[98:99], v[98:99], v[66:67], v[110:111]
	v_pk_fma_f32 v[96:97], v[96:97], v[64:65], v[108:109]
	global_store_dwordx4 v[114:115], v[100:103], off offset:512 sc1
	global_store_dwordx4 v[114:115], v[96:99], off offset:528 sc1
.LBB0_1684:
	s_nop 1
	v_or_b32_e32 v96, 48, v156
	v_ashrrev_i32_e32 v97, 31, v96
	v_lshlrev_b64 v[96:97], 11, v[96:97]
	v_readlane_b32 s24, v249, 60
	v_lshl_add_u64 v[98:99], v[96:97], 0, v[154:155]
	v_readlane_b32 s25, v249, 61
	s_mov_b64 s[18:19], -1
	s_and_b64 vcc, exec, s[38:39]
	v_lshl_add_u64 v[96:97], v[98:99], 1, s[24:25]
	s_cbranch_vccnz .LBB0_1686
	global_load_dwordx4 v[100:103], v[96:97], off
	s_mov_b64 s[18:19], 0
	s_waitcnt vmcnt(0)
	v_lshlrev_b32_e32 v104, 16, v100
	v_and_b32_e32 v105, 0xffff0000, v100
	v_lshlrev_b32_e32 v100, 16, v101
	v_and_b32_e32 v101, 0xffff0000, v101
	v_lshlrev_b32_e32 v106, 16, v102
	v_and_b32_e32 v107, 0xffff0000, v102
	v_lshlrev_b32_e32 v102, 16, v103
	v_and_b32_e32 v103, 0xffff0000, v103
	v_pk_fma_f32 v[108:109], v[94:95], v[86:87], v[100:101]
	v_pk_fma_f32 v[100:101], v[92:93], v[84:85], v[104:105]
	v_pk_fma_f32 v[104:105], v[90:91], v[82:83], v[102:103]
	v_pk_fma_f32 v[102:103], v[88:89], v[80:81], v[106:107]
	v_cvt_pk_bf16_f32 v100, v100, v101
	v_cvt_pk_bf16_f32 v101, v108, v109
	s_nop 0
	v_cvt_pk_bf16_f32 v102, v102, v103
	v_cvt_pk_bf16_f32 v103, v104, v105
	global_store_dwordx4 v[96:97], v[100:103], off sc1
.LBB0_1686:
	s_andn2_b64 vcc, exec, s[18:19]
	v_readlane_b32 s18, v249, 58
	v_readlane_b32 s19, v249, 59
	s_nop 1
	v_lshl_add_u64 v[98:99], v[98:99], 2, s[18:19]
	s_cbranch_vccnz .LBB0_1721
	global_load_dwordx4 v[100:103], v[98:99], off
	global_load_dwordx4 v[104:107], v[98:99], off offset:16
	s_waitcnt vmcnt(0)
	v_pk_fma_f32 v[94:95], v[94:95], v[86:87], v[102:103]
	v_pk_fma_f32 v[92:93], v[92:93], v[84:85], v[100:101]
	v_pk_fma_f32 v[90:91], v[90:91], v[82:83], v[106:107]
	v_pk_fma_f32 v[88:89], v[88:89], v[80:81], v[104:105]
	global_store_dwordx4 v[98:99], v[92:95], off sc1
	global_store_dwordx4 v[98:99], v[88:91], off offset:16 sc1
	s_and_b64 vcc, exec, s[38:39]
	s_mov_b64 s[18:19], -1
	s_cbranch_vccz .LBB0_1722

.LBB0_1689:
	global_load_dwordx4 v[88:91], v[98:99], off offset:512
	global_load_dwordx4 v[92:95], v[98:99], off offset:528
	s_waitcnt vmcnt(0)
	v_pk_fma_f32 v[78:79], v[78:79], v[70:71], v[90:91]
	v_pk_fma_f32 v[76:77], v[76:77], v[68:69], v[88:89]
	v_pk_fma_f32 v[74:75], v[74:75], v[66:67], v[94:95]
	v_pk_fma_f32 v[72:73], v[72:73], v[64:65], v[92:93]
	global_store_dwordx4 v[98:99], v[76:79], off offset:512 sc1
	global_store_dwordx4 v[98:99], v[72:75], off offset:528 sc1
.LBB0_1690:
	s_nop 1
	v_lshlrev_b64 v[72:73], 11, v[156:157]
	v_lshl_add_u64 v[72:73], v[72:73], 0, v[154:155]
	s_mov_b64 s[18:19], 0x40000
	v_readlane_b32 s24, v249, 60
	v_lshl_add_u64 v[74:75], v[72:73], 0, s[18:19]
	v_readlane_b32 s25, v249, 61
	s_mov_b64 s[18:19], -1
	s_and_b64 vcc, exec, s[38:39]
	v_lshl_add_u64 v[72:73], v[74:75], 1, s[24:25]
	s_cbranch_vccnz .LBB0_1692
	global_load_dwordx4 v[76:79], v[72:73], off
	s_mov_b64 s[18:19], 0
	s_waitcnt vmcnt(0)
	v_lshlrev_b32_e32 v88, 16, v76
	v_and_b32_e32 v89, 0xffff0000, v76
	v_lshlrev_b32_e32 v76, 16, v77
	v_and_b32_e32 v77, 0xffff0000, v77
	v_lshlrev_b32_e32 v90, 16, v78
	v_and_b32_e32 v91, 0xffff0000, v78
	v_lshlrev_b32_e32 v78, 16, v79
	v_and_b32_e32 v79, 0xffff0000, v79
	v_pk_fma_f32 v[92:93], v[62:63], v[86:87], v[76:77]
	v_pk_fma_f32 v[76:77], v[60:61], v[84:85], v[88:89]
	v_pk_fma_f32 v[88:89], v[58:59], v[82:83], v[78:79]
	v_pk_fma_f32 v[78:79], v[56:57], v[80:81], v[90:91]
	v_cvt_pk_bf16_f32 v76, v76, v77
	v_cvt_pk_bf16_f32 v77, v92, v93
	s_nop 0
	v_cvt_pk_bf16_f32 v78, v78, v79
	v_cvt_pk_bf16_f32 v79, v88, v89
	global_store_dwordx4 v[72:73], v[76:79], off sc1
.LBB0_1692:
	s_andn2_b64 vcc, exec, s[18:19]
	v_readlane_b32 s18, v249, 58
	v_readlane_b32 s19, v249, 59
	s_nop 1
	v_lshl_add_u64 v[74:75], v[74:75], 2, s[18:19]
	s_cbranch_vccnz .LBB0_1723
	global_load_dwordx4 v[76:79], v[74:75], off
	global_load_dwordx4 v[88:91], v[74:75], off offset:16
	s_waitcnt vmcnt(0)
	v_pk_fma_f32 v[62:63], v[62:63], v[86:87], v[78:79]
	v_pk_fma_f32 v[60:61], v[60:61], v[84:85], v[76:77]
	v_pk_fma_f32 v[58:59], v[58:59], v[82:83], v[90:91]
	v_pk_fma_f32 v[56:57], v[56:57], v[80:81], v[88:89]
	global_store_dwordx4 v[74:75], v[60:63], off sc1
	global_store_dwordx4 v[74:75], v[56:59], off offset:16 sc1
	s_and_b64 vcc, exec, s[38:39]
	s_mov_b64 s[18:19], -1
	s_cbranch_vccz .LBB0_1724

.LBB0_1695:
	global_load_dwordx4 v[56:59], v[74:75], off offset:512
	global_load_dwordx4 v[60:63], v[74:75], off offset:528
	s_waitcnt vmcnt(0)
	v_pk_fma_f32 v[54:55], v[54:55], v[70:71], v[58:59]
	v_pk_fma_f32 v[52:53], v[52:53], v[68:69], v[56:57]
	v_pk_fma_f32 v[50:51], v[50:51], v[66:67], v[62:63]
	v_pk_fma_f32 v[48:49], v[48:49], v[64:65], v[60:61]
	global_store_dwordx4 v[74:75], v[52:55], off offset:512 sc1
	global_store_dwordx4 v[74:75], v[48:51], off offset:528 sc1
.LBB0_1696:
	s_nop 1
	v_lshlrev_b64 v[48:49], 11, v[156:157]
	v_lshl_add_u64 v[48:49], v[48:49], 0, v[154:155]
	s_mov_b64 s[18:19], 0x48000
	v_readlane_b32 s24, v249, 60
	v_lshl_add_u64 v[50:51], v[48:49], 0, s[18:19]
	v_readlane_b32 s25, v249, 61
	s_mov_b64 s[18:19], -1
	s_and_b64 vcc, exec, s[38:39]
	v_lshl_add_u64 v[48:49], v[50:51], 1, s[24:25]
	s_cbranch_vccnz .LBB0_1698
	global_load_dwordx4 v[52:55], v[48:49], off
	s_mov_b64 s[18:19], 0
	s_waitcnt vmcnt(0)
	v_lshlrev_b32_e32 v56, 16, v52
	v_and_b32_e32 v57, 0xffff0000, v52
	v_lshlrev_b32_e32 v52, 16, v53
	v_and_b32_e32 v53, 0xffff0000, v53
	v_lshlrev_b32_e32 v58, 16, v54
	v_and_b32_e32 v59, 0xffff0000, v54
	v_lshlrev_b32_e32 v54, 16, v55
	v_and_b32_e32 v55, 0xffff0000, v55
	v_pk_fma_f32 v[60:61], v[46:47], v[86:87], v[52:53]
	v_pk_fma_f32 v[52:53], v[44:45], v[84:85], v[56:57]
	v_pk_fma_f32 v[56:57], v[42:43], v[82:83], v[54:55]
	v_pk_fma_f32 v[54:55], v[40:41], v[80:81], v[58:59]
	v_cvt_pk_bf16_f32 v52, v52, v53
	v_cvt_pk_bf16_f32 v53, v60, v61
	s_nop 0
	v_cvt_pk_bf16_f32 v54, v54, v55
	v_cvt_pk_bf16_f32 v55, v56, v57
	global_store_dwordx4 v[48:49], v[52:55], off sc1
.LBB0_1698:
	s_andn2_b64 vcc, exec, s[18:19]
	v_readlane_b32 s18, v249, 58
	v_readlane_b32 s19, v249, 59
	s_nop 1
	v_lshl_add_u64 v[50:51], v[50:51], 2, s[18:19]
	s_cbranch_vccnz .LBB0_1725
	global_load_dwordx4 v[52:55], v[50:51], off
	global_load_dwordx4 v[56:59], v[50:51], off offset:16
	s_waitcnt vmcnt(0)
	v_pk_fma_f32 v[46:47], v[46:47], v[86:87], v[54:55]
	v_pk_fma_f32 v[44:45], v[44:45], v[84:85], v[52:53]
	v_pk_fma_f32 v[42:43], v[42:43], v[82:83], v[58:59]
	v_pk_fma_f32 v[40:41], v[40:41], v[80:81], v[56:57]
	global_store_dwordx4 v[50:51], v[44:47], off sc1
	global_store_dwordx4 v[50:51], v[40:43], off offset:16 sc1
	s_and_b64 vcc, exec, s[38:39]
	s_mov_b64 s[18:19], -1
	s_cbranch_vccz .LBB0_1726

.LBB0_1701:
	global_load_dwordx4 v[40:43], v[50:51], off offset:512
	global_load_dwordx4 v[44:47], v[50:51], off offset:528
	s_waitcnt vmcnt(0)
	v_pk_fma_f32 v[38:39], v[38:39], v[70:71], v[42:43]
	v_pk_fma_f32 v[36:37], v[36:37], v[68:69], v[40:41]
	v_pk_fma_f32 v[34:35], v[34:35], v[66:67], v[46:47]
	v_pk_fma_f32 v[32:33], v[32:33], v[64:65], v[44:45]
	global_store_dwordx4 v[50:51], v[36:39], off offset:512 sc1
	global_store_dwordx4 v[50:51], v[32:35], off offset:528 sc1
.LBB0_1702:
	s_nop 1
	v_lshlrev_b64 v[32:33], 11, v[156:157]
	v_lshl_add_u64 v[32:33], v[32:33], 0, v[154:155]
	s_mov_b64 s[18:19], 0x50000
	v_readlane_b32 s24, v249, 60
	v_lshl_add_u64 v[34:35], v[32:33], 0, s[18:19]
	v_readlane_b32 s25, v249, 61
	s_mov_b64 s[18:19], -1
	s_and_b64 vcc, exec, s[38:39]
	v_lshl_add_u64 v[32:33], v[34:35], 1, s[24:25]
	s_cbranch_vccnz .LBB0_1704
	global_load_dwordx4 v[36:39], v[32:33], off
	s_mov_b64 s[18:19], 0
	s_waitcnt vmcnt(0)
	v_lshlrev_b32_e32 v40, 16, v36
	v_and_b32_e32 v41, 0xffff0000, v36
	v_lshlrev_b32_e32 v36, 16, v37
	v_and_b32_e32 v37, 0xffff0000, v37
	v_lshlrev_b32_e32 v42, 16, v38
	v_and_b32_e32 v43, 0xffff0000, v38
	v_lshlrev_b32_e32 v38, 16, v39
	v_and_b32_e32 v39, 0xffff0000, v39
	v_pk_fma_f32 v[44:45], v[30:31], v[86:87], v[36:37]
	v_pk_fma_f32 v[36:37], v[28:29], v[84:85], v[40:41]
	v_pk_fma_f32 v[40:41], v[26:27], v[82:83], v[38:39]
	v_pk_fma_f32 v[38:39], v[24:25], v[80:81], v[42:43]
	v_cvt_pk_bf16_f32 v36, v36, v37
	v_cvt_pk_bf16_f32 v37, v44, v45
	s_nop 0
	v_cvt_pk_bf16_f32 v38, v38, v39
	v_cvt_pk_bf16_f32 v39, v40, v41
	global_store_dwordx4 v[32:33], v[36:39], off sc1
.LBB0_1704:
	s_andn2_b64 vcc, exec, s[18:19]
	v_readlane_b32 s18, v249, 58
	v_readlane_b32 s19, v249, 59
	s_nop 1
	v_lshl_add_u64 v[34:35], v[34:35], 2, s[18:19]
	s_cbranch_vccnz .LBB0_1727
	global_load_dwordx4 v[36:39], v[34:35], off
	global_load_dwordx4 v[40:43], v[34:35], off offset:16
	s_waitcnt vmcnt(0)
	v_pk_fma_f32 v[30:31], v[30:31], v[86:87], v[38:39]
	v_pk_fma_f32 v[28:29], v[28:29], v[84:85], v[36:37]
	v_pk_fma_f32 v[26:27], v[26:27], v[82:83], v[42:43]
	v_pk_fma_f32 v[24:25], v[24:25], v[80:81], v[40:41]
	global_store_dwordx4 v[34:35], v[28:31], off sc1
	global_store_dwordx4 v[34:35], v[24:27], off offset:16 sc1
	s_and_b64 vcc, exec, s[38:39]
	s_mov_b64 s[18:19], -1
	s_cbranch_vccz .LBB0_1728

.LBB0_1707:
	global_load_dwordx4 v[24:27], v[34:35], off offset:512
	global_load_dwordx4 v[28:31], v[34:35], off offset:528
	s_waitcnt vmcnt(0)
	v_pk_fma_f32 v[22:23], v[22:23], v[70:71], v[26:27]
	v_pk_fma_f32 v[20:21], v[20:21], v[68:69], v[24:25]
	v_pk_fma_f32 v[18:19], v[18:19], v[66:67], v[30:31]
	v_pk_fma_f32 v[16:17], v[16:17], v[64:65], v[28:29]
	global_store_dwordx4 v[34:35], v[20:23], off offset:512 sc1
	global_store_dwordx4 v[34:35], v[16:19], off offset:528 sc1
.LBB0_1708:
	s_nop 1
	v_lshlrev_b64 v[16:17], 11, v[156:157]
	v_lshl_add_u64 v[16:17], v[16:17], 0, v[154:155]
	s_mov_b64 s[18:19], 0x58000
	v_readlane_b32 s24, v249, 60
	v_lshl_add_u64 v[18:19], v[16:17], 0, s[18:19]
	v_readlane_b32 s25, v249, 61
	s_mov_b64 s[18:19], -1
	s_and_b64 vcc, exec, s[38:39]
	v_lshl_add_u64 v[16:17], v[18:19], 1, s[24:25]
	s_cbranch_vccnz .LBB0_1710
	global_load_dwordx4 v[20:23], v[16:17], off
	s_mov_b64 s[18:19], 0
	s_waitcnt vmcnt(0)
	v_lshlrev_b32_e32 v24, 16, v20
	v_and_b32_e32 v25, 0xffff0000, v20
	v_lshlrev_b32_e32 v20, 16, v21
	v_and_b32_e32 v21, 0xffff0000, v21
	v_lshlrev_b32_e32 v26, 16, v22
	v_and_b32_e32 v27, 0xffff0000, v22
	v_lshlrev_b32_e32 v22, 16, v23
	v_and_b32_e32 v23, 0xffff0000, v23
	v_pk_fma_f32 v[28:29], v[14:15], v[86:87], v[20:21]
	v_pk_fma_f32 v[20:21], v[12:13], v[84:85], v[24:25]
	v_pk_fma_f32 v[24:25], v[10:11], v[82:83], v[22:23]
	v_pk_fma_f32 v[22:23], v[8:9], v[80:81], v[26:27]
	v_cvt_pk_bf16_f32 v20, v20, v21
	v_cvt_pk_bf16_f32 v21, v28, v29
	s_nop 0
	v_cvt_pk_bf16_f32 v22, v22, v23
	v_cvt_pk_bf16_f32 v23, v24, v25
	global_store_dwordx4 v[16:17], v[20:23], off sc1
.LBB0_1710:
	s_andn2_b64 vcc, exec, s[18:19]
	v_readlane_b32 s18, v249, 58
	v_readlane_b32 s19, v249, 59
	s_nop 1
	v_lshl_add_u64 v[18:19], v[18:19], 2, s[18:19]
	s_cbranch_vccnz .LBB0_1729
	global_load_dwordx4 v[20:23], v[18:19], off
	global_load_dwordx4 v[24:27], v[18:19], off offset:16
	s_waitcnt vmcnt(0)
	v_pk_fma_f32 v[14:15], v[14:15], v[86:87], v[22:23]
	v_pk_fma_f32 v[12:13], v[12:13], v[84:85], v[20:21]
	v_pk_fma_f32 v[10:11], v[10:11], v[82:83], v[26:27]
	v_pk_fma_f32 v[8:9], v[8:9], v[80:81], v[24:25]
	global_store_dwordx4 v[18:19], v[12:15], off sc1
	global_store_dwordx4 v[18:19], v[8:11], off offset:16 sc1
	s_and_b64 vcc, exec, s[38:39]
	s_mov_b64 s[18:19], -1
	s_cbranch_vccz .LBB0_1730

.LBB0_1713:
	global_load_dwordx4 v[8:11], v[18:19], off offset:512
	global_load_dwordx4 v[12:15], v[18:19], off offset:528
	s_waitcnt vmcnt(0)
	v_pk_fma_f32 v[6:7], v[6:7], v[70:71], v[10:11]
	v_pk_fma_f32 v[4:5], v[4:5], v[68:69], v[8:9]
	v_pk_fma_f32 v[2:3], v[2:3], v[66:67], v[14:15]
	v_pk_fma_f32 v[0:1], v[0:1], v[64:65], v[12:13]
	global_store_dwordx4 v[18:19], v[4:7], off offset:512 sc1
	global_store_dwordx4 v[18:19], v[0:3], off offset:528 sc1

.LBB0_1718:
	global_load_dwordx4 v[120:123], v[128:129], off offset:256
	s_waitcnt vmcnt(0)
	v_lshlrev_b32_e32 v124, 16, v120
	v_and_b32_e32 v125, 0xffff0000, v120
	v_lshlrev_b32_e32 v120, 16, v121
	v_and_b32_e32 v121, 0xffff0000, v121
	v_lshlrev_b32_e32 v126, 16, v122
	v_and_b32_e32 v127, 0xffff0000, v122
	v_lshlrev_b32_e32 v122, 16, v123
	v_and_b32_e32 v123, 0xffff0000, v123
	v_pk_fma_f32 v[132:133], v[118:119], v[70:71], v[120:121]
	v_pk_fma_f32 v[120:121], v[116:117], v[68:69], v[124:125]
	v_pk_fma_f32 v[124:125], v[114:115], v[66:67], v[122:123]
	v_pk_fma_f32 v[122:123], v[112:113], v[64:65], v[126:127]
	v_cvt_pk_bf16_f32 v120, v120, v121
	v_cvt_pk_bf16_f32 v121, v132, v133
	s_nop 0
	v_cvt_pk_bf16_f32 v122, v122, v123
	v_cvt_pk_bf16_f32 v123, v124, v125
	global_store_dwordx4 v[128:129], v[120:123], off offset:256 sc1
	s_cbranch_execz .LBB0_1677
	s_branch .LBB0_1678

.LBB0_1720:
	global_load_dwordx4 v[104:107], v[112:113], off offset:256
	s_waitcnt vmcnt(0)
	v_lshlrev_b32_e32 v108, 16, v104
	v_and_b32_e32 v109, 0xffff0000, v104
	v_lshlrev_b32_e32 v104, 16, v105
	v_and_b32_e32 v105, 0xffff0000, v105
	v_lshlrev_b32_e32 v110, 16, v106
	v_and_b32_e32 v111, 0xffff0000, v106
	v_lshlrev_b32_e32 v106, 16, v107
	v_and_b32_e32 v107, 0xffff0000, v107
	v_pk_fma_f32 v[116:117], v[102:103], v[70:71], v[104:105]
	v_pk_fma_f32 v[104:105], v[100:101], v[68:69], v[108:109]
	v_pk_fma_f32 v[108:109], v[98:99], v[66:67], v[106:107]
	v_pk_fma_f32 v[106:107], v[96:97], v[64:65], v[110:111]
	v_cvt_pk_bf16_f32 v104, v104, v105
	v_cvt_pk_bf16_f32 v105, v116, v117
	s_nop 0
	v_cvt_pk_bf16_f32 v106, v106, v107
	v_cvt_pk_bf16_f32 v107, v108, v109
	global_store_dwordx4 v[112:113], v[104:107], off offset:256 sc1
	s_cbranch_execz .LBB0_1683
	s_branch .LBB0_1684

.LBB0_1722:
	global_load_dwordx4 v[88:91], v[96:97], off offset:256
	s_waitcnt vmcnt(0)
	v_lshlrev_b32_e32 v92, 16, v88
	v_and_b32_e32 v93, 0xffff0000, v88
	v_lshlrev_b32_e32 v88, 16, v89
	v_and_b32_e32 v89, 0xffff0000, v89
	v_lshlrev_b32_e32 v94, 16, v90
	v_and_b32_e32 v95, 0xffff0000, v90
	v_lshlrev_b32_e32 v90, 16, v91
	v_and_b32_e32 v91, 0xffff0000, v91
	v_pk_fma_f32 v[100:101], v[78:79], v[70:71], v[88:89]
	v_pk_fma_f32 v[88:89], v[76:77], v[68:69], v[92:93]
	v_pk_fma_f32 v[92:93], v[74:75], v[66:67], v[90:91]
	v_pk_fma_f32 v[90:91], v[72:73], v[64:65], v[94:95]
	v_cvt_pk_bf16_f32 v88, v88, v89
	v_cvt_pk_bf16_f32 v89, v100, v101
	s_nop 0
	v_cvt_pk_bf16_f32 v90, v90, v91
	v_cvt_pk_bf16_f32 v91, v92, v93
	global_store_dwordx4 v[96:97], v[88:91], off offset:256 sc1
	s_cbranch_execz .LBB0_1689
	s_branch .LBB0_1690

.LBB0_1724:
	global_load_dwordx4 v[56:59], v[72:73], off offset:256
	s_waitcnt vmcnt(0)
	v_lshlrev_b32_e32 v60, 16, v56
	v_and_b32_e32 v61, 0xffff0000, v56
	v_lshlrev_b32_e32 v56, 16, v57
	v_and_b32_e32 v57, 0xffff0000, v57
	v_lshlrev_b32_e32 v62, 16, v58
	v_and_b32_e32 v63, 0xffff0000, v58
	v_lshlrev_b32_e32 v58, 16, v59
	v_and_b32_e32 v59, 0xffff0000, v59
	v_pk_fma_f32 v[76:77], v[54:55], v[70:71], v[56:57]
	v_pk_fma_f32 v[56:57], v[52:53], v[68:69], v[60:61]
	v_pk_fma_f32 v[60:61], v[50:51], v[66:67], v[58:59]
	v_pk_fma_f32 v[58:59], v[48:49], v[64:65], v[62:63]
	v_cvt_pk_bf16_f32 v56, v56, v57
	v_cvt_pk_bf16_f32 v57, v76, v77
	s_nop 0
	v_cvt_pk_bf16_f32 v58, v58, v59
	v_cvt_pk_bf16_f32 v59, v60, v61
	global_store_dwordx4 v[72:73], v[56:59], off offset:256 sc1
	s_cbranch_execz .LBB0_1695
	s_branch .LBB0_1696

.LBB0_1726:
	global_load_dwordx4 v[40:43], v[48:49], off offset:256
	s_waitcnt vmcnt(0)
	v_lshlrev_b32_e32 v44, 16, v40
	v_and_b32_e32 v45, 0xffff0000, v40
	v_lshlrev_b32_e32 v40, 16, v41
	v_and_b32_e32 v41, 0xffff0000, v41
	v_lshlrev_b32_e32 v46, 16, v42
	v_and_b32_e32 v47, 0xffff0000, v42
	v_lshlrev_b32_e32 v42, 16, v43
	v_and_b32_e32 v43, 0xffff0000, v43
	v_pk_fma_f32 v[52:53], v[38:39], v[70:71], v[40:41]
	v_pk_fma_f32 v[40:41], v[36:37], v[68:69], v[44:45]
	v_pk_fma_f32 v[44:45], v[34:35], v[66:67], v[42:43]
	v_pk_fma_f32 v[42:43], v[32:33], v[64:65], v[46:47]
	v_cvt_pk_bf16_f32 v40, v40, v41
	v_cvt_pk_bf16_f32 v41, v52, v53
	s_nop 0
	v_cvt_pk_bf16_f32 v42, v42, v43
	v_cvt_pk_bf16_f32 v43, v44, v45
	global_store_dwordx4 v[48:49], v[40:43], off offset:256 sc1
	s_cbranch_execz .LBB0_1701
	s_branch .LBB0_1702

.LBB0_1728:
	global_load_dwordx4 v[24:27], v[32:33], off offset:256
	s_waitcnt vmcnt(0)
	v_lshlrev_b32_e32 v28, 16, v24
	v_and_b32_e32 v29, 0xffff0000, v24
	v_lshlrev_b32_e32 v24, 16, v25
	v_and_b32_e32 v25, 0xffff0000, v25
	v_lshlrev_b32_e32 v30, 16, v26
	v_and_b32_e32 v31, 0xffff0000, v26
	v_lshlrev_b32_e32 v26, 16, v27
	v_and_b32_e32 v27, 0xffff0000, v27
	v_pk_fma_f32 v[36:37], v[22:23], v[70:71], v[24:25]
	v_pk_fma_f32 v[24:25], v[20:21], v[68:69], v[28:29]
	v_pk_fma_f32 v[28:29], v[18:19], v[66:67], v[26:27]
	v_pk_fma_f32 v[26:27], v[16:17], v[64:65], v[30:31]
	v_cvt_pk_bf16_f32 v24, v24, v25
	v_cvt_pk_bf16_f32 v25, v36, v37
	s_nop 0
	v_cvt_pk_bf16_f32 v26, v26, v27
	v_cvt_pk_bf16_f32 v27, v28, v29
	global_store_dwordx4 v[32:33], v[24:27], off offset:256 sc1
	s_cbranch_execz .LBB0_1707
	s_branch .LBB0_1708

.LBB0_1730:
	global_load_dwordx4 v[8:11], v[16:17], off offset:256
	s_waitcnt vmcnt(0)
	v_lshlrev_b32_e32 v12, 16, v8
	v_and_b32_e32 v13, 0xffff0000, v8
	v_lshlrev_b32_e32 v8, 16, v9
	v_and_b32_e32 v9, 0xffff0000, v9
	v_lshlrev_b32_e32 v14, 16, v10
	v_and_b32_e32 v15, 0xffff0000, v10
	v_lshlrev_b32_e32 v10, 16, v11
	v_and_b32_e32 v11, 0xffff0000, v11
	v_pk_fma_f32 v[20:21], v[6:7], v[70:71], v[8:9]
	v_pk_fma_f32 v[8:9], v[4:5], v[68:69], v[12:13]
	v_pk_fma_f32 v[12:13], v[2:3], v[66:67], v[10:11]
	v_pk_fma_f32 v[10:11], v[0:1], v[64:65], v[14:15]
	v_cvt_pk_bf16_f32 v8, v8, v9
	v_cvt_pk_bf16_f32 v9, v20, v21
	s_nop 0
	v_cvt_pk_bf16_f32 v10, v10, v11
	v_cvt_pk_bf16_f32 v11, v12, v13
	global_store_dwordx4 v[16:17], v[8:11], off offset:256 sc1
	s_cbranch_execz .LBB0_1713
	s_branch .LBB0_1714

.LBB0_1744:
	v_lshl_or_b32 v112, s31, 8, v173
	v_ashrrev_i32_e32 v113, 31, v112
	v_lshlrev_b64 v[170:171], 2, v[112:113]
	v_lshl_add_u64 v[120:121], s[0:1], 0, v[170:171]
	global_load_dwordx4 v[116:119], v[120:121], off offset:16
	global_load_dwordx4 v[124:127], v[120:121], off
	global_load_dwordx4 v[112:115], v[120:121], off offset:528
	s_nop 0
	global_load_dwordx4 v[120:123], v[120:121], off offset:512
	s_ashr_i32 s31, s30, 31
	s_lshl_b64 s[28:29], s[30:31], 21
	v_readlane_b32 s30, v250, 6
	v_readlane_b32 s31, v250, 7
	s_add_u32 s28, s30, s28
	s_addc_u32 s29, s31, s29
	v_lshl_add_u64 v[170:171], s[28:29], 0, v[170:171]
	v_lshl_add_u64 v[176:177], v[170:171], 0, v[150:151]
	s_mov_b64 s[30:31], -1
	s_andn2_b64 vcc, exec, s[16:17]
	s_waitcnt vmcnt(0)
	v_pk_mul_f32 v[138:139], v[138:139], v[118:119]
	v_pk_mul_f32 v[142:143], v[142:143], v[126:127]
	v_pk_mul_f32 v[130:131], v[130:131], v[114:115]
	v_pk_mul_f32 v[128:129], v[128:129], v[112:113]
	global_store_dwordx4 v[176:177], v[128:131], off offset:528 sc1
	v_pk_mul_f32 v[98:99], v[98:99], v[114:115]
	v_pk_mul_f32 v[96:97], v[96:97], v[112:113]
	v_lshl_add_u64 v[128:129], v[170:171], 0, v[152:153]
	global_store_dwordx4 v[128:129], v[96:99], off offset:528 sc1
	v_pk_mul_f32 v[82:83], v[82:83], v[114:115]
	v_pk_mul_f32 v[80:81], v[80:81], v[112:113]
	v_lshl_add_u64 v[96:97], v[170:171], 0, v[154:155]
	global_store_dwordx4 v[96:97], v[80:83], off offset:528 sc1
	v_pk_mul_f32 v[66:67], v[66:67], v[114:115]
	v_pk_mul_f32 v[64:65], v[64:65], v[112:113]
	v_lshl_add_u64 v[80:81], v[170:171], 0, v[156:157]
	global_store_dwordx4 v[80:81], v[64:67], off offset:528 sc1
	v_pk_mul_f32 v[50:51], v[50:51], v[114:115]
	v_pk_mul_f32 v[48:49], v[48:49], v[112:113]
	v_lshl_add_u64 v[64:65], v[170:171], 0, v[158:159]
	global_store_dwordx4 v[64:65], v[48:51], off offset:528 sc1
	v_pk_mul_f32 v[34:35], v[34:35], v[122:123]
	v_pk_mul_f32 v[32:33], v[32:33], v[120:121]
	v_lshl_add_u64 v[48:49], v[170:171], 0, v[160:161]
	global_store_dwordx4 v[48:49], v[32:35], off offset:512 sc1
	v_pk_mul_f32 v[26:27], v[26:27], v[114:115]
	v_pk_mul_f32 v[24:25], v[24:25], v[112:113]
	v_lshl_add_u64 v[32:33], v[170:171], 0, v[162:163]
	v_pk_mul_f32 v[18:19], v[18:19], v[122:123]
	v_pk_mul_f32 v[16:17], v[16:17], v[120:121]
	v_pk_mul_f32 v[10:11], v[10:11], v[114:115]
	v_pk_mul_f32 v[8:9], v[8:9], v[112:113]
	global_store_dwordx4 v[48:49], v[24:27], off offset:528 sc1
	global_store_dwordx4 v[32:33], v[16:19], off offset:512 sc1
	global_store_dwordx4 v[32:33], v[8:11], off offset:528 sc1
	v_pk_mul_f32 v[26:27], v[38:39], v[126:127]
	v_pk_mul_f32 v[24:25], v[36:37], v[124:125]
	v_lshl_add_u64 v[16:17], v[170:171], 0, v[164:165]
	v_pk_mul_f32 v[10:11], v[22:23], v[126:127]
	v_pk_mul_f32 v[8:9], v[20:21], v[124:125]
	v_pk_mul_f32 v[140:141], v[140:141], v[124:125]
	v_pk_mul_f32 v[136:137], v[136:137], v[116:117]
	v_pk_mul_f32 v[134:135], v[134:135], v[122:123]
	v_pk_mul_f32 v[132:133], v[132:133], v[120:121]
	v_pk_mul_f32 v[110:111], v[110:111], v[126:127]
	v_pk_mul_f32 v[108:109], v[108:109], v[124:125]
	v_pk_mul_f32 v[106:107], v[106:107], v[118:119]
	v_pk_mul_f32 v[104:105], v[104:105], v[116:117]
	v_pk_mul_f32 v[102:103], v[102:103], v[122:123]
	v_pk_mul_f32 v[100:101], v[100:101], v[120:121]
	v_pk_mul_f32 v[94:95], v[94:95], v[126:127]
	v_pk_mul_f32 v[92:93], v[92:93], v[124:125]
	v_pk_mul_f32 v[90:91], v[90:91], v[118:119]
	v_pk_mul_f32 v[88:89], v[88:89], v[116:117]
	v_pk_mul_f32 v[86:87], v[86:87], v[122:123]
	v_pk_mul_f32 v[84:85], v[84:85], v[120:121]
	v_pk_mul_f32 v[78:79], v[78:79], v[126:127]
	v_pk_mul_f32 v[76:77], v[76:77], v[124:125]
	v_pk_mul_f32 v[74:75], v[74:75], v[118:119]
	v_pk_mul_f32 v[72:73], v[72:73], v[116:117]
	v_pk_mul_f32 v[70:71], v[70:71], v[122:123]
	v_pk_mul_f32 v[68:69], v[68:69], v[120:121]
	v_pk_mul_f32 v[62:63], v[62:63], v[126:127]
	v_pk_mul_f32 v[60:61], v[60:61], v[124:125]
	v_pk_mul_f32 v[58:59], v[58:59], v[118:119]
	v_pk_mul_f32 v[56:57], v[56:57], v[116:117]
	v_pk_mul_f32 v[54:55], v[54:55], v[122:123]
	v_pk_mul_f32 v[52:53], v[52:53], v[120:121]
	v_pk_mul_f32 v[46:47], v[46:47], v[126:127]
	v_pk_mul_f32 v[44:45], v[44:45], v[124:125]
	v_pk_mul_f32 v[42:43], v[42:43], v[118:119]
	v_pk_mul_f32 v[40:41], v[40:41], v[116:117]
	global_store_dwordx4 v[32:33], v[24:27], off sc1
	global_store_dwordx4 v[16:17], v[8:11], off sc1
	v_pk_mul_f32 v[6:7], v[6:7], v[122:123]
	v_pk_mul_f32 v[26:27], v[30:31], v[118:119]
	v_pk_mul_f32 v[24:25], v[28:29], v[116:117]
	v_pk_mul_f32 v[10:11], v[14:15], v[118:119]
	v_pk_mul_f32 v[8:9], v[12:13], v[116:117]
	v_pk_mul_f32 v[4:5], v[4:5], v[120:121]
	v_pk_mul_f32 v[2:3], v[2:3], v[114:115]
	v_pk_mul_f32 v[0:1], v[0:1], v[112:113]
	global_store_dwordx4 v[176:177], v[140:143], off sc1
	global_store_dwordx4 v[176:177], v[136:139], off offset:16 sc1
	global_store_dwordx4 v[176:177], v[132:135], off offset:512 sc1
	global_store_dwordx4 v[128:129], v[108:111], off sc1
	global_store_dwordx4 v[128:129], v[104:107], off offset:16 sc1
	global_store_dwordx4 v[128:129], v[100:103], off offset:512 sc1
	global_store_dwordx4 v[96:97], v[92:95], off sc1
	global_store_dwordx4 v[96:97], v[88:91], off offset:16 sc1
	global_store_dwordx4 v[96:97], v[84:87], off offset:512 sc1
	global_store_dwordx4 v[80:81], v[76:79], off sc1
	global_store_dwordx4 v[80:81], v[72:75], off offset:16 sc1
	global_store_dwordx4 v[80:81], v[68:71], off offset:512 sc1
	global_store_dwordx4 v[64:65], v[60:63], off sc1
	global_store_dwordx4 v[64:65], v[56:59], off offset:16 sc1
	global_store_dwordx4 v[64:65], v[52:55], off offset:512 sc1
	global_store_dwordx4 v[48:49], v[44:47], off sc1
	global_store_dwordx4 v[48:49], v[40:43], off offset:16 sc1
	global_store_dwordx4 v[32:33], v[24:27], off offset:16 sc1
	global_store_dwordx4 v[16:17], v[8:11], off offset:16 sc1
	global_store_dwordx4 v[16:17], v[4:7], off offset:512 sc1
	global_store_dwordx4 v[16:17], v[0:3], off offset:528 sc1
	s_cbranch_vccnz .LBB0_1737
	s_andn2_b64 vcc, exec, s[6:7]
	s_cbranch_vccnz .LBB0_1736
	s_barrier
	s_branch .LBB0_1736
